# all 16-byte global stores made write-through (sc1) so the release fence at each grid barrier finds less dirty L2
# baseline (speedup 1.0000x reference)
; #define GAS __attribute__((address_space(1)))
; #define LAS __attribute__((address_space(3)))
; #define LDS_WAIT() asm volatile("s_waitcnt lgkmcnt(0)" ::: "memory")
; __device__ __forceinline__ unsigned cvt_pk_bf16(float lo, float hi) { unsigned r; asm volatile("v_cvt_pk_bf16_f32 %0, %1, %2" : "=v"(r) : "v"(lo), "v"(hi)); return r; }
; template <class ColMap>
; __device__ __forceinline__ void transpose_item(const float* W, int K, int N, bf16* WT, LAS float* scr, int item, int lane, const ColMap& cm) {
;     const int nblk = N / 64, kb = item / nblk, nb = item % nblk, k0 = 64 * kb, n0 = 64 * nb;
;     const int s0 = cm(n0);
; #pragma unroll 4
;     for (int i = 0; i < 16; ++i) { const int kk = 4 * i + (lane >> 4), c4 = (lane & 15) * 4;
;         const f32x4 v = *(const GAS f32x4*)(W + (size_t)(k0 + kk) * N + s0 + c4);
;         LAS float* d = scr + kk * 65 + c4; d[0] = v[0]; d[1] = v[1]; d[2] = v[2]; d[3] = v[3]; }
;     LDS_WAIT(); asm volatile("" ::: "memory");
;     const int c = lane & 7;
; #pragma unroll
;     for (int j = 0; j < 8; ++j) { const int n = (lane >> 3) + 8 * j; const LAS float* s = scr + (8 * c) * 65 + n;
;         v4u o; o.x = cvt_pk_bf16(s[0 * 65], s[1 * 65]); o.y = cvt_pk_bf16(s[2 * 65], s[3 * 65]); o.z = cvt_pk_bf16(s[4 * 65], s[5 * 65]); o.w = cvt_pk_bf16(s[6 * 65], s[7 * 65]);
;         *(GAS v4u*)(WT + (size_t)(n0 + n) * K + k0 + 8 * c) = o; }
;     LDS_WAIT(); asm volatile("" ::: "memory");
; }
.LBB0_35:
	v_lshl_add_u64 v[26:27], v[10:11], 0, s[8:9]
	v_ashrrev_i32_e32 v5, 31, v4
	v_lshl_add_u64 v[28:29], v[8:9], 0, s[8:9]
	v_lshl_add_u64 v[30:31], v[6:7], 0, s[8:9]
	global_load_dwordx4 v[14:17], v[26:27], off
	global_load_dwordx4 v[18:21], v[28:29], off
	global_load_dwordx4 v[22:25], v[30:31], off
	v_lshlrev_b64 v[26:27], 13, v[4:5]
	v_lshl_add_u64 v[26:27], v[2:3], 0, v[26:27]
	global_load_dwordx4 v[26:29], v[26:27], off
	s_add_u32 s8, s8, 0x20000
	s_addc_u32 s9, s9, 0
	v_add_u32_e32 v0, 0x410, v13
	v_add_u32_e32 v5, 0x418, v13
	v_add_u32_e32 v30, 0x820, v13
	v_add_u32_e32 v31, 0x828, v13
	v_add_u32_e32 v32, 0xc30, v13
	v_add_u32_e32 v33, 0xc38, v13
	v_add_u32_e32 v4, 16, v4
	s_cmp_lg_u32 s8, 0x80000
	s_waitcnt vmcnt(3)
	ds_write2_b32 v13, v14, v15 offset1:1
	ds_write2_b32 v13, v16, v17 offset0:2 offset1:3
	s_waitcnt vmcnt(2)
	ds_write2_b32 v0, v18, v19 offset1:1
	ds_write2_b32 v5, v20, v21 offset1:1
	s_waitcnt vmcnt(1)
	ds_write2_b32 v30, v22, v23 offset1:1
	ds_write2_b32 v31, v24, v25 offset1:1
	v_add_u32_e32 v13, 0x1040, v13
	s_waitcnt vmcnt(0)
	ds_write2_b32 v32, v26, v27 offset1:1
	ds_write2_b32 v33, v28, v29 offset1:1
	s_cbranch_scc1 .LBB0_35
	v_lshlrev_b32_e32 v2, 3, v12
	v_ashrrev_i32_e32 v0, 3, v12
	v_and_b32_e32 v9, 56, v2
	s_waitcnt lgkmcnt(0)
	v_mul_u32_u24_e32 v2, 0x104, v9
	v_lshlrev_b32_e32 v3, 2, v0
	s_lshl_b64 s[6:7], s[6:7], 1
	v_add3_u32 v14, s17, v2, v3
	s_add_u32 s6, s18, s6
	v_add_u32_e32 v8, s4, v0
	ds_read2_b32 v[2:3], v14 offset1:65
	s_addc_u32 s7, s19, s7
	v_lshlrev_b32_e32 v0, 1, v9
	v_ashrrev_i32_e32 v9, 31, v8
	s_waitcnt lgkmcnt(0)
	v_cvt_pk_bf16_f32 v2, v2, v3
	ds_read2_b32 v[4:5], v14 offset0:130 offset1:195
	v_add_u32_e32 v15, 0x400, v14
	v_lshl_add_u64 v[10:11], s[6:7], 0, v[0:1]
	v_lshlrev_b64 v[12:13], 12, v[8:9]
	s_waitcnt lgkmcnt(0)
	v_cvt_pk_bf16_f32 v3, v4, v5
	ds_read2_b32 v[4:5], v15 offset0:4 offset1:69
	v_lshl_add_u64 v[12:13], v[10:11], 0, v[12:13]
	s_waitcnt lgkmcnt(0)
	v_cvt_pk_bf16_f32 v4, v4, v5
	ds_read2_b32 v[6:7], v15 offset0:134 offset1:199
	s_waitcnt lgkmcnt(0)
	v_cvt_pk_bf16_f32 v5, v6, v7
	global_store_dwordx4 v[12:13], v[2:5], off sc1
	v_add_u32_e32 v12, 8, v8
	v_ashrrev_i32_e32 v13, 31, v12
	ds_read2_b32 v[6:7], v14 offset0:8 offset1:73
	s_waitcnt lgkmcnt(0)
	v_cvt_pk_bf16_f32 v2, v6, v7
	ds_read2_b32 v[4:5], v14 offset0:138 offset1:203
	v_lshlrev_b64 v[12:13], 12, v[12:13]
	s_waitcnt lgkmcnt(0)
	v_cvt_pk_bf16_f32 v3, v4, v5
	ds_read2_b32 v[4:5], v15 offset0:12 offset1:77
	v_lshl_add_u64 v[12:13], v[10:11], 0, v[12:13]
	s_waitcnt lgkmcnt(0)
	v_cvt_pk_bf16_f32 v4, v4, v5
	ds_read2_b32 v[6:7], v15 offset0:142 offset1:207
	s_waitcnt lgkmcnt(0)
	v_cvt_pk_bf16_f32 v5, v6, v7
	global_store_dwordx4 v[12:13], v[2:5], off sc1
	v_add_u32_e32 v12, 16, v8
	v_ashrrev_i32_e32 v13, 31, v12
	ds_read2_b32 v[6:7], v14 offset0:16 offset1:81
	s_waitcnt lgkmcnt(0)
	v_cvt_pk_bf16_f32 v2, v6, v7
	ds_read2_b32 v[4:5], v14 offset0:146 offset1:211
	v_lshlrev_b64 v[12:13], 12, v[12:13]
	s_waitcnt lgkmcnt(0)
	v_cvt_pk_bf16_f32 v3, v4, v5
	ds_read2_b32 v[4:5], v15 offset0:20 offset1:85
	v_lshl_add_u64 v[12:13], v[10:11], 0, v[12:13]
	s_waitcnt lgkmcnt(0)
	v_cvt_pk_bf16_f32 v4, v4, v5
	ds_read2_b32 v[6:7], v15 offset0:150 offset1:215
	s_waitcnt lgkmcnt(0)
	v_cvt_pk_bf16_f32 v5, v6, v7
	global_store_dwordx4 v[12:13], v[2:5], off sc1
	v_add_u32_e32 v12, 24, v8
	v_ashrrev_i32_e32 v13, 31, v12
	ds_read2_b32 v[6:7], v14 offset0:24 offset1:89
	s_waitcnt lgkmcnt(0)
	v_cvt_pk_bf16_f32 v2, v6, v7
	ds_read2_b32 v[4:5], v14 offset0:154 offset1:219
	v_lshlrev_b64 v[12:13], 12, v[12:13]
	s_waitcnt lgkmcnt(0)
	v_cvt_pk_bf16_f32 v3, v4, v5
	ds_read2_b32 v[4:5], v15 offset0:28 offset1:93
	v_lshl_add_u64 v[12:13], v[10:11], 0, v[12:13]
	s_waitcnt lgkmcnt(0)
	v_cvt_pk_bf16_f32 v4, v4, v5
	ds_read2_b32 v[6:7], v15 offset0:158 offset1:223
	s_waitcnt lgkmcnt(0)
	v_cvt_pk_bf16_f32 v5, v6, v7
	global_store_dwordx4 v[12:13], v[2:5], off sc1
	v_add_u32_e32 v12, 32, v8
	v_ashrrev_i32_e32 v13, 31, v12
	ds_read2_b32 v[6:7], v14 offset0:32 offset1:97
	s_waitcnt lgkmcnt(0)
	v_cvt_pk_bf16_f32 v2, v6, v7
	ds_read2_b32 v[4:5], v14 offset0:162 offset1:227
	v_lshlrev_b64 v[12:13], 12, v[12:13]
	s_waitcnt lgkmcnt(0)
	v_cvt_pk_bf16_f32 v3, v4, v5
	ds_read2_b32 v[4:5], v15 offset0:36 offset1:101
	v_lshl_add_u64 v[12:13], v[10:11], 0, v[12:13]
	s_waitcnt lgkmcnt(0)
	v_cvt_pk_bf16_f32 v4, v4, v5
	ds_read2_b32 v[6:7], v15 offset0:166 offset1:231
	s_waitcnt lgkmcnt(0)
	v_cvt_pk_bf16_f32 v5, v6, v7
	global_store_dwordx4 v[12:13], v[2:5], off sc1
	v_add_u32_e32 v12, 40, v8
	ds_read2_b32 v[6:7], v14 offset0:40 offset1:105
	s_waitcnt lgkmcnt(0)
	v_cvt_pk_bf16_f32 v2, v6, v7
	ds_read2_b32 v[4:5], v14 offset0:170 offset1:235
	v_ashrrev_i32_e32 v13, 31, v12
	s_waitcnt lgkmcnt(0)
	v_cvt_pk_bf16_f32 v3, v4, v5
	ds_read2_b32 v[4:5], v15 offset0:44 offset1:109
	v_lshlrev_b64 v[12:13], 12, v[12:13]
	s_waitcnt lgkmcnt(0)
	v_cvt_pk_bf16_f32 v4, v4, v5
	ds_read2_b32 v[6:7], v15 offset0:174 offset1:239
	s_waitcnt lgkmcnt(0)
	v_cvt_pk_bf16_f32 v5, v6, v7
	v_lshl_add_u64 v[12:13], v[10:11], 0, v[12:13]
	ds_read2_b32 v[6:7], v14 offset0:48 offset1:113
	global_store_dwordx4 v[12:13], v[2:5], off sc1
	v_add_u32_e32 v12, 48, v8
	v_ashrrev_i32_e32 v13, 31, v12
	s_waitcnt lgkmcnt(0)
	v_cvt_pk_bf16_f32 v2, v6, v7
	ds_read2_b32 v[4:5], v14 offset0:178 offset1:243
	s_waitcnt lgkmcnt(0)
	v_cvt_pk_bf16_f32 v3, v4, v5
	ds_read2_b32 v[4:5], v15 offset0:52 offset1:117
	s_waitcnt lgkmcnt(0)
	v_cvt_pk_bf16_f32 v4, v4, v5
	ds_read2_b32 v[6:7], v15 offset0:182 offset1:247
	v_lshlrev_b64 v[12:13], 12, v[12:13]
	s_waitcnt lgkmcnt(0)
	v_cvt_pk_bf16_f32 v5, v6, v7
	ds_read2_b32 v[6:7], v14 offset0:56 offset1:121
	v_lshl_add_u64 v[12:13], v[10:11], 0, v[12:13]
	global_store_dwordx4 v[12:13], v[2:5], off sc1
	s_add_i32 s16, s16, s25
	s_cmpk_lt_i32 s16, 0x400
	s_waitcnt lgkmcnt(0)
	v_cvt_pk_bf16_f32 v2, v6, v7
	v_add_u32_e32 v6, 56, v8
	v_ashrrev_i32_e32 v7, 31, v6
	ds_read2_b32 v[4:5], v14 offset0:186 offset1:251
	v_lshlrev_b64 v[6:7], 12, v[6:7]
	s_waitcnt lgkmcnt(0)
	v_cvt_pk_bf16_f32 v3, v4, v5
	ds_read2_b32 v[4:5], v15 offset0:60 offset1:125
	v_lshl_add_u64 v[6:7], v[10:11], 0, v[6:7]
	s_waitcnt lgkmcnt(0)
	v_cvt_pk_bf16_f32 v4, v4, v5
	ds_read2_b32 v[8:9], v15 offset0:190 offset1:255
	s_waitcnt lgkmcnt(0)
	v_cvt_pk_bf16_f32 v5, v8, v9
	global_store_dwordx4 v[6:7], v[2:5], off sc1
	s_waitcnt lgkmcnt(0)
	s_cbranch_scc1 .LBB0_34

; #define GAS __attribute__((address_space(1)))
; #define LAS __attribute__((address_space(3)))
; __device__ __forceinline__ void do_slabs_impl(LAS unsigned char* lds, unsigned char* ws, const float* w_up, const float* w_dn, const float* w_in, int vcu, int G, int wave, int j0, int j1) {
;     ...
;             for (int i = 0; i < 8; ++i) { const int q = tid + NTHR * i, n = q >> 7, kc = q & 127; const float inv = red[256 + n];
;                 const int sx_ = ((n >> 3) & 3) << 3;
;                 const v4u a = *(const LAS v4u*)(slab + n * PITCH + ((kc * 16) ^ sx_)), b = *(const LAS v4u*)(slab + n * PITCH + ((kc * 16 + 8) ^ sx_));
;                 const unsigned src[8] = {a.x, a.y, a.z, a.w, b.x, b.y, b.z, b.w}; unsigned o[4];
;                 if (done.fp8) {
; #pragma unroll
;                     for (int d = 0; d < 4; ++d) { int w = __builtin_amdgcn_cvt_pk_fp8_f32(bf_lo(src[2 * d]) * inv, bf_hi(src[2 * d]) * inv, 0, false);
;                         w = __builtin_amdgcn_cvt_pk_fp8_f32(bf_lo(src[2 * d + 1]) * inv, bf_hi(src[2 * d + 1]) * inv, w, true); o[d] = (unsigned)w; }
;                 } else {
; #pragma unroll
;                 for (int d = 0; d < 4; ++d) { unsigned w = 0u;
; #pragma unroll
;                     for (int h2 = 0; h2 < 2; ++h2) { const unsigned u2 = src[2 * d + h2]; const int q0 = (int)__builtin_rintf(bf_lo(u2) * inv), q1 = (int)__builtin_rintf(bf_hi(u2) * inv);
;                         w |= ((unsigned)(q0 & 0xff) << (16 * h2)) | ((unsigned)(q1 & 0xff) << (16 * h2 + 8)); }
;                     o[d] = w; }
;                 }
;                 __builtin_nontemporal_store((v4u){o[0], o[1], o[2], o[3]}, (GAS v4u*)(done.WQ + ((size_t)done.e * done.NS + done.n0 + n) * D + kc * 16)); }
.LBB0_56:
	v_add_u32_e32 v244, s15, v192
	v_ashrrev_i32_e32 v242, 7, v244
	v_mul_lo_u32 v234, v242, s25
	v_lshrrev_b32_e32 v239, 7, v244
	v_add_u32_e32 v238, 0, v234
	v_bitop3_b32 v234, v239, v194, 24 bitop3:0x6c
	v_lshl_add_u32 v234, v234, 1, v238
	ds_read_b128 v[234:237], v234
	v_lshl_add_u32 v240, v242, 2, s24
	ds_read_b32 v243, v240 offset:1024
	v_bitop3_b32 v239, v239, v201, 24 bitop3:0x6c
	v_lshl_add_u32 v238, v239, 1, v238
	s_waitcnt lgkmcnt(1)
	v_lshlrev_b32_e32 v240, 16, v234
	v_and_b32_e32 v234, 0xffff0000, v234
	s_waitcnt lgkmcnt(0)
	v_mul_f32_e32 v234, v243, v234
	v_mul_f32_e32 v245, v243, v240
	v_rndne_f32_e32 v234, v234
	v_rndne_f32_e32 v245, v245
	v_cvt_i32_f32_e32 v234, v234
	v_cvt_i32_f32_e32 v245, v245
	ds_read_b128 v[238:241], v238
	s_addk_i32 s15, 0x400
	v_lshlrev_b32_e32 v234, 8, v234
	v_perm_b32 v234, v234, v245, s31
	v_lshlrev_b32_e32 v245, 16, v235
	v_and_b32_e32 v235, 0xffff0000, v235
	v_mul_f32_e32 v245, v243, v245
	v_mul_f32_e32 v235, v243, v235
	v_rndne_f32_e32 v245, v245
	v_rndne_f32_e32 v235, v235
	v_cvt_i32_f32_sdwa v245, v245 dst_sel:WORD_1 dst_unused:UNUSED_PAD src0_sel:DWORD
	v_cvt_i32_f32_e32 v235, v235
	s_cmpk_lg_i32 s15, 0x1000
	v_perm_b32 v235, v235, v245, s33
	v_or_b32_e32 v234, v235, v234
	v_lshlrev_b32_e32 v235, 16, v236
	v_and_b32_e32 v236, 0xffff0000, v236
	v_mul_f32_e32 v236, v243, v236
	v_mul_f32_e32 v235, v243, v235
	v_rndne_f32_e32 v236, v236
	v_rndne_f32_e32 v235, v235
	v_cvt_i32_f32_e32 v236, v236
	v_cvt_i32_f32_e32 v235, v235
	v_lshlrev_b32_e32 v236, 8, v236
	v_perm_b32 v235, v236, v235, s31
	v_lshlrev_b32_e32 v236, 16, v237
	v_and_b32_e32 v237, 0xffff0000, v237
	v_mul_f32_e32 v236, v243, v236
	v_mul_f32_e32 v237, v243, v237
	v_rndne_f32_e32 v236, v236
	v_rndne_f32_e32 v237, v237
	v_cvt_i32_f32_sdwa v236, v236 dst_sel:WORD_1 dst_unused:UNUSED_PAD src0_sel:DWORD
	v_cvt_i32_f32_e32 v237, v237
	v_perm_b32 v236, v237, v236, s33
	s_waitcnt lgkmcnt(0)
	v_and_b32_e32 v237, 0xffff0000, v238
	v_or_b32_e32 v235, v236, v235
	v_lshlrev_b32_e32 v236, 16, v238
	v_mul_f32_e32 v237, v243, v237
	v_mul_f32_e32 v236, v243, v236
	v_rndne_f32_e32 v237, v237
	v_rndne_f32_e32 v236, v236
	v_cvt_i32_f32_e32 v237, v237
	v_cvt_i32_f32_e32 v236, v236
	v_and_b32_e32 v238, 0xffff0000, v239
	v_mul_f32_e32 v238, v243, v238
	v_lshlrev_b32_e32 v237, 8, v237
	v_perm_b32 v236, v237, v236, s31
	v_lshlrev_b32_e32 v237, 16, v239
	v_mul_f32_e32 v237, v243, v237
	v_rndne_f32_e32 v237, v237
	v_rndne_f32_e32 v238, v238
	v_cvt_i32_f32_sdwa v237, v237 dst_sel:WORD_1 dst_unused:UNUSED_PAD src0_sel:DWORD
	v_cvt_i32_f32_e32 v238, v238
	v_and_b32_e32 v239, 0xffff0000, v241
	v_mul_f32_e32 v239, v243, v239
	v_rndne_f32_e32 v239, v239
	v_perm_b32 v237, v238, v237, s33
	v_and_b32_e32 v238, 0xffff0000, v240
	v_or_b32_e32 v236, v237, v236
	v_lshlrev_b32_e32 v237, 16, v240
	v_mul_f32_e32 v238, v243, v238
	v_mul_f32_e32 v237, v243, v237
	v_rndne_f32_e32 v238, v238
	v_rndne_f32_e32 v237, v237
	v_cvt_i32_f32_e32 v238, v238
	v_cvt_i32_f32_e32 v237, v237
	v_cvt_i32_f32_e32 v239, v239
	v_lshlrev_b32_e32 v238, 8, v238
	v_perm_b32 v237, v238, v237, s31
	v_lshlrev_b32_e32 v238, 16, v241
	v_mul_f32_e32 v238, v243, v238
	v_rndne_f32_e32 v238, v238
	v_cvt_i32_f32_sdwa v238, v238 dst_sel:WORD_1 dst_unused:UNUSED_PAD src0_sel:DWORD
	v_ashrrev_i32_e32 v243, 31, v242
	v_perm_b32 v238, v239, v238, s33
	v_or_b32_e32 v237, v238, v237
	v_lshl_add_u64 v[238:239], v[242:243], 0, s[8:9]
	v_lshlrev_b64 v[238:239], 11, v[238:239]
	v_lshl_add_u64 v[238:239], v[198:199], 0, v[238:239]
	global_store_dwordx4 v[238:239], v[234:237], off nt sc1
	s_nop 1
	v_add_u32_e32 v234, 0x200, v244
	v_ashrrev_i32_e32 v242, 7, v234
	v_mul_lo_u32 v235, v242, s25
	v_lshrrev_b32_e32 v239, 7, v234
	v_add_u32_e32 v238, 0, v235
	v_bitop3_b32 v234, v239, v194, 24 bitop3:0x6c
	v_lshl_add_u32 v234, v234, 1, v238
	ds_read_b128 v[234:237], v234
	v_lshl_add_u32 v240, v242, 2, s24
	ds_read_b32 v243, v240 offset:1024
	v_bitop3_b32 v239, v239, v201, 24 bitop3:0x6c
	v_lshl_add_u32 v238, v239, 1, v238
	s_waitcnt lgkmcnt(1)
; #define GAS __attribute__((address_space(1)))
; #define LAS __attribute__((address_space(3)))
; __device__ __forceinline__ void do_slabs_impl(LAS unsigned char* lds, unsigned char* ws, const float* w_up, const float* w_dn, const float* w_in, int vcu, int G, int wave, int j0, int j1) {
;     ...
;             for (int i = 0; i < 8; ++i) { const int q = tid + NTHR * i, n = q >> 7, kc = q & 127; const float inv = red[256 + n];
;                 const int sx_ = ((n >> 3) & 3) << 3;
;                 const v4u a = *(const LAS v4u*)(slab + n * PITCH + ((kc * 16) ^ sx_)), b = *(const LAS v4u*)(slab + n * PITCH + ((kc * 16 + 8) ^ sx_));
;                 const unsigned src[8] = {a.x, a.y, a.z, a.w, b.x, b.y, b.z, b.w}; unsigned o[4];
;                 if (done.fp8) {
; #pragma unroll
;                     for (int d = 0; d < 4; ++d) { int w = __builtin_amdgcn_cvt_pk_fp8_f32(bf_lo(src[2 * d]) * inv, bf_hi(src[2 * d]) * inv, 0, false);
;                         w = __builtin_amdgcn_cvt_pk_fp8_f32(bf_lo(src[2 * d + 1]) * inv, bf_hi(src[2 * d + 1]) * inv, w, true); o[d] = (unsigned)w; }
;                 } else {
; #pragma unroll
;                 for (int d = 0; d < 4; ++d) { unsigned w = 0u;
; #pragma unroll
;                     for (int h2 = 0; h2 < 2; ++h2) { const unsigned u2 = src[2 * d + h2]; const int q0 = (int)__builtin_rintf(bf_lo(u2) * inv), q1 = (int)__builtin_rintf(bf_hi(u2) * inv);
;                         w |= ((unsigned)(q0 & 0xff) << (16 * h2)) | ((unsigned)(q1 & 0xff) << (16 * h2 + 8)); }
;                     o[d] = w; }
;                 }
;                 __builtin_nontemporal_store((v4u){o[0], o[1], o[2], o[3]}, (GAS v4u*)(done.WQ + ((size_t)done.e * done.NS + done.n0 + n) * D + kc * 16)); }
	v_lshlrev_b32_e32 v240, 16, v234
	v_and_b32_e32 v234, 0xffff0000, v234
	s_waitcnt lgkmcnt(0)
	v_mul_f32_e32 v234, v243, v234
	v_mul_f32_e32 v244, v243, v240
	v_rndne_f32_e32 v234, v234
	v_rndne_f32_e32 v244, v244
	v_cvt_i32_f32_e32 v234, v234
	v_cvt_i32_f32_e32 v244, v244
	ds_read_b128 v[238:241], v238
	v_lshlrev_b32_e32 v234, 8, v234
	v_perm_b32 v234, v234, v244, s31
	v_lshlrev_b32_e32 v244, 16, v235
	v_and_b32_e32 v235, 0xffff0000, v235
	v_mul_f32_e32 v244, v243, v244
	v_mul_f32_e32 v235, v243, v235
	v_rndne_f32_e32 v244, v244
	v_rndne_f32_e32 v235, v235
	v_cvt_i32_f32_sdwa v244, v244 dst_sel:WORD_1 dst_unused:UNUSED_PAD src0_sel:DWORD
	v_cvt_i32_f32_e32 v235, v235
	v_perm_b32 v235, v235, v244, s33
	v_or_b32_e32 v234, v235, v234
	v_lshlrev_b32_e32 v235, 16, v236
	v_and_b32_e32 v236, 0xffff0000, v236
	v_mul_f32_e32 v236, v243, v236
	v_mul_f32_e32 v235, v243, v235
	v_rndne_f32_e32 v236, v236
	v_rndne_f32_e32 v235, v235
	v_cvt_i32_f32_e32 v236, v236
	v_cvt_i32_f32_e32 v235, v235
	v_lshlrev_b32_e32 v236, 8, v236
	v_perm_b32 v235, v236, v235, s31
	v_lshlrev_b32_e32 v236, 16, v237
	v_and_b32_e32 v237, 0xffff0000, v237
	v_mul_f32_e32 v236, v243, v236
	v_mul_f32_e32 v237, v243, v237
	v_rndne_f32_e32 v236, v236
	v_rndne_f32_e32 v237, v237
	v_cvt_i32_f32_sdwa v236, v236 dst_sel:WORD_1 dst_unused:UNUSED_PAD src0_sel:DWORD
	v_cvt_i32_f32_e32 v237, v237
	v_perm_b32 v236, v237, v236, s33
	s_waitcnt lgkmcnt(0)
	v_and_b32_e32 v237, 0xffff0000, v238
	v_or_b32_e32 v235, v236, v235
	v_lshlrev_b32_e32 v236, 16, v238
	v_mul_f32_e32 v237, v243, v237
	v_mul_f32_e32 v236, v243, v236
	v_rndne_f32_e32 v237, v237
	v_rndne_f32_e32 v236, v236
	v_cvt_i32_f32_e32 v237, v237
	v_cvt_i32_f32_e32 v236, v236
	v_and_b32_e32 v238, 0xffff0000, v239
	v_mul_f32_e32 v238, v243, v238
	v_lshlrev_b32_e32 v237, 8, v237
	v_perm_b32 v236, v237, v236, s31
	v_lshlrev_b32_e32 v237, 16, v239
	v_mul_f32_e32 v237, v243, v237
	v_rndne_f32_e32 v237, v237
	v_rndne_f32_e32 v238, v238
	v_cvt_i32_f32_sdwa v237, v237 dst_sel:WORD_1 dst_unused:UNUSED_PAD src0_sel:DWORD
	v_cvt_i32_f32_e32 v238, v238
	v_and_b32_e32 v239, 0xffff0000, v241
	v_mul_f32_e32 v239, v243, v239
	v_rndne_f32_e32 v239, v239
	v_perm_b32 v237, v238, v237, s33
	v_and_b32_e32 v238, 0xffff0000, v240
	v_or_b32_e32 v236, v237, v236
	v_lshlrev_b32_e32 v237, 16, v240
	v_mul_f32_e32 v238, v243, v238
	v_mul_f32_e32 v237, v243, v237
	v_rndne_f32_e32 v238, v238
	v_rndne_f32_e32 v237, v237
	v_cvt_i32_f32_e32 v238, v238
	v_cvt_i32_f32_e32 v237, v237
	v_cvt_i32_f32_e32 v239, v239
	v_lshlrev_b32_e32 v238, 8, v238
	v_perm_b32 v237, v238, v237, s31
	v_lshlrev_b32_e32 v238, 16, v241
	v_mul_f32_e32 v238, v243, v238
	v_rndne_f32_e32 v238, v238
	v_cvt_i32_f32_sdwa v238, v238 dst_sel:WORD_1 dst_unused:UNUSED_PAD src0_sel:DWORD
	v_ashrrev_i32_e32 v243, 31, v242
	v_perm_b32 v238, v239, v238, s33
	v_or_b32_e32 v237, v238, v237
	v_lshl_add_u64 v[238:239], v[242:243], 0, s[8:9]
	v_lshlrev_b64 v[238:239], 11, v[238:239]
	v_lshl_add_u64 v[238:239], v[198:199], 0, v[238:239]
	global_store_dwordx4 v[238:239], v[234:237], off nt sc1
	s_cbranch_scc1 .LBB0_56
	s_branch .LBB0_43

; #define GAS __attribute__((address_space(1)))
; #define LAS __attribute__((address_space(3)))
; __device__ __forceinline__ void do_slabs_impl(LAS unsigned char* lds, unsigned char* ws, const float* w_up, const float* w_dn, const float* w_in, int vcu, int G, int wave, int j0, int j1) {
;     ...
;             for (int i = 0; i < 8; ++i) { const int q = tid + NTHR * i, n = q >> 7, kc = q & 127; const float inv = red[256 + n];
;                 const int sx_ = ((n >> 3) & 3) << 3;
;                 const v4u a = *(const LAS v4u*)(slab + n * PITCH + ((kc * 16) ^ sx_)), b = *(const LAS v4u*)(slab + n * PITCH + ((kc * 16 + 8) ^ sx_));
;                 const unsigned src[8] = {a.x, a.y, a.z, a.w, b.x, b.y, b.z, b.w}; unsigned o[4];
;                 if (done.fp8) {
; #pragma unroll
;                     for (int d = 0; d < 4; ++d) { int w = __builtin_amdgcn_cvt_pk_fp8_f32(bf_lo(src[2 * d]) * inv, bf_hi(src[2 * d]) * inv, 0, false);
;                         w = __builtin_amdgcn_cvt_pk_fp8_f32(bf_lo(src[2 * d + 1]) * inv, bf_hi(src[2 * d + 1]) * inv, w, true); o[d] = (unsigned)w; }
;                 } else {
; #pragma unroll
;                 for (int d = 0; d < 4; ++d) { unsigned w = 0u;
; #pragma unroll
;                     for (int h2 = 0; h2 < 2; ++h2) { const unsigned u2 = src[2 * d + h2]; const int q0 = (int)__builtin_rintf(bf_lo(u2) * inv), q1 = (int)__builtin_rintf(bf_hi(u2) * inv);
;                         w |= ((unsigned)(q0 & 0xff) << (16 * h2)) | ((unsigned)(q1 & 0xff) << (16 * h2 + 8)); }
;                     o[d] = w; }
;                 }
;                 __builtin_nontemporal_store((v4u){o[0], o[1], o[2], o[3]}, (GAS v4u*)(done.WQ + ((size_t)done.e * done.NS + done.n0 + n) * D + kc * 16)); }
.LBB0_141:
	v_ashrrev_i32_e32 v139, 31, v138
	v_lshl_add_u64 v[138:139], s[34:35], 0, v[138:139]
	v_lshlrev_b64 v[138:139], 11, v[138:139]
	s_addk_i32 s24, 0x400
	v_lshl_add_u64 v[138:139], v[136:137], 0, v[138:139]
	s_cmpk_lg_i32 s24, 0x1000
	global_store_dwordx4 v[138:139], v[128:131], off nt sc1
	s_cbranch_scc0 .LBB0_120

; #define GAS __attribute__((address_space(1)))
; #define LAS __attribute__((address_space(3)))
; __device__ __forceinline__ void do_slabs_impl(LAS unsigned char* lds, unsigned char* ws, const float* w_up, const float* w_dn, const float* w_in, int vcu, int G, int wave, int j0, int j1) {
;     ...
;             for (int i = 0; i < 8; ++i) { const int q = tid + NTHR * i, n = q >> 7, kc = q & 127; const float inv = red[256 + n];
;                 const int sx_ = ((n >> 3) & 3) << 3;
;                 const v4u a = *(const LAS v4u*)(slab + n * PITCH + ((kc * 16) ^ sx_)), b = *(const LAS v4u*)(slab + n * PITCH + ((kc * 16 + 8) ^ sx_));
;                 const unsigned src[8] = {a.x, a.y, a.z, a.w, b.x, b.y, b.z, b.w}; unsigned o[4];
;                 if (done.fp8) {
; #pragma unroll
;                     for (int d = 0; d < 4; ++d) { int w = __builtin_amdgcn_cvt_pk_fp8_f32(bf_lo(src[2 * d]) * inv, bf_hi(src[2 * d]) * inv, 0, false);
;                         w = __builtin_amdgcn_cvt_pk_fp8_f32(bf_lo(src[2 * d + 1]) * inv, bf_hi(src[2 * d + 1]) * inv, w, true); o[d] = (unsigned)w; }
;                 } else {
; #pragma unroll
;                 for (int d = 0; d < 4; ++d) { unsigned w = 0u;
; #pragma unroll
;                     for (int h2 = 0; h2 < 2; ++h2) { const unsigned u2 = src[2 * d + h2]; const int q0 = (int)__builtin_rintf(bf_lo(u2) * inv), q1 = (int)__builtin_rintf(bf_hi(u2) * inv);
;                         w |= ((unsigned)(q0 & 0xff) << (16 * h2)) | ((unsigned)(q1 & 0xff) << (16 * h2 + 8)); }
;                     o[d] = w; }
;                 }
;                 __builtin_nontemporal_store((v4u){o[0], o[1], o[2], o[3]}, (GAS v4u*)(done.WQ + ((size_t)done.e * done.NS + done.n0 + n) * D + kc * 16)); }
.LBB0_145:
	v_ashrrev_i32_e32 v139, 31, v138
	v_lshl_add_u64 v[138:139], s[34:35], 0, v[138:139]
	v_lshlrev_b64 v[138:139], 11, v[138:139]
	v_lshl_add_u64 v[184:185], v[136:137], 0, v[138:139]
	v_add_u32_e32 v139, 0x200, v180
	v_ashrrev_i32_e32 v138, 7, v139
	v_lshrrev_b32_e32 v186, 7, v139
	v_mul_lo_u32 v139, v138, s3
	v_add_u32_e32 v187, 0, v139
	v_bitop3_b32 v139, v186, v134, 24 bitop3:0x6c
	v_lshl_add_u32 v180, v138, 2, s2
	v_lshl_add_u32 v181, v139, 1, v187
	ds_read_b32 v139, v180 offset:1024
	ds_read_b128 v[180:183], v181
	global_store_dwordx4 v[184:185], v[128:131], off nt sc1
	s_and_b64 vcc, exec, s[8:9]
	s_waitcnt lgkmcnt(0)
	v_lshlrev_b32_e32 v184, 16, v180
	v_bitop3_b32 v128, v186, v143, 24 bitop3:0x6c
	v_lshl_add_u32 v128, v128, 1, v187
	ds_read_b128 v[128:131], v128
	v_and_b32_e32 v180, 0xffff0000, v180
	v_mul_f32_e32 v194, v139, v184
	v_mul_f32_e32 v195, v139, v180
	v_lshlrev_b32_e32 v193, 16, v181
	v_and_b32_e32 v192, 0xffff0000, v181
	v_lshlrev_b32_e32 v191, 16, v182
	v_and_b32_e32 v190, 0xffff0000, v182
	v_lshlrev_b32_e32 v189, 16, v183
	v_and_b32_e32 v188, 0xffff0000, v183
	s_waitcnt lgkmcnt(0)
	v_lshlrev_b32_e32 v187, 16, v128
	v_and_b32_e32 v186, 0xffff0000, v128
	v_lshlrev_b32_e32 v185, 16, v129
	v_and_b32_e32 v184, 0xffff0000, v129
	v_lshlrev_b32_e32 v183, 16, v130
	v_and_b32_e32 v182, 0xffff0000, v130
	v_lshlrev_b32_e32 v181, 16, v131
	v_and_b32_e32 v180, 0xffff0000, v131
	s_cbranch_vccnz .LBB0_148
	v_mov_b32_e32 v128, 0
	v_cvt_pk_fp8_f32 v128, v194, v195
	v_mul_f32_e32 v196, v139, v191
	v_mul_f32_e32 v197, v139, v190
	v_mov_b32_e32 v129, 0
	v_cvt_pk_fp8_f32 v129, v196, v197
	v_mul_f32_e32 v130, v139, v193
	v_mul_f32_e32 v131, v139, v192
	v_cvt_pk_fp8_f32 v128, v130, v131 op_sel:[0,0,1]
	v_mul_f32_e32 v130, v139, v189
	v_mul_f32_e32 v131, v139, v188
	v_cvt_pk_fp8_f32 v129, v130, v131 op_sel:[0,0,1]
	v_mul_f32_e32 v131, v139, v187
	v_mul_f32_e32 v196, v139, v186
	v_mov_b32_e32 v130, 0
	v_cvt_pk_fp8_f32 v130, v131, v196
	v_mul_f32_e32 v198, v139, v183
	v_mul_f32_e32 v199, v139, v182
	v_mov_b32_e32 v131, 0
	v_cvt_pk_fp8_f32 v131, v198, v199
	v_mul_f32_e32 v196, v139, v185
	v_mul_f32_e32 v197, v139, v184
	v_cvt_pk_fp8_f32 v130, v196, v197 op_sel:[0,0,1]
	v_mul_f32_e32 v196, v139, v181
	v_mul_f32_e32 v197, v139, v180
	v_cvt_pk_fp8_f32 v131, v196, v197 op_sel:[0,0,1]
	s_cbranch_execnz .LBB0_141
	s_branch .LBB0_140

; #define GAS __attribute__((address_space(1)))
; __device__ __forceinline__ v4u pack8(const f32x4 a, const f32x4 b) { v4u w; w.x = cvt_pk_bf16(a[0], a[1]); w.y = cvt_pk_bf16(a[2], a[3]); w.z = cvt_pk_bf16(b[0], b[1]); w.w = cvt_pk_bf16(b[2], b[3]); return w; }
; __device__ __forceinline__ float fexp(float x) { return __builtin_amdgcn_exp2f(x * 1.4426950408889634f); }
; #define EPI_LOOP_AM for (int ai = 0; ai < 2; ++ai) _Pragma("unroll") for (int m = 0; m < 4; ++m)
;     __device__ __forceinline__ void operator()(AccI& acci, const Unit& u, LAS unsigned char*, int wr, int wc, int fr, int fq) const {
;     ...
;         f32x4 swc[2][2];
; #pragma unroll
;         for (int bj = 0; bj < 2; ++bj)
; #pragma unroll
;             for (int n = 0; n < 2; ++n) swc[bj][n] = *(const GAS f32x4*)(swin + u.p2 + 128 * bj + c0 + 4 * n);
;     ...
;         } else {
; #pragma unroll
;             EPI_LOOP_AM {
;                 const int r = 128 * ai + 64 * wr + 16 * m + fr, tok = pm * 256 + r; const float sxr = sx0[tok];
; #pragma unroll
;                 for (int bj = 0; bj < 2; ++bj) { f32x4 v[2];
; #pragma unroll
;                     for (int n = 0; n < 2; ++n)
; #pragma unroll
;                         for (int j = 0; j < 4; ++j) { const float g = ACCF(ai, bj, m, n, j); v[n][j] = g * __builtin_amdgcn_rcpf(1.f + fexp(-g)); }
;                     *(GAS v4u*)(gs + (size_t)tok * RW + (pn - 8) * 256 + bj * 128 + c0) = pack8(v[0], v[1]); }
.LBB0_182:
	s_ashr_i32 s73, s72, 31
	v_mov_b32_e32 v154, v161
	s_waitcnt vmcnt(0)
	v_mov_b32_e32 v32, v162
	s_lshl_b64 s[72:73], s[72:73], 2
	s_add_u32 s72, s36, s72
	v_lshl_add_u32 v150, v32, 3, s27
	s_addc_u32 s73, s37, s73
	v_ashrrev_i32_e32 v151, 31, v150
	v_lshl_add_u64 v[44:45], v[150:151], 2, s[72:73]
	global_load_dwordx4 v[32:35], v[44:45], off offset:16
	global_load_dwordx4 v[40:43], v[44:45], off
	global_load_dwordx4 v[36:39], v[44:45], off offset:528
	s_nop 0
	global_load_dwordx4 v[44:47], v[44:45], off offset:512
	s_cmp_lt_i32 s24, 8
	s_mov_b64 s[72:73], -1
	s_cbranch_scc1 .LBB0_184
	s_lshl_b32 s0, s4, 8
	s_add_i32 s0, s0, s26
	v_add_u32_e32 v144, s0, v154
	v_ashrrev_i32_e32 v145, 31, v144
	v_lshl_add_u64 v[146:147], v[144:145], 2, s[34:35]
	global_load_dword v148, v[146:147], off
	v_lshlrev_b64 v[146:147], 11, v[144:145]
	v_cvt_f32_i32_e32 v145, v140
	s_lshl_b32 s0, s24, 8
	s_add_i32 s6, s0, 0xfffff800
	v_lshl_add_u64 v[146:147], s[42:43], 0, v[146:147]
	s_lshl_b64 s[72:73], s[6:7], 1
	s_waitcnt vmcnt(0)
	v_mul_f32_e32 v152, v40, v148
	v_mul_f32_e32 v145, v152, v145
	v_mul_f32_e32 v152, 0xbfb8aa3b, v145
	v_exp_f32_e32 v152, v152
	v_mul_f32_e32 v153, v41, v148
	v_mul_f32_e32 v155, v42, v148
	v_mul_f32_e32 v156, v43, v148
	v_add_f32_e32 v152, 1.0, v152
	v_rcp_f32_e32 v152, v152
	v_mul_f32_e32 v157, v32, v148
	v_mul_f32_e32 v145, v145, v152
	v_cvt_f32_i32_e32 v152, v141
	v_mul_f32_e32 v152, v153, v152
	v_mul_f32_e32 v153, 0xbfb8aa3b, v152
	v_exp_f32_e32 v153, v153
	s_nop 0
	v_add_f32_e32 v153, 1.0, v153
	v_rcp_f32_e32 v153, v153
	s_nop 0
	v_mul_f32_e32 v152, v152, v153
	v_cvt_f32_i32_e32 v153, v142
	v_mul_f32_e32 v153, v155, v153
	v_mul_f32_e32 v155, 0xbfb8aa3b, v153
	v_exp_f32_e32 v155, v155
	s_nop 0
	v_add_f32_e32 v155, 1.0, v155
	v_rcp_f32_e32 v155, v155
	s_nop 0
	v_mul_f32_e32 v153, v153, v155
	v_cvt_f32_i32_e32 v155, v143
	v_mul_f32_e32 v155, v156, v155
	v_mul_f32_e32 v156, 0xbfb8aa3b, v155
	v_exp_f32_e32 v156, v156
	s_nop 0
	v_add_f32_e32 v156, 1.0, v156
	v_rcp_f32_e32 v156, v156
	s_nop 0
	v_mul_f32_e32 v155, v155, v156
	v_cvt_f32_i32_e32 v156, v132
	v_mul_f32_e32 v156, v157, v156
	v_mul_f32_e32 v157, 0xbfb8aa3b, v156
	v_exp_f32_e32 v157, v157
	s_nop 0
	v_add_f32_e32 v157, 1.0, v157
	v_rcp_f32_e32 v157, v157
	s_nop 0
	v_mul_f32_e32 v158, v156, v157
	v_cvt_f32_i32_e32 v156, v133
	v_mul_f32_e32 v157, v33, v148
	v_mul_f32_e32 v156, v157, v156
	v_mul_f32_e32 v157, 0xbfb8aa3b, v156
	v_exp_f32_e32 v157, v157
	s_nop 0
	v_add_f32_e32 v157, 1.0, v157
	v_rcp_f32_e32 v157, v157
	s_nop 0
	v_mul_f32_e32 v159, v156, v157
	v_cvt_f32_i32_e32 v156, v134
	v_mul_f32_e32 v157, v34, v148
	v_mul_f32_e32 v156, v157, v156
	v_mul_f32_e32 v157, 0xbfb8aa3b, v156
	v_exp_f32_e32 v157, v157
	s_nop 0
	v_add_f32_e32 v157, 1.0, v157
	v_rcp_f32_e32 v157, v157
	s_nop 0
	v_mul_f32_e32 v165, v156, v157
	v_cvt_f32_i32_e32 v156, v135
	v_mul_f32_e32 v157, v35, v148
	v_mul_f32_e32 v156, v157, v156
	v_mul_f32_e32 v157, 0xbfb8aa3b, v156
	v_exp_f32_e32 v157, v157
	s_nop 0
	v_add_f32_e32 v157, 1.0, v157
	v_rcp_f32_e32 v157, v157
	s_nop 0
	v_mul_f32_e32 v166, v156, v157
	v_cvt_pk_bf16_f32 v156, v145, v152
	v_cvt_f32_i32_e32 v145, v136
	v_cvt_pk_bf16_f32 v157, v153, v155
	v_mul_f32_e32 v155, v44, v148
	v_lshl_add_u64 v[152:153], v[146:147], 0, s[72:73]
	v_mul_f32_e32 v145, v155, v145
	v_mul_f32_e32 v155, 0xbfb8aa3b, v145
	v_exp_f32_e32 v155, v155
	v_lshlrev_b64 v[146:147], 1, v[150:151]
	v_lshl_add_u64 v[152:153], v[152:153], 0, v[146:147]
	v_cvt_pk_bf16_f32 v158, v158, v159
	v_add_f32_e32 v155, 1.0, v155
	v_rcp_f32_e32 v155, v155
	v_cvt_pk_bf16_f32 v159, v165, v166
	global_store_dwordx4 v[152:153], v[156:159], off sc1
	v_mul_f32_e32 v165, v37, v148
	v_mul_f32_e32 v145, v145, v155
	v_cvt_f32_i32_e32 v155, v137
	v_mul_f32_e32 v156, v45, v148
	v_mul_f32_e32 v157, v46, v148
	v_mul_f32_e32 v158, v47, v148
	v_mul_f32_e32 v155, v156, v155
	v_mul_f32_e32 v156, 0xbfb8aa3b, v155
	v_exp_f32_e32 v156, v156
	v_mul_f32_e32 v159, v36, v148
	v_mul_f32_e32 v166, v38, v148
	v_mul_f32_e32 v148, v39, v148
	v_add_f32_e32 v156, 1.0, v156
	v_rcp_f32_e32 v156, v156
	s_nop 0
	v_mul_f32_e32 v155, v155, v156
	v_cvt_f32_i32_e32 v156, v138
	v_mul_f32_e32 v156, v157, v156
	v_mul_f32_e32 v157, 0xbfb8aa3b, v156
	v_exp_f32_e32 v157, v157
	s_nop 0
	v_add_f32_e32 v157, 1.0, v157
	v_rcp_f32_e32 v157, v157
	s_nop 0
	v_mul_f32_e32 v157, v156, v157
	v_cvt_f32_i32_e32 v156, v139
	v_mul_f32_e32 v156, v158, v156
	v_mul_f32_e32 v158, 0xbfb8aa3b, v156
	v_exp_f32_e32 v158, v158
	s_nop 0
	v_add_f32_e32 v158, 1.0, v158
	v_rcp_f32_e32 v158, v158
	s_nop 0
	v_mul_f32_e32 v158, v156, v158
	v_cvt_f32_i32_e32 v156, v128
	v_mul_f32_e32 v156, v159, v156
	v_mul_f32_e32 v159, 0xbfb8aa3b, v156
	v_exp_f32_e32 v159, v159
	s_nop 0
	v_add_f32_e32 v159, 1.0, v159
	v_rcp_f32_e32 v159, v159
	s_nop 0
	v_mul_f32_e32 v159, v156, v159
	v_cvt_f32_i32_e32 v156, v129
	v_mul_f32_e32 v156, v165, v156
	v_mul_f32_e32 v165, 0xbfb8aa3b, v156
	v_exp_f32_e32 v165, v165
	s_nop 0
	v_add_f32_e32 v165, 1.0, v165
	v_rcp_f32_e32 v165, v165
	s_nop 0
	v_mul_f32_e32 v165, v156, v165
	v_cvt_f32_i32_e32 v156, v130
	v_mul_f32_e32 v156, v166, v156
	v_mul_f32_e32 v166, 0xbfb8aa3b, v156
	v_exp_f32_e32 v166, v166
	s_nop 0
	v_add_f32_e32 v166, 1.0, v166
	v_rcp_f32_e32 v166, v166
	s_nop 0
	v_mul_f32_e32 v166, v156, v166
	v_cvt_f32_i32_e32 v156, v131
	v_mul_f32_e32 v148, v148, v156
	v_mul_f32_e32 v156, 0xbfb8aa3b, v148
	v_exp_f32_e32 v156, v156
	s_nop 0
	v_add_f32_e32 v156, 1.0, v156
	v_rcp_f32_e32 v156, v156
	s_nop 0
	v_mul_f32_e32 v148, v148, v156
	v_cvt_pk_bf16_f32 v156, v145, v155
	v_cvt_pk_bf16_f32 v157, v157, v158
	v_cvt_pk_bf16_f32 v158, v159, v165
	v_cvt_pk_bf16_f32 v159, v166, v148
	global_store_dwordx4 v[152:153], v[156:159], off offset:256 sc1
	v_add_u32_e32 v152, 16, v144
	v_ashrrev_i32_e32 v153, 31, v152
	v_lshl_add_u64 v[156:157], v[152:153], 2, s[34:35]
	global_load_dword v145, v[156:157], off
	v_cvt_f32_i32_e32 v148, v124
	v_lshlrev_b64 v[152:153], 11, v[152:153]
	v_lshl_add_u64 v[152:153], s[42:43], 0, v[152:153]
	v_lshl_add_u64 v[152:153], v[152:153], 0, s[72:73]
	v_lshl_add_u64 v[152:153], v[152:153], 0, v[146:147]
	s_waitcnt vmcnt(0)
; #define GAS __attribute__((address_space(1)))
; __device__ __forceinline__ v4u pack8(const f32x4 a, const f32x4 b) { v4u w; w.x = cvt_pk_bf16(a[0], a[1]); w.y = cvt_pk_bf16(a[2], a[3]); w.z = cvt_pk_bf16(b[0], b[1]); w.w = cvt_pk_bf16(b[2], b[3]); return w; }
; __device__ __forceinline__ float fexp(float x) { return __builtin_amdgcn_exp2f(x * 1.4426950408889634f); }
; #define EPI_LOOP_AM for (int ai = 0; ai < 2; ++ai) _Pragma("unroll") for (int m = 0; m < 4; ++m)
;     __device__ __forceinline__ void operator()(AccI& acci, const Unit& u, LAS unsigned char*, int wr, int wc, int fr, int fq) const {
;     ...
;             EPI_LOOP_AM {
;                 const int r = 128 * ai + 64 * wr + 16 * m + fr, tok = pm * 256 + r; const float sxr = sx0[tok];
; #pragma unroll
;                 for (int bj = 0; bj < 2; ++bj) { f32x4 v[2];
; #pragma unroll
;                     for (int n = 0; n < 2; ++n)
; #pragma unroll
;                         for (int j = 0; j < 4; ++j) { const float g = ACCF(ai, bj, m, n, j); v[n][j] = g * __builtin_amdgcn_rcpf(1.f + fexp(-g)); }
;                     *(GAS v4u*)(gs + (size_t)tok * RW + (pn - 8) * 256 + bj * 128 + c0) = pack8(v[0], v[1]); }
	v_mul_f32_e32 v155, v40, v145
	v_mul_f32_e32 v148, v155, v148
	v_mul_f32_e32 v155, 0xbfb8aa3b, v148
	v_exp_f32_e32 v155, v155
	v_mul_f32_e32 v156, v41, v145
	v_mul_f32_e32 v157, v42, v145
	v_mul_f32_e32 v158, v43, v145
	v_add_f32_e32 v155, 1.0, v155
	v_rcp_f32_e32 v155, v155
	v_mul_f32_e32 v159, v32, v145
	v_mul_f32_e32 v165, v33, v145
	v_mul_f32_e32 v166, v34, v145
	v_mul_f32_e32 v148, v148, v155
	v_cvt_f32_i32_e32 v155, v125
	v_mul_f32_e32 v167, v35, v145
	v_mul_f32_e32 v155, v156, v155
	v_mul_f32_e32 v156, 0xbfb8aa3b, v155
	v_exp_f32_e32 v156, v156
	s_nop 0
	v_add_f32_e32 v156, 1.0, v156
	v_rcp_f32_e32 v156, v156
	s_nop 0
	v_mul_f32_e32 v155, v155, v156
	v_cvt_f32_i32_e32 v156, v126
	v_mul_f32_e32 v156, v157, v156
	v_mul_f32_e32 v157, 0xbfb8aa3b, v156
	v_exp_f32_e32 v157, v157
	s_nop 0
	v_add_f32_e32 v157, 1.0, v157
	v_rcp_f32_e32 v157, v157
	s_nop 0
	v_mul_f32_e32 v157, v156, v157
	v_cvt_f32_i32_e32 v156, v127
	v_mul_f32_e32 v156, v158, v156
	v_mul_f32_e32 v158, 0xbfb8aa3b, v156
	v_exp_f32_e32 v158, v158
	s_nop 0
	v_add_f32_e32 v158, 1.0, v158
	v_rcp_f32_e32 v158, v158
	s_nop 0
	v_mul_f32_e32 v158, v156, v158
	v_cvt_f32_i32_e32 v156, v116
	v_mul_f32_e32 v156, v159, v156
	v_mul_f32_e32 v159, 0xbfb8aa3b, v156
	v_exp_f32_e32 v159, v159
	s_nop 0
	v_add_f32_e32 v159, 1.0, v159
	v_rcp_f32_e32 v159, v159
	s_nop 0
	v_mul_f32_e32 v159, v156, v159
	v_cvt_f32_i32_e32 v156, v117
	v_mul_f32_e32 v156, v165, v156
	v_mul_f32_e32 v165, 0xbfb8aa3b, v156
	v_exp_f32_e32 v165, v165
	s_nop 0
	v_add_f32_e32 v165, 1.0, v165
	v_rcp_f32_e32 v165, v165
	s_nop 0
	v_mul_f32_e32 v165, v156, v165
	v_cvt_f32_i32_e32 v156, v118
	v_mul_f32_e32 v156, v166, v156
	v_mul_f32_e32 v166, 0xbfb8aa3b, v156
	v_exp_f32_e32 v166, v166
	s_nop 0
	v_add_f32_e32 v166, 1.0, v166
	v_rcp_f32_e32 v166, v166
	s_nop 0
	v_mul_f32_e32 v166, v156, v166
	v_cvt_f32_i32_e32 v156, v119
	v_mul_f32_e32 v156, v167, v156
	v_mul_f32_e32 v167, 0xbfb8aa3b, v156
	v_exp_f32_e32 v167, v167
	s_nop 0
	v_add_f32_e32 v167, 1.0, v167
	v_rcp_f32_e32 v167, v167
	s_nop 0
	v_mul_f32_e32 v167, v156, v167
	v_cvt_pk_bf16_f32 v156, v148, v155
	v_cvt_f32_i32_e32 v148, v120
	v_mul_f32_e32 v155, v44, v145
	v_cvt_pk_bf16_f32 v157, v157, v158
	v_cvt_pk_bf16_f32 v158, v159, v165
	v_mul_f32_e32 v148, v155, v148
	v_mul_f32_e32 v155, 0xbfb8aa3b, v148
	v_exp_f32_e32 v155, v155
	v_cvt_pk_bf16_f32 v159, v166, v167
	global_store_dwordx4 v[152:153], v[156:159], off sc1
	v_mul_f32_e32 v165, v37, v145
	v_add_f32_e32 v155, 1.0, v155
	v_rcp_f32_e32 v155, v155
	v_mul_f32_e32 v156, v45, v145
	v_mul_f32_e32 v157, v46, v145
	v_mul_f32_e32 v158, v47, v145
	v_mul_f32_e32 v148, v148, v155
	v_cvt_f32_i32_e32 v155, v121
	v_mul_f32_e32 v159, v36, v145
	v_mul_f32_e32 v166, v38, v145
	v_mul_f32_e32 v145, v39, v145
	v_mul_f32_e32 v155, v156, v155
	v_mul_f32_e32 v156, 0xbfb8aa3b, v155
	v_exp_f32_e32 v156, v156
	s_nop 0
	v_add_f32_e32 v156, 1.0, v156
	v_rcp_f32_e32 v156, v156
	s_nop 0
	v_mul_f32_e32 v155, v155, v156
	v_cvt_f32_i32_e32 v156, v122
	v_mul_f32_e32 v156, v157, v156
	v_mul_f32_e32 v157, 0xbfb8aa3b, v156
	v_exp_f32_e32 v157, v157
	s_nop 0
	v_add_f32_e32 v157, 1.0, v157
	v_rcp_f32_e32 v157, v157
	s_nop 0
	v_mul_f32_e32 v157, v156, v157
	v_cvt_f32_i32_e32 v156, v123
	v_mul_f32_e32 v156, v158, v156
	v_mul_f32_e32 v158, 0xbfb8aa3b, v156
	v_exp_f32_e32 v158, v158
	s_nop 0
	v_add_f32_e32 v158, 1.0, v158
	v_rcp_f32_e32 v158, v158
	s_nop 0
	v_mul_f32_e32 v158, v156, v158
	v_cvt_f32_i32_e32 v156, v112
	v_mul_f32_e32 v156, v159, v156
	v_mul_f32_e32 v159, 0xbfb8aa3b, v156
	v_exp_f32_e32 v159, v159
	s_nop 0
	v_add_f32_e32 v159, 1.0, v159
	v_rcp_f32_e32 v159, v159
	s_nop 0
	v_mul_f32_e32 v159, v156, v159
	v_cvt_f32_i32_e32 v156, v113
	v_mul_f32_e32 v156, v165, v156
	v_mul_f32_e32 v165, 0xbfb8aa3b, v156
	v_exp_f32_e32 v165, v165
	s_nop 0
	v_add_f32_e32 v165, 1.0, v165
	v_rcp_f32_e32 v165, v165
	s_nop 0
	v_mul_f32_e32 v165, v156, v165
	v_cvt_f32_i32_e32 v156, v114
	v_mul_f32_e32 v156, v166, v156
	v_mul_f32_e32 v166, 0xbfb8aa3b, v156
	v_exp_f32_e32 v166, v166
	s_nop 0
	v_add_f32_e32 v166, 1.0, v166
	v_rcp_f32_e32 v166, v166
	s_nop 0
	v_mul_f32_e32 v166, v156, v166
	v_cvt_f32_i32_e32 v156, v115
	v_mul_f32_e32 v145, v145, v156
	v_mul_f32_e32 v156, 0xbfb8aa3b, v145
	v_exp_f32_e32 v156, v156
	s_nop 0
	v_add_f32_e32 v156, 1.0, v156
	v_rcp_f32_e32 v156, v156
	s_nop 0
	v_mul_f32_e32 v145, v145, v156
	v_cvt_pk_bf16_f32 v156, v148, v155
	v_cvt_pk_bf16_f32 v157, v157, v158
	v_cvt_pk_bf16_f32 v158, v159, v165
	v_cvt_pk_bf16_f32 v159, v166, v145
	global_store_dwordx4 v[152:153], v[156:159], off offset:256 sc1
	v_add_u32_e32 v152, 32, v144
	v_ashrrev_i32_e32 v153, 31, v152
	v_lshl_add_u64 v[156:157], v[152:153], 2, s[34:35]
	global_load_dword v145, v[156:157], off
	v_cvt_f32_i32_e32 v148, v108
	v_lshlrev_b64 v[152:153], 11, v[152:153]
	v_lshl_add_u64 v[152:153], s[42:43], 0, v[152:153]
	v_lshl_add_u64 v[152:153], v[152:153], 0, s[72:73]
	v_lshl_add_u64 v[152:153], v[152:153], 0, v[146:147]
	s_waitcnt vmcnt(0)
; #define GAS __attribute__((address_space(1)))
; __device__ __forceinline__ v4u pack8(const f32x4 a, const f32x4 b) { v4u w; w.x = cvt_pk_bf16(a[0], a[1]); w.y = cvt_pk_bf16(a[2], a[3]); w.z = cvt_pk_bf16(b[0], b[1]); w.w = cvt_pk_bf16(b[2], b[3]); return w; }
; __device__ __forceinline__ float fexp(float x) { return __builtin_amdgcn_exp2f(x * 1.4426950408889634f); }
; #define EPI_LOOP_AM for (int ai = 0; ai < 2; ++ai) _Pragma("unroll") for (int m = 0; m < 4; ++m)
;     __device__ __forceinline__ void operator()(AccI& acci, const Unit& u, LAS unsigned char*, int wr, int wc, int fr, int fq) const {
;     ...
;             EPI_LOOP_AM {
;                 const int r = 128 * ai + 64 * wr + 16 * m + fr, tok = pm * 256 + r; const float sxr = sx0[tok];
; #pragma unroll
;                 for (int bj = 0; bj < 2; ++bj) { f32x4 v[2];
; #pragma unroll
;                     for (int n = 0; n < 2; ++n)
; #pragma unroll
;                         for (int j = 0; j < 4; ++j) { const float g = ACCF(ai, bj, m, n, j); v[n][j] = g * __builtin_amdgcn_rcpf(1.f + fexp(-g)); }
;                     *(GAS v4u*)(gs + (size_t)tok * RW + (pn - 8) * 256 + bj * 128 + c0) = pack8(v[0], v[1]); }
	v_mul_f32_e32 v155, v40, v145
	v_mul_f32_e32 v148, v155, v148
	v_mul_f32_e32 v155, 0xbfb8aa3b, v148
	v_exp_f32_e32 v155, v155
	v_mul_f32_e32 v156, v41, v145
	v_mul_f32_e32 v157, v42, v145
	v_mul_f32_e32 v158, v43, v145
	v_add_f32_e32 v155, 1.0, v155
	v_rcp_f32_e32 v155, v155
	v_mul_f32_e32 v159, v32, v145
	v_mul_f32_e32 v165, v33, v145
	v_mul_f32_e32 v166, v34, v145
	v_mul_f32_e32 v148, v148, v155
	v_cvt_f32_i32_e32 v155, v109
	v_mul_f32_e32 v167, v35, v145
	v_mul_f32_e32 v155, v156, v155
	v_mul_f32_e32 v156, 0xbfb8aa3b, v155
	v_exp_f32_e32 v156, v156
	s_nop 0
	v_add_f32_e32 v156, 1.0, v156
	v_rcp_f32_e32 v156, v156
	s_nop 0
	v_mul_f32_e32 v155, v155, v156
	v_cvt_f32_i32_e32 v156, v110
	v_mul_f32_e32 v156, v157, v156
	v_mul_f32_e32 v157, 0xbfb8aa3b, v156
	v_exp_f32_e32 v157, v157
	s_nop 0
	v_add_f32_e32 v157, 1.0, v157
	v_rcp_f32_e32 v157, v157
	s_nop 0
	v_mul_f32_e32 v157, v156, v157
	v_cvt_f32_i32_e32 v156, v111
	v_mul_f32_e32 v156, v158, v156
	v_mul_f32_e32 v158, 0xbfb8aa3b, v156
	v_exp_f32_e32 v158, v158
	s_nop 0
	v_add_f32_e32 v158, 1.0, v158
	v_rcp_f32_e32 v158, v158
	s_nop 0
	v_mul_f32_e32 v158, v156, v158
	v_cvt_f32_i32_e32 v156, v100
	v_mul_f32_e32 v156, v159, v156
	v_mul_f32_e32 v159, 0xbfb8aa3b, v156
	v_exp_f32_e32 v159, v159
	s_nop 0
	v_add_f32_e32 v159, 1.0, v159
	v_rcp_f32_e32 v159, v159
	s_nop 0
	v_mul_f32_e32 v159, v156, v159
	v_cvt_f32_i32_e32 v156, v101
	v_mul_f32_e32 v156, v165, v156
	v_mul_f32_e32 v165, 0xbfb8aa3b, v156
	v_exp_f32_e32 v165, v165
	s_nop 0
	v_add_f32_e32 v165, 1.0, v165
	v_rcp_f32_e32 v165, v165
	s_nop 0
	v_mul_f32_e32 v165, v156, v165
	v_cvt_f32_i32_e32 v156, v102
	v_mul_f32_e32 v156, v166, v156
	v_mul_f32_e32 v166, 0xbfb8aa3b, v156
	v_exp_f32_e32 v166, v166
	s_nop 0
	v_add_f32_e32 v166, 1.0, v166
	v_rcp_f32_e32 v166, v166
	s_nop 0
	v_mul_f32_e32 v166, v156, v166
	v_cvt_f32_i32_e32 v156, v103
	v_mul_f32_e32 v156, v167, v156
	v_mul_f32_e32 v167, 0xbfb8aa3b, v156
	v_exp_f32_e32 v167, v167
	s_nop 0
	v_add_f32_e32 v167, 1.0, v167
	v_rcp_f32_e32 v167, v167
	s_nop 0
	v_mul_f32_e32 v167, v156, v167
	v_cvt_pk_bf16_f32 v156, v148, v155
	v_cvt_f32_i32_e32 v148, v104
	v_mul_f32_e32 v155, v44, v145
	v_cvt_pk_bf16_f32 v157, v157, v158
	v_cvt_pk_bf16_f32 v158, v159, v165
	v_mul_f32_e32 v148, v155, v148
	v_mul_f32_e32 v155, 0xbfb8aa3b, v148
	v_exp_f32_e32 v155, v155
	v_cvt_pk_bf16_f32 v159, v166, v167
	global_store_dwordx4 v[152:153], v[156:159], off sc1
	v_mul_f32_e32 v165, v37, v145
	v_add_f32_e32 v155, 1.0, v155
	v_rcp_f32_e32 v155, v155
	v_mul_f32_e32 v156, v45, v145
	v_mul_f32_e32 v157, v46, v145
	v_mul_f32_e32 v158, v47, v145
	v_mul_f32_e32 v148, v148, v155
	v_cvt_f32_i32_e32 v155, v105
	v_mul_f32_e32 v159, v36, v145
	v_mul_f32_e32 v166, v38, v145
	v_mul_f32_e32 v145, v39, v145
	v_mul_f32_e32 v155, v156, v155
	v_mul_f32_e32 v156, 0xbfb8aa3b, v155
	v_exp_f32_e32 v156, v156
	s_nop 0
	v_add_f32_e32 v156, 1.0, v156
	v_rcp_f32_e32 v156, v156
	s_nop 0
	v_mul_f32_e32 v155, v155, v156
	v_cvt_f32_i32_e32 v156, v106
	v_mul_f32_e32 v156, v157, v156
	v_mul_f32_e32 v157, 0xbfb8aa3b, v156
	v_exp_f32_e32 v157, v157
	s_nop 0
	v_add_f32_e32 v157, 1.0, v157
	v_rcp_f32_e32 v157, v157
	s_nop 0
	v_mul_f32_e32 v157, v156, v157
	v_cvt_f32_i32_e32 v156, v107
	v_mul_f32_e32 v156, v158, v156
	v_mul_f32_e32 v158, 0xbfb8aa3b, v156
	v_exp_f32_e32 v158, v158
	s_nop 0
	v_add_f32_e32 v158, 1.0, v158
	v_rcp_f32_e32 v158, v158
	s_nop 0
	v_mul_f32_e32 v158, v156, v158
	v_cvt_f32_i32_e32 v156, v96
	v_mul_f32_e32 v156, v159, v156
	v_mul_f32_e32 v159, 0xbfb8aa3b, v156
	v_exp_f32_e32 v159, v159
	s_nop 0
	v_add_f32_e32 v159, 1.0, v159
	v_rcp_f32_e32 v159, v159
	s_nop 0
	v_mul_f32_e32 v159, v156, v159
	v_cvt_f32_i32_e32 v156, v97
	v_mul_f32_e32 v156, v165, v156
	v_mul_f32_e32 v165, 0xbfb8aa3b, v156
	v_exp_f32_e32 v165, v165
	s_nop 0
	v_add_f32_e32 v165, 1.0, v165
	v_rcp_f32_e32 v165, v165
	s_nop 0
	v_mul_f32_e32 v165, v156, v165
	v_cvt_f32_i32_e32 v156, v98
	v_mul_f32_e32 v156, v166, v156
	v_mul_f32_e32 v166, 0xbfb8aa3b, v156
	v_exp_f32_e32 v166, v166
	s_nop 0
	v_add_f32_e32 v166, 1.0, v166
	v_rcp_f32_e32 v166, v166
	s_nop 0
	v_mul_f32_e32 v166, v156, v166
	v_cvt_f32_i32_e32 v156, v99
	v_mul_f32_e32 v145, v145, v156
	v_mul_f32_e32 v156, 0xbfb8aa3b, v145
	v_exp_f32_e32 v156, v156
	s_nop 0
	v_add_f32_e32 v156, 1.0, v156
	v_rcp_f32_e32 v156, v156
	s_nop 0
	v_mul_f32_e32 v145, v145, v156
	v_cvt_pk_bf16_f32 v156, v148, v155
	v_cvt_pk_bf16_f32 v157, v157, v158
	v_cvt_pk_bf16_f32 v158, v159, v165
	v_cvt_pk_bf16_f32 v159, v166, v145
	global_store_dwordx4 v[152:153], v[156:159], off offset:256 sc1
	v_add_u32_e32 v152, 48, v144
	v_ashrrev_i32_e32 v153, 31, v152
	v_lshl_add_u64 v[156:157], v[152:153], 2, s[34:35]
	global_load_dword v145, v[156:157], off
	v_cvt_f32_i32_e32 v148, v92
	v_lshlrev_b64 v[152:153], 11, v[152:153]
	v_lshl_add_u64 v[152:153], s[42:43], 0, v[152:153]
	v_lshl_add_u64 v[152:153], v[152:153], 0, s[72:73]
	v_lshl_add_u64 v[152:153], v[152:153], 0, v[146:147]
	s_waitcnt vmcnt(0)
; #define GAS __attribute__((address_space(1)))
; __device__ __forceinline__ v4u pack8(const f32x4 a, const f32x4 b) { v4u w; w.x = cvt_pk_bf16(a[0], a[1]); w.y = cvt_pk_bf16(a[2], a[3]); w.z = cvt_pk_bf16(b[0], b[1]); w.w = cvt_pk_bf16(b[2], b[3]); return w; }
; __device__ __forceinline__ float fexp(float x) { return __builtin_amdgcn_exp2f(x * 1.4426950408889634f); }
; #define EPI_LOOP_AM for (int ai = 0; ai < 2; ++ai) _Pragma("unroll") for (int m = 0; m < 4; ++m)
;     __device__ __forceinline__ void operator()(AccI& acci, const Unit& u, LAS unsigned char*, int wr, int wc, int fr, int fq) const {
;     ...
;             EPI_LOOP_AM {
;                 const int r = 128 * ai + 64 * wr + 16 * m + fr, tok = pm * 256 + r; const float sxr = sx0[tok];
; #pragma unroll
;                 for (int bj = 0; bj < 2; ++bj) { f32x4 v[2];
; #pragma unroll
;                     for (int n = 0; n < 2; ++n)
; #pragma unroll
;                         for (int j = 0; j < 4; ++j) { const float g = ACCF(ai, bj, m, n, j); v[n][j] = g * __builtin_amdgcn_rcpf(1.f + fexp(-g)); }
;                     *(GAS v4u*)(gs + (size_t)tok * RW + (pn - 8) * 256 + bj * 128 + c0) = pack8(v[0], v[1]); }
	v_mul_f32_e32 v155, v40, v145
	v_mul_f32_e32 v148, v155, v148
	v_mul_f32_e32 v155, 0xbfb8aa3b, v148
	v_exp_f32_e32 v155, v155
	v_mul_f32_e32 v156, v41, v145
	v_mul_f32_e32 v157, v42, v145
	v_mul_f32_e32 v158, v43, v145
	v_add_f32_e32 v155, 1.0, v155
	v_rcp_f32_e32 v155, v155
	v_mul_f32_e32 v159, v32, v145
	v_mul_f32_e32 v165, v33, v145
	v_mul_f32_e32 v166, v34, v145
	v_mul_f32_e32 v148, v148, v155
	v_cvt_f32_i32_e32 v155, v93
	v_mul_f32_e32 v167, v35, v145
	v_mul_f32_e32 v155, v156, v155
	v_mul_f32_e32 v156, 0xbfb8aa3b, v155
	v_exp_f32_e32 v156, v156
	s_nop 0
	v_add_f32_e32 v156, 1.0, v156
	v_rcp_f32_e32 v156, v156
	s_nop 0
	v_mul_f32_e32 v155, v155, v156
	v_cvt_f32_i32_e32 v156, v94
	v_mul_f32_e32 v156, v157, v156
	v_mul_f32_e32 v157, 0xbfb8aa3b, v156
	v_exp_f32_e32 v157, v157
	s_nop 0
	v_add_f32_e32 v157, 1.0, v157
	v_rcp_f32_e32 v157, v157
	s_nop 0
	v_mul_f32_e32 v157, v156, v157
	v_cvt_f32_i32_e32 v156, v95
	v_mul_f32_e32 v156, v158, v156
	v_mul_f32_e32 v158, 0xbfb8aa3b, v156
	v_exp_f32_e32 v158, v158
	s_nop 0
	v_add_f32_e32 v158, 1.0, v158
	v_rcp_f32_e32 v158, v158
	s_nop 0
	v_mul_f32_e32 v158, v156, v158
	v_cvt_f32_i32_e32 v156, v84
	v_mul_f32_e32 v156, v159, v156
	v_mul_f32_e32 v159, 0xbfb8aa3b, v156
	v_exp_f32_e32 v159, v159
	s_nop 0
	v_add_f32_e32 v159, 1.0, v159
	v_rcp_f32_e32 v159, v159
	s_nop 0
	v_mul_f32_e32 v159, v156, v159
	v_cvt_f32_i32_e32 v156, v85
	v_mul_f32_e32 v156, v165, v156
	v_mul_f32_e32 v165, 0xbfb8aa3b, v156
	v_exp_f32_e32 v165, v165
	s_nop 0
	v_add_f32_e32 v165, 1.0, v165
	v_rcp_f32_e32 v165, v165
	s_nop 0
	v_mul_f32_e32 v165, v156, v165
	v_cvt_f32_i32_e32 v156, v86
	v_mul_f32_e32 v156, v166, v156
	v_mul_f32_e32 v166, 0xbfb8aa3b, v156
	v_exp_f32_e32 v166, v166
	s_nop 0
	v_add_f32_e32 v166, 1.0, v166
	v_rcp_f32_e32 v166, v166
	s_nop 0
	v_mul_f32_e32 v166, v156, v166
	v_cvt_f32_i32_e32 v156, v87
	v_mul_f32_e32 v156, v167, v156
	v_mul_f32_e32 v167, 0xbfb8aa3b, v156
	v_exp_f32_e32 v167, v167
	s_nop 0
	v_add_f32_e32 v167, 1.0, v167
	v_rcp_f32_e32 v167, v167
	s_nop 0
	v_mul_f32_e32 v167, v156, v167
	v_cvt_pk_bf16_f32 v156, v148, v155
	v_cvt_f32_i32_e32 v148, v88
	v_mul_f32_e32 v155, v44, v145
	v_cvt_pk_bf16_f32 v157, v157, v158
	v_cvt_pk_bf16_f32 v158, v159, v165
	v_mul_f32_e32 v148, v155, v148
	v_mul_f32_e32 v155, 0xbfb8aa3b, v148
	v_exp_f32_e32 v155, v155
	v_cvt_pk_bf16_f32 v159, v166, v167
	global_store_dwordx4 v[152:153], v[156:159], off sc1
	v_mul_f32_e32 v165, v37, v145
	v_add_f32_e32 v155, 1.0, v155
	v_rcp_f32_e32 v155, v155
	v_mul_f32_e32 v156, v45, v145
	v_mul_f32_e32 v157, v46, v145
	v_mul_f32_e32 v158, v47, v145
	v_mul_f32_e32 v148, v148, v155
	v_cvt_f32_i32_e32 v155, v89
	v_mul_f32_e32 v159, v36, v145
	v_mul_f32_e32 v166, v38, v145
	v_mul_f32_e32 v145, v39, v145
	v_mul_f32_e32 v155, v156, v155
	v_mul_f32_e32 v156, 0xbfb8aa3b, v155
	v_exp_f32_e32 v156, v156
	s_nop 0
	v_add_f32_e32 v156, 1.0, v156
	v_rcp_f32_e32 v156, v156
	s_nop 0
	v_mul_f32_e32 v155, v155, v156
	v_cvt_f32_i32_e32 v156, v90
	v_mul_f32_e32 v156, v157, v156
	v_mul_f32_e32 v157, 0xbfb8aa3b, v156
	v_exp_f32_e32 v157, v157
	s_nop 0
	v_add_f32_e32 v157, 1.0, v157
	v_rcp_f32_e32 v157, v157
	s_nop 0
	v_mul_f32_e32 v157, v156, v157
	v_cvt_f32_i32_e32 v156, v91
	v_mul_f32_e32 v156, v158, v156
	v_mul_f32_e32 v158, 0xbfb8aa3b, v156
	v_exp_f32_e32 v158, v158
	s_nop 0
	v_add_f32_e32 v158, 1.0, v158
	v_rcp_f32_e32 v158, v158
	s_nop 0
	v_mul_f32_e32 v158, v156, v158
	v_cvt_f32_i32_e32 v156, v80
	v_mul_f32_e32 v156, v159, v156
	v_mul_f32_e32 v159, 0xbfb8aa3b, v156
	v_exp_f32_e32 v159, v159
	s_nop 0
	v_add_f32_e32 v159, 1.0, v159
	v_rcp_f32_e32 v159, v159
	s_nop 0
	v_mul_f32_e32 v159, v156, v159
	v_cvt_f32_i32_e32 v156, v81
	v_mul_f32_e32 v156, v165, v156
	v_mul_f32_e32 v165, 0xbfb8aa3b, v156
	v_exp_f32_e32 v165, v165
	s_nop 0
	v_add_f32_e32 v165, 1.0, v165
	v_rcp_f32_e32 v165, v165
	s_nop 0
	v_mul_f32_e32 v165, v156, v165
	v_cvt_f32_i32_e32 v156, v82
	v_mul_f32_e32 v156, v166, v156
	v_mul_f32_e32 v166, 0xbfb8aa3b, v156
	v_exp_f32_e32 v166, v166
	s_nop 0
	v_add_f32_e32 v166, 1.0, v166
	v_rcp_f32_e32 v166, v166
	s_nop 0
	v_mul_f32_e32 v166, v156, v166
	v_cvt_f32_i32_e32 v156, v83
	v_mul_f32_e32 v145, v145, v156
	v_mul_f32_e32 v156, 0xbfb8aa3b, v145
	v_exp_f32_e32 v156, v156
	s_nop 0
	v_add_f32_e32 v156, 1.0, v156
	v_rcp_f32_e32 v156, v156
	s_nop 0
	v_mul_f32_e32 v145, v145, v156
	v_cvt_pk_bf16_f32 v156, v148, v155
	v_cvt_pk_bf16_f32 v157, v157, v158
	v_cvt_pk_bf16_f32 v158, v159, v165
	v_cvt_pk_bf16_f32 v159, v166, v145
	global_store_dwordx4 v[152:153], v[156:159], off offset:256 sc1
	v_add_u32_e32 v152, 0x80, v144
	v_ashrrev_i32_e32 v153, 31, v152
	v_lshl_add_u64 v[156:157], v[152:153], 2, s[34:35]
	global_load_dword v145, v[156:157], off
	v_cvt_f32_i32_e32 v148, v76
	v_lshlrev_b64 v[152:153], 11, v[152:153]
	v_lshl_add_u64 v[152:153], s[42:43], 0, v[152:153]
	v_lshl_add_u64 v[152:153], v[152:153], 0, s[72:73]
	v_lshl_add_u64 v[152:153], v[152:153], 0, v[146:147]
	s_waitcnt vmcnt(0)
; #define GAS __attribute__((address_space(1)))
; __device__ __forceinline__ v4u pack8(const f32x4 a, const f32x4 b) { v4u w; w.x = cvt_pk_bf16(a[0], a[1]); w.y = cvt_pk_bf16(a[2], a[3]); w.z = cvt_pk_bf16(b[0], b[1]); w.w = cvt_pk_bf16(b[2], b[3]); return w; }
; __device__ __forceinline__ float fexp(float x) { return __builtin_amdgcn_exp2f(x * 1.4426950408889634f); }
; #define EPI_LOOP_AM for (int ai = 0; ai < 2; ++ai) _Pragma("unroll") for (int m = 0; m < 4; ++m)
;     __device__ __forceinline__ void operator()(AccI& acci, const Unit& u, LAS unsigned char*, int wr, int wc, int fr, int fq) const {
;     ...
;             EPI_LOOP_AM {
;                 const int r = 128 * ai + 64 * wr + 16 * m + fr, tok = pm * 256 + r; const float sxr = sx0[tok];
; #pragma unroll
;                 for (int bj = 0; bj < 2; ++bj) { f32x4 v[2];
; #pragma unroll
;                     for (int n = 0; n < 2; ++n)
; #pragma unroll
;                         for (int j = 0; j < 4; ++j) { const float g = ACCF(ai, bj, m, n, j); v[n][j] = g * __builtin_amdgcn_rcpf(1.f + fexp(-g)); }
;                     *(GAS v4u*)(gs + (size_t)tok * RW + (pn - 8) * 256 + bj * 128 + c0) = pack8(v[0], v[1]); }
	v_mul_f32_e32 v155, v40, v145
	v_mul_f32_e32 v148, v155, v148
	v_mul_f32_e32 v155, 0xbfb8aa3b, v148
	v_exp_f32_e32 v155, v155
	v_mul_f32_e32 v156, v41, v145
	v_mul_f32_e32 v157, v42, v145
	v_mul_f32_e32 v158, v43, v145
	v_add_f32_e32 v155, 1.0, v155
	v_rcp_f32_e32 v155, v155
	v_mul_f32_e32 v159, v32, v145
	v_mul_f32_e32 v165, v33, v145
	v_mul_f32_e32 v166, v34, v145
	v_mul_f32_e32 v148, v148, v155
	v_cvt_f32_i32_e32 v155, v77
	v_mul_f32_e32 v167, v35, v145
	v_mul_f32_e32 v155, v156, v155
	v_mul_f32_e32 v156, 0xbfb8aa3b, v155
	v_exp_f32_e32 v156, v156
	s_nop 0
	v_add_f32_e32 v156, 1.0, v156
	v_rcp_f32_e32 v156, v156
	s_nop 0
	v_mul_f32_e32 v155, v155, v156
	v_cvt_f32_i32_e32 v156, v78
	v_mul_f32_e32 v156, v157, v156
	v_mul_f32_e32 v157, 0xbfb8aa3b, v156
	v_exp_f32_e32 v157, v157
	s_nop 0
	v_add_f32_e32 v157, 1.0, v157
	v_rcp_f32_e32 v157, v157
	s_nop 0
	v_mul_f32_e32 v157, v156, v157
	v_cvt_f32_i32_e32 v156, v79
	v_mul_f32_e32 v156, v158, v156
	v_mul_f32_e32 v158, 0xbfb8aa3b, v156
	v_exp_f32_e32 v158, v158
	s_nop 0
	v_add_f32_e32 v158, 1.0, v158
	v_rcp_f32_e32 v158, v158
	s_nop 0
	v_mul_f32_e32 v158, v156, v158
	v_cvt_f32_i32_e32 v156, v68
	v_mul_f32_e32 v156, v159, v156
	v_mul_f32_e32 v159, 0xbfb8aa3b, v156
	v_exp_f32_e32 v159, v159
	s_nop 0
	v_add_f32_e32 v159, 1.0, v159
	v_rcp_f32_e32 v159, v159
	s_nop 0
	v_mul_f32_e32 v159, v156, v159
	v_cvt_f32_i32_e32 v156, v69
	v_mul_f32_e32 v156, v165, v156
	v_mul_f32_e32 v165, 0xbfb8aa3b, v156
	v_exp_f32_e32 v165, v165
	s_nop 0
	v_add_f32_e32 v165, 1.0, v165
	v_rcp_f32_e32 v165, v165
	s_nop 0
	v_mul_f32_e32 v165, v156, v165
	v_cvt_f32_i32_e32 v156, v70
	v_mul_f32_e32 v156, v166, v156
	v_mul_f32_e32 v166, 0xbfb8aa3b, v156
	v_exp_f32_e32 v166, v166
	s_nop 0
	v_add_f32_e32 v166, 1.0, v166
	v_rcp_f32_e32 v166, v166
	s_nop 0
	v_mul_f32_e32 v166, v156, v166
	v_cvt_f32_i32_e32 v156, v71
	v_mul_f32_e32 v156, v167, v156
	v_mul_f32_e32 v167, 0xbfb8aa3b, v156
	v_exp_f32_e32 v167, v167
	s_nop 0
	v_add_f32_e32 v167, 1.0, v167
	v_rcp_f32_e32 v167, v167
	s_nop 0
	v_mul_f32_e32 v167, v156, v167
	v_cvt_pk_bf16_f32 v156, v148, v155
	v_cvt_f32_i32_e32 v148, v72
	v_mul_f32_e32 v155, v44, v145
	v_cvt_pk_bf16_f32 v157, v157, v158
	v_cvt_pk_bf16_f32 v158, v159, v165
	v_mul_f32_e32 v148, v155, v148
	v_mul_f32_e32 v155, 0xbfb8aa3b, v148
	v_exp_f32_e32 v155, v155
	v_cvt_pk_bf16_f32 v159, v166, v167
	global_store_dwordx4 v[152:153], v[156:159], off sc1
	v_mul_f32_e32 v165, v37, v145
	v_add_f32_e32 v155, 1.0, v155
	v_rcp_f32_e32 v155, v155
	v_mul_f32_e32 v156, v45, v145
	v_mul_f32_e32 v157, v46, v145
	v_mul_f32_e32 v158, v47, v145
	v_mul_f32_e32 v148, v148, v155
	v_cvt_f32_i32_e32 v155, v73
	v_mul_f32_e32 v159, v36, v145
	v_mul_f32_e32 v166, v38, v145
	v_mul_f32_e32 v145, v39, v145
	v_mul_f32_e32 v155, v156, v155
	v_mul_f32_e32 v156, 0xbfb8aa3b, v155
	v_exp_f32_e32 v156, v156
	s_nop 0
	v_add_f32_e32 v156, 1.0, v156
	v_rcp_f32_e32 v156, v156
	s_nop 0
	v_mul_f32_e32 v155, v155, v156
	v_cvt_f32_i32_e32 v156, v74
	v_mul_f32_e32 v156, v157, v156
	v_mul_f32_e32 v157, 0xbfb8aa3b, v156
	v_exp_f32_e32 v157, v157
	s_nop 0
	v_add_f32_e32 v157, 1.0, v157
	v_rcp_f32_e32 v157, v157
	s_nop 0
	v_mul_f32_e32 v157, v156, v157
	v_cvt_f32_i32_e32 v156, v75
	v_mul_f32_e32 v156, v158, v156
	v_mul_f32_e32 v158, 0xbfb8aa3b, v156
	v_exp_f32_e32 v158, v158
	s_nop 0
	v_add_f32_e32 v158, 1.0, v158
	v_rcp_f32_e32 v158, v158
	s_nop 0
	v_mul_f32_e32 v158, v156, v158
	v_cvt_f32_i32_e32 v156, v64
	v_mul_f32_e32 v156, v159, v156
	v_mul_f32_e32 v159, 0xbfb8aa3b, v156
	v_exp_f32_e32 v159, v159
	s_nop 0
	v_add_f32_e32 v159, 1.0, v159
	v_rcp_f32_e32 v159, v159
	s_nop 0
	v_mul_f32_e32 v159, v156, v159
	v_cvt_f32_i32_e32 v156, v65
	v_mul_f32_e32 v156, v165, v156
	v_mul_f32_e32 v165, 0xbfb8aa3b, v156
	v_exp_f32_e32 v165, v165
	s_nop 0
	v_add_f32_e32 v165, 1.0, v165
	v_rcp_f32_e32 v165, v165
	s_nop 0
	v_mul_f32_e32 v165, v156, v165
	v_cvt_f32_i32_e32 v156, v66
	v_mul_f32_e32 v156, v166, v156
	v_mul_f32_e32 v166, 0xbfb8aa3b, v156
	v_exp_f32_e32 v166, v166
	s_nop 0
	v_add_f32_e32 v166, 1.0, v166
	v_rcp_f32_e32 v166, v166
	s_nop 0
	v_mul_f32_e32 v166, v156, v166
	v_cvt_f32_i32_e32 v156, v67
	v_mul_f32_e32 v145, v145, v156
	v_mul_f32_e32 v156, 0xbfb8aa3b, v145
	v_exp_f32_e32 v156, v156
	s_nop 0
	v_add_f32_e32 v156, 1.0, v156
	v_rcp_f32_e32 v156, v156
	s_nop 0
	v_mul_f32_e32 v145, v145, v156
	v_cvt_pk_bf16_f32 v156, v148, v155
	v_cvt_pk_bf16_f32 v157, v157, v158
	v_cvt_pk_bf16_f32 v158, v159, v165
	v_cvt_pk_bf16_f32 v159, v166, v145
	global_store_dwordx4 v[152:153], v[156:159], off offset:256 sc1
	v_add_u32_e32 v152, 0x90, v144
	v_ashrrev_i32_e32 v153, 31, v152
	v_lshl_add_u64 v[156:157], v[152:153], 2, s[34:35]
	global_load_dword v145, v[156:157], off
	v_cvt_f32_i32_e32 v148, v60
	v_lshlrev_b64 v[152:153], 11, v[152:153]
	v_lshl_add_u64 v[152:153], s[42:43], 0, v[152:153]
	v_lshl_add_u64 v[152:153], v[152:153], 0, s[72:73]
	v_lshl_add_u64 v[152:153], v[152:153], 0, v[146:147]
	s_waitcnt vmcnt(0)
; #define GAS __attribute__((address_space(1)))
; __device__ __forceinline__ v4u pack8(const f32x4 a, const f32x4 b) { v4u w; w.x = cvt_pk_bf16(a[0], a[1]); w.y = cvt_pk_bf16(a[2], a[3]); w.z = cvt_pk_bf16(b[0], b[1]); w.w = cvt_pk_bf16(b[2], b[3]); return w; }
; __device__ __forceinline__ float fexp(float x) { return __builtin_amdgcn_exp2f(x * 1.4426950408889634f); }
; #define EPI_LOOP_AM for (int ai = 0; ai < 2; ++ai) _Pragma("unroll") for (int m = 0; m < 4; ++m)
;     __device__ __forceinline__ void operator()(AccI& acci, const Unit& u, LAS unsigned char*, int wr, int wc, int fr, int fq) const {
;     ...
;             EPI_LOOP_AM {
;                 const int r = 128 * ai + 64 * wr + 16 * m + fr, tok = pm * 256 + r; const float sxr = sx0[tok];
; #pragma unroll
;                 for (int bj = 0; bj < 2; ++bj) { f32x4 v[2];
; #pragma unroll
;                     for (int n = 0; n < 2; ++n)
; #pragma unroll
;                         for (int j = 0; j < 4; ++j) { const float g = ACCF(ai, bj, m, n, j); v[n][j] = g * __builtin_amdgcn_rcpf(1.f + fexp(-g)); }
;                     *(GAS v4u*)(gs + (size_t)tok * RW + (pn - 8) * 256 + bj * 128 + c0) = pack8(v[0], v[1]); }
	v_mul_f32_e32 v155, v40, v145
	v_mul_f32_e32 v148, v155, v148
	v_mul_f32_e32 v155, 0xbfb8aa3b, v148
	v_exp_f32_e32 v155, v155
	v_mul_f32_e32 v156, v41, v145
	v_mul_f32_e32 v157, v42, v145
	v_mul_f32_e32 v158, v43, v145
	v_add_f32_e32 v155, 1.0, v155
	v_rcp_f32_e32 v155, v155
	v_mul_f32_e32 v159, v32, v145
	v_mul_f32_e32 v165, v33, v145
	v_mul_f32_e32 v166, v34, v145
	v_mul_f32_e32 v148, v148, v155
	v_cvt_f32_i32_e32 v155, v61
	v_mul_f32_e32 v167, v35, v145
	v_mul_f32_e32 v155, v156, v155
	v_mul_f32_e32 v156, 0xbfb8aa3b, v155
	v_exp_f32_e32 v156, v156
	s_nop 0
	v_add_f32_e32 v156, 1.0, v156
	v_rcp_f32_e32 v156, v156
	s_nop 0
	v_mul_f32_e32 v155, v155, v156
	v_cvt_f32_i32_e32 v156, v62
	v_mul_f32_e32 v156, v157, v156
	v_mul_f32_e32 v157, 0xbfb8aa3b, v156
	v_exp_f32_e32 v157, v157
	s_nop 0
	v_add_f32_e32 v157, 1.0, v157
	v_rcp_f32_e32 v157, v157
	s_nop 0
	v_mul_f32_e32 v157, v156, v157
	v_cvt_f32_i32_e32 v156, v63
	v_mul_f32_e32 v156, v158, v156
	v_mul_f32_e32 v158, 0xbfb8aa3b, v156
	v_exp_f32_e32 v158, v158
	s_nop 0
	v_add_f32_e32 v158, 1.0, v158
	v_rcp_f32_e32 v158, v158
	s_nop 0
	v_mul_f32_e32 v158, v156, v158
	v_cvt_f32_i32_e32 v156, v52
	v_mul_f32_e32 v156, v159, v156
	v_mul_f32_e32 v159, 0xbfb8aa3b, v156
	v_exp_f32_e32 v159, v159
	s_nop 0
	v_add_f32_e32 v159, 1.0, v159
	v_rcp_f32_e32 v159, v159
	s_nop 0
	v_mul_f32_e32 v159, v156, v159
	v_cvt_f32_i32_e32 v156, v53
	v_mul_f32_e32 v156, v165, v156
	v_mul_f32_e32 v165, 0xbfb8aa3b, v156
	v_exp_f32_e32 v165, v165
	s_nop 0
	v_add_f32_e32 v165, 1.0, v165
	v_rcp_f32_e32 v165, v165
	s_nop 0
	v_mul_f32_e32 v165, v156, v165
	v_cvt_f32_i32_e32 v156, v54
	v_mul_f32_e32 v156, v166, v156
	v_mul_f32_e32 v166, 0xbfb8aa3b, v156
	v_exp_f32_e32 v166, v166
	s_nop 0
	v_add_f32_e32 v166, 1.0, v166
	v_rcp_f32_e32 v166, v166
	s_nop 0
	v_mul_f32_e32 v166, v156, v166
	v_cvt_f32_i32_e32 v156, v55
	v_mul_f32_e32 v156, v167, v156
	v_mul_f32_e32 v167, 0xbfb8aa3b, v156
	v_exp_f32_e32 v167, v167
	s_nop 0
	v_add_f32_e32 v167, 1.0, v167
	v_rcp_f32_e32 v167, v167
	s_nop 0
	v_mul_f32_e32 v167, v156, v167
	v_cvt_pk_bf16_f32 v156, v148, v155
	v_cvt_f32_i32_e32 v148, v56
	v_mul_f32_e32 v155, v44, v145
	v_cvt_pk_bf16_f32 v157, v157, v158
	v_cvt_pk_bf16_f32 v158, v159, v165
	v_mul_f32_e32 v148, v155, v148
	v_mul_f32_e32 v155, 0xbfb8aa3b, v148
	v_exp_f32_e32 v155, v155
	v_cvt_pk_bf16_f32 v159, v166, v167
	global_store_dwordx4 v[152:153], v[156:159], off sc1
	v_mul_f32_e32 v165, v37, v145
	v_add_f32_e32 v155, 1.0, v155
	v_rcp_f32_e32 v155, v155
	v_mul_f32_e32 v156, v45, v145
	v_mul_f32_e32 v157, v46, v145
	v_mul_f32_e32 v158, v47, v145
	v_mul_f32_e32 v148, v148, v155
	v_cvt_f32_i32_e32 v155, v57
	v_mul_f32_e32 v159, v36, v145
	v_mul_f32_e32 v166, v38, v145
	v_mul_f32_e32 v145, v39, v145
	v_mul_f32_e32 v155, v156, v155
	v_mul_f32_e32 v156, 0xbfb8aa3b, v155
	v_exp_f32_e32 v156, v156
	s_nop 0
	v_add_f32_e32 v156, 1.0, v156
	v_rcp_f32_e32 v156, v156
	s_nop 0
	v_mul_f32_e32 v155, v155, v156
	v_cvt_f32_i32_e32 v156, v58
	v_mul_f32_e32 v156, v157, v156
	v_mul_f32_e32 v157, 0xbfb8aa3b, v156
	v_exp_f32_e32 v157, v157
	s_nop 0
	v_add_f32_e32 v157, 1.0, v157
	v_rcp_f32_e32 v157, v157
	s_nop 0
	v_mul_f32_e32 v157, v156, v157
	v_cvt_f32_i32_e32 v156, v59
	v_mul_f32_e32 v156, v158, v156
	v_mul_f32_e32 v158, 0xbfb8aa3b, v156
	v_exp_f32_e32 v158, v158
	s_nop 0
	v_add_f32_e32 v158, 1.0, v158
	v_rcp_f32_e32 v158, v158
	s_nop 0
	v_mul_f32_e32 v158, v156, v158
	v_cvt_f32_i32_e32 v156, v48
	v_mul_f32_e32 v156, v159, v156
	v_mul_f32_e32 v159, 0xbfb8aa3b, v156
	v_exp_f32_e32 v159, v159
	s_nop 0
	v_add_f32_e32 v159, 1.0, v159
	v_rcp_f32_e32 v159, v159
	s_nop 0
	v_mul_f32_e32 v159, v156, v159
	v_cvt_f32_i32_e32 v156, v49
	v_mul_f32_e32 v156, v165, v156
	v_mul_f32_e32 v165, 0xbfb8aa3b, v156
	v_exp_f32_e32 v165, v165
	s_nop 0
	v_add_f32_e32 v165, 1.0, v165
	v_rcp_f32_e32 v165, v165
	s_nop 0
	v_mul_f32_e32 v165, v156, v165
	v_cvt_f32_i32_e32 v156, v50
	v_mul_f32_e32 v156, v166, v156
	v_mul_f32_e32 v166, 0xbfb8aa3b, v156
	v_exp_f32_e32 v166, v166
	s_nop 0
	v_add_f32_e32 v166, 1.0, v166
	v_rcp_f32_e32 v166, v166
	s_nop 0
	v_mul_f32_e32 v166, v156, v166
	v_cvt_f32_i32_e32 v156, v51
	v_mul_f32_e32 v145, v145, v156
	v_mul_f32_e32 v156, 0xbfb8aa3b, v145
	v_exp_f32_e32 v156, v156
	s_nop 0
	v_add_f32_e32 v156, 1.0, v156
	v_rcp_f32_e32 v156, v156
	s_nop 0
	v_mul_f32_e32 v145, v145, v156
	v_cvt_pk_bf16_f32 v156, v148, v155
	v_cvt_pk_bf16_f32 v157, v157, v158
	v_cvt_pk_bf16_f32 v158, v159, v165
	v_cvt_pk_bf16_f32 v159, v166, v145
	global_store_dwordx4 v[152:153], v[156:159], off offset:256 sc1
	v_add_u32_e32 v152, 0xa0, v144
	v_ashrrev_i32_e32 v153, 31, v152
	v_lshl_add_u64 v[156:157], v[152:153], 2, s[34:35]
	global_load_dword v145, v[156:157], off
	v_cvt_f32_i32_e32 v148, v28
	v_lshlrev_b64 v[152:153], 11, v[152:153]
	v_lshl_add_u64 v[152:153], s[42:43], 0, v[152:153]
	v_lshl_add_u64 v[152:153], v[152:153], 0, s[72:73]
	v_lshl_add_u64 v[152:153], v[152:153], 0, v[146:147]
	v_add_u32_e32 v144, 0xb0, v144
	s_waitcnt vmcnt(0)
; #define GAS __attribute__((address_space(1)))
; __device__ __forceinline__ v4u pack8(const f32x4 a, const f32x4 b) { v4u w; w.x = cvt_pk_bf16(a[0], a[1]); w.y = cvt_pk_bf16(a[2], a[3]); w.z = cvt_pk_bf16(b[0], b[1]); w.w = cvt_pk_bf16(b[2], b[3]); return w; }
; __device__ __forceinline__ float fexp(float x) { return __builtin_amdgcn_exp2f(x * 1.4426950408889634f); }
; #define EPI_LOOP_AM for (int ai = 0; ai < 2; ++ai) _Pragma("unroll") for (int m = 0; m < 4; ++m)
;     __device__ __forceinline__ void operator()(AccI& acci, const Unit& u, LAS unsigned char*, int wr, int wc, int fr, int fq) const {
;     ...
;             EPI_LOOP_AM {
;                 const int r = 128 * ai + 64 * wr + 16 * m + fr, tok = pm * 256 + r; const float sxr = sx0[tok];
; #pragma unroll
;                 for (int bj = 0; bj < 2; ++bj) { f32x4 v[2];
; #pragma unroll
;                     for (int n = 0; n < 2; ++n)
; #pragma unroll
;                         for (int j = 0; j < 4; ++j) { const float g = ACCF(ai, bj, m, n, j); v[n][j] = g * __builtin_amdgcn_rcpf(1.f + fexp(-g)); }
;                     *(GAS v4u*)(gs + (size_t)tok * RW + (pn - 8) * 256 + bj * 128 + c0) = pack8(v[0], v[1]); }
	v_mul_f32_e32 v155, v40, v145
	v_mul_f32_e32 v148, v155, v148
	v_mul_f32_e32 v155, 0xbfb8aa3b, v148
	v_exp_f32_e32 v155, v155
	v_mul_f32_e32 v156, v41, v145
	v_mul_f32_e32 v157, v42, v145
	v_mul_f32_e32 v158, v43, v145
	v_add_f32_e32 v155, 1.0, v155
	v_rcp_f32_e32 v155, v155
	v_mul_f32_e32 v159, v32, v145
	v_mul_f32_e32 v165, v33, v145
	v_mul_f32_e32 v166, v34, v145
	v_mul_f32_e32 v148, v148, v155
	v_cvt_f32_i32_e32 v155, v29
	v_mul_f32_e32 v167, v35, v145
	v_mul_f32_e32 v155, v156, v155
	v_mul_f32_e32 v156, 0xbfb8aa3b, v155
	v_exp_f32_e32 v156, v156
	s_nop 0
	v_add_f32_e32 v156, 1.0, v156
	v_rcp_f32_e32 v156, v156
	s_nop 0
	v_mul_f32_e32 v155, v155, v156
	v_cvt_f32_i32_e32 v156, v30
	v_mul_f32_e32 v156, v157, v156
	v_mul_f32_e32 v157, 0xbfb8aa3b, v156
	v_exp_f32_e32 v157, v157
	s_nop 0
	v_add_f32_e32 v157, 1.0, v157
	v_rcp_f32_e32 v157, v157
	s_nop 0
	v_mul_f32_e32 v157, v156, v157
	v_cvt_f32_i32_e32 v156, v31
	v_mul_f32_e32 v156, v158, v156
	v_mul_f32_e32 v158, 0xbfb8aa3b, v156
	v_exp_f32_e32 v158, v158
	s_nop 0
	v_add_f32_e32 v158, 1.0, v158
	v_rcp_f32_e32 v158, v158
	s_nop 0
	v_mul_f32_e32 v158, v156, v158
	v_cvt_f32_i32_e32 v156, v20
	v_mul_f32_e32 v156, v159, v156
	v_mul_f32_e32 v159, 0xbfb8aa3b, v156
	v_exp_f32_e32 v159, v159
	s_nop 0
	v_add_f32_e32 v159, 1.0, v159
	v_rcp_f32_e32 v159, v159
	s_nop 0
	v_mul_f32_e32 v159, v156, v159
	v_cvt_f32_i32_e32 v156, v21
	v_mul_f32_e32 v156, v165, v156
	v_mul_f32_e32 v165, 0xbfb8aa3b, v156
	v_exp_f32_e32 v165, v165
	s_nop 0
	v_add_f32_e32 v165, 1.0, v165
	v_rcp_f32_e32 v165, v165
	s_nop 0
	v_mul_f32_e32 v165, v156, v165
	v_cvt_f32_i32_e32 v156, v22
	v_mul_f32_e32 v156, v166, v156
	v_mul_f32_e32 v166, 0xbfb8aa3b, v156
	v_exp_f32_e32 v166, v166
	s_nop 0
	v_add_f32_e32 v166, 1.0, v166
	v_rcp_f32_e32 v166, v166
	s_nop 0
	v_mul_f32_e32 v166, v156, v166
	v_cvt_f32_i32_e32 v156, v23
	v_mul_f32_e32 v156, v167, v156
	v_mul_f32_e32 v167, 0xbfb8aa3b, v156
	v_exp_f32_e32 v167, v167
	s_nop 0
	v_add_f32_e32 v167, 1.0, v167
	v_rcp_f32_e32 v167, v167
	s_nop 0
	v_mul_f32_e32 v167, v156, v167
	v_cvt_pk_bf16_f32 v156, v148, v155
	v_cvt_f32_i32_e32 v148, v24
	v_mul_f32_e32 v155, v44, v145
	v_cvt_pk_bf16_f32 v157, v157, v158
	v_cvt_pk_bf16_f32 v158, v159, v165
	v_mul_f32_e32 v148, v155, v148
	v_mul_f32_e32 v155, 0xbfb8aa3b, v148
	v_exp_f32_e32 v155, v155
	v_cvt_pk_bf16_f32 v159, v166, v167
	global_store_dwordx4 v[152:153], v[156:159], off sc1
	v_mul_f32_e32 v165, v37, v145
	v_add_f32_e32 v155, 1.0, v155
	v_rcp_f32_e32 v155, v155
	v_mul_f32_e32 v156, v45, v145
	v_mul_f32_e32 v157, v46, v145
	v_mul_f32_e32 v158, v47, v145
	v_mul_f32_e32 v148, v148, v155
	v_cvt_f32_i32_e32 v155, v25
	v_mul_f32_e32 v159, v36, v145
	v_mul_f32_e32 v166, v38, v145
	v_mul_f32_e32 v145, v39, v145
	v_mul_f32_e32 v155, v156, v155
	v_mul_f32_e32 v156, 0xbfb8aa3b, v155
	v_exp_f32_e32 v156, v156
	s_nop 0
	v_add_f32_e32 v156, 1.0, v156
	v_rcp_f32_e32 v156, v156
	s_nop 0
	v_mul_f32_e32 v155, v155, v156
	v_cvt_f32_i32_e32 v156, v26
	v_mul_f32_e32 v156, v157, v156
	v_mul_f32_e32 v157, 0xbfb8aa3b, v156
	v_exp_f32_e32 v157, v157
	s_nop 0
	v_add_f32_e32 v157, 1.0, v157
	v_rcp_f32_e32 v157, v157
	s_nop 0
	v_mul_f32_e32 v157, v156, v157
	v_cvt_f32_i32_e32 v156, v27
	v_mul_f32_e32 v156, v158, v156
	v_mul_f32_e32 v158, 0xbfb8aa3b, v156
	v_exp_f32_e32 v158, v158
	s_nop 0
	v_add_f32_e32 v158, 1.0, v158
	v_rcp_f32_e32 v158, v158
	s_nop 0
	v_mul_f32_e32 v158, v156, v158
	v_cvt_f32_i32_e32 v156, v16
	v_mul_f32_e32 v156, v159, v156
	v_mul_f32_e32 v159, 0xbfb8aa3b, v156
	v_exp_f32_e32 v159, v159
	s_nop 0
	v_add_f32_e32 v159, 1.0, v159
	v_rcp_f32_e32 v159, v159
	s_nop 0
	v_mul_f32_e32 v159, v156, v159
	v_cvt_f32_i32_e32 v156, v17
	v_mul_f32_e32 v156, v165, v156
	v_mul_f32_e32 v165, 0xbfb8aa3b, v156
	v_exp_f32_e32 v165, v165
	s_nop 0
	v_add_f32_e32 v165, 1.0, v165
	v_rcp_f32_e32 v165, v165
	s_nop 0
	v_mul_f32_e32 v165, v156, v165
	v_cvt_f32_i32_e32 v156, v18
	v_mul_f32_e32 v156, v166, v156
	v_mul_f32_e32 v166, 0xbfb8aa3b, v156
	v_exp_f32_e32 v166, v166
	s_nop 0
	v_add_f32_e32 v166, 1.0, v166
	v_rcp_f32_e32 v166, v166
	s_nop 0
	v_mul_f32_e32 v166, v156, v166
	v_cvt_f32_i32_e32 v156, v19
	v_mul_f32_e32 v145, v145, v156
	v_mul_f32_e32 v156, 0xbfb8aa3b, v145
	v_exp_f32_e32 v156, v156
	s_nop 0
	v_add_f32_e32 v156, 1.0, v156
	v_rcp_f32_e32 v156, v156
	s_nop 0
	v_mul_f32_e32 v145, v145, v156
	v_cvt_pk_bf16_f32 v156, v148, v155
	v_cvt_pk_bf16_f32 v157, v157, v158
	v_cvt_pk_bf16_f32 v158, v159, v165
	v_cvt_pk_bf16_f32 v159, v166, v145
	v_ashrrev_i32_e32 v145, 31, v144
	global_store_dwordx4 v[152:153], v[156:159], off offset:256 sc1
	v_lshl_add_u64 v[152:153], v[144:145], 2, s[34:35]
	global_load_dword v148, v[152:153], off
	v_cvt_f32_i32_e32 v152, v12
	v_lshlrev_b64 v[144:145], 11, v[144:145]
	v_lshl_add_u64 v[144:145], s[42:43], 0, v[144:145]
	v_lshl_add_u64 v[144:145], v[144:145], 0, s[72:73]
	s_mov_b64 s[72:73], 0
	s_waitcnt vmcnt(0)
; #define GAS __attribute__((address_space(1)))
; __device__ __forceinline__ v4u pack8(const f32x4 a, const f32x4 b) { v4u w; w.x = cvt_pk_bf16(a[0], a[1]); w.y = cvt_pk_bf16(a[2], a[3]); w.z = cvt_pk_bf16(b[0], b[1]); w.w = cvt_pk_bf16(b[2], b[3]); return w; }
; __device__ __forceinline__ float fexp(float x) { return __builtin_amdgcn_exp2f(x * 1.4426950408889634f); }
; #define EPI_LOOP_AM for (int ai = 0; ai < 2; ++ai) _Pragma("unroll") for (int m = 0; m < 4; ++m)
;     __device__ __forceinline__ void operator()(AccI& acci, const Unit& u, LAS unsigned char*, int wr, int wc, int fr, int fq) const {
;     ...
;             EPI_LOOP_AM {
;                 const int r = 128 * ai + 64 * wr + 16 * m + fr, tok = pm * 256 + r; const float sxr = sx0[tok];
; #pragma unroll
;                 for (int bj = 0; bj < 2; ++bj) { f32x4 v[2];
; #pragma unroll
;                     for (int n = 0; n < 2; ++n)
; #pragma unroll
;                         for (int j = 0; j < 4; ++j) { const float g = ACCF(ai, bj, m, n, j); v[n][j] = g * __builtin_amdgcn_rcpf(1.f + fexp(-g)); }
;                     *(GAS v4u*)(gs + (size_t)tok * RW + (pn - 8) * 256 + bj * 128 + c0) = pack8(v[0], v[1]); }
	v_mul_f32_e32 v153, v40, v148
	v_mul_f32_e32 v152, v153, v152
	v_mul_f32_e32 v153, 0xbfb8aa3b, v152
	v_exp_f32_e32 v153, v153
	v_mul_f32_e32 v155, v41, v148
	v_mul_f32_e32 v156, v42, v148
	v_mul_f32_e32 v157, v43, v148
	v_add_f32_e32 v153, 1.0, v153
	v_rcp_f32_e32 v153, v153
	v_mul_f32_e32 v158, v32, v148
	v_mul_f32_e32 v159, v33, v148
	v_mul_f32_e32 v165, v34, v148
	v_mul_f32_e32 v152, v152, v153
	v_cvt_f32_i32_e32 v153, v13
	v_mul_f32_e32 v166, v35, v148
	v_mul_f32_e32 v153, v155, v153
	v_mul_f32_e32 v155, 0xbfb8aa3b, v153
	v_exp_f32_e32 v155, v155
	s_nop 0
	v_add_f32_e32 v155, 1.0, v155
	v_rcp_f32_e32 v155, v155
	s_nop 0
	v_mul_f32_e32 v153, v153, v155
	v_cvt_f32_i32_e32 v155, v14
	v_mul_f32_e32 v155, v156, v155
	v_mul_f32_e32 v156, 0xbfb8aa3b, v155
	v_exp_f32_e32 v156, v156
	s_nop 0
	v_add_f32_e32 v156, 1.0, v156
	v_rcp_f32_e32 v156, v156
	s_nop 0
	v_mul_f32_e32 v155, v155, v156
	v_cvt_f32_i32_e32 v156, v15
	v_mul_f32_e32 v156, v157, v156
	v_mul_f32_e32 v157, 0xbfb8aa3b, v156
	v_exp_f32_e32 v157, v157
	s_nop 0
	v_add_f32_e32 v157, 1.0, v157
	v_rcp_f32_e32 v157, v157
	s_nop 0
	v_mul_f32_e32 v157, v156, v157
	v_cvt_f32_i32_e32 v156, v4
	v_mul_f32_e32 v156, v158, v156
	v_mul_f32_e32 v158, 0xbfb8aa3b, v156
	v_exp_f32_e32 v158, v158
	s_nop 0
	v_add_f32_e32 v158, 1.0, v158
	v_rcp_f32_e32 v158, v158
	s_nop 0
	v_mul_f32_e32 v158, v156, v158
	v_cvt_f32_i32_e32 v156, v5
	v_mul_f32_e32 v156, v159, v156
	v_mul_f32_e32 v159, 0xbfb8aa3b, v156
	v_exp_f32_e32 v159, v159
	s_nop 0
	v_add_f32_e32 v159, 1.0, v159
	v_rcp_f32_e32 v159, v159
	s_nop 0
	v_mul_f32_e32 v159, v156, v159
	v_cvt_f32_i32_e32 v156, v6
	v_mul_f32_e32 v156, v165, v156
	v_mul_f32_e32 v165, 0xbfb8aa3b, v156
	v_exp_f32_e32 v165, v165
	s_nop 0
	v_add_f32_e32 v165, 1.0, v165
	v_rcp_f32_e32 v165, v165
	s_nop 0
	v_mul_f32_e32 v165, v156, v165
	v_cvt_f32_i32_e32 v156, v7
	v_mul_f32_e32 v156, v166, v156
	v_mul_f32_e32 v166, 0xbfb8aa3b, v156
	v_exp_f32_e32 v166, v166
	s_nop 0
	v_add_f32_e32 v166, 1.0, v166
	v_rcp_f32_e32 v166, v166
	s_nop 0
	v_mul_f32_e32 v166, v156, v166
	v_cvt_pk_bf16_f32 v156, v152, v153
	v_lshl_add_u64 v[152:153], v[144:145], 0, v[146:147]
	v_cvt_f32_i32_e32 v144, v8
	v_mul_f32_e32 v145, v44, v148
	v_mul_f32_e32 v146, v45, v148
	v_mul_f32_e32 v147, v46, v148
	v_mul_f32_e32 v144, v145, v144
	v_mul_f32_e32 v145, 0xbfb8aa3b, v144
	v_exp_f32_e32 v145, v145
	v_cvt_pk_bf16_f32 v157, v155, v157
	v_mul_f32_e32 v155, v47, v148
	v_cvt_pk_bf16_f32 v158, v158, v159
	v_add_f32_e32 v145, 1.0, v145
	v_rcp_f32_e32 v145, v145
	v_cvt_pk_bf16_f32 v159, v165, v166
	global_store_dwordx4 v[152:153], v[156:159], off sc1
	v_lshl_add_u64 v[152:153], v[152:153], 0, s[52:53]
	v_mul_f32_e32 v144, v144, v145
	v_cvt_f32_i32_e32 v145, v9
	v_mul_f32_e32 v156, v36, v148
	v_mul_f32_e32 v157, v37, v148
	v_mul_f32_e32 v158, v38, v148
	v_mul_f32_e32 v145, v146, v145
	v_mul_f32_e32 v146, 0xbfb8aa3b, v145
	v_exp_f32_e32 v146, v146
	v_mul_f32_e32 v148, v39, v148
	v_add_f32_e32 v146, 1.0, v146
	v_rcp_f32_e32 v146, v146
	s_nop 0
	v_mul_f32_e32 v145, v145, v146
	v_cvt_f32_i32_e32 v146, v10
	v_cvt_pk_bf16_f32 v144, v144, v145
	v_mul_f32_e32 v146, v147, v146
	v_mul_f32_e32 v147, 0xbfb8aa3b, v146
	v_exp_f32_e32 v147, v147
	s_nop 0
	v_add_f32_e32 v147, 1.0, v147
	v_rcp_f32_e32 v147, v147
	s_nop 0
	v_mul_f32_e32 v146, v146, v147
	v_cvt_f32_i32_e32 v147, v11
	v_mul_f32_e32 v147, v155, v147
	v_mul_f32_e32 v155, 0xbfb8aa3b, v147
	v_exp_f32_e32 v155, v155
	s_nop 0
	v_add_f32_e32 v155, 1.0, v155
	v_rcp_f32_e32 v155, v155
	s_nop 0
	v_mul_f32_e32 v147, v147, v155
	v_cvt_f32_i32_e32 v155, v0
	v_cvt_pk_bf16_f32 v145, v146, v147
	v_mul_f32_e32 v155, v156, v155
	v_mul_f32_e32 v156, 0xbfb8aa3b, v155
	v_exp_f32_e32 v156, v156
	s_nop 0
	v_add_f32_e32 v156, 1.0, v156
	v_rcp_f32_e32 v156, v156
	s_nop 0
	v_mul_f32_e32 v155, v155, v156
	v_cvt_f32_i32_e32 v156, v1
	v_mul_f32_e32 v156, v157, v156
	v_mul_f32_e32 v157, 0xbfb8aa3b, v156
	v_exp_f32_e32 v157, v157
	s_nop 0
	v_add_f32_e32 v157, 1.0, v157
	v_rcp_f32_e32 v157, v157
	s_nop 0
	v_mul_f32_e32 v156, v156, v157
	v_cvt_f32_i32_e32 v157, v2
	v_cvt_pk_bf16_f32 v146, v155, v156
	v_mul_f32_e32 v157, v158, v157
	v_mul_f32_e32 v158, 0xbfb8aa3b, v157
	v_exp_f32_e32 v158, v158
	s_nop 0
	v_add_f32_e32 v158, 1.0, v158
	v_rcp_f32_e32 v158, v158
	s_nop 0
	v_mul_f32_e32 v157, v157, v158
	v_cvt_f32_i32_e32 v158, v3
	v_mul_f32_e32 v148, v148, v158
	v_mul_f32_e32 v158, 0xbfb8aa3b, v148
	v_exp_f32_e32 v158, v158
	s_nop 0
	v_add_f32_e32 v158, 1.0, v158
	v_rcp_f32_e32 v158, v158
	s_nop 0
	v_mul_f32_e32 v148, v148, v158
	v_cvt_pk_bf16_f32 v147, v157, v148
; #define GAS __attribute__((address_space(1)))
; __device__ __forceinline__ v4u pack8(const f32x4 a, const f32x4 b) { v4u w; w.x = cvt_pk_bf16(a[0], a[1]); w.y = cvt_pk_bf16(a[2], a[3]); w.z = cvt_pk_bf16(b[0], b[1]); w.w = cvt_pk_bf16(b[2], b[3]); return w; }
; __device__ __forceinline__ float fexp(float x) { return __builtin_amdgcn_exp2f(x * 1.4426950408889634f); }
; #define EPI_LOOP_AM for (int ai = 0; ai < 2; ++ai) _Pragma("unroll") for (int m = 0; m < 4; ++m)
;     __device__ __forceinline__ void operator()(AccI& acci, const Unit& u, LAS unsigned char*, int wr, int wc, int fr, int fq) const {
;     ...
;         if (pn < 8) {
;             const int h = pn & 3; const bool isq = pn < 4;
;             float inv[8];
; #pragma unroll
;             for (int e = 0; e < 8; ++e) inv[e] = __builtin_amdgcn_exp2f(-(float)(c0 + e) * (13.287712379549449f / 128.f)) * 0.15915494309189535f;
;             const float lgf = -fexp(dec_f[h]), lgb = -fexp(dec_b[h]);
; #pragma unroll
;             EPI_LOOP_AM {
;                 const int r = 128 * ai + 64 * wr + 16 * m + fr, tok = pm * 256 + r; const float pos = (float)tok; const float sxr = sx0[tok];
;                 f32x4 o1[2], o2[2];
; #pragma unroll
;                 for (int n = 0; n < 2; ++n)
; #pragma unroll
;                     for (int j = 0; j < 4; ++j) { float c, s; cs_rev(pos * inv[4 * n + j], c, s); const float x1 = ACCF(ai, 0, m, n, j), x2 = ACCF(ai, 1, m, n, j); o1[n][j] = x1 * c - x2 * s; o2[n][j] = x2 * c + x1 * s; }
;                 if (isq) {
;                     bf16* q = qs + (size_t)tok * RW + h * HD + c0; *(GAS v4u*)q = pack8(o1[0], o1[1]); *(GAS v4u*)(q + 128) = pack8(o2[0], o2[1]);
;                     const int il = r; const float wf = fexp(lgf * (float)(il + 1)), wb = fexp(lgb * (float)(255 - il));
;                     bf16* a = Acat + ((size_t)h * T + tok) * CAT + c0;
;                     *(GAS v4u*)(a + 256) = pack8(o1[0] * wf, o1[1] * wf); *(GAS v4u*)(a + 384) = pack8(o2[0] * wf, o2[1] * wf);
;                     *(GAS v4u*)(a + 512) = pack8(o1[0] * wb, o1[1] * wb); *(GAS v4u*)(a + 640) = pack8(o2[0] * wb, o2[1] * wb);
;                 } else {
;                     bf16* k = kk + (size_t)tok * RW + h * HD + c0; *(GAS v4u*)k = pack8(o1[0] * 0.0625f, o1[1] * 0.0625f); *(GAS v4u*)(k + 128) = pack8(o2[0] * 0.0625f, o2[1] * 0.0625f);
;                 }
.LBB0_184:
	s_andn2_b64 vcc, exec, s[72:73]
	s_cbranch_vccnz .LBB0_217
	v_cvt_f32_i32_e32 v144, v150
	s_and_b32 s0, s24, 3
	s_cmp_gt_i32 s24, 3
	s_cselect_b64 s[72:73], -1, 0
	v_mul_f32_e32 v144, 0xbdd49a78, v144
	v_exp_f32_e32 v144, v144
	s_lshl_b32 s2, s0, 2
	v_add_u32_e32 v172, s26, v154
	v_cvt_f32_i32_e32 v141, v141
	v_mul_f32_e32 v148, 0.15915494, v144
	v_or_b32_e32 v144, 1, v150
	v_cvt_f32_i32_e32 v144, v144
	v_cvt_f32_i32_e32 v140, v140
	v_cvt_f32_i32_e32 v137, v137
	v_cvt_f32_i32_e32 v136, v136
	v_mul_f32_e32 v144, 0xbdd49a78, v144
	v_exp_f32_e32 v144, v144
	v_cvt_f32_i32_e32 v143, v143
	v_cvt_f32_i32_e32 v142, v142
	v_cvt_f32_i32_e32 v139, v139
	v_mul_f32_e32 v165, 0.15915494, v144
	v_or_b32_e32 v144, 2, v150
	v_cvt_f32_i32_e32 v144, v144
	v_cvt_f32_i32_e32 v138, v138
	v_cvt_f32_i32_e32 v133, v133
	v_cvt_f32_i32_e32 v132, v132
	v_mul_f32_e32 v144, 0xbdd49a78, v144
	v_exp_f32_e32 v144, v144
	v_cvt_f32_i32_e32 v129, v129
	v_cvt_f32_i32_e32 v128, v128
	v_cvt_f32_i32_e32 v135, v135
	v_mul_f32_e32 v166, 0.15915494, v144
	v_or_b32_e32 v144, 3, v150
	v_cvt_f32_i32_e32 v144, v144
	v_cvt_f32_i32_e32 v134, v134
	v_cvt_f32_i32_e32 v131, v131
	v_cvt_f32_i32_e32 v130, v130
	v_mul_f32_e32 v144, 0xbdd49a78, v144
	v_exp_f32_e32 v144, v144
	s_lshl_b32 s19, s0, 8
	s_and_b64 vcc, exec, s[72:73]
	v_mul_f32_e32 v167, 0.15915494, v144
	v_or_b32_e32 v144, 4, v150
	v_cvt_f32_i32_e32 v144, v144
	v_mul_f32_e32 v144, 0xbdd49a78, v144
	v_exp_f32_e32 v144, v144
	s_nop 0
	v_mul_f32_e32 v168, 0.15915494, v144
	v_or_b32_e32 v144, 5, v150
	v_cvt_f32_i32_e32 v144, v144
	v_mul_f32_e32 v144, 0xbdd49a78, v144
	v_exp_f32_e32 v144, v144
	s_nop 0
	v_mul_f32_e32 v169, 0.15915494, v144
	v_or_b32_e32 v144, 6, v150
	v_cvt_f32_i32_e32 v144, v144
	v_mul_f32_e32 v144, 0xbdd49a78, v144
	v_exp_f32_e32 v144, v144
	s_nop 0
	v_mul_f32_e32 v170, 0.15915494, v144
	v_or_b32_e32 v144, 7, v150
	v_cvt_f32_i32_e32 v144, v144
	v_mul_f32_e32 v144, 0xbdd49a78, v144
	v_exp_f32_e32 v144, v144
	s_nop 0
	v_mul_f32_e32 v171, 0.15915494, v144
	v_mov_b32_e32 v144, s2
	global_load_dword v174, v144, s[14:15]
	global_load_dword v173, v144, s[30:31]
	v_lshl_add_u32 v144, s4, 8, v172
	v_ashrrev_i32_e32 v145, 31, v144
	v_lshl_add_u64 v[152:153], v[144:145], 2, s[34:35]
	global_load_dword v146, v[152:153], off
	v_cvt_f32_i32_e32 v147, v144
	s_mov_b64 s[4:5], -1
	v_mul_f32_e32 v152, v148, v147
	v_fract_f32_e32 v153, v152
	v_cos_f32_e32 v152, v153
	v_sin_f32_e32 v154, v153
	v_mul_f32_e32 v153, v165, v147
	v_fract_f32_e32 v155, v153
	v_cos_f32_e32 v153, v155
	v_sin_f32_e32 v155, v155
	s_waitcnt vmcnt(0)
	v_pk_mul_f32 v[156:157], v[40:41], v[146:147] op_sel_hi:[1,0]
	s_nop 0
	v_pk_mul_f32 v[156:157], v[156:157], v[140:141]
	v_pk_mul_f32 v[140:141], v[44:45], v[146:147] op_sel_hi:[1,0]
	s_nop 0
	v_pk_mul_f32 v[136:137], v[140:141], v[136:137]
	s_nop 0
	v_pk_mul_f32 v[140:141], v[154:155], v[136:137]
	v_pk_mul_f32 v[136:137], v[152:153], v[136:137]
	v_pk_fma_f32 v[140:141], v[152:153], v[156:157], v[140:141] neg_lo:[0,0,1] neg_hi:[0,0,1]
	v_mul_f32_e32 v152, v166, v147
	v_mul_f32_e32 v153, v167, v147
	v_fract_f32_e32 v152, v152
	v_fract_f32_e32 v153, v153
	v_pk_fma_f32 v[136:137], v[154:155], v[156:157], v[136:137]
	v_cos_f32_e32 v154, v152
	v_sin_f32_e32 v152, v152
	v_cos_f32_e32 v155, v153
	v_sin_f32_e32 v153, v153
	v_pk_mul_f32 v[156:157], v[42:43], v[146:147] op_sel_hi:[1,0]
	s_nop 0
	v_pk_mul_f32 v[156:157], v[156:157], v[142:143]
	v_pk_mul_f32 v[142:143], v[46:47], v[146:147] op_sel_hi:[1,0]
	s_nop 0
	v_pk_mul_f32 v[138:139], v[142:143], v[138:139]
	s_nop 0
	v_pk_mul_f32 v[142:143], v[152:153], v[138:139]
	v_pk_mul_f32 v[138:139], v[154:155], v[138:139]
	v_pk_fma_f32 v[142:143], v[154:155], v[156:157], v[142:143] neg_lo:[0,0,1] neg_hi:[0,0,1]
	v_pk_fma_f32 v[138:139], v[152:153], v[156:157], v[138:139]
	v_mul_f32_e32 v152, v168, v147
	v_fract_f32_e32 v153, v152
	v_cos_f32_e32 v152, v153
	v_sin_f32_e32 v156, v153
	v_mul_f32_e32 v153, v169, v147
	v_fract_f32_e32 v154, v153
	v_cos_f32_e32 v153, v154
	v_sin_f32_e32 v157, v154
	v_pk_mul_f32 v[154:155], v[32:33], v[146:147] op_sel_hi:[1,0]
	s_nop 0
	v_pk_mul_f32 v[132:133], v[154:155], v[132:133]
	v_pk_mul_f32 v[154:155], v[36:37], v[146:147] op_sel_hi:[1,0]
	s_nop 0
	v_pk_mul_f32 v[128:129], v[154:155], v[128:129]
	s_nop 0
	v_pk_mul_f32 v[154:155], v[156:157], v[128:129]
	v_pk_mul_f32 v[128:129], v[152:153], v[128:129]
	v_pk_fma_f32 v[154:155], v[152:153], v[132:133], v[154:155] neg_lo:[0,0,1] neg_hi:[0,0,1]
	v_pk_fma_f32 v[152:153], v[156:157], v[132:133], v[128:129]
	v_mul_f32_e32 v128, v170, v147
	v_fract_f32_e32 v129, v128
	v_cos_f32_e32 v128, v129
	v_sin_f32_e32 v132, v129
	v_mul_f32_e32 v129, v171, v147
	v_fract_f32_e32 v133, v129
	v_cos_f32_e32 v129, v133
	v_sin_f32_e32 v133, v133
	v_pk_mul_f32 v[156:157], v[34:35], v[146:147] op_sel_hi:[1,0]
	s_nop 0
	v_pk_mul_f32 v[156:157], v[156:157], v[134:135]
	v_pk_mul_f32 v[134:135], v[38:39], v[146:147] op_sel_hi:[1,0]
	s_nop 0
	v_pk_mul_f32 v[130:131], v[134:135], v[130:131]
	s_nop 0
	v_pk_mul_f32 v[134:135], v[128:129], v[130:131]
	v_pk_mul_f32 v[130:131], v[132:133], v[130:131]
	v_pk_fma_f32 v[134:135], v[132:133], v[156:157], v[134:135]
	v_pk_fma_f32 v[146:147], v[128:129], v[156:157], v[130:131] neg_lo:[0,0,1] neg_hi:[0,0,1]
	v_lshlrev_b64 v[156:157], 11, v[144:145]
	s_cbranch_vccz .LBB0_187
	v_lshl_add_u64 v[128:129], s[40:41], 0, v[156:157]
	s_lshl_b32 s6, s19, 1
	v_lshl_add_u64 v[128:129], v[128:129], 0, s[6:7]
	v_lshl_add_u64 v[132:133], v[150:151], 1, v[128:129]
	v_pk_mul_f32 v[130:131], v[142:143], s[54:55] op_sel_hi:[1,0]
	v_pk_mul_f32 v[128:129], v[140:141], s[54:55] op_sel_hi:[1,0]
	v_pk_mul_f32 v[158:159], v[154:155], s[54:55] op_sel_hi:[1,0]
	v_pk_mul_f32 v[176:177], v[146:147], s[54:55] op_sel_hi:[1,0]
	v_cvt_pk_bf16_f32 v128, v128, v129
	v_cvt_pk_bf16_f32 v129, v130, v131
	v_cvt_pk_bf16_f32 v130, v158, v159
	v_pk_mul_f32 v[158:159], v[152:153], s[54:55] op_sel_hi:[1,0]
	v_cvt_pk_bf16_f32 v131, v176, v177
	global_store_dwordx4 v[132:133], v[128:131], off sc1
	v_pk_mul_f32 v[176:177], v[134:135], s[54:55] op_sel_hi:[1,0]
	s_mov_b64 s[4:5], 0
	v_pk_mul_f32 v[130:131], v[138:139], s[54:55] op_sel_hi:[1,0]
	v_pk_mul_f32 v[128:129], v[136:137], s[54:55] op_sel_hi:[1,0]
	s_nop 0
	v_cvt_pk_bf16_f32 v128, v128, v129
	v_cvt_pk_bf16_f32 v129, v130, v131
	v_cvt_pk_bf16_f32 v130, v158, v159
	v_cvt_pk_bf16_f32 v131, v176, v177
	v_lshl_add_u64 v[158:159], v[132:133], 0, s[52:53]
; #define GAS __attribute__((address_space(1)))
; __device__ __forceinline__ v4u pack8(const f32x4 a, const f32x4 b) { v4u w; w.x = cvt_pk_bf16(a[0], a[1]); w.y = cvt_pk_bf16(a[2], a[3]); w.z = cvt_pk_bf16(b[0], b[1]); w.w = cvt_pk_bf16(b[2], b[3]); return w; }
; __device__ __forceinline__ float fexp(float x) { return __builtin_amdgcn_exp2f(x * 1.4426950408889634f); }
; __device__ __forceinline__ void cs_rev(float rev, float& c, float& s) { const float f = __builtin_amdgcn_fractf(rev); c = __builtin_amdgcn_cosf(f); s = __builtin_amdgcn_sinf(f); }
; #define EPI_LOOP_AM for (int ai = 0; ai < 2; ++ai) _Pragma("unroll") for (int m = 0; m < 4; ++m)
;     __device__ __forceinline__ void operator()(AccI& acci, const Unit& u, LAS unsigned char*, int wr, int wc, int fr, int fq) const {
;     ...
;             const float lgf = -fexp(dec_f[h]), lgb = -fexp(dec_b[h]);
; #pragma unroll
;             EPI_LOOP_AM {
;                 const int r = 128 * ai + 64 * wr + 16 * m + fr, tok = pm * 256 + r; const float pos = (float)tok; const float sxr = sx0[tok];
;                 f32x4 o1[2], o2[2];
; #pragma unroll
;                 for (int n = 0; n < 2; ++n)
; #pragma unroll
;                     for (int j = 0; j < 4; ++j) { float c, s; cs_rev(pos * inv[4 * n + j], c, s); const float x1 = ACCF(ai, 0, m, n, j), x2 = ACCF(ai, 1, m, n, j); o1[n][j] = x1 * c - x2 * s; o2[n][j] = x2 * c + x1 * s; }
;                 if (isq) {
;                     bf16* q = qs + (size_t)tok * RW + h * HD + c0; *(GAS v4u*)q = pack8(o1[0], o1[1]); *(GAS v4u*)(q + 128) = pack8(o2[0], o2[1]);
;                     const int il = r; const float wf = fexp(lgf * (float)(il + 1)), wb = fexp(lgb * (float)(255 - il));
;                     bf16* a = Acat + ((size_t)h * T + tok) * CAT + c0;
;                     *(GAS v4u*)(a + 256) = pack8(o1[0] * wf, o1[1] * wf); *(GAS v4u*)(a + 384) = pack8(o2[0] * wf, o2[1] * wf);
;                     *(GAS v4u*)(a + 512) = pack8(o1[0] * wb, o1[1] * wb); *(GAS v4u*)(a + 640) = pack8(o2[0] * wb, o2[1] * wb);
.LBB0_187:
	v_mul_f32_e32 v132, 0x3fb8aa3b, v174
	v_exp_f32_e32 v174, v132
	v_mul_f32_e32 v132, 0x3fb8aa3b, v173
	v_exp_f32_e32 v173, v132
	s_lshl_b32 s6, s0, 14
	s_andn2_b64 vcc, exec, s[4:5]
	v_lshlrev_b64 v[132:133], 1, v[150:151]
	s_cbranch_vccnz .LBB0_189
	v_lshl_add_u64 v[128:129], s[38:39], 0, v[156:157]
	s_lshl_b32 s4, s19, 1
	s_mov_b32 s5, s7
	v_lshl_add_u64 v[128:129], v[128:129], 0, s[4:5]
	v_lshl_add_u64 v[156:157], v[128:129], 0, v[132:133]
	v_cvt_pk_bf16_f32 v128, v140, v141
	v_cvt_pk_bf16_f32 v129, v142, v143
	v_cvt_pk_bf16_f32 v130, v154, v155
	v_cvt_pk_bf16_f32 v131, v146, v147
	global_store_dwordx4 v[156:157], v[128:131], off sc1
	v_add_u32_e32 v158, 1, v172
	v_cvt_f32_i32_e32 v158, v158
	v_cvt_pk_bf16_f32 v128, v136, v137
	v_cvt_pk_bf16_f32 v129, v138, v139
	v_cvt_pk_bf16_f32 v130, v152, v153
	v_cvt_pk_bf16_f32 v131, v134, v135
	global_store_dwordx4 v[156:157], v[128:131], off offset:256 sc1
	s_nop 1
	v_sub_u32_e32 v128, 0xff, v172
	v_cvt_f32_i32_e32 v128, v128
	v_mul_f32_e64 v129, v158, -v174
	v_mul_f32_e32 v129, 0x3fb8aa3b, v129
	v_exp_f32_e32 v156, v129
	v_mul_f32_e64 v128, v128, -v173
	v_mul_f32_e32 v128, 0x3fb8aa3b, v128
	v_exp_f32_e32 v158, v128
	v_lshl_add_u64 v[128:129], s[6:7], 0, v[144:145]
	v_mov_b64_e32 v[130:131], s[44:45]
	v_mad_u64_u32 v[130:131], s[4:5], v128, s10, v[130:131]
	v_mad_i32_i24 v131, v129, s10, v131
	v_lshl_add_u64 v[176:177], v[130:131], 0, v[132:133]
	v_pk_mul_f32 v[130:131], v[156:157], v[142:143] op_sel_hi:[0,1]
	v_pk_mul_f32 v[128:129], v[156:157], v[140:141] op_sel_hi:[0,1]
	v_pk_mul_f32 v[178:179], v[156:157], v[154:155] op_sel_hi:[0,1]
	v_pk_mul_f32 v[180:181], v[156:157], v[146:147] op_sel_hi:[0,1]
	v_cvt_pk_bf16_f32 v128, v128, v129
	v_cvt_pk_bf16_f32 v129, v130, v131
	v_cvt_pk_bf16_f32 v130, v178, v179
	v_cvt_pk_bf16_f32 v131, v180, v181
	global_store_dwordx4 v[176:177], v[128:131], off offset:512 sc1
	v_pk_mul_f32 v[178:179], v[156:157], v[152:153] op_sel_hi:[0,1]
	s_nop 0
	v_pk_mul_f32 v[130:131], v[156:157], v[138:139] op_sel_hi:[0,1]
	v_pk_mul_f32 v[128:129], v[156:157], v[136:137] op_sel_hi:[0,1]
	v_pk_mul_f32 v[156:157], v[156:157], v[134:135] op_sel_hi:[0,1]
	v_cvt_pk_bf16_f32 v128, v128, v129
	v_cvt_pk_bf16_f32 v129, v130, v131
	v_cvt_pk_bf16_f32 v130, v178, v179
	v_cvt_pk_bf16_f32 v131, v156, v157
	global_store_dwordx4 v[176:177], v[128:131], off offset:768 sc1
	v_pk_mul_f32 v[134:135], v[158:159], v[134:135] op_sel_hi:[0,1]
	s_nop 0
	v_pk_mul_f32 v[130:131], v[158:159], v[142:143] op_sel_hi:[0,1]
	v_pk_mul_f32 v[128:129], v[158:159], v[140:141] op_sel_hi:[0,1]
	v_pk_mul_f32 v[140:141], v[158:159], v[154:155] op_sel_hi:[0,1]
	v_pk_mul_f32 v[142:143], v[158:159], v[146:147] op_sel_hi:[0,1]
	v_cvt_pk_bf16_f32 v128, v128, v129
	v_cvt_pk_bf16_f32 v129, v130, v131
	v_cvt_pk_bf16_f32 v130, v140, v141
	v_cvt_pk_bf16_f32 v131, v142, v143
	global_store_dwordx4 v[176:177], v[128:131], off offset:1024 sc1
	s_nop 1
	v_pk_mul_f32 v[130:131], v[158:159], v[138:139] op_sel_hi:[0,1]
	v_pk_mul_f32 v[128:129], v[158:159], v[136:137] op_sel_hi:[0,1]
	v_pk_mul_f32 v[136:137], v[158:159], v[152:153] op_sel_hi:[0,1]
	v_lshl_add_u64 v[158:159], v[176:177], 0, s[56:57]
	v_cvt_pk_bf16_f32 v128, v128, v129
	v_cvt_pk_bf16_f32 v129, v130, v131
	v_cvt_pk_bf16_f32 v130, v136, v137
	v_cvt_pk_bf16_f32 v131, v134, v135
.LBB0_189:
	global_store_dwordx4 v[158:159], v[128:131], off sc1
	v_cvt_f32_i32_e32 v125, v125
	v_cvt_f32_i32_e32 v124, v124
	v_add_u32_e32 v128, 16, v144
	v_ashrrev_i32_e32 v129, 31, v128
	v_lshl_add_u64 v[130:131], v[128:129], 2, s[34:35]
	global_load_dword v134, v[130:131], off
	v_cvt_f32_i32_e32 v135, v128
	v_cvt_f32_i32_e32 v121, v121
	v_cvt_f32_i32_e32 v120, v120
	v_cvt_f32_i32_e32 v127, v127
	v_mul_f32_e32 v130, v148, v135
	v_fract_f32_e32 v131, v130
	v_cos_f32_e32 v130, v131
	v_sin_f32_e32 v136, v131
	v_mul_f32_e32 v131, v165, v135
	v_fract_f32_e32 v137, v131
	v_cos_f32_e32 v131, v137
	v_sin_f32_e32 v137, v137
	v_cvt_f32_i32_e32 v126, v126
	v_cvt_f32_i32_e32 v123, v123
	v_cvt_f32_i32_e32 v122, v122
	v_cvt_f32_i32_e32 v117, v117
	v_cvt_f32_i32_e32 v116, v116
	v_cvt_f32_i32_e32 v113, v113
	v_cvt_f32_i32_e32 v112, v112
	v_cvt_f32_i32_e32 v119, v119
	v_cvt_f32_i32_e32 v118, v118
	v_cvt_f32_i32_e32 v115, v115
	v_cvt_f32_i32_e32 v114, v114
	s_mov_b64 s[74:75], -1
	s_andn2_b64 vcc, exec, s[72:73]
	s_waitcnt vmcnt(0)
; #define GAS __attribute__((address_space(1)))
; __device__ __forceinline__ v4u pack8(const f32x4 a, const f32x4 b) { v4u w; w.x = cvt_pk_bf16(a[0], a[1]); w.y = cvt_pk_bf16(a[2], a[3]); w.z = cvt_pk_bf16(b[0], b[1]); w.w = cvt_pk_bf16(b[2], b[3]); return w; }
; __device__ __forceinline__ float fexp(float x) { return __builtin_amdgcn_exp2f(x * 1.4426950408889634f); }
; __device__ __forceinline__ void cs_rev(float rev, float& c, float& s) { const float f = __builtin_amdgcn_fractf(rev); c = __builtin_amdgcn_cosf(f); s = __builtin_amdgcn_sinf(f); }
;     __device__ __forceinline__ void operator()(AccI& acci, const Unit& u, LAS unsigned char*, int wr, int wc, int fr, int fq) const {
;     ...
;                 const int r = 128 * ai + 64 * wr + 16 * m + fr, tok = pm * 256 + r; const float pos = (float)tok; const float sxr = sx0[tok];
;                 f32x4 o1[2], o2[2];
; #pragma unroll
;                 for (int n = 0; n < 2; ++n)
; #pragma unroll
;                     for (int j = 0; j < 4; ++j) { float c, s; cs_rev(pos * inv[4 * n + j], c, s); const float x1 = ACCF(ai, 0, m, n, j), x2 = ACCF(ai, 1, m, n, j); o1[n][j] = x1 * c - x2 * s; o2[n][j] = x2 * c + x1 * s; }
;                 if (isq) {
;                     bf16* q = qs + (size_t)tok * RW + h * HD + c0; *(GAS v4u*)q = pack8(o1[0], o1[1]); *(GAS v4u*)(q + 128) = pack8(o2[0], o2[1]);
;                     const int il = r; const float wf = fexp(lgf * (float)(il + 1)), wb = fexp(lgb * (float)(255 - il));
;                     bf16* a = Acat + ((size_t)h * T + tok) * CAT + c0;
;                     *(GAS v4u*)(a + 256) = pack8(o1[0] * wf, o1[1] * wf); *(GAS v4u*)(a + 384) = pack8(o2[0] * wf, o2[1] * wf);
;                     *(GAS v4u*)(a + 512) = pack8(o1[0] * wb, o1[1] * wb); *(GAS v4u*)(a + 640) = pack8(o2[0] * wb, o2[1] * wb);
;                 } else {
;                     bf16* k = kk + (size_t)tok * RW + h * HD + c0; *(GAS v4u*)k = pack8(o1[0] * 0.0625f, o1[1] * 0.0625f); *(GAS v4u*)(k + 128) = pack8(o2[0] * 0.0625f, o2[1] * 0.0625f);
	v_pk_mul_f32 v[138:139], v[40:41], v[134:135] op_sel_hi:[1,0]
	s_nop 0
	v_pk_mul_f32 v[124:125], v[138:139], v[124:125]
	v_pk_mul_f32 v[138:139], v[44:45], v[134:135] op_sel_hi:[1,0]
	s_nop 0
	v_pk_mul_f32 v[138:139], v[138:139], v[120:121]
	s_nop 0
	v_pk_mul_f32 v[120:121], v[130:131], v[138:139]
	s_nop 0
	v_pk_fma_f32 v[120:121], v[136:137], v[124:125], v[120:121]
	v_pk_mul_f32 v[136:137], v[136:137], v[138:139]
	v_pk_mul_f32 v[138:139], v[42:43], v[134:135] op_sel_hi:[1,0]
	v_pk_fma_f32 v[124:125], v[130:131], v[124:125], v[136:137] neg_lo:[0,0,1] neg_hi:[0,0,1]
	v_mul_f32_e32 v130, v166, v135
	v_fract_f32_e32 v131, v130
	v_cos_f32_e32 v130, v131
	v_sin_f32_e32 v136, v131
	v_mul_f32_e32 v131, v167, v135
	v_fract_f32_e32 v137, v131
	v_cos_f32_e32 v131, v137
	v_sin_f32_e32 v137, v137
	v_pk_mul_f32 v[126:127], v[138:139], v[126:127]
	v_pk_mul_f32 v[138:139], v[46:47], v[134:135] op_sel_hi:[1,0]
	s_nop 0
	v_pk_mul_f32 v[138:139], v[138:139], v[122:123]
	s_nop 0
	v_pk_mul_f32 v[122:123], v[130:131], v[138:139]
	s_nop 0
	v_pk_fma_f32 v[122:123], v[136:137], v[126:127], v[122:123]
	v_pk_mul_f32 v[136:137], v[136:137], v[138:139]
	v_pk_mul_f32 v[138:139], v[32:33], v[134:135] op_sel_hi:[1,0]
	v_pk_fma_f32 v[126:127], v[130:131], v[126:127], v[136:137] neg_lo:[0,0,1] neg_hi:[0,0,1]
	v_mul_f32_e32 v130, v168, v135
	v_fract_f32_e32 v131, v130
	v_cos_f32_e32 v130, v131
	v_sin_f32_e32 v136, v131
	v_mul_f32_e32 v131, v169, v135
	v_fract_f32_e32 v137, v131
	v_cos_f32_e32 v131, v137
	v_sin_f32_e32 v137, v137
	v_pk_mul_f32 v[138:139], v[138:139], v[116:117]
	v_pk_mul_f32 v[116:117], v[36:37], v[134:135] op_sel_hi:[1,0]
	s_nop 0
	v_pk_mul_f32 v[112:113], v[116:117], v[112:113]
	s_nop 0
	v_pk_mul_f32 v[116:117], v[130:131], v[112:113]
	v_pk_mul_f32 v[112:113], v[136:137], v[112:113]
	v_pk_fma_f32 v[116:117], v[136:137], v[138:139], v[116:117]
	v_pk_fma_f32 v[130:131], v[130:131], v[138:139], v[112:113] neg_lo:[0,0,1] neg_hi:[0,0,1]
	v_mul_f32_e32 v112, v170, v135
	v_fract_f32_e32 v113, v112
	v_cos_f32_e32 v112, v113
	v_sin_f32_e32 v136, v113
	v_mul_f32_e32 v113, v171, v135
	v_fract_f32_e32 v135, v113
	v_cos_f32_e32 v113, v135
	v_sin_f32_e32 v137, v135
	v_pk_mul_f32 v[138:139], v[34:35], v[134:135] op_sel_hi:[1,0]
	s_nop 0
	v_pk_mul_f32 v[138:139], v[138:139], v[118:119]
	v_pk_mul_f32 v[118:119], v[38:39], v[134:135] op_sel_hi:[1,0]
	s_nop 0
	v_pk_mul_f32 v[114:115], v[118:119], v[114:115]
	s_nop 0
	v_pk_mul_f32 v[118:119], v[112:113], v[114:115]
	v_pk_mul_f32 v[114:115], v[136:137], v[114:115]
	v_pk_fma_f32 v[118:119], v[136:137], v[138:139], v[118:119]
	v_pk_fma_f32 v[134:135], v[112:113], v[138:139], v[114:115] neg_lo:[0,0,1] neg_hi:[0,0,1]
	v_cndmask_b32_e64 v112, 0, 1, s[72:73]
	v_lshlrev_b64 v[136:137], 11, v[128:129]
	v_cmp_ne_u32_e64 s[4:5], 1, v112
	s_cbranch_vccnz .LBB0_191
	v_lshl_add_u64 v[112:113], s[40:41], 0, v[136:137]
	s_lshl_b32 s72, s19, 1
	s_mov_b32 s73, s7
	v_lshl_add_u64 v[112:113], v[112:113], 0, s[72:73]
	v_lshl_add_u64 v[138:139], v[150:151], 1, v[112:113]
	v_pk_mul_f32 v[114:115], v[126:127], s[54:55] op_sel_hi:[1,0]
	v_pk_mul_f32 v[112:113], v[124:125], s[54:55] op_sel_hi:[1,0]
	v_pk_mul_f32 v[140:141], v[130:131], s[54:55] op_sel_hi:[1,0]
	v_pk_mul_f32 v[142:143], v[134:135], s[54:55] op_sel_hi:[1,0]
	v_cvt_pk_bf16_f32 v112, v112, v113
	v_cvt_pk_bf16_f32 v113, v114, v115
	v_cvt_pk_bf16_f32 v114, v140, v141
	s_mov_b64 s[74:75], 0
	v_cvt_pk_bf16_f32 v115, v142, v143
	global_store_dwordx4 v[138:139], v[112:115], off sc1
	v_lshl_add_u64 v[138:139], v[138:139], 0, s[52:53]
	v_pk_mul_f32 v[140:141], v[116:117], s[54:55] op_sel_hi:[1,0]
	v_pk_mul_f32 v[114:115], v[122:123], s[54:55] op_sel_hi:[1,0]
	v_pk_mul_f32 v[112:113], v[120:121], s[54:55] op_sel_hi:[1,0]
	v_pk_mul_f32 v[142:143], v[118:119], s[54:55] op_sel_hi:[1,0]
	v_cvt_pk_bf16_f32 v112, v112, v113
	v_cvt_pk_bf16_f32 v113, v114, v115
	v_cvt_pk_bf16_f32 v114, v140, v141
	s_nop 0
	v_cvt_pk_bf16_f32 v115, v142, v143
.LBB0_191:
	s_andn2_b64 vcc, exec, s[74:75]
	s_cbranch_vccnz .LBB0_193
	v_lshl_add_u64 v[112:113], s[38:39], 0, v[136:137]
	s_lshl_b32 s72, s19, 1
	s_mov_b32 s73, s7
	v_lshl_add_u64 v[112:113], v[112:113], 0, s[72:73]
	v_lshl_add_u64 v[136:137], v[112:113], 0, v[132:133]
	v_cvt_pk_bf16_f32 v112, v124, v125
	v_cvt_pk_bf16_f32 v113, v126, v127
	v_cvt_pk_bf16_f32 v114, v130, v131
	v_cvt_pk_bf16_f32 v115, v134, v135
	global_store_dwordx4 v[136:137], v[112:115], off sc1
	v_add_u32_e32 v138, 17, v172
	v_cvt_f32_i32_e32 v138, v138
	v_cvt_pk_bf16_f32 v112, v120, v121
	v_cvt_pk_bf16_f32 v113, v122, v123
	v_cvt_pk_bf16_f32 v114, v116, v117
	v_cvt_pk_bf16_f32 v115, v118, v119
	global_store_dwordx4 v[136:137], v[112:115], off offset:256 sc1
	s_nop 1
	v_sub_u32_e32 v112, 0xef, v172
	v_cvt_f32_i32_e32 v112, v112
	v_mul_f32_e64 v113, v138, -v174
	v_mul_f32_e32 v113, 0x3fb8aa3b, v113
	v_exp_f32_e32 v136, v113
	v_mul_f32_e64 v112, v112, -v173
	v_mul_f32_e32 v112, 0x3fb8aa3b, v112
	v_exp_f32_e32 v138, v112
	v_lshl_add_u64 v[112:113], s[6:7], 0, v[128:129]
	v_mov_b64_e32 v[114:115], s[44:45]
	v_mad_u64_u32 v[114:115], s[72:73], v112, s10, v[114:115]
	v_mad_i32_i24 v115, v113, s10, v115
	v_lshl_add_u64 v[128:129], v[114:115], 0, v[132:133]
	v_pk_mul_f32 v[114:115], v[136:137], v[126:127] op_sel_hi:[0,1]
	v_pk_mul_f32 v[112:113], v[136:137], v[124:125] op_sel_hi:[0,1]
	v_pk_mul_f32 v[140:141], v[136:137], v[130:131] op_sel_hi:[0,1]
	v_pk_mul_f32 v[142:143], v[136:137], v[134:135] op_sel_hi:[0,1]
	v_cvt_pk_bf16_f32 v112, v112, v113
	v_cvt_pk_bf16_f32 v113, v114, v115
	v_cvt_pk_bf16_f32 v114, v140, v141
	v_cvt_pk_bf16_f32 v115, v142, v143
	global_store_dwordx4 v[128:129], v[112:115], off offset:512 sc1
; #define GAS __attribute__((address_space(1)))
; __device__ __forceinline__ v4u pack8(const f32x4 a, const f32x4 b) { v4u w; w.x = cvt_pk_bf16(a[0], a[1]); w.y = cvt_pk_bf16(a[2], a[3]); w.z = cvt_pk_bf16(b[0], b[1]); w.w = cvt_pk_bf16(b[2], b[3]); return w; }
; __device__ __forceinline__ float fexp(float x) { return __builtin_amdgcn_exp2f(x * 1.4426950408889634f); }
; __device__ __forceinline__ void cs_rev(float rev, float& c, float& s) { const float f = __builtin_amdgcn_fractf(rev); c = __builtin_amdgcn_cosf(f); s = __builtin_amdgcn_sinf(f); }
;     __device__ __forceinline__ void operator()(AccI& acci, const Unit& u, LAS unsigned char*, int wr, int wc, int fr, int fq) const {
;     ...
;                 const int r = 128 * ai + 64 * wr + 16 * m + fr, tok = pm * 256 + r; const float pos = (float)tok; const float sxr = sx0[tok];
;                 f32x4 o1[2], o2[2];
; #pragma unroll
;                 for (int n = 0; n < 2; ++n)
; #pragma unroll
;                     for (int j = 0; j < 4; ++j) { float c, s; cs_rev(pos * inv[4 * n + j], c, s); const float x1 = ACCF(ai, 0, m, n, j), x2 = ACCF(ai, 1, m, n, j); o1[n][j] = x1 * c - x2 * s; o2[n][j] = x2 * c + x1 * s; }
;                 if (isq) {
;                     bf16* q = qs + (size_t)tok * RW + h * HD + c0; *(GAS v4u*)q = pack8(o1[0], o1[1]); *(GAS v4u*)(q + 128) = pack8(o2[0], o2[1]);
;                     const int il = r; const float wf = fexp(lgf * (float)(il + 1)), wb = fexp(lgb * (float)(255 - il));
;                     bf16* a = Acat + ((size_t)h * T + tok) * CAT + c0;
;                     *(GAS v4u*)(a + 256) = pack8(o1[0] * wf, o1[1] * wf); *(GAS v4u*)(a + 384) = pack8(o2[0] * wf, o2[1] * wf);
;                     *(GAS v4u*)(a + 512) = pack8(o1[0] * wb, o1[1] * wb); *(GAS v4u*)(a + 640) = pack8(o2[0] * wb, o2[1] * wb);
;                 } else {
;                     bf16* k = kk + (size_t)tok * RW + h * HD + c0; *(GAS v4u*)k = pack8(o1[0] * 0.0625f, o1[1] * 0.0625f); *(GAS v4u*)(k + 128) = pack8(o2[0] * 0.0625f, o2[1] * 0.0625f);
	v_pk_mul_f32 v[140:141], v[136:137], v[116:117] op_sel_hi:[0,1]
	v_pk_mul_f32 v[116:117], v[138:139], v[116:117] op_sel_hi:[0,1]
	v_pk_mul_f32 v[114:115], v[136:137], v[122:123] op_sel_hi:[0,1]
	v_pk_mul_f32 v[112:113], v[136:137], v[120:121] op_sel_hi:[0,1]
	v_pk_mul_f32 v[136:137], v[136:137], v[118:119] op_sel_hi:[0,1]
	v_cvt_pk_bf16_f32 v112, v112, v113
	v_cvt_pk_bf16_f32 v113, v114, v115
	v_cvt_pk_bf16_f32 v114, v140, v141
	v_cvt_pk_bf16_f32 v115, v136, v137
	global_store_dwordx4 v[128:129], v[112:115], off offset:768 sc1
	v_pk_mul_f32 v[118:119], v[138:139], v[118:119] op_sel_hi:[0,1]
	s_nop 0
	v_pk_mul_f32 v[114:115], v[138:139], v[126:127] op_sel_hi:[0,1]
	v_pk_mul_f32 v[112:113], v[138:139], v[124:125] op_sel_hi:[0,1]
	v_pk_mul_f32 v[124:125], v[138:139], v[130:131] op_sel_hi:[0,1]
	v_pk_mul_f32 v[126:127], v[138:139], v[134:135] op_sel_hi:[0,1]
	v_cvt_pk_bf16_f32 v112, v112, v113
	v_cvt_pk_bf16_f32 v113, v114, v115
	v_cvt_pk_bf16_f32 v114, v124, v125
	v_cvt_pk_bf16_f32 v115, v126, v127
	global_store_dwordx4 v[128:129], v[112:115], off offset:1024 sc1
	s_nop 1
	v_pk_mul_f32 v[114:115], v[138:139], v[122:123] op_sel_hi:[0,1]
	v_pk_mul_f32 v[112:113], v[138:139], v[120:121] op_sel_hi:[0,1]
	v_lshl_add_u64 v[138:139], v[128:129], 0, s[56:57]
	v_cvt_pk_bf16_f32 v112, v112, v113
	v_cvt_pk_bf16_f32 v113, v114, v115
	v_cvt_pk_bf16_f32 v114, v116, v117
	v_cvt_pk_bf16_f32 v115, v118, v119
.LBB0_193:
	global_store_dwordx4 v[138:139], v[112:115], off sc1
	v_cvt_f32_i32_e32 v109, v109
	v_cvt_f32_i32_e32 v108, v108
	v_add_u32_e32 v112, 32, v144
	v_ashrrev_i32_e32 v113, 31, v112
	v_lshl_add_u64 v[114:115], v[112:113], 2, s[34:35]
	global_load_dword v116, v[114:115], off
	v_cvt_f32_i32_e32 v117, v112
	v_cvt_f32_i32_e32 v105, v105
	v_cvt_f32_i32_e32 v104, v104
	v_cvt_f32_i32_e32 v111, v111
	v_mul_f32_e32 v114, v148, v117
	v_fract_f32_e32 v115, v114
	v_cos_f32_e32 v114, v115
	v_sin_f32_e32 v118, v115
	v_mul_f32_e32 v115, v165, v117
	v_fract_f32_e32 v119, v115
	v_cos_f32_e32 v115, v119
	v_sin_f32_e32 v119, v119
	v_cvt_f32_i32_e32 v110, v110
	v_cvt_f32_i32_e32 v107, v107
	v_cvt_f32_i32_e32 v106, v106
	v_cvt_f32_i32_e32 v101, v101
	v_cvt_f32_i32_e32 v100, v100
	v_cvt_f32_i32_e32 v97, v97
	v_cvt_f32_i32_e32 v96, v96
	v_cvt_f32_i32_e32 v103, v103
	v_cvt_f32_i32_e32 v102, v102
	v_cvt_f32_i32_e32 v99, v99
	v_cvt_f32_i32_e32 v98, v98
	s_mov_b64 s[72:73], -1
	s_and_b64 vcc, exec, s[4:5]
	s_waitcnt vmcnt(0)
	v_pk_mul_f32 v[120:121], v[40:41], v[116:117] op_sel_hi:[1,0]
	s_nop 0
	v_pk_mul_f32 v[108:109], v[120:121], v[108:109]
	v_pk_mul_f32 v[120:121], v[44:45], v[116:117] op_sel_hi:[1,0]
	s_nop 0
	v_pk_mul_f32 v[120:121], v[120:121], v[104:105]
	s_nop 0
	v_pk_mul_f32 v[104:105], v[114:115], v[120:121]
	s_nop 0
	v_pk_fma_f32 v[104:105], v[118:119], v[108:109], v[104:105]
	v_pk_mul_f32 v[118:119], v[118:119], v[120:121]
	v_pk_mul_f32 v[120:121], v[42:43], v[116:117] op_sel_hi:[1,0]
	v_pk_fma_f32 v[108:109], v[114:115], v[108:109], v[118:119] neg_lo:[0,0,1] neg_hi:[0,0,1]
	v_mul_f32_e32 v114, v166, v117
	v_fract_f32_e32 v115, v114
	v_cos_f32_e32 v114, v115
	v_sin_f32_e32 v118, v115
	v_mul_f32_e32 v115, v167, v117
	v_fract_f32_e32 v119, v115
	v_cos_f32_e32 v115, v119
	v_sin_f32_e32 v119, v119
	v_pk_mul_f32 v[110:111], v[120:121], v[110:111]
	v_pk_mul_f32 v[120:121], v[46:47], v[116:117] op_sel_hi:[1,0]
	s_nop 0
	v_pk_mul_f32 v[120:121], v[120:121], v[106:107]
	s_nop 0
	v_pk_mul_f32 v[106:107], v[114:115], v[120:121]
	s_nop 0
	v_pk_fma_f32 v[106:107], v[118:119], v[110:111], v[106:107]
	v_pk_mul_f32 v[118:119], v[118:119], v[120:121]
	v_pk_mul_f32 v[120:121], v[32:33], v[116:117] op_sel_hi:[1,0]
	v_pk_fma_f32 v[110:111], v[114:115], v[110:111], v[118:119] neg_lo:[0,0,1] neg_hi:[0,0,1]
	v_mul_f32_e32 v114, v168, v117
	v_fract_f32_e32 v115, v114
	v_cos_f32_e32 v114, v115
	v_sin_f32_e32 v118, v115
	v_mul_f32_e32 v115, v169, v117
	v_fract_f32_e32 v119, v115
	v_cos_f32_e32 v115, v119
	v_sin_f32_e32 v119, v119
	v_pk_mul_f32 v[120:121], v[120:121], v[100:101]
	v_pk_mul_f32 v[100:101], v[36:37], v[116:117] op_sel_hi:[1,0]
	s_nop 0
	v_pk_mul_f32 v[96:97], v[100:101], v[96:97]
	s_nop 0
	v_pk_mul_f32 v[100:101], v[114:115], v[96:97]
	v_pk_mul_f32 v[96:97], v[118:119], v[96:97]
	v_pk_fma_f32 v[100:101], v[118:119], v[120:121], v[100:101]
	v_pk_fma_f32 v[114:115], v[114:115], v[120:121], v[96:97] neg_lo:[0,0,1] neg_hi:[0,0,1]
	v_mul_f32_e32 v96, v170, v117
	v_fract_f32_e32 v97, v96
	v_cos_f32_e32 v96, v97
	v_sin_f32_e32 v118, v97
	v_mul_f32_e32 v97, v171, v117
	v_fract_f32_e32 v117, v97
	v_cos_f32_e32 v97, v117
	v_sin_f32_e32 v119, v117
	v_pk_mul_f32 v[120:121], v[34:35], v[116:117] op_sel_hi:[1,0]
	s_nop 0
	v_pk_mul_f32 v[120:121], v[120:121], v[102:103]
	v_pk_mul_f32 v[102:103], v[38:39], v[116:117] op_sel_hi:[1,0]
	s_nop 0
	v_pk_mul_f32 v[98:99], v[102:103], v[98:99]
	s_nop 0
	v_pk_mul_f32 v[102:103], v[96:97], v[98:99]
	v_pk_mul_f32 v[98:99], v[118:119], v[98:99]
	v_pk_fma_f32 v[102:103], v[118:119], v[120:121], v[102:103]
	v_pk_fma_f32 v[116:117], v[96:97], v[120:121], v[98:99] neg_lo:[0,0,1] neg_hi:[0,0,1]
	v_lshlrev_b64 v[118:119], 11, v[112:113]
	s_cbranch_vccnz .LBB0_195
	v_lshl_add_u64 v[96:97], s[40:41], 0, v[118:119]
	s_lshl_b32 s72, s19, 1
	s_mov_b32 s73, s7
	v_lshl_add_u64 v[96:97], v[96:97], 0, s[72:73]
	v_lshl_add_u64 v[120:121], v[150:151], 1, v[96:97]
	v_pk_mul_f32 v[98:99], v[110:111], s[54:55] op_sel_hi:[1,0]
	v_pk_mul_f32 v[96:97], v[108:109], s[54:55] op_sel_hi:[1,0]
	v_pk_mul_f32 v[122:123], v[114:115], s[54:55] op_sel_hi:[1,0]
	v_pk_mul_f32 v[124:125], v[116:117], s[54:55] op_sel_hi:[1,0]
	v_cvt_pk_bf16_f32 v96, v96, v97
	v_cvt_pk_bf16_f32 v97, v98, v99
	v_cvt_pk_bf16_f32 v98, v122, v123
	s_mov_b64 s[72:73], 0
	v_cvt_pk_bf16_f32 v99, v124, v125
	global_store_dwordx4 v[120:121], v[96:99], off sc1
	v_lshl_add_u64 v[120:121], v[120:121], 0, s[52:53]
	v_pk_mul_f32 v[122:123], v[100:101], s[54:55] op_sel_hi:[1,0]
	v_pk_mul_f32 v[98:99], v[106:107], s[54:55] op_sel_hi:[1,0]
	v_pk_mul_f32 v[96:97], v[104:105], s[54:55] op_sel_hi:[1,0]
	v_pk_mul_f32 v[124:125], v[102:103], s[54:55] op_sel_hi:[1,0]
	v_cvt_pk_bf16_f32 v96, v96, v97
	v_cvt_pk_bf16_f32 v97, v98, v99
	v_cvt_pk_bf16_f32 v98, v122, v123
	s_nop 0
	v_cvt_pk_bf16_f32 v99, v124, v125
; #define GAS __attribute__((address_space(1)))
; __device__ __forceinline__ v4u pack8(const f32x4 a, const f32x4 b) { v4u w; w.x = cvt_pk_bf16(a[0], a[1]); w.y = cvt_pk_bf16(a[2], a[3]); w.z = cvt_pk_bf16(b[0], b[1]); w.w = cvt_pk_bf16(b[2], b[3]); return w; }
; __device__ __forceinline__ float fexp(float x) { return __builtin_amdgcn_exp2f(x * 1.4426950408889634f); }
; __device__ __forceinline__ void cs_rev(float rev, float& c, float& s) { const float f = __builtin_amdgcn_fractf(rev); c = __builtin_amdgcn_cosf(f); s = __builtin_amdgcn_sinf(f); }
;     __device__ __forceinline__ void operator()(AccI& acci, const Unit& u, LAS unsigned char*, int wr, int wc, int fr, int fq) const {
;     ...
;                 const int r = 128 * ai + 64 * wr + 16 * m + fr, tok = pm * 256 + r; const float pos = (float)tok; const float sxr = sx0[tok];
;                 f32x4 o1[2], o2[2];
; #pragma unroll
;                 for (int n = 0; n < 2; ++n)
; #pragma unroll
;                     for (int j = 0; j < 4; ++j) { float c, s; cs_rev(pos * inv[4 * n + j], c, s); const float x1 = ACCF(ai, 0, m, n, j), x2 = ACCF(ai, 1, m, n, j); o1[n][j] = x1 * c - x2 * s; o2[n][j] = x2 * c + x1 * s; }
;                 if (isq) {
;                     bf16* q = qs + (size_t)tok * RW + h * HD + c0; *(GAS v4u*)q = pack8(o1[0], o1[1]); *(GAS v4u*)(q + 128) = pack8(o2[0], o2[1]);
;                     const int il = r; const float wf = fexp(lgf * (float)(il + 1)), wb = fexp(lgb * (float)(255 - il));
;                     bf16* a = Acat + ((size_t)h * T + tok) * CAT + c0;
;                     *(GAS v4u*)(a + 256) = pack8(o1[0] * wf, o1[1] * wf); *(GAS v4u*)(a + 384) = pack8(o2[0] * wf, o2[1] * wf);
;                     *(GAS v4u*)(a + 512) = pack8(o1[0] * wb, o1[1] * wb); *(GAS v4u*)(a + 640) = pack8(o2[0] * wb, o2[1] * wb);
;                 } else {
;                     bf16* k = kk + (size_t)tok * RW + h * HD + c0; *(GAS v4u*)k = pack8(o1[0] * 0.0625f, o1[1] * 0.0625f); *(GAS v4u*)(k + 128) = pack8(o2[0] * 0.0625f, o2[1] * 0.0625f);
.LBB0_195:
	s_andn2_b64 vcc, exec, s[72:73]
	s_cbranch_vccnz .LBB0_197
	v_lshl_add_u64 v[96:97], s[38:39], 0, v[118:119]
	s_lshl_b32 s72, s19, 1
	s_mov_b32 s73, s7
	v_lshl_add_u64 v[96:97], v[96:97], 0, s[72:73]
	v_lshl_add_u64 v[118:119], v[96:97], 0, v[132:133]
	v_cvt_pk_bf16_f32 v96, v108, v109
	v_cvt_pk_bf16_f32 v97, v110, v111
	v_cvt_pk_bf16_f32 v98, v114, v115
	v_cvt_pk_bf16_f32 v99, v116, v117
	global_store_dwordx4 v[118:119], v[96:99], off sc1
	v_add_u32_e32 v120, 33, v172
	v_cvt_f32_i32_e32 v120, v120
	v_cvt_pk_bf16_f32 v96, v104, v105
	v_cvt_pk_bf16_f32 v97, v106, v107
	v_cvt_pk_bf16_f32 v98, v100, v101
	v_cvt_pk_bf16_f32 v99, v102, v103
	global_store_dwordx4 v[118:119], v[96:99], off offset:256 sc1
	s_nop 1
	v_sub_u32_e32 v96, 0xdf, v172
	v_cvt_f32_i32_e32 v96, v96
	v_mul_f32_e64 v97, v120, -v174
	v_mul_f32_e32 v97, 0x3fb8aa3b, v97
	v_exp_f32_e32 v118, v97
	v_mul_f32_e64 v96, v96, -v173
	v_mul_f32_e32 v96, 0x3fb8aa3b, v96
	v_exp_f32_e32 v120, v96
	v_lshl_add_u64 v[96:97], s[6:7], 0, v[112:113]
	v_mov_b64_e32 v[98:99], s[44:45]
	v_mad_u64_u32 v[98:99], s[72:73], v96, s10, v[98:99]
	v_mad_i32_i24 v99, v97, s10, v99
	v_lshl_add_u64 v[112:113], v[98:99], 0, v[132:133]
	v_pk_mul_f32 v[98:99], v[118:119], v[110:111] op_sel_hi:[0,1]
	v_pk_mul_f32 v[96:97], v[118:119], v[108:109] op_sel_hi:[0,1]
	v_pk_mul_f32 v[122:123], v[118:119], v[114:115] op_sel_hi:[0,1]
	v_pk_mul_f32 v[124:125], v[118:119], v[116:117] op_sel_hi:[0,1]
	v_cvt_pk_bf16_f32 v96, v96, v97
	v_cvt_pk_bf16_f32 v97, v98, v99
	v_cvt_pk_bf16_f32 v98, v122, v123
	v_cvt_pk_bf16_f32 v99, v124, v125
	global_store_dwordx4 v[112:113], v[96:99], off offset:512 sc1
	v_pk_mul_f32 v[122:123], v[118:119], v[100:101] op_sel_hi:[0,1]
	v_pk_mul_f32 v[100:101], v[120:121], v[100:101] op_sel_hi:[0,1]
	v_pk_mul_f32 v[98:99], v[118:119], v[106:107] op_sel_hi:[0,1]
	v_pk_mul_f32 v[96:97], v[118:119], v[104:105] op_sel_hi:[0,1]
	v_pk_mul_f32 v[118:119], v[118:119], v[102:103] op_sel_hi:[0,1]
	v_cvt_pk_bf16_f32 v96, v96, v97
	v_cvt_pk_bf16_f32 v97, v98, v99
	v_cvt_pk_bf16_f32 v98, v122, v123
	v_cvt_pk_bf16_f32 v99, v118, v119
	global_store_dwordx4 v[112:113], v[96:99], off offset:768 sc1
	v_pk_mul_f32 v[102:103], v[120:121], v[102:103] op_sel_hi:[0,1]
	s_nop 0
	v_pk_mul_f32 v[98:99], v[120:121], v[110:111] op_sel_hi:[0,1]
	v_pk_mul_f32 v[96:97], v[120:121], v[108:109] op_sel_hi:[0,1]
	v_pk_mul_f32 v[108:109], v[120:121], v[114:115] op_sel_hi:[0,1]
	v_pk_mul_f32 v[110:111], v[120:121], v[116:117] op_sel_hi:[0,1]
	v_cvt_pk_bf16_f32 v96, v96, v97
	v_cvt_pk_bf16_f32 v97, v98, v99
	v_cvt_pk_bf16_f32 v98, v108, v109
	v_cvt_pk_bf16_f32 v99, v110, v111
	global_store_dwordx4 v[112:113], v[96:99], off offset:1024 sc1
	s_nop 1
	v_pk_mul_f32 v[98:99], v[120:121], v[106:107] op_sel_hi:[0,1]
	v_pk_mul_f32 v[96:97], v[120:121], v[104:105] op_sel_hi:[0,1]
	v_lshl_add_u64 v[120:121], v[112:113], 0, s[56:57]
	v_cvt_pk_bf16_f32 v96, v96, v97
	v_cvt_pk_bf16_f32 v97, v98, v99
	v_cvt_pk_bf16_f32 v98, v100, v101
	v_cvt_pk_bf16_f32 v99, v102, v103
.LBB0_197:
	global_store_dwordx4 v[120:121], v[96:99], off sc1
	v_cvt_f32_i32_e32 v93, v93
	v_cvt_f32_i32_e32 v92, v92
	v_add_u32_e32 v96, 48, v144
	v_ashrrev_i32_e32 v97, 31, v96
	v_lshl_add_u64 v[98:99], v[96:97], 2, s[34:35]
	global_load_dword v100, v[98:99], off
	v_cvt_f32_i32_e32 v101, v96
	v_cvt_f32_i32_e32 v89, v89
	v_cvt_f32_i32_e32 v88, v88
	v_cvt_f32_i32_e32 v95, v95
	v_mul_f32_e32 v98, v148, v101
	v_fract_f32_e32 v99, v98
	v_cos_f32_e32 v98, v99
	v_sin_f32_e32 v102, v99
	v_mul_f32_e32 v99, v165, v101
	v_fract_f32_e32 v103, v99
	v_cos_f32_e32 v99, v103
	v_sin_f32_e32 v103, v103
	v_cvt_f32_i32_e32 v94, v94
	v_cvt_f32_i32_e32 v91, v91
	v_cvt_f32_i32_e32 v90, v90
	v_cvt_f32_i32_e32 v85, v85
	v_cvt_f32_i32_e32 v84, v84
	v_cvt_f32_i32_e32 v81, v81
	v_cvt_f32_i32_e32 v80, v80
	v_cvt_f32_i32_e32 v87, v87
	v_cvt_f32_i32_e32 v86, v86
	v_cvt_f32_i32_e32 v83, v83
	v_cvt_f32_i32_e32 v82, v82
	s_mov_b64 s[72:73], -1
	s_and_b64 vcc, exec, s[4:5]
	s_waitcnt vmcnt(0)
	v_pk_mul_f32 v[104:105], v[40:41], v[100:101] op_sel_hi:[1,0]
	s_nop 0
	v_pk_mul_f32 v[92:93], v[104:105], v[92:93]
	v_pk_mul_f32 v[104:105], v[44:45], v[100:101] op_sel_hi:[1,0]
	s_nop 0
	v_pk_mul_f32 v[104:105], v[104:105], v[88:89]
	s_nop 0
	v_pk_mul_f32 v[88:89], v[98:99], v[104:105]
	s_nop 0
	v_pk_fma_f32 v[88:89], v[102:103], v[92:93], v[88:89]
	v_pk_mul_f32 v[102:103], v[102:103], v[104:105]
	v_pk_mul_f32 v[104:105], v[42:43], v[100:101] op_sel_hi:[1,0]
	v_pk_fma_f32 v[92:93], v[98:99], v[92:93], v[102:103] neg_lo:[0,0,1] neg_hi:[0,0,1]
	v_mul_f32_e32 v98, v166, v101
	v_fract_f32_e32 v99, v98
	v_cos_f32_e32 v98, v99
	v_sin_f32_e32 v102, v99
	v_mul_f32_e32 v99, v167, v101
	v_fract_f32_e32 v103, v99
	v_cos_f32_e32 v99, v103
	v_sin_f32_e32 v103, v103
	v_pk_mul_f32 v[94:95], v[104:105], v[94:95]
	v_pk_mul_f32 v[104:105], v[46:47], v[100:101] op_sel_hi:[1,0]
	s_nop 0
	v_pk_mul_f32 v[104:105], v[104:105], v[90:91]
	s_nop 0
	v_pk_mul_f32 v[90:91], v[98:99], v[104:105]
	s_nop 0
	v_pk_fma_f32 v[90:91], v[102:103], v[94:95], v[90:91]
	v_pk_mul_f32 v[102:103], v[102:103], v[104:105]
	v_pk_mul_f32 v[104:105], v[32:33], v[100:101] op_sel_hi:[1,0]
	v_pk_fma_f32 v[94:95], v[98:99], v[94:95], v[102:103] neg_lo:[0,0,1] neg_hi:[0,0,1]
	v_mul_f32_e32 v98, v168, v101
	v_fract_f32_e32 v99, v98
	v_cos_f32_e32 v98, v99
	v_sin_f32_e32 v102, v99
	v_mul_f32_e32 v99, v169, v101
	v_fract_f32_e32 v103, v99
	v_cos_f32_e32 v99, v103
	v_sin_f32_e32 v103, v103
	v_pk_mul_f32 v[104:105], v[104:105], v[84:85]
	v_pk_mul_f32 v[84:85], v[36:37], v[100:101] op_sel_hi:[1,0]
	s_nop 0
	v_pk_mul_f32 v[80:81], v[84:85], v[80:81]
	s_nop 0
	v_pk_mul_f32 v[84:85], v[98:99], v[80:81]
	v_pk_mul_f32 v[80:81], v[102:103], v[80:81]
	v_pk_fma_f32 v[84:85], v[102:103], v[104:105], v[84:85]
	v_pk_fma_f32 v[98:99], v[98:99], v[104:105], v[80:81] neg_lo:[0,0,1] neg_hi:[0,0,1]
	v_mul_f32_e32 v80, v170, v101
	v_fract_f32_e32 v81, v80
	v_cos_f32_e32 v80, v81
	v_sin_f32_e32 v102, v81
	v_mul_f32_e32 v81, v171, v101
	v_fract_f32_e32 v101, v81
	v_cos_f32_e32 v81, v101
	v_sin_f32_e32 v103, v101
	v_pk_mul_f32 v[104:105], v[34:35], v[100:101] op_sel_hi:[1,0]
	s_nop 0
	v_pk_mul_f32 v[104:105], v[104:105], v[86:87]
	v_pk_mul_f32 v[86:87], v[38:39], v[100:101] op_sel_hi:[1,0]
	s_nop 0
	v_pk_mul_f32 v[82:83], v[86:87], v[82:83]
	s_nop 0
	v_pk_mul_f32 v[86:87], v[80:81], v[82:83]
	v_pk_mul_f32 v[82:83], v[102:103], v[82:83]
	v_pk_fma_f32 v[86:87], v[102:103], v[104:105], v[86:87]
	v_pk_fma_f32 v[100:101], v[80:81], v[104:105], v[82:83] neg_lo:[0,0,1] neg_hi:[0,0,1]
	v_lshlrev_b64 v[102:103], 11, v[96:97]
	s_cbranch_vccnz .LBB0_199
; #define GAS __attribute__((address_space(1)))
; __device__ __forceinline__ v4u pack8(const f32x4 a, const f32x4 b) { v4u w; w.x = cvt_pk_bf16(a[0], a[1]); w.y = cvt_pk_bf16(a[2], a[3]); w.z = cvt_pk_bf16(b[0], b[1]); w.w = cvt_pk_bf16(b[2], b[3]); return w; }
; __device__ __forceinline__ float fexp(float x) { return __builtin_amdgcn_exp2f(x * 1.4426950408889634f); }
; __device__ __forceinline__ void cs_rev(float rev, float& c, float& s) { const float f = __builtin_amdgcn_fractf(rev); c = __builtin_amdgcn_cosf(f); s = __builtin_amdgcn_sinf(f); }
;     __device__ __forceinline__ void operator()(AccI& acci, const Unit& u, LAS unsigned char*, int wr, int wc, int fr, int fq) const {
;     ...
;                 const int r = 128 * ai + 64 * wr + 16 * m + fr, tok = pm * 256 + r; const float pos = (float)tok; const float sxr = sx0[tok];
;                 f32x4 o1[2], o2[2];
; #pragma unroll
;                 for (int n = 0; n < 2; ++n)
; #pragma unroll
;                     for (int j = 0; j < 4; ++j) { float c, s; cs_rev(pos * inv[4 * n + j], c, s); const float x1 = ACCF(ai, 0, m, n, j), x2 = ACCF(ai, 1, m, n, j); o1[n][j] = x1 * c - x2 * s; o2[n][j] = x2 * c + x1 * s; }
;                 if (isq) {
;                     bf16* q = qs + (size_t)tok * RW + h * HD + c0; *(GAS v4u*)q = pack8(o1[0], o1[1]); *(GAS v4u*)(q + 128) = pack8(o2[0], o2[1]);
;                     const int il = r; const float wf = fexp(lgf * (float)(il + 1)), wb = fexp(lgb * (float)(255 - il));
;                     bf16* a = Acat + ((size_t)h * T + tok) * CAT + c0;
;                     *(GAS v4u*)(a + 256) = pack8(o1[0] * wf, o1[1] * wf); *(GAS v4u*)(a + 384) = pack8(o2[0] * wf, o2[1] * wf);
;                     *(GAS v4u*)(a + 512) = pack8(o1[0] * wb, o1[1] * wb); *(GAS v4u*)(a + 640) = pack8(o2[0] * wb, o2[1] * wb);
;                 } else {
;                     bf16* k = kk + (size_t)tok * RW + h * HD + c0; *(GAS v4u*)k = pack8(o1[0] * 0.0625f, o1[1] * 0.0625f); *(GAS v4u*)(k + 128) = pack8(o2[0] * 0.0625f, o2[1] * 0.0625f);
	v_lshl_add_u64 v[80:81], s[40:41], 0, v[102:103]
	s_lshl_b32 s72, s19, 1
	s_mov_b32 s73, s7
	v_lshl_add_u64 v[80:81], v[80:81], 0, s[72:73]
	v_lshl_add_u64 v[104:105], v[150:151], 1, v[80:81]
	v_pk_mul_f32 v[82:83], v[94:95], s[54:55] op_sel_hi:[1,0]
	v_pk_mul_f32 v[80:81], v[92:93], s[54:55] op_sel_hi:[1,0]
	v_pk_mul_f32 v[106:107], v[98:99], s[54:55] op_sel_hi:[1,0]
	v_pk_mul_f32 v[108:109], v[100:101], s[54:55] op_sel_hi:[1,0]
	v_cvt_pk_bf16_f32 v80, v80, v81
	v_cvt_pk_bf16_f32 v81, v82, v83
	v_cvt_pk_bf16_f32 v82, v106, v107
	s_mov_b64 s[72:73], 0
	v_cvt_pk_bf16_f32 v83, v108, v109
	global_store_dwordx4 v[104:105], v[80:83], off sc1
	v_lshl_add_u64 v[104:105], v[104:105], 0, s[52:53]
	v_pk_mul_f32 v[106:107], v[84:85], s[54:55] op_sel_hi:[1,0]
	v_pk_mul_f32 v[82:83], v[90:91], s[54:55] op_sel_hi:[1,0]
	v_pk_mul_f32 v[80:81], v[88:89], s[54:55] op_sel_hi:[1,0]
	v_pk_mul_f32 v[108:109], v[86:87], s[54:55] op_sel_hi:[1,0]
	v_cvt_pk_bf16_f32 v80, v80, v81
	v_cvt_pk_bf16_f32 v81, v82, v83
	v_cvt_pk_bf16_f32 v82, v106, v107
	s_nop 0
	v_cvt_pk_bf16_f32 v83, v108, v109
.LBB0_199:
	s_andn2_b64 vcc, exec, s[72:73]
	s_cbranch_vccnz .LBB0_201
	v_lshl_add_u64 v[80:81], s[38:39], 0, v[102:103]
	s_lshl_b32 s72, s19, 1
	s_mov_b32 s73, s7
	v_lshl_add_u64 v[80:81], v[80:81], 0, s[72:73]
	v_lshl_add_u64 v[102:103], v[80:81], 0, v[132:133]
	v_cvt_pk_bf16_f32 v80, v92, v93
	v_cvt_pk_bf16_f32 v81, v94, v95
	v_cvt_pk_bf16_f32 v82, v98, v99
	v_cvt_pk_bf16_f32 v83, v100, v101
	global_store_dwordx4 v[102:103], v[80:83], off sc1
	v_add_u32_e32 v104, 49, v172
	v_cvt_f32_i32_e32 v104, v104
	v_cvt_pk_bf16_f32 v80, v88, v89
	v_cvt_pk_bf16_f32 v81, v90, v91
	v_cvt_pk_bf16_f32 v82, v84, v85
	v_cvt_pk_bf16_f32 v83, v86, v87
	global_store_dwordx4 v[102:103], v[80:83], off offset:256 sc1
	s_nop 1
	v_sub_u32_e32 v80, 0xcf, v172
	v_cvt_f32_i32_e32 v80, v80
	v_mul_f32_e64 v81, v104, -v174
	v_mul_f32_e32 v81, 0x3fb8aa3b, v81
	v_exp_f32_e32 v102, v81
	v_mul_f32_e64 v80, v80, -v173
	v_mul_f32_e32 v80, 0x3fb8aa3b, v80
	v_exp_f32_e32 v104, v80
	v_lshl_add_u64 v[80:81], s[6:7], 0, v[96:97]
	v_mov_b64_e32 v[82:83], s[44:45]
	v_mad_u64_u32 v[82:83], s[72:73], v80, s10, v[82:83]
	v_mad_i32_i24 v83, v81, s10, v83
	v_lshl_add_u64 v[96:97], v[82:83], 0, v[132:133]
	v_pk_mul_f32 v[82:83], v[102:103], v[94:95] op_sel_hi:[0,1]
	v_pk_mul_f32 v[80:81], v[102:103], v[92:93] op_sel_hi:[0,1]
	v_pk_mul_f32 v[106:107], v[102:103], v[98:99] op_sel_hi:[0,1]
	v_pk_mul_f32 v[108:109], v[102:103], v[100:101] op_sel_hi:[0,1]
	v_cvt_pk_bf16_f32 v80, v80, v81
	v_cvt_pk_bf16_f32 v81, v82, v83
	v_cvt_pk_bf16_f32 v82, v106, v107
	v_cvt_pk_bf16_f32 v83, v108, v109
	global_store_dwordx4 v[96:97], v[80:83], off offset:512 sc1
	v_pk_mul_f32 v[106:107], v[102:103], v[84:85] op_sel_hi:[0,1]
	v_pk_mul_f32 v[84:85], v[104:105], v[84:85] op_sel_hi:[0,1]
	v_pk_mul_f32 v[82:83], v[102:103], v[90:91] op_sel_hi:[0,1]
	v_pk_mul_f32 v[80:81], v[102:103], v[88:89] op_sel_hi:[0,1]
	v_pk_mul_f32 v[102:103], v[102:103], v[86:87] op_sel_hi:[0,1]
	v_cvt_pk_bf16_f32 v80, v80, v81
	v_cvt_pk_bf16_f32 v81, v82, v83
	v_cvt_pk_bf16_f32 v82, v106, v107
	v_cvt_pk_bf16_f32 v83, v102, v103
	global_store_dwordx4 v[96:97], v[80:83], off offset:768 sc1
	v_pk_mul_f32 v[86:87], v[104:105], v[86:87] op_sel_hi:[0,1]
	s_nop 0
	v_pk_mul_f32 v[82:83], v[104:105], v[94:95] op_sel_hi:[0,1]
	v_pk_mul_f32 v[80:81], v[104:105], v[92:93] op_sel_hi:[0,1]
	v_pk_mul_f32 v[92:93], v[104:105], v[98:99] op_sel_hi:[0,1]
	v_pk_mul_f32 v[94:95], v[104:105], v[100:101] op_sel_hi:[0,1]
	v_cvt_pk_bf16_f32 v80, v80, v81
	v_cvt_pk_bf16_f32 v81, v82, v83
	v_cvt_pk_bf16_f32 v82, v92, v93
	v_cvt_pk_bf16_f32 v83, v94, v95
	global_store_dwordx4 v[96:97], v[80:83], off offset:1024 sc1
	s_nop 1
	v_pk_mul_f32 v[82:83], v[104:105], v[90:91] op_sel_hi:[0,1]
	v_pk_mul_f32 v[80:81], v[104:105], v[88:89] op_sel_hi:[0,1]
	v_lshl_add_u64 v[104:105], v[96:97], 0, s[56:57]
	v_cvt_pk_bf16_f32 v80, v80, v81
	v_cvt_pk_bf16_f32 v81, v82, v83
	v_cvt_pk_bf16_f32 v82, v84, v85
	v_cvt_pk_bf16_f32 v83, v86, v87
.LBB0_201:
	global_store_dwordx4 v[104:105], v[80:83], off sc1
	v_cvt_f32_i32_e32 v77, v77
	v_cvt_f32_i32_e32 v76, v76
	v_add_u32_e32 v80, 0x80, v144
	v_ashrrev_i32_e32 v81, 31, v80
	v_lshl_add_u64 v[82:83], v[80:81], 2, s[34:35]
	global_load_dword v84, v[82:83], off
	v_cvt_f32_i32_e32 v85, v80
	v_cvt_f32_i32_e32 v73, v73
	v_cvt_f32_i32_e32 v72, v72
	v_cvt_f32_i32_e32 v79, v79
	v_mul_f32_e32 v82, v148, v85
	v_fract_f32_e32 v83, v82
	v_cos_f32_e32 v82, v83
	v_sin_f32_e32 v86, v83
	v_mul_f32_e32 v83, v165, v85
	v_fract_f32_e32 v87, v83
	v_cos_f32_e32 v83, v87
	v_sin_f32_e32 v87, v87
	v_cvt_f32_i32_e32 v78, v78
	v_cvt_f32_i32_e32 v75, v75
	v_cvt_f32_i32_e32 v74, v74
	v_cvt_f32_i32_e32 v69, v69
	v_cvt_f32_i32_e32 v68, v68
	v_cvt_f32_i32_e32 v65, v65
	v_cvt_f32_i32_e32 v64, v64
	v_cvt_f32_i32_e32 v71, v71
	v_cvt_f32_i32_e32 v70, v70
	v_cvt_f32_i32_e32 v67, v67
	v_cvt_f32_i32_e32 v66, v66
	s_mov_b64 s[72:73], -1
	s_and_b64 vcc, exec, s[4:5]
	s_waitcnt vmcnt(0)
; #define GAS __attribute__((address_space(1)))
; __device__ __forceinline__ v4u pack8(const f32x4 a, const f32x4 b) { v4u w; w.x = cvt_pk_bf16(a[0], a[1]); w.y = cvt_pk_bf16(a[2], a[3]); w.z = cvt_pk_bf16(b[0], b[1]); w.w = cvt_pk_bf16(b[2], b[3]); return w; }
; __device__ __forceinline__ float fexp(float x) { return __builtin_amdgcn_exp2f(x * 1.4426950408889634f); }
; __device__ __forceinline__ void cs_rev(float rev, float& c, float& s) { const float f = __builtin_amdgcn_fractf(rev); c = __builtin_amdgcn_cosf(f); s = __builtin_amdgcn_sinf(f); }
;     __device__ __forceinline__ void operator()(AccI& acci, const Unit& u, LAS unsigned char*, int wr, int wc, int fr, int fq) const {
;     ...
;                 const int r = 128 * ai + 64 * wr + 16 * m + fr, tok = pm * 256 + r; const float pos = (float)tok; const float sxr = sx0[tok];
;                 f32x4 o1[2], o2[2];
; #pragma unroll
;                 for (int n = 0; n < 2; ++n)
; #pragma unroll
;                     for (int j = 0; j < 4; ++j) { float c, s; cs_rev(pos * inv[4 * n + j], c, s); const float x1 = ACCF(ai, 0, m, n, j), x2 = ACCF(ai, 1, m, n, j); o1[n][j] = x1 * c - x2 * s; o2[n][j] = x2 * c + x1 * s; }
;                 if (isq) {
;                     bf16* q = qs + (size_t)tok * RW + h * HD + c0; *(GAS v4u*)q = pack8(o1[0], o1[1]); *(GAS v4u*)(q + 128) = pack8(o2[0], o2[1]);
;                     const int il = r; const float wf = fexp(lgf * (float)(il + 1)), wb = fexp(lgb * (float)(255 - il));
;                     bf16* a = Acat + ((size_t)h * T + tok) * CAT + c0;
;                     *(GAS v4u*)(a + 256) = pack8(o1[0] * wf, o1[1] * wf); *(GAS v4u*)(a + 384) = pack8(o2[0] * wf, o2[1] * wf);
;                     *(GAS v4u*)(a + 512) = pack8(o1[0] * wb, o1[1] * wb); *(GAS v4u*)(a + 640) = pack8(o2[0] * wb, o2[1] * wb);
;                 } else {
;                     bf16* k = kk + (size_t)tok * RW + h * HD + c0; *(GAS v4u*)k = pack8(o1[0] * 0.0625f, o1[1] * 0.0625f); *(GAS v4u*)(k + 128) = pack8(o2[0] * 0.0625f, o2[1] * 0.0625f);
	v_pk_mul_f32 v[88:89], v[40:41], v[84:85] op_sel_hi:[1,0]
	s_nop 0
	v_pk_mul_f32 v[76:77], v[88:89], v[76:77]
	v_pk_mul_f32 v[88:89], v[44:45], v[84:85] op_sel_hi:[1,0]
	s_nop 0
	v_pk_mul_f32 v[88:89], v[88:89], v[72:73]
	s_nop 0
	v_pk_mul_f32 v[72:73], v[82:83], v[88:89]
	s_nop 0
	v_pk_fma_f32 v[72:73], v[86:87], v[76:77], v[72:73]
	v_pk_mul_f32 v[86:87], v[86:87], v[88:89]
	v_pk_mul_f32 v[88:89], v[42:43], v[84:85] op_sel_hi:[1,0]
	v_pk_fma_f32 v[76:77], v[82:83], v[76:77], v[86:87] neg_lo:[0,0,1] neg_hi:[0,0,1]
	v_mul_f32_e32 v82, v166, v85
	v_fract_f32_e32 v83, v82
	v_cos_f32_e32 v82, v83
	v_sin_f32_e32 v86, v83
	v_mul_f32_e32 v83, v167, v85
	v_fract_f32_e32 v87, v83
	v_cos_f32_e32 v83, v87
	v_sin_f32_e32 v87, v87
	v_pk_mul_f32 v[78:79], v[88:89], v[78:79]
	v_pk_mul_f32 v[88:89], v[46:47], v[84:85] op_sel_hi:[1,0]
	s_nop 0
	v_pk_mul_f32 v[88:89], v[88:89], v[74:75]
	s_nop 0
	v_pk_mul_f32 v[74:75], v[82:83], v[88:89]
	s_nop 0
	v_pk_fma_f32 v[74:75], v[86:87], v[78:79], v[74:75]
	v_pk_mul_f32 v[86:87], v[86:87], v[88:89]
	v_pk_mul_f32 v[88:89], v[32:33], v[84:85] op_sel_hi:[1,0]
	v_pk_fma_f32 v[78:79], v[82:83], v[78:79], v[86:87] neg_lo:[0,0,1] neg_hi:[0,0,1]
	v_mul_f32_e32 v82, v168, v85
	v_fract_f32_e32 v83, v82
	v_cos_f32_e32 v82, v83
	v_sin_f32_e32 v86, v83
	v_mul_f32_e32 v83, v169, v85
	v_fract_f32_e32 v87, v83
	v_cos_f32_e32 v83, v87
	v_sin_f32_e32 v87, v87
	v_pk_mul_f32 v[88:89], v[88:89], v[68:69]
	v_pk_mul_f32 v[68:69], v[36:37], v[84:85] op_sel_hi:[1,0]
	s_nop 0
	v_pk_mul_f32 v[64:65], v[68:69], v[64:65]
	s_nop 0
	v_pk_mul_f32 v[68:69], v[82:83], v[64:65]
	v_pk_mul_f32 v[64:65], v[86:87], v[64:65]
	v_pk_fma_f32 v[68:69], v[86:87], v[88:89], v[68:69]
	v_pk_fma_f32 v[82:83], v[82:83], v[88:89], v[64:65] neg_lo:[0,0,1] neg_hi:[0,0,1]
	v_mul_f32_e32 v64, v170, v85
	v_fract_f32_e32 v65, v64
	v_cos_f32_e32 v64, v65
	v_sin_f32_e32 v86, v65
	v_mul_f32_e32 v65, v171, v85
	v_fract_f32_e32 v85, v65
	v_cos_f32_e32 v65, v85
	v_sin_f32_e32 v87, v85
	v_pk_mul_f32 v[88:89], v[34:35], v[84:85] op_sel_hi:[1,0]
	s_nop 0
	v_pk_mul_f32 v[88:89], v[88:89], v[70:71]
	v_pk_mul_f32 v[70:71], v[38:39], v[84:85] op_sel_hi:[1,0]
	s_nop 0
	v_pk_mul_f32 v[66:67], v[70:71], v[66:67]
	s_nop 0
	v_pk_mul_f32 v[70:71], v[64:65], v[66:67]
	v_pk_mul_f32 v[66:67], v[86:87], v[66:67]
	v_pk_fma_f32 v[70:71], v[86:87], v[88:89], v[70:71]
	v_pk_fma_f32 v[84:85], v[64:65], v[88:89], v[66:67] neg_lo:[0,0,1] neg_hi:[0,0,1]
	v_lshlrev_b64 v[86:87], 11, v[80:81]
	s_cbranch_vccnz .LBB0_203
	v_lshl_add_u64 v[64:65], s[40:41], 0, v[86:87]
	s_lshl_b32 s72, s19, 1
	s_mov_b32 s73, s7
	v_lshl_add_u64 v[64:65], v[64:65], 0, s[72:73]
	v_lshl_add_u64 v[88:89], v[150:151], 1, v[64:65]
	v_pk_mul_f32 v[66:67], v[78:79], s[54:55] op_sel_hi:[1,0]
	v_pk_mul_f32 v[64:65], v[76:77], s[54:55] op_sel_hi:[1,0]
	v_pk_mul_f32 v[90:91], v[82:83], s[54:55] op_sel_hi:[1,0]
	v_pk_mul_f32 v[92:93], v[84:85], s[54:55] op_sel_hi:[1,0]
	v_cvt_pk_bf16_f32 v64, v64, v65
	v_cvt_pk_bf16_f32 v65, v66, v67
	v_cvt_pk_bf16_f32 v66, v90, v91
	s_mov_b64 s[72:73], 0
	v_cvt_pk_bf16_f32 v67, v92, v93
	global_store_dwordx4 v[88:89], v[64:67], off sc1
	v_lshl_add_u64 v[88:89], v[88:89], 0, s[52:53]
	v_pk_mul_f32 v[90:91], v[68:69], s[54:55] op_sel_hi:[1,0]
	v_pk_mul_f32 v[66:67], v[74:75], s[54:55] op_sel_hi:[1,0]
	v_pk_mul_f32 v[64:65], v[72:73], s[54:55] op_sel_hi:[1,0]
	v_pk_mul_f32 v[92:93], v[70:71], s[54:55] op_sel_hi:[1,0]
	v_cvt_pk_bf16_f32 v64, v64, v65
	v_cvt_pk_bf16_f32 v65, v66, v67
	v_cvt_pk_bf16_f32 v66, v90, v91
	s_nop 0
	v_cvt_pk_bf16_f32 v67, v92, v93
.LBB0_203:
	s_andn2_b64 vcc, exec, s[72:73]
	s_cbranch_vccnz .LBB0_205
	v_lshl_add_u64 v[64:65], s[38:39], 0, v[86:87]
	s_lshl_b32 s72, s19, 1
	s_mov_b32 s73, s7
	v_lshl_add_u64 v[64:65], v[64:65], 0, s[72:73]
	v_lshl_add_u64 v[86:87], v[64:65], 0, v[132:133]
	v_cvt_pk_bf16_f32 v64, v76, v77
	v_cvt_pk_bf16_f32 v65, v78, v79
	v_cvt_pk_bf16_f32 v66, v82, v83
	v_cvt_pk_bf16_f32 v67, v84, v85
	global_store_dwordx4 v[86:87], v[64:67], off sc1
	v_add_u32_e32 v88, 0x81, v172
	v_cvt_f32_i32_e32 v88, v88
	v_cvt_pk_bf16_f32 v64, v72, v73
	v_cvt_pk_bf16_f32 v65, v74, v75
	v_cvt_pk_bf16_f32 v66, v68, v69
	v_cvt_pk_bf16_f32 v67, v70, v71
	global_store_dwordx4 v[86:87], v[64:67], off offset:256 sc1
	s_nop 1
	v_sub_u32_e32 v64, 0x7f, v172
	v_cvt_f32_i32_e32 v64, v64
	v_mul_f32_e64 v65, v88, -v174
	v_mul_f32_e32 v65, 0x3fb8aa3b, v65
	v_exp_f32_e32 v86, v65
	v_mul_f32_e64 v64, v64, -v173
	v_mul_f32_e32 v64, 0x3fb8aa3b, v64
	v_exp_f32_e32 v88, v64
	v_lshl_add_u64 v[64:65], s[6:7], 0, v[80:81]
	v_mov_b64_e32 v[66:67], s[44:45]
	v_mad_u64_u32 v[66:67], s[72:73], v64, s10, v[66:67]
	v_mad_i32_i24 v67, v65, s10, v67
	v_lshl_add_u64 v[80:81], v[66:67], 0, v[132:133]
	v_pk_mul_f32 v[66:67], v[86:87], v[78:79] op_sel_hi:[0,1]
	v_pk_mul_f32 v[64:65], v[86:87], v[76:77] op_sel_hi:[0,1]
	v_pk_mul_f32 v[90:91], v[86:87], v[82:83] op_sel_hi:[0,1]
	v_pk_mul_f32 v[92:93], v[86:87], v[84:85] op_sel_hi:[0,1]
	v_cvt_pk_bf16_f32 v64, v64, v65
	v_cvt_pk_bf16_f32 v65, v66, v67
	v_cvt_pk_bf16_f32 v66, v90, v91
	v_cvt_pk_bf16_f32 v67, v92, v93
	global_store_dwordx4 v[80:81], v[64:67], off offset:512 sc1
	v_pk_mul_f32 v[90:91], v[86:87], v[68:69] op_sel_hi:[0,1]
	v_pk_mul_f32 v[68:69], v[88:89], v[68:69] op_sel_hi:[0,1]
	v_pk_mul_f32 v[66:67], v[86:87], v[74:75] op_sel_hi:[0,1]
	v_pk_mul_f32 v[64:65], v[86:87], v[72:73] op_sel_hi:[0,1]
	v_pk_mul_f32 v[86:87], v[86:87], v[70:71] op_sel_hi:[0,1]
	v_cvt_pk_bf16_f32 v64, v64, v65
	v_cvt_pk_bf16_f32 v65, v66, v67
	v_cvt_pk_bf16_f32 v66, v90, v91
	v_cvt_pk_bf16_f32 v67, v86, v87
	global_store_dwordx4 v[80:81], v[64:67], off offset:768 sc1
	v_pk_mul_f32 v[70:71], v[88:89], v[70:71] op_sel_hi:[0,1]
	s_nop 0
	v_pk_mul_f32 v[66:67], v[88:89], v[78:79] op_sel_hi:[0,1]
	v_pk_mul_f32 v[64:65], v[88:89], v[76:77] op_sel_hi:[0,1]
	v_pk_mul_f32 v[76:77], v[88:89], v[82:83] op_sel_hi:[0,1]
	v_pk_mul_f32 v[78:79], v[88:89], v[84:85] op_sel_hi:[0,1]
	v_cvt_pk_bf16_f32 v64, v64, v65
	v_cvt_pk_bf16_f32 v65, v66, v67
	v_cvt_pk_bf16_f32 v66, v76, v77
	v_cvt_pk_bf16_f32 v67, v78, v79
	global_store_dwordx4 v[80:81], v[64:67], off offset:1024 sc1
	s_nop 1
	v_pk_mul_f32 v[66:67], v[88:89], v[74:75] op_sel_hi:[0,1]
	v_pk_mul_f32 v[64:65], v[88:89], v[72:73] op_sel_hi:[0,1]
	v_lshl_add_u64 v[88:89], v[80:81], 0, s[56:57]
	v_cvt_pk_bf16_f32 v64, v64, v65
	v_cvt_pk_bf16_f32 v65, v66, v67
	v_cvt_pk_bf16_f32 v66, v68, v69
	v_cvt_pk_bf16_f32 v67, v70, v71
; #define GAS __attribute__((address_space(1)))
; __device__ __forceinline__ v4u pack8(const f32x4 a, const f32x4 b) { v4u w; w.x = cvt_pk_bf16(a[0], a[1]); w.y = cvt_pk_bf16(a[2], a[3]); w.z = cvt_pk_bf16(b[0], b[1]); w.w = cvt_pk_bf16(b[2], b[3]); return w; }
; __device__ __forceinline__ float fexp(float x) { return __builtin_amdgcn_exp2f(x * 1.4426950408889634f); }
; __device__ __forceinline__ void cs_rev(float rev, float& c, float& s) { const float f = __builtin_amdgcn_fractf(rev); c = __builtin_amdgcn_cosf(f); s = __builtin_amdgcn_sinf(f); }
;     __device__ __forceinline__ void operator()(AccI& acci, const Unit& u, LAS unsigned char*, int wr, int wc, int fr, int fq) const {
;     ...
;                 const int r = 128 * ai + 64 * wr + 16 * m + fr, tok = pm * 256 + r; const float pos = (float)tok; const float sxr = sx0[tok];
;                 f32x4 o1[2], o2[2];
; #pragma unroll
;                 for (int n = 0; n < 2; ++n)
; #pragma unroll
;                     for (int j = 0; j < 4; ++j) { float c, s; cs_rev(pos * inv[4 * n + j], c, s); const float x1 = ACCF(ai, 0, m, n, j), x2 = ACCF(ai, 1, m, n, j); o1[n][j] = x1 * c - x2 * s; o2[n][j] = x2 * c + x1 * s; }
;                 if (isq) {
;                     bf16* q = qs + (size_t)tok * RW + h * HD + c0; *(GAS v4u*)q = pack8(o1[0], o1[1]); *(GAS v4u*)(q + 128) = pack8(o2[0], o2[1]);
;                     const int il = r; const float wf = fexp(lgf * (float)(il + 1)), wb = fexp(lgb * (float)(255 - il));
;                     bf16* a = Acat + ((size_t)h * T + tok) * CAT + c0;
;                     *(GAS v4u*)(a + 256) = pack8(o1[0] * wf, o1[1] * wf); *(GAS v4u*)(a + 384) = pack8(o2[0] * wf, o2[1] * wf);
;                     *(GAS v4u*)(a + 512) = pack8(o1[0] * wb, o1[1] * wb); *(GAS v4u*)(a + 640) = pack8(o2[0] * wb, o2[1] * wb);
;                 } else {
;                     bf16* k = kk + (size_t)tok * RW + h * HD + c0; *(GAS v4u*)k = pack8(o1[0] * 0.0625f, o1[1] * 0.0625f); *(GAS v4u*)(k + 128) = pack8(o2[0] * 0.0625f, o2[1] * 0.0625f);
.LBB0_205:
	global_store_dwordx4 v[88:89], v[64:67], off sc1
	v_cvt_f32_i32_e32 v61, v61
	v_cvt_f32_i32_e32 v60, v60
	v_add_u32_e32 v64, 0x90, v144
	v_ashrrev_i32_e32 v65, 31, v64
	v_lshl_add_u64 v[66:67], v[64:65], 2, s[34:35]
	global_load_dword v68, v[66:67], off
	v_cvt_f32_i32_e32 v69, v64
	v_cvt_f32_i32_e32 v57, v57
	v_cvt_f32_i32_e32 v56, v56
	v_cvt_f32_i32_e32 v63, v63
	v_mul_f32_e32 v66, v148, v69
	v_fract_f32_e32 v67, v66
	v_cos_f32_e32 v66, v67
	v_sin_f32_e32 v70, v67
	v_mul_f32_e32 v67, v165, v69
	v_fract_f32_e32 v71, v67
	v_cos_f32_e32 v67, v71
	v_sin_f32_e32 v71, v71
	v_cvt_f32_i32_e32 v62, v62
	v_cvt_f32_i32_e32 v59, v59
	v_cvt_f32_i32_e32 v58, v58
	v_cvt_f32_i32_e32 v53, v53
	v_cvt_f32_i32_e32 v52, v52
	v_cvt_f32_i32_e32 v49, v49
	v_cvt_f32_i32_e32 v48, v48
	v_cvt_f32_i32_e32 v55, v55
	v_cvt_f32_i32_e32 v54, v54
	v_cvt_f32_i32_e32 v51, v51
	v_cvt_f32_i32_e32 v50, v50
	s_mov_b64 s[72:73], -1
	s_and_b64 vcc, exec, s[4:5]
	s_waitcnt vmcnt(0)
	v_pk_mul_f32 v[72:73], v[40:41], v[68:69] op_sel_hi:[1,0]
	s_nop 0
	v_pk_mul_f32 v[60:61], v[72:73], v[60:61]
	v_pk_mul_f32 v[72:73], v[44:45], v[68:69] op_sel_hi:[1,0]
	s_nop 0
	v_pk_mul_f32 v[72:73], v[72:73], v[56:57]
	s_nop 0
	v_pk_mul_f32 v[56:57], v[66:67], v[72:73]
	s_nop 0
	v_pk_fma_f32 v[56:57], v[70:71], v[60:61], v[56:57]
	v_pk_mul_f32 v[70:71], v[70:71], v[72:73]
	v_pk_mul_f32 v[72:73], v[42:43], v[68:69] op_sel_hi:[1,0]
	v_pk_fma_f32 v[60:61], v[66:67], v[60:61], v[70:71] neg_lo:[0,0,1] neg_hi:[0,0,1]
	v_mul_f32_e32 v66, v166, v69
	v_fract_f32_e32 v67, v66
	v_cos_f32_e32 v66, v67
	v_sin_f32_e32 v70, v67
	v_mul_f32_e32 v67, v167, v69
	v_fract_f32_e32 v71, v67
	v_cos_f32_e32 v67, v71
	v_sin_f32_e32 v71, v71
	v_pk_mul_f32 v[62:63], v[72:73], v[62:63]
	v_pk_mul_f32 v[72:73], v[46:47], v[68:69] op_sel_hi:[1,0]
	s_nop 0
	v_pk_mul_f32 v[72:73], v[72:73], v[58:59]
	s_nop 0
	v_pk_mul_f32 v[58:59], v[66:67], v[72:73]
	s_nop 0
	v_pk_fma_f32 v[58:59], v[70:71], v[62:63], v[58:59]
	v_pk_mul_f32 v[70:71], v[70:71], v[72:73]
	v_pk_mul_f32 v[72:73], v[32:33], v[68:69] op_sel_hi:[1,0]
	v_pk_fma_f32 v[62:63], v[66:67], v[62:63], v[70:71] neg_lo:[0,0,1] neg_hi:[0,0,1]
	v_mul_f32_e32 v66, v168, v69
	v_fract_f32_e32 v67, v66
	v_cos_f32_e32 v66, v67
	v_sin_f32_e32 v70, v67
	v_mul_f32_e32 v67, v169, v69
	v_fract_f32_e32 v71, v67
	v_cos_f32_e32 v67, v71
	v_sin_f32_e32 v71, v71
	v_pk_mul_f32 v[72:73], v[72:73], v[52:53]
	v_pk_mul_f32 v[52:53], v[36:37], v[68:69] op_sel_hi:[1,0]
	s_nop 0
	v_pk_mul_f32 v[48:49], v[52:53], v[48:49]
	s_nop 0
	v_pk_mul_f32 v[52:53], v[66:67], v[48:49]
	v_pk_mul_f32 v[48:49], v[70:71], v[48:49]
	v_pk_fma_f32 v[52:53], v[70:71], v[72:73], v[52:53]
	v_pk_fma_f32 v[66:67], v[66:67], v[72:73], v[48:49] neg_lo:[0,0,1] neg_hi:[0,0,1]
	v_mul_f32_e32 v48, v170, v69
	v_fract_f32_e32 v49, v48
	v_cos_f32_e32 v48, v49
	v_sin_f32_e32 v70, v49
	v_mul_f32_e32 v49, v171, v69
	v_fract_f32_e32 v69, v49
	v_cos_f32_e32 v49, v69
	v_sin_f32_e32 v71, v69
	v_pk_mul_f32 v[72:73], v[34:35], v[68:69] op_sel_hi:[1,0]
	s_nop 0
	v_pk_mul_f32 v[72:73], v[72:73], v[54:55]
	v_pk_mul_f32 v[54:55], v[38:39], v[68:69] op_sel_hi:[1,0]
	s_nop 0
	v_pk_mul_f32 v[50:51], v[54:55], v[50:51]
	s_nop 0
	v_pk_mul_f32 v[54:55], v[48:49], v[50:51]
	v_pk_mul_f32 v[50:51], v[70:71], v[50:51]
	v_pk_fma_f32 v[54:55], v[70:71], v[72:73], v[54:55]
	v_pk_fma_f32 v[68:69], v[48:49], v[72:73], v[50:51] neg_lo:[0,0,1] neg_hi:[0,0,1]
	v_lshlrev_b64 v[70:71], 11, v[64:65]
	s_cbranch_vccnz .LBB0_207
	v_lshl_add_u64 v[48:49], s[40:41], 0, v[70:71]
	s_lshl_b32 s72, s19, 1
	s_mov_b32 s73, s7
	v_lshl_add_u64 v[48:49], v[48:49], 0, s[72:73]
	v_lshl_add_u64 v[72:73], v[150:151], 1, v[48:49]
	v_pk_mul_f32 v[50:51], v[62:63], s[54:55] op_sel_hi:[1,0]
	v_pk_mul_f32 v[48:49], v[60:61], s[54:55] op_sel_hi:[1,0]
	v_pk_mul_f32 v[74:75], v[66:67], s[54:55] op_sel_hi:[1,0]
	v_pk_mul_f32 v[76:77], v[68:69], s[54:55] op_sel_hi:[1,0]
	v_cvt_pk_bf16_f32 v48, v48, v49
	v_cvt_pk_bf16_f32 v49, v50, v51
	v_cvt_pk_bf16_f32 v50, v74, v75
	s_mov_b64 s[72:73], 0
	v_cvt_pk_bf16_f32 v51, v76, v77
	global_store_dwordx4 v[72:73], v[48:51], off sc1
	v_lshl_add_u64 v[72:73], v[72:73], 0, s[52:53]
	v_pk_mul_f32 v[74:75], v[52:53], s[54:55] op_sel_hi:[1,0]
	v_pk_mul_f32 v[50:51], v[58:59], s[54:55] op_sel_hi:[1,0]
	v_pk_mul_f32 v[48:49], v[56:57], s[54:55] op_sel_hi:[1,0]
	v_pk_mul_f32 v[76:77], v[54:55], s[54:55] op_sel_hi:[1,0]
	v_cvt_pk_bf16_f32 v48, v48, v49
	v_cvt_pk_bf16_f32 v49, v50, v51
	v_cvt_pk_bf16_f32 v50, v74, v75
	s_nop 0
	v_cvt_pk_bf16_f32 v51, v76, v77
; #define GAS __attribute__((address_space(1)))
; __device__ __forceinline__ v4u pack8(const f32x4 a, const f32x4 b) { v4u w; w.x = cvt_pk_bf16(a[0], a[1]); w.y = cvt_pk_bf16(a[2], a[3]); w.z = cvt_pk_bf16(b[0], b[1]); w.w = cvt_pk_bf16(b[2], b[3]); return w; }
; __device__ __forceinline__ float fexp(float x) { return __builtin_amdgcn_exp2f(x * 1.4426950408889634f); }
; __device__ __forceinline__ void cs_rev(float rev, float& c, float& s) { const float f = __builtin_amdgcn_fractf(rev); c = __builtin_amdgcn_cosf(f); s = __builtin_amdgcn_sinf(f); }
;     __device__ __forceinline__ void operator()(AccI& acci, const Unit& u, LAS unsigned char*, int wr, int wc, int fr, int fq) const {
;     ...
;                 const int r = 128 * ai + 64 * wr + 16 * m + fr, tok = pm * 256 + r; const float pos = (float)tok; const float sxr = sx0[tok];
;                 f32x4 o1[2], o2[2];
; #pragma unroll
;                 for (int n = 0; n < 2; ++n)
; #pragma unroll
;                     for (int j = 0; j < 4; ++j) { float c, s; cs_rev(pos * inv[4 * n + j], c, s); const float x1 = ACCF(ai, 0, m, n, j), x2 = ACCF(ai, 1, m, n, j); o1[n][j] = x1 * c - x2 * s; o2[n][j] = x2 * c + x1 * s; }
;                 if (isq) {
;                     bf16* q = qs + (size_t)tok * RW + h * HD + c0; *(GAS v4u*)q = pack8(o1[0], o1[1]); *(GAS v4u*)(q + 128) = pack8(o2[0], o2[1]);
;                     const int il = r; const float wf = fexp(lgf * (float)(il + 1)), wb = fexp(lgb * (float)(255 - il));
;                     bf16* a = Acat + ((size_t)h * T + tok) * CAT + c0;
;                     *(GAS v4u*)(a + 256) = pack8(o1[0] * wf, o1[1] * wf); *(GAS v4u*)(a + 384) = pack8(o2[0] * wf, o2[1] * wf);
;                     *(GAS v4u*)(a + 512) = pack8(o1[0] * wb, o1[1] * wb); *(GAS v4u*)(a + 640) = pack8(o2[0] * wb, o2[1] * wb);
;                 } else {
;                     bf16* k = kk + (size_t)tok * RW + h * HD + c0; *(GAS v4u*)k = pack8(o1[0] * 0.0625f, o1[1] * 0.0625f); *(GAS v4u*)(k + 128) = pack8(o2[0] * 0.0625f, o2[1] * 0.0625f);
.LBB0_207:
	s_andn2_b64 vcc, exec, s[72:73]
	s_cbranch_vccnz .LBB0_209
	v_lshl_add_u64 v[48:49], s[38:39], 0, v[70:71]
	s_lshl_b32 s72, s19, 1
	s_mov_b32 s73, s7
	v_lshl_add_u64 v[48:49], v[48:49], 0, s[72:73]
	v_lshl_add_u64 v[70:71], v[48:49], 0, v[132:133]
	v_cvt_pk_bf16_f32 v48, v60, v61
	v_cvt_pk_bf16_f32 v49, v62, v63
	v_cvt_pk_bf16_f32 v50, v66, v67
	v_cvt_pk_bf16_f32 v51, v68, v69
	global_store_dwordx4 v[70:71], v[48:51], off sc1
	v_add_u32_e32 v72, 0x91, v172
	v_cvt_f32_i32_e32 v72, v72
	v_cvt_pk_bf16_f32 v48, v56, v57
	v_cvt_pk_bf16_f32 v49, v58, v59
	v_cvt_pk_bf16_f32 v50, v52, v53
	v_cvt_pk_bf16_f32 v51, v54, v55
	global_store_dwordx4 v[70:71], v[48:51], off offset:256 sc1
	s_nop 1
	v_sub_u32_e32 v48, 0x6f, v172
	v_cvt_f32_i32_e32 v48, v48
	v_mul_f32_e64 v49, v72, -v174
	v_mul_f32_e32 v49, 0x3fb8aa3b, v49
	v_exp_f32_e32 v70, v49
	v_mul_f32_e64 v48, v48, -v173
	v_mul_f32_e32 v48, 0x3fb8aa3b, v48
	v_exp_f32_e32 v72, v48
	v_lshl_add_u64 v[48:49], s[6:7], 0, v[64:65]
	v_mov_b64_e32 v[50:51], s[44:45]
	v_mad_u64_u32 v[50:51], s[72:73], v48, s10, v[50:51]
	v_mad_i32_i24 v51, v49, s10, v51
	v_lshl_add_u64 v[64:65], v[50:51], 0, v[132:133]
	v_pk_mul_f32 v[50:51], v[70:71], v[62:63] op_sel_hi:[0,1]
	v_pk_mul_f32 v[48:49], v[70:71], v[60:61] op_sel_hi:[0,1]
	v_pk_mul_f32 v[74:75], v[70:71], v[66:67] op_sel_hi:[0,1]
	v_pk_mul_f32 v[76:77], v[70:71], v[68:69] op_sel_hi:[0,1]
	v_cvt_pk_bf16_f32 v48, v48, v49
	v_cvt_pk_bf16_f32 v49, v50, v51
	v_cvt_pk_bf16_f32 v50, v74, v75
	v_cvt_pk_bf16_f32 v51, v76, v77
	global_store_dwordx4 v[64:65], v[48:51], off offset:512 sc1
	v_pk_mul_f32 v[74:75], v[70:71], v[52:53] op_sel_hi:[0,1]
	v_pk_mul_f32 v[52:53], v[72:73], v[52:53] op_sel_hi:[0,1]
	v_pk_mul_f32 v[50:51], v[70:71], v[58:59] op_sel_hi:[0,1]
	v_pk_mul_f32 v[48:49], v[70:71], v[56:57] op_sel_hi:[0,1]
	v_pk_mul_f32 v[70:71], v[70:71], v[54:55] op_sel_hi:[0,1]
	v_cvt_pk_bf16_f32 v48, v48, v49
	v_cvt_pk_bf16_f32 v49, v50, v51
	v_cvt_pk_bf16_f32 v50, v74, v75
	v_cvt_pk_bf16_f32 v51, v70, v71
	global_store_dwordx4 v[64:65], v[48:51], off offset:768 sc1
	v_pk_mul_f32 v[54:55], v[72:73], v[54:55] op_sel_hi:[0,1]
	s_nop 0
	v_pk_mul_f32 v[50:51], v[72:73], v[62:63] op_sel_hi:[0,1]
	v_pk_mul_f32 v[48:49], v[72:73], v[60:61] op_sel_hi:[0,1]
	v_pk_mul_f32 v[60:61], v[72:73], v[66:67] op_sel_hi:[0,1]
	v_pk_mul_f32 v[62:63], v[72:73], v[68:69] op_sel_hi:[0,1]
	v_cvt_pk_bf16_f32 v48, v48, v49
	v_cvt_pk_bf16_f32 v49, v50, v51
	v_cvt_pk_bf16_f32 v50, v60, v61
	v_cvt_pk_bf16_f32 v51, v62, v63
	global_store_dwordx4 v[64:65], v[48:51], off offset:1024 sc1
	s_nop 1
	v_pk_mul_f32 v[50:51], v[72:73], v[58:59] op_sel_hi:[0,1]
	v_pk_mul_f32 v[48:49], v[72:73], v[56:57] op_sel_hi:[0,1]
	v_lshl_add_u64 v[72:73], v[64:65], 0, s[56:57]
	v_cvt_pk_bf16_f32 v48, v48, v49
	v_cvt_pk_bf16_f32 v49, v50, v51
	v_cvt_pk_bf16_f32 v50, v52, v53
	v_cvt_pk_bf16_f32 v51, v54, v55
.LBB0_209:
	global_store_dwordx4 v[72:73], v[48:51], off sc1
	v_cvt_f32_i32_e32 v29, v29
	v_cvt_f32_i32_e32 v28, v28
	v_add_u32_e32 v48, 0xa0, v144
	v_ashrrev_i32_e32 v49, 31, v48
	v_lshl_add_u64 v[50:51], v[48:49], 2, s[34:35]
	global_load_dword v52, v[50:51], off
	v_cvt_f32_i32_e32 v53, v48
	v_cvt_f32_i32_e32 v25, v25
	v_cvt_f32_i32_e32 v24, v24
	v_cvt_f32_i32_e32 v31, v31
	v_mul_f32_e32 v50, v148, v53
	v_fract_f32_e32 v51, v50
	v_cos_f32_e32 v50, v51
	v_sin_f32_e32 v54, v51
	v_mul_f32_e32 v51, v165, v53
	v_fract_f32_e32 v55, v51
	v_cos_f32_e32 v51, v55
	v_sin_f32_e32 v55, v55
	v_cvt_f32_i32_e32 v30, v30
	v_cvt_f32_i32_e32 v27, v27
	v_cvt_f32_i32_e32 v26, v26
	v_cvt_f32_i32_e32 v21, v21
	v_cvt_f32_i32_e32 v20, v20
	v_cvt_f32_i32_e32 v17, v17
	v_cvt_f32_i32_e32 v16, v16
	v_cvt_f32_i32_e32 v23, v23
	v_cvt_f32_i32_e32 v22, v22
	v_cvt_f32_i32_e32 v19, v19
	v_cvt_f32_i32_e32 v18, v18
	s_mov_b64 s[72:73], -1
	s_and_b64 vcc, exec, s[4:5]
	s_waitcnt vmcnt(0)
	v_pk_mul_f32 v[56:57], v[40:41], v[52:53] op_sel_hi:[1,0]
	s_nop 0
	v_pk_mul_f32 v[28:29], v[56:57], v[28:29]
	v_pk_mul_f32 v[56:57], v[44:45], v[52:53] op_sel_hi:[1,0]
	s_nop 0
	v_pk_mul_f32 v[56:57], v[56:57], v[24:25]
	s_nop 0
	v_pk_mul_f32 v[24:25], v[50:51], v[56:57]
	s_nop 0
	v_pk_fma_f32 v[24:25], v[54:55], v[28:29], v[24:25]
	v_pk_mul_f32 v[54:55], v[54:55], v[56:57]
	v_pk_mul_f32 v[56:57], v[42:43], v[52:53] op_sel_hi:[1,0]
	v_pk_fma_f32 v[28:29], v[50:51], v[28:29], v[54:55] neg_lo:[0,0,1] neg_hi:[0,0,1]
	v_mul_f32_e32 v50, v166, v53
	v_fract_f32_e32 v51, v50
	v_cos_f32_e32 v50, v51
	v_sin_f32_e32 v54, v51
	v_mul_f32_e32 v51, v167, v53
	v_fract_f32_e32 v55, v51
	v_cos_f32_e32 v51, v55
	v_sin_f32_e32 v55, v55
	v_pk_mul_f32 v[30:31], v[56:57], v[30:31]
	v_pk_mul_f32 v[56:57], v[46:47], v[52:53] op_sel_hi:[1,0]
	s_nop 0
	v_pk_mul_f32 v[56:57], v[56:57], v[26:27]
	s_nop 0
	v_pk_mul_f32 v[26:27], v[50:51], v[56:57]
	s_nop 0
	v_pk_fma_f32 v[26:27], v[54:55], v[30:31], v[26:27]
	v_pk_mul_f32 v[54:55], v[54:55], v[56:57]
	v_pk_mul_f32 v[56:57], v[32:33], v[52:53] op_sel_hi:[1,0]
	v_pk_fma_f32 v[30:31], v[50:51], v[30:31], v[54:55] neg_lo:[0,0,1] neg_hi:[0,0,1]
	v_mul_f32_e32 v50, v168, v53
	v_fract_f32_e32 v51, v50
	v_cos_f32_e32 v50, v51
	v_sin_f32_e32 v54, v51
	v_mul_f32_e32 v51, v169, v53
	v_fract_f32_e32 v55, v51
	v_cos_f32_e32 v51, v55
	v_sin_f32_e32 v55, v55
	v_pk_mul_f32 v[56:57], v[56:57], v[20:21]
	v_pk_mul_f32 v[20:21], v[36:37], v[52:53] op_sel_hi:[1,0]
	s_nop 0
	v_pk_mul_f32 v[16:17], v[20:21], v[16:17]
	s_nop 0
	v_pk_mul_f32 v[20:21], v[50:51], v[16:17]
	v_pk_mul_f32 v[16:17], v[54:55], v[16:17]
	v_pk_fma_f32 v[20:21], v[54:55], v[56:57], v[20:21]
	v_pk_fma_f32 v[50:51], v[50:51], v[56:57], v[16:17] neg_lo:[0,0,1] neg_hi:[0,0,1]
	v_mul_f32_e32 v16, v170, v53
	v_fract_f32_e32 v17, v16
	v_cos_f32_e32 v16, v17
	v_sin_f32_e32 v54, v17
	v_mul_f32_e32 v17, v171, v53
	v_fract_f32_e32 v53, v17
	v_cos_f32_e32 v17, v53
	v_sin_f32_e32 v55, v53
	v_pk_mul_f32 v[56:57], v[34:35], v[52:53] op_sel_hi:[1,0]
	s_nop 0
	v_pk_mul_f32 v[56:57], v[56:57], v[22:23]
	v_pk_mul_f32 v[22:23], v[38:39], v[52:53] op_sel_hi:[1,0]
	s_nop 0
	v_pk_mul_f32 v[18:19], v[22:23], v[18:19]
	s_nop 0
	v_pk_mul_f32 v[22:23], v[16:17], v[18:19]
	v_pk_mul_f32 v[18:19], v[54:55], v[18:19]
	v_pk_fma_f32 v[22:23], v[54:55], v[56:57], v[22:23]
	v_pk_fma_f32 v[52:53], v[16:17], v[56:57], v[18:19] neg_lo:[0,0,1] neg_hi:[0,0,1]
	v_lshlrev_b64 v[54:55], 11, v[48:49]
	s_cbranch_vccnz .LBB0_211
; #define GAS __attribute__((address_space(1)))
; __device__ __forceinline__ v4u pack8(const f32x4 a, const f32x4 b) { v4u w; w.x = cvt_pk_bf16(a[0], a[1]); w.y = cvt_pk_bf16(a[2], a[3]); w.z = cvt_pk_bf16(b[0], b[1]); w.w = cvt_pk_bf16(b[2], b[3]); return w; }
; __device__ __forceinline__ float fexp(float x) { return __builtin_amdgcn_exp2f(x * 1.4426950408889634f); }
; __device__ __forceinline__ void cs_rev(float rev, float& c, float& s) { const float f = __builtin_amdgcn_fractf(rev); c = __builtin_amdgcn_cosf(f); s = __builtin_amdgcn_sinf(f); }
;     __device__ __forceinline__ void operator()(AccI& acci, const Unit& u, LAS unsigned char*, int wr, int wc, int fr, int fq) const {
;     ...
;                 const int r = 128 * ai + 64 * wr + 16 * m + fr, tok = pm * 256 + r; const float pos = (float)tok; const float sxr = sx0[tok];
;                 f32x4 o1[2], o2[2];
; #pragma unroll
;                 for (int n = 0; n < 2; ++n)
; #pragma unroll
;                     for (int j = 0; j < 4; ++j) { float c, s; cs_rev(pos * inv[4 * n + j], c, s); const float x1 = ACCF(ai, 0, m, n, j), x2 = ACCF(ai, 1, m, n, j); o1[n][j] = x1 * c - x2 * s; o2[n][j] = x2 * c + x1 * s; }
;                 if (isq) {
;                     bf16* q = qs + (size_t)tok * RW + h * HD + c0; *(GAS v4u*)q = pack8(o1[0], o1[1]); *(GAS v4u*)(q + 128) = pack8(o2[0], o2[1]);
;                     const int il = r; const float wf = fexp(lgf * (float)(il + 1)), wb = fexp(lgb * (float)(255 - il));
;                     bf16* a = Acat + ((size_t)h * T + tok) * CAT + c0;
;                     *(GAS v4u*)(a + 256) = pack8(o1[0] * wf, o1[1] * wf); *(GAS v4u*)(a + 384) = pack8(o2[0] * wf, o2[1] * wf);
;                     *(GAS v4u*)(a + 512) = pack8(o1[0] * wb, o1[1] * wb); *(GAS v4u*)(a + 640) = pack8(o2[0] * wb, o2[1] * wb);
;                 } else {
;                     bf16* k = kk + (size_t)tok * RW + h * HD + c0; *(GAS v4u*)k = pack8(o1[0] * 0.0625f, o1[1] * 0.0625f); *(GAS v4u*)(k + 128) = pack8(o2[0] * 0.0625f, o2[1] * 0.0625f);
	v_lshl_add_u64 v[16:17], s[40:41], 0, v[54:55]
	s_lshl_b32 s72, s19, 1
	s_mov_b32 s73, s7
	v_lshl_add_u64 v[16:17], v[16:17], 0, s[72:73]
	v_lshl_add_u64 v[56:57], v[150:151], 1, v[16:17]
	v_pk_mul_f32 v[18:19], v[30:31], s[54:55] op_sel_hi:[1,0]
	v_pk_mul_f32 v[16:17], v[28:29], s[54:55] op_sel_hi:[1,0]
	v_pk_mul_f32 v[58:59], v[50:51], s[54:55] op_sel_hi:[1,0]
	v_pk_mul_f32 v[60:61], v[52:53], s[54:55] op_sel_hi:[1,0]
	v_cvt_pk_bf16_f32 v16, v16, v17
	v_cvt_pk_bf16_f32 v17, v18, v19
	v_cvt_pk_bf16_f32 v18, v58, v59
	s_mov_b64 s[72:73], 0
	v_cvt_pk_bf16_f32 v19, v60, v61
	global_store_dwordx4 v[56:57], v[16:19], off sc1
	v_lshl_add_u64 v[56:57], v[56:57], 0, s[52:53]
	v_pk_mul_f32 v[58:59], v[20:21], s[54:55] op_sel_hi:[1,0]
	v_pk_mul_f32 v[18:19], v[26:27], s[54:55] op_sel_hi:[1,0]
	v_pk_mul_f32 v[16:17], v[24:25], s[54:55] op_sel_hi:[1,0]
	v_pk_mul_f32 v[60:61], v[22:23], s[54:55] op_sel_hi:[1,0]
	v_cvt_pk_bf16_f32 v16, v16, v17
	v_cvt_pk_bf16_f32 v17, v18, v19
	v_cvt_pk_bf16_f32 v18, v58, v59
	s_nop 0
	v_cvt_pk_bf16_f32 v19, v60, v61
.LBB0_211:
	s_andn2_b64 vcc, exec, s[72:73]
	s_cbranch_vccnz .LBB0_213
	v_lshl_add_u64 v[16:17], s[38:39], 0, v[54:55]
	s_lshl_b32 s72, s19, 1
	s_mov_b32 s73, s7
	v_lshl_add_u64 v[16:17], v[16:17], 0, s[72:73]
	v_lshl_add_u64 v[54:55], v[16:17], 0, v[132:133]
	v_cvt_pk_bf16_f32 v16, v28, v29
	v_cvt_pk_bf16_f32 v17, v30, v31
	v_cvt_pk_bf16_f32 v18, v50, v51
	v_cvt_pk_bf16_f32 v19, v52, v53
	global_store_dwordx4 v[54:55], v[16:19], off sc1
	v_add_u32_e32 v56, 0xa1, v172
	v_cvt_f32_i32_e32 v56, v56
	v_cvt_pk_bf16_f32 v16, v24, v25
	v_cvt_pk_bf16_f32 v17, v26, v27
	v_cvt_pk_bf16_f32 v18, v20, v21
	v_cvt_pk_bf16_f32 v19, v22, v23
	global_store_dwordx4 v[54:55], v[16:19], off offset:256 sc1
	s_nop 1
	v_sub_u32_e32 v16, 0x5f, v172
	v_cvt_f32_i32_e32 v16, v16
	v_mul_f32_e64 v17, v56, -v174
	v_mul_f32_e32 v17, 0x3fb8aa3b, v17
	v_exp_f32_e32 v54, v17
	v_mul_f32_e64 v16, v16, -v173
	v_mul_f32_e32 v16, 0x3fb8aa3b, v16
	v_exp_f32_e32 v56, v16
	v_lshl_add_u64 v[16:17], s[6:7], 0, v[48:49]
	v_mov_b64_e32 v[18:19], s[44:45]
	v_mad_u64_u32 v[18:19], s[72:73], v16, s10, v[18:19]
	v_mad_i32_i24 v19, v17, s10, v19
	v_lshl_add_u64 v[48:49], v[18:19], 0, v[132:133]
	v_pk_mul_f32 v[18:19], v[54:55], v[30:31] op_sel_hi:[0,1]
	v_pk_mul_f32 v[16:17], v[54:55], v[28:29] op_sel_hi:[0,1]
	v_pk_mul_f32 v[58:59], v[54:55], v[50:51] op_sel_hi:[0,1]
	v_pk_mul_f32 v[60:61], v[54:55], v[52:53] op_sel_hi:[0,1]
	v_cvt_pk_bf16_f32 v16, v16, v17
	v_cvt_pk_bf16_f32 v17, v18, v19
	v_cvt_pk_bf16_f32 v18, v58, v59
	v_cvt_pk_bf16_f32 v19, v60, v61
	global_store_dwordx4 v[48:49], v[16:19], off offset:512 sc1
	v_pk_mul_f32 v[58:59], v[54:55], v[20:21] op_sel_hi:[0,1]
	v_pk_mul_f32 v[20:21], v[56:57], v[20:21] op_sel_hi:[0,1]
	v_pk_mul_f32 v[18:19], v[54:55], v[26:27] op_sel_hi:[0,1]
	v_pk_mul_f32 v[16:17], v[54:55], v[24:25] op_sel_hi:[0,1]
	v_pk_mul_f32 v[54:55], v[54:55], v[22:23] op_sel_hi:[0,1]
	v_cvt_pk_bf16_f32 v16, v16, v17
	v_cvt_pk_bf16_f32 v17, v18, v19
	v_cvt_pk_bf16_f32 v18, v58, v59
	v_cvt_pk_bf16_f32 v19, v54, v55
	global_store_dwordx4 v[48:49], v[16:19], off offset:768 sc1
	v_pk_mul_f32 v[22:23], v[56:57], v[22:23] op_sel_hi:[0,1]
	s_nop 0
	v_pk_mul_f32 v[18:19], v[56:57], v[30:31] op_sel_hi:[0,1]
	v_pk_mul_f32 v[16:17], v[56:57], v[28:29] op_sel_hi:[0,1]
	v_pk_mul_f32 v[28:29], v[56:57], v[50:51] op_sel_hi:[0,1]
	v_pk_mul_f32 v[30:31], v[56:57], v[52:53] op_sel_hi:[0,1]
	v_cvt_pk_bf16_f32 v16, v16, v17
	v_cvt_pk_bf16_f32 v17, v18, v19
	v_cvt_pk_bf16_f32 v18, v28, v29
	v_cvt_pk_bf16_f32 v19, v30, v31
	global_store_dwordx4 v[48:49], v[16:19], off offset:1024 sc1
	s_nop 1
	v_pk_mul_f32 v[18:19], v[56:57], v[26:27] op_sel_hi:[0,1]
	v_pk_mul_f32 v[16:17], v[56:57], v[24:25] op_sel_hi:[0,1]
	v_lshl_add_u64 v[56:57], v[48:49], 0, s[56:57]
	v_cvt_pk_bf16_f32 v16, v16, v17
	v_cvt_pk_bf16_f32 v17, v18, v19
	v_cvt_pk_bf16_f32 v18, v20, v21
	v_cvt_pk_bf16_f32 v19, v22, v23
.LBB0_213:
	global_store_dwordx4 v[56:57], v[16:19], off sc1
	v_cvt_f32_i32_e32 v9, v9
	v_cvt_f32_i32_e32 v8, v8
	v_add_u32_e32 v16, 0xb0, v144
	v_ashrrev_i32_e32 v17, 31, v16
	v_lshl_add_u64 v[18:19], v[16:17], 2, s[34:35]
	global_load_dword v20, v[18:19], off
	v_cvt_f32_i32_e32 v21, v16
	v_cvt_f32_i32_e32 v11, v11
	v_cvt_f32_i32_e32 v10, v10
	v_cvt_f32_i32_e32 v1, v1
	v_mul_f32_e32 v22, v148, v21
	v_mul_f32_e32 v23, v165, v21
	v_mul_f32_e32 v24, v166, v21
	v_mul_f32_e32 v25, v167, v21
	v_mul_f32_e32 v26, v168, v21
	v_mul_f32_e32 v27, v169, v21
	v_mul_f32_e32 v28, v170, v21
	v_mul_f32_e32 v21, v171, v21
	v_cvt_f32_i32_e32 v0, v0
	v_cvt_f32_i32_e32 v3, v3
	v_cvt_f32_i32_e32 v2, v2
	v_fract_f32_e32 v29, v22
	v_fract_f32_e32 v30, v23
	v_fract_f32_e32 v31, v24
	v_fract_f32_e32 v48, v25
	v_fract_f32_e32 v49, v26
	v_fract_f32_e32 v50, v27
	v_fract_f32_e32 v51, v28
	v_fract_f32_e32 v21, v21
	v_cvt_f32_i32_e32 v13, v13
	v_cvt_f32_i32_e32 v12, v12
	v_cvt_f32_i32_e32 v15, v15
	v_cvt_f32_i32_e32 v14, v14
	v_cvt_f32_i32_e32 v5, v5
	v_cvt_f32_i32_e32 v4, v4
	v_cvt_f32_i32_e32 v7, v7
	v_cvt_f32_i32_e32 v6, v6
	v_cos_f32_e32 v22, v29
	v_sin_f32_e32 v24, v29
	v_cos_f32_e32 v23, v30
	v_sin_f32_e32 v25, v30
	v_cos_f32_e32 v26, v31
	v_sin_f32_e32 v28, v31
	v_cos_f32_e32 v27, v48
	v_sin_f32_e32 v29, v48
	v_cos_f32_e32 v30, v49
	v_sin_f32_e32 v48, v49
	v_cos_f32_e32 v31, v50
	v_sin_f32_e32 v49, v50
	v_cos_f32_e32 v50, v51
	v_sin_f32_e32 v52, v51
	v_cos_f32_e32 v51, v21
	v_sin_f32_e32 v53, v21
	v_lshlrev_b64 v[18:19], 11, v[16:17]
	s_and_b64 vcc, exec, s[4:5]
	s_mov_b64 s[4:5], -1
	s_waitcnt vmcnt(0)
; #define GAS __attribute__((address_space(1)))
; __device__ __forceinline__ v4u pack8(const f32x4 a, const f32x4 b) { v4u w; w.x = cvt_pk_bf16(a[0], a[1]); w.y = cvt_pk_bf16(a[2], a[3]); w.z = cvt_pk_bf16(b[0], b[1]); w.w = cvt_pk_bf16(b[2], b[3]); return w; }
; __device__ __forceinline__ float fexp(float x) { return __builtin_amdgcn_exp2f(x * 1.4426950408889634f); }
; __device__ __forceinline__ void cs_rev(float rev, float& c, float& s) { const float f = __builtin_amdgcn_fractf(rev); c = __builtin_amdgcn_cosf(f); s = __builtin_amdgcn_sinf(f); }
;     __device__ __forceinline__ void operator()(AccI& acci, const Unit& u, LAS unsigned char*, int wr, int wc, int fr, int fq) const {
;     ...
;                 const int r = 128 * ai + 64 * wr + 16 * m + fr, tok = pm * 256 + r; const float pos = (float)tok; const float sxr = sx0[tok];
;                 f32x4 o1[2], o2[2];
; #pragma unroll
;                 for (int n = 0; n < 2; ++n)
; #pragma unroll
;                     for (int j = 0; j < 4; ++j) { float c, s; cs_rev(pos * inv[4 * n + j], c, s); const float x1 = ACCF(ai, 0, m, n, j), x2 = ACCF(ai, 1, m, n, j); o1[n][j] = x1 * c - x2 * s; o2[n][j] = x2 * c + x1 * s; }
;                 if (isq) {
;                     bf16* q = qs + (size_t)tok * RW + h * HD + c0; *(GAS v4u*)q = pack8(o1[0], o1[1]); *(GAS v4u*)(q + 128) = pack8(o2[0], o2[1]);
;                     const int il = r; const float wf = fexp(lgf * (float)(il + 1)), wb = fexp(lgb * (float)(255 - il));
;                     bf16* a = Acat + ((size_t)h * T + tok) * CAT + c0;
;                     *(GAS v4u*)(a + 256) = pack8(o1[0] * wf, o1[1] * wf); *(GAS v4u*)(a + 384) = pack8(o2[0] * wf, o2[1] * wf);
;                     *(GAS v4u*)(a + 512) = pack8(o1[0] * wb, o1[1] * wb); *(GAS v4u*)(a + 640) = pack8(o2[0] * wb, o2[1] * wb);
;                 } else {
;                     bf16* k = kk + (size_t)tok * RW + h * HD + c0; *(GAS v4u*)k = pack8(o1[0] * 0.0625f, o1[1] * 0.0625f); *(GAS v4u*)(k + 128) = pack8(o2[0] * 0.0625f, o2[1] * 0.0625f);
;                 }
	v_pk_mul_f32 v[40:41], v[40:41], v[20:21] op_sel_hi:[1,0]
	v_pk_mul_f32 v[44:45], v[44:45], v[20:21] op_sel_hi:[1,0]
	v_pk_mul_f32 v[42:43], v[42:43], v[20:21] op_sel_hi:[1,0]
	v_pk_mul_f32 v[46:47], v[46:47], v[20:21] op_sel_hi:[1,0]
	v_pk_mul_f32 v[32:33], v[32:33], v[20:21] op_sel_hi:[1,0]
	v_pk_mul_f32 v[36:37], v[36:37], v[20:21] op_sel_hi:[1,0]
	v_pk_mul_f32 v[34:35], v[34:35], v[20:21] op_sel_hi:[1,0]
	v_pk_mul_f32 v[20:21], v[38:39], v[20:21] op_sel_hi:[1,0]
	v_pk_mul_f32 v[8:9], v[44:45], v[8:9]
	v_pk_mul_f32 v[10:11], v[46:47], v[10:11]
	v_pk_mul_f32 v[0:1], v[36:37], v[0:1]
	v_pk_mul_f32 v[2:3], v[20:21], v[2:3]
	v_pk_mul_f32 v[12:13], v[40:41], v[12:13]
	v_pk_mul_f32 v[14:15], v[42:43], v[14:15]
	v_pk_mul_f32 v[32:33], v[32:33], v[4:5]
	v_pk_mul_f32 v[34:35], v[34:35], v[6:7]
	v_pk_mul_f32 v[4:5], v[22:23], v[8:9]
	v_pk_mul_f32 v[6:7], v[24:25], v[8:9]
	v_pk_mul_f32 v[20:21], v[26:27], v[10:11]
	v_pk_mul_f32 v[10:11], v[28:29], v[10:11]
	v_pk_mul_f32 v[36:37], v[30:31], v[0:1]
	v_pk_mul_f32 v[38:39], v[48:49], v[0:1]
	v_pk_mul_f32 v[40:41], v[50:51], v[2:3]
	v_pk_mul_f32 v[42:43], v[52:53], v[2:3]
	v_pk_fma_f32 v[0:1], v[24:25], v[12:13], v[4:5]
	v_pk_fma_f32 v[8:9], v[22:23], v[12:13], v[6:7] neg_lo:[0,0,1] neg_hi:[0,0,1]
	v_pk_fma_f32 v[2:3], v[28:29], v[14:15], v[20:21]
	v_pk_fma_f32 v[12:13], v[26:27], v[14:15], v[10:11] neg_lo:[0,0,1] neg_hi:[0,0,1]
	v_pk_fma_f32 v[4:5], v[48:49], v[32:33], v[36:37]
	v_pk_fma_f32 v[10:11], v[30:31], v[32:33], v[38:39] neg_lo:[0,0,1] neg_hi:[0,0,1]
	v_pk_fma_f32 v[6:7], v[52:53], v[34:35], v[40:41]
	v_pk_fma_f32 v[14:15], v[50:51], v[34:35], v[42:43] neg_lo:[0,0,1] neg_hi:[0,0,1]
	s_cbranch_vccnz .LBB0_215
	v_lshl_add_u64 v[20:21], s[40:41], 0, v[18:19]
	s_lshl_b32 s4, s19, 1
	s_mov_b32 s5, s7
	v_lshl_add_u64 v[20:21], v[20:21], 0, s[4:5]
	v_lshl_add_u64 v[24:25], v[150:151], 1, v[20:21]
	v_pk_mul_f32 v[22:23], v[12:13], s[54:55] op_sel_hi:[1,0]
	v_pk_mul_f32 v[20:21], v[8:9], s[54:55] op_sel_hi:[1,0]
	v_pk_mul_f32 v[26:27], v[10:11], s[54:55] op_sel_hi:[1,0]
	v_pk_mul_f32 v[28:29], v[14:15], s[54:55] op_sel_hi:[1,0]
	v_cvt_pk_bf16_f32 v20, v20, v21
	v_cvt_pk_bf16_f32 v21, v22, v23
	v_cvt_pk_bf16_f32 v22, v26, v27
	v_lshl_add_u64 v[152:153], v[24:25], 0, s[52:53]
	v_cvt_pk_bf16_f32 v23, v28, v29
	s_mov_b64 s[4:5], 0
	global_store_dwordx4 v[24:25], v[20:23], off sc1
	v_pk_mul_f32 v[26:27], v[4:5], s[54:55] op_sel_hi:[1,0]
	v_pk_mul_f32 v[28:29], v[6:7], s[54:55] op_sel_hi:[1,0]
	v_pk_mul_f32 v[20:21], v[2:3], s[54:55] op_sel_hi:[1,0]
	v_pk_mul_f32 v[22:23], v[0:1], s[54:55] op_sel_hi:[1,0]
	s_nop 0
	v_cvt_pk_bf16_f32 v144, v22, v23
	v_cvt_pk_bf16_f32 v145, v20, v21
	v_cvt_pk_bf16_f32 v146, v26, v27
	v_cvt_pk_bf16_f32 v147, v28, v29
.LBB0_215:
	s_andn2_b64 vcc, exec, s[4:5]
	s_cbranch_vccnz .LBB0_217
	v_lshl_add_u64 v[18:19], s[38:39], 0, v[18:19]
	s_lshl_b32 s4, s19, 1
	s_mov_b32 s5, s7
	v_lshl_add_u64 v[18:19], v[18:19], 0, s[4:5]
	v_lshl_add_u64 v[22:23], v[18:19], 0, v[132:133]
	v_cvt_pk_bf16_f32 v18, v8, v9
	v_cvt_pk_bf16_f32 v19, v12, v13
	v_cvt_pk_bf16_f32 v20, v10, v11
	v_cvt_pk_bf16_f32 v21, v14, v15
	global_store_dwordx4 v[22:23], v[18:21], off sc1
	v_add_u32_e32 v24, 0xb1, v172
	v_cvt_f32_i32_e32 v24, v24
	v_cvt_pk_bf16_f32 v18, v0, v1
	v_cvt_pk_bf16_f32 v19, v2, v3
	v_cvt_pk_bf16_f32 v20, v4, v5
	v_cvt_pk_bf16_f32 v21, v6, v7
	global_store_dwordx4 v[22:23], v[18:21], off offset:256 sc1
	v_lshl_add_u64 v[16:17], s[6:7], 0, v[16:17]
	s_nop 0
	v_sub_u32_e32 v18, 0x4f, v172
	v_cvt_f32_i32_e32 v18, v18
	v_mul_f32_e64 v19, v24, -v174
	v_mul_f32_e32 v19, 0x3fb8aa3b, v19
	v_exp_f32_e32 v20, v19
	v_mul_f32_e64 v18, v18, -v173
	v_mul_f32_e32 v18, 0x3fb8aa3b, v18
	v_exp_f32_e32 v22, v18
	v_mov_b64_e32 v[18:19], s[44:45]
	v_mad_u64_u32 v[18:19], s[4:5], v16, s10, v[18:19]
	v_mad_i32_i24 v19, v17, s10, v19
	v_lshl_add_u64 v[24:25], v[18:19], 0, v[132:133]
	v_pk_mul_f32 v[18:19], v[20:21], v[12:13] op_sel_hi:[0,1]
	v_pk_mul_f32 v[16:17], v[20:21], v[8:9] op_sel_hi:[0,1]
	v_pk_mul_f32 v[26:27], v[20:21], v[10:11] op_sel_hi:[0,1]
	v_pk_mul_f32 v[28:29], v[20:21], v[14:15] op_sel_hi:[0,1]
	v_cvt_pk_bf16_f32 v16, v16, v17
	v_cvt_pk_bf16_f32 v17, v18, v19
	v_cvt_pk_bf16_f32 v18, v26, v27
	v_cvt_pk_bf16_f32 v19, v28, v29
	global_store_dwordx4 v[24:25], v[16:19], off offset:512 sc1
	v_pk_mul_f32 v[8:9], v[22:23], v[8:9] op_sel_hi:[0,1]
	v_pk_mul_f32 v[10:11], v[22:23], v[10:11] op_sel_hi:[0,1]
	v_pk_mul_f32 v[18:19], v[20:21], v[2:3] op_sel_hi:[0,1]
	v_pk_mul_f32 v[16:17], v[20:21], v[0:1] op_sel_hi:[0,1]
	v_lshl_add_u64 v[152:153], v[24:25], 0, s[56:57]
	v_pk_mul_f32 v[26:27], v[20:21], v[4:5] op_sel_hi:[0,1]
	v_pk_mul_f32 v[20:21], v[20:21], v[6:7] op_sel_hi:[0,1]
	v_cvt_pk_bf16_f32 v16, v16, v17
	v_cvt_pk_bf16_f32 v17, v18, v19
	v_cvt_pk_bf16_f32 v18, v26, v27
	v_cvt_pk_bf16_f32 v19, v20, v21
	global_store_dwordx4 v[24:25], v[16:19], off offset:768 sc1
	v_pk_mul_f32 v[12:13], v[22:23], v[12:13] op_sel_hi:[0,1]
	v_pk_mul_f32 v[14:15], v[22:23], v[14:15] op_sel_hi:[0,1]
	v_cvt_pk_bf16_f32 v8, v8, v9
	v_cvt_pk_bf16_f32 v9, v12, v13
	v_cvt_pk_bf16_f32 v10, v10, v11
	v_cvt_pk_bf16_f32 v11, v14, v15
	global_store_dwordx4 v[24:25], v[8:11], off offset:1024 sc1
	v_pk_mul_f32 v[2:3], v[22:23], v[2:3] op_sel_hi:[0,1]
	v_pk_mul_f32 v[0:1], v[22:23], v[0:1] op_sel_hi:[0,1]
	v_pk_mul_f32 v[4:5], v[22:23], v[4:5] op_sel_hi:[0,1]
	v_pk_mul_f32 v[6:7], v[22:23], v[6:7] op_sel_hi:[0,1]
	v_cvt_pk_bf16_f32 v144, v0, v1
	v_cvt_pk_bf16_f32 v145, v2, v3
	v_cvt_pk_bf16_f32 v146, v4, v5
	v_cvt_pk_bf16_f32 v147, v6, v7
.LBB0_217:
	s_andn2_b64 vcc, exec, s[60:61]
	s_mov_b64 s[4:5], -1
	global_store_dwordx4 v[152:153], v[144:147], off sc1
	s_cbranch_vccnz .LBB0_166
	s_andn2_b64 vcc, exec, s[8:9]
	s_cbranch_vccnz .LBB0_165
	s_barrier
	s_branch .LBB0_165

; #define GAS __attribute__((address_space(1)))
; #define LAS __attribute__((address_space(3)))
; __device__ __forceinline__ v4u pack8(const f32x4 a, const f32x4 b) { v4u w; w.x = cvt_pk_bf16(a[0], a[1]); w.y = cvt_pk_bf16(a[2], a[3]); w.z = cvt_pk_bf16(b[0], b[1]); w.w = cvt_pk_bf16(b[2], b[3]); return w; }
; #define EPI_LOOP_AM for (int ai = 0; ai < 2; ++ai) _Pragma("unroll") for (int m = 0; m < 4; ++m)
;     __device__ __forceinline__ void operator()(AccI& acc, const Unit& u, LAS unsigned char*, int wr, int wc, int fr, int fq) const {
;         const int a0 = wc * 32 + 8 * fq;
;         float sxc[2][8];
; #pragma unroll
;         for (int bj = 0; bj < 2; ++bj)
; #pragma unroll
;             for (int e = 0; e < 8; ++e) sxc[bj][e] = sx0[128 * (a0 + e) + 2 * u.p1 + bj];
; #pragma unroll
;         EPI_LOOP_AM { const int cch = u.p0 * 256 + 128 * ai + 64 * wr + 16 * m + fr; const float swr = swin[cch];
; #pragma unroll
;             for (int bj = 0; bj < 2; ++bj) { f32x4 v0, v1;
; #pragma unroll
;                 for (int j = 0; j < 4; ++j) { v0[j] = (float)acc[ai][bj][m][0][j] * (swr * sxc[bj][j]); v1[j] = (float)acc[ai][bj][m][1][j] * (swr * sxc[bj][4 + j]); }
;                 *(GAS v4u*)(uTT + ((size_t)cch * 128 + (2 * u.p1 + bj)) * 128 + a0) = pack8(v0, v1); } }
.LBB0_252:
	v_mov_b32_e32 v128, v150
	v_mov_b32_e32 v143, v149
	s_lshl_b32 s56, s33, 1
	v_lshl_add_u32 v154, v128, 3, s27
	v_lshl_add_u32 v144, v154, 7, s56
	v_add_u32_e32 v134, 0x100, v144
	v_ashrrev_i32_e32 v135, 31, v134
	v_add_u32_e32 v132, 0x80, v144
	v_lshl_add_u64 v[138:139], v[134:135], 2, s[34:35]
	v_add_u32_e32 v134, 0x180, v144
	s_lshl_b32 s33, s54, 8
	v_ashrrev_i32_e32 v145, 31, v144
	v_ashrrev_i32_e32 v133, 31, v132
	v_ashrrev_i32_e32 v135, 31, v134
	s_add_i32 s33, s33, s26
	v_lshl_add_u64 v[130:131], v[144:145], 2, s[34:35]
	v_lshl_add_u64 v[132:133], v[132:133], 2, s[34:35]
	v_lshl_add_u64 v[140:141], v[134:135], 2, s[34:35]
	v_add_u32_e32 v146, s33, v143
	global_load_dwordx2 v[136:137], v[130:131], off
	global_load_dwordx2 v[134:135], v[132:133], off
	s_nop 0
	global_load_dwordx2 v[132:133], v[138:139], off
	global_load_dwordx2 v[130:131], v[140:141], off
	v_add_u32_e32 v138, 0x200, v144
	v_add_u32_e32 v140, 0x280, v144
	v_add_u32_e32 v142, 0x300, v144
	v_ashrrev_i32_e32 v147, 31, v146
	v_add_u32_e32 v144, 0x380, v144
	v_ashrrev_i32_e32 v139, 31, v138
	v_ashrrev_i32_e32 v141, 31, v140
	v_lshl_add_u64 v[156:157], v[146:147], 2, s[36:37]
	v_ashrrev_i32_e32 v145, 31, v144
	v_lshl_add_u64 v[138:139], v[138:139], 2, s[34:35]
	v_lshl_add_u64 v[140:141], v[140:141], 2, s[34:35]
	global_load_dword v128, v[156:157], off
	v_ashrrev_i32_e32 v143, 31, v142
	v_lshl_add_u64 v[144:145], v[144:145], 2, s[34:35]
	v_lshl_add_u64 v[156:157], v[142:143], 2, s[34:35]
	global_load_dwordx2 v[142:143], v[138:139], off
	s_nop 0
	global_load_dwordx2 v[140:141], v[140:141], off
	s_nop 0
	global_load_dwordx2 v[138:139], v[156:157], off
	v_cvt_f32_i32_e32 v153, v124
	global_load_dwordx2 v[144:145], v[144:145], off
	v_cvt_f32_i32_e32 v120, v120
	v_cvt_f32_i32_e32 v156, v125
	v_cvt_f32_i32_e32 v121, v121
	v_cvt_f32_i32_e32 v126, v126
	v_cvt_f32_i32_e32 v122, v122
	v_cvt_f32_i32_e32 v127, v127
	v_cvt_f32_i32_e32 v123, v123
	v_cvt_f32_i32_e32 v157, v116
	v_cvt_f32_i32_e32 v159, v117
	s_ashr_i32 s57, s56, 31
	v_lshlrev_b64 v[116:117], 15, v[146:147]
	s_lshl_b64 s[54:55], s[56:57], 8
	v_ashrrev_i32_e32 v155, 31, v154
	v_lshl_add_u64 v[124:125], s[6:7], 0, v[116:117]
	v_cvt_f32_i32_e32 v158, v112
	v_cvt_f32_i32_e32 v160, v113
	v_lshlrev_b64 v[112:113], 1, v[154:155]
	v_lshl_add_u64 v[116:117], v[124:125], 0, s[54:55]
	v_lshl_add_u64 v[116:117], v[116:117], 0, v[112:113]
	v_cvt_f32_i32_e32 v114, v114
	v_cvt_f32_i32_e32 v119, v119
	s_or_b32 s58, s56, 1
	s_ashr_i32 s59, s58, 31
	s_lshl_b64 s[56:57], s[58:59], 8
	v_cvt_f32_i32_e32 v108, v108
	v_cvt_f32_i32_e32 v104, v104
	v_cvt_f32_i32_e32 v109, v109
	v_cvt_f32_i32_e32 v105, v105
	v_cvt_f32_i32_e32 v110, v110
	v_cvt_f32_i32_e32 v106, v106
	v_cvt_f32_i32_e32 v111, v111
	v_cvt_f32_i32_e32 v107, v107
	v_cvt_f32_i32_e32 v98, v98
	v_cvt_f32_i32_e32 v99, v99
	v_cvt_f32_i32_e32 v92, v92
	v_cvt_f32_i32_e32 v93, v93
	v_cvt_f32_i32_e32 v94, v94
	v_cvt_f32_i32_e32 v95, v95
	v_cvt_f32_i32_e32 v76, v76
	v_cvt_f32_i32_e32 v77, v77
	v_cvt_f32_i32_e32 v78, v78
	v_cvt_f32_i32_e32 v79, v79
	v_cvt_f32_i32_e32 v60, v60
	v_cvt_f32_i32_e32 v61, v61
	v_cvt_f32_i32_e32 v62, v62
	v_cvt_f32_i32_e32 v63, v63
	v_cvt_f32_i32_e32 v44, v44
	v_cvt_f32_i32_e32 v45, v45
	v_cvt_f32_i32_e32 v46, v46
	v_cvt_f32_i32_e32 v47, v47
	v_cvt_f32_i32_e32 v28, v28
	v_cvt_f32_i32_e32 v29, v29
	v_cvt_f32_i32_e32 v30, v30
	v_cvt_f32_i32_e32 v31, v31
	v_cvt_f32_i32_e32 v12, v12
	v_cvt_f32_i32_e32 v8, v8
	v_cvt_f32_i32_e32 v13, v13
	v_cvt_f32_i32_e32 v9, v9
	v_cvt_f32_i32_e32 v14, v14
	v_cvt_f32_i32_e32 v10, v10
	v_cvt_f32_i32_e32 v15, v15
	v_cvt_f32_i32_e32 v11, v11
	s_andn2_b64 vcc, exec, s[52:53]
	s_mov_b64 s[52:53], -1
	s_waitcnt vmcnt(0)
	v_mul_f32_e32 v147, v136, v128
	v_mul_f32_e32 v147, v147, v153
	v_mul_f32_e32 v153, v142, v128
	v_mul_f32_e32 v155, v134, v128
	v_mul_f32_e32 v161, v140, v128
	v_mul_f32_e32 v162, v132, v128
	v_mul_f32_e32 v163, v138, v128
	v_mul_f32_e32 v164, v130, v128
	v_mul_f32_e32 v165, v144, v128
	v_mul_f32_e32 v153, v153, v120
	v_mul_f32_e32 v120, v155, v156
	v_mul_f32_e32 v155, v161, v121
	v_mul_f32_e32 v121, v162, v126
	v_mul_f32_e32 v126, v163, v122
	v_mul_f32_e32 v122, v164, v127
	v_mul_f32_e32 v123, v165, v123
	v_cvt_pk_bf16_f32 v120, v147, v120
	v_cvt_pk_bf16_f32 v121, v121, v122
	v_cvt_pk_bf16_f32 v122, v153, v155
	v_cvt_pk_bf16_f32 v123, v126, v123
	global_store_dwordx4 v[116:117], v[120:123], off sc1
	v_cvt_f32_i32_e32 v117, v118
	v_mul_f32_e32 v118, v133, v128
	v_mul_f32_e32 v154, v137, v128
	v_mul_f32_e32 v116, v141, v128
	v_mul_f32_e32 v117, v118, v117
	v_mul_f32_e32 v118, v139, v128
	v_mul_f32_e32 v118, v118, v114
	v_cvt_f32_i32_e32 v114, v115
	v_mul_f32_e32 v115, v131, v128
	v_mul_f32_e32 v115, v115, v119
	v_mul_f32_e32 v119, v145, v128
	v_mul_f32_e32 v154, v154, v157
	v_mul_f32_e32 v157, v143, v128
	v_mul_f32_e32 v166, v135, v128
	v_mul_f32_e32 v116, v116, v160
	v_mul_f32_e32 v119, v119, v114
	v_mul_f32_e32 v127, v157, v158
	v_mul_f32_e32 v156, v166, v159
	v_cvt_pk_bf16_f32 v114, v154, v156
	v_cvt_pk_bf16_f32 v115, v117, v115
	v_cvt_pk_bf16_f32 v116, v127, v116
	v_cvt_pk_bf16_f32 v117, v118, v119
	v_lshl_add_u64 v[118:119], v[124:125], 0, s[56:57]
	v_lshl_add_u64 v[118:119], v[118:119], 0, v[112:113]
	global_store_dwordx4 v[118:119], v[114:117], off sc1
	v_cvt_f32_i32_e32 v118, v96
	v_cvt_f32_i32_e32 v120, v97
	v_add_u32_e32 v114, 16, v146
	v_ashrrev_i32_e32 v115, 31, v114
	v_lshl_add_u64 v[116:117], v[114:115], 2, s[36:37]
	global_load_dword v116, v[116:117], off
	v_lshlrev_b64 v[96:97], 15, v[114:115]
	v_cvt_f32_i32_e32 v117, v100
	v_cvt_f32_i32_e32 v119, v101
	v_lshl_add_u64 v[100:101], s[6:7], 0, v[96:97]
	v_lshl_add_u64 v[96:97], v[100:101], 0, s[54:55]
	v_cvt_f32_i32_e32 v121, v102
	v_cvt_f32_i32_e32 v122, v103
	v_lshl_add_u64 v[102:103], v[96:97], 0, v[112:113]
	v_lshl_add_u64 v[100:101], v[100:101], 0, s[56:57]
	v_lshl_add_u64 v[100:101], v[100:101], 0, v[112:113]
	s_waitcnt vmcnt(0)
; #define GAS __attribute__((address_space(1)))
; __device__ __forceinline__ v4u pack8(const f32x4 a, const f32x4 b) { v4u w; w.x = cvt_pk_bf16(a[0], a[1]); w.y = cvt_pk_bf16(a[2], a[3]); w.z = cvt_pk_bf16(b[0], b[1]); w.w = cvt_pk_bf16(b[2], b[3]); return w; }
; #define EPI_LOOP_AM for (int ai = 0; ai < 2; ++ai) _Pragma("unroll") for (int m = 0; m < 4; ++m)
;     __device__ __forceinline__ void operator()(AccI& acc, const Unit& u, LAS unsigned char*, int wr, int wc, int fr, int fq) const {
;     ...
;             for (int e = 0; e < 8; ++e) sxc[bj][e] = sx0[128 * (a0 + e) + 2 * u.p1 + bj];
; #pragma unroll
;         EPI_LOOP_AM { const int cch = u.p0 * 256 + 128 * ai + 64 * wr + 16 * m + fr; const float swr = swin[cch];
; #pragma unroll
;             for (int bj = 0; bj < 2; ++bj) { f32x4 v0, v1;
; #pragma unroll
;                 for (int j = 0; j < 4; ++j) { v0[j] = (float)acc[ai][bj][m][0][j] * (swr * sxc[bj][j]); v1[j] = (float)acc[ai][bj][m][1][j] * (swr * sxc[bj][4 + j]); }
;                 *(GAS v4u*)(uTT + ((size_t)cch * 128 + (2 * u.p1 + bj)) * 128 + a0) = pack8(v0, v1); } }
	v_mul_f32_e32 v96, v136, v116
	v_mul_f32_e32 v97, v142, v116
	v_mul_f32_e32 v114, v134, v116
	v_mul_f32_e32 v96, v96, v108
	v_mul_f32_e32 v115, v140, v116
	v_mul_f32_e32 v123, v132, v116
	v_mul_f32_e32 v124, v138, v116
	v_mul_f32_e32 v125, v130, v116
	v_mul_f32_e32 v126, v144, v116
	v_mul_f32_e32 v127, v137, v116
	v_mul_f32_e32 v128, v143, v116
	v_mul_f32_e32 v147, v135, v116
	v_mul_f32_e32 v153, v141, v116
	v_mul_f32_e32 v154, v133, v116
	v_mul_f32_e32 v155, v139, v116
	v_mul_f32_e32 v156, v131, v116
	v_mul_f32_e32 v116, v145, v116
	v_mul_f32_e32 v104, v97, v104
	v_mul_f32_e32 v97, v114, v109
	v_cvt_pk_bf16_f32 v96, v96, v97
	v_mul_f32_e32 v105, v115, v105
	v_mul_f32_e32 v108, v123, v110
	v_mul_f32_e32 v106, v124, v106
	v_mul_f32_e32 v109, v125, v111
	v_mul_f32_e32 v107, v126, v107
	v_mul_f32_e32 v110, v127, v117
	v_mul_f32_e32 v111, v128, v118
	v_mul_f32_e32 v114, v147, v119
	v_mul_f32_e32 v118, v155, v98
	v_mul_f32_e32 v116, v116, v99
	v_cvt_pk_bf16_f32 v97, v108, v109
	v_cvt_pk_bf16_f32 v98, v104, v105
	v_cvt_pk_bf16_f32 v99, v106, v107
	global_store_dwordx4 v[102:103], v[96:99], off sc1
	v_mul_f32_e32 v115, v153, v120
	v_mul_f32_e32 v117, v154, v121
	v_cvt_pk_bf16_f32 v96, v110, v114
	v_mul_f32_e32 v119, v156, v122
	v_cvt_pk_bf16_f32 v97, v117, v119
	v_cvt_pk_bf16_f32 v98, v111, v115
	v_cvt_pk_bf16_f32 v99, v118, v116
	global_store_dwordx4 v[100:101], v[96:99], off sc1
	v_cvt_f32_i32_e32 v100, v89
	v_cvt_f32_i32_e32 v104, v80
	v_add_u32_e32 v96, 32, v146
	v_ashrrev_i32_e32 v97, 31, v96
	v_lshl_add_u64 v[98:99], v[96:97], 2, s[36:37]
	global_load_dword v98, v[98:99], off
	v_cvt_f32_i32_e32 v99, v88
	v_cvt_f32_i32_e32 v106, v81
	v_lshlrev_b64 v[80:81], 15, v[96:97]
	v_cvt_f32_i32_e32 v101, v90
	v_cvt_f32_i32_e32 v102, v91
	v_lshl_add_u64 v[80:81], s[6:7], 0, v[80:81]
	v_cvt_f32_i32_e32 v103, v84
	v_cvt_f32_i32_e32 v105, v85
	v_cvt_f32_i32_e32 v107, v86
	v_cvt_f32_i32_e32 v108, v82
	v_cvt_f32_i32_e32 v109, v87
	v_cvt_f32_i32_e32 v110, v83
	v_lshl_add_u64 v[82:83], v[80:81], 0, s[54:55]
	v_lshl_add_u64 v[80:81], v[80:81], 0, s[56:57]
	v_lshl_add_u64 v[88:89], v[82:83], 0, v[112:113]
	v_lshl_add_u64 v[90:91], v[80:81], 0, v[112:113]
	v_add_u32_e32 v84, 48, v146
	v_ashrrev_i32_e32 v85, 31, v84
	v_lshl_add_u64 v[86:87], v[84:85], 2, s[36:37]
	s_waitcnt vmcnt(0)
	v_mul_f32_e32 v80, v136, v98
	v_mul_f32_e32 v81, v142, v98
	v_mul_f32_e32 v82, v134, v98
	v_mul_f32_e32 v83, v140, v98
	v_mul_f32_e32 v96, v132, v98
	v_mul_f32_e32 v97, v138, v98
	v_mul_f32_e32 v111, v130, v98
	v_mul_f32_e32 v114, v144, v98
	v_mul_f32_e32 v80, v80, v92
	v_mul_f32_e32 v92, v81, v99
	v_mul_f32_e32 v81, v82, v93
	v_mul_f32_e32 v82, v83, v100
	v_mul_f32_e32 v83, v96, v94
	v_mul_f32_e32 v115, v137, v98
	v_mul_f32_e32 v116, v143, v98
	v_mul_f32_e32 v117, v135, v98
	v_mul_f32_e32 v118, v141, v98
	v_mul_f32_e32 v119, v133, v98
	v_mul_f32_e32 v120, v139, v98
	v_mul_f32_e32 v121, v131, v98
	v_mul_f32_e32 v98, v145, v98
	v_mul_f32_e32 v93, v97, v101
	v_mul_f32_e32 v94, v111, v95
	v_mul_f32_e32 v95, v114, v102
	v_cvt_pk_bf16_f32 v80, v80, v81
	v_cvt_pk_bf16_f32 v81, v83, v94
	v_cvt_pk_bf16_f32 v82, v92, v82
	v_cvt_pk_bf16_f32 v83, v93, v95
	v_mul_f32_e32 v96, v115, v103
	v_mul_f32_e32 v97, v116, v104
	v_mul_f32_e32 v99, v117, v105
	v_mul_f32_e32 v100, v118, v106
	v_mul_f32_e32 v101, v119, v107
	v_mul_f32_e32 v102, v120, v108
	v_mul_f32_e32 v103, v121, v109
	v_mul_f32_e32 v98, v98, v110
	global_store_dwordx4 v[88:89], v[80:83], off sc1
	v_cvt_f32_i32_e32 v88, v64
	v_cvt_f32_i32_e32 v89, v69
	v_cvt_pk_bf16_f32 v80, v96, v99
	v_cvt_pk_bf16_f32 v81, v101, v103
	v_cvt_pk_bf16_f32 v82, v97, v100
	v_cvt_pk_bf16_f32 v83, v102, v98
	global_store_dwordx4 v[90:91], v[80:83], off sc1
	global_load_dword v80, v[86:87], off
	v_cvt_f32_i32_e32 v90, v65
	v_cvt_f32_i32_e32 v81, v72
	v_cvt_f32_i32_e32 v82, v73
	v_lshlrev_b64 v[64:65], 15, v[84:85]
	v_cvt_f32_i32_e32 v83, v74
	v_cvt_f32_i32_e32 v86, v75
	v_lshl_add_u64 v[64:65], s[6:7], 0, v[64:65]
	v_cvt_f32_i32_e32 v87, v68
	v_cvt_f32_i32_e32 v91, v70
	v_cvt_f32_i32_e32 v92, v66
	v_cvt_f32_i32_e32 v93, v71
	v_cvt_f32_i32_e32 v94, v67
	v_lshl_add_u64 v[66:67], v[64:65], 0, s[54:55]
	v_lshl_add_u64 v[64:65], v[64:65], 0, s[56:57]
	v_lshl_add_u64 v[72:73], v[66:67], 0, v[112:113]
	v_lshl_add_u64 v[74:75], v[64:65], 0, v[112:113]
	v_add_u32_e32 v68, 0x80, v146
	v_ashrrev_i32_e32 v69, 31, v68
	v_lshl_add_u64 v[70:71], v[68:69], 2, s[36:37]
	s_waitcnt vmcnt(0)
	v_mul_f32_e32 v64, v136, v80
	v_mul_f32_e32 v65, v142, v80
	v_mul_f32_e32 v66, v134, v80
	v_mul_f32_e32 v67, v140, v80
	v_mul_f32_e32 v84, v132, v80
	v_mul_f32_e32 v85, v138, v80
	v_mul_f32_e32 v95, v130, v80
	v_mul_f32_e32 v96, v144, v80
	v_mul_f32_e32 v64, v64, v76
	v_mul_f32_e32 v76, v65, v81
	v_mul_f32_e32 v65, v66, v77
	v_mul_f32_e32 v66, v67, v82
	v_mul_f32_e32 v67, v84, v78
	v_mul_f32_e32 v97, v137, v80
	v_mul_f32_e32 v98, v143, v80
	v_mul_f32_e32 v99, v135, v80
	v_mul_f32_e32 v100, v141, v80
	v_mul_f32_e32 v101, v133, v80
	v_mul_f32_e32 v102, v139, v80
	v_mul_f32_e32 v103, v131, v80
	v_mul_f32_e32 v80, v145, v80
	v_mul_f32_e32 v77, v85, v83
	v_mul_f32_e32 v78, v95, v79
	v_mul_f32_e32 v79, v96, v86
	v_cvt_pk_bf16_f32 v64, v64, v65
	v_cvt_pk_bf16_f32 v65, v67, v78
	v_cvt_pk_bf16_f32 v66, v76, v66
	v_cvt_pk_bf16_f32 v67, v77, v79
	v_mul_f32_e32 v81, v97, v87
	v_mul_f32_e32 v82, v98, v88
	v_mul_f32_e32 v83, v99, v89
	v_mul_f32_e32 v84, v100, v90
	v_mul_f32_e32 v85, v101, v91
	v_mul_f32_e32 v86, v102, v92
	v_mul_f32_e32 v87, v103, v93
	v_mul_f32_e32 v80, v80, v94
	global_store_dwordx4 v[72:73], v[64:67], off sc1
	v_cvt_f32_i32_e32 v72, v48
	v_cvt_f32_i32_e32 v73, v53
	v_cvt_pk_bf16_f32 v64, v81, v83
	v_cvt_pk_bf16_f32 v65, v85, v87
	v_cvt_pk_bf16_f32 v66, v82, v84
	v_cvt_pk_bf16_f32 v67, v86, v80
	global_store_dwordx4 v[74:75], v[64:67], off sc1
	global_load_dword v64, v[70:71], off
	v_cvt_f32_i32_e32 v74, v49
	v_cvt_f32_i32_e32 v65, v56
	v_cvt_f32_i32_e32 v66, v57
	v_lshlrev_b64 v[48:49], 15, v[68:69]
	v_cvt_f32_i32_e32 v67, v58
	v_cvt_f32_i32_e32 v70, v59
	v_lshl_add_u64 v[48:49], s[6:7], 0, v[48:49]
	v_cvt_f32_i32_e32 v71, v52
	v_cvt_f32_i32_e32 v75, v54
	v_cvt_f32_i32_e32 v76, v50
	v_cvt_f32_i32_e32 v77, v55
	v_cvt_f32_i32_e32 v78, v51
	v_lshl_add_u64 v[50:51], v[48:49], 0, s[54:55]
	v_lshl_add_u64 v[48:49], v[48:49], 0, s[56:57]
	v_lshl_add_u64 v[56:57], v[50:51], 0, v[112:113]
	v_lshl_add_u64 v[58:59], v[48:49], 0, v[112:113]
	v_add_u32_e32 v52, 0x90, v146
	v_ashrrev_i32_e32 v53, 31, v52
	v_lshl_add_u64 v[54:55], v[52:53], 2, s[36:37]
	s_waitcnt vmcnt(0)
; #define GAS __attribute__((address_space(1)))
; __device__ __forceinline__ v4u pack8(const f32x4 a, const f32x4 b) { v4u w; w.x = cvt_pk_bf16(a[0], a[1]); w.y = cvt_pk_bf16(a[2], a[3]); w.z = cvt_pk_bf16(b[0], b[1]); w.w = cvt_pk_bf16(b[2], b[3]); return w; }
; #define EPI_LOOP_AM for (int ai = 0; ai < 2; ++ai) _Pragma("unroll") for (int m = 0; m < 4; ++m)
;     __device__ __forceinline__ void operator()(AccI& acc, const Unit& u, LAS unsigned char*, int wr, int wc, int fr, int fq) const {
;     ...
;             for (int e = 0; e < 8; ++e) sxc[bj][e] = sx0[128 * (a0 + e) + 2 * u.p1 + bj];
; #pragma unroll
;         EPI_LOOP_AM { const int cch = u.p0 * 256 + 128 * ai + 64 * wr + 16 * m + fr; const float swr = swin[cch];
; #pragma unroll
;             for (int bj = 0; bj < 2; ++bj) { f32x4 v0, v1;
; #pragma unroll
;                 for (int j = 0; j < 4; ++j) { v0[j] = (float)acc[ai][bj][m][0][j] * (swr * sxc[bj][j]); v1[j] = (float)acc[ai][bj][m][1][j] * (swr * sxc[bj][4 + j]); }
;                 *(GAS v4u*)(uTT + ((size_t)cch * 128 + (2 * u.p1 + bj)) * 128 + a0) = pack8(v0, v1); } }
	v_mul_f32_e32 v48, v136, v64
	v_mul_f32_e32 v49, v142, v64
	v_mul_f32_e32 v50, v134, v64
	v_mul_f32_e32 v51, v140, v64
	v_mul_f32_e32 v68, v132, v64
	v_mul_f32_e32 v69, v138, v64
	v_mul_f32_e32 v79, v130, v64
	v_mul_f32_e32 v80, v144, v64
	v_mul_f32_e32 v48, v48, v60
	v_mul_f32_e32 v60, v49, v65
	v_mul_f32_e32 v49, v50, v61
	v_mul_f32_e32 v50, v51, v66
	v_mul_f32_e32 v51, v68, v62
	v_mul_f32_e32 v81, v137, v64
	v_mul_f32_e32 v82, v143, v64
	v_mul_f32_e32 v83, v135, v64
	v_mul_f32_e32 v84, v141, v64
	v_mul_f32_e32 v85, v133, v64
	v_mul_f32_e32 v86, v139, v64
	v_mul_f32_e32 v87, v131, v64
	v_mul_f32_e32 v64, v145, v64
	v_mul_f32_e32 v61, v69, v67
	v_mul_f32_e32 v62, v79, v63
	v_mul_f32_e32 v63, v80, v70
	v_cvt_pk_bf16_f32 v48, v48, v49
	v_cvt_pk_bf16_f32 v49, v51, v62
	v_cvt_pk_bf16_f32 v50, v60, v50
	v_cvt_pk_bf16_f32 v51, v61, v63
	v_mul_f32_e32 v65, v81, v71
	v_mul_f32_e32 v66, v82, v72
	v_mul_f32_e32 v67, v83, v73
	v_mul_f32_e32 v68, v84, v74
	v_mul_f32_e32 v69, v85, v75
	v_mul_f32_e32 v70, v86, v76
	v_mul_f32_e32 v71, v87, v77
	v_mul_f32_e32 v64, v64, v78
	global_store_dwordx4 v[56:57], v[48:51], off sc1
	v_cvt_f32_i32_e32 v56, v32
	v_cvt_f32_i32_e32 v57, v37
	v_cvt_pk_bf16_f32 v48, v65, v67
	v_cvt_pk_bf16_f32 v49, v69, v71
	v_cvt_pk_bf16_f32 v50, v66, v68
	v_cvt_pk_bf16_f32 v51, v70, v64
	global_store_dwordx4 v[58:59], v[48:51], off sc1
	global_load_dword v48, v[54:55], off
	v_cvt_f32_i32_e32 v58, v33
	v_cvt_f32_i32_e32 v49, v40
	v_cvt_f32_i32_e32 v50, v41
	v_lshlrev_b64 v[32:33], 15, v[52:53]
	v_cvt_f32_i32_e32 v51, v42
	v_cvt_f32_i32_e32 v54, v43
	v_lshl_add_u64 v[32:33], s[6:7], 0, v[32:33]
	v_cvt_f32_i32_e32 v55, v36
	v_cvt_f32_i32_e32 v59, v38
	v_cvt_f32_i32_e32 v60, v34
	v_cvt_f32_i32_e32 v61, v39
	v_cvt_f32_i32_e32 v62, v35
	v_lshl_add_u64 v[34:35], v[32:33], 0, s[54:55]
	v_lshl_add_u64 v[32:33], v[32:33], 0, s[56:57]
	v_lshl_add_u64 v[40:41], v[34:35], 0, v[112:113]
	v_lshl_add_u64 v[42:43], v[32:33], 0, v[112:113]
	v_add_u32_e32 v36, 0xa0, v146
	v_ashrrev_i32_e32 v37, 31, v36
	v_lshl_add_u64 v[38:39], v[36:37], 2, s[36:37]
	s_waitcnt vmcnt(0)
	v_mul_f32_e32 v32, v136, v48
	v_mul_f32_e32 v33, v142, v48
	v_mul_f32_e32 v34, v134, v48
	v_mul_f32_e32 v35, v140, v48
	v_mul_f32_e32 v52, v132, v48
	v_mul_f32_e32 v53, v138, v48
	v_mul_f32_e32 v63, v130, v48
	v_mul_f32_e32 v64, v144, v48
	v_mul_f32_e32 v32, v32, v44
	v_mul_f32_e32 v44, v33, v49
	v_mul_f32_e32 v33, v34, v45
	v_mul_f32_e32 v34, v35, v50
	v_mul_f32_e32 v35, v52, v46
	v_mul_f32_e32 v65, v137, v48
	v_mul_f32_e32 v66, v143, v48
	v_mul_f32_e32 v67, v135, v48
	v_mul_f32_e32 v68, v141, v48
	v_mul_f32_e32 v69, v133, v48
	v_mul_f32_e32 v70, v139, v48
	v_mul_f32_e32 v71, v131, v48
	v_mul_f32_e32 v48, v145, v48
	v_mul_f32_e32 v45, v53, v51
	v_mul_f32_e32 v46, v63, v47
	v_mul_f32_e32 v47, v64, v54
	v_cvt_pk_bf16_f32 v32, v32, v33
	v_cvt_pk_bf16_f32 v33, v35, v46
	v_cvt_pk_bf16_f32 v34, v44, v34
	v_cvt_pk_bf16_f32 v35, v45, v47
	v_mul_f32_e32 v49, v65, v55
	v_mul_f32_e32 v50, v66, v56
	v_mul_f32_e32 v51, v67, v57
	v_mul_f32_e32 v52, v68, v58
	v_mul_f32_e32 v53, v69, v59
	v_mul_f32_e32 v54, v70, v60
	v_mul_f32_e32 v55, v71, v61
	v_mul_f32_e32 v48, v48, v62
	global_store_dwordx4 v[40:41], v[32:35], off sc1
	v_cvt_f32_i32_e32 v40, v16
	v_cvt_f32_i32_e32 v41, v21
	v_cvt_pk_bf16_f32 v32, v49, v51
	v_cvt_pk_bf16_f32 v33, v53, v55
	v_cvt_pk_bf16_f32 v34, v50, v52
	v_cvt_pk_bf16_f32 v35, v54, v48
	global_store_dwordx4 v[42:43], v[32:35], off sc1
	global_load_dword v32, v[38:39], off
	v_cvt_f32_i32_e32 v42, v17
	v_cvt_f32_i32_e32 v33, v24
	v_cvt_f32_i32_e32 v34, v25
	v_lshlrev_b64 v[16:17], 15, v[36:37]
	v_cvt_f32_i32_e32 v35, v26
	v_cvt_f32_i32_e32 v38, v27
	v_lshl_add_u64 v[16:17], s[6:7], 0, v[16:17]
	v_cvt_f32_i32_e32 v39, v20
	v_cvt_f32_i32_e32 v43, v22
	v_cvt_f32_i32_e32 v44, v18
	v_cvt_f32_i32_e32 v45, v23
	v_cvt_f32_i32_e32 v46, v19
	v_lshl_add_u64 v[18:19], v[16:17], 0, s[54:55]
	v_lshl_add_u64 v[16:17], v[16:17], 0, s[56:57]
	v_lshl_add_u64 v[24:25], v[18:19], 0, v[112:113]
	v_lshl_add_u64 v[26:27], v[16:17], 0, v[112:113]
	v_add_u32_e32 v20, 0xb0, v146
	v_ashrrev_i32_e32 v21, 31, v20
	v_lshl_add_u64 v[22:23], v[20:21], 2, s[36:37]
	s_waitcnt vmcnt(0)
; #define GAS __attribute__((address_space(1)))
; __device__ __forceinline__ v4u pack8(const f32x4 a, const f32x4 b) { v4u w; w.x = cvt_pk_bf16(a[0], a[1]); w.y = cvt_pk_bf16(a[2], a[3]); w.z = cvt_pk_bf16(b[0], b[1]); w.w = cvt_pk_bf16(b[2], b[3]); return w; }
; #define EPI_LOOP_AM for (int ai = 0; ai < 2; ++ai) _Pragma("unroll") for (int m = 0; m < 4; ++m)
;     __device__ __forceinline__ void operator()(AccI& acc, const Unit& u, LAS unsigned char*, int wr, int wc, int fr, int fq) const {
;     ...
;             for (int e = 0; e < 8; ++e) sxc[bj][e] = sx0[128 * (a0 + e) + 2 * u.p1 + bj];
; #pragma unroll
;         EPI_LOOP_AM { const int cch = u.p0 * 256 + 128 * ai + 64 * wr + 16 * m + fr; const float swr = swin[cch];
; #pragma unroll
;             for (int bj = 0; bj < 2; ++bj) { f32x4 v0, v1;
; #pragma unroll
;                 for (int j = 0; j < 4; ++j) { v0[j] = (float)acc[ai][bj][m][0][j] * (swr * sxc[bj][j]); v1[j] = (float)acc[ai][bj][m][1][j] * (swr * sxc[bj][4 + j]); }
;                 *(GAS v4u*)(uTT + ((size_t)cch * 128 + (2 * u.p1 + bj)) * 128 + a0) = pack8(v0, v1); } }
	v_mul_f32_e32 v16, v136, v32
	v_mul_f32_e32 v17, v142, v32
	v_mul_f32_e32 v18, v134, v32
	v_mul_f32_e32 v19, v140, v32
	v_mul_f32_e32 v36, v132, v32
	v_mul_f32_e32 v37, v138, v32
	v_mul_f32_e32 v47, v130, v32
	v_mul_f32_e32 v48, v144, v32
	v_mul_f32_e32 v16, v16, v28
	v_mul_f32_e32 v28, v17, v33
	v_mul_f32_e32 v17, v18, v29
	v_mul_f32_e32 v18, v19, v34
	v_mul_f32_e32 v19, v36, v30
	v_mul_f32_e32 v49, v137, v32
	v_mul_f32_e32 v50, v143, v32
	v_mul_f32_e32 v51, v135, v32
	v_mul_f32_e32 v52, v141, v32
	v_mul_f32_e32 v53, v133, v32
	v_mul_f32_e32 v54, v139, v32
	v_mul_f32_e32 v55, v131, v32
	v_mul_f32_e32 v32, v145, v32
	v_mul_f32_e32 v29, v37, v35
	v_mul_f32_e32 v30, v47, v31
	v_mul_f32_e32 v31, v48, v38
	v_cvt_pk_bf16_f32 v16, v16, v17
	v_cvt_pk_bf16_f32 v17, v19, v30
	v_cvt_pk_bf16_f32 v18, v28, v18
	v_cvt_pk_bf16_f32 v19, v29, v31
	v_mul_f32_e32 v33, v49, v39
	v_mul_f32_e32 v34, v50, v40
	v_mul_f32_e32 v35, v51, v41
	v_mul_f32_e32 v36, v52, v42
	v_mul_f32_e32 v37, v53, v43
	v_mul_f32_e32 v38, v54, v44
	v_mul_f32_e32 v39, v55, v45
	v_mul_f32_e32 v32, v32, v46
	global_store_dwordx4 v[24:25], v[16:19], off sc1
	v_cvt_f32_i32_e32 v24, v2
	v_cvt_f32_i32_e32 v25, v7
	v_cvt_pk_bf16_f32 v16, v33, v35
	v_cvt_pk_bf16_f32 v17, v37, v39
	v_cvt_pk_bf16_f32 v18, v34, v36
	v_cvt_pk_bf16_f32 v19, v38, v32
	global_store_dwordx4 v[26:27], v[16:19], off sc1
	global_load_dword v16, v[22:23], off
	v_cvt_f32_i32_e32 v22, v1
	v_cvt_f32_i32_e32 v18, v0
	v_lshlrev_b64 v[0:1], 15, v[20:21]
	v_lshl_add_u64 v[0:1], s[6:7], 0, v[0:1]
	v_cvt_f32_i32_e32 v17, v4
	v_cvt_f32_i32_e32 v19, v5
	v_cvt_f32_i32_e32 v23, v6
	v_cvt_f32_i32_e32 v26, v3
	v_lshl_add_u64 v[2:3], v[0:1], 0, s[54:55]
	v_lshl_add_u64 v[0:1], v[0:1], 0, s[56:57]
	v_lshl_add_u64 v[4:5], v[2:3], 0, v[112:113]
	v_lshl_add_u64 v[6:7], v[0:1], 0, v[112:113]
	s_waitcnt vmcnt(0)
	v_mul_f32_e32 v0, v136, v16
	v_mul_f32_e32 v1, v142, v16
	v_mul_f32_e32 v2, v134, v16
	v_mul_f32_e32 v3, v140, v16
	v_mul_f32_e32 v20, v132, v16
	v_mul_f32_e32 v21, v138, v16
	v_mul_f32_e32 v27, v130, v16
	v_mul_f32_e32 v28, v144, v16
	v_mul_f32_e32 v0, v0, v12
	v_mul_f32_e32 v8, v1, v8
	v_mul_f32_e32 v1, v2, v13
	v_mul_f32_e32 v2, v3, v9
	v_mul_f32_e32 v3, v20, v14
	v_mul_f32_e32 v29, v137, v16
	v_mul_f32_e32 v30, v143, v16
	v_mul_f32_e32 v31, v135, v16
	v_mul_f32_e32 v32, v141, v16
	v_mul_f32_e32 v33, v133, v16
	v_mul_f32_e32 v34, v139, v16
	v_mul_f32_e32 v35, v131, v16
	v_mul_f32_e32 v16, v145, v16
	v_mul_f32_e32 v9, v21, v10
	v_mul_f32_e32 v10, v27, v15
	v_mul_f32_e32 v11, v28, v11
	v_cvt_pk_bf16_f32 v0, v0, v1
	v_cvt_pk_bf16_f32 v1, v3, v10
	v_cvt_pk_bf16_f32 v2, v8, v2
	v_cvt_pk_bf16_f32 v3, v9, v11
	v_mul_f32_e32 v12, v29, v17
	v_mul_f32_e32 v13, v30, v18
	v_mul_f32_e32 v14, v31, v19
	v_mul_f32_e32 v15, v32, v22
	v_mul_f32_e32 v17, v33, v23
	v_mul_f32_e32 v18, v34, v24
	v_mul_f32_e32 v19, v35, v25
	v_mul_f32_e32 v16, v16, v26
	global_store_dwordx4 v[4:5], v[0:3], off sc1
	s_nop 1
	v_cvt_pk_bf16_f32 v0, v12, v14
	v_cvt_pk_bf16_f32 v1, v17, v19
	v_cvt_pk_bf16_f32 v2, v13, v15
	v_cvt_pk_bf16_f32 v3, v18, v16
	global_store_dwordx4 v[6:7], v[0:3], off sc1
	s_cbranch_vccnz .LBB0_240
	s_andn2_b64 vcc, exec, s[4:5]
	s_cbranch_vccnz .LBB0_239
	s_barrier
	s_branch .LBB0_239

; #define GAS __attribute__((address_space(1)))
; __device__ __forceinline__ v4u pack8(const f32x4 a, const f32x4 b) { v4u w; w.x = cvt_pk_bf16(a[0], a[1]); w.y = cvt_pk_bf16(a[2], a[3]); w.z = cvt_pk_bf16(b[0], b[1]); w.w = cvt_pk_bf16(b[2], b[3]); return w; }
; #define EPI_LOOP_AM for (int ai = 0; ai < 2; ++ai) _Pragma("unroll") for (int m = 0; m < 4; ++m)
;     __device__ __forceinline__ void operator()(AccI& acc, const Unit& u, LAS unsigned char*, int wr, int wc, int fr, int fq) const {
;     ...
;         f32x4 sxc[2][2];
; #pragma unroll
;         for (int bj = 0; bj < 2; ++bj)
; #pragma unroll
;             for (int n = 0; n < 2; ++n) sxc[bj][n] = *(const GAS f32x4*)(sx0 + n_ch * 256 + 128 * bj + c0 + 4 * n);
;         if (pm < 4) {
;     ...
;             const int h = pm - 4;
; #pragma unroll
;             EPI_LOOP_AM { const int dv = 128 * ai + 64 * wr + 16 * m + fr; const float swr = swin[u.p2 + dv];
; #pragma unroll
;                 for (int bj = 0; bj < 2; ++bj) { f32x4 v0, v1;
; #pragma unroll
;                     for (int j = 0; j < 4; ++j) { v0[j] = (float)acc[ai][bj][m][0][j] * (swr * sxc[bj][0][j]); v1[j] = (float)acc[ai][bj][m][1][j] * (swr * sxc[bj][1][j]); }
;                     *(GAS v4u*)(Bcat + ((size_t)(h * NCH + n_ch) * 256 + dv) * CAT + 128 * bj + c0) = pack8(v0, v1); } }
.LBB0_291:
	s_lshl_b32 s62, s60, 8
	s_ashr_i32 s63, s62, 31
	v_mov_b32_e32 v92, v156
	v_mov_b32_e32 v148, v155
	s_lshl_b64 s[64:65], s[62:63], 2
	s_add_u32 s64, s34, s64
	v_lshl_add_u32 v150, v92, 3, s27
	s_addc_u32 s65, s35, s65
	v_ashrrev_i32_e32 v151, 31, v150
	v_lshl_add_u64 v[100:101], v[150:151], 2, s[64:65]
	global_load_dwordx4 v[112:115], v[100:101], off offset:16
	global_load_dwordx4 v[120:123], v[100:101], off
	global_load_dwordx4 v[92:95], v[100:101], off offset:528
	s_nop 0
	global_load_dwordx4 v[100:103], v[100:101], off offset:512
	s_cmp_lt_i32 s58, 4
	s_mov_b64 s[64:65], -1
	s_cbranch_scc1 .LBB0_294
	v_add_u32_e32 v152, s26, v148
	v_add_u32_e32 v144, s56, v152
	v_ashrrev_i32_e32 v145, 31, v144
	v_lshl_add_u64 v[144:145], v[144:145], 2, s[36:37]
	global_load_dword v159, v[144:145], off
	s_lshl_b32 s45, s58, 6
	s_add_i32 s45, s60, s45
	v_add_u32_e32 v164, 16, v152
	s_add_i32 s64, s45, 0xffffff00
	v_add_u32_e32 v160, s56, v164
	s_ashr_i32 s65, s64, 31
	v_ashrrev_i32_e32 v153, 31, v152
	v_ashrrev_i32_e32 v161, 31, v160
	s_lshl_b64 s[64:65], s[64:65], 8
	v_cvt_f32_i32_e32 v165, v140
	v_cvt_f32_i32_e32 v170, v132
	v_cvt_f32_i32_e32 v171, v141
	v_cvt_f32_i32_e32 v172, v133
	v_cvt_f32_i32_e32 v173, v142
	v_cvt_f32_i32_e32 v174, v134
	v_mov_b64_e32 v[144:145], s[8:9]
	v_lshl_add_u64 v[166:167], v[160:161], 2, s[36:37]
	v_lshl_add_u64 v[160:161], s[64:65], 0, v[152:153]
	v_cvt_f32_i32_e32 v175, v143
	v_cvt_f32_i32_e32 v176, v135
	v_mad_u64_u32 v[162:163], s[66:67], v160, s57, v[144:145]
	v_lshlrev_b64 v[146:147], 1, v[150:151]
	v_cvt_f32_i32_e32 v177, v124
	v_cvt_f32_i32_e32 v178, v108
	v_cvt_f32_i32_e32 v179, v125
	v_cvt_f32_i32_e32 v180, v109
	v_cvt_f32_i32_e32 v181, v126
	v_cvt_f32_i32_e32 v182, v110
	v_cvt_f32_i32_e32 v183, v127
	v_cvt_f32_i32_e32 v184, v111
	v_mad_i32_i24 v163, v161, s57, v163
	v_lshl_add_u64 v[168:169], v[162:163], 0, v[146:147]
	s_waitcnt vmcnt(0)
	v_mul_f32_e32 v153, v120, v159
	v_mul_f32_e32 v160, v112, v159
	v_mul_f32_e32 v161, v121, v159
	v_mul_f32_e32 v162, v113, v159
	v_mul_f32_e32 v163, v122, v159
	v_mul_f32_e32 v185, v114, v159
	v_mul_f32_e32 v186, v123, v159
	v_mul_f32_e32 v187, v115, v159
	v_mul_f32_e32 v153, v153, v165
	v_mul_f32_e32 v165, v160, v170
	v_mul_f32_e32 v160, v161, v171
	v_mul_f32_e32 v162, v162, v172
	v_mul_f32_e32 v161, v163, v173
	v_mul_f32_e32 v163, v185, v174
	v_mul_f32_e32 v188, v100, v159
	v_mul_f32_e32 v189, v92, v159
	v_mul_f32_e32 v190, v101, v159
	v_mul_f32_e32 v191, v93, v159
	v_mul_f32_e32 v192, v102, v159
	v_mul_f32_e32 v193, v94, v159
	v_mul_f32_e32 v194, v103, v159
	v_mul_f32_e32 v159, v95, v159
	v_mul_f32_e32 v170, v186, v175
	v_mul_f32_e32 v171, v187, v176
	v_cvt_pk_bf16_f32 v160, v153, v160
	v_cvt_pk_bf16_f32 v161, v161, v170
	v_cvt_pk_bf16_f32 v162, v165, v162
	v_cvt_pk_bf16_f32 v163, v163, v171
	v_mul_f32_e32 v172, v188, v177
	v_mul_f32_e32 v173, v189, v178
	v_mul_f32_e32 v174, v190, v179
	v_mul_f32_e32 v175, v191, v180
	v_mul_f32_e32 v176, v192, v181
	v_mul_f32_e32 v177, v193, v182
	v_mul_f32_e32 v178, v194, v183
	v_mul_f32_e32 v159, v159, v184
	global_store_dwordx4 v[168:169], v[160:163], off sc1
	v_ashrrev_i32_e32 v165, 31, v164
	v_cvt_f32_i32_e32 v170, v97
	v_cvt_pk_bf16_f32 v160, v172, v174
	v_cvt_pk_bf16_f32 v161, v176, v178
	v_cvt_pk_bf16_f32 v162, v173, v175
	v_cvt_pk_bf16_f32 v163, v177, v159
	global_store_dwordx4 v[168:169], v[160:163], off offset:256 sc1
	global_load_dword v153, v[166:167], off
	v_add_u32_e32 v166, 32, v152
	v_add_u32_e32 v160, s56, v166
	v_ashrrev_i32_e32 v161, 31, v160
	v_cvt_f32_i32_e32 v159, v96
	v_cvt_f32_i32_e32 v167, v88
	v_cvt_f32_i32_e32 v171, v89
	v_cvt_f32_i32_e32 v172, v98
	v_cvt_f32_i32_e32 v173, v90
	v_lshl_add_u64 v[168:169], v[160:161], 2, s[36:37]
	v_lshl_add_u64 v[160:161], s[64:65], 0, v[164:165]
	v_cvt_f32_i32_e32 v174, v99
	v_cvt_f32_i32_e32 v175, v91
	v_mad_u64_u32 v[162:163], s[66:67], v160, s57, v[144:145]
	v_cvt_f32_i32_e32 v176, v76
	v_cvt_f32_i32_e32 v177, v72
	v_cvt_f32_i32_e32 v178, v77
	v_cvt_f32_i32_e32 v179, v73
	v_cvt_f32_i32_e32 v180, v78
	v_cvt_f32_i32_e32 v181, v74
	v_cvt_f32_i32_e32 v182, v79
	v_cvt_f32_i32_e32 v183, v75
	v_mad_i32_i24 v163, v161, s57, v163
	v_lshl_add_u64 v[164:165], v[162:163], 0, v[146:147]
	s_waitcnt vmcnt(0)
	v_mul_f32_e32 v160, v120, v153
	v_mul_f32_e32 v161, v112, v153
	v_mul_f32_e32 v162, v121, v153
	v_mul_f32_e32 v163, v113, v153
	v_mul_f32_e32 v184, v122, v153
	v_mul_f32_e32 v185, v114, v153
	v_mul_f32_e32 v186, v123, v153
	v_mul_f32_e32 v187, v115, v153
	v_mul_f32_e32 v159, v160, v159
	v_mul_f32_e32 v167, v161, v167
	v_mul_f32_e32 v160, v162, v170
	v_mul_f32_e32 v162, v163, v171
	v_mul_f32_e32 v161, v184, v172
	v_mul_f32_e32 v163, v185, v173
	v_mul_f32_e32 v188, v100, v153
	v_mul_f32_e32 v189, v92, v153
	v_mul_f32_e32 v190, v101, v153
	v_mul_f32_e32 v191, v93, v153
	v_mul_f32_e32 v192, v102, v153
	v_mul_f32_e32 v193, v94, v153
	v_mul_f32_e32 v194, v103, v153
	v_mul_f32_e32 v153, v95, v153
	v_mul_f32_e32 v170, v186, v174
	v_mul_f32_e32 v171, v187, v175
	v_cvt_pk_bf16_f32 v160, v159, v160
	v_cvt_pk_bf16_f32 v161, v161, v170
	v_cvt_pk_bf16_f32 v162, v167, v162
	v_cvt_pk_bf16_f32 v163, v163, v171
	v_mul_f32_e32 v172, v188, v176
	v_mul_f32_e32 v173, v189, v177
	v_mul_f32_e32 v174, v190, v178
	v_mul_f32_e32 v175, v191, v179
	v_mul_f32_e32 v176, v192, v180
	v_mul_f32_e32 v177, v193, v181
	v_mul_f32_e32 v178, v194, v182
	v_mul_f32_e32 v153, v153, v183
	global_store_dwordx4 v[164:165], v[160:163], off sc1
	v_ashrrev_i32_e32 v167, 31, v166
	v_cvt_f32_i32_e32 v159, v60
	v_cvt_pk_bf16_f32 v160, v172, v174
	v_cvt_pk_bf16_f32 v161, v176, v178
	v_cvt_pk_bf16_f32 v162, v173, v175
	v_cvt_pk_bf16_f32 v163, v177, v153
	global_store_dwordx4 v[164:165], v[160:163], off offset:256 sc1
	global_load_dword v153, v[168:169], off
	v_add_u32_e32 v164, 48, v152
	v_add_u32_e32 v160, s56, v164
	v_ashrrev_i32_e32 v161, 31, v160
	v_cvt_f32_i32_e32 v165, v56
	v_cvt_f32_i32_e32 v170, v61
	v_cvt_f32_i32_e32 v171, v57
	v_cvt_f32_i32_e32 v172, v62
	v_cvt_f32_i32_e32 v173, v58
	v_lshl_add_u64 v[168:169], v[160:161], 2, s[36:37]
	v_lshl_add_u64 v[160:161], s[64:65], 0, v[166:167]
	v_cvt_f32_i32_e32 v174, v63
	v_cvt_f32_i32_e32 v175, v59
	v_mad_u64_u32 v[162:163], s[66:67], v160, s57, v[144:145]
	v_cvt_f32_i32_e32 v176, v44
	v_cvt_f32_i32_e32 v177, v40
	v_cvt_f32_i32_e32 v178, v45
	v_cvt_f32_i32_e32 v179, v41
	v_cvt_f32_i32_e32 v180, v46
	v_cvt_f32_i32_e32 v181, v42
	v_cvt_f32_i32_e32 v182, v47
	v_cvt_f32_i32_e32 v183, v43
	v_mad_i32_i24 v163, v161, s57, v163
	v_lshl_add_u64 v[166:167], v[162:163], 0, v[146:147]
	s_waitcnt vmcnt(0)
; #define GAS __attribute__((address_space(1)))
; __device__ __forceinline__ v4u pack8(const f32x4 a, const f32x4 b) { v4u w; w.x = cvt_pk_bf16(a[0], a[1]); w.y = cvt_pk_bf16(a[2], a[3]); w.z = cvt_pk_bf16(b[0], b[1]); w.w = cvt_pk_bf16(b[2], b[3]); return w; }
; #define EPI_LOOP_AM for (int ai = 0; ai < 2; ++ai) _Pragma("unroll") for (int m = 0; m < 4; ++m)
;     __device__ __forceinline__ void operator()(AccI& acc, const Unit& u, LAS unsigned char*, int wr, int wc, int fr, int fq) const {
;     ...
;             const int h = pm - 4;
; #pragma unroll
;             EPI_LOOP_AM { const int dv = 128 * ai + 64 * wr + 16 * m + fr; const float swr = swin[u.p2 + dv];
; #pragma unroll
;                 for (int bj = 0; bj < 2; ++bj) { f32x4 v0, v1;
; #pragma unroll
;                     for (int j = 0; j < 4; ++j) { v0[j] = (float)acc[ai][bj][m][0][j] * (swr * sxc[bj][0][j]); v1[j] = (float)acc[ai][bj][m][1][j] * (swr * sxc[bj][1][j]); }
;                     *(GAS v4u*)(Bcat + ((size_t)(h * NCH + n_ch) * 256 + dv) * CAT + 128 * bj + c0) = pack8(v0, v1); } }
	v_mul_f32_e32 v160, v120, v153
	v_mul_f32_e32 v161, v112, v153
	v_mul_f32_e32 v162, v121, v153
	v_mul_f32_e32 v163, v113, v153
	v_mul_f32_e32 v184, v122, v153
	v_mul_f32_e32 v185, v114, v153
	v_mul_f32_e32 v186, v123, v153
	v_mul_f32_e32 v187, v115, v153
	v_mul_f32_e32 v159, v160, v159
	v_mul_f32_e32 v165, v161, v165
	v_mul_f32_e32 v160, v162, v170
	v_mul_f32_e32 v162, v163, v171
	v_mul_f32_e32 v161, v184, v172
	v_mul_f32_e32 v163, v185, v173
	v_mul_f32_e32 v188, v100, v153
	v_mul_f32_e32 v189, v92, v153
	v_mul_f32_e32 v190, v101, v153
	v_mul_f32_e32 v191, v93, v153
	v_mul_f32_e32 v192, v102, v153
	v_mul_f32_e32 v193, v94, v153
	v_mul_f32_e32 v194, v103, v153
	v_mul_f32_e32 v153, v95, v153
	v_mul_f32_e32 v170, v186, v174
	v_mul_f32_e32 v171, v187, v175
	v_cvt_pk_bf16_f32 v160, v159, v160
	v_cvt_pk_bf16_f32 v161, v161, v170
	v_cvt_pk_bf16_f32 v162, v165, v162
	v_cvt_pk_bf16_f32 v163, v163, v171
	v_mul_f32_e32 v172, v188, v176
	v_mul_f32_e32 v173, v189, v177
	v_mul_f32_e32 v174, v190, v178
	v_mul_f32_e32 v175, v191, v179
	v_mul_f32_e32 v176, v192, v180
	v_mul_f32_e32 v177, v193, v181
	v_mul_f32_e32 v178, v194, v182
	v_mul_f32_e32 v153, v153, v183
	global_store_dwordx4 v[166:167], v[160:163], off sc1
	v_ashrrev_i32_e32 v165, 31, v164
	v_cvt_f32_i32_e32 v159, v28
	v_cvt_pk_bf16_f32 v160, v172, v174
	v_cvt_pk_bf16_f32 v161, v176, v178
	v_cvt_pk_bf16_f32 v162, v173, v175
	v_cvt_pk_bf16_f32 v163, v177, v153
	global_store_dwordx4 v[166:167], v[160:163], off offset:256 sc1
	global_load_dword v153, v[168:169], off
	v_add_u32_e32 v166, 0x80, v152
	v_add_u32_e32 v160, s56, v166
	v_ashrrev_i32_e32 v161, 31, v160
	v_cvt_f32_i32_e32 v167, v24
	v_cvt_f32_i32_e32 v170, v29
	v_cvt_f32_i32_e32 v171, v25
	v_cvt_f32_i32_e32 v172, v30
	v_cvt_f32_i32_e32 v173, v26
	v_lshl_add_u64 v[168:169], v[160:161], 2, s[36:37]
	v_lshl_add_u64 v[160:161], s[64:65], 0, v[164:165]
	v_cvt_f32_i32_e32 v174, v31
	v_cvt_f32_i32_e32 v175, v27
	v_mad_u64_u32 v[162:163], s[66:67], v160, s57, v[144:145]
	v_cvt_f32_i32_e32 v176, v12
	v_cvt_f32_i32_e32 v177, v8
	v_cvt_f32_i32_e32 v178, v13
	v_cvt_f32_i32_e32 v179, v9
	v_cvt_f32_i32_e32 v180, v14
	v_cvt_f32_i32_e32 v181, v10
	v_cvt_f32_i32_e32 v182, v15
	v_cvt_f32_i32_e32 v183, v11
	v_mad_i32_i24 v163, v161, s57, v163
	v_lshl_add_u64 v[164:165], v[162:163], 0, v[146:147]
	s_waitcnt vmcnt(0)
	v_mul_f32_e32 v160, v120, v153
	v_mul_f32_e32 v161, v112, v153
	v_mul_f32_e32 v162, v121, v153
	v_mul_f32_e32 v163, v113, v153
	v_mul_f32_e32 v184, v122, v153
	v_mul_f32_e32 v185, v114, v153
	v_mul_f32_e32 v186, v123, v153
	v_mul_f32_e32 v187, v115, v153
	v_mul_f32_e32 v159, v160, v159
	v_mul_f32_e32 v167, v161, v167
	v_mul_f32_e32 v160, v162, v170
	v_mul_f32_e32 v162, v163, v171
	v_mul_f32_e32 v161, v184, v172
	v_mul_f32_e32 v163, v185, v173
	v_mul_f32_e32 v188, v100, v153
	v_mul_f32_e32 v189, v92, v153
	v_mul_f32_e32 v190, v101, v153
	v_mul_f32_e32 v191, v93, v153
	v_mul_f32_e32 v192, v102, v153
	v_mul_f32_e32 v193, v94, v153
	v_mul_f32_e32 v194, v103, v153
	v_mul_f32_e32 v153, v95, v153
	v_mul_f32_e32 v170, v186, v174
	v_mul_f32_e32 v171, v187, v175
	v_cvt_pk_bf16_f32 v160, v159, v160
	v_cvt_pk_bf16_f32 v161, v161, v170
	v_cvt_pk_bf16_f32 v162, v167, v162
	v_cvt_pk_bf16_f32 v163, v163, v171
	v_mul_f32_e32 v172, v188, v176
	v_mul_f32_e32 v173, v189, v177
	v_mul_f32_e32 v174, v190, v178
	v_mul_f32_e32 v175, v191, v179
	v_mul_f32_e32 v176, v192, v180
	v_mul_f32_e32 v177, v193, v181
	v_mul_f32_e32 v178, v194, v182
	v_mul_f32_e32 v153, v153, v183
	global_store_dwordx4 v[164:165], v[160:163], off sc1
	v_ashrrev_i32_e32 v167, 31, v166
	v_cvt_f32_i32_e32 v159, v136
	v_cvt_pk_bf16_f32 v160, v172, v174
	v_cvt_pk_bf16_f32 v161, v176, v178
	v_cvt_pk_bf16_f32 v162, v173, v175
	v_cvt_pk_bf16_f32 v163, v177, v153
	global_store_dwordx4 v[164:165], v[160:163], off offset:256 sc1
	global_load_dword v153, v[168:169], off
	v_add_u32_e32 v164, 0x90, v152
	v_add_u32_e32 v160, s56, v164
	v_ashrrev_i32_e32 v161, 31, v160
	v_cvt_f32_i32_e32 v165, v128
	v_cvt_f32_i32_e32 v170, v137
	v_cvt_f32_i32_e32 v171, v129
	v_cvt_f32_i32_e32 v172, v138
	v_cvt_f32_i32_e32 v173, v130
	v_lshl_add_u64 v[168:169], v[160:161], 2, s[36:37]
	v_lshl_add_u64 v[160:161], s[64:65], 0, v[166:167]
	v_cvt_f32_i32_e32 v174, v139
	v_cvt_f32_i32_e32 v175, v131
	v_mad_u64_u32 v[162:163], s[66:67], v160, s57, v[144:145]
	v_cvt_f32_i32_e32 v176, v116
	v_cvt_f32_i32_e32 v177, v104
	v_cvt_f32_i32_e32 v178, v117
	v_cvt_f32_i32_e32 v179, v105
	v_cvt_f32_i32_e32 v180, v118
	v_cvt_f32_i32_e32 v181, v106
	v_cvt_f32_i32_e32 v182, v119
	v_cvt_f32_i32_e32 v183, v107
	v_mad_i32_i24 v163, v161, s57, v163
	v_lshl_add_u64 v[166:167], v[162:163], 0, v[146:147]
	s_waitcnt vmcnt(0)
; #define GAS __attribute__((address_space(1)))
; __device__ __forceinline__ v4u pack8(const f32x4 a, const f32x4 b) { v4u w; w.x = cvt_pk_bf16(a[0], a[1]); w.y = cvt_pk_bf16(a[2], a[3]); w.z = cvt_pk_bf16(b[0], b[1]); w.w = cvt_pk_bf16(b[2], b[3]); return w; }
; #define EPI_LOOP_AM for (int ai = 0; ai < 2; ++ai) _Pragma("unroll") for (int m = 0; m < 4; ++m)
;     __device__ __forceinline__ void operator()(AccI& acc, const Unit& u, LAS unsigned char*, int wr, int wc, int fr, int fq) const {
;     ...
;             const int h = pm - 4;
; #pragma unroll
;             EPI_LOOP_AM { const int dv = 128 * ai + 64 * wr + 16 * m + fr; const float swr = swin[u.p2 + dv];
; #pragma unroll
;                 for (int bj = 0; bj < 2; ++bj) { f32x4 v0, v1;
; #pragma unroll
;                     for (int j = 0; j < 4; ++j) { v0[j] = (float)acc[ai][bj][m][0][j] * (swr * sxc[bj][0][j]); v1[j] = (float)acc[ai][bj][m][1][j] * (swr * sxc[bj][1][j]); }
;                     *(GAS v4u*)(Bcat + ((size_t)(h * NCH + n_ch) * 256 + dv) * CAT + 128 * bj + c0) = pack8(v0, v1); } }
	v_mul_f32_e32 v160, v120, v153
	v_mul_f32_e32 v161, v112, v153
	v_mul_f32_e32 v162, v121, v153
	v_mul_f32_e32 v163, v113, v153
	v_mul_f32_e32 v184, v122, v153
	v_mul_f32_e32 v185, v114, v153
	v_mul_f32_e32 v186, v123, v153
	v_mul_f32_e32 v187, v115, v153
	v_mul_f32_e32 v159, v160, v159
	v_mul_f32_e32 v165, v161, v165
	v_mul_f32_e32 v160, v162, v170
	v_mul_f32_e32 v162, v163, v171
	v_mul_f32_e32 v161, v184, v172
	v_mul_f32_e32 v163, v185, v173
	v_mul_f32_e32 v188, v100, v153
	v_mul_f32_e32 v189, v92, v153
	v_mul_f32_e32 v190, v101, v153
	v_mul_f32_e32 v191, v93, v153
	v_mul_f32_e32 v192, v102, v153
	v_mul_f32_e32 v193, v94, v153
	v_mul_f32_e32 v194, v103, v153
	v_mul_f32_e32 v153, v95, v153
	v_mul_f32_e32 v170, v186, v174
	v_mul_f32_e32 v171, v187, v175
	v_cvt_pk_bf16_f32 v160, v159, v160
	v_cvt_pk_bf16_f32 v161, v161, v170
	v_cvt_pk_bf16_f32 v162, v165, v162
	v_cvt_pk_bf16_f32 v163, v163, v171
	v_mul_f32_e32 v172, v188, v176
	v_mul_f32_e32 v173, v189, v177
	v_mul_f32_e32 v174, v190, v178
	v_mul_f32_e32 v175, v191, v179
	v_mul_f32_e32 v176, v192, v180
	v_mul_f32_e32 v177, v193, v181
	v_mul_f32_e32 v178, v194, v182
	v_mul_f32_e32 v153, v153, v183
	global_store_dwordx4 v[166:167], v[160:163], off sc1
	v_ashrrev_i32_e32 v165, 31, v164
	v_cvt_f32_i32_e32 v159, v84
	v_cvt_pk_bf16_f32 v160, v172, v174
	v_cvt_pk_bf16_f32 v161, v176, v178
	v_cvt_pk_bf16_f32 v162, v173, v175
	v_cvt_pk_bf16_f32 v163, v177, v153
	global_store_dwordx4 v[166:167], v[160:163], off offset:256 sc1
	global_load_dword v153, v[168:169], off
	v_add_u32_e32 v166, 0xa0, v152
	v_add_u32_e32 v160, s56, v166
	v_ashrrev_i32_e32 v161, 31, v160
	v_cvt_f32_i32_e32 v167, v80
	v_cvt_f32_i32_e32 v170, v85
	v_cvt_f32_i32_e32 v171, v81
	v_cvt_f32_i32_e32 v172, v86
	v_cvt_f32_i32_e32 v173, v82
	v_lshl_add_u64 v[168:169], v[160:161], 2, s[36:37]
	v_lshl_add_u64 v[160:161], s[64:65], 0, v[164:165]
	v_cvt_f32_i32_e32 v174, v87
	v_cvt_f32_i32_e32 v175, v83
	v_mad_u64_u32 v[162:163], s[66:67], v160, s57, v[144:145]
	v_cvt_f32_i32_e32 v176, v68
	v_cvt_f32_i32_e32 v177, v64
	v_cvt_f32_i32_e32 v178, v69
	v_cvt_f32_i32_e32 v179, v65
	v_cvt_f32_i32_e32 v180, v70
	v_cvt_f32_i32_e32 v181, v66
	v_cvt_f32_i32_e32 v182, v71
	v_cvt_f32_i32_e32 v183, v67
	v_mad_i32_i24 v163, v161, s57, v163
	v_lshl_add_u64 v[164:165], v[162:163], 0, v[146:147]
	v_add_u32_e32 v152, 0xb0, v152
	s_waitcnt vmcnt(0)
	v_mul_f32_e32 v160, v120, v153
	v_mul_f32_e32 v161, v112, v153
	v_mul_f32_e32 v162, v121, v153
	v_mul_f32_e32 v163, v113, v153
	v_mul_f32_e32 v184, v122, v153
	v_mul_f32_e32 v185, v114, v153
	v_mul_f32_e32 v186, v123, v153
	v_mul_f32_e32 v187, v115, v153
	v_mul_f32_e32 v159, v160, v159
	v_mul_f32_e32 v167, v161, v167
	v_mul_f32_e32 v160, v162, v170
	v_mul_f32_e32 v162, v163, v171
	v_mul_f32_e32 v161, v184, v172
	v_mul_f32_e32 v163, v185, v173
	v_mul_f32_e32 v188, v100, v153
	v_mul_f32_e32 v189, v92, v153
	v_mul_f32_e32 v190, v101, v153
	v_mul_f32_e32 v191, v93, v153
	v_mul_f32_e32 v192, v102, v153
	v_mul_f32_e32 v193, v94, v153
	v_mul_f32_e32 v194, v103, v153
	v_mul_f32_e32 v153, v95, v153
	v_mul_f32_e32 v170, v186, v174
	v_mul_f32_e32 v171, v187, v175
	v_cvt_pk_bf16_f32 v160, v159, v160
	v_cvt_pk_bf16_f32 v161, v161, v170
	v_cvt_pk_bf16_f32 v162, v167, v162
	v_cvt_pk_bf16_f32 v163, v163, v171
	v_mul_f32_e32 v172, v188, v176
	v_mul_f32_e32 v173, v189, v177
	v_mul_f32_e32 v174, v190, v178
	v_mul_f32_e32 v175, v191, v179
	v_mul_f32_e32 v176, v192, v180
	v_mul_f32_e32 v177, v193, v181
	v_mul_f32_e32 v178, v194, v182
	v_mul_f32_e32 v153, v153, v183
	global_store_dwordx4 v[164:165], v[160:163], off sc1
	v_ashrrev_i32_e32 v167, 31, v166
	v_cvt_f32_i32_e32 v159, v52
	v_cvt_pk_bf16_f32 v160, v172, v174
	v_cvt_pk_bf16_f32 v161, v176, v178
	v_cvt_pk_bf16_f32 v162, v173, v175
	v_cvt_pk_bf16_f32 v163, v177, v153
	global_store_dwordx4 v[164:165], v[160:163], off offset:256 sc1
	global_load_dword v153, v[168:169], off
	v_cvt_f32_i32_e32 v168, v48
	v_add_u32_e32 v160, s56, v152
	v_ashrrev_i32_e32 v161, 31, v160
	v_cvt_f32_i32_e32 v169, v53
	v_cvt_f32_i32_e32 v170, v49
	v_cvt_f32_i32_e32 v171, v54
	v_cvt_f32_i32_e32 v172, v50
	v_lshl_add_u64 v[164:165], v[160:161], 2, s[36:37]
	v_lshl_add_u64 v[160:161], s[64:65], 0, v[166:167]
	v_cvt_f32_i32_e32 v173, v55
	v_cvt_f32_i32_e32 v174, v51
	v_mad_u64_u32 v[162:163], s[66:67], v160, s57, v[144:145]
	v_cvt_f32_i32_e32 v175, v36
	v_cvt_f32_i32_e32 v176, v32
	v_cvt_f32_i32_e32 v177, v37
	v_cvt_f32_i32_e32 v178, v33
	v_cvt_f32_i32_e32 v179, v38
	v_cvt_f32_i32_e32 v180, v34
	v_cvt_f32_i32_e32 v181, v39
	v_cvt_f32_i32_e32 v182, v35
	v_mad_i32_i24 v163, v161, s57, v163
	v_lshl_add_u64 v[166:167], v[162:163], 0, v[146:147]
	s_mov_b64 s[66:67], 0x100
	s_waitcnt vmcnt(0)
; #define GAS __attribute__((address_space(1)))
; __device__ __forceinline__ v4u pack8(const f32x4 a, const f32x4 b) { v4u w; w.x = cvt_pk_bf16(a[0], a[1]); w.y = cvt_pk_bf16(a[2], a[3]); w.z = cvt_pk_bf16(b[0], b[1]); w.w = cvt_pk_bf16(b[2], b[3]); return w; }
; #define EPI_LOOP_AM for (int ai = 0; ai < 2; ++ai) _Pragma("unroll") for (int m = 0; m < 4; ++m)
;     __device__ __forceinline__ void operator()(AccI& acc, const Unit& u, LAS unsigned char*, int wr, int wc, int fr, int fq) const {
;     ...
;             const int h = pm - 4;
; #pragma unroll
;             EPI_LOOP_AM { const int dv = 128 * ai + 64 * wr + 16 * m + fr; const float swr = swin[u.p2 + dv];
; #pragma unroll
;                 for (int bj = 0; bj < 2; ++bj) { f32x4 v0, v1;
; #pragma unroll
;                     for (int j = 0; j < 4; ++j) { v0[j] = (float)acc[ai][bj][m][0][j] * (swr * sxc[bj][0][j]); v1[j] = (float)acc[ai][bj][m][1][j] * (swr * sxc[bj][1][j]); }
;                     *(GAS v4u*)(Bcat + ((size_t)(h * NCH + n_ch) * 256 + dv) * CAT + 128 * bj + c0) = pack8(v0, v1); } }
	v_mul_f32_e32 v160, v120, v153
	v_mul_f32_e32 v161, v112, v153
	v_mul_f32_e32 v162, v121, v153
	v_mul_f32_e32 v163, v113, v153
	v_mul_f32_e32 v183, v122, v153
	v_mul_f32_e32 v184, v114, v153
	v_mul_f32_e32 v185, v123, v153
	v_mul_f32_e32 v186, v115, v153
	v_mul_f32_e32 v159, v160, v159
	v_mul_f32_e32 v168, v161, v168
	v_mul_f32_e32 v160, v162, v169
	v_mul_f32_e32 v162, v163, v170
	v_mul_f32_e32 v161, v183, v171
	v_mul_f32_e32 v163, v184, v172
	v_mul_f32_e32 v187, v100, v153
	v_mul_f32_e32 v188, v92, v153
	v_mul_f32_e32 v189, v101, v153
	v_mul_f32_e32 v190, v93, v153
	v_mul_f32_e32 v191, v102, v153
	v_mul_f32_e32 v192, v94, v153
	v_mul_f32_e32 v193, v103, v153
	v_mul_f32_e32 v153, v95, v153
	v_mul_f32_e32 v169, v185, v173
	v_mul_f32_e32 v170, v186, v174
	v_cvt_pk_bf16_f32 v160, v159, v160
	v_cvt_pk_bf16_f32 v161, v161, v169
	v_cvt_pk_bf16_f32 v162, v168, v162
	v_cvt_pk_bf16_f32 v163, v163, v170
	v_mul_f32_e32 v171, v187, v175
	v_mul_f32_e32 v172, v188, v176
	v_mul_f32_e32 v173, v189, v177
	v_mul_f32_e32 v174, v190, v178
	v_mul_f32_e32 v175, v191, v179
	v_mul_f32_e32 v176, v192, v180
	v_mul_f32_e32 v177, v193, v181
	v_mul_f32_e32 v153, v153, v182
	global_store_dwordx4 v[166:167], v[160:163], off sc1
	v_cvt_f32_i32_e32 v168, v23
	v_cvt_f32_i32_e32 v169, v19
	v_cvt_pk_bf16_f32 v160, v171, v173
	v_cvt_pk_bf16_f32 v161, v175, v177
	v_cvt_pk_bf16_f32 v162, v172, v174
	v_cvt_pk_bf16_f32 v163, v176, v153
	global_store_dwordx4 v[166:167], v[160:163], off offset:256 sc1
	global_load_dword v159, v[164:165], off
	v_ashrrev_i32_e32 v153, 31, v152
	v_cvt_f32_i32_e32 v162, v20
	v_cvt_f32_i32_e32 v163, v16
	v_cvt_f32_i32_e32 v164, v21
	v_cvt_f32_i32_e32 v165, v17
	v_cvt_f32_i32_e32 v166, v22
	v_lshl_add_u64 v[152:153], s[64:65], 0, v[152:153]
	v_cvt_f32_i32_e32 v167, v18
	v_mad_u64_u32 v[144:145], s[64:65], v152, s57, v[144:145]
	v_cvt_f32_i32_e32 v170, v4
	v_cvt_f32_i32_e32 v171, v0
	v_cvt_f32_i32_e32 v172, v5
	v_cvt_f32_i32_e32 v173, v1
	v_cvt_f32_i32_e32 v174, v6
	v_cvt_f32_i32_e32 v175, v2
	v_cvt_f32_i32_e32 v176, v7
	v_cvt_f32_i32_e32 v177, v3
	v_mad_i32_i24 v145, v153, s57, v145
	v_lshl_add_u64 v[160:161], v[144:145], 0, v[146:147]
	v_lshl_add_u64 v[152:153], v[160:161], 0, s[66:67]
	s_waitcnt vmcnt(0)
	v_mul_f32_e32 v144, v120, v159
	v_mul_f32_e32 v145, v112, v159
	v_mul_f32_e32 v146, v121, v159
	v_mul_f32_e32 v147, v113, v159
	v_mul_f32_e32 v178, v122, v159
	v_mul_f32_e32 v179, v114, v159
	v_mul_f32_e32 v180, v123, v159
	v_mul_f32_e32 v181, v115, v159
	v_mul_f32_e32 v144, v144, v162
	v_mul_f32_e32 v162, v145, v163
	v_mul_f32_e32 v145, v146, v164
	v_mul_f32_e32 v146, v147, v165
	v_mul_f32_e32 v147, v178, v166
	v_mul_f32_e32 v182, v100, v159
	v_mul_f32_e32 v183, v92, v159
	v_mul_f32_e32 v184, v101, v159
	v_mul_f32_e32 v185, v93, v159
	v_mul_f32_e32 v186, v102, v159
	v_mul_f32_e32 v187, v94, v159
	v_mul_f32_e32 v188, v103, v159
	v_mul_f32_e32 v159, v95, v159
	v_mul_f32_e32 v163, v179, v167
	v_mul_f32_e32 v164, v180, v168
	v_mul_f32_e32 v165, v181, v169
	v_cvt_pk_bf16_f32 v144, v144, v145
	v_cvt_pk_bf16_f32 v145, v147, v164
	v_cvt_pk_bf16_f32 v146, v162, v146
	v_cvt_pk_bf16_f32 v147, v163, v165
	v_mul_f32_e32 v166, v182, v170
	v_mul_f32_e32 v167, v183, v171
	v_mul_f32_e32 v168, v184, v172
	v_mul_f32_e32 v169, v185, v173
	v_mul_f32_e32 v170, v186, v174
	v_mul_f32_e32 v171, v187, v175
	v_mul_f32_e32 v172, v188, v176
	v_mul_f32_e32 v159, v159, v177
	global_store_dwordx4 v[160:161], v[144:147], off sc1
	s_nop 1
	v_cvt_pk_bf16_f32 v144, v166, v168
	v_cvt_pk_bf16_f32 v145, v170, v172
	v_cvt_pk_bf16_f32 v146, v167, v169
	v_cvt_pk_bf16_f32 v147, v171, v159
	s_cbranch_execz .LBB0_295
.LBB0_293:
	s_andn2_b64 vcc, exec, s[46:47]
	s_mov_b64 s[46:47], -1
	global_store_dwordx4 v[152:153], v[144:147], off sc1
	s_cbranch_vccnz .LBB0_275
	s_branch .LBB0_296

; __device__ __forceinline__ float fexp(float x) { return __builtin_amdgcn_exp2f(x * 1.4426950408889634f); }
; __device__ __forceinline__ void cs_rev(float rev, float& c, float& s) { const float f = __builtin_amdgcn_fractf(rev); c = __builtin_amdgcn_cosf(f); s = __builtin_amdgcn_sinf(f); }
;     __device__ __forceinline__ void operator()(AccI& acc, const Unit& u, LAS unsigned char*, int wr, int wc, int fr, int fq) const {
;     ...
;             const int h = pm; const float lgf = -fexp(dec_f[h]), lgb = -fexp(dec_b[h]);
; #pragma unroll
;             for (int m = 0; m < 4; ++m) {
;                 const int d = 64 * wr + 16 * m + fr;
;                 const float sw1 = swin[u.p2 + d], sw2 = swin[u.p2 + 128 + d];
;                 const float inv = __builtin_amdgcn_exp2f(-(float)d * (13.287712379549449f / 128.f)) * 0.15915494309189535f;
; #pragma unroll
;                 for (int bj = 0; bj < 2; ++bj) {
;                     f32x4 f1[2], f2[2], b1[2], b2[2];
; #pragma unroll
;                     for (int n = 0; n < 2; ++n)
; #pragma unroll
;                         for (int j = 0; j < 4; ++j) { const int il = 128 * bj + c0 + 4 * n + j; const float pos = (float)(n_ch * 256 + il); float c, s; cs_rev(pos * inv, c, s);
;                             const float x1 = (float)acc[0][bj][m][n][j] * (sw1 * sxc[bj][n][j]), x2 = (float)acc[1][bj][m][n][j] * (sw2 * sxc[bj][n][j]); const float o1 = (x1 * c - x2 * s) * 0.0625f, o2 = (x2 * c + x1 * s) * 0.0625f;
;                             const float wf = fexp(lgf * (float)(255 - il)), wb = fexp(lgb * (float)(il + 1));
;                             f1[n][j] = o1 * wf; f2[n][j] = o2 * wf; b1[n][j] = o1 * wb; b2[n][j] = o2 * wb; }
.LBB0_295:
	s_ashr_i32 s59, s58, 31
	v_add_u32_e32 v146, s26, v148
	s_lshl_b64 s[64:65], s[58:59], 2
	v_add_u32_e32 v144, s56, v146
	s_add_u32 s66, s14, s64
	v_ashrrev_i32_e32 v145, 31, v144
	s_addc_u32 s67, s15, s65
	v_lshl_add_u64 v[152:153], v[144:145], 2, s[36:37]
	v_add_u32_e32 v144, 0x80, v144
	global_load_dword v159, v149, s[66:67]
	s_add_u32 s64, s30, s64
	v_ashrrev_i32_e32 v145, 31, v144
	v_lshl_add_u64 v[160:161], v[144:145], 2, s[36:37]
	global_load_dword v144, v[152:153], off
	global_load_dword v145, v[160:161], off
	s_addc_u32 s65, s31, s65
	global_load_dword v153, v149, s[64:65]
	v_cvt_f32_i32_e32 v162, v141
	v_cvt_f32_i32_e32 v141, v146
	v_cvt_f32_i32_e32 v160, v140
	v_or_b32_e32 v140, 1, v150
	v_or_b32_e32 v176, 2, v150
	v_cvt_f32_i32_e32 v177, v140
	v_add_u32_e32 v147, s62, v140
	v_sub_u32_e32 v140, 0xff, v140
	v_add_u32_e32 v164, s62, v176
	v_cvt_f32_i32_e32 v181, v140
	v_mul_f32_e32 v140, 0xbdd49a78, v141
	v_add_u32_e32 v179, s62, v150
	v_cvt_f32_i32_e32 v148, v147
	v_cvt_f32_i32_e32 v147, v164
	v_exp_f32_e32 v164, v140
	v_cvt_f32_i32_e32 v152, v179
	v_cvt_f32_i32_e32 v161, v136
	v_cvt_f32_i32_e32 v163, v137
	v_mul_f32_e32 v184, 0.15915494, v164
	v_mul_f32_e32 v164, v184, v152
	v_mul_f32_e32 v165, v184, v148
	v_fract_f32_e32 v164, v164
	v_fract_f32_e32 v166, v165
	v_sin_f32_e32 v165, v164
	v_cos_f32_e32 v164, v164
	v_sin_f32_e32 v167, v166
	v_cos_f32_e32 v166, v166
	v_sub_u32_e32 v136, 0xff, v150
	v_cvt_f32_i32_e32 v136, v136
	v_cvt_f32_i32_e32 v180, v176
	v_mov_b32_e32 v168, v165
	v_mov_b32_e32 v169, v164
	v_mov_b32_e32 v170, v167
	v_mov_b32_e32 v171, v166
	v_add_u32_e32 v178, 0x84, v150
	v_add_u32_e32 v137, s62, v178
	v_cvt_f32_i32_e32 v137, v137
	s_lshl_b32 s45, s58, 8
	v_add_u32_e32 v140, s45, v146
	v_ashrrev_i32_e32 v141, 31, v140
	s_ashr_i32 s61, s60, 31
	v_lshlrev_b64 v[140:141], 15, v[140:141]
	s_lshl_b64 s[58:59], s[60:61], 9
	v_cvt_f32_i32_e32 v178, v178
	v_cvt_f32_i32_e32 v87, v87
	v_cvt_f32_i32_e32 v83, v83
	v_cvt_f32_i32_e32 v71, v71
	v_cvt_f32_i32_e32 v67, v67
	v_cvt_f32_i32_e32 v55, v55
	v_cvt_f32_i32_e32 v51, v51
	v_cvt_f32_i32_e32 v39, v39
	v_cvt_f32_i32_e32 v35, v35
	v_cvt_f32_i32_e32 v23, v23
	v_cvt_f32_i32_e32 v19, v19
	v_cvt_f32_i32_e32 v7, v7
	v_cvt_f32_i32_e32 v3, v3
	s_waitcnt vmcnt(0)
	v_mul_f32_e32 v159, 0x3fb8aa3b, v159
	v_exp_f32_e32 v182, v159
	v_pk_mul_f32 v[172:173], v[120:121], v[144:145] op_sel_hi:[0,1]
	v_pk_mul_f32 v[174:175], v[120:121], v[144:145] op_sel:[1,0]
	v_mul_f32_e32 v153, 0x3fb8aa3b, v153
	v_pk_mul_f32 v[160:161], v[172:173], v[160:161]
	v_pk_mul_f32 v[162:163], v[174:175], v[162:163]
	v_exp_f32_e32 v183, v153
	v_pk_mul_f32 v[164:165], v[164:165], v[160:161]
	v_pk_mul_f32 v[160:161], v[168:169], v[160:161]
	v_pk_mul_f32 v[166:167], v[166:167], v[162:163]
	v_pk_mul_f32 v[162:163], v[170:171], v[162:163]
	v_sub_f32_e32 v153, v164, v165
	v_add_f32_e32 v159, v160, v161
	v_add_f32_e32 v161, v162, v163
	v_mul_f32_e32 v163, 0x3d800000, v153
	v_mul_f32_e64 v136, v136, -v182
	v_mul_f32_e64 v153, v181, -v182
	v_mul_f32_e32 v136, 0x3fb8aa3b, v136
	v_mul_f32_e32 v153, 0x3fb8aa3b, v153
	v_mul_f32_e32 v164, 0x3d800000, v159
	v_exp_f32_e32 v162, v136
	v_mul_f32_e64 v136, v177, -v183
	v_exp_f32_e32 v159, v153
	v_mul_f32_e64 v153, v180, -v183
	v_sub_f32_e32 v160, v166, v167
	v_mul_f32_e32 v136, 0x3fb8aa3b, v136
	v_mul_f32_e32 v153, 0x3fb8aa3b, v153
	v_mul_f32_e32 v165, 0x3d800000, v160
	v_exp_f32_e32 v160, v136
	v_exp_f32_e32 v153, v153
	v_mul_f32_e32 v136, v184, v147
	v_fract_f32_e32 v136, v136
	v_cvt_f32_i32_e32 v167, v138
	v_cvt_f32_i32_e32 v166, v142
	v_mul_f32_e32 v175, v162, v164
	v_mul_f32_e32 v177, v159, v165
	v_mul_f32_e32 v185, v160, v164
	v_mul_f32_e32 v186, v153, v165
	v_cos_f32_e32 v164, v136
	v_sin_f32_e32 v165, v136
	v_pk_mul_f32 v[168:169], v[122:123], v[144:145] op_sel_hi:[0,1]
	v_pk_mul_f32 v[166:167], v[168:169], v[166:167]
	v_sub_u32_e32 v142, 0xff, v176
	v_pk_mul_f32 v[168:169], v[164:165], v[166:167]
	v_cvt_f32_i32_e32 v142, v142
	v_sub_f32_e32 v136, v168, v169
	v_mov_b32_e32 v168, v165
	v_mov_b32_e32 v169, v164
	v_pk_mul_f32 v[164:165], v[168:169], v[166:167]
	v_or_b32_e32 v168, 3, v150
	v_mul_f32_e32 v174, v162, v163
	v_mul_f32_e32 v181, v160, v163
	v_cvt_f32_i32_e32 v163, v168
	v_mul_f32_e64 v142, v142, -v182
	v_mul_f32_e32 v161, 0x3d800000, v161
	v_mul_f32_e32 v142, 0x3fb8aa3b, v142
	v_mul_f32_e32 v180, v159, v161
	v_mul_f32_e32 v187, v153, v161
	v_exp_f32_e32 v161, v142
	v_mul_f32_e64 v142, v163, -v183
	v_mul_f32_e32 v142, 0x3fb8aa3b, v142
	v_add_u32_e32 v163, s62, v168
	v_exp_f32_e32 v142, v142
	v_cvt_f32_i32_e32 v163, v163
	v_mul_f32_e32 v136, 0x3d800000, v136
	v_add_f32_e32 v138, v164, v165
	v_mul_f32_e32 v176, v161, v136
	v_mul_f32_e32 v189, v142, v136
	v_mul_f32_e32 v136, v184, v163
	v_mul_f32_e32 v138, 0x3d800000, v138
	v_fract_f32_e32 v136, v136
	v_cvt_f32_i32_e32 v165, v139
	v_cvt_f32_i32_e32 v164, v143
	v_mul_f32_e32 v188, v161, v138
	v_mul_f32_e32 v190, v142, v138
	v_cos_f32_e32 v138, v136
	v_sin_f32_e32 v139, v136
	v_mov_b32_e32 v136, v123
	v_pk_mul_f32 v[166:167], v[136:137], v[144:145] op_sel_hi:[0,1]
	v_pk_mul_f32 v[164:165], v[166:167], v[164:165]
	v_or_b32_e32 v170, 4, v150
	v_pk_mul_f32 v[166:167], v[138:139], v[164:165]
	v_or_b32_e32 v172, 6, v150
	v_sub_f32_e32 v123, v166, v167
	v_mov_b32_e32 v166, v139
	v_mov_b32_e32 v167, v138
	v_pk_mul_f32 v[138:139], v[166:167], v[164:165]
	v_mul_f32_e32 v169, 0x3d800000, v123
	v_add_f32_e32 v123, v138, v139
	v_sub_u32_e32 v138, 0xff, v168
	v_cvt_f32_i32_e32 v138, v138
	v_mul_f32_e32 v165, 0x3d800000, v123
	v_cvt_f32_i32_e32 v123, v170
	v_cvt_f32_i32_e32 v167, v128
	v_mul_f32_e64 v138, v138, -v182
; #define GAS __attribute__((address_space(1)))
; __device__ __forceinline__ v4u pack8(const f32x4 a, const f32x4 b) { v4u w; w.x = cvt_pk_bf16(a[0], a[1]); w.y = cvt_pk_bf16(a[2], a[3]); w.z = cvt_pk_bf16(b[0], b[1]); w.w = cvt_pk_bf16(b[2], b[3]); return w; }
; __device__ __forceinline__ float fexp(float x) { return __builtin_amdgcn_exp2f(x * 1.4426950408889634f); }
; __device__ __forceinline__ void cs_rev(float rev, float& c, float& s) { const float f = __builtin_amdgcn_fractf(rev); c = __builtin_amdgcn_cosf(f); s = __builtin_amdgcn_sinf(f); }
;     __device__ __forceinline__ void operator()(AccI& acc, const Unit& u, LAS unsigned char*, int wr, int wc, int fr, int fq) const {
;     ...
;                 const float inv = __builtin_amdgcn_exp2f(-(float)d * (13.287712379549449f / 128.f)) * 0.15915494309189535f;
; #pragma unroll
;                 for (int bj = 0; bj < 2; ++bj) {
;                     f32x4 f1[2], f2[2], b1[2], b2[2];
; #pragma unroll
;                     for (int n = 0; n < 2; ++n)
; #pragma unroll
;                         for (int j = 0; j < 4; ++j) { const int il = 128 * bj + c0 + 4 * n + j; const float pos = (float)(n_ch * 256 + il); float c, s; cs_rev(pos * inv, c, s);
;                             const float x1 = (float)acc[0][bj][m][n][j] * (sw1 * sxc[bj][n][j]), x2 = (float)acc[1][bj][m][n][j] * (sw2 * sxc[bj][n][j]); const float o1 = (x1 * c - x2 * s) * 0.0625f, o2 = (x2 * c + x1 * s) * 0.0625f;
;                             const float wf = fexp(lgf * (float)(255 - il)), wb = fexp(lgb * (float)(il + 1));
;                             f1[n][j] = o1 * wf; f2[n][j] = o2 * wf; b1[n][j] = o1 * wb; b2[n][j] = o2 * wb; }
;                     const size_t tcol = (size_t)n_ch * 256 + 128 * bj + c0;
;                     bf16* pf = kTw + ((size_t)(h * HD + d)) * T + tcol; bf16* pb = pf + (size_t)RW * T;
;                     *(GAS v4u*)pf = pack8(f1[0], f1[1]); *(GAS v4u*)(pf + (size_t)128 * T) = pack8(f2[0], f2[1]);
;                     *(GAS v4u*)pb = pack8(b1[0], b1[1]); *(GAS v4u*)(pb + (size_t)128 * T) = pack8(b2[0], b2[1]);
	v_mul_f32_e32 v138, 0x3fb8aa3b, v138
	v_exp_f32_e32 v143, v138
	v_add_u32_e32 v138, s62, v170
	v_cvt_f32_i32_e32 v164, v138
	v_mul_f32_e64 v123, v123, -v183
	v_mul_f32_e32 v123, 0x3fb8aa3b, v123
	v_exp_f32_e32 v123, v123
	v_mul_f32_e32 v138, v184, v164
	v_fract_f32_e32 v139, v138
	v_cvt_f32_i32_e32 v166, v132
	v_cos_f32_e32 v138, v139
	v_sin_f32_e32 v139, v139
	v_mul_f32_e32 v191, v143, v169
	v_mul_f32_e32 v193, v123, v169
	v_pk_mul_f32 v[168:169], v[112:113], v[144:145] op_sel_hi:[0,1]
	v_pk_mul_f32 v[166:167], v[168:169], v[166:167]
	v_mul_f32_e32 v192, v143, v165
	v_pk_mul_f32 v[168:169], v[138:139], v[166:167]
	v_mul_f32_e32 v194, v123, v165
	v_sub_f32_e32 v128, v168, v169
	v_mov_b32_e32 v168, v139
	v_mov_b32_e32 v169, v138
	v_pk_mul_f32 v[138:139], v[168:169], v[166:167]
	v_or_b32_e32 v168, 5, v150
	v_add_f32_e32 v132, v138, v139
	v_sub_u32_e32 v138, 0xff, v170
	v_cvt_f32_i32_e32 v138, v138
	v_cvt_f32_i32_e32 v139, v168
	v_mul_f32_e32 v128, 0x3d800000, v128
	v_mul_f32_e32 v132, 0x3d800000, v132
	v_mul_f32_e64 v138, v138, -v182
	v_mul_f32_e32 v138, 0x3fb8aa3b, v138
	v_exp_f32_e32 v166, v138
	v_mul_f32_e64 v138, v139, -v183
	v_mul_f32_e32 v138, 0x3fb8aa3b, v138
	v_exp_f32_e32 v165, v138
	v_add_u32_e32 v138, s62, v168
	v_cvt_f32_i32_e32 v167, v138
	v_mul_f32_e32 v195, v166, v128
	v_mul_f32_e32 v197, v165, v128
	v_cvt_f32_i32_e32 v139, v129
	v_mul_f32_e32 v128, v184, v167
	v_fract_f32_e32 v169, v128
	v_cvt_f32_i32_e32 v138, v133
	v_cos_f32_e32 v128, v169
	v_sin_f32_e32 v129, v169
	v_mul_f32_e32 v196, v166, v132
	v_mul_f32_e32 v198, v165, v132
	v_pk_mul_f32 v[132:133], v[112:113], v[144:145] op_sel:[1,0]
	s_nop 0
	v_pk_mul_f32 v[132:133], v[132:133], v[138:139]
	s_nop 0
	v_pk_mul_f32 v[138:139], v[128:129], v[132:133]
	s_nop 0
	v_sub_f32_e32 v138, v138, v139
	v_mul_f32_e32 v170, 0x3d800000, v138
	v_mov_b32_e32 v138, v129
	v_mov_b32_e32 v139, v128
	v_pk_mul_f32 v[128:129], v[138:139], v[132:133]
	v_cvt_f32_i32_e32 v132, v172
	v_add_f32_e32 v128, v128, v129
	v_sub_u32_e32 v129, 0xff, v168
	v_cvt_f32_i32_e32 v129, v129
	v_cvt_f32_i32_e32 v139, v130
	v_cvt_f32_i32_e32 v138, v134
	v_mul_f32_e32 v128, 0x3d800000, v128
	v_mul_f32_e64 v129, v129, -v182
	v_mul_f32_e32 v129, 0x3fb8aa3b, v129
	v_exp_f32_e32 v168, v129
	v_mul_f32_e64 v129, v132, -v183
	v_add_u32_e32 v132, s62, v172
	v_cvt_f32_i32_e32 v169, v132
	v_mul_f32_e32 v129, 0x3fb8aa3b, v129
	v_exp_f32_e32 v129, v129
	v_mul_f32_e32 v199, v168, v170
	v_mul_f32_e32 v132, v184, v169
	v_fract_f32_e32 v133, v132
	v_cos_f32_e32 v132, v133
	v_sin_f32_e32 v133, v133
	v_mul_f32_e32 v201, v129, v170
	v_pk_mul_f32 v[170:171], v[114:115], v[144:145] op_sel_hi:[0,1]
	v_pk_mul_f32 v[138:139], v[170:171], v[138:139]
	v_mul_f32_e32 v200, v168, v128
	v_pk_mul_f32 v[170:171], v[132:133], v[138:139]
	v_mul_f32_e32 v202, v129, v128
	v_sub_f32_e32 v128, v170, v171
	v_mov_b32_e32 v170, v133
	v_mov_b32_e32 v171, v132
	v_pk_mul_f32 v[132:133], v[170:171], v[138:139]
	v_or_b32_e32 v138, 7, v150
	v_add_f32_e32 v130, v132, v133
	v_sub_u32_e32 v132, 0xff, v172
	v_cvt_f32_i32_e32 v132, v132
	v_cvt_f32_i32_e32 v133, v138
	v_mul_f32_e32 v128, 0x3d800000, v128
	v_mul_f32_e32 v130, 0x3d800000, v130
	v_mul_f32_e64 v132, v132, -v182
	v_mul_f32_e32 v132, 0x3fb8aa3b, v132
	v_exp_f32_e32 v171, v132
	v_mul_f32_e64 v132, v133, -v183
	v_mul_f32_e32 v132, 0x3fb8aa3b, v132
	v_exp_f32_e32 v170, v132
	v_add_u32_e32 v132, s62, v138
	v_cvt_f32_i32_e32 v172, v132
	v_mul_f32_e32 v203, v171, v128
	v_mul_f32_e32 v205, v170, v128
	v_cvt_f32_i32_e32 v133, v131
	v_mul_f32_e32 v128, v184, v172
	v_fract_f32_e32 v128, v128
	v_cvt_f32_i32_e32 v132, v135
	v_mul_f32_e32 v204, v171, v130
	v_mul_f32_e32 v206, v170, v130
	v_cos_f32_e32 v130, v128
	v_sin_f32_e32 v131, v128
	v_mov_b32_e32 v128, v115
	v_pk_mul_f32 v[134:135], v[128:129], v[144:145] op_sel_hi:[0,1]
	v_pk_mul_f32 v[132:133], v[134:135], v[132:133]
	s_nop 0
	v_pk_mul_f32 v[134:135], v[130:131], v[132:133]
	s_nop 0
	v_sub_f32_e32 v115, v134, v135
	v_mov_b32_e32 v134, v131
	v_mov_b32_e32 v135, v130
	v_pk_mul_f32 v[130:131], v[134:135], v[132:133]
	v_mul_f32_e32 v139, 0x3d800000, v115
	v_sub_u32_e32 v115, 0xff, v138
	v_add_f32_e32 v130, v130, v131
	v_add_u32_e32 v131, 8, v150
	v_cvt_f32_i32_e32 v115, v115
	v_cvt_f32_i32_e32 v131, v131
	v_mul_f32_e32 v130, 0x3d800000, v130
	v_cvt_pk_bf16_f32 v138, v174, v177
	v_mul_f32_e64 v115, v115, -v182
	v_mul_f32_e64 v131, v131, -v183
	v_mul_f32_e32 v115, 0x3fb8aa3b, v115
	v_mul_f32_e32 v131, 0x3fb8aa3b, v131
	v_exp_f32_e32 v115, v115
	v_exp_f32_e32 v173, v131
	v_mul_f32_e32 v135, v115, v130
	v_mul_f32_e32 v208, v173, v130
	v_lshl_add_u64 v[130:131], s[6:7], 0, v[140:141]
	v_lshl_add_u64 v[132:133], v[130:131], 0, s[58:59]
	v_lshlrev_b64 v[130:131], 1, v[150:151]
	v_mul_f32_e32 v134, v115, v139
	v_lshl_add_u64 v[132:133], v[132:133], 0, v[130:131]
	v_mul_f32_e32 v207, v173, v139
	v_cvt_pk_bf16_f32 v139, v176, v191
	v_cvt_pk_bf16_f32 v140, v195, v199
	v_cvt_pk_bf16_f32 v141, v203, v134
	v_add_co_u32_e32 v134, vcc, s72, v132
	global_store_dwordx4 v[132:133], v[138:141], off sc1
	s_nop 1
	v_cvt_pk_bf16_f32 v138, v175, v180
	v_cvt_pk_bf16_f32 v139, v188, v192
	v_cvt_pk_bf16_f32 v140, v196, v200
	v_cvt_pk_bf16_f32 v141, v204, v135
	v_addc_co_u32_e32 v135, vcc, 0, v133, vcc
	global_store_dwordx4 v[134:135], v[138:141], off sc1
	v_cvt_pk_bf16_f32 v174, v181, v186
	v_cvt_pk_bf16_f32 v175, v189, v193
	v_cvt_pk_bf16_f32 v176, v197, v201
	v_cvt_pk_bf16_f32 v177, v205, v207
	v_cvt_f32_i32_e32 v186, v124
	s_nop 0
	v_add_u32_e32 v140, 0x80, v179
	v_cvt_f32_i32_e32 v151, v140
	v_add_co_u32_e32 v138, vcc, s73, v132
	v_pk_mul_f32 v[188:189], v[102:103], v[144:145] op_sel_hi:[0,1]
; #define GAS __attribute__((address_space(1)))
; __device__ __forceinline__ v4u pack8(const f32x4 a, const f32x4 b) { v4u w; w.x = cvt_pk_bf16(a[0], a[1]); w.y = cvt_pk_bf16(a[2], a[3]); w.z = cvt_pk_bf16(b[0], b[1]); w.w = cvt_pk_bf16(b[2], b[3]); return w; }
; __device__ __forceinline__ float fexp(float x) { return __builtin_amdgcn_exp2f(x * 1.4426950408889634f); }
; __device__ __forceinline__ void cs_rev(float rev, float& c, float& s) { const float f = __builtin_amdgcn_fractf(rev); c = __builtin_amdgcn_cosf(f); s = __builtin_amdgcn_sinf(f); }
;     __device__ __forceinline__ void operator()(AccI& acc, const Unit& u, LAS unsigned char*, int wr, int wc, int fr, int fq) const {
;     ...
;                         for (int j = 0; j < 4; ++j) { const int il = 128 * bj + c0 + 4 * n + j; const float pos = (float)(n_ch * 256 + il); float c, s; cs_rev(pos * inv, c, s);
;                             const float x1 = (float)acc[0][bj][m][n][j] * (sw1 * sxc[bj][n][j]), x2 = (float)acc[1][bj][m][n][j] * (sw2 * sxc[bj][n][j]); const float o1 = (x1 * c - x2 * s) * 0.0625f, o2 = (x2 * c + x1 * s) * 0.0625f;
;                             const float wf = fexp(lgf * (float)(255 - il)), wb = fexp(lgb * (float)(il + 1));
;                             f1[n][j] = o1 * wf; f2[n][j] = o2 * wf; b1[n][j] = o1 * wb; b2[n][j] = o2 * wb; }
;                     const size_t tcol = (size_t)n_ch * 256 + 128 * bj + c0;
;                     bf16* pf = kTw + ((size_t)(h * HD + d)) * T + tcol; bf16* pb = pf + (size_t)RW * T;
;                     *(GAS v4u*)pf = pack8(f1[0], f1[1]); *(GAS v4u*)(pf + (size_t)128 * T) = pack8(f2[0], f2[1]);
;                     *(GAS v4u*)pb = pack8(b1[0], b1[1]); *(GAS v4u*)(pb + (size_t)128 * T) = pack8(b2[0], b2[1]);
	s_nop 0
	v_addc_co_u32_e32 v139, vcc, 0, v133, vcc
	v_mul_f32_e32 v179, v184, v151
	global_store_dwordx4 v[138:139], v[174:177], off sc1
	v_fract_f32_e32 v179, v179
	v_add_co_u32_e32 v140, vcc, s74, v132
	v_cvt_pk_bf16_f32 v174, v185, v187
	v_cvt_f32_i32_e32 v187, v116
	v_cos_f32_e32 v180, v179
	v_sin_f32_e32 v181, v179
	v_cvt_pk_bf16_f32 v175, v190, v194
	v_addc_co_u32_e32 v141, vcc, 0, v133, vcc
	v_cvt_pk_bf16_f32 v176, v198, v202
	v_cvt_pk_bf16_f32 v177, v206, v208
	global_store_dwordx4 v[140:141], v[174:177], off sc1
	s_nop 1
	v_pk_mul_f32 v[174:175], v[100:101], v[144:145] op_sel_hi:[0,1]
	v_pk_mul_f32 v[174:175], v[174:175], v[186:187]
	v_cvt_f32_i32_e32 v187, v118
	v_pk_mul_f32 v[176:177], v[180:181], v[174:175]
	v_cvt_f32_i32_e32 v186, v126
	v_sub_f32_e32 v116, v176, v177
	v_mov_b32_e32 v176, v181
	v_mov_b32_e32 v177, v180
	v_pk_mul_f32 v[174:175], v[176:177], v[174:175]
	v_mul_f32_e32 v116, 0x3d800000, v116
	v_add_f32_e32 v124, v174, v175
	v_sub_u32_e32 v174, 0x7f, v150
	v_add_u32_e32 v175, 0x81, v150
	v_cvt_f32_i32_e32 v174, v174
	v_mul_f32_e32 v179, 0x3d800000, v124
	v_cvt_f32_i32_e32 v124, v175
	v_add_u32_e32 v175, s62, v175
	v_mul_f32_e64 v174, v174, -v182
	v_mul_f32_e32 v174, 0x3fb8aa3b, v174
	v_mul_f32_e64 v124, v124, -v183
	v_mul_f32_e32 v124, 0x3fb8aa3b, v124
	v_exp_f32_e32 v174, v174
	v_exp_f32_e32 v124, v124
	v_cvt_f32_i32_e32 v175, v175
	v_cvt_f32_i32_e32 v177, v117
	v_mul_f32_e32 v190, v174, v116
	v_mul_f32_e32 v192, v124, v116
	v_mul_f32_e32 v116, v184, v175
	v_fract_f32_e32 v180, v116
	v_cvt_f32_i32_e32 v176, v125
	v_cos_f32_e32 v116, v180
	v_sin_f32_e32 v117, v180
	v_pk_mul_f32 v[180:181], v[100:101], v[144:145] op_sel:[1,0]
	v_mul_f32_e32 v191, v174, v179
	v_pk_mul_f32 v[176:177], v[180:181], v[176:177]
	v_mul_f32_e32 v193, v124, v179
	v_pk_mul_f32 v[180:181], v[116:117], v[176:177]
	v_pk_mul_f32 v[186:187], v[188:189], v[186:187]
	v_sub_f32_e32 v125, v180, v181
	v_mov_b32_e32 v180, v117
	v_mov_b32_e32 v181, v116
	v_pk_mul_f32 v[116:117], v[180:181], v[176:177]
	v_add_u32_e32 v176, 0x82, v150
	v_add_f32_e32 v116, v116, v117
	v_sub_u32_e32 v117, 0x7e, v150
	v_cvt_f32_i32_e32 v117, v117
	v_cvt_f32_i32_e32 v177, v176
	v_add_u32_e32 v176, s62, v176
	v_cvt_f32_i32_e32 v176, v176
	v_mul_f32_e64 v117, v117, -v182
	v_mul_f32_e32 v117, 0x3fb8aa3b, v117
	v_mul_f32_e32 v179, 0x3d800000, v125
	v_exp_f32_e32 v125, v117
	v_mul_f32_e64 v117, v177, -v183
	v_mul_f32_e32 v177, v184, v176
	v_fract_f32_e32 v177, v177
	v_mul_f32_e32 v117, 0x3fb8aa3b, v117
	v_cos_f32_e32 v180, v177
	v_sin_f32_e32 v181, v177
	v_exp_f32_e32 v117, v117
	v_mul_f32_e32 v116, 0x3d800000, v116
	v_mul_f32_e32 v195, v125, v116
	v_pk_mul_f32 v[188:189], v[180:181], v[186:187]
	v_mul_f32_e32 v197, v117, v116
	v_sub_f32_e32 v116, v188, v189
	v_mov_b32_e32 v188, v181
	v_mov_b32_e32 v189, v180
	v_pk_mul_f32 v[180:181], v[188:189], v[186:187]
	v_sub_u32_e32 v126, 0x7d, v150
	v_add_f32_e32 v118, v180, v181
	v_add_u32_e32 v177, 0x83, v150
	v_mul_f32_e32 v194, v125, v179
	v_mul_f32_e32 v196, v117, v179
	v_cvt_f32_i32_e32 v126, v126
	v_mul_f32_e32 v179, 0x3d800000, v118
	v_cvt_f32_i32_e32 v118, v177
	v_add_u32_e32 v177, s62, v177
	v_mul_f32_e64 v126, v126, -v182
	v_mul_f32_e32 v126, 0x3fb8aa3b, v126
	v_mul_f32_e64 v118, v118, -v183
	v_mul_f32_e32 v118, 0x3fb8aa3b, v118
	v_exp_f32_e32 v126, v126
	v_exp_f32_e32 v118, v118
	v_cvt_f32_i32_e32 v177, v177
	v_mul_f32_e32 v116, 0x3d800000, v116
	v_mul_f32_e32 v198, v126, v116
	v_mul_f32_e32 v200, v118, v116
	v_mul_f32_e32 v116, v184, v177
	v_fract_f32_e32 v116, v116
	v_cvt_f32_i32_e32 v187, v119
	v_cvt_f32_i32_e32 v186, v127
	v_cos_f32_e32 v180, v116
	v_sin_f32_e32 v181, v116
	v_mov_b32_e32 v116, v103
	v_pk_mul_f32 v[188:189], v[116:117], v[144:145] op_sel_hi:[0,1]
	v_pk_mul_f32 v[186:187], v[188:189], v[186:187]
	v_mul_f32_e32 v199, v126, v179
	v_pk_mul_f32 v[188:189], v[180:181], v[186:187]
	v_mul_f32_e32 v201, v118, v179
	v_sub_f32_e32 v103, v188, v189
	v_mul_f32_e32 v127, 0x3d800000, v103
	v_sub_u32_e32 v103, 0x7c, v150
	v_cvt_f32_i32_e32 v103, v103
	v_mov_b32_e32 v188, v181
	v_mov_b32_e32 v189, v180
	v_pk_mul_f32 v[180:181], v[188:189], v[186:187]
	v_mul_f32_e64 v103, v103, -v182
	v_mul_f32_e32 v103, 0x3fb8aa3b, v103
	v_exp_f32_e32 v119, v103
	v_mul_f32_e64 v103, v178, -v183
	v_mul_f32_e32 v103, 0x3fb8aa3b, v103
	v_exp_f32_e32 v103, v103
	v_mul_f32_e32 v202, v119, v127
	v_add_f32_e32 v179, v180, v181
	v_cvt_f32_i32_e32 v181, v104
	v_mul_f32_e32 v204, v103, v127
	v_mul_f32_e32 v127, v184, v137
	v_fract_f32_e32 v127, v127
	v_cvt_f32_i32_e32 v180, v108
	v_mul_f32_e32 v185, 0x3d800000, v179
	v_cos_f32_e32 v178, v127
	v_sin_f32_e32 v179, v127
	v_pk_mul_f32 v[186:187], v[92:93], v[144:145] op_sel_hi:[0,1]
	v_pk_mul_f32 v[180:181], v[186:187], v[180:181]
	v_sub_u32_e32 v127, 0x7b, v150
	v_pk_mul_f32 v[186:187], v[178:179], v[180:181]
	v_cvt_f32_i32_e32 v127, v127
	v_sub_f32_e32 v104, v186, v187
	v_mov_b32_e32 v186, v179
	v_mov_b32_e32 v187, v178
	v_pk_mul_f32 v[178:179], v[186:187], v[180:181]
	v_mul_f32_e64 v127, v127, -v182
	v_add_f32_e32 v108, v178, v179
	v_add_u32_e32 v178, 0x85, v150
	v_mul_f32_e32 v179, 0x3d800000, v108
	v_cvt_f32_i32_e32 v108, v178
	v_mul_f32_e32 v127, 0x3fb8aa3b, v127
	v_add_u32_e32 v178, s62, v178
	v_exp_f32_e32 v127, v127
	v_mul_f32_e64 v108, v108, -v183
	v_mul_f32_e32 v108, 0x3fb8aa3b, v108
	v_exp_f32_e32 v108, v108
	v_cvt_f32_i32_e32 v178, v178
	v_mul_f32_e32 v104, 0x3d800000, v104
	v_mul_f32_e32 v206, v127, v104
	v_mul_f32_e32 v208, v108, v104
	v_mul_f32_e32 v104, v184, v178
	v_mul_f32_e32 v203, v119, v185
	v_mul_f32_e32 v205, v103, v185
	v_fract_f32_e32 v185, v104
	v_cvt_f32_i32_e32 v181, v105
; #define GAS __attribute__((address_space(1)))
; __device__ __forceinline__ v4u pack8(const f32x4 a, const f32x4 b) { v4u w; w.x = cvt_pk_bf16(a[0], a[1]); w.y = cvt_pk_bf16(a[2], a[3]); w.z = cvt_pk_bf16(b[0], b[1]); w.w = cvt_pk_bf16(b[2], b[3]); return w; }
; __device__ __forceinline__ float fexp(float x) { return __builtin_amdgcn_exp2f(x * 1.4426950408889634f); }
; __device__ __forceinline__ void cs_rev(float rev, float& c, float& s) { const float f = __builtin_amdgcn_fractf(rev); c = __builtin_amdgcn_cosf(f); s = __builtin_amdgcn_sinf(f); }
;     __device__ __forceinline__ void operator()(AccI& acc, const Unit& u, LAS unsigned char*, int wr, int wc, int fr, int fq) const {
;     ...
;                         for (int j = 0; j < 4; ++j) { const int il = 128 * bj + c0 + 4 * n + j; const float pos = (float)(n_ch * 256 + il); float c, s; cs_rev(pos * inv, c, s);
;                             const float x1 = (float)acc[0][bj][m][n][j] * (sw1 * sxc[bj][n][j]), x2 = (float)acc[1][bj][m][n][j] * (sw2 * sxc[bj][n][j]); const float o1 = (x1 * c - x2 * s) * 0.0625f, o2 = (x2 * c + x1 * s) * 0.0625f;
;                             const float wf = fexp(lgf * (float)(255 - il)), wb = fexp(lgb * (float)(il + 1));
;                             f1[n][j] = o1 * wf; f2[n][j] = o2 * wf; b1[n][j] = o1 * wb; b2[n][j] = o2 * wb; }
;                     const size_t tcol = (size_t)n_ch * 256 + 128 * bj + c0;
;                     bf16* pf = kTw + ((size_t)(h * HD + d)) * T + tcol; bf16* pb = pf + (size_t)RW * T;
;                     *(GAS v4u*)pf = pack8(f1[0], f1[1]); *(GAS v4u*)(pf + (size_t)128 * T) = pack8(f2[0], f2[1]);
;                     *(GAS v4u*)pb = pack8(b1[0], b1[1]); *(GAS v4u*)(pb + (size_t)128 * T) = pack8(b2[0], b2[1]);
	v_cvt_f32_i32_e32 v180, v109
	v_cos_f32_e32 v104, v185
	v_sin_f32_e32 v105, v185
	v_pk_mul_f32 v[186:187], v[92:93], v[144:145] op_sel:[1,0]
	v_mul_f32_e32 v207, v127, v179
	v_pk_mul_f32 v[180:181], v[186:187], v[180:181]
	v_mul_f32_e32 v209, v108, v179
	v_pk_mul_f32 v[186:187], v[104:105], v[180:181]
	v_add_u32_e32 v179, 0x86, v150
	v_sub_f32_e32 v109, v186, v187
	v_mov_b32_e32 v186, v105
	v_mov_b32_e32 v187, v104
	v_pk_mul_f32 v[104:105], v[186:187], v[180:181]
	v_cvt_f32_i32_e32 v180, v179
	v_add_f32_e32 v104, v104, v105
	v_sub_u32_e32 v105, 0x7a, v150
	v_cvt_f32_i32_e32 v105, v105
	v_add_u32_e32 v179, s62, v179
	v_cvt_f32_i32_e32 v179, v179
	v_mul_f32_e32 v185, 0x3d800000, v109
	v_mul_f32_e64 v105, v105, -v182
	v_mul_f32_e32 v105, 0x3fb8aa3b, v105
	v_exp_f32_e32 v109, v105
	v_mul_f32_e64 v105, v180, -v183
	v_mul_f32_e32 v180, v184, v179
	v_fract_f32_e32 v181, v180
	v_cvt_f32_i32_e32 v187, v106
	v_cvt_f32_i32_e32 v186, v110
	v_mul_f32_e32 v105, 0x3fb8aa3b, v105
	v_cos_f32_e32 v180, v181
	v_sin_f32_e32 v181, v181
	v_exp_f32_e32 v105, v105
	v_pk_mul_f32 v[188:189], v[94:95], v[144:145] op_sel_hi:[0,1]
	v_pk_mul_f32 v[186:187], v[188:189], v[186:187]
	v_mul_f32_e32 v104, 0x3d800000, v104
	v_pk_mul_f32 v[188:189], v[180:181], v[186:187]
	v_mul_f32_e32 v211, v109, v104
	v_mul_f32_e32 v213, v105, v104
	v_sub_f32_e32 v104, v188, v189
	v_mov_b32_e32 v188, v181
	v_mov_b32_e32 v189, v180
	v_sub_u32_e32 v110, 0x79, v150
	v_pk_mul_f32 v[180:181], v[188:189], v[186:187]
	v_cvt_f32_i32_e32 v110, v110
	v_add_f32_e32 v106, v180, v181
	v_add_u32_e32 v181, 0x87, v150
	v_mul_f32_e32 v210, v109, v185
	v_mul_f32_e32 v212, v105, v185
	v_cvt_f32_i32_e32 v185, v181
	v_mul_f32_e64 v110, v110, -v182
	v_mul_f32_e32 v110, 0x3fb8aa3b, v110
	v_exp_f32_e32 v180, v110
	v_mul_f32_e64 v110, v185, -v183
	v_mul_f32_e32 v110, 0x3fb8aa3b, v110
	v_add_u32_e32 v181, s62, v181
	v_exp_f32_e32 v110, v110
	v_cvt_f32_i32_e32 v181, v181
	v_mul_f32_e32 v104, 0x3d800000, v104
	v_mul_f32_e32 v186, v180, v104
	v_mul_f32_e32 v188, v110, v104
	v_mul_f32_e32 v104, v184, v181
	v_mul_f32_e32 v106, 0x3d800000, v106
	v_fract_f32_e32 v104, v104
	v_cvt_f32_i32_e32 v185, v107
	v_cvt_f32_i32_e32 v184, v111
	v_mul_f32_e32 v187, v180, v106
	v_mul_f32_e32 v189, v110, v106
	v_cos_f32_e32 v106, v104
	v_sin_f32_e32 v107, v104
	v_mov_b32_e32 v104, v95
	v_pk_mul_f32 v[144:145], v[104:105], v[144:145] op_sel_hi:[0,1]
	v_pk_mul_f32 v[144:145], v[144:145], v[184:185]
	s_nop 0
	v_pk_mul_f32 v[184:185], v[106:107], v[144:145]
	s_nop 0
	v_sub_f32_e32 v95, v184, v185
	v_mov_b32_e32 v184, v107
	v_mov_b32_e32 v185, v106
	v_mul_f32_e32 v214, 0x3d800000, v95
	v_pk_mul_f32 v[106:107], v[184:185], v[144:145]
	v_sub_u32_e32 v95, 0x78, v150
	v_cvt_f32_i32_e32 v95, v95
	v_add_f32_e32 v106, v106, v107
	v_add_u32_e32 v107, 0x88, v150
	v_cvt_f32_i32_e32 v107, v107
	v_mul_f32_e64 v95, v95, -v182
	v_mul_f32_e32 v95, 0x3fb8aa3b, v95
	v_exp_f32_e32 v95, v95
	v_mul_f32_e64 v107, v107, -v183
	v_mul_f32_e32 v107, 0x3fb8aa3b, v107
	v_exp_f32_e32 v111, v107
	v_mul_f32_e32 v106, 0x3d800000, v106
	v_mul_f32_e32 v107, v95, v214
	v_cvt_pk_bf16_f32 v182, v190, v194
	v_cvt_pk_bf16_f32 v183, v198, v202
	v_cvt_pk_bf16_f32 v184, v206, v210
	v_cvt_pk_bf16_f32 v185, v186, v107
	v_mul_f32_e32 v144, v95, v106
	v_mul_f32_e32 v145, v111, v214
	v_mul_f32_e32 v106, v111, v106
	global_store_dwordx4 v[132:133], v[182:185], off offset:256 sc1
	s_nop 1
	v_cvt_pk_bf16_f32 v182, v191, v195
	v_cvt_pk_bf16_f32 v183, v199, v203
	v_cvt_pk_bf16_f32 v184, v207, v211
	v_cvt_pk_bf16_f32 v185, v187, v144
	global_store_dwordx4 v[134:135], v[182:185], off offset:256 sc1
	v_cvt_pk_bf16_f32 v132, v192, v196
	v_cvt_pk_bf16_f32 v133, v200, v204
	v_cvt_pk_bf16_f32 v134, v208, v212
	v_cvt_pk_bf16_f32 v135, v188, v145
	global_store_dwordx4 v[138:139], v[132:135], off offset:256 sc1
	v_add_u32_e32 v138, 16, v146
	v_cvt_f32_i32_e32 v139, v84
	v_cvt_pk_bf16_f32 v132, v193, v197
	v_cvt_pk_bf16_f32 v133, v201, v205
	v_cvt_pk_bf16_f32 v134, v209, v213
	v_cvt_pk_bf16_f32 v135, v189, v106
	v_add_u32_e32 v106, s56, v138
	v_ashrrev_i32_e32 v107, 31, v106
	global_store_dwordx4 v[140:141], v[132:135], off offset:256 sc1
	s_nop 1
	v_lshl_add_u64 v[132:133], v[106:107], 2, s[36:37]
	v_add_u32_e32 v106, 0x80, v106
	v_ashrrev_i32_e32 v107, 31, v106
	v_lshl_add_u64 v[134:135], v[106:107], 2, s[36:37]
	global_load_dword v106, v[132:133], off
	global_load_dword v107, v[134:135], off
	v_cvt_f32_i32_e32 v132, v138
	v_mul_f32_e32 v132, 0xbdd49a78, v132
	v_exp_f32_e32 v132, v132
	s_waitcnt vmcnt(0)
; #define GAS __attribute__((address_space(1)))
; __device__ __forceinline__ v4u pack8(const f32x4 a, const f32x4 b) { v4u w; w.x = cvt_pk_bf16(a[0], a[1]); w.y = cvt_pk_bf16(a[2], a[3]); w.z = cvt_pk_bf16(b[0], b[1]); w.w = cvt_pk_bf16(b[2], b[3]); return w; }
; __device__ __forceinline__ float fexp(float x) { return __builtin_amdgcn_exp2f(x * 1.4426950408889634f); }
; __device__ __forceinline__ void cs_rev(float rev, float& c, float& s) { const float f = __builtin_amdgcn_fractf(rev); c = __builtin_amdgcn_cosf(f); s = __builtin_amdgcn_sinf(f); }
;     __device__ __forceinline__ void operator()(AccI& acc, const Unit& u, LAS unsigned char*, int wr, int wc, int fr, int fq) const {
;     ...
;                         for (int j = 0; j < 4; ++j) { const int il = 128 * bj + c0 + 4 * n + j; const float pos = (float)(n_ch * 256 + il); float c, s; cs_rev(pos * inv, c, s);
;                             const float x1 = (float)acc[0][bj][m][n][j] * (sw1 * sxc[bj][n][j]), x2 = (float)acc[1][bj][m][n][j] * (sw2 * sxc[bj][n][j]); const float o1 = (x1 * c - x2 * s) * 0.0625f, o2 = (x2 * c + x1 * s) * 0.0625f;
;                             const float wf = fexp(lgf * (float)(255 - il)), wb = fexp(lgb * (float)(il + 1));
;                             f1[n][j] = o1 * wf; f2[n][j] = o2 * wf; b1[n][j] = o1 * wb; b2[n][j] = o2 * wb; }
;                     const size_t tcol = (size_t)n_ch * 256 + 128 * bj + c0;
;                     bf16* pf = kTw + ((size_t)(h * HD + d)) * T + tcol; bf16* pb = pf + (size_t)RW * T;
;                     *(GAS v4u*)pf = pack8(f1[0], f1[1]); *(GAS v4u*)(pf + (size_t)128 * T) = pack8(f2[0], f2[1]);
;                     *(GAS v4u*)pb = pack8(b1[0], b1[1]); *(GAS v4u*)(pb + (size_t)128 * T) = pack8(b2[0], b2[1]);
	v_pk_mul_f32 v[140:141], v[120:121], v[106:107] op_sel_hi:[0,1]
	v_mul_f32_e32 v144, 0.15915494, v132
	v_mul_f32_e32 v134, v144, v152
	v_add_u32_e32 v132, s45, v138
	v_fract_f32_e32 v135, v134
	v_cvt_f32_i32_e32 v138, v96
	v_cos_f32_e32 v134, v135
	v_sin_f32_e32 v135, v135
	v_ashrrev_i32_e32 v133, 31, v132
	v_pk_mul_f32 v[138:139], v[140:141], v[138:139]
	v_lshlrev_b64 v[132:133], 15, v[132:133]
	v_pk_mul_f32 v[140:141], v[134:135], v[138:139]
	s_nop 0
	v_sub_f32_e32 v84, v140, v141
	v_mul_f32_e32 v84, 0x3d800000, v84
	v_mov_b32_e32 v140, v135
	v_mov_b32_e32 v141, v134
	v_pk_mul_f32 v[134:135], v[140:141], v[138:139]
	v_mul_f32_e32 v138, v162, v84
	v_mul_f32_e32 v140, v160, v84
	v_mul_f32_e32 v84, v144, v148
	v_add_f32_e32 v96, v134, v135
	v_fract_f32_e32 v141, v84
	v_cvt_f32_i32_e32 v135, v85
	v_cvt_f32_i32_e32 v134, v97
	v_cos_f32_e32 v84, v141
	v_sin_f32_e32 v85, v141
	v_mul_f32_e32 v96, 0x3d800000, v96
	v_mul_f32_e32 v139, v162, v96
	v_mul_f32_e32 v141, v160, v96
	v_pk_mul_f32 v[96:97], v[120:121], v[106:107] op_sel:[1,0]
	s_nop 0
	v_pk_mul_f32 v[96:97], v[96:97], v[134:135]
	s_nop 0
	v_pk_mul_f32 v[134:135], v[84:85], v[96:97]
	s_nop 0
	v_sub_f32_e32 v134, v134, v135
	v_mul_f32_e32 v145, 0x3d800000, v134
	v_mov_b32_e32 v134, v85
	v_mov_b32_e32 v135, v84
	v_pk_mul_f32 v[84:85], v[134:135], v[96:97]
	v_cvt_f32_i32_e32 v97, v86
	v_add_f32_e32 v84, v84, v85
	v_mul_f32_e32 v134, 0x3d800000, v84
	v_mul_f32_e32 v84, v144, v147
	v_fract_f32_e32 v85, v84
	v_cvt_f32_i32_e32 v96, v98
	v_cos_f32_e32 v84, v85
	v_sin_f32_e32 v85, v85
	v_mul_f32_e32 v182, v159, v134
	v_mul_f32_e32 v98, v153, v134
	v_pk_mul_f32 v[134:135], v[122:123], v[106:107] op_sel_hi:[0,1]
	v_pk_mul_f32 v[96:97], v[134:135], v[96:97]
	v_mul_f32_e32 v150, v159, v145
	v_pk_mul_f32 v[134:135], v[84:85], v[96:97]
	v_mul_f32_e32 v145, v153, v145
	v_sub_f32_e32 v86, v134, v135
	v_mov_b32_e32 v134, v85
	v_mov_b32_e32 v135, v84
	v_pk_mul_f32 v[84:85], v[134:135], v[96:97]
	v_mul_f32_e32 v86, 0x3d800000, v86
	v_add_f32_e32 v84, v84, v85
	v_mul_f32_e32 v96, 0x3d800000, v84
	v_mul_f32_e32 v84, v144, v163
	v_mul_f32_e32 v134, v161, v86
	v_mul_f32_e32 v183, v142, v86
	v_fract_f32_e32 v85, v84
	v_cvt_f32_i32_e32 v86, v99
	v_cos_f32_e32 v84, v85
	v_sin_f32_e32 v85, v85
	v_mul_f32_e32 v135, v161, v96
	v_mul_f32_e32 v99, v142, v96
	v_pk_mul_f32 v[96:97], v[136:137], v[106:107] op_sel_hi:[0,1]
	v_pk_mul_f32 v[86:87], v[96:97], v[86:87]
	s_nop 0
	v_pk_mul_f32 v[96:97], v[84:85], v[86:87]
	s_nop 0
	v_sub_f32_e32 v96, v96, v97
	v_mul_f32_e32 v184, 0x3d800000, v96
	v_mov_b32_e32 v96, v85
	v_mov_b32_e32 v97, v84
	v_pk_mul_f32 v[84:85], v[96:97], v[86:87]
	v_cvt_f32_i32_e32 v87, v80
	v_add_f32_e32 v84, v84, v85
	v_mul_f32_e32 v96, 0x3d800000, v84
	v_mul_f32_e32 v84, v144, v164
	v_fract_f32_e32 v85, v84
	v_cvt_f32_i32_e32 v86, v88
	v_cos_f32_e32 v84, v85
	v_sin_f32_e32 v85, v85
	v_mul_f32_e32 v186, v143, v96
	v_mul_f32_e32 v187, v123, v96
	v_pk_mul_f32 v[96:97], v[112:113], v[106:107] op_sel_hi:[0,1]
	v_pk_mul_f32 v[86:87], v[96:97], v[86:87]
	v_mul_f32_e32 v185, v143, v184
	v_pk_mul_f32 v[96:97], v[84:85], v[86:87]
	v_mul_f32_e32 v184, v123, v184
	v_sub_f32_e32 v80, v96, v97
	v_mov_b32_e32 v96, v85
	v_mov_b32_e32 v97, v84
	v_mul_f32_e32 v80, 0x3d800000, v80
	v_pk_mul_f32 v[84:85], v[96:97], v[86:87]
	v_mul_f32_e32 v88, v166, v80
	v_add_f32_e32 v84, v84, v85
	v_mul_f32_e32 v97, v165, v80
	v_mul_f32_e32 v80, v144, v167
	v_mul_f32_e32 v86, 0x3d800000, v84
	v_fract_f32_e32 v87, v80
	v_cvt_f32_i32_e32 v85, v81
	v_cvt_f32_i32_e32 v84, v89
	v_cos_f32_e32 v80, v87
	v_sin_f32_e32 v81, v87
	v_mul_f32_e32 v96, v166, v86
	v_mul_f32_e32 v188, v165, v86
	v_pk_mul_f32 v[86:87], v[112:113], v[106:107] op_sel:[1,0]
	s_nop 0
	v_pk_mul_f32 v[84:85], v[86:87], v[84:85]
	s_nop 0
	v_pk_mul_f32 v[86:87], v[80:81], v[84:85]
	s_nop 0
	v_sub_f32_e32 v86, v86, v87
	v_mul_f32_e32 v89, 0x3d800000, v86
	v_mov_b32_e32 v86, v81
	v_mov_b32_e32 v87, v80
	v_pk_mul_f32 v[80:81], v[86:87], v[84:85]
	v_cvt_f32_i32_e32 v85, v82
	v_add_f32_e32 v80, v80, v81
	v_mul_f32_e32 v86, 0x3d800000, v80
	v_mul_f32_e32 v80, v144, v169
	v_fract_f32_e32 v81, v80
	v_cvt_f32_i32_e32 v84, v90
	v_cos_f32_e32 v80, v81
	v_sin_f32_e32 v81, v81
	v_mul_f32_e32 v190, v168, v86
	v_mul_f32_e32 v90, v129, v86
	v_pk_mul_f32 v[86:87], v[114:115], v[106:107] op_sel_hi:[0,1]
	v_pk_mul_f32 v[84:85], v[86:87], v[84:85]
	v_mul_f32_e32 v189, v168, v89
	v_pk_mul_f32 v[86:87], v[80:81], v[84:85]
	v_mul_f32_e32 v89, v129, v89
	v_sub_f32_e32 v82, v86, v87
	v_mov_b32_e32 v86, v81
	v_mov_b32_e32 v87, v80
	v_pk_mul_f32 v[80:81], v[86:87], v[84:85]
	v_mul_f32_e32 v82, 0x3d800000, v82
	v_add_f32_e32 v80, v80, v81
	v_mul_f32_e32 v84, 0x3d800000, v80
	v_mul_f32_e32 v80, v144, v172
	v_mul_f32_e32 v86, v171, v82
	v_mul_f32_e32 v191, v170, v82
	v_fract_f32_e32 v81, v80
	v_cvt_f32_i32_e32 v82, v91
	v_cos_f32_e32 v80, v81
	v_sin_f32_e32 v81, v81
	v_mul_f32_e32 v87, v171, v84
	v_mul_f32_e32 v91, v170, v84
	v_pk_mul_f32 v[84:85], v[128:129], v[106:107] op_sel_hi:[0,1]
	v_pk_mul_f32 v[82:83], v[84:85], v[82:83]
	s_nop 0
	v_pk_mul_f32 v[84:85], v[80:81], v[82:83]
	s_nop 0
	v_sub_f32_e32 v84, v84, v85
	v_mul_f32_e32 v192, 0x3d800000, v84
	v_mov_b32_e32 v84, v81
	v_mov_b32_e32 v85, v80
	v_pk_mul_f32 v[80:81], v[84:85], v[82:83]
	v_mul_f32_e32 v85, v115, v192
	v_add_f32_e32 v80, v80, v81
	v_mul_f32_e32 v80, 0x3d800000, v80
	v_mul_f32_e32 v193, v115, v80
	v_mul_f32_e32 v194, v173, v80
	v_lshl_add_u64 v[80:81], s[6:7], 0, v[132:133]
	v_lshl_add_u64 v[80:81], v[80:81], 0, s[58:59]
	v_lshl_add_u64 v[80:81], v[80:81], 0, v[130:131]
	v_cvt_pk_bf16_f32 v82, v138, v150
	v_cvt_pk_bf16_f32 v83, v134, v185
; #define GAS __attribute__((address_space(1)))
; __device__ __forceinline__ v4u pack8(const f32x4 a, const f32x4 b) { v4u w; w.x = cvt_pk_bf16(a[0], a[1]); w.y = cvt_pk_bf16(a[2], a[3]); w.z = cvt_pk_bf16(b[0], b[1]); w.w = cvt_pk_bf16(b[2], b[3]); return w; }
; __device__ __forceinline__ float fexp(float x) { return __builtin_amdgcn_exp2f(x * 1.4426950408889634f); }
; __device__ __forceinline__ void cs_rev(float rev, float& c, float& s) { const float f = __builtin_amdgcn_fractf(rev); c = __builtin_amdgcn_cosf(f); s = __builtin_amdgcn_sinf(f); }
;     __device__ __forceinline__ void operator()(AccI& acc, const Unit& u, LAS unsigned char*, int wr, int wc, int fr, int fq) const {
;     ...
;                         for (int j = 0; j < 4; ++j) { const int il = 128 * bj + c0 + 4 * n + j; const float pos = (float)(n_ch * 256 + il); float c, s; cs_rev(pos * inv, c, s);
;                             const float x1 = (float)acc[0][bj][m][n][j] * (sw1 * sxc[bj][n][j]), x2 = (float)acc[1][bj][m][n][j] * (sw2 * sxc[bj][n][j]); const float o1 = (x1 * c - x2 * s) * 0.0625f, o2 = (x2 * c + x1 * s) * 0.0625f;
;                             const float wf = fexp(lgf * (float)(255 - il)), wb = fexp(lgb * (float)(il + 1));
;                             f1[n][j] = o1 * wf; f2[n][j] = o2 * wf; b1[n][j] = o1 * wb; b2[n][j] = o2 * wb; }
;                     const size_t tcol = (size_t)n_ch * 256 + 128 * bj + c0;
;                     bf16* pf = kTw + ((size_t)(h * HD + d)) * T + tcol; bf16* pb = pf + (size_t)RW * T;
;                     *(GAS v4u*)pf = pack8(f1[0], f1[1]); *(GAS v4u*)(pf + (size_t)128 * T) = pack8(f2[0], f2[1]);
;                     *(GAS v4u*)pb = pack8(b1[0], b1[1]); *(GAS v4u*)(pb + (size_t)128 * T) = pack8(b2[0], b2[1]);
	v_cvt_pk_bf16_f32 v84, v88, v189
	v_cvt_pk_bf16_f32 v85, v86, v85
	global_store_dwordx4 v[80:81], v[82:85], off sc1
	v_mul_f32_e32 v192, v173, v192
	s_nop 0
	v_add_co_u32_e32 v82, vcc, s72, v80
	v_cvt_pk_bf16_f32 v84, v139, v182
	v_cvt_pk_bf16_f32 v85, v135, v186
	v_cvt_pk_bf16_f32 v86, v96, v190
	v_cvt_pk_bf16_f32 v87, v87, v193
	s_nop 1
	v_addc_co_u32_e32 v83, vcc, 0, v81, vcc
	v_add_co_u32_e32 v88, vcc, s73, v80
	global_store_dwordx4 v[82:83], v[84:87], off sc1
	v_mul_f32_e32 v96, v144, v151
	s_nop 0
	v_cvt_pk_bf16_f32 v84, v140, v145
	v_cvt_pk_bf16_f32 v85, v183, v184
	v_cvt_pk_bf16_f32 v86, v97, v89
	v_addc_co_u32_e32 v89, vcc, 0, v81, vcc
	v_cvt_pk_bf16_f32 v87, v191, v192
	global_store_dwordx4 v[88:89], v[84:87], off sc1
	v_fract_f32_e32 v97, v96
	v_cos_f32_e32 v96, v97
	v_cvt_pk_bf16_f32 v84, v141, v98
	v_cvt_pk_bf16_f32 v85, v99, v187
	v_cvt_f32_i32_e32 v99, v68
	v_cvt_f32_i32_e32 v98, v76
	v_cvt_pk_bf16_f32 v86, v188, v90
	v_add_co_u32_e32 v90, vcc, s74, v80
	v_sin_f32_e32 v97, v97
	v_cvt_pk_bf16_f32 v87, v91, v194
	s_nop 0
	v_addc_co_u32_e32 v91, vcc, 0, v81, vcc
	global_store_dwordx4 v[90:91], v[84:87], off sc1
	s_nop 1
	v_pk_mul_f32 v[84:85], v[100:101], v[106:107] op_sel_hi:[0,1]
	v_pk_mul_f32 v[84:85], v[84:85], v[98:99]
	s_nop 0
	v_pk_mul_f32 v[86:87], v[96:97], v[84:85]
	s_nop 0
	v_sub_f32_e32 v68, v86, v87
	v_mul_f32_e32 v68, 0x3d800000, v68
	v_mov_b32_e32 v86, v97
	v_mov_b32_e32 v87, v96
	v_pk_mul_f32 v[84:85], v[86:87], v[84:85]
	v_mul_f32_e32 v86, v174, v68
	v_mul_f32_e32 v96, v124, v68
	v_mul_f32_e32 v68, v144, v175
	v_add_f32_e32 v76, v84, v85
	v_fract_f32_e32 v97, v68
	v_cvt_f32_i32_e32 v85, v69
	v_cvt_f32_i32_e32 v84, v77
	v_cos_f32_e32 v68, v97
	v_sin_f32_e32 v69, v97
	v_mul_f32_e32 v76, 0x3d800000, v76
	v_mul_f32_e32 v87, v174, v76
	v_mul_f32_e32 v97, v124, v76
	v_pk_mul_f32 v[76:77], v[100:101], v[106:107] op_sel:[1,0]
	s_nop 0
	v_pk_mul_f32 v[76:77], v[76:77], v[84:85]
	s_nop 0
	v_pk_mul_f32 v[84:85], v[68:69], v[76:77]
	s_nop 0
	v_sub_f32_e32 v84, v84, v85
	v_mul_f32_e32 v98, 0x3d800000, v84
	v_mov_b32_e32 v84, v69
	v_mov_b32_e32 v85, v68
	v_pk_mul_f32 v[68:69], v[84:85], v[76:77]
	v_cvt_f32_i32_e32 v77, v70
	v_add_f32_e32 v68, v68, v69
	v_mul_f32_e32 v84, 0x3d800000, v68
	v_mul_f32_e32 v68, v144, v176
	v_fract_f32_e32 v69, v68
	v_cvt_f32_i32_e32 v76, v78
	v_cos_f32_e32 v68, v69
	v_sin_f32_e32 v69, v69
	v_mul_f32_e32 v132, v125, v84
	v_mul_f32_e32 v78, v117, v84
	v_pk_mul_f32 v[84:85], v[102:103], v[106:107] op_sel_hi:[0,1]
	v_pk_mul_f32 v[76:77], v[84:85], v[76:77]
	v_mul_f32_e32 v99, v125, v98
	v_pk_mul_f32 v[84:85], v[68:69], v[76:77]
	v_mul_f32_e32 v98, v117, v98
	v_sub_f32_e32 v70, v84, v85
	v_mov_b32_e32 v84, v69
	v_mov_b32_e32 v85, v68
	v_pk_mul_f32 v[68:69], v[84:85], v[76:77]
	v_mul_f32_e32 v70, 0x3d800000, v70
	v_add_f32_e32 v68, v68, v69
	v_mul_f32_e32 v76, 0x3d800000, v68
	v_mul_f32_e32 v68, v144, v177
	v_mul_f32_e32 v84, v126, v70
	v_mul_f32_e32 v133, v118, v70
	v_fract_f32_e32 v69, v68
	v_cvt_f32_i32_e32 v70, v79
	v_cos_f32_e32 v68, v69
	v_sin_f32_e32 v69, v69
	v_mul_f32_e32 v85, v126, v76
	v_mul_f32_e32 v79, v118, v76
	v_pk_mul_f32 v[76:77], v[116:117], v[106:107] op_sel_hi:[0,1]
	v_pk_mul_f32 v[70:71], v[76:77], v[70:71]
	s_nop 0
	v_pk_mul_f32 v[76:77], v[68:69], v[70:71]
	s_nop 0
	v_sub_f32_e32 v76, v76, v77
	v_mul_f32_e32 v134, 0x3d800000, v76
	v_mov_b32_e32 v76, v69
	v_mov_b32_e32 v77, v68
	v_pk_mul_f32 v[68:69], v[76:77], v[70:71]
	v_cvt_f32_i32_e32 v71, v64
	v_add_f32_e32 v68, v68, v69
	v_mul_f32_e32 v76, 0x3d800000, v68
	v_mul_f32_e32 v68, v144, v137
	v_fract_f32_e32 v69, v68
	v_cvt_f32_i32_e32 v70, v72
	v_cos_f32_e32 v68, v69
	v_sin_f32_e32 v69, v69
	v_mul_f32_e32 v138, v119, v76
	v_mul_f32_e32 v72, v103, v76
	v_pk_mul_f32 v[76:77], v[92:93], v[106:107] op_sel_hi:[0,1]
	v_pk_mul_f32 v[70:71], v[76:77], v[70:71]
	v_mul_f32_e32 v135, v119, v134
	v_pk_mul_f32 v[76:77], v[68:69], v[70:71]
	v_mul_f32_e32 v134, v103, v134
	v_sub_f32_e32 v64, v76, v77
	v_mov_b32_e32 v76, v69
	v_mov_b32_e32 v77, v68
	v_mul_f32_e32 v64, 0x3d800000, v64
	v_pk_mul_f32 v[68:69], v[76:77], v[70:71]
	v_mul_f32_e32 v76, v127, v64
	v_add_f32_e32 v68, v68, v69
	v_mul_f32_e32 v139, v108, v64
	v_mul_f32_e32 v64, v144, v178
	v_mul_f32_e32 v70, 0x3d800000, v68
	v_fract_f32_e32 v71, v64
	v_cvt_f32_i32_e32 v69, v65
	v_cvt_f32_i32_e32 v68, v73
	v_cos_f32_e32 v64, v71
	v_sin_f32_e32 v65, v71
	v_mul_f32_e32 v77, v127, v70
	v_mul_f32_e32 v73, v108, v70
	v_pk_mul_f32 v[70:71], v[92:93], v[106:107] op_sel:[1,0]
	s_nop 0
	v_pk_mul_f32 v[68:69], v[70:71], v[68:69]
	s_nop 0
	v_pk_mul_f32 v[70:71], v[64:65], v[68:69]
	s_nop 0
	v_sub_f32_e32 v70, v70, v71
	v_mul_f32_e32 v140, 0x3d800000, v70
	v_mov_b32_e32 v70, v65
	v_mov_b32_e32 v71, v64
	v_pk_mul_f32 v[64:65], v[70:71], v[68:69]
	v_cvt_f32_i32_e32 v69, v66
	v_add_f32_e32 v64, v64, v65
	v_mul_f32_e32 v70, 0x3d800000, v64
	v_mul_f32_e32 v64, v144, v179
	v_fract_f32_e32 v65, v64
	v_cvt_f32_i32_e32 v68, v74
	v_cos_f32_e32 v64, v65
	v_sin_f32_e32 v65, v65
	v_mul_f32_e32 v145, v109, v70
	v_mul_f32_e32 v74, v105, v70
	v_pk_mul_f32 v[70:71], v[94:95], v[106:107] op_sel_hi:[0,1]
	v_pk_mul_f32 v[68:69], v[70:71], v[68:69]
	v_mul_f32_e32 v141, v109, v140
	v_pk_mul_f32 v[70:71], v[64:65], v[68:69]
	v_mul_f32_e32 v140, v105, v140
	v_sub_f32_e32 v66, v70, v71
	v_mov_b32_e32 v70, v65
	v_mov_b32_e32 v71, v64
	v_pk_mul_f32 v[64:65], v[70:71], v[68:69]
	v_mul_f32_e32 v66, 0x3d800000, v66
	v_add_f32_e32 v64, v64, v65
	v_mul_f32_e32 v68, 0x3d800000, v64
	v_mul_f32_e32 v64, v144, v181
	v_mul_f32_e32 v70, v180, v66
	v_mul_f32_e32 v150, v110, v66
	v_fract_f32_e32 v65, v64
	v_cvt_f32_i32_e32 v66, v75
; #define GAS __attribute__((address_space(1)))
; __device__ __forceinline__ v4u pack8(const f32x4 a, const f32x4 b) { v4u w; w.x = cvt_pk_bf16(a[0], a[1]); w.y = cvt_pk_bf16(a[2], a[3]); w.z = cvt_pk_bf16(b[0], b[1]); w.w = cvt_pk_bf16(b[2], b[3]); return w; }
; __device__ __forceinline__ float fexp(float x) { return __builtin_amdgcn_exp2f(x * 1.4426950408889634f); }
; __device__ __forceinline__ void cs_rev(float rev, float& c, float& s) { const float f = __builtin_amdgcn_fractf(rev); c = __builtin_amdgcn_cosf(f); s = __builtin_amdgcn_sinf(f); }
;     __device__ __forceinline__ void operator()(AccI& acc, const Unit& u, LAS unsigned char*, int wr, int wc, int fr, int fq) const {
;     ...
;                         for (int j = 0; j < 4; ++j) { const int il = 128 * bj + c0 + 4 * n + j; const float pos = (float)(n_ch * 256 + il); float c, s; cs_rev(pos * inv, c, s);
;                             const float x1 = (float)acc[0][bj][m][n][j] * (sw1 * sxc[bj][n][j]), x2 = (float)acc[1][bj][m][n][j] * (sw2 * sxc[bj][n][j]); const float o1 = (x1 * c - x2 * s) * 0.0625f, o2 = (x2 * c + x1 * s) * 0.0625f;
;                             const float wf = fexp(lgf * (float)(255 - il)), wb = fexp(lgb * (float)(il + 1));
;                             f1[n][j] = o1 * wf; f2[n][j] = o2 * wf; b1[n][j] = o1 * wb; b2[n][j] = o2 * wb; }
;                     const size_t tcol = (size_t)n_ch * 256 + 128 * bj + c0;
;                     bf16* pf = kTw + ((size_t)(h * HD + d)) * T + tcol; bf16* pb = pf + (size_t)RW * T;
;                     *(GAS v4u*)pf = pack8(f1[0], f1[1]); *(GAS v4u*)(pf + (size_t)128 * T) = pack8(f2[0], f2[1]);
;                     *(GAS v4u*)pb = pack8(b1[0], b1[1]); *(GAS v4u*)(pb + (size_t)128 * T) = pack8(b2[0], b2[1]);
	v_cos_f32_e32 v64, v65
	v_sin_f32_e32 v65, v65
	v_mul_f32_e32 v71, v180, v68
	v_mul_f32_e32 v75, v110, v68
	v_pk_mul_f32 v[68:69], v[104:105], v[106:107] op_sel_hi:[0,1]
	v_pk_mul_f32 v[66:67], v[68:69], v[66:67]
	s_nop 0
	v_pk_mul_f32 v[68:69], v[64:65], v[66:67]
	s_nop 0
	v_sub_f32_e32 v68, v68, v69
	v_mul_f32_e32 v106, 0x3d800000, v68
	v_mov_b32_e32 v68, v65
	v_mov_b32_e32 v69, v64
	v_pk_mul_f32 v[64:65], v[68:69], v[66:67]
	v_mul_f32_e32 v67, v95, v106
	v_add_f32_e32 v64, v64, v65
	v_mul_f32_e32 v64, 0x3d800000, v64
	v_mul_f32_e32 v68, v95, v64
	v_mul_f32_e32 v69, v111, v106
	v_mul_f32_e32 v106, v111, v64
	v_cvt_pk_bf16_f32 v64, v86, v99
	v_cvt_pk_bf16_f32 v65, v84, v135
	v_cvt_pk_bf16_f32 v66, v76, v141
	v_cvt_pk_bf16_f32 v67, v70, v67
	global_store_dwordx4 v[80:81], v[64:67], off offset:256 sc1
	v_add_u32_e32 v70, 32, v146
	s_nop 0
	v_cvt_pk_bf16_f32 v64, v87, v132
	v_cvt_pk_bf16_f32 v65, v85, v138
	v_cvt_pk_bf16_f32 v66, v77, v145
	v_cvt_pk_bf16_f32 v67, v71, v68
	global_store_dwordx4 v[82:83], v[64:67], off offset:256 sc1
	v_cvt_f32_i32_e32 v71, v52
	s_nop 0
	v_cvt_pk_bf16_f32 v64, v96, v98
	v_cvt_pk_bf16_f32 v65, v133, v134
	v_cvt_pk_bf16_f32 v66, v139, v140
	v_cvt_pk_bf16_f32 v67, v150, v69
	global_store_dwordx4 v[88:89], v[64:67], off offset:256 sc1
	s_nop 1
	v_cvt_pk_bf16_f32 v64, v97, v78
	v_cvt_pk_bf16_f32 v65, v79, v72
	v_cvt_pk_bf16_f32 v66, v73, v74
	v_cvt_pk_bf16_f32 v67, v75, v106
	global_store_dwordx4 v[90:91], v[64:67], off offset:256 sc1
	s_nop 1
	v_add_u32_e32 v64, s56, v70
	v_ashrrev_i32_e32 v65, 31, v64
	v_lshl_add_u64 v[66:67], v[64:65], 2, s[36:37]
	v_add_u32_e32 v64, 0x80, v64
	v_ashrrev_i32_e32 v65, 31, v64
	v_lshl_add_u64 v[68:69], v[64:65], 2, s[36:37]
	global_load_dword v64, v[66:67], off
	global_load_dword v65, v[68:69], off
	v_cvt_f32_i32_e32 v66, v70
	v_mul_f32_e32 v66, 0xbdd49a78, v66
	v_exp_f32_e32 v66, v66
	s_waitcnt vmcnt(0)
	v_pk_mul_f32 v[72:73], v[120:121], v[64:65] op_sel_hi:[0,1]
	v_mul_f32_e32 v74, 0.15915494, v66
	v_mul_f32_e32 v68, v74, v152
	v_add_u32_e32 v66, s45, v70
	v_fract_f32_e32 v69, v68
	v_cvt_f32_i32_e32 v70, v60
	v_cos_f32_e32 v68, v69
	v_sin_f32_e32 v69, v69
	v_ashrrev_i32_e32 v67, 31, v66
	v_pk_mul_f32 v[70:71], v[72:73], v[70:71]
	v_lshlrev_b64 v[66:67], 15, v[66:67]
	v_pk_mul_f32 v[72:73], v[68:69], v[70:71]
	s_nop 0
	v_sub_f32_e32 v52, v72, v73
	v_mul_f32_e32 v52, 0x3d800000, v52
	v_mov_b32_e32 v72, v69
	v_mov_b32_e32 v73, v68
	v_pk_mul_f32 v[68:69], v[72:73], v[70:71]
	v_mul_f32_e32 v70, v162, v52
	v_mul_f32_e32 v72, v160, v52
	v_mul_f32_e32 v52, v74, v148
	v_add_f32_e32 v60, v68, v69
	v_fract_f32_e32 v73, v52
	v_cvt_f32_i32_e32 v69, v53
	v_cvt_f32_i32_e32 v68, v61
	v_cos_f32_e32 v52, v73
	v_sin_f32_e32 v53, v73
	v_mul_f32_e32 v60, 0x3d800000, v60
	v_mul_f32_e32 v71, v162, v60
	v_mul_f32_e32 v73, v160, v60
	v_pk_mul_f32 v[60:61], v[120:121], v[64:65] op_sel:[1,0]
	s_nop 0
	v_pk_mul_f32 v[60:61], v[60:61], v[68:69]
	s_nop 0
	v_pk_mul_f32 v[68:69], v[52:53], v[60:61]
	s_nop 0
	v_sub_f32_e32 v68, v68, v69
	v_mul_f32_e32 v75, 0x3d800000, v68
	v_mov_b32_e32 v68, v53
	v_mov_b32_e32 v69, v52
	v_pk_mul_f32 v[52:53], v[68:69], v[60:61]
	v_cvt_f32_i32_e32 v61, v54
	v_add_f32_e32 v52, v52, v53
	v_mul_f32_e32 v68, 0x3d800000, v52
	v_mul_f32_e32 v52, v74, v147
	v_fract_f32_e32 v53, v52
	v_cvt_f32_i32_e32 v60, v62
	v_cos_f32_e32 v52, v53
	v_sin_f32_e32 v53, v53
	v_mul_f32_e32 v77, v159, v68
	v_mul_f32_e32 v62, v153, v68
	v_pk_mul_f32 v[68:69], v[122:123], v[64:65] op_sel_hi:[0,1]
	v_pk_mul_f32 v[60:61], v[68:69], v[60:61]
	v_mul_f32_e32 v76, v159, v75
	v_pk_mul_f32 v[68:69], v[52:53], v[60:61]
	v_mul_f32_e32 v75, v153, v75
	v_sub_f32_e32 v54, v68, v69
	v_mov_b32_e32 v68, v53
	v_mov_b32_e32 v69, v52
	v_pk_mul_f32 v[52:53], v[68:69], v[60:61]
	v_mul_f32_e32 v54, 0x3d800000, v54
	v_add_f32_e32 v52, v52, v53
	v_mul_f32_e32 v60, 0x3d800000, v52
	v_mul_f32_e32 v52, v74, v163
	v_mul_f32_e32 v68, v161, v54
	v_mul_f32_e32 v78, v142, v54
	v_fract_f32_e32 v53, v52
	v_cvt_f32_i32_e32 v54, v63
	v_cos_f32_e32 v52, v53
	v_sin_f32_e32 v53, v53
	v_mul_f32_e32 v69, v161, v60
	v_mul_f32_e32 v63, v142, v60
	v_pk_mul_f32 v[60:61], v[136:137], v[64:65] op_sel_hi:[0,1]
	v_pk_mul_f32 v[54:55], v[60:61], v[54:55]
	s_nop 0
	v_pk_mul_f32 v[60:61], v[52:53], v[54:55]
	s_nop 0
	v_sub_f32_e32 v60, v60, v61
	v_mul_f32_e32 v79, 0x3d800000, v60
	v_mov_b32_e32 v60, v53
	v_mov_b32_e32 v61, v52
	v_pk_mul_f32 v[52:53], v[60:61], v[54:55]
	v_cvt_f32_i32_e32 v55, v48
	v_add_f32_e32 v52, v52, v53
	v_mul_f32_e32 v60, 0x3d800000, v52
	v_mul_f32_e32 v52, v74, v164
	v_fract_f32_e32 v53, v52
	v_cvt_f32_i32_e32 v54, v56
	v_cos_f32_e32 v52, v53
	v_sin_f32_e32 v53, v53
	v_mul_f32_e32 v81, v143, v60
	v_mul_f32_e32 v82, v123, v60
	v_pk_mul_f32 v[60:61], v[112:113], v[64:65] op_sel_hi:[0,1]
	v_pk_mul_f32 v[54:55], v[60:61], v[54:55]
	v_mul_f32_e32 v80, v143, v79
	v_pk_mul_f32 v[60:61], v[52:53], v[54:55]
	v_mul_f32_e32 v79, v123, v79
	v_sub_f32_e32 v48, v60, v61
	v_mov_b32_e32 v60, v53
	v_mov_b32_e32 v61, v52
	v_mul_f32_e32 v48, 0x3d800000, v48
	v_pk_mul_f32 v[52:53], v[60:61], v[54:55]
	v_mul_f32_e32 v56, v166, v48
	v_add_f32_e32 v52, v52, v53
	v_mul_f32_e32 v61, v165, v48
	v_mul_f32_e32 v48, v74, v167
	v_mul_f32_e32 v54, 0x3d800000, v52
	v_fract_f32_e32 v55, v48
	v_cvt_f32_i32_e32 v53, v49
	v_cvt_f32_i32_e32 v52, v57
	v_cos_f32_e32 v48, v55
	v_sin_f32_e32 v49, v55
	v_mul_f32_e32 v60, v166, v54
	v_mul_f32_e32 v83, v165, v54
	v_pk_mul_f32 v[54:55], v[112:113], v[64:65] op_sel:[1,0]
	s_nop 0
	v_pk_mul_f32 v[52:53], v[54:55], v[52:53]
	s_nop 0
	v_pk_mul_f32 v[54:55], v[48:49], v[52:53]
	s_nop 0
	v_sub_f32_e32 v54, v54, v55
; #define GAS __attribute__((address_space(1)))
; __device__ __forceinline__ v4u pack8(const f32x4 a, const f32x4 b) { v4u w; w.x = cvt_pk_bf16(a[0], a[1]); w.y = cvt_pk_bf16(a[2], a[3]); w.z = cvt_pk_bf16(b[0], b[1]); w.w = cvt_pk_bf16(b[2], b[3]); return w; }
; __device__ __forceinline__ float fexp(float x) { return __builtin_amdgcn_exp2f(x * 1.4426950408889634f); }
; __device__ __forceinline__ void cs_rev(float rev, float& c, float& s) { const float f = __builtin_amdgcn_fractf(rev); c = __builtin_amdgcn_cosf(f); s = __builtin_amdgcn_sinf(f); }
;     __device__ __forceinline__ void operator()(AccI& acc, const Unit& u, LAS unsigned char*, int wr, int wc, int fr, int fq) const {
;     ...
;                         for (int j = 0; j < 4; ++j) { const int il = 128 * bj + c0 + 4 * n + j; const float pos = (float)(n_ch * 256 + il); float c, s; cs_rev(pos * inv, c, s);
;                             const float x1 = (float)acc[0][bj][m][n][j] * (sw1 * sxc[bj][n][j]), x2 = (float)acc[1][bj][m][n][j] * (sw2 * sxc[bj][n][j]); const float o1 = (x1 * c - x2 * s) * 0.0625f, o2 = (x2 * c + x1 * s) * 0.0625f;
;                             const float wf = fexp(lgf * (float)(255 - il)), wb = fexp(lgb * (float)(il + 1));
;                             f1[n][j] = o1 * wf; f2[n][j] = o2 * wf; b1[n][j] = o1 * wb; b2[n][j] = o2 * wb; }
;                     const size_t tcol = (size_t)n_ch * 256 + 128 * bj + c0;
;                     bf16* pf = kTw + ((size_t)(h * HD + d)) * T + tcol; bf16* pb = pf + (size_t)RW * T;
;                     *(GAS v4u*)pf = pack8(f1[0], f1[1]); *(GAS v4u*)(pf + (size_t)128 * T) = pack8(f2[0], f2[1]);
;                     *(GAS v4u*)pb = pack8(b1[0], b1[1]); *(GAS v4u*)(pb + (size_t)128 * T) = pack8(b2[0], b2[1]);
	v_mul_f32_e32 v57, 0x3d800000, v54
	v_mov_b32_e32 v54, v49
	v_mov_b32_e32 v55, v48
	v_pk_mul_f32 v[48:49], v[54:55], v[52:53]
	v_cvt_f32_i32_e32 v53, v50
	v_add_f32_e32 v48, v48, v49
	v_mul_f32_e32 v54, 0x3d800000, v48
	v_mul_f32_e32 v48, v74, v169
	v_fract_f32_e32 v49, v48
	v_cvt_f32_i32_e32 v52, v58
	v_cos_f32_e32 v48, v49
	v_sin_f32_e32 v49, v49
	v_mul_f32_e32 v85, v168, v54
	v_mul_f32_e32 v58, v129, v54
	v_pk_mul_f32 v[54:55], v[114:115], v[64:65] op_sel_hi:[0,1]
	v_pk_mul_f32 v[52:53], v[54:55], v[52:53]
	v_mul_f32_e32 v84, v168, v57
	v_pk_mul_f32 v[54:55], v[48:49], v[52:53]
	v_mul_f32_e32 v57, v129, v57
	v_sub_f32_e32 v50, v54, v55
	v_mov_b32_e32 v54, v49
	v_mov_b32_e32 v55, v48
	v_pk_mul_f32 v[48:49], v[54:55], v[52:53]
	v_mul_f32_e32 v50, 0x3d800000, v50
	v_add_f32_e32 v48, v48, v49
	v_mul_f32_e32 v52, 0x3d800000, v48
	v_mul_f32_e32 v48, v74, v172
	v_mul_f32_e32 v54, v171, v50
	v_mul_f32_e32 v86, v170, v50
	v_fract_f32_e32 v49, v48
	v_cvt_f32_i32_e32 v50, v59
	v_cos_f32_e32 v48, v49
	v_sin_f32_e32 v49, v49
	v_mul_f32_e32 v55, v171, v52
	v_mul_f32_e32 v59, v170, v52
	v_pk_mul_f32 v[52:53], v[128:129], v[64:65] op_sel_hi:[0,1]
	v_pk_mul_f32 v[50:51], v[52:53], v[50:51]
	s_nop 0
	v_pk_mul_f32 v[52:53], v[48:49], v[50:51]
	s_nop 0
	v_sub_f32_e32 v52, v52, v53
	v_mul_f32_e32 v87, 0x3d800000, v52
	v_mov_b32_e32 v52, v49
	v_mov_b32_e32 v53, v48
	v_pk_mul_f32 v[48:49], v[52:53], v[50:51]
	v_mul_f32_e32 v53, v115, v87
	v_add_f32_e32 v48, v48, v49
	v_mul_f32_e32 v48, 0x3d800000, v48
	v_mul_f32_e32 v88, v115, v48
	v_mul_f32_e32 v89, v173, v48
	v_lshl_add_u64 v[48:49], s[6:7], 0, v[66:67]
	v_lshl_add_u64 v[48:49], v[48:49], 0, s[58:59]
	v_lshl_add_u64 v[48:49], v[48:49], 0, v[130:131]
	v_cvt_pk_bf16_f32 v50, v70, v76
	v_cvt_pk_bf16_f32 v51, v68, v80
	v_cvt_pk_bf16_f32 v52, v56, v84
	v_cvt_pk_bf16_f32 v53, v54, v53
	global_store_dwordx4 v[48:49], v[50:53], off sc1
	v_mul_f32_e32 v87, v173, v87
	s_nop 0
	v_add_co_u32_e32 v50, vcc, s72, v48
	v_cvt_pk_bf16_f32 v52, v71, v77
	v_cvt_pk_bf16_f32 v53, v69, v81
	v_cvt_pk_bf16_f32 v54, v60, v85
	v_cvt_pk_bf16_f32 v55, v55, v88
	s_nop 1
	v_addc_co_u32_e32 v51, vcc, 0, v49, vcc
	v_add_co_u32_e32 v56, vcc, s73, v48
	global_store_dwordx4 v[50:51], v[52:55], off sc1
	v_mul_f32_e32 v60, v74, v151
	s_nop 0
	v_cvt_pk_bf16_f32 v52, v72, v75
	v_cvt_pk_bf16_f32 v53, v78, v79
	v_cvt_pk_bf16_f32 v54, v61, v57
	v_addc_co_u32_e32 v57, vcc, 0, v49, vcc
	v_cvt_pk_bf16_f32 v55, v86, v87
	global_store_dwordx4 v[56:57], v[52:55], off sc1
	v_fract_f32_e32 v61, v60
	v_cos_f32_e32 v60, v61
	v_cvt_pk_bf16_f32 v52, v73, v62
	v_cvt_pk_bf16_f32 v53, v63, v82
	v_cvt_f32_i32_e32 v63, v36
	v_cvt_f32_i32_e32 v62, v44
	v_cvt_pk_bf16_f32 v54, v83, v58
	v_add_co_u32_e32 v58, vcc, s74, v48
	v_sin_f32_e32 v61, v61
	v_cvt_pk_bf16_f32 v55, v59, v89
	s_nop 0
	v_addc_co_u32_e32 v59, vcc, 0, v49, vcc
	global_store_dwordx4 v[58:59], v[52:55], off sc1
	s_nop 1
	v_pk_mul_f32 v[52:53], v[100:101], v[64:65] op_sel_hi:[0,1]
	v_pk_mul_f32 v[52:53], v[52:53], v[62:63]
	s_nop 0
	v_pk_mul_f32 v[54:55], v[60:61], v[52:53]
	s_nop 0
	v_sub_f32_e32 v36, v54, v55
	v_mul_f32_e32 v36, 0x3d800000, v36
	v_mov_b32_e32 v54, v61
	v_mov_b32_e32 v55, v60
	v_pk_mul_f32 v[52:53], v[54:55], v[52:53]
	v_mul_f32_e32 v54, v174, v36
	v_mul_f32_e32 v60, v124, v36
	v_mul_f32_e32 v36, v74, v175
	v_add_f32_e32 v44, v52, v53
	v_fract_f32_e32 v61, v36
	v_cvt_f32_i32_e32 v53, v37
	v_cvt_f32_i32_e32 v52, v45
	v_cos_f32_e32 v36, v61
	v_sin_f32_e32 v37, v61
	v_mul_f32_e32 v44, 0x3d800000, v44
	v_mul_f32_e32 v55, v174, v44
	v_mul_f32_e32 v61, v124, v44
	v_pk_mul_f32 v[44:45], v[100:101], v[64:65] op_sel:[1,0]
	s_nop 0
	v_pk_mul_f32 v[44:45], v[44:45], v[52:53]
	s_nop 0
	v_pk_mul_f32 v[52:53], v[36:37], v[44:45]
	s_nop 0
	v_sub_f32_e32 v52, v52, v53
	v_mul_f32_e32 v62, 0x3d800000, v52
	v_mov_b32_e32 v52, v37
	v_mov_b32_e32 v53, v36
	v_pk_mul_f32 v[36:37], v[52:53], v[44:45]
	v_cvt_f32_i32_e32 v45, v38
	v_add_f32_e32 v36, v36, v37
	v_mul_f32_e32 v52, 0x3d800000, v36
	v_mul_f32_e32 v36, v74, v176
	v_fract_f32_e32 v37, v36
	v_cvt_f32_i32_e32 v44, v46
	v_cos_f32_e32 v36, v37
	v_sin_f32_e32 v37, v37
	v_mul_f32_e32 v66, v125, v52
	v_mul_f32_e32 v46, v117, v52
	v_pk_mul_f32 v[52:53], v[102:103], v[64:65] op_sel_hi:[0,1]
	v_pk_mul_f32 v[44:45], v[52:53], v[44:45]
	v_mul_f32_e32 v63, v125, v62
	v_pk_mul_f32 v[52:53], v[36:37], v[44:45]
	v_mul_f32_e32 v62, v117, v62
	v_sub_f32_e32 v38, v52, v53
	v_mov_b32_e32 v52, v37
	v_mov_b32_e32 v53, v36
	v_pk_mul_f32 v[36:37], v[52:53], v[44:45]
	v_mul_f32_e32 v38, 0x3d800000, v38
	v_add_f32_e32 v36, v36, v37
	v_mul_f32_e32 v44, 0x3d800000, v36
	v_mul_f32_e32 v36, v74, v177
	v_mul_f32_e32 v52, v126, v38
	v_mul_f32_e32 v67, v118, v38
	v_fract_f32_e32 v37, v36
	v_cvt_f32_i32_e32 v38, v47
	v_cos_f32_e32 v36, v37
	v_sin_f32_e32 v37, v37
	v_mul_f32_e32 v53, v126, v44
	v_mul_f32_e32 v47, v118, v44
	v_pk_mul_f32 v[44:45], v[116:117], v[64:65] op_sel_hi:[0,1]
	v_pk_mul_f32 v[38:39], v[44:45], v[38:39]
	s_nop 0
	v_pk_mul_f32 v[44:45], v[36:37], v[38:39]
	s_nop 0
	v_sub_f32_e32 v44, v44, v45
	v_mul_f32_e32 v68, 0x3d800000, v44
	v_mov_b32_e32 v44, v37
	v_mov_b32_e32 v45, v36
	v_pk_mul_f32 v[36:37], v[44:45], v[38:39]
	v_cvt_f32_i32_e32 v39, v32
	v_add_f32_e32 v36, v36, v37
	v_mul_f32_e32 v44, 0x3d800000, v36
	v_mul_f32_e32 v36, v74, v137
	v_fract_f32_e32 v37, v36
	v_cvt_f32_i32_e32 v38, v40
	v_cos_f32_e32 v36, v37
	v_sin_f32_e32 v37, v37
	v_mul_f32_e32 v70, v119, v44
	v_mul_f32_e32 v40, v103, v44
	v_pk_mul_f32 v[44:45], v[92:93], v[64:65] op_sel_hi:[0,1]
	v_pk_mul_f32 v[38:39], v[44:45], v[38:39]
	v_mul_f32_e32 v69, v119, v68
	v_pk_mul_f32 v[44:45], v[36:37], v[38:39]
; #define GAS __attribute__((address_space(1)))
; __device__ __forceinline__ v4u pack8(const f32x4 a, const f32x4 b) { v4u w; w.x = cvt_pk_bf16(a[0], a[1]); w.y = cvt_pk_bf16(a[2], a[3]); w.z = cvt_pk_bf16(b[0], b[1]); w.w = cvt_pk_bf16(b[2], b[3]); return w; }
; __device__ __forceinline__ float fexp(float x) { return __builtin_amdgcn_exp2f(x * 1.4426950408889634f); }
; __device__ __forceinline__ void cs_rev(float rev, float& c, float& s) { const float f = __builtin_amdgcn_fractf(rev); c = __builtin_amdgcn_cosf(f); s = __builtin_amdgcn_sinf(f); }
;     __device__ __forceinline__ void operator()(AccI& acc, const Unit& u, LAS unsigned char*, int wr, int wc, int fr, int fq) const {
;     ...
;                         for (int j = 0; j < 4; ++j) { const int il = 128 * bj + c0 + 4 * n + j; const float pos = (float)(n_ch * 256 + il); float c, s; cs_rev(pos * inv, c, s);
;                             const float x1 = (float)acc[0][bj][m][n][j] * (sw1 * sxc[bj][n][j]), x2 = (float)acc[1][bj][m][n][j] * (sw2 * sxc[bj][n][j]); const float o1 = (x1 * c - x2 * s) * 0.0625f, o2 = (x2 * c + x1 * s) * 0.0625f;
;                             const float wf = fexp(lgf * (float)(255 - il)), wb = fexp(lgb * (float)(il + 1));
;                             f1[n][j] = o1 * wf; f2[n][j] = o2 * wf; b1[n][j] = o1 * wb; b2[n][j] = o2 * wb; }
;                     const size_t tcol = (size_t)n_ch * 256 + 128 * bj + c0;
;                     bf16* pf = kTw + ((size_t)(h * HD + d)) * T + tcol; bf16* pb = pf + (size_t)RW * T;
;                     *(GAS v4u*)pf = pack8(f1[0], f1[1]); *(GAS v4u*)(pf + (size_t)128 * T) = pack8(f2[0], f2[1]);
;                     *(GAS v4u*)pb = pack8(b1[0], b1[1]); *(GAS v4u*)(pb + (size_t)128 * T) = pack8(b2[0], b2[1]);
	v_mul_f32_e32 v68, v103, v68
	v_sub_f32_e32 v32, v44, v45
	v_mov_b32_e32 v44, v37
	v_mov_b32_e32 v45, v36
	v_mul_f32_e32 v32, 0x3d800000, v32
	v_pk_mul_f32 v[36:37], v[44:45], v[38:39]
	v_mul_f32_e32 v44, v127, v32
	v_add_f32_e32 v36, v36, v37
	v_mul_f32_e32 v71, v108, v32
	v_mul_f32_e32 v32, v74, v178
	v_mul_f32_e32 v38, 0x3d800000, v36
	v_fract_f32_e32 v39, v32
	v_cvt_f32_i32_e32 v37, v33
	v_cvt_f32_i32_e32 v36, v41
	v_cos_f32_e32 v32, v39
	v_sin_f32_e32 v33, v39
	v_mul_f32_e32 v45, v127, v38
	v_mul_f32_e32 v41, v108, v38
	v_pk_mul_f32 v[38:39], v[92:93], v[64:65] op_sel:[1,0]
	s_nop 0
	v_pk_mul_f32 v[36:37], v[38:39], v[36:37]
	s_nop 0
	v_pk_mul_f32 v[38:39], v[32:33], v[36:37]
	s_nop 0
	v_sub_f32_e32 v38, v38, v39
	v_mul_f32_e32 v72, 0x3d800000, v38
	v_mov_b32_e32 v38, v33
	v_mov_b32_e32 v39, v32
	v_pk_mul_f32 v[32:33], v[38:39], v[36:37]
	v_cvt_f32_i32_e32 v37, v34
	v_add_f32_e32 v32, v32, v33
	v_mul_f32_e32 v38, 0x3d800000, v32
	v_mul_f32_e32 v32, v74, v179
	v_fract_f32_e32 v33, v32
	v_cvt_f32_i32_e32 v36, v42
	v_cos_f32_e32 v32, v33
	v_sin_f32_e32 v33, v33
	v_mul_f32_e32 v75, v109, v38
	v_mul_f32_e32 v42, v105, v38
	v_pk_mul_f32 v[38:39], v[94:95], v[64:65] op_sel_hi:[0,1]
	v_pk_mul_f32 v[36:37], v[38:39], v[36:37]
	v_mul_f32_e32 v73, v109, v72
	v_pk_mul_f32 v[38:39], v[32:33], v[36:37]
	v_mul_f32_e32 v72, v105, v72
	v_sub_f32_e32 v34, v38, v39
	v_mov_b32_e32 v38, v33
	v_mov_b32_e32 v39, v32
	v_pk_mul_f32 v[32:33], v[38:39], v[36:37]
	v_mul_f32_e32 v34, 0x3d800000, v34
	v_add_f32_e32 v32, v32, v33
	v_mul_f32_e32 v36, 0x3d800000, v32
	v_mul_f32_e32 v32, v74, v181
	v_mul_f32_e32 v38, v180, v34
	v_mul_f32_e32 v76, v110, v34
	v_fract_f32_e32 v33, v32
	v_cvt_f32_i32_e32 v34, v43
	v_cos_f32_e32 v32, v33
	v_sin_f32_e32 v33, v33
	v_mul_f32_e32 v39, v180, v36
	v_mul_f32_e32 v43, v110, v36
	v_pk_mul_f32 v[36:37], v[104:105], v[64:65] op_sel_hi:[0,1]
	v_pk_mul_f32 v[34:35], v[36:37], v[34:35]
	s_nop 0
	v_pk_mul_f32 v[36:37], v[32:33], v[34:35]
	s_nop 0
	v_sub_f32_e32 v36, v36, v37
	v_mul_f32_e32 v64, 0x3d800000, v36
	v_mov_b32_e32 v36, v33
	v_mov_b32_e32 v37, v32
	v_pk_mul_f32 v[32:33], v[36:37], v[34:35]
	v_mul_f32_e32 v35, v95, v64
	v_add_f32_e32 v32, v32, v33
	v_mul_f32_e32 v32, 0x3d800000, v32
	v_mul_f32_e32 v36, v95, v32
	v_mul_f32_e32 v37, v111, v64
	v_mul_f32_e32 v64, v111, v32
	v_cvt_pk_bf16_f32 v32, v54, v63
	v_cvt_pk_bf16_f32 v33, v52, v69
	v_cvt_pk_bf16_f32 v34, v44, v73
	v_cvt_pk_bf16_f32 v35, v38, v35
	global_store_dwordx4 v[48:49], v[32:35], off offset:256 sc1
	v_add_u32_e32 v38, 48, v146
	s_nop 0
	v_cvt_pk_bf16_f32 v32, v55, v66
	v_cvt_pk_bf16_f32 v33, v53, v70
	v_cvt_pk_bf16_f32 v34, v45, v75
	v_cvt_pk_bf16_f32 v35, v39, v36
	global_store_dwordx4 v[50:51], v[32:35], off offset:256 sc1
	v_cvt_f32_i32_e32 v39, v20
	s_nop 0
	v_cvt_pk_bf16_f32 v32, v60, v62
	v_cvt_pk_bf16_f32 v33, v67, v68
	v_cvt_pk_bf16_f32 v34, v71, v72
	v_cvt_pk_bf16_f32 v35, v76, v37
	global_store_dwordx4 v[56:57], v[32:35], off offset:256 sc1
	s_nop 1
	v_cvt_pk_bf16_f32 v32, v61, v46
	v_cvt_pk_bf16_f32 v33, v47, v40
	v_cvt_pk_bf16_f32 v34, v41, v42
	v_cvt_pk_bf16_f32 v35, v43, v64
	global_store_dwordx4 v[58:59], v[32:35], off offset:256 sc1
	s_nop 1
	v_add_u32_e32 v32, s56, v38
	v_ashrrev_i32_e32 v33, 31, v32
	v_lshl_add_u64 v[34:35], v[32:33], 2, s[36:37]
	v_add_u32_e32 v32, 0x80, v32
	v_ashrrev_i32_e32 v33, 31, v32
	v_lshl_add_u64 v[36:37], v[32:33], 2, s[36:37]
	global_load_dword v32, v[34:35], off
	global_load_dword v33, v[36:37], off
	v_cvt_f32_i32_e32 v34, v38
	v_mul_f32_e32 v34, 0xbdd49a78, v34
	v_exp_f32_e32 v34, v34
	s_waitcnt vmcnt(0)
	v_pk_mul_f32 v[40:41], v[120:121], v[32:33] op_sel_hi:[0,1]
	v_mul_f32_e32 v42, 0.15915494, v34
	v_mul_f32_e32 v36, v42, v152
	v_add_u32_e32 v34, s45, v38
	v_fract_f32_e32 v37, v36
	v_cvt_f32_i32_e32 v38, v28
	v_cos_f32_e32 v36, v37
	v_sin_f32_e32 v37, v37
	v_ashrrev_i32_e32 v35, 31, v34
	v_pk_mul_f32 v[38:39], v[40:41], v[38:39]
	v_lshlrev_b64 v[34:35], 15, v[34:35]
	v_pk_mul_f32 v[40:41], v[36:37], v[38:39]
	s_nop 0
	v_sub_f32_e32 v20, v40, v41
	v_mul_f32_e32 v20, 0x3d800000, v20
	v_mov_b32_e32 v40, v37
	v_mov_b32_e32 v41, v36
	v_pk_mul_f32 v[36:37], v[40:41], v[38:39]
	v_mul_f32_e32 v38, v162, v20
	v_mul_f32_e32 v40, v160, v20
	v_mul_f32_e32 v20, v42, v148
	v_add_f32_e32 v28, v36, v37
	v_fract_f32_e32 v41, v20
	v_cvt_f32_i32_e32 v37, v21
	v_cvt_f32_i32_e32 v36, v29
	v_cos_f32_e32 v20, v41
	v_sin_f32_e32 v21, v41
	v_mul_f32_e32 v28, 0x3d800000, v28
	v_mul_f32_e32 v39, v162, v28
	v_mul_f32_e32 v41, v160, v28
	v_pk_mul_f32 v[28:29], v[120:121], v[32:33] op_sel:[1,0]
	s_nop 0
	v_pk_mul_f32 v[28:29], v[28:29], v[36:37]
	s_nop 0
	v_pk_mul_f32 v[36:37], v[20:21], v[28:29]
	s_nop 0
	v_sub_f32_e32 v36, v36, v37
	v_mul_f32_e32 v43, 0x3d800000, v36
	v_mov_b32_e32 v36, v21
	v_mov_b32_e32 v37, v20
	v_pk_mul_f32 v[20:21], v[36:37], v[28:29]
	v_cvt_f32_i32_e32 v29, v22
	v_add_f32_e32 v20, v20, v21
	v_mul_f32_e32 v36, 0x3d800000, v20
	v_mul_f32_e32 v20, v42, v147
	v_fract_f32_e32 v21, v20
	v_cvt_f32_i32_e32 v28, v30
	v_cos_f32_e32 v20, v21
	v_sin_f32_e32 v21, v21
	v_mul_f32_e32 v45, v159, v36
	v_mul_f32_e32 v30, v153, v36
	v_pk_mul_f32 v[36:37], v[122:123], v[32:33] op_sel_hi:[0,1]
	v_pk_mul_f32 v[28:29], v[36:37], v[28:29]
	v_mul_f32_e32 v44, v159, v43
	v_pk_mul_f32 v[36:37], v[20:21], v[28:29]
	v_mul_f32_e32 v43, v153, v43
	v_sub_f32_e32 v22, v36, v37
	v_mov_b32_e32 v36, v21
	v_mov_b32_e32 v37, v20
	v_pk_mul_f32 v[20:21], v[36:37], v[28:29]
	v_mul_f32_e32 v22, 0x3d800000, v22
	v_add_f32_e32 v20, v20, v21
	v_mul_f32_e32 v28, 0x3d800000, v20
	v_mul_f32_e32 v20, v42, v163
	v_mul_f32_e32 v36, v161, v22
	v_mul_f32_e32 v46, v142, v22
; #define GAS __attribute__((address_space(1)))
; __device__ __forceinline__ v4u pack8(const f32x4 a, const f32x4 b) { v4u w; w.x = cvt_pk_bf16(a[0], a[1]); w.y = cvt_pk_bf16(a[2], a[3]); w.z = cvt_pk_bf16(b[0], b[1]); w.w = cvt_pk_bf16(b[2], b[3]); return w; }
; __device__ __forceinline__ float fexp(float x) { return __builtin_amdgcn_exp2f(x * 1.4426950408889634f); }
; __device__ __forceinline__ void cs_rev(float rev, float& c, float& s) { const float f = __builtin_amdgcn_fractf(rev); c = __builtin_amdgcn_cosf(f); s = __builtin_amdgcn_sinf(f); }
;     __device__ __forceinline__ void operator()(AccI& acc, const Unit& u, LAS unsigned char*, int wr, int wc, int fr, int fq) const {
;     ...
;                         for (int j = 0; j < 4; ++j) { const int il = 128 * bj + c0 + 4 * n + j; const float pos = (float)(n_ch * 256 + il); float c, s; cs_rev(pos * inv, c, s);
;                             const float x1 = (float)acc[0][bj][m][n][j] * (sw1 * sxc[bj][n][j]), x2 = (float)acc[1][bj][m][n][j] * (sw2 * sxc[bj][n][j]); const float o1 = (x1 * c - x2 * s) * 0.0625f, o2 = (x2 * c + x1 * s) * 0.0625f;
;                             const float wf = fexp(lgf * (float)(255 - il)), wb = fexp(lgb * (float)(il + 1));
;                             f1[n][j] = o1 * wf; f2[n][j] = o2 * wf; b1[n][j] = o1 * wb; b2[n][j] = o2 * wb; }
;                     const size_t tcol = (size_t)n_ch * 256 + 128 * bj + c0;
;                     bf16* pf = kTw + ((size_t)(h * HD + d)) * T + tcol; bf16* pb = pf + (size_t)RW * T;
;                     *(GAS v4u*)pf = pack8(f1[0], f1[1]); *(GAS v4u*)(pf + (size_t)128 * T) = pack8(f2[0], f2[1]);
;                     *(GAS v4u*)pb = pack8(b1[0], b1[1]); *(GAS v4u*)(pb + (size_t)128 * T) = pack8(b2[0], b2[1]);
	v_fract_f32_e32 v21, v20
	v_cvt_f32_i32_e32 v22, v31
	v_cos_f32_e32 v20, v21
	v_sin_f32_e32 v21, v21
	v_mul_f32_e32 v37, v161, v28
	v_mul_f32_e32 v31, v142, v28
	v_pk_mul_f32 v[28:29], v[136:137], v[32:33] op_sel_hi:[0,1]
	v_pk_mul_f32 v[22:23], v[28:29], v[22:23]
	s_nop 0
	v_pk_mul_f32 v[28:29], v[20:21], v[22:23]
	s_nop 0
	v_sub_f32_e32 v28, v28, v29
	v_mul_f32_e32 v47, 0x3d800000, v28
	v_mov_b32_e32 v28, v21
	v_mov_b32_e32 v29, v20
	v_pk_mul_f32 v[20:21], v[28:29], v[22:23]
	v_cvt_f32_i32_e32 v23, v16
	v_add_f32_e32 v20, v20, v21
	v_mul_f32_e32 v28, 0x3d800000, v20
	v_mul_f32_e32 v20, v42, v164
	v_fract_f32_e32 v21, v20
	v_cvt_f32_i32_e32 v22, v24
	v_cos_f32_e32 v20, v21
	v_sin_f32_e32 v21, v21
	v_mul_f32_e32 v49, v143, v28
	v_mul_f32_e32 v50, v123, v28
	v_pk_mul_f32 v[28:29], v[112:113], v[32:33] op_sel_hi:[0,1]
	v_pk_mul_f32 v[22:23], v[28:29], v[22:23]
	v_mul_f32_e32 v48, v143, v47
	v_pk_mul_f32 v[28:29], v[20:21], v[22:23]
	v_mul_f32_e32 v47, v123, v47
	v_sub_f32_e32 v16, v28, v29
	v_mov_b32_e32 v28, v21
	v_mov_b32_e32 v29, v20
	v_mul_f32_e32 v16, 0x3d800000, v16
	v_pk_mul_f32 v[20:21], v[28:29], v[22:23]
	v_mul_f32_e32 v24, v166, v16
	v_add_f32_e32 v20, v20, v21
	v_mul_f32_e32 v29, v165, v16
	v_mul_f32_e32 v16, v42, v167
	v_mul_f32_e32 v22, 0x3d800000, v20
	v_fract_f32_e32 v23, v16
	v_cvt_f32_i32_e32 v21, v17
	v_cvt_f32_i32_e32 v20, v25
	v_cos_f32_e32 v16, v23
	v_sin_f32_e32 v17, v23
	v_mul_f32_e32 v28, v166, v22
	v_mul_f32_e32 v51, v165, v22
	v_pk_mul_f32 v[22:23], v[112:113], v[32:33] op_sel:[1,0]
	s_nop 0
	v_pk_mul_f32 v[20:21], v[22:23], v[20:21]
	s_nop 0
	v_pk_mul_f32 v[22:23], v[16:17], v[20:21]
	s_nop 0
	v_sub_f32_e32 v22, v22, v23
	v_mul_f32_e32 v25, 0x3d800000, v22
	v_mov_b32_e32 v22, v17
	v_mov_b32_e32 v23, v16
	v_pk_mul_f32 v[16:17], v[22:23], v[20:21]
	v_cvt_f32_i32_e32 v21, v18
	v_add_f32_e32 v16, v16, v17
	v_mul_f32_e32 v22, 0x3d800000, v16
	v_mul_f32_e32 v16, v42, v169
	v_fract_f32_e32 v17, v16
	v_cvt_f32_i32_e32 v20, v26
	v_cos_f32_e32 v16, v17
	v_sin_f32_e32 v17, v17
	v_mul_f32_e32 v53, v168, v22
	v_mul_f32_e32 v26, v129, v22
	v_pk_mul_f32 v[22:23], v[114:115], v[32:33] op_sel_hi:[0,1]
	v_pk_mul_f32 v[20:21], v[22:23], v[20:21]
	v_mul_f32_e32 v52, v168, v25
	v_pk_mul_f32 v[22:23], v[16:17], v[20:21]
	v_mul_f32_e32 v25, v129, v25
	v_sub_f32_e32 v18, v22, v23
	v_mov_b32_e32 v22, v17
	v_mov_b32_e32 v23, v16
	v_pk_mul_f32 v[16:17], v[22:23], v[20:21]
	v_mul_f32_e32 v18, 0x3d800000, v18
	v_add_f32_e32 v16, v16, v17
	v_mul_f32_e32 v20, 0x3d800000, v16
	v_mul_f32_e32 v16, v42, v172
	v_mul_f32_e32 v22, v171, v18
	v_mul_f32_e32 v54, v170, v18
	v_fract_f32_e32 v17, v16
	v_cvt_f32_i32_e32 v18, v27
	v_cos_f32_e32 v16, v17
	v_sin_f32_e32 v17, v17
	v_mul_f32_e32 v23, v171, v20
	v_mul_f32_e32 v27, v170, v20
	v_pk_mul_f32 v[20:21], v[128:129], v[32:33] op_sel_hi:[0,1]
	v_pk_mul_f32 v[18:19], v[20:21], v[18:19]
	s_nop 0
	v_pk_mul_f32 v[20:21], v[16:17], v[18:19]
	s_nop 0
	v_sub_f32_e32 v20, v20, v21
	v_mul_f32_e32 v55, 0x3d800000, v20
	v_mov_b32_e32 v20, v17
	v_mov_b32_e32 v21, v16
	v_pk_mul_f32 v[16:17], v[20:21], v[18:19]
	v_mul_f32_e32 v21, v115, v55
	v_add_f32_e32 v16, v16, v17
	v_mul_f32_e32 v16, 0x3d800000, v16
	v_mul_f32_e32 v56, v115, v16
	v_mul_f32_e32 v57, v173, v16
	v_lshl_add_u64 v[16:17], s[6:7], 0, v[34:35]
	v_lshl_add_u64 v[16:17], v[16:17], 0, s[58:59]
	v_lshl_add_u64 v[16:17], v[16:17], 0, v[130:131]
	v_cvt_pk_bf16_f32 v18, v38, v44
	v_cvt_pk_bf16_f32 v19, v36, v48
	v_cvt_pk_bf16_f32 v20, v24, v52
	v_cvt_pk_bf16_f32 v21, v22, v21
	global_store_dwordx4 v[16:17], v[18:21], off sc1
	v_mul_f32_e32 v55, v173, v55
	s_mov_b64 s[58:59], 0x2400100
	v_add_co_u32_e32 v18, vcc, s72, v16
	v_cvt_pk_bf16_f32 v20, v39, v45
	v_cvt_pk_bf16_f32 v21, v37, v49
	v_cvt_pk_bf16_f32 v22, v28, v53
	v_cvt_pk_bf16_f32 v23, v23, v56
	s_nop 1
	v_addc_co_u32_e32 v19, vcc, 0, v17, vcc
	v_add_co_u32_e32 v24, vcc, s73, v16
	global_store_dwordx4 v[18:19], v[20:23], off sc1
	v_mul_f32_e32 v28, v42, v151
	v_lshl_add_u64 v[152:153], v[16:17], 0, s[58:59]
	v_cvt_pk_bf16_f32 v20, v40, v43
	v_cvt_pk_bf16_f32 v21, v46, v47
	v_cvt_pk_bf16_f32 v22, v29, v25
	v_addc_co_u32_e32 v25, vcc, 0, v17, vcc
	v_cvt_pk_bf16_f32 v23, v54, v55
	global_store_dwordx4 v[24:25], v[20:23], off sc1
	v_fract_f32_e32 v29, v28
	v_cos_f32_e32 v28, v29
	v_cvt_pk_bf16_f32 v20, v41, v30
	v_cvt_pk_bf16_f32 v21, v31, v50
	v_cvt_f32_i32_e32 v31, v4
	v_cvt_f32_i32_e32 v30, v12
	v_cvt_pk_bf16_f32 v22, v51, v26
	v_add_co_u32_e32 v26, vcc, s74, v16
	v_sin_f32_e32 v29, v29
	v_cvt_pk_bf16_f32 v23, v27, v57
	s_nop 0
	v_addc_co_u32_e32 v27, vcc, 0, v17, vcc
	global_store_dwordx4 v[26:27], v[20:23], off sc1
	s_nop 1
	v_pk_mul_f32 v[20:21], v[100:101], v[32:33] op_sel_hi:[0,1]
	v_pk_mul_f32 v[20:21], v[20:21], v[30:31]
	s_nop 0
	v_pk_mul_f32 v[22:23], v[28:29], v[20:21]
	s_nop 0
	v_sub_f32_e32 v4, v22, v23
	v_mul_f32_e32 v4, 0x3d800000, v4
	v_mov_b32_e32 v22, v29
	v_mov_b32_e32 v23, v28
	v_pk_mul_f32 v[20:21], v[22:23], v[20:21]
	v_mul_f32_e32 v22, v174, v4
	v_mul_f32_e32 v26, v124, v4
	v_mul_f32_e32 v4, v42, v175
	v_add_f32_e32 v12, v20, v21
	v_fract_f32_e32 v27, v4
	v_cvt_f32_i32_e32 v21, v5
	v_cvt_f32_i32_e32 v20, v13
; #define GAS __attribute__((address_space(1)))
; __device__ __forceinline__ v4u pack8(const f32x4 a, const f32x4 b) { v4u w; w.x = cvt_pk_bf16(a[0], a[1]); w.y = cvt_pk_bf16(a[2], a[3]); w.z = cvt_pk_bf16(b[0], b[1]); w.w = cvt_pk_bf16(b[2], b[3]); return w; }
; __device__ __forceinline__ float fexp(float x) { return __builtin_amdgcn_exp2f(x * 1.4426950408889634f); }
; __device__ __forceinline__ void cs_rev(float rev, float& c, float& s) { const float f = __builtin_amdgcn_fractf(rev); c = __builtin_amdgcn_cosf(f); s = __builtin_amdgcn_sinf(f); }
;     __device__ __forceinline__ void operator()(AccI& acc, const Unit& u, LAS unsigned char*, int wr, int wc, int fr, int fq) const {
;     ...
;                         for (int j = 0; j < 4; ++j) { const int il = 128 * bj + c0 + 4 * n + j; const float pos = (float)(n_ch * 256 + il); float c, s; cs_rev(pos * inv, c, s);
;                             const float x1 = (float)acc[0][bj][m][n][j] * (sw1 * sxc[bj][n][j]), x2 = (float)acc[1][bj][m][n][j] * (sw2 * sxc[bj][n][j]); const float o1 = (x1 * c - x2 * s) * 0.0625f, o2 = (x2 * c + x1 * s) * 0.0625f;
;                             const float wf = fexp(lgf * (float)(255 - il)), wb = fexp(lgb * (float)(il + 1));
;                             f1[n][j] = o1 * wf; f2[n][j] = o2 * wf; b1[n][j] = o1 * wb; b2[n][j] = o2 * wb; }
;                     const size_t tcol = (size_t)n_ch * 256 + 128 * bj + c0;
;                     bf16* pf = kTw + ((size_t)(h * HD + d)) * T + tcol; bf16* pb = pf + (size_t)RW * T;
;                     *(GAS v4u*)pf = pack8(f1[0], f1[1]); *(GAS v4u*)(pf + (size_t)128 * T) = pack8(f2[0], f2[1]);
;                     *(GAS v4u*)pb = pack8(b1[0], b1[1]); *(GAS v4u*)(pb + (size_t)128 * T) = pack8(b2[0], b2[1]);
	v_cos_f32_e32 v4, v27
	v_sin_f32_e32 v5, v27
	v_mul_f32_e32 v12, 0x3d800000, v12
	v_mul_f32_e32 v23, v174, v12
	v_mul_f32_e32 v27, v124, v12
	v_pk_mul_f32 v[12:13], v[100:101], v[32:33] op_sel:[1,0]
	s_nop 0
	v_pk_mul_f32 v[12:13], v[12:13], v[20:21]
	s_nop 0
	v_pk_mul_f32 v[20:21], v[4:5], v[12:13]
	s_nop 0
	v_sub_f32_e32 v20, v20, v21
	v_mul_f32_e32 v28, 0x3d800000, v20
	v_mov_b32_e32 v20, v5
	v_mov_b32_e32 v21, v4
	v_pk_mul_f32 v[4:5], v[20:21], v[12:13]
	v_cvt_f32_i32_e32 v13, v6
	v_add_f32_e32 v4, v4, v5
	v_mul_f32_e32 v20, 0x3d800000, v4
	v_mul_f32_e32 v4, v42, v176
	v_fract_f32_e32 v5, v4
	v_cvt_f32_i32_e32 v12, v14
	v_cos_f32_e32 v4, v5
	v_sin_f32_e32 v5, v5
	v_mul_f32_e32 v30, v125, v20
	v_mul_f32_e32 v14, v117, v20
	v_pk_mul_f32 v[20:21], v[102:103], v[32:33] op_sel_hi:[0,1]
	v_pk_mul_f32 v[12:13], v[20:21], v[12:13]
	v_mul_f32_e32 v29, v125, v28
	v_pk_mul_f32 v[20:21], v[4:5], v[12:13]
	v_mul_f32_e32 v28, v117, v28
	v_sub_f32_e32 v6, v20, v21
	v_mov_b32_e32 v20, v5
	v_mov_b32_e32 v21, v4
	v_pk_mul_f32 v[4:5], v[20:21], v[12:13]
	v_mul_f32_e32 v6, 0x3d800000, v6
	v_add_f32_e32 v4, v4, v5
	v_mul_f32_e32 v12, 0x3d800000, v4
	v_mul_f32_e32 v4, v42, v177
	v_mul_f32_e32 v20, v126, v6
	v_mul_f32_e32 v31, v118, v6
	v_fract_f32_e32 v5, v4
	v_cvt_f32_i32_e32 v6, v15
	v_cos_f32_e32 v4, v5
	v_sin_f32_e32 v5, v5
	v_mul_f32_e32 v21, v126, v12
	v_mul_f32_e32 v15, v118, v12
	v_pk_mul_f32 v[12:13], v[116:117], v[32:33] op_sel_hi:[0,1]
	v_pk_mul_f32 v[6:7], v[12:13], v[6:7]
	s_nop 0
	v_pk_mul_f32 v[12:13], v[4:5], v[6:7]
	s_nop 0
	v_sub_f32_e32 v12, v12, v13
	v_mul_f32_e32 v34, 0x3d800000, v12
	v_mov_b32_e32 v12, v5
	v_mov_b32_e32 v13, v4
	v_pk_mul_f32 v[4:5], v[12:13], v[6:7]
	v_cvt_f32_i32_e32 v7, v0
	v_add_f32_e32 v4, v4, v5
	v_mul_f32_e32 v12, 0x3d800000, v4
	v_mul_f32_e32 v4, v42, v137
	v_fract_f32_e32 v5, v4
	v_cvt_f32_i32_e32 v6, v8
	v_cos_f32_e32 v4, v5
	v_sin_f32_e32 v5, v5
	v_mul_f32_e32 v36, v119, v12
	v_mul_f32_e32 v8, v103, v12
	v_pk_mul_f32 v[12:13], v[92:93], v[32:33] op_sel_hi:[0,1]
	v_pk_mul_f32 v[6:7], v[12:13], v[6:7]
	v_mul_f32_e32 v35, v119, v34
	v_pk_mul_f32 v[12:13], v[4:5], v[6:7]
	v_mul_f32_e32 v34, v103, v34
	v_sub_f32_e32 v0, v12, v13
	v_mov_b32_e32 v12, v5
	v_mov_b32_e32 v13, v4
	v_mul_f32_e32 v0, 0x3d800000, v0
	v_pk_mul_f32 v[4:5], v[12:13], v[6:7]
	v_mul_f32_e32 v12, v127, v0
	v_add_f32_e32 v4, v4, v5
	v_mul_f32_e32 v37, v108, v0
	v_mul_f32_e32 v0, v42, v178
	v_mul_f32_e32 v6, 0x3d800000, v4
	v_fract_f32_e32 v7, v0
	v_cvt_f32_i32_e32 v5, v1
	v_cvt_f32_i32_e32 v4, v9
	v_cos_f32_e32 v0, v7
	v_sin_f32_e32 v1, v7
	v_mul_f32_e32 v13, v127, v6
	v_mul_f32_e32 v9, v108, v6
	v_pk_mul_f32 v[6:7], v[92:93], v[32:33] op_sel:[1,0]
	s_nop 0
	v_pk_mul_f32 v[4:5], v[6:7], v[4:5]
	s_nop 0
	v_pk_mul_f32 v[6:7], v[0:1], v[4:5]
	s_nop 0
	v_sub_f32_e32 v6, v6, v7
	v_mul_f32_e32 v38, 0x3d800000, v6
	v_mov_b32_e32 v6, v1
	v_mov_b32_e32 v7, v0
	v_pk_mul_f32 v[0:1], v[6:7], v[4:5]
	v_cvt_f32_i32_e32 v5, v2
	v_add_f32_e32 v0, v0, v1
	v_mul_f32_e32 v6, 0x3d800000, v0
	v_mul_f32_e32 v0, v42, v179
	v_fract_f32_e32 v1, v0
	v_cvt_f32_i32_e32 v4, v10
	v_cos_f32_e32 v0, v1
	v_sin_f32_e32 v1, v1
	v_mul_f32_e32 v40, v109, v6
	v_mul_f32_e32 v10, v105, v6
	v_pk_mul_f32 v[6:7], v[94:95], v[32:33] op_sel_hi:[0,1]
	v_pk_mul_f32 v[4:5], v[6:7], v[4:5]
	v_mul_f32_e32 v39, v109, v38
	v_pk_mul_f32 v[6:7], v[0:1], v[4:5]
	v_mul_f32_e32 v38, v105, v38
	v_sub_f32_e32 v2, v6, v7
	v_mov_b32_e32 v6, v1
	v_mov_b32_e32 v7, v0
	v_pk_mul_f32 v[0:1], v[6:7], v[4:5]
	v_mul_f32_e32 v2, 0x3d800000, v2
	v_add_f32_e32 v0, v0, v1
	v_mul_f32_e32 v4, 0x3d800000, v0
	v_mul_f32_e32 v0, v42, v181
	v_mul_f32_e32 v6, v180, v2
	v_mul_f32_e32 v41, v110, v2
	v_fract_f32_e32 v1, v0
	v_cvt_f32_i32_e32 v2, v11
	v_cos_f32_e32 v0, v1
	v_sin_f32_e32 v1, v1
	v_mul_f32_e32 v7, v180, v4
	v_mul_f32_e32 v11, v110, v4
	v_pk_mul_f32 v[4:5], v[104:105], v[32:33] op_sel_hi:[0,1]
	v_pk_mul_f32 v[2:3], v[4:5], v[2:3]
	s_nop 0
	v_pk_mul_f32 v[4:5], v[0:1], v[2:3]
	s_nop 0
	v_sub_f32_e32 v4, v4, v5
	v_mul_f32_e32 v32, 0x3d800000, v4
	v_mov_b32_e32 v4, v1
	v_mov_b32_e32 v5, v0
	v_pk_mul_f32 v[0:1], v[4:5], v[2:3]
	v_mul_f32_e32 v3, v95, v32
	v_add_f32_e32 v0, v0, v1
	v_mul_f32_e32 v0, 0x3d800000, v0
	v_mul_f32_e32 v4, v95, v0
	v_mul_f32_e32 v5, v111, v32
	v_mul_f32_e32 v32, v111, v0
	v_cvt_pk_bf16_f32 v0, v22, v29
	v_cvt_pk_bf16_f32 v1, v20, v35
	v_cvt_pk_bf16_f32 v2, v12, v39
	v_cvt_pk_bf16_f32 v3, v6, v3
	global_store_dwordx4 v[16:17], v[0:3], off offset:256 sc1
	s_nop 1
	v_cvt_pk_bf16_f32 v0, v23, v30
	v_cvt_pk_bf16_f32 v1, v21, v36
	v_cvt_pk_bf16_f32 v2, v13, v40
	v_cvt_pk_bf16_f32 v3, v7, v4
	global_store_dwordx4 v[18:19], v[0:3], off offset:256 sc1
	s_nop 1
	v_cvt_pk_bf16_f32 v0, v26, v28
	v_cvt_pk_bf16_f32 v1, v31, v34
	v_cvt_pk_bf16_f32 v2, v37, v38
	v_cvt_pk_bf16_f32 v3, v41, v5
	global_store_dwordx4 v[24:25], v[0:3], off offset:256 sc1
	v_cvt_pk_bf16_f32 v144, v27, v14
	v_cvt_pk_bf16_f32 v145, v15, v8
	v_cvt_pk_bf16_f32 v146, v9, v10
	v_cvt_pk_bf16_f32 v147, v11, v32
	s_andn2_b64 vcc, exec, s[46:47]
	s_mov_b64 s[46:47], -1
	global_store_dwordx4 v[152:153], v[144:147], off sc1
	s_cbranch_vccnz .LBB0_275

; #define GAS __attribute__((address_space(1)))
; #define LAS __attribute__((address_space(3)))
; __device__ __forceinline__ void do_slabs_impl(LAS unsigned char* lds, unsigned char* ws, const float* w_up, const float* w_dn, const float* w_in, int vcu, int G, int wave, int j0, int j1) {
;     ...
;             for (int i = 0; i < 8; ++i) { const int q = tid + NTHR * i, n = q >> 7, kc = q & 127; const float inv = red[256 + n];
;                 const int sx_ = ((n >> 3) & 3) << 3;
;                 const v4u a = *(const LAS v4u*)(slab + n * PITCH + ((kc * 16) ^ sx_)), b = *(const LAS v4u*)(slab + n * PITCH + ((kc * 16 + 8) ^ sx_));
;                 const unsigned src[8] = {a.x, a.y, a.z, a.w, b.x, b.y, b.z, b.w}; unsigned o[4];
;                 if (done.fp8) {
; #pragma unroll
;                     for (int d = 0; d < 4; ++d) { int w = __builtin_amdgcn_cvt_pk_fp8_f32(bf_lo(src[2 * d]) * inv, bf_hi(src[2 * d]) * inv, 0, false);
;                         w = __builtin_amdgcn_cvt_pk_fp8_f32(bf_lo(src[2 * d + 1]) * inv, bf_hi(src[2 * d + 1]) * inv, w, true); o[d] = (unsigned)w; }
;                 } else {
; #pragma unroll
;                 for (int d = 0; d < 4; ++d) { unsigned w = 0u;
; #pragma unroll
;                     for (int h2 = 0; h2 < 2; ++h2) { const unsigned u2 = src[2 * d + h2]; const int q0 = (int)__builtin_rintf(bf_lo(u2) * inv), q1 = (int)__builtin_rintf(bf_hi(u2) * inv);
;                         w |= ((unsigned)(q0 & 0xff) << (16 * h2)) | ((unsigned)(q1 & 0xff) << (16 * h2 + 8)); }
;                     o[d] = w; }
;                 }
;                 __builtin_nontemporal_store((v4u){o[0], o[1], o[2], o[3]}, (GAS v4u*)(done.WQ + ((size_t)done.e * done.NS + done.n0 + n) * D + kc * 16)); }
.LBB0_345:
	v_ashrrev_i32_e32 v139, 31, v138
	v_lshl_add_u64 v[138:139], s[38:39], 0, v[138:139]
	v_lshlrev_b64 v[138:139], 11, v[138:139]
	s_addk_i32 s1, 0x400
	v_lshl_add_u64 v[138:139], v[136:137], 0, v[138:139]
	s_cmpk_lg_i32 s1, 0x1000
	global_store_dwordx4 v[138:139], v[128:131], off nt sc1
	s_cbranch_scc0 .LBB0_324

; #define GAS __attribute__((address_space(1)))
; #define LAS __attribute__((address_space(3)))
; __device__ __forceinline__ void do_slabs_impl(LAS unsigned char* lds, unsigned char* ws, const float* w_up, const float* w_dn, const float* w_in, int vcu, int G, int wave, int j0, int j1) {
;     ...
;             for (int i = 0; i < 8; ++i) { const int q = tid + NTHR * i, n = q >> 7, kc = q & 127; const float inv = red[256 + n];
;                 const int sx_ = ((n >> 3) & 3) << 3;
;                 const v4u a = *(const LAS v4u*)(slab + n * PITCH + ((kc * 16) ^ sx_)), b = *(const LAS v4u*)(slab + n * PITCH + ((kc * 16 + 8) ^ sx_));
;                 const unsigned src[8] = {a.x, a.y, a.z, a.w, b.x, b.y, b.z, b.w}; unsigned o[4];
;                 if (done.fp8) {
; #pragma unroll
;                     for (int d = 0; d < 4; ++d) { int w = __builtin_amdgcn_cvt_pk_fp8_f32(bf_lo(src[2 * d]) * inv, bf_hi(src[2 * d]) * inv, 0, false);
;                         w = __builtin_amdgcn_cvt_pk_fp8_f32(bf_lo(src[2 * d + 1]) * inv, bf_hi(src[2 * d + 1]) * inv, w, true); o[d] = (unsigned)w; }
;                 } else {
; #pragma unroll
;                 for (int d = 0; d < 4; ++d) { unsigned w = 0u;
; #pragma unroll
;                     for (int h2 = 0; h2 < 2; ++h2) { const unsigned u2 = src[2 * d + h2]; const int q0 = (int)__builtin_rintf(bf_lo(u2) * inv), q1 = (int)__builtin_rintf(bf_hi(u2) * inv);
;                         w |= ((unsigned)(q0 & 0xff) << (16 * h2)) | ((unsigned)(q1 & 0xff) << (16 * h2 + 8)); }
;                     o[d] = w; }
;                 }
;                 __builtin_nontemporal_store((v4u){o[0], o[1], o[2], o[3]}, (GAS v4u*)(done.WQ + ((size_t)done.e * done.NS + done.n0 + n) * D + kc * 16)); }
.LBB0_349:
	v_ashrrev_i32_e32 v139, 31, v138
	v_lshl_add_u64 v[138:139], s[38:39], 0, v[138:139]
	v_lshlrev_b64 v[138:139], 11, v[138:139]
	v_lshl_add_u64 v[184:185], v[136:137], 0, v[138:139]
	v_add_u32_e32 v139, 0x200, v180
	v_ashrrev_i32_e32 v138, 7, v139
	v_lshrrev_b32_e32 v186, 7, v139
	v_mul_lo_u32 v139, v138, s10
	v_add_u32_e32 v187, 0, v139
	v_bitop3_b32 v139, v186, v134, 24 bitop3:0x6c
	v_lshl_add_u32 v180, v138, 2, s2
	v_lshl_add_u32 v181, v139, 1, v187
	ds_read_b32 v139, v180 offset:1024
	ds_read_b128 v[180:183], v181
	global_store_dwordx4 v[184:185], v[128:131], off nt sc1
	s_and_b64 vcc, exec, s[8:9]
	s_waitcnt lgkmcnt(0)
	v_lshlrev_b32_e32 v184, 16, v180
	v_bitop3_b32 v128, v186, v143, 24 bitop3:0x6c
	v_lshl_add_u32 v128, v128, 1, v187
	ds_read_b128 v[128:131], v128
	v_and_b32_e32 v180, 0xffff0000, v180
	v_mul_f32_e32 v194, v139, v184
	v_mul_f32_e32 v195, v139, v180
	v_lshlrev_b32_e32 v193, 16, v181
	v_and_b32_e32 v192, 0xffff0000, v181
	v_lshlrev_b32_e32 v191, 16, v182
	v_and_b32_e32 v190, 0xffff0000, v182
	v_lshlrev_b32_e32 v189, 16, v183
	v_and_b32_e32 v188, 0xffff0000, v183
	s_waitcnt lgkmcnt(0)
	v_lshlrev_b32_e32 v187, 16, v128
	v_and_b32_e32 v186, 0xffff0000, v128
	v_lshlrev_b32_e32 v185, 16, v129
	v_and_b32_e32 v184, 0xffff0000, v129
	v_lshlrev_b32_e32 v183, 16, v130
	v_and_b32_e32 v182, 0xffff0000, v130
	v_lshlrev_b32_e32 v181, 16, v131
	v_and_b32_e32 v180, 0xffff0000, v131
	s_cbranch_vccnz .LBB0_352
	v_mov_b32_e32 v128, 0
	v_cvt_pk_fp8_f32 v128, v194, v195
	v_mul_f32_e32 v196, v139, v191
	v_mul_f32_e32 v197, v139, v190
	v_mov_b32_e32 v129, 0
	v_cvt_pk_fp8_f32 v129, v196, v197
	v_mul_f32_e32 v130, v139, v193
	v_mul_f32_e32 v131, v139, v192
	v_cvt_pk_fp8_f32 v128, v130, v131 op_sel:[0,0,1]
	v_mul_f32_e32 v130, v139, v189
	v_mul_f32_e32 v131, v139, v188
	v_cvt_pk_fp8_f32 v129, v130, v131 op_sel:[0,0,1]
	v_mul_f32_e32 v131, v139, v187
	v_mul_f32_e32 v196, v139, v186
	v_mov_b32_e32 v130, 0
	v_cvt_pk_fp8_f32 v130, v131, v196
	v_mul_f32_e32 v198, v139, v183
	v_mul_f32_e32 v199, v139, v182
	v_mov_b32_e32 v131, 0
	v_cvt_pk_fp8_f32 v131, v198, v199
	v_mul_f32_e32 v196, v139, v185
	v_mul_f32_e32 v197, v139, v184
	v_cvt_pk_fp8_f32 v130, v196, v197 op_sel:[0,0,1]
	v_mul_f32_e32 v196, v139, v181
	v_mul_f32_e32 v197, v139, v180
	v_cvt_pk_fp8_f32 v131, v196, v197 op_sel:[0,0,1]
	s_cbranch_execnz .LBB0_345
	s_branch .LBB0_344

; #define GAS __attribute__((address_space(1)))
; #define LAS __attribute__((address_space(3)))
; __device__ __forceinline__ void do_slabs_impl(LAS unsigned char* lds, unsigned char* ws, const float* w_up, const float* w_dn, const float* w_in, int vcu, int G, int wave, int j0, int j1) {
;     ...
;             for (int i = 0; i < 8; ++i) { const int q = tid + NTHR * i, n = q >> 7, kc = q & 127; const float inv = red[256 + n];
;                 const int sx_ = ((n >> 3) & 3) << 3;
;                 const v4u a = *(const LAS v4u*)(slab + n * PITCH + ((kc * 16) ^ sx_)), b = *(const LAS v4u*)(slab + n * PITCH + ((kc * 16 + 8) ^ sx_));
;                 const unsigned src[8] = {a.x, a.y, a.z, a.w, b.x, b.y, b.z, b.w}; unsigned o[4];
;                 if (done.fp8) {
; #pragma unroll
;                     for (int d = 0; d < 4; ++d) { int w = __builtin_amdgcn_cvt_pk_fp8_f32(bf_lo(src[2 * d]) * inv, bf_hi(src[2 * d]) * inv, 0, false);
;                         w = __builtin_amdgcn_cvt_pk_fp8_f32(bf_lo(src[2 * d + 1]) * inv, bf_hi(src[2 * d + 1]) * inv, w, true); o[d] = (unsigned)w; }
;                 } else {
; #pragma unroll
;                 for (int d = 0; d < 4; ++d) { unsigned w = 0u;
; #pragma unroll
;                     for (int h2 = 0; h2 < 2; ++h2) { const unsigned u2 = src[2 * d + h2]; const int q0 = (int)__builtin_rintf(bf_lo(u2) * inv), q1 = (int)__builtin_rintf(bf_hi(u2) * inv);
;                         w |= ((unsigned)(q0 & 0xff) << (16 * h2)) | ((unsigned)(q1 & 0xff) << (16 * h2 + 8)); }
;                     o[d] = w; }
;                 }
;                 __builtin_nontemporal_store((v4u){o[0], o[1], o[2], o[3]}, (GAS v4u*)(done.WQ + ((size_t)done.e * done.NS + done.n0 + n) * D + kc * 16)); }
.LBB0_380:
	v_ashrrev_i32_e32 v139, 31, v138
	v_lshl_add_u64 v[138:139], s[38:39], 0, v[138:139]
	v_lshlrev_b64 v[138:139], 11, v[138:139]
	s_addk_i32 s3, 0x400
	v_lshl_add_u64 v[138:139], v[136:137], 0, v[138:139]
	s_cmpk_lg_i32 s3, 0x1000
	global_store_dwordx4 v[138:139], v[128:131], off nt sc1
	s_cbranch_scc0 .LBB0_359

; #define GAS __attribute__((address_space(1)))
; #define LAS __attribute__((address_space(3)))
; __device__ __forceinline__ void do_slabs_impl(LAS unsigned char* lds, unsigned char* ws, const float* w_up, const float* w_dn, const float* w_in, int vcu, int G, int wave, int j0, int j1) {
;     ...
;             for (int i = 0; i < 8; ++i) { const int q = tid + NTHR * i, n = q >> 7, kc = q & 127; const float inv = red[256 + n];
;                 const int sx_ = ((n >> 3) & 3) << 3;
;                 const v4u a = *(const LAS v4u*)(slab + n * PITCH + ((kc * 16) ^ sx_)), b = *(const LAS v4u*)(slab + n * PITCH + ((kc * 16 + 8) ^ sx_));
;                 const unsigned src[8] = {a.x, a.y, a.z, a.w, b.x, b.y, b.z, b.w}; unsigned o[4];
;                 if (done.fp8) {
; #pragma unroll
;                     for (int d = 0; d < 4; ++d) { int w = __builtin_amdgcn_cvt_pk_fp8_f32(bf_lo(src[2 * d]) * inv, bf_hi(src[2 * d]) * inv, 0, false);
;                         w = __builtin_amdgcn_cvt_pk_fp8_f32(bf_lo(src[2 * d + 1]) * inv, bf_hi(src[2 * d + 1]) * inv, w, true); o[d] = (unsigned)w; }
;                 } else {
; #pragma unroll
;                 for (int d = 0; d < 4; ++d) { unsigned w = 0u;
; #pragma unroll
;                     for (int h2 = 0; h2 < 2; ++h2) { const unsigned u2 = src[2 * d + h2]; const int q0 = (int)__builtin_rintf(bf_lo(u2) * inv), q1 = (int)__builtin_rintf(bf_hi(u2) * inv);
;                         w |= ((unsigned)(q0 & 0xff) << (16 * h2)) | ((unsigned)(q1 & 0xff) << (16 * h2 + 8)); }
;                     o[d] = w; }
;                 }
;                 __builtin_nontemporal_store((v4u){o[0], o[1], o[2], o[3]}, (GAS v4u*)(done.WQ + ((size_t)done.e * done.NS + done.n0 + n) * D + kc * 16)); }
.LBB0_415:
	v_ashrrev_i32_e32 v139, 31, v138
	v_lshl_add_u64 v[138:139], s[14:15], 0, v[138:139]
	v_lshlrev_b64 v[138:139], 11, v[138:139]
	s_addk_i32 s1, 0x400
	v_lshl_add_u64 v[138:139], v[136:137], 0, v[138:139]
	s_cmpk_lg_i32 s1, 0x1000
	global_store_dwordx4 v[138:139], v[128:131], off nt sc1
	s_cbranch_scc0 .LBB0_394

; #define GAS __attribute__((address_space(1)))
; #define LAS __attribute__((address_space(3)))
; __device__ __forceinline__ void do_slabs_impl(LAS unsigned char* lds, unsigned char* ws, const float* w_up, const float* w_dn, const float* w_in, int vcu, int G, int wave, int j0, int j1) {
;     ...
;             for (int i = 0; i < 8; ++i) { const int q = tid + NTHR * i, n = q >> 7, kc = q & 127; const float inv = red[256 + n];
;                 const int sx_ = ((n >> 3) & 3) << 3;
;                 const v4u a = *(const LAS v4u*)(slab + n * PITCH + ((kc * 16) ^ sx_)), b = *(const LAS v4u*)(slab + n * PITCH + ((kc * 16 + 8) ^ sx_));
;                 const unsigned src[8] = {a.x, a.y, a.z, a.w, b.x, b.y, b.z, b.w}; unsigned o[4];
;                 if (done.fp8) {
; #pragma unroll
;                     for (int d = 0; d < 4; ++d) { int w = __builtin_amdgcn_cvt_pk_fp8_f32(bf_lo(src[2 * d]) * inv, bf_hi(src[2 * d]) * inv, 0, false);
;                         w = __builtin_amdgcn_cvt_pk_fp8_f32(bf_lo(src[2 * d + 1]) * inv, bf_hi(src[2 * d + 1]) * inv, w, true); o[d] = (unsigned)w; }
;                 } else {
; #pragma unroll
;                 for (int d = 0; d < 4; ++d) { unsigned w = 0u;
; #pragma unroll
;                     for (int h2 = 0; h2 < 2; ++h2) { const unsigned u2 = src[2 * d + h2]; const int q0 = (int)__builtin_rintf(bf_lo(u2) * inv), q1 = (int)__builtin_rintf(bf_hi(u2) * inv);
;                         w |= ((unsigned)(q0 & 0xff) << (16 * h2)) | ((unsigned)(q1 & 0xff) << (16 * h2 + 8)); }
;                     o[d] = w; }
;                 }
;                 __builtin_nontemporal_store((v4u){o[0], o[1], o[2], o[3]}, (GAS v4u*)(done.WQ + ((size_t)done.e * done.NS + done.n0 + n) * D + kc * 16)); }
.LBB0_419:
	v_ashrrev_i32_e32 v139, 31, v138
	v_lshl_add_u64 v[138:139], s[14:15], 0, v[138:139]
	v_lshlrev_b64 v[138:139], 11, v[138:139]
	v_lshl_add_u64 v[184:185], v[136:137], 0, v[138:139]
	v_add_u32_e32 v139, 0x200, v180
	v_ashrrev_i32_e32 v138, 7, v139
	v_lshrrev_b32_e32 v186, 7, v139
	v_mul_lo_u32 v139, v138, s3
	v_add_u32_e32 v187, 0, v139
	v_bitop3_b32 v139, v186, v134, 24 bitop3:0x6c
	v_lshl_add_u32 v180, v138, 2, s2
	v_lshl_add_u32 v181, v139, 1, v187
	ds_read_b32 v139, v180 offset:1024
	ds_read_b128 v[180:183], v181
	global_store_dwordx4 v[184:185], v[128:131], off nt sc1
	s_and_b64 vcc, exec, s[8:9]
	s_waitcnt lgkmcnt(0)
	v_lshlrev_b32_e32 v184, 16, v180
	v_bitop3_b32 v128, v186, v143, 24 bitop3:0x6c
	v_lshl_add_u32 v128, v128, 1, v187
	ds_read_b128 v[128:131], v128
	v_and_b32_e32 v180, 0xffff0000, v180
	v_mul_f32_e32 v194, v139, v184
	v_mul_f32_e32 v195, v139, v180
	v_lshlrev_b32_e32 v193, 16, v181
	v_and_b32_e32 v192, 0xffff0000, v181
	v_lshlrev_b32_e32 v191, 16, v182
	v_and_b32_e32 v190, 0xffff0000, v182
	v_lshlrev_b32_e32 v189, 16, v183
	v_and_b32_e32 v188, 0xffff0000, v183
	s_waitcnt lgkmcnt(0)
	v_lshlrev_b32_e32 v187, 16, v128
	v_and_b32_e32 v186, 0xffff0000, v128
	v_lshlrev_b32_e32 v185, 16, v129
	v_and_b32_e32 v184, 0xffff0000, v129
	v_lshlrev_b32_e32 v183, 16, v130
	v_and_b32_e32 v182, 0xffff0000, v130
	v_lshlrev_b32_e32 v181, 16, v131
	v_and_b32_e32 v180, 0xffff0000, v131
	s_cbranch_vccnz .LBB0_422
	v_mov_b32_e32 v128, 0
	v_cvt_pk_fp8_f32 v128, v194, v195
	v_mul_f32_e32 v196, v139, v191
	v_mul_f32_e32 v197, v139, v190
	v_mov_b32_e32 v129, 0
	v_cvt_pk_fp8_f32 v129, v196, v197
	v_mul_f32_e32 v130, v139, v193
	v_mul_f32_e32 v131, v139, v192
	v_cvt_pk_fp8_f32 v128, v130, v131 op_sel:[0,0,1]
	v_mul_f32_e32 v130, v139, v189
	v_mul_f32_e32 v131, v139, v188
	v_cvt_pk_fp8_f32 v129, v130, v131 op_sel:[0,0,1]
	v_mul_f32_e32 v131, v139, v187
	v_mul_f32_e32 v196, v139, v186
	v_mov_b32_e32 v130, 0
	v_cvt_pk_fp8_f32 v130, v131, v196
	v_mul_f32_e32 v198, v139, v183
	v_mul_f32_e32 v199, v139, v182
	v_mov_b32_e32 v131, 0
	v_cvt_pk_fp8_f32 v131, v198, v199
	v_mul_f32_e32 v196, v139, v185
	v_mul_f32_e32 v197, v139, v184
	v_cvt_pk_fp8_f32 v130, v196, v197 op_sel:[0,0,1]
	v_mul_f32_e32 v196, v139, v181
	v_mul_f32_e32 v197, v139, v180
	v_cvt_pk_fp8_f32 v131, v196, v197 op_sel:[0,0,1]
	s_cbranch_execnz .LBB0_415
	s_branch .LBB0_414

; #define GAS __attribute__((address_space(1)))
; #define LAS __attribute__((address_space(3)))
; __device__ __forceinline__ void do_slabs_impl(LAS unsigned char* lds, unsigned char* ws, const float* w_up, const float* w_dn, const float* w_in, int vcu, int G, int wave, int j0, int j1) {
;     ...
;             for (int i = 0; i < 8; ++i) { const int q = tid + NTHR * i, n = q >> 7, kc = q & 127; const float inv = red[256 + n];
;                 const int sx_ = ((n >> 3) & 3) << 3;
;                 const v4u a = *(const LAS v4u*)(slab + n * PITCH + ((kc * 16) ^ sx_)), b = *(const LAS v4u*)(slab + n * PITCH + ((kc * 16 + 8) ^ sx_));
;                 const unsigned src[8] = {a.x, a.y, a.z, a.w, b.x, b.y, b.z, b.w}; unsigned o[4];
;                 if (done.fp8) {
; #pragma unroll
;                     for (int d = 0; d < 4; ++d) { int w = __builtin_amdgcn_cvt_pk_fp8_f32(bf_lo(src[2 * d]) * inv, bf_hi(src[2 * d]) * inv, 0, false);
;                         w = __builtin_amdgcn_cvt_pk_fp8_f32(bf_lo(src[2 * d + 1]) * inv, bf_hi(src[2 * d + 1]) * inv, w, true); o[d] = (unsigned)w; }
;                 } else {
; #pragma unroll
;                 for (int d = 0; d < 4; ++d) { unsigned w = 0u;
; #pragma unroll
;                     for (int h2 = 0; h2 < 2; ++h2) { const unsigned u2 = src[2 * d + h2]; const int q0 = (int)__builtin_rintf(bf_lo(u2) * inv), q1 = (int)__builtin_rintf(bf_hi(u2) * inv);
;                         w |= ((unsigned)(q0 & 0xff) << (16 * h2)) | ((unsigned)(q1 & 0xff) << (16 * h2 + 8)); }
;                     o[d] = w; }
;                 }
;                 __builtin_nontemporal_store((v4u){o[0], o[1], o[2], o[3]}, (GAS v4u*)(done.WQ + ((size_t)done.e * done.NS + done.n0 + n) * D + kc * 16)); }
.LBB0_502:
	v_ashrrev_i32_e32 v139, 31, v138
	v_lshl_add_u64 v[138:139], s[34:35], 0, v[138:139]
	v_lshlrev_b64 v[138:139], 11, v[138:139]
	s_addk_i32 s40, 0x400
	v_lshl_add_u64 v[138:139], v[136:137], 0, v[138:139]
	s_cmpk_lg_i32 s40, 0x1000
	global_store_dwordx4 v[138:139], v[128:131], off nt sc1
	s_cbranch_scc0 .LBB0_481

; #define GAS __attribute__((address_space(1)))
; #define LAS __attribute__((address_space(3)))
; __device__ __forceinline__ void do_slabs_impl(LAS unsigned char* lds, unsigned char* ws, const float* w_up, const float* w_dn, const float* w_in, int vcu, int G, int wave, int j0, int j1) {
;     ...
;             for (int i = 0; i < 8; ++i) { const int q = tid + NTHR * i, n = q >> 7, kc = q & 127; const float inv = red[256 + n];
;                 const int sx_ = ((n >> 3) & 3) << 3;
;                 const v4u a = *(const LAS v4u*)(slab + n * PITCH + ((kc * 16) ^ sx_)), b = *(const LAS v4u*)(slab + n * PITCH + ((kc * 16 + 8) ^ sx_));
;                 const unsigned src[8] = {a.x, a.y, a.z, a.w, b.x, b.y, b.z, b.w}; unsigned o[4];
;                 if (done.fp8) {
; #pragma unroll
;                     for (int d = 0; d < 4; ++d) { int w = __builtin_amdgcn_cvt_pk_fp8_f32(bf_lo(src[2 * d]) * inv, bf_hi(src[2 * d]) * inv, 0, false);
;                         w = __builtin_amdgcn_cvt_pk_fp8_f32(bf_lo(src[2 * d + 1]) * inv, bf_hi(src[2 * d + 1]) * inv, w, true); o[d] = (unsigned)w; }
;                 } else {
; #pragma unroll
;                 for (int d = 0; d < 4; ++d) { unsigned w = 0u;
; #pragma unroll
;                     for (int h2 = 0; h2 < 2; ++h2) { const unsigned u2 = src[2 * d + h2]; const int q0 = (int)__builtin_rintf(bf_lo(u2) * inv), q1 = (int)__builtin_rintf(bf_hi(u2) * inv);
;                         w |= ((unsigned)(q0 & 0xff) << (16 * h2)) | ((unsigned)(q1 & 0xff) << (16 * h2 + 8)); }
;                     o[d] = w; }
;                 }
;                 __builtin_nontemporal_store((v4u){o[0], o[1], o[2], o[3]}, (GAS v4u*)(done.WQ + ((size_t)done.e * done.NS + done.n0 + n) * D + kc * 16)); }
.LBB0_506:
	v_ashrrev_i32_e32 v139, 31, v138
	v_lshl_add_u64 v[138:139], s[34:35], 0, v[138:139]
	v_lshlrev_b64 v[138:139], 11, v[138:139]
	v_lshl_add_u64 v[184:185], v[136:137], 0, v[138:139]
	v_add_u32_e32 v139, 0x200, v180
	v_ashrrev_i32_e32 v138, 7, v139
	v_lshrrev_b32_e32 v186, 7, v139
	v_mul_lo_u32 v139, v138, s20
	v_add_u32_e32 v187, 0, v139
	v_bitop3_b32 v139, v186, v134, 24 bitop3:0x6c
	v_lshl_add_u32 v180, v138, 2, s3
	v_lshl_add_u32 v181, v139, 1, v187
	ds_read_b32 v139, v180 offset:1024
	ds_read_b128 v[180:183], v181
	global_store_dwordx4 v[184:185], v[128:131], off nt sc1
	s_and_b64 vcc, exec, s[8:9]
	s_waitcnt lgkmcnt(0)
	v_lshlrev_b32_e32 v184, 16, v180
	v_bitop3_b32 v128, v186, v143, 24 bitop3:0x6c
	v_lshl_add_u32 v128, v128, 1, v187
	ds_read_b128 v[128:131], v128
	v_and_b32_e32 v180, 0xffff0000, v180
	v_mul_f32_e32 v194, v139, v184
	v_mul_f32_e32 v195, v139, v180
	v_lshlrev_b32_e32 v193, 16, v181
	v_and_b32_e32 v192, 0xffff0000, v181
	v_lshlrev_b32_e32 v191, 16, v182
	v_and_b32_e32 v190, 0xffff0000, v182
	v_lshlrev_b32_e32 v189, 16, v183
	v_and_b32_e32 v188, 0xffff0000, v183
	s_waitcnt lgkmcnt(0)
	v_lshlrev_b32_e32 v187, 16, v128
	v_and_b32_e32 v186, 0xffff0000, v128
	v_lshlrev_b32_e32 v185, 16, v129
	v_and_b32_e32 v184, 0xffff0000, v129
	v_lshlrev_b32_e32 v183, 16, v130
	v_and_b32_e32 v182, 0xffff0000, v130
	v_lshlrev_b32_e32 v181, 16, v131
	v_and_b32_e32 v180, 0xffff0000, v131
	s_cbranch_vccnz .LBB0_509
	v_mov_b32_e32 v128, 0
	v_cvt_pk_fp8_f32 v128, v194, v195
	v_mul_f32_e32 v196, v139, v191
	v_mul_f32_e32 v197, v139, v190
	v_mov_b32_e32 v129, 0
	v_cvt_pk_fp8_f32 v129, v196, v197
	v_mul_f32_e32 v130, v139, v193
	v_mul_f32_e32 v131, v139, v192
	v_cvt_pk_fp8_f32 v128, v130, v131 op_sel:[0,0,1]
	v_mul_f32_e32 v130, v139, v189
	v_mul_f32_e32 v131, v139, v188
	v_cvt_pk_fp8_f32 v129, v130, v131 op_sel:[0,0,1]
	v_mul_f32_e32 v131, v139, v187
	v_mul_f32_e32 v196, v139, v186
	v_mov_b32_e32 v130, 0
	v_cvt_pk_fp8_f32 v130, v131, v196
	v_mul_f32_e32 v198, v139, v183
	v_mul_f32_e32 v199, v139, v182
	v_mov_b32_e32 v131, 0
	v_cvt_pk_fp8_f32 v131, v198, v199
	v_mul_f32_e32 v196, v139, v185
	v_mul_f32_e32 v197, v139, v184
	v_cvt_pk_fp8_f32 v130, v196, v197 op_sel:[0,0,1]
	v_mul_f32_e32 v196, v139, v181
	v_mul_f32_e32 v197, v139, v180
	v_cvt_pk_fp8_f32 v131, v196, v197 op_sel:[0,0,1]
	s_cbranch_execnz .LBB0_502
	s_branch .LBB0_501

; #define GAS __attribute__((address_space(1)))
; __device__ __forceinline__ v4u pack8(const f32x4 a, const f32x4 b) { v4u w; w.x = cvt_pk_bf16(a[0], a[1]); w.y = cvt_pk_bf16(a[2], a[3]); w.z = cvt_pk_bf16(b[0], b[1]); w.w = cvt_pk_bf16(b[2], b[3]); return w; }
; __device__ __forceinline__ void cs_rev(float rev, float& c, float& s) { const float f = __builtin_amdgcn_fractf(rev); c = __builtin_amdgcn_cosf(f); s = __builtin_amdgcn_sinf(f); }
; #define EPI_FENCE __builtin_amdgcn_sched_barrier(0)
;     __device__ __forceinline__ void operator()(Acc& acc, const Unit& u, LAS unsigned char*, int wr, int wc, int fr, int fq) const {
;         const int b0 = wc * 32 + 8 * fq;
; #pragma unroll
;         for (int m = 0; m < 4; ++m) { const int k1 = 64 * wr + 16 * m + fr;
; #pragma unroll
;             for (int bj = 0; bj < 2; ++bj) { const int cch = 2 * u.p1 + bj; f32x4 re[2], im[2];
; #pragma unroll
;                 for (int n = 0; n < 2; ++n)
; #pragma unroll
;                     for (int j = 0; j < 4; ++j) { const int b = b0 + 4 * n + j; float c, s; cs_rev((float)(k1 * b) * (1.f / 16384.f), c, s);
;                         const float xr = acc[0][bj][m][n][j], xi = acc[1][bj][m][n][j]; re[n][j] = xr * c + xi * s; im[n][j] = xi * c - xr * s; }
;                 bf16* p = A1 + (((size_t)k1 * 1024 + cch) * 2) * 128 + b0;
;                 *(GAS v4u*)p = pack8(re[0], re[1]); *(GAS v4u*)(p + 128) = pack8(im[0], im[1]); EPI_FENCE; } }
.LBB0_525:
	v_mov_b32_e32 v128, v135
	v_mov_b32_e32 v130, v136
	v_mov_b32_e32 v149, v116
	v_lshl_add_u32 v132, v130, 3, s22
	v_add_u32_e32 v130, s21, v128
	v_ashrrev_i32_e32 v131, 31, v130
	v_lshlrev_b64 v[142:143], 19, v[130:131]
	v_mul_lo_u32 v131, v132, v130
	v_cvt_f32_i32_e32 v145, v131
	v_or_b32_e32 v128, 4, v132
	v_mul_lo_u32 v141, v128, v130
	v_cvt_f32_i32_e32 v144, v141
	v_mul_f32_e32 v145, 0x38800000, v145
	v_fract_f32_e32 v145, v145
	v_cos_f32_e32 v146, v145
	v_sin_f32_e32 v147, v145
	v_add_u32_e32 v154, v131, v130
	v_mul_f32_e32 v144, 0x38800000, v144
	v_cvt_f32_i32_e32 v150, v154
	v_fract_f32_e32 v148, v144
	v_cos_f32_e32 v144, v148
	v_sin_f32_e32 v145, v148
	v_mov_b32_e32 v148, v124
	v_pk_mul_f32 v[148:149], v[148:149], v[146:147]
	v_add_u32_e32 v157, v154, v130
	v_add_f32_e32 v155, v148, v149
	v_mov_b32_e32 v148, v116
	v_mul_f32_e32 v116, 0x38800000, v150
	v_fract_f32_e32 v116, v116
	v_cos_f32_e32 v150, v116
	v_sin_f32_e32 v151, v116
	v_cvt_f32_i32_e32 v152, v157
	v_mov_b32_e32 v149, v124
	v_pk_mul_f32 v[148:149], v[148:149], v[146:147]
	v_mov_b32_e32 v116, v125
	v_mov_b32_e32 v124, v117
	v_sub_f32_e32 v156, v148, v149
	v_pk_mul_f32 v[148:149], v[116:117], v[150:151]
	v_pk_mul_f32 v[116:117], v[124:125], v[150:151]
	v_mul_f32_e32 v124, 0x38800000, v152
	v_fract_f32_e32 v125, v124
	v_cos_f32_e32 v124, v125
	v_sin_f32_e32 v125, v125
	v_add_u32_e32 v160, v157, v130
	v_add_f32_e32 v158, v148, v149
	v_cvt_f32_i32_e32 v148, v160
	v_sub_f32_e32 v159, v116, v117
	v_mov_b32_e32 v116, v126
	v_mov_b32_e32 v117, v118
	v_pk_mul_f32 v[116:117], v[116:117], v[124:125]
	v_lshl_add_u32 v164, v130, 1, v160
	v_add_f32_e32 v161, v116, v117
	v_mov_b32_e32 v116, v118
	v_mul_f32_e32 v118, 0x38800000, v148
	v_fract_f32_e32 v118, v118
	v_cos_f32_e32 v148, v118
	v_sin_f32_e32 v149, v118
	v_mov_b32_e32 v117, v126
	v_pk_mul_f32 v[116:117], v[116:117], v[124:125]
	v_mov_b32_e32 v118, v127
	v_sub_f32_e32 v162, v116, v117
	v_pk_mul_f32 v[116:117], v[118:119], v[148:149]
	v_mov_b32_e32 v126, v119
	v_cvt_f32_i32_e32 v119, v164
	v_add_f32_e32 v118, v116, v117
	v_pk_mul_f32 v[116:117], v[126:127], v[148:149]
	v_add_u32_e32 v167, v164, v130
	v_sub_f32_e32 v163, v116, v117
	v_mov_b32_e32 v116, v120
	v_mov_b32_e32 v117, v108
	v_pk_mul_f32 v[116:117], v[116:117], v[144:145]
	v_add_u32_e32 v170, v167, v130
	v_add_f32_e32 v165, v116, v117
	v_mov_b32_e32 v116, v108
	v_mul_f32_e32 v108, 0x38800000, v119
	v_fract_f32_e32 v108, v108
	v_cos_f32_e32 v126, v108
	v_sin_f32_e32 v127, v108
	v_cvt_f32_i32_e32 v119, v167
	v_mov_b32_e32 v117, v120
	v_pk_mul_f32 v[116:117], v[116:117], v[144:145]
	v_mov_b32_e32 v108, v121
	v_sub_f32_e32 v166, v116, v117
	v_pk_mul_f32 v[116:117], v[108:109], v[126:127]
	v_mov_b32_e32 v120, v109
	v_add_f32_e32 v168, v116, v117
	v_mul_f32_e32 v116, 0x38800000, v119
	v_fract_f32_e32 v116, v116
	v_pk_mul_f32 v[108:109], v[120:121], v[126:127]
	v_cos_f32_e32 v120, v116
	v_sin_f32_e32 v121, v116
	v_cvt_f32_i32_e32 v116, v170
	v_sub_f32_e32 v169, v108, v109
	v_mov_b32_e32 v108, v122
	v_mov_b32_e32 v109, v110
	v_pk_mul_f32 v[108:109], v[108:109], v[120:121]
	s_lshl_b32 s56, s74, 1
	v_add_f32_e32 v119, v108, v109
	v_mov_b32_e32 v108, v110
	v_mul_f32_e32 v110, 0x38800000, v116
	v_fract_f32_e32 v110, v110
	v_cos_f32_e32 v152, v110
	v_sin_f32_e32 v153, v110
	v_mov_b32_e32 v109, v122
	v_pk_mul_f32 v[108:109], v[108:109], v[120:121]
	v_mov_b32_e32 v110, v123
	v_sub_f32_e32 v171, v108, v109
	v_pk_mul_f32 v[108:109], v[110:111], v[152:153]
	v_mov_b32_e32 v122, v111
	s_ashr_i32 s57, s56, 31
	v_ashrrev_i32_e32 v133, 31, v132
	v_add_f32_e32 v172, v108, v109
	v_pk_mul_f32 v[108:109], v[122:123], v[152:153]
	v_lshl_add_u64 v[110:111], s[38:39], 0, v[142:143]
	s_lshl_b64 s[54:55], s[56:57], 9
	v_sub_f32_e32 v173, v108, v109
	v_lshl_add_u64 v[116:117], v[110:111], 0, s[54:55]
	v_lshlrev_b64 v[108:109], 1, v[132:133]
	v_lshl_add_u64 v[122:123], v[116:117], 0, v[108:109]
	v_cvt_pk_bf16_f32 v116, v155, v158
	v_cvt_pk_bf16_f32 v117, v161, v118
	v_cvt_pk_bf16_f32 v118, v165, v168
	v_cvt_pk_bf16_f32 v119, v119, v172
	global_store_dwordx4 v[122:123], v[116:119], off sc1
	s_nop 1
	v_cvt_pk_bf16_f32 v116, v156, v159
	v_cvt_pk_bf16_f32 v117, v162, v163
	v_cvt_pk_bf16_f32 v118, v166, v169
	v_cvt_pk_bf16_f32 v119, v171, v173
	global_store_dwordx4 v[122:123], v[116:119], off offset:256 sc1
	s_nop 1
	v_mov_b32_e32 v116, v112
	v_mov_b32_e32 v117, v100
	v_pk_mul_f32 v[116:117], v[116:117], v[146:147]
	s_or_b32 s56, s56, 1
	v_add_f32_e32 v118, v116, v117
	v_mov_b32_e32 v116, v100
	v_mov_b32_e32 v117, v112
	v_pk_mul_f32 v[116:117], v[116:117], v[146:147]
	v_mov_b32_e32 v100, v113
	v_mov_b32_e32 v112, v101
	v_sub_f32_e32 v119, v116, v117
	v_pk_mul_f32 v[116:117], v[100:101], v[150:151]
	v_pk_mul_f32 v[100:101], v[112:113], v[150:151]
	v_add_f32_e32 v116, v116, v117
	v_sub_f32_e32 v112, v100, v101
	v_mov_b32_e32 v100, v114
	v_mov_b32_e32 v101, v102
	v_pk_mul_f32 v[100:101], v[100:101], v[124:125]
	s_ashr_i32 s57, s56, 31
	v_add_f32_e32 v113, v100, v101
	v_mov_b32_e32 v100, v102
	v_mov_b32_e32 v101, v114
	v_pk_mul_f32 v[100:101], v[100:101], v[124:125]
	v_mov_b32_e32 v102, v115
	v_sub_f32_e32 v117, v100, v101
	v_pk_mul_f32 v[100:101], v[102:103], v[148:149]
	v_mov_b32_e32 v114, v103
	v_add_f32_e32 v102, v100, v101
	v_pk_mul_f32 v[100:101], v[114:115], v[148:149]
	s_lshl_b64 s[56:57], s[56:57], 9
	v_sub_f32_e32 v103, v100, v101
	v_mov_b32_e32 v100, v104
	v_mov_b32_e32 v101, v96
	v_pk_mul_f32 v[100:101], v[100:101], v[144:145]
	s_nop 0
	v_add_f32_e32 v114, v100, v101
	v_mov_b32_e32 v100, v96
	v_mov_b32_e32 v101, v104
	v_pk_mul_f32 v[100:101], v[100:101], v[144:145]
	v_mov_b32_e32 v96, v105
; #define GAS __attribute__((address_space(1)))
; __device__ __forceinline__ v4u pack8(const f32x4 a, const f32x4 b) { v4u w; w.x = cvt_pk_bf16(a[0], a[1]); w.y = cvt_pk_bf16(a[2], a[3]); w.z = cvt_pk_bf16(b[0], b[1]); w.w = cvt_pk_bf16(b[2], b[3]); return w; }
; __device__ __forceinline__ void cs_rev(float rev, float& c, float& s) { const float f = __builtin_amdgcn_fractf(rev); c = __builtin_amdgcn_cosf(f); s = __builtin_amdgcn_sinf(f); }
; #define EPI_FENCE __builtin_amdgcn_sched_barrier(0)
;     __device__ __forceinline__ void operator()(Acc& acc, const Unit& u, LAS unsigned char*, int wr, int wc, int fr, int fq) const {
;         const int b0 = wc * 32 + 8 * fq;
; #pragma unroll
;         for (int m = 0; m < 4; ++m) { const int k1 = 64 * wr + 16 * m + fr;
; #pragma unroll
;             for (int bj = 0; bj < 2; ++bj) { const int cch = 2 * u.p1 + bj; f32x4 re[2], im[2];
; #pragma unroll
;                 for (int n = 0; n < 2; ++n)
; #pragma unroll
;                     for (int j = 0; j < 4; ++j) { const int b = b0 + 4 * n + j; float c, s; cs_rev((float)(k1 * b) * (1.f / 16384.f), c, s);
;                         const float xr = acc[0][bj][m][n][j], xi = acc[1][bj][m][n][j]; re[n][j] = xr * c + xi * s; im[n][j] = xi * c - xr * s; }
;                 bf16* p = A1 + (((size_t)k1 * 1024 + cch) * 2) * 128 + b0;
;                 *(GAS v4u*)p = pack8(re[0], re[1]); *(GAS v4u*)(p + 128) = pack8(im[0], im[1]); EPI_FENCE; } }
	v_mov_b32_e32 v104, v97
	v_sub_f32_e32 v115, v100, v101
	v_pk_mul_f32 v[100:101], v[96:97], v[126:127]
	v_pk_mul_f32 v[96:97], v[104:105], v[126:127]
	v_add_f32_e32 v122, v100, v101
	v_sub_f32_e32 v104, v96, v97
	v_mov_b32_e32 v96, v106
	v_mov_b32_e32 v97, v98
	v_pk_mul_f32 v[96:97], v[96:97], v[120:121]
	s_nop 0
	v_add_f32_e32 v105, v96, v97
	v_mov_b32_e32 v96, v98
	v_mov_b32_e32 v97, v106
	v_pk_mul_f32 v[96:97], v[96:97], v[120:121]
	v_mov_b32_e32 v98, v107
	v_sub_f32_e32 v120, v96, v97
	v_pk_mul_f32 v[96:97], v[98:99], v[152:153]
	v_mov_b32_e32 v106, v99
	v_add_f32_e32 v121, v96, v97
	v_pk_mul_f32 v[96:97], v[106:107], v[152:153]
	s_nop 0
	v_sub_f32_e32 v106, v96, v97
	v_lshl_add_u64 v[96:97], v[110:111], 0, s[56:57]
	v_lshl_add_u64 v[100:101], v[96:97], 0, v[108:109]
	v_cvt_pk_bf16_f32 v96, v118, v116
	v_cvt_pk_bf16_f32 v97, v113, v102
	v_cvt_pk_bf16_f32 v98, v114, v122
	v_cvt_pk_bf16_f32 v99, v105, v121
	global_store_dwordx4 v[100:101], v[96:99], off sc1
	s_nop 1
	v_cvt_pk_bf16_f32 v96, v119, v112
	v_cvt_pk_bf16_f32 v97, v117, v103
	v_cvt_pk_bf16_f32 v98, v115, v104
	v_cvt_pk_bf16_f32 v99, v120, v106
	global_store_dwordx4 v[100:101], v[96:99], off offset:256 sc1
	s_nop 1
	v_add_u32_e32 v96, 16, v130
	v_ashrrev_i32_e32 v97, 31, v96
	v_lshlrev_b64 v[100:101], 19, v[96:97]
	v_lshlrev_b32_e32 v97, 4, v132
	v_add_u32_e32 v117, v131, v97
	v_cvt_f32_i32_e32 v99, v117
	v_lshlrev_b32_e32 v96, 4, v128
	v_add_u32_e32 v116, v141, v96
	v_cvt_f32_i32_e32 v98, v116
	v_mul_f32_e32 v99, 0x38800000, v99
	v_fract_f32_e32 v99, v99
	v_cos_f32_e32 v104, v99
	v_sin_f32_e32 v105, v99
	v_mul_f32_e32 v98, 0x38800000, v98
	v_fract_f32_e32 v98, v98
	v_cos_f32_e32 v102, v98
	v_sin_f32_e32 v103, v98
	v_mov_b32_e32 v98, v92
	v_mov_b32_e32 v99, v84
	v_pk_mul_f32 v[106:107], v[98:99], v[104:105]
	v_or_b32_e32 v98, 16, v97
	v_add_u32_e32 v99, v154, v98
	v_cvt_f32_i32_e32 v110, v99
	v_add_f32_e32 v118, v106, v107
	v_mov_b32_e32 v106, v84
	v_mov_b32_e32 v107, v92
	v_mul_f32_e32 v84, 0x38800000, v110
	v_fract_f32_e32 v84, v84
	v_cos_f32_e32 v110, v84
	v_sin_f32_e32 v111, v84
	v_pk_mul_f32 v[106:107], v[106:107], v[104:105]
	v_mov_b32_e32 v84, v93
	v_sub_f32_e32 v119, v106, v107
	v_pk_mul_f32 v[106:107], v[84:85], v[110:111]
	v_or_b32_e32 v84, 32, v97
	v_add_u32_e32 v120, v157, v84
	v_cvt_f32_i32_e32 v112, v120
	v_mov_b32_e32 v92, v85
	v_add_f32_e32 v121, v106, v107
	v_pk_mul_f32 v[92:93], v[92:93], v[110:111]
	v_mul_f32_e32 v85, 0x38800000, v112
	v_fract_f32_e32 v85, v85
	v_cos_f32_e32 v106, v85
	v_sin_f32_e32 v107, v85
	v_or_b32_e32 v85, 48, v97
	v_add_u32_e32 v123, v160, v85
	v_cvt_f32_i32_e32 v112, v123
	v_sub_f32_e32 v122, v92, v93
	v_mov_b32_e32 v92, v94
	v_mov_b32_e32 v93, v86
	v_pk_mul_f32 v[92:93], v[92:93], v[106:107]
	s_nop 0
	v_add_f32_e32 v124, v92, v93
	v_mov_b32_e32 v92, v86
	v_mul_f32_e32 v86, 0x38800000, v112
	v_fract_f32_e32 v86, v86
	v_cos_f32_e32 v112, v86
	v_sin_f32_e32 v113, v86
	v_mov_b32_e32 v93, v94
	v_pk_mul_f32 v[92:93], v[92:93], v[106:107]
	v_mov_b32_e32 v86, v95
	v_mov_b32_e32 v94, v87
	v_sub_f32_e32 v125, v92, v93
	v_pk_mul_f32 v[92:93], v[86:87], v[112:113]
	v_pk_mul_f32 v[86:87], v[94:95], v[112:113]
	v_add_f32_e32 v126, v92, v93
	v_sub_f32_e32 v127, v86, v87
	v_mov_b32_e32 v86, v88
	v_mov_b32_e32 v87, v76
	v_pk_mul_f32 v[92:93], v[86:87], v[102:103]
	v_or_b32_e32 v86, 0x50, v97
	v_add_u32_e32 v87, v164, v86
	v_cvt_f32_i32_e32 v94, v87
	v_add_f32_e32 v128, v92, v93
	v_mov_b32_e32 v92, v76
	v_mov_b32_e32 v93, v88
	v_mul_f32_e32 v76, 0x38800000, v94
	v_fract_f32_e32 v76, v76
	v_cos_f32_e32 v94, v76
	v_sin_f32_e32 v95, v76
	v_pk_mul_f32 v[92:93], v[92:93], v[102:103]
	v_mov_b32_e32 v76, v89
	v_sub_f32_e32 v131, v92, v93
	v_pk_mul_f32 v[92:93], v[76:77], v[94:95]
	v_or_b32_e32 v76, 0x60, v97
	v_add_u32_e32 v132, v167, v76
	v_cvt_f32_i32_e32 v114, v132
	v_mov_b32_e32 v88, v77
	v_add_f32_e32 v133, v92, v93
	v_pk_mul_f32 v[88:89], v[88:89], v[94:95]
	v_mul_f32_e32 v77, 0x38800000, v114
	v_fract_f32_e32 v77, v77
	v_cos_f32_e32 v92, v77
	v_sin_f32_e32 v93, v77
	v_or_b32_e32 v77, 0x70, v97
	v_add_u32_e32 v142, v170, v77
	v_cvt_f32_i32_e32 v114, v142
	v_sub_f32_e32 v141, v88, v89
	v_mov_b32_e32 v88, v90
	v_mov_b32_e32 v89, v78
	v_pk_mul_f32 v[88:89], v[88:89], v[92:93]
	s_nop 0
	v_add_f32_e32 v143, v88, v89
	v_mov_b32_e32 v88, v78
	v_mul_f32_e32 v78, 0x38800000, v114
	v_fract_f32_e32 v78, v78
	v_cos_f32_e32 v114, v78
	v_sin_f32_e32 v115, v78
	v_mov_b32_e32 v89, v90
	v_pk_mul_f32 v[88:89], v[88:89], v[92:93]
	v_mov_b32_e32 v78, v91
	v_mov_b32_e32 v90, v79
	v_sub_f32_e32 v144, v88, v89
	v_pk_mul_f32 v[88:89], v[78:79], v[114:115]
	v_pk_mul_f32 v[78:79], v[90:91], v[114:115]
	v_add_f32_e32 v145, v88, v89
	v_sub_f32_e32 v146, v78, v79
	v_lshl_add_u64 v[78:79], s[38:39], 0, v[100:101]
	v_lshl_add_u64 v[88:89], v[78:79], 0, s[54:55]
	v_lshl_add_u64 v[100:101], v[88:89], 0, v[108:109]
	v_cvt_pk_bf16_f32 v88, v118, v121
	v_cvt_pk_bf16_f32 v89, v124, v126
	v_cvt_pk_bf16_f32 v90, v128, v133
	v_cvt_pk_bf16_f32 v91, v143, v145
	global_store_dwordx4 v[100:101], v[88:91], off sc1
	s_nop 1
	v_cvt_pk_bf16_f32 v88, v119, v122
	v_cvt_pk_bf16_f32 v89, v125, v127
	v_cvt_pk_bf16_f32 v90, v131, v141
	v_cvt_pk_bf16_f32 v91, v144, v146
	global_store_dwordx4 v[100:101], v[88:91], off offset:256 sc1
	s_nop 1
	v_mov_b32_e32 v88, v80
	v_mov_b32_e32 v89, v68
	v_pk_mul_f32 v[88:89], v[88:89], v[104:105]
	s_nop 0
	v_add_f32_e32 v90, v88, v89
	v_mov_b32_e32 v88, v68
	v_mov_b32_e32 v89, v80
	v_pk_mul_f32 v[88:89], v[88:89], v[104:105]
	v_mov_b32_e32 v68, v81
	v_mov_b32_e32 v80, v69
	v_sub_f32_e32 v91, v88, v89
	v_pk_mul_f32 v[88:89], v[68:69], v[110:111]
; #define GAS __attribute__((address_space(1)))
; __device__ __forceinline__ v4u pack8(const f32x4 a, const f32x4 b) { v4u w; w.x = cvt_pk_bf16(a[0], a[1]); w.y = cvt_pk_bf16(a[2], a[3]); w.z = cvt_pk_bf16(b[0], b[1]); w.w = cvt_pk_bf16(b[2], b[3]); return w; }
; __device__ __forceinline__ void cs_rev(float rev, float& c, float& s) { const float f = __builtin_amdgcn_fractf(rev); c = __builtin_amdgcn_cosf(f); s = __builtin_amdgcn_sinf(f); }
; #define EPI_FENCE __builtin_amdgcn_sched_barrier(0)
;     __device__ __forceinline__ void operator()(Acc& acc, const Unit& u, LAS unsigned char*, int wr, int wc, int fr, int fq) const {
;         const int b0 = wc * 32 + 8 * fq;
; #pragma unroll
;         for (int m = 0; m < 4; ++m) { const int k1 = 64 * wr + 16 * m + fr;
; #pragma unroll
;             for (int bj = 0; bj < 2; ++bj) { const int cch = 2 * u.p1 + bj; f32x4 re[2], im[2];
; #pragma unroll
;                 for (int n = 0; n < 2; ++n)
; #pragma unroll
;                     for (int j = 0; j < 4; ++j) { const int b = b0 + 4 * n + j; float c, s; cs_rev((float)(k1 * b) * (1.f / 16384.f), c, s);
;                         const float xr = acc[0][bj][m][n][j], xi = acc[1][bj][m][n][j]; re[n][j] = xr * c + xi * s; im[n][j] = xi * c - xr * s; }
;                 bf16* p = A1 + (((size_t)k1 * 1024 + cch) * 2) * 128 + b0;
;                 *(GAS v4u*)p = pack8(re[0], re[1]); *(GAS v4u*)(p + 128) = pack8(im[0], im[1]); EPI_FENCE; } }
	v_pk_mul_f32 v[68:69], v[80:81], v[110:111]
	v_add_f32_e32 v88, v88, v89
	v_sub_f32_e32 v80, v68, v69
	v_mov_b32_e32 v68, v82
	v_mov_b32_e32 v69, v70
	v_pk_mul_f32 v[68:69], v[68:69], v[106:107]
	s_nop 0
	v_add_f32_e32 v81, v68, v69
	v_mov_b32_e32 v68, v70
	v_mov_b32_e32 v69, v82
	v_pk_mul_f32 v[68:69], v[68:69], v[106:107]
	v_mov_b32_e32 v70, v83
	v_sub_f32_e32 v89, v68, v69
	v_pk_mul_f32 v[68:69], v[70:71], v[112:113]
	v_mov_b32_e32 v82, v71
	v_add_f32_e32 v70, v68, v69
	v_pk_mul_f32 v[68:69], v[82:83], v[112:113]
	s_nop 0
	v_sub_f32_e32 v71, v68, v69
	v_mov_b32_e32 v68, v72
	v_mov_b32_e32 v69, v64
	v_pk_mul_f32 v[68:69], v[68:69], v[102:103]
	s_nop 0
	v_add_f32_e32 v82, v68, v69
	v_mov_b32_e32 v68, v64
	v_mov_b32_e32 v69, v72
	v_pk_mul_f32 v[68:69], v[68:69], v[102:103]
	v_mov_b32_e32 v64, v73
	v_mov_b32_e32 v72, v65
	v_sub_f32_e32 v83, v68, v69
	v_pk_mul_f32 v[68:69], v[64:65], v[94:95]
	v_pk_mul_f32 v[64:65], v[72:73], v[94:95]
	v_add_f32_e32 v100, v68, v69
	v_sub_f32_e32 v72, v64, v65
	v_mov_b32_e32 v64, v74
	v_mov_b32_e32 v65, v66
	v_pk_mul_f32 v[64:65], v[64:65], v[92:93]
	s_nop 0
	v_add_f32_e32 v73, v64, v65
	v_mov_b32_e32 v64, v66
	v_mov_b32_e32 v65, v74
	v_pk_mul_f32 v[64:65], v[64:65], v[92:93]
	v_mov_b32_e32 v66, v75
	v_sub_f32_e32 v92, v64, v65
	v_pk_mul_f32 v[64:65], v[66:67], v[114:115]
	v_mov_b32_e32 v74, v67
	v_add_f32_e32 v93, v64, v65
	v_pk_mul_f32 v[64:65], v[74:75], v[114:115]
	s_nop 0
	v_sub_f32_e32 v74, v64, v65
	v_lshl_add_u64 v[64:65], v[78:79], 0, s[56:57]
	v_lshl_add_u64 v[68:69], v[64:65], 0, v[108:109]
	v_cvt_pk_bf16_f32 v64, v90, v88
	v_cvt_pk_bf16_f32 v65, v81, v70
	v_cvt_pk_bf16_f32 v66, v82, v100
	v_cvt_pk_bf16_f32 v67, v73, v93
	global_store_dwordx4 v[68:69], v[64:67], off sc1
	s_nop 1
	v_cvt_pk_bf16_f32 v64, v91, v80
	v_cvt_pk_bf16_f32 v65, v89, v71
	v_cvt_pk_bf16_f32 v66, v83, v72
	v_cvt_pk_bf16_f32 v67, v92, v74
	global_store_dwordx4 v[68:69], v[64:67], off offset:256 sc1
	v_add_u32_e32 v75, v117, v97
	s_nop 0
	v_cvt_f32_i32_e32 v67, v75
	v_add_u32_e32 v74, v116, v96
	v_cvt_f32_i32_e32 v66, v74
	v_add_u32_e32 v78, v99, v98
	v_mul_f32_e32 v67, 0x38800000, v67
	v_fract_f32_e32 v67, v67
	v_cos_f32_e32 v68, v67
	v_sin_f32_e32 v69, v67
	v_mul_f32_e32 v66, 0x38800000, v66
	v_cvt_f32_i32_e32 v72, v78
	v_fract_f32_e32 v70, v66
	v_cos_f32_e32 v66, v70
	v_sin_f32_e32 v67, v70
	v_mov_b32_e32 v70, v60
	v_mov_b32_e32 v71, v52
	v_pk_mul_f32 v[70:71], v[70:71], v[68:69]
	v_add_u32_e32 v81, v120, v84
	v_add_f32_e32 v79, v70, v71
	v_mov_b32_e32 v70, v52
	v_mul_f32_e32 v52, 0x38800000, v72
	v_fract_f32_e32 v52, v52
	v_cos_f32_e32 v72, v52
	v_sin_f32_e32 v73, v52
	v_cvt_f32_i32_e32 v82, v81
	v_mov_b32_e32 v71, v60
	v_pk_mul_f32 v[70:71], v[70:71], v[68:69]
	v_mov_b32_e32 v52, v61
	v_mov_b32_e32 v60, v53
	v_sub_f32_e32 v80, v70, v71
	v_pk_mul_f32 v[70:71], v[52:53], v[72:73]
	v_pk_mul_f32 v[52:53], v[60:61], v[72:73]
	v_mul_f32_e32 v60, 0x38800000, v82
	v_fract_f32_e32 v61, v60
	v_cos_f32_e32 v60, v61
	v_sin_f32_e32 v61, v61
	v_add_u32_e32 v88, v123, v85
	v_add_f32_e32 v83, v70, v71
	v_cvt_f32_i32_e32 v70, v88
	v_sub_f32_e32 v82, v52, v53
	v_mov_b32_e32 v52, v62
	v_mov_b32_e32 v53, v54
	v_pk_mul_f32 v[52:53], v[52:53], v[60:61]
	v_add_u32_e32 v87, v87, v86
	v_add_f32_e32 v89, v52, v53
	v_mov_b32_e32 v52, v54
	v_mul_f32_e32 v54, 0x38800000, v70
	v_fract_f32_e32 v54, v54
	v_cos_f32_e32 v70, v54
	v_sin_f32_e32 v71, v54
	v_mov_b32_e32 v53, v62
	v_pk_mul_f32 v[52:53], v[52:53], v[60:61]
	v_mov_b32_e32 v54, v63
	v_sub_f32_e32 v90, v52, v53
	v_pk_mul_f32 v[52:53], v[54:55], v[70:71]
	v_mov_b32_e32 v62, v55
	v_cvt_f32_i32_e32 v54, v87
	v_add_f32_e32 v91, v52, v53
	v_pk_mul_f32 v[52:53], v[62:63], v[70:71]
	v_add_u32_e32 v95, v132, v76
	v_sub_f32_e32 v92, v52, v53
	v_mov_b32_e32 v52, v56
	v_mov_b32_e32 v53, v44
	v_pk_mul_f32 v[52:53], v[52:53], v[66:67]
	v_cvt_f32_i32_e32 v62, v95
	v_add_f32_e32 v93, v52, v53
	v_mov_b32_e32 v52, v44
	v_mul_f32_e32 v44, 0x38800000, v54
	v_fract_f32_e32 v44, v44
	v_cos_f32_e32 v54, v44
	v_sin_f32_e32 v55, v44
	v_mov_b32_e32 v53, v56
	v_pk_mul_f32 v[52:53], v[52:53], v[66:67]
	v_mov_b32_e32 v44, v57
	v_sub_f32_e32 v94, v52, v53
	v_pk_mul_f32 v[52:53], v[44:45], v[54:55]
	v_mov_b32_e32 v56, v45
	v_add_f32_e32 v99, v52, v53
	v_mul_f32_e32 v52, 0x38800000, v62
	v_fract_f32_e32 v53, v52
	v_cos_f32_e32 v52, v53
	v_sin_f32_e32 v53, v53
	v_add_u32_e32 v101, v142, v77
	v_pk_mul_f32 v[44:45], v[56:57], v[54:55]
	v_cvt_f32_i32_e32 v56, v101
	v_sub_f32_e32 v100, v44, v45
	v_mov_b32_e32 v44, v58
	v_mov_b32_e32 v45, v46
	v_pk_mul_f32 v[44:45], v[44:45], v[52:53]
	v_add_u32_e32 v64, 32, v130
	v_add_f32_e32 v102, v44, v45
	v_mov_b32_e32 v44, v46
	v_mul_f32_e32 v46, 0x38800000, v56
	v_fract_f32_e32 v46, v46
	v_cos_f32_e32 v56, v46
	v_sin_f32_e32 v57, v46
	v_mov_b32_e32 v45, v58
	v_ashrrev_i32_e32 v65, 31, v64
	v_pk_mul_f32 v[44:45], v[44:45], v[52:53]
	v_mov_b32_e32 v46, v59
	v_lshlrev_b64 v[64:65], 19, v[64:65]
	v_sub_f32_e32 v103, v44, v45
	v_pk_mul_f32 v[44:45], v[46:47], v[56:57]
	v_mov_b32_e32 v58, v47
	v_add_f32_e32 v104, v44, v45
	v_pk_mul_f32 v[44:45], v[58:59], v[56:57]
	v_lshl_add_u64 v[58:59], s[38:39], 0, v[64:65]
	v_sub_f32_e32 v105, v44, v45
	v_lshl_add_u64 v[44:45], v[58:59], 0, s[54:55]
	v_lshl_add_u64 v[62:63], v[44:45], 0, v[108:109]
	v_cvt_pk_bf16_f32 v44, v79, v83
	v_cvt_pk_bf16_f32 v45, v89, v91
	v_cvt_pk_bf16_f32 v46, v93, v99
	v_cvt_pk_bf16_f32 v47, v102, v104
	global_store_dwordx4 v[62:63], v[44:47], off sc1
	s_nop 1
	v_cvt_pk_bf16_f32 v44, v80, v82
	v_cvt_pk_bf16_f32 v45, v90, v92
	v_cvt_pk_bf16_f32 v46, v94, v100
	v_cvt_pk_bf16_f32 v47, v103, v105
	global_store_dwordx4 v[62:63], v[44:47], off offset:256 sc1
	s_nop 1
	v_mov_b32_e32 v44, v48
	v_mov_b32_e32 v45, v36
	v_pk_mul_f32 v[44:45], v[44:45], v[68:69]
	s_nop 0
	v_add_f32_e32 v46, v44, v45
	v_mov_b32_e32 v44, v36
	v_mov_b32_e32 v45, v48
	v_pk_mul_f32 v[44:45], v[44:45], v[68:69]
	v_mov_b32_e32 v36, v49
	v_mov_b32_e32 v48, v37
	v_sub_f32_e32 v47, v44, v45
	v_pk_mul_f32 v[44:45], v[36:37], v[72:73]
	v_pk_mul_f32 v[36:37], v[48:49], v[72:73]
	v_add_f32_e32 v44, v44, v45
	v_sub_f32_e32 v45, v36, v37
	v_mov_b32_e32 v36, v50
	v_mov_b32_e32 v37, v38
	v_pk_mul_f32 v[36:37], v[36:37], v[60:61]
	s_nop 0
	v_add_f32_e32 v48, v36, v37
	v_mov_b32_e32 v36, v38
	v_mov_b32_e32 v37, v50
	v_pk_mul_f32 v[36:37], v[36:37], v[60:61]
	v_mov_b32_e32 v38, v51
	v_sub_f32_e32 v49, v36, v37
	v_pk_mul_f32 v[36:37], v[38:39], v[70:71]
	v_mov_b32_e32 v50, v39
	v_add_f32_e32 v38, v36, v37
	v_pk_mul_f32 v[36:37], v[50:51], v[70:71]
	s_nop 0
	v_sub_f32_e32 v39, v36, v37
	v_mov_b32_e32 v36, v40
	v_mov_b32_e32 v37, v32
	v_pk_mul_f32 v[36:37], v[36:37], v[66:67]
	s_nop 0
	v_add_f32_e32 v50, v36, v37
	v_mov_b32_e32 v36, v32
	v_mov_b32_e32 v37, v40
	v_pk_mul_f32 v[36:37], v[36:37], v[66:67]
	v_mov_b32_e32 v32, v41
	v_mov_b32_e32 v40, v33
	v_sub_f32_e32 v51, v36, v37
	v_pk_mul_f32 v[36:37], v[32:33], v[54:55]
	v_pk_mul_f32 v[32:33], v[40:41], v[54:55]
	v_add_f32_e32 v60, v36, v37
	v_sub_f32_e32 v40, v32, v33
	v_mov_b32_e32 v32, v42
	v_mov_b32_e32 v33, v34
	v_pk_mul_f32 v[32:33], v[32:33], v[52:53]
	s_nop 0
	v_add_f32_e32 v41, v32, v33
	v_mov_b32_e32 v32, v34
	v_mov_b32_e32 v33, v42
	v_pk_mul_f32 v[32:33], v[32:33], v[52:53]
	v_mov_b32_e32 v34, v43
	v_sub_f32_e32 v52, v32, v33
	v_pk_mul_f32 v[32:33], v[34:35], v[56:57]
	v_mov_b32_e32 v42, v35
	v_add_f32_e32 v53, v32, v33
	v_pk_mul_f32 v[32:33], v[42:43], v[56:57]
	s_nop 0
	v_sub_f32_e32 v42, v32, v33
	v_lshl_add_u64 v[32:33], v[58:59], 0, s[56:57]
	v_lshl_add_u64 v[36:37], v[32:33], 0, v[108:109]
	v_cvt_pk_bf16_f32 v32, v46, v44
	v_cvt_pk_bf16_f32 v33, v48, v38
	v_cvt_pk_bf16_f32 v34, v50, v60
	v_cvt_pk_bf16_f32 v35, v41, v53
	global_store_dwordx4 v[36:37], v[32:35], off sc1
	s_nop 1
	v_cvt_pk_bf16_f32 v32, v47, v45
	v_cvt_pk_bf16_f32 v33, v49, v39
	v_cvt_pk_bf16_f32 v34, v51, v40
	v_cvt_pk_bf16_f32 v35, v52, v42
	global_store_dwordx4 v[36:37], v[32:35], off offset:256 sc1
	s_nop 1
	v_add_u32_e32 v35, v75, v97
	v_cvt_f32_i32_e32 v35, v35
	v_add_u32_e32 v34, v74, v96
	v_cvt_f32_i32_e32 v34, v34
	v_add_u32_e32 v40, v78, v98
	v_mul_f32_e32 v35, 0x38800000, v35
	v_fract_f32_e32 v35, v35
	v_cos_f32_e32 v36, v35
	v_sin_f32_e32 v37, v35
	v_mul_f32_e32 v34, 0x38800000, v34
	v_cvt_f32_i32_e32 v40, v40
	v_fract_f32_e32 v38, v34
	v_cos_f32_e32 v34, v38
	v_sin_f32_e32 v35, v38
	v_mov_b32_e32 v38, v28
	v_mov_b32_e32 v39, v20
	v_pk_mul_f32 v[38:39], v[38:39], v[36:37]
	v_add_u32_e32 v32, 48, v130
	v_add_f32_e32 v42, v38, v39
	v_mov_b32_e32 v38, v20
	v_mul_f32_e32 v20, 0x38800000, v40
	v_fract_f32_e32 v20, v20
	v_cos_f32_e32 v40, v20
	v_sin_f32_e32 v41, v20
	v_mov_b32_e32 v39, v28
	v_pk_mul_f32 v[38:39], v[38:39], v[36:37]
	v_mov_b32_e32 v20, v29
	v_sub_f32_e32 v43, v38, v39
	v_pk_mul_f32 v[38:39], v[20:21], v[40:41]
	v_add_u32_e32 v20, v81, v84
	v_cvt_f32_i32_e32 v44, v20
	v_mov_b32_e32 v28, v21
	v_pk_mul_f32 v[20:21], v[28:29], v[40:41]
	v_add_f32_e32 v45, v38, v39
	v_mul_f32_e32 v28, 0x38800000, v44
	v_fract_f32_e32 v29, v28
	v_cos_f32_e32 v28, v29
	v_sin_f32_e32 v29, v29
	v_add_u32_e32 v38, v88, v85
	v_cvt_f32_i32_e32 v38, v38
	v_sub_f32_e32 v44, v20, v21
	v_mov_b32_e32 v20, v30
	v_mov_b32_e32 v21, v22
	v_pk_mul_f32 v[20:21], v[20:21], v[28:29]
	v_ashrrev_i32_e32 v33, 31, v32
	v_add_f32_e32 v46, v20, v21
	v_mov_b32_e32 v20, v22
	v_mul_f32_e32 v22, 0x38800000, v38
	v_fract_f32_e32 v22, v22
	v_cos_f32_e32 v38, v22
	v_sin_f32_e32 v39, v22
	v_mov_b32_e32 v21, v30
	v_pk_mul_f32 v[20:21], v[20:21], v[28:29]
	v_mov_b32_e32 v22, v31
	v_sub_f32_e32 v47, v20, v21
	v_pk_mul_f32 v[20:21], v[22:23], v[38:39]
	v_add_u32_e32 v22, v87, v86
	v_mov_b32_e32 v30, v23
	v_cvt_f32_i32_e32 v22, v22
	v_add_f32_e32 v48, v20, v21
	v_pk_mul_f32 v[20:21], v[30:31], v[38:39]
	v_lshlrev_b64 v[32:33], 19, v[32:33]
	v_sub_f32_e32 v49, v20, v21
	v_mov_b32_e32 v20, v24
	v_mov_b32_e32 v21, v12
	v_pk_mul_f32 v[20:21], v[20:21], v[34:35]
	s_nop 0
	v_add_f32_e32 v50, v20, v21
	v_mov_b32_e32 v20, v12
	v_mul_f32_e32 v12, 0x38800000, v22
	v_fract_f32_e32 v12, v12
	v_cos_f32_e32 v22, v12
	v_sin_f32_e32 v23, v12
	v_mov_b32_e32 v21, v24
	v_pk_mul_f32 v[20:21], v[20:21], v[34:35]
	v_mov_b32_e32 v12, v25
	v_sub_f32_e32 v51, v20, v21
	v_pk_mul_f32 v[20:21], v[12:13], v[22:23]
	v_add_u32_e32 v12, v95, v76
	v_cvt_f32_i32_e32 v30, v12
	v_add_f32_e32 v52, v20, v21
	v_mov_b32_e32 v24, v13
	v_pk_mul_f32 v[12:13], v[24:25], v[22:23]
	v_mul_f32_e32 v20, 0x38800000, v30
	v_fract_f32_e32 v21, v20
	v_cos_f32_e32 v20, v21
	v_sin_f32_e32 v21, v21
	v_add_u32_e32 v24, v101, v77
	v_cvt_f32_i32_e32 v24, v24
	v_sub_f32_e32 v53, v12, v13
	v_mov_b32_e32 v12, v26
	v_mov_b32_e32 v13, v14
	v_pk_mul_f32 v[12:13], v[12:13], v[20:21]
	s_nop 0
	v_add_f32_e32 v54, v12, v13
	v_mov_b32_e32 v12, v14
	v_mul_f32_e32 v14, 0x38800000, v24
	v_fract_f32_e32 v14, v14
	v_cos_f32_e32 v24, v14
	v_sin_f32_e32 v25, v14
	v_mov_b32_e32 v13, v26
	v_pk_mul_f32 v[12:13], v[12:13], v[20:21]
	v_mov_b32_e32 v14, v27
	v_sub_f32_e32 v55, v12, v13
	v_pk_mul_f32 v[12:13], v[14:15], v[24:25]
	v_mov_b32_e32 v26, v15
	v_add_f32_e32 v56, v12, v13
	v_pk_mul_f32 v[12:13], v[26:27], v[24:25]
	v_lshl_add_u64 v[26:27], s[38:39], 0, v[32:33]
	v_sub_f32_e32 v57, v12, v13
	v_lshl_add_u64 v[12:13], v[26:27], 0, s[54:55]
	v_lshl_add_u64 v[30:31], v[12:13], 0, v[108:109]
	v_cvt_pk_bf16_f32 v12, v42, v45
	v_cvt_pk_bf16_f32 v13, v46, v48
	v_cvt_pk_bf16_f32 v14, v50, v52
	v_cvt_pk_bf16_f32 v15, v54, v56
	global_store_dwordx4 v[30:31], v[12:15], off sc1
	s_nop 1
	v_cvt_pk_bf16_f32 v12, v43, v44
	v_cvt_pk_bf16_f32 v13, v47, v49
	v_cvt_pk_bf16_f32 v14, v51, v53
	v_cvt_pk_bf16_f32 v15, v55, v57
	global_store_dwordx4 v[30:31], v[12:15], off offset:256 sc1
	s_nop 1
	v_mov_b32_e32 v12, v16
	v_mov_b32_e32 v13, v4
	v_pk_mul_f32 v[12:13], v[12:13], v[36:37]
	s_nop 0
	v_add_f32_e32 v14, v12, v13
	v_mov_b32_e32 v12, v4
	v_mov_b32_e32 v13, v16
	v_pk_mul_f32 v[12:13], v[12:13], v[36:37]
	v_mov_b32_e32 v4, v17
	v_mov_b32_e32 v16, v5
	v_sub_f32_e32 v15, v12, v13
	v_pk_mul_f32 v[12:13], v[4:5], v[40:41]
	v_pk_mul_f32 v[4:5], v[16:17], v[40:41]
	v_add_f32_e32 v12, v12, v13
	v_sub_f32_e32 v13, v4, v5
	v_mov_b32_e32 v4, v18
	v_mov_b32_e32 v5, v6
	v_pk_mul_f32 v[4:5], v[4:5], v[28:29]
	s_nop 0
	v_add_f32_e32 v16, v4, v5
	v_mov_b32_e32 v4, v6
	v_mov_b32_e32 v5, v18
	v_pk_mul_f32 v[4:5], v[4:5], v[28:29]
	v_mov_b32_e32 v6, v19
	v_sub_f32_e32 v17, v4, v5
	v_pk_mul_f32 v[4:5], v[6:7], v[38:39]
	v_mov_b32_e32 v18, v7
	v_add_f32_e32 v6, v4, v5
	v_pk_mul_f32 v[4:5], v[18:19], v[38:39]
	s_nop 0
	v_sub_f32_e32 v7, v4, v5
	v_mov_b32_e32 v4, v8
	v_mov_b32_e32 v5, v0
	v_pk_mul_f32 v[4:5], v[4:5], v[34:35]
	s_nop 0
	v_add_f32_e32 v18, v4, v5
	v_mov_b32_e32 v4, v0
	v_mov_b32_e32 v5, v8
	v_pk_mul_f32 v[4:5], v[4:5], v[34:35]
	v_mov_b32_e32 v0, v9
	v_mov_b32_e32 v8, v1
	v_sub_f32_e32 v19, v4, v5
	v_pk_mul_f32 v[4:5], v[0:1], v[22:23]
	v_pk_mul_f32 v[0:1], v[8:9], v[22:23]
	v_add_f32_e32 v28, v4, v5
	v_sub_f32_e32 v8, v0, v1
	v_mov_b32_e32 v0, v10
	v_mov_b32_e32 v1, v2
	v_pk_mul_f32 v[0:1], v[0:1], v[20:21]
	s_nop 0
	v_add_f32_e32 v9, v0, v1
	v_mov_b32_e32 v0, v2
	v_mov_b32_e32 v1, v10
	v_pk_mul_f32 v[0:1], v[0:1], v[20:21]
	v_mov_b32_e32 v2, v11
	v_sub_f32_e32 v20, v0, v1
	v_pk_mul_f32 v[0:1], v[2:3], v[24:25]
	v_mov_b32_e32 v10, v3
	v_add_f32_e32 v21, v0, v1
	v_pk_mul_f32 v[0:1], v[10:11], v[24:25]
	s_nop 0
	v_sub_f32_e32 v10, v0, v1
	v_lshl_add_u64 v[0:1], v[26:27], 0, s[56:57]
	v_lshl_add_u64 v[4:5], v[0:1], 0, v[108:109]
	v_cvt_pk_bf16_f32 v0, v14, v12
	v_cvt_pk_bf16_f32 v1, v16, v6
	v_cvt_pk_bf16_f32 v2, v18, v28
	v_cvt_pk_bf16_f32 v3, v9, v21
	global_store_dwordx4 v[4:5], v[0:3], off sc1
	s_nop 1
	v_cvt_pk_bf16_f32 v0, v15, v13
	v_cvt_pk_bf16_f32 v1, v17, v7
	v_cvt_pk_bf16_f32 v2, v19, v8
	v_cvt_pk_bf16_f32 v3, v20, v10
	global_store_dwordx4 v[4:5], v[0:3], off offset:256 sc1
	s_andn2_b64 vcc, exec, s[52:53]
	s_mov_b64 s[52:53], -1
	s_cbranch_vccnz .LBB0_517
	s_andn2_b64 vcc, exec, s[36:37]
	s_cbranch_vccnz .LBB0_516
	s_barrier
	s_branch .LBB0_516

.LBB0_552:
	s_ashr_i32 s55, s54, 31
	s_lshl_b64 s[56:57], s[54:55], 2
	s_add_u32 s58, s14, s56
	s_addc_u32 s59, s15, s57
	s_add_u32 s56, s30, s56
	v_mov_b32_e32 v128, v135
	v_mov_b32_e32 v130, v136
	s_addc_u32 s57, s31, s57
	global_load_dword v141, v129, s[58:59]
	global_load_dword v150, v129, s[56:57]
	v_lshl_add_u32 v130, v130, 3, s22
	v_add_u32_e32 v132, s21, v128
	v_sub_u32_e32 v128, v132, v130
	v_or_b32_e32 v148, 1, v130
	v_cvt_f32_i32_e32 v149, v128
	v_sub_u32_e32 v128, v132, v148
	v_cvt_f32_i32_e32 v157, v128
	s_lshl_b32 s41, s52, 8
	s_lshl_b64 s[54:55], s[54:55], 14
	s_ashr_i32 s53, s41, 31
	v_or_b32_e32 v146, 2, v130
	s_add_u32 s52, s54, s41
	v_ashrrev_i32_e32 v133, 31, v132
	v_sub_u32_e32 v151, v132, v146
	s_addc_u32 s53, s55, s53
	v_cmp_lt_i32_e32 vcc, v132, v130
	v_or_b32_e32 v142, 4, v130
	v_or_b32_e32 v143, 5, v130
	v_cvt_f32_i32_e32 v158, v151
	v_or_b32_e32 v147, 3, v130
	v_sub_u32_e32 v153, v132, v142
	v_sub_u32_e32 v154, v132, v143
	v_or_b32_e32 v144, 6, v130
	v_or_b32_e32 v145, 7, v130
	v_sub_u32_e32 v152, v132, v147
	v_cvt_f32_i32_e32 v153, v153
	v_cvt_f32_i32_e32 v154, v154
	v_sub_u32_e32 v155, v132, v144
	v_sub_u32_e32 v156, v132, v145
	v_cvt_f32_i32_e32 v152, v152
	v_cvt_f32_i32_e32 v155, v155
	v_cvt_f32_i32_e32 v156, v156
	v_ashrrev_i32_e32 v131, 31, v130
	s_waitcnt vmcnt(0)
	v_mul_f32_e32 v128, 0x3fb8aa3b, v141
	v_mul_f32_e32 v141, 0x3fb8aa3b, v150
	v_exp_f32_e32 v128, v128
	v_exp_f32_e32 v141, v141
	v_lshl_add_u64 v[150:151], s[52:53], 0, v[132:133]
	v_cndmask_b32_e64 v133, -v128, v141, vcc
	v_cmp_gt_i32_e32 vcc, v132, v130
	v_mul_f32_e32 v133, v133, v149
	v_mul_f32_e32 v133, 0x3fb8aa3b, v133
	v_cndmask_b32_e64 v159, v141, -v128, vcc
	v_cmp_lt_i32_e32 vcc, v132, v146
	v_mul_f32_e32 v157, v159, v157
	v_mul_f32_e32 v157, 0x3fb8aa3b, v157
	v_cndmask_b32_e64 v160, -v128, v141, vcc
	v_cmp_lt_i32_e32 vcc, v132, v147
	v_mul_f32_e32 v158, v160, v158
	v_mul_f32_e32 v158, 0x3fb8aa3b, v158
	v_cndmask_b32_e64 v161, -v128, v141, vcc
	v_cmp_lt_i32_e32 vcc, v132, v142
	v_mul_f32_e32 v152, v161, v152
	v_mul_f32_e32 v152, 0x3fb8aa3b, v152
	v_cndmask_b32_e64 v162, -v128, v141, vcc
	v_cmp_lt_i32_e32 vcc, v132, v143
	v_mul_f32_e32 v153, v162, v153
	v_mul_f32_e32 v153, 0x3fb8aa3b, v153
	v_cndmask_b32_e64 v163, -v128, v141, vcc
	v_cmp_lt_i32_e32 vcc, v132, v144
	v_mul_f32_e32 v154, v163, v154
	v_mul_f32_e32 v154, 0x3fb8aa3b, v154
	v_cndmask_b32_e64 v164, -v128, v141, vcc
	v_cmp_lt_i32_e32 vcc, v132, v145
	v_mul_f32_e32 v155, v164, v155
	v_exp_f32_e32 v133, v133
	v_cndmask_b32_e64 v165, -v128, v141, vcc
	v_mul_f32_e32 v156, v165, v156
	v_exp_f32_e32 v157, v157
	v_exp_f32_e32 v158, v158
	v_exp_f32_e32 v153, v153
	v_exp_f32_e32 v154, v154
	v_mul_f32_e32 v155, 0x3fb8aa3b, v155
	v_mul_f32_e32 v156, 0x3fb8aa3b, v156
	v_exp_f32_e32 v152, v152
	v_exp_f32_e32 v155, v155
	v_exp_f32_e32 v156, v156
	v_mul_f32_e32 v124, v124, v133
	v_mul_f32_e32 v125, v125, v157
	v_mul_f32_e32 v126, v126, v158
	v_mul_f32_e32 v120, v120, v153
	v_mul_f32_e32 v121, v121, v154
	v_mul_f32_e32 v127, v127, v152
	v_cvt_pk_bf16_f32 v124, v124, v125
	v_cvt_pk_bf16_f32 v125, v126, v127
	v_cvt_pk_bf16_f32 v126, v120, v121
	v_mov_b64_e32 v[120:121], s[6:7]
	v_mul_f32_e32 v122, v122, v155
	v_mul_f32_e32 v123, v123, v156
	v_mad_u64_u32 v[152:153], s[54:55], v150, s77, v[120:121]
	v_cvt_pk_bf16_f32 v127, v122, v123
	v_mad_i32_i24 v153, v151, s77, v153
	v_lshlrev_b64 v[122:123], 1, v[130:131]
	v_lshl_add_u64 v[150:151], v[152:153], 0, v[122:123]
	global_store_dwordx4 v[150:151], v[124:127], off sc1
	s_nop 1
	v_add_u32_e32 v125, 0x80, v130
	v_sub_u32_e32 v124, v132, v125
	v_cvt_f32_i32_e32 v124, v124
	v_cmp_lt_i32_e32 vcc, v132, v125
	s_nop 1
	v_cndmask_b32_e64 v126, -v128, v141, vcc
	v_mul_f32_e32 v124, v126, v124
	v_mul_f32_e32 v124, 0x3fb8aa3b, v124
	v_exp_f32_e32 v126, v124
	v_add_u32_e32 v124, 0x81, v130
	v_sub_u32_e32 v127, v132, v124
	v_cvt_f32_i32_e32 v127, v127
	v_cmp_lt_i32_e32 vcc, v132, v124
	v_mul_f32_e32 v131, v116, v126
	s_nop 0
	v_cndmask_b32_e64 v116, -v128, v141, vcc
	v_mul_f32_e32 v116, v116, v127
	v_mul_f32_e32 v116, 0x3fb8aa3b, v116
	v_exp_f32_e32 v126, v116
	v_add_u32_e32 v116, 0x82, v130
	v_sub_u32_e32 v127, v132, v116
	v_cvt_f32_i32_e32 v127, v127
	v_cmp_lt_i32_e32 vcc, v132, v116
	v_mul_f32_e32 v133, v117, v126
	s_nop 0
	v_cndmask_b32_e64 v117, -v128, v141, vcc
	v_mul_f32_e32 v117, v117, v127
	v_mul_f32_e32 v117, 0x3fb8aa3b, v117
	v_exp_f32_e32 v126, v117
	v_add_u32_e32 v117, 0x83, v130
	v_sub_u32_e32 v127, v132, v117
	v_cvt_f32_i32_e32 v127, v127
	v_cmp_lt_i32_e32 vcc, v132, v117
	v_mul_f32_e32 v152, v118, v126
	s_nop 0
	v_cndmask_b32_e64 v118, -v128, v141, vcc
	v_mul_f32_e32 v118, v118, v127
	v_mul_f32_e32 v118, 0x3fb8aa3b, v118
	v_exp_f32_e32 v126, v118
	v_add_u32_e32 v118, 0x84, v130
	v_sub_u32_e32 v127, v132, v118
	v_cvt_f32_i32_e32 v127, v127
	v_cmp_lt_i32_e32 vcc, v132, v118
	v_mul_f32_e32 v153, v119, v126
	s_nop 0
	v_cndmask_b32_e64 v119, -v128, v141, vcc
	v_mul_f32_e32 v119, v119, v127
	v_mul_f32_e32 v126, 0x3fb8aa3b, v119
	v_add_u32_e32 v119, 0x85, v130
	v_sub_u32_e32 v127, v132, v119
	v_cvt_f32_i32_e32 v127, v127
	v_cmp_lt_i32_e32 vcc, v132, v119
	v_exp_f32_e32 v154, v126
	s_nop 0
	v_cndmask_b32_e64 v126, -v128, v141, vcc
	v_mul_f32_e32 v126, v126, v127
	v_mul_f32_e32 v127, 0x3fb8aa3b, v126
	v_add_u32_e32 v126, 0x86, v130
	v_sub_u32_e32 v155, v132, v126
	v_cvt_f32_i32_e32 v155, v155
	v_cmp_lt_i32_e32 vcc, v132, v126
	v_exp_f32_e32 v156, v127
	v_mul_f32_e32 v154, v112, v154
	v_cndmask_b32_e64 v127, -v128, v141, vcc
	v_mul_f32_e32 v127, v127, v155
	v_mul_f32_e32 v155, 0x3fb8aa3b, v127
	v_add_u32_e32 v127, 0x87, v130
	v_sub_u32_e32 v157, v132, v127
	v_cvt_f32_i32_e32 v157, v157
	v_cmp_lt_i32_e32 vcc, v132, v127
	v_exp_f32_e32 v155, v155
	v_mul_f32_e32 v156, v113, v156
	v_cndmask_b32_e64 v158, -v128, v141, vcc
	v_mul_f32_e32 v157, v158, v157
	v_mul_f32_e32 v157, 0x3fb8aa3b, v157
	v_exp_f32_e32 v157, v157
	v_mul_f32_e32 v155, v114, v155
	v_cvt_pk_bf16_f32 v112, v131, v133
	v_cvt_pk_bf16_f32 v113, v152, v153
	v_mul_f32_e32 v115, v115, v157
	v_cvt_pk_bf16_f32 v114, v154, v156
	v_cvt_pk_bf16_f32 v115, v155, v115
	global_store_dwordx4 v[150:151], v[112:115], off offset:256 sc1
	s_nop 1
	v_add_u32_e32 v112, 16, v132
	v_sub_u32_e32 v114, v112, v130
	v_cvt_f32_i32_e32 v131, v114
	v_ashrrev_i32_e32 v113, 31, v112
	v_cmp_lt_i32_e32 vcc, v112, v130
	v_lshl_add_u64 v[114:115], s[52:53], 0, v[112:113]
	s_nop 0
	v_cndmask_b32_e64 v113, -v128, v141, vcc
	v_mul_f32_e32 v113, v113, v131
	v_sub_u32_e32 v131, v112, v148
	v_cvt_f32_i32_e32 v131, v131
	v_mul_f32_e32 v113, 0x3fb8aa3b, v113
	v_exp_f32_e32 v113, v113
	v_cmp_gt_i32_e32 vcc, v112, v130
	v_mul_f32_e32 v108, v108, v113
	s_nop 0
	v_cndmask_b32_e64 v133, v141, -v128, vcc
	v_mul_f32_e32 v131, v133, v131
	v_mul_f32_e32 v131, 0x3fb8aa3b, v131
	v_exp_f32_e32 v131, v131
	v_sub_u32_e32 v113, v112, v146
	v_cvt_f32_i32_e32 v113, v113
	v_cmp_lt_i32_e32 vcc, v112, v146
	v_mul_f32_e32 v109, v109, v131
	s_nop 0
	v_cndmask_b32_e64 v131, -v128, v141, vcc
	v_mul_f32_e32 v113, v131, v113
	v_sub_u32_e32 v131, v112, v147
	v_cvt_f32_i32_e32 v131, v131
	v_mul_f32_e32 v113, 0x3fb8aa3b, v113
	v_exp_f32_e32 v113, v113
	v_cmp_lt_i32_e32 vcc, v112, v147
	v_mul_f32_e32 v110, v110, v113
	s_nop 0
	v_cndmask_b32_e64 v133, -v128, v141, vcc
	v_mul_f32_e32 v131, v133, v131
	v_mul_f32_e32 v131, 0x3fb8aa3b, v131
	v_exp_f32_e32 v131, v131
	v_sub_u32_e32 v113, v112, v142
	v_cvt_f32_i32_e32 v113, v113
	v_cmp_lt_i32_e32 vcc, v112, v142
	v_mul_f32_e32 v111, v111, v131
	s_nop 0
	v_cndmask_b32_e64 v131, -v128, v141, vcc
	v_mul_f32_e32 v113, v131, v113
	v_sub_u32_e32 v131, v112, v143
	v_cvt_f32_i32_e32 v131, v131
	v_cmp_lt_i32_e32 vcc, v112, v143
	v_mul_f32_e32 v113, 0x3fb8aa3b, v113
	v_exp_f32_e32 v113, v113
	v_cndmask_b32_e64 v133, -v128, v141, vcc
	v_mul_f32_e32 v131, v133, v131
	v_sub_u32_e32 v133, v112, v144
	v_cvt_f32_i32_e32 v133, v133
	v_cmp_lt_i32_e32 vcc, v112, v144
	v_mul_f32_e32 v131, 0x3fb8aa3b, v131
	v_exp_f32_e32 v131, v131
	v_cndmask_b32_e64 v150, -v128, v141, vcc
	v_mul_f32_e32 v133, v150, v133
	v_sub_u32_e32 v150, v112, v145
	v_cvt_f32_i32_e32 v150, v150
	v_cmp_lt_i32_e32 vcc, v112, v145
	v_mul_f32_e32 v133, 0x3fb8aa3b, v133
	v_exp_f32_e32 v133, v133
	v_cndmask_b32_e64 v151, -v128, v141, vcc
	v_mul_f32_e32 v150, v151, v150
	v_mul_f32_e32 v150, 0x3fb8aa3b, v150
	v_exp_f32_e32 v150, v150
	v_mul_f32_e32 v113, v104, v113
	v_cvt_pk_bf16_f32 v104, v108, v109
	v_mad_u64_u32 v[108:109], s[54:55], v114, s77, v[120:121]
	v_mad_i32_i24 v109, v115, s77, v109
	v_mul_f32_e32 v107, v107, v150
	v_lshl_add_u64 v[108:109], v[108:109], 0, v[122:123]
	v_mul_f32_e32 v131, v105, v131
	v_mul_f32_e32 v133, v106, v133
	v_cvt_pk_bf16_f32 v105, v110, v111
	v_cvt_pk_bf16_f32 v106, v113, v131
	v_cvt_pk_bf16_f32 v107, v133, v107
	global_store_dwordx4 v[108:109], v[104:107], off sc1
	s_nop 1
	v_sub_u32_e32 v104, v112, v125
	v_cvt_f32_i32_e32 v104, v104
	v_cmp_lt_i32_e32 vcc, v112, v125
	v_sub_u32_e32 v106, v112, v124
	s_nop 0
	v_cndmask_b32_e64 v105, -v128, v141, vcc
	v_mul_f32_e32 v104, v105, v104
	v_cvt_f32_i32_e32 v105, v106
	v_mul_f32_e32 v104, 0x3fb8aa3b, v104
	v_exp_f32_e32 v104, v104
	v_cmp_lt_i32_e32 vcc, v112, v124
	v_mul_f32_e32 v100, v100, v104
	s_nop 0
	v_cndmask_b32_e64 v106, -v128, v141, vcc
	v_mul_f32_e32 v105, v106, v105
	v_mul_f32_e32 v105, 0x3fb8aa3b, v105
	v_exp_f32_e32 v105, v105
	v_sub_u32_e32 v104, v112, v116
	v_cvt_f32_i32_e32 v104, v104
	v_cmp_lt_i32_e32 vcc, v112, v116
	v_mul_f32_e32 v101, v101, v105
	s_nop 0
	v_cndmask_b32_e64 v105, -v128, v141, vcc
	v_mul_f32_e32 v104, v105, v104
	v_sub_u32_e32 v105, v112, v117
	v_cvt_f32_i32_e32 v105, v105
	v_mul_f32_e32 v104, 0x3fb8aa3b, v104
	v_exp_f32_e32 v104, v104
	v_cmp_lt_i32_e32 vcc, v112, v117
	v_mul_f32_e32 v102, v102, v104
	s_nop 0
	v_cndmask_b32_e64 v106, -v128, v141, vcc
	v_mul_f32_e32 v105, v106, v105
	v_mul_f32_e32 v105, 0x3fb8aa3b, v105
	v_exp_f32_e32 v105, v105
	v_sub_u32_e32 v104, v112, v118
	v_cvt_f32_i32_e32 v104, v104
	v_cmp_lt_i32_e32 vcc, v112, v118
	v_mul_f32_e32 v103, v103, v105
	s_nop 0
	v_cndmask_b32_e64 v105, -v128, v141, vcc
	v_mul_f32_e32 v104, v105, v104
	v_sub_u32_e32 v105, v112, v119
	v_cvt_f32_i32_e32 v105, v105
	v_cmp_lt_i32_e32 vcc, v112, v119
	v_mul_f32_e32 v104, 0x3fb8aa3b, v104
	v_exp_f32_e32 v104, v104
	v_cndmask_b32_e64 v106, -v128, v141, vcc
	v_mul_f32_e32 v105, v106, v105
	v_sub_u32_e32 v106, v112, v126
	v_cvt_f32_i32_e32 v106, v106
	v_cmp_lt_i32_e32 vcc, v112, v126
	v_mul_f32_e32 v105, 0x3fb8aa3b, v105
	v_exp_f32_e32 v105, v105
	v_cndmask_b32_e64 v107, -v128, v141, vcc
	v_mul_f32_e32 v106, v107, v106
	v_sub_u32_e32 v107, v112, v127
	v_cvt_f32_i32_e32 v107, v107
	v_cmp_lt_i32_e32 vcc, v112, v127
	v_mul_f32_e32 v106, 0x3fb8aa3b, v106
	v_exp_f32_e32 v106, v106
	v_cndmask_b32_e64 v110, -v128, v141, vcc
	v_mul_f32_e32 v107, v110, v107
	v_mul_f32_e32 v107, 0x3fb8aa3b, v107
	v_exp_f32_e32 v107, v107
	v_mul_f32_e32 v104, v96, v104
	v_mul_f32_e32 v105, v97, v105
	v_mul_f32_e32 v106, v98, v106
	v_mul_f32_e32 v99, v99, v107
	v_cvt_pk_bf16_f32 v96, v100, v101
	v_cvt_pk_bf16_f32 v97, v102, v103
	v_cvt_pk_bf16_f32 v98, v104, v105
	v_cvt_pk_bf16_f32 v99, v106, v99
	global_store_dwordx4 v[108:109], v[96:99], off offset:256 sc1
	s_nop 1
	v_add_u32_e32 v96, 32, v132
	v_sub_u32_e32 v98, v96, v130
	v_cvt_f32_i32_e32 v100, v98
	v_ashrrev_i32_e32 v97, 31, v96
	v_cmp_lt_i32_e32 vcc, v96, v130
	v_lshl_add_u64 v[98:99], s[52:53], 0, v[96:97]
	s_nop 0
	v_cndmask_b32_e64 v97, -v128, v141, vcc
	v_mul_f32_e32 v97, v97, v100
	v_sub_u32_e32 v100, v96, v148
	v_cvt_f32_i32_e32 v100, v100
	v_mul_f32_e32 v97, 0x3fb8aa3b, v97
	v_exp_f32_e32 v97, v97
	v_cmp_gt_i32_e32 vcc, v96, v130
	v_mul_f32_e32 v92, v92, v97
	s_nop 0
	v_cndmask_b32_e64 v101, v141, -v128, vcc
	v_mul_f32_e32 v100, v101, v100
	v_mul_f32_e32 v100, 0x3fb8aa3b, v100
	v_exp_f32_e32 v100, v100
	v_sub_u32_e32 v97, v96, v146
	v_cvt_f32_i32_e32 v97, v97
	v_cmp_lt_i32_e32 vcc, v96, v146
	v_mul_f32_e32 v93, v93, v100
	s_nop 0
	v_cndmask_b32_e64 v100, -v128, v141, vcc
	v_mul_f32_e32 v97, v100, v97
	v_sub_u32_e32 v100, v96, v147
	v_cvt_f32_i32_e32 v100, v100
	v_mul_f32_e32 v97, 0x3fb8aa3b, v97
	v_exp_f32_e32 v97, v97
	v_cmp_lt_i32_e32 vcc, v96, v147
	v_mul_f32_e32 v94, v94, v97
	s_nop 0
	v_cndmask_b32_e64 v101, -v128, v141, vcc
	v_mul_f32_e32 v100, v101, v100
	v_mul_f32_e32 v100, 0x3fb8aa3b, v100
	v_exp_f32_e32 v100, v100
	v_sub_u32_e32 v97, v96, v142
	v_cvt_f32_i32_e32 v97, v97
	v_cmp_lt_i32_e32 vcc, v96, v142
	v_mul_f32_e32 v95, v95, v100
	s_nop 0
	v_cndmask_b32_e64 v100, -v128, v141, vcc
	v_mul_f32_e32 v97, v100, v97
	v_sub_u32_e32 v100, v96, v143
	v_cvt_f32_i32_e32 v100, v100
	v_cmp_lt_i32_e32 vcc, v96, v143
	v_mul_f32_e32 v97, 0x3fb8aa3b, v97
	v_exp_f32_e32 v97, v97
	v_cndmask_b32_e64 v101, -v128, v141, vcc
	v_mul_f32_e32 v100, v101, v100
	v_sub_u32_e32 v101, v96, v144
	v_cvt_f32_i32_e32 v101, v101
	v_cmp_lt_i32_e32 vcc, v96, v144
	v_mul_f32_e32 v100, 0x3fb8aa3b, v100
	v_exp_f32_e32 v100, v100
	v_cndmask_b32_e64 v102, -v128, v141, vcc
	v_mul_f32_e32 v101, v102, v101
	v_sub_u32_e32 v102, v96, v145
	v_cvt_f32_i32_e32 v102, v102
	v_cmp_lt_i32_e32 vcc, v96, v145
	v_mul_f32_e32 v101, 0x3fb8aa3b, v101
	v_exp_f32_e32 v101, v101
	v_cndmask_b32_e64 v103, -v128, v141, vcc
	v_mul_f32_e32 v102, v103, v102
	v_mul_f32_e32 v102, 0x3fb8aa3b, v102
	v_exp_f32_e32 v102, v102
	v_mul_f32_e32 v97, v88, v97
	v_cvt_pk_bf16_f32 v88, v92, v93
	v_mad_u64_u32 v[92:93], s[54:55], v98, s77, v[120:121]
	v_mad_i32_i24 v93, v99, s77, v93
	v_mul_f32_e32 v91, v91, v102
	v_lshl_add_u64 v[92:93], v[92:93], 0, v[122:123]
	v_mul_f32_e32 v100, v89, v100
	v_mul_f32_e32 v101, v90, v101
	v_cvt_pk_bf16_f32 v89, v94, v95
	v_cvt_pk_bf16_f32 v90, v97, v100
	v_cvt_pk_bf16_f32 v91, v101, v91
	global_store_dwordx4 v[92:93], v[88:91], off sc1
	s_nop 1
	v_sub_u32_e32 v88, v96, v125
	v_cvt_f32_i32_e32 v88, v88
	v_cmp_lt_i32_e32 vcc, v96, v125
	v_sub_u32_e32 v90, v96, v124
	s_nop 0
	v_cndmask_b32_e64 v89, -v128, v141, vcc
	v_mul_f32_e32 v88, v89, v88
	v_cvt_f32_i32_e32 v89, v90
	v_mul_f32_e32 v88, 0x3fb8aa3b, v88
	v_exp_f32_e32 v88, v88
	v_cmp_lt_i32_e32 vcc, v96, v124
	v_mul_f32_e32 v84, v84, v88
	s_nop 0
	v_cndmask_b32_e64 v90, -v128, v141, vcc
	v_mul_f32_e32 v89, v90, v89
	v_mul_f32_e32 v89, 0x3fb8aa3b, v89
	v_exp_f32_e32 v89, v89
	v_sub_u32_e32 v88, v96, v116
	v_cvt_f32_i32_e32 v88, v88
	v_cmp_lt_i32_e32 vcc, v96, v116
	v_mul_f32_e32 v85, v85, v89
	s_nop 0
	v_cndmask_b32_e64 v89, -v128, v141, vcc
	v_mul_f32_e32 v88, v89, v88
	v_sub_u32_e32 v89, v96, v117
	v_cvt_f32_i32_e32 v89, v89
	v_mul_f32_e32 v88, 0x3fb8aa3b, v88
	v_exp_f32_e32 v88, v88
	v_cmp_lt_i32_e32 vcc, v96, v117
	v_mul_f32_e32 v86, v86, v88
	s_nop 0
	v_cndmask_b32_e64 v90, -v128, v141, vcc
	v_mul_f32_e32 v89, v90, v89
	v_mul_f32_e32 v89, 0x3fb8aa3b, v89
	v_exp_f32_e32 v89, v89
	v_sub_u32_e32 v88, v96, v118
	v_cvt_f32_i32_e32 v88, v88
	v_cmp_lt_i32_e32 vcc, v96, v118
	v_mul_f32_e32 v87, v87, v89
	s_nop 0
	v_cndmask_b32_e64 v89, -v128, v141, vcc
	v_mul_f32_e32 v88, v89, v88
	v_sub_u32_e32 v89, v96, v119
	v_cvt_f32_i32_e32 v89, v89
	v_cmp_lt_i32_e32 vcc, v96, v119
	v_mul_f32_e32 v88, 0x3fb8aa3b, v88
	v_exp_f32_e32 v88, v88
	v_cndmask_b32_e64 v90, -v128, v141, vcc
	v_mul_f32_e32 v89, v90, v89
	v_sub_u32_e32 v90, v96, v126
	v_cvt_f32_i32_e32 v90, v90
	v_cmp_lt_i32_e32 vcc, v96, v126
	v_mul_f32_e32 v89, 0x3fb8aa3b, v89
	v_exp_f32_e32 v89, v89
	v_cndmask_b32_e64 v91, -v128, v141, vcc
	v_mul_f32_e32 v90, v91, v90
	v_sub_u32_e32 v91, v96, v127
	v_cvt_f32_i32_e32 v91, v91
	v_cmp_lt_i32_e32 vcc, v96, v127
	v_mul_f32_e32 v90, 0x3fb8aa3b, v90
	v_exp_f32_e32 v90, v90
	v_cndmask_b32_e64 v94, -v128, v141, vcc
	v_mul_f32_e32 v91, v94, v91
	v_mul_f32_e32 v91, 0x3fb8aa3b, v91
	v_exp_f32_e32 v91, v91
	v_mul_f32_e32 v88, v80, v88
	v_mul_f32_e32 v89, v81, v89
	v_mul_f32_e32 v90, v82, v90
	v_mul_f32_e32 v83, v83, v91
	v_cvt_pk_bf16_f32 v80, v84, v85
	v_cvt_pk_bf16_f32 v81, v86, v87
	v_cvt_pk_bf16_f32 v82, v88, v89
	v_cvt_pk_bf16_f32 v83, v90, v83
	global_store_dwordx4 v[92:93], v[80:83], off offset:256 sc1
	s_nop 1
	v_add_u32_e32 v80, 48, v132
	v_sub_u32_e32 v82, v80, v130
	v_cvt_f32_i32_e32 v84, v82
	v_ashrrev_i32_e32 v81, 31, v80
	v_cmp_lt_i32_e32 vcc, v80, v130
	v_lshl_add_u64 v[82:83], s[52:53], 0, v[80:81]
	s_nop 0
	v_cndmask_b32_e64 v81, -v128, v141, vcc
	v_mul_f32_e32 v81, v81, v84
	v_sub_u32_e32 v84, v80, v148
	v_cvt_f32_i32_e32 v84, v84
	v_mul_f32_e32 v81, 0x3fb8aa3b, v81
	v_exp_f32_e32 v81, v81
	v_cmp_gt_i32_e32 vcc, v80, v130
	v_mul_f32_e32 v76, v76, v81
	s_nop 0
	v_cndmask_b32_e64 v85, v141, -v128, vcc
	v_mul_f32_e32 v84, v85, v84
	v_mul_f32_e32 v84, 0x3fb8aa3b, v84
	v_exp_f32_e32 v84, v84
	v_sub_u32_e32 v81, v80, v146
	v_cvt_f32_i32_e32 v81, v81
	v_cmp_lt_i32_e32 vcc, v80, v146
	v_mul_f32_e32 v77, v77, v84
	s_nop 0
	v_cndmask_b32_e64 v84, -v128, v141, vcc
	v_mul_f32_e32 v81, v84, v81
	v_sub_u32_e32 v84, v80, v147
	v_cvt_f32_i32_e32 v84, v84
	v_mul_f32_e32 v81, 0x3fb8aa3b, v81
	v_exp_f32_e32 v81, v81
	v_cmp_lt_i32_e32 vcc, v80, v147
	v_mul_f32_e32 v78, v78, v81
	s_nop 0
	v_cndmask_b32_e64 v85, -v128, v141, vcc
	v_mul_f32_e32 v84, v85, v84
	v_mul_f32_e32 v84, 0x3fb8aa3b, v84
	v_exp_f32_e32 v84, v84
	v_sub_u32_e32 v81, v80, v142
	v_cvt_f32_i32_e32 v81, v81
	v_cmp_lt_i32_e32 vcc, v80, v142
	v_mul_f32_e32 v79, v79, v84
	s_nop 0
	v_cndmask_b32_e64 v84, -v128, v141, vcc
	v_mul_f32_e32 v81, v84, v81
	v_sub_u32_e32 v84, v80, v143
	v_cvt_f32_i32_e32 v84, v84
	v_cmp_lt_i32_e32 vcc, v80, v143
	v_mul_f32_e32 v81, 0x3fb8aa3b, v81
	v_exp_f32_e32 v81, v81
	v_cndmask_b32_e64 v85, -v128, v141, vcc
	v_mul_f32_e32 v84, v85, v84
	v_sub_u32_e32 v85, v80, v144
	v_cvt_f32_i32_e32 v85, v85
	v_cmp_lt_i32_e32 vcc, v80, v144
	v_mul_f32_e32 v84, 0x3fb8aa3b, v84
	v_exp_f32_e32 v84, v84
	v_cndmask_b32_e64 v86, -v128, v141, vcc
	v_mul_f32_e32 v85, v86, v85
	v_sub_u32_e32 v86, v80, v145
	v_cvt_f32_i32_e32 v86, v86
	v_cmp_lt_i32_e32 vcc, v80, v145
	v_mul_f32_e32 v85, 0x3fb8aa3b, v85
	v_exp_f32_e32 v85, v85
	v_cndmask_b32_e64 v87, -v128, v141, vcc
	v_mul_f32_e32 v86, v87, v86
	v_mul_f32_e32 v86, 0x3fb8aa3b, v86
	v_exp_f32_e32 v86, v86
	v_mul_f32_e32 v81, v72, v81
	v_cvt_pk_bf16_f32 v72, v76, v77
	v_mad_u64_u32 v[76:77], s[54:55], v82, s77, v[120:121]
	v_mad_i32_i24 v77, v83, s77, v77
	v_mul_f32_e32 v75, v75, v86
	v_lshl_add_u64 v[76:77], v[76:77], 0, v[122:123]
	v_mul_f32_e32 v84, v73, v84
	v_mul_f32_e32 v85, v74, v85
	v_cvt_pk_bf16_f32 v73, v78, v79
	v_cvt_pk_bf16_f32 v74, v81, v84
	v_cvt_pk_bf16_f32 v75, v85, v75
	global_store_dwordx4 v[76:77], v[72:75], off sc1
	s_nop 1
	v_sub_u32_e32 v72, v80, v125
	v_cvt_f32_i32_e32 v72, v72
	v_cmp_lt_i32_e32 vcc, v80, v125
	v_sub_u32_e32 v74, v80, v124
	s_nop 0
	v_cndmask_b32_e64 v73, -v128, v141, vcc
	v_mul_f32_e32 v72, v73, v72
	v_cvt_f32_i32_e32 v73, v74
	v_mul_f32_e32 v72, 0x3fb8aa3b, v72
	v_exp_f32_e32 v72, v72
	v_cmp_lt_i32_e32 vcc, v80, v124
	v_mul_f32_e32 v68, v68, v72
	s_nop 0
	v_cndmask_b32_e64 v74, -v128, v141, vcc
	v_mul_f32_e32 v73, v74, v73
	v_mul_f32_e32 v73, 0x3fb8aa3b, v73
	v_exp_f32_e32 v73, v73
	v_sub_u32_e32 v72, v80, v116
	v_cvt_f32_i32_e32 v72, v72
	v_cmp_lt_i32_e32 vcc, v80, v116
	v_mul_f32_e32 v69, v69, v73
	s_nop 0
	v_cndmask_b32_e64 v73, -v128, v141, vcc
	v_mul_f32_e32 v72, v73, v72
	v_sub_u32_e32 v73, v80, v117
	v_cvt_f32_i32_e32 v73, v73
	v_mul_f32_e32 v72, 0x3fb8aa3b, v72
	v_exp_f32_e32 v72, v72
	v_cmp_lt_i32_e32 vcc, v80, v117
	v_mul_f32_e32 v70, v70, v72
	s_nop 0
	v_cndmask_b32_e64 v74, -v128, v141, vcc
	v_mul_f32_e32 v73, v74, v73
	v_mul_f32_e32 v73, 0x3fb8aa3b, v73
	v_exp_f32_e32 v73, v73
	v_sub_u32_e32 v72, v80, v118
	v_cvt_f32_i32_e32 v72, v72
	v_cmp_lt_i32_e32 vcc, v80, v118
	v_mul_f32_e32 v71, v71, v73
	s_nop 0
	v_cndmask_b32_e64 v73, -v128, v141, vcc
	v_mul_f32_e32 v72, v73, v72
	v_sub_u32_e32 v73, v80, v119
	v_cvt_f32_i32_e32 v73, v73
	v_cmp_lt_i32_e32 vcc, v80, v119
	v_mul_f32_e32 v72, 0x3fb8aa3b, v72
	v_exp_f32_e32 v72, v72
	v_cndmask_b32_e64 v74, -v128, v141, vcc
	v_mul_f32_e32 v73, v74, v73
	v_sub_u32_e32 v74, v80, v126
	v_cvt_f32_i32_e32 v74, v74
	v_cmp_lt_i32_e32 vcc, v80, v126
	v_mul_f32_e32 v73, 0x3fb8aa3b, v73
	v_exp_f32_e32 v73, v73
	v_cndmask_b32_e64 v75, -v128, v141, vcc
	v_mul_f32_e32 v74, v75, v74
	v_sub_u32_e32 v75, v80, v127
	v_cvt_f32_i32_e32 v75, v75
	v_cmp_lt_i32_e32 vcc, v80, v127
	v_mul_f32_e32 v74, 0x3fb8aa3b, v74
	v_exp_f32_e32 v74, v74
	v_cndmask_b32_e64 v78, -v128, v141, vcc
	v_mul_f32_e32 v75, v78, v75
	v_mul_f32_e32 v75, 0x3fb8aa3b, v75
	v_exp_f32_e32 v75, v75
	v_mul_f32_e32 v72, v64, v72
	v_mul_f32_e32 v73, v65, v73
	v_mul_f32_e32 v74, v66, v74
	v_mul_f32_e32 v67, v67, v75
	v_cvt_pk_bf16_f32 v64, v68, v69
	v_cvt_pk_bf16_f32 v65, v70, v71
	v_cvt_pk_bf16_f32 v66, v72, v73
	v_cvt_pk_bf16_f32 v67, v74, v67
	global_store_dwordx4 v[76:77], v[64:67], off offset:256 sc1
	s_nop 1
	v_add_u32_e32 v64, 0x80, v132
	v_sub_u32_e32 v66, v64, v130
	v_cvt_f32_i32_e32 v68, v66
	v_ashrrev_i32_e32 v65, 31, v64
	v_cmp_lt_i32_e32 vcc, v64, v130
	v_lshl_add_u64 v[66:67], s[52:53], 0, v[64:65]
	s_nop 0
	v_cndmask_b32_e64 v65, -v128, v141, vcc
	v_mul_f32_e32 v65, v65, v68
	v_sub_u32_e32 v68, v64, v148
	v_cvt_f32_i32_e32 v68, v68
	v_mul_f32_e32 v65, 0x3fb8aa3b, v65
	v_exp_f32_e32 v65, v65
	v_cmp_gt_i32_e32 vcc, v64, v130
	v_mul_f32_e32 v60, v60, v65
	s_nop 0
	v_cndmask_b32_e64 v69, v141, -v128, vcc
	v_mul_f32_e32 v68, v69, v68
	v_mul_f32_e32 v68, 0x3fb8aa3b, v68
	v_exp_f32_e32 v68, v68
	v_sub_u32_e32 v65, v64, v146
	v_cvt_f32_i32_e32 v65, v65
	v_cmp_lt_i32_e32 vcc, v64, v146
	v_mul_f32_e32 v61, v61, v68
	s_nop 0
	v_cndmask_b32_e64 v68, -v128, v141, vcc
	v_mul_f32_e32 v65, v68, v65
	v_sub_u32_e32 v68, v64, v147
	v_cvt_f32_i32_e32 v68, v68
	v_mul_f32_e32 v65, 0x3fb8aa3b, v65
	v_exp_f32_e32 v65, v65
	v_cmp_lt_i32_e32 vcc, v64, v147
	v_mul_f32_e32 v62, v62, v65
	s_nop 0
	v_cndmask_b32_e64 v69, -v128, v141, vcc
	v_mul_f32_e32 v68, v69, v68
	v_mul_f32_e32 v68, 0x3fb8aa3b, v68
	v_exp_f32_e32 v68, v68
	v_sub_u32_e32 v65, v64, v142
	v_cvt_f32_i32_e32 v65, v65
	v_cmp_lt_i32_e32 vcc, v64, v142
	v_mul_f32_e32 v63, v63, v68
	s_nop 0
	v_cndmask_b32_e64 v68, -v128, v141, vcc
	v_mul_f32_e32 v65, v68, v65
	v_sub_u32_e32 v68, v64, v143
	v_cvt_f32_i32_e32 v68, v68
	v_cmp_lt_i32_e32 vcc, v64, v143
	v_mul_f32_e32 v65, 0x3fb8aa3b, v65
	v_exp_f32_e32 v65, v65
	v_cndmask_b32_e64 v69, -v128, v141, vcc
	v_mul_f32_e32 v68, v69, v68
	v_sub_u32_e32 v69, v64, v144
	v_cvt_f32_i32_e32 v69, v69
	v_cmp_lt_i32_e32 vcc, v64, v144
	v_mul_f32_e32 v68, 0x3fb8aa3b, v68
	v_exp_f32_e32 v68, v68
	v_cndmask_b32_e64 v70, -v128, v141, vcc
	v_mul_f32_e32 v69, v70, v69
	v_sub_u32_e32 v70, v64, v145
	v_cvt_f32_i32_e32 v70, v70
	v_cmp_lt_i32_e32 vcc, v64, v145
	v_mul_f32_e32 v69, 0x3fb8aa3b, v69
	v_exp_f32_e32 v69, v69
	v_cndmask_b32_e64 v71, -v128, v141, vcc
	v_mul_f32_e32 v70, v71, v70
	v_mul_f32_e32 v70, 0x3fb8aa3b, v70
	v_exp_f32_e32 v70, v70
	v_mul_f32_e32 v65, v56, v65
	v_cvt_pk_bf16_f32 v56, v60, v61
	v_mad_u64_u32 v[60:61], s[54:55], v66, s77, v[120:121]
	v_mad_i32_i24 v61, v67, s77, v61
	v_mul_f32_e32 v59, v59, v70
	v_lshl_add_u64 v[60:61], v[60:61], 0, v[122:123]
	v_mul_f32_e32 v68, v57, v68
	v_mul_f32_e32 v69, v58, v69
	v_cvt_pk_bf16_f32 v57, v62, v63
	v_cvt_pk_bf16_f32 v58, v65, v68
	v_cvt_pk_bf16_f32 v59, v69, v59
	global_store_dwordx4 v[60:61], v[56:59], off sc1
	v_cmp_gt_i32_e32 vcc, v125, v64
	s_nop 0
	v_sub_u32_e32 v57, v64, v124
	v_cvt_f32_i32_e32 v57, v57
	v_cndmask_b32_e64 v56, -v128, v141, vcc
	v_mul_f32_e32 v56, v56, v149
	v_mul_f32_e32 v56, 0x3fb8aa3b, v56
	v_exp_f32_e32 v56, v56
	v_cmp_lt_i32_e32 vcc, v64, v124
	v_mul_f32_e32 v52, v52, v56
	s_nop 0
	v_cndmask_b32_e64 v58, -v128, v141, vcc
	v_mul_f32_e32 v57, v58, v57
	v_mul_f32_e32 v57, 0x3fb8aa3b, v57
	v_exp_f32_e32 v57, v57
	v_sub_u32_e32 v56, v64, v116
	v_cvt_f32_i32_e32 v56, v56
	v_cmp_lt_i32_e32 vcc, v64, v116
	v_mul_f32_e32 v53, v53, v57
	s_nop 0
	v_cndmask_b32_e64 v57, -v128, v141, vcc
	v_mul_f32_e32 v56, v57, v56
	v_sub_u32_e32 v57, v64, v117
	v_cvt_f32_i32_e32 v57, v57
	v_mul_f32_e32 v56, 0x3fb8aa3b, v56
	v_exp_f32_e32 v56, v56
	v_cmp_lt_i32_e32 vcc, v64, v117
	v_mul_f32_e32 v54, v54, v56
	s_nop 0
	v_cndmask_b32_e64 v58, -v128, v141, vcc
	v_mul_f32_e32 v57, v58, v57
	v_mul_f32_e32 v57, 0x3fb8aa3b, v57
	v_exp_f32_e32 v57, v57
	v_sub_u32_e32 v56, v64, v118
	v_cvt_f32_i32_e32 v56, v56
	v_cmp_lt_i32_e32 vcc, v64, v118
	v_mul_f32_e32 v55, v55, v57
	s_nop 0
	v_cndmask_b32_e64 v57, -v128, v141, vcc
	v_mul_f32_e32 v56, v57, v56
	v_sub_u32_e32 v57, v64, v119
	v_cvt_f32_i32_e32 v57, v57
	v_cmp_lt_i32_e32 vcc, v64, v119
	v_mul_f32_e32 v56, 0x3fb8aa3b, v56
	v_exp_f32_e32 v56, v56
	v_cndmask_b32_e64 v58, -v128, v141, vcc
	v_mul_f32_e32 v57, v58, v57
	v_sub_u32_e32 v58, v64, v126
	v_cvt_f32_i32_e32 v58, v58
	v_cmp_lt_i32_e32 vcc, v64, v126
	v_mul_f32_e32 v57, 0x3fb8aa3b, v57
	v_exp_f32_e32 v57, v57
	v_cndmask_b32_e64 v59, -v128, v141, vcc
	v_mul_f32_e32 v58, v59, v58
	v_sub_u32_e32 v59, v64, v127
	v_cvt_f32_i32_e32 v59, v59
	v_cmp_lt_i32_e32 vcc, v64, v127
	v_mul_f32_e32 v58, 0x3fb8aa3b, v58
	v_exp_f32_e32 v58, v58
	v_cndmask_b32_e64 v62, -v128, v141, vcc
	v_mul_f32_e32 v59, v62, v59
	v_mul_f32_e32 v59, 0x3fb8aa3b, v59
	v_exp_f32_e32 v59, v59
	v_mul_f32_e32 v56, v48, v56
	v_mul_f32_e32 v57, v49, v57
	v_mul_f32_e32 v58, v50, v58
	v_mul_f32_e32 v51, v51, v59
	v_cvt_pk_bf16_f32 v48, v52, v53
	v_cvt_pk_bf16_f32 v49, v54, v55
	v_cvt_pk_bf16_f32 v50, v56, v57
	v_cvt_pk_bf16_f32 v51, v58, v51
	global_store_dwordx4 v[60:61], v[48:51], off offset:256 sc1
	s_nop 1
	v_add_u32_e32 v48, 0x90, v132
	v_sub_u32_e32 v50, v48, v130
	v_cvt_f32_i32_e32 v52, v50
	v_ashrrev_i32_e32 v49, 31, v48
	v_cmp_lt_i32_e32 vcc, v48, v130
	v_lshl_add_u64 v[50:51], s[52:53], 0, v[48:49]
	s_nop 0
	v_cndmask_b32_e64 v49, -v128, v141, vcc
	v_mul_f32_e32 v49, v49, v52
	v_sub_u32_e32 v52, v48, v148
	v_cvt_f32_i32_e32 v52, v52
	v_mul_f32_e32 v49, 0x3fb8aa3b, v49
	v_exp_f32_e32 v49, v49
	v_cmp_gt_i32_e32 vcc, v48, v130
	v_mul_f32_e32 v44, v44, v49
	s_nop 0
	v_cndmask_b32_e64 v53, v141, -v128, vcc
	v_mul_f32_e32 v52, v53, v52
	v_mul_f32_e32 v52, 0x3fb8aa3b, v52
	v_exp_f32_e32 v52, v52
	v_sub_u32_e32 v49, v48, v146
	v_cvt_f32_i32_e32 v49, v49
	v_cmp_lt_i32_e32 vcc, v48, v146
	v_mul_f32_e32 v45, v45, v52
	s_nop 0
	v_cndmask_b32_e64 v52, -v128, v141, vcc
	v_mul_f32_e32 v49, v52, v49
	v_sub_u32_e32 v52, v48, v147
	v_cvt_f32_i32_e32 v52, v52
	v_mul_f32_e32 v49, 0x3fb8aa3b, v49
	v_exp_f32_e32 v49, v49
	v_cmp_lt_i32_e32 vcc, v48, v147
	v_mul_f32_e32 v46, v46, v49
	s_nop 0
	v_cndmask_b32_e64 v53, -v128, v141, vcc
	v_mul_f32_e32 v52, v53, v52
	v_mul_f32_e32 v52, 0x3fb8aa3b, v52
	v_exp_f32_e32 v52, v52
	v_sub_u32_e32 v49, v48, v142
	v_cvt_f32_i32_e32 v49, v49
	v_cmp_lt_i32_e32 vcc, v48, v142
	v_mul_f32_e32 v47, v47, v52
	s_nop 0
	v_cndmask_b32_e64 v52, -v128, v141, vcc
	v_mul_f32_e32 v49, v52, v49
	v_sub_u32_e32 v52, v48, v143
	v_cvt_f32_i32_e32 v52, v52
	v_cmp_lt_i32_e32 vcc, v48, v143
	v_mul_f32_e32 v49, 0x3fb8aa3b, v49
	v_exp_f32_e32 v49, v49
	v_cndmask_b32_e64 v53, -v128, v141, vcc
	v_mul_f32_e32 v52, v53, v52
	v_sub_u32_e32 v53, v48, v144
	v_cvt_f32_i32_e32 v53, v53
	v_cmp_lt_i32_e32 vcc, v48, v144
	v_mul_f32_e32 v52, 0x3fb8aa3b, v52
	v_exp_f32_e32 v52, v52
	v_cndmask_b32_e64 v54, -v128, v141, vcc
	v_mul_f32_e32 v53, v54, v53
	v_sub_u32_e32 v54, v48, v145
	v_cvt_f32_i32_e32 v54, v54
	v_cmp_lt_i32_e32 vcc, v48, v145
	v_mul_f32_e32 v53, 0x3fb8aa3b, v53
	v_exp_f32_e32 v53, v53
	v_cndmask_b32_e64 v55, -v128, v141, vcc
	v_mul_f32_e32 v54, v55, v54
	v_mul_f32_e32 v54, 0x3fb8aa3b, v54
	v_exp_f32_e32 v54, v54
	v_mul_f32_e32 v49, v40, v49
	v_cvt_pk_bf16_f32 v40, v44, v45
	v_mad_u64_u32 v[44:45], s[54:55], v50, s77, v[120:121]
	v_mad_i32_i24 v45, v51, s77, v45
	v_mul_f32_e32 v43, v43, v54
	v_lshl_add_u64 v[44:45], v[44:45], 0, v[122:123]
	v_mul_f32_e32 v52, v41, v52
	v_mul_f32_e32 v53, v42, v53
	v_cvt_pk_bf16_f32 v41, v46, v47
	v_cvt_pk_bf16_f32 v42, v49, v52
	v_cvt_pk_bf16_f32 v43, v53, v43
	global_store_dwordx4 v[44:45], v[40:43], off sc1
	s_nop 1
	v_sub_u32_e32 v40, v48, v125
	v_cvt_f32_i32_e32 v40, v40
	v_cmp_lt_i32_e32 vcc, v48, v125
	v_sub_u32_e32 v42, v48, v124
	s_nop 0
	v_cndmask_b32_e64 v41, -v128, v141, vcc
	v_mul_f32_e32 v40, v41, v40
	v_cvt_f32_i32_e32 v41, v42
	v_mul_f32_e32 v40, 0x3fb8aa3b, v40
	v_exp_f32_e32 v40, v40
	v_cmp_lt_i32_e32 vcc, v48, v124
	v_mul_f32_e32 v36, v36, v40
	s_nop 0
	v_cndmask_b32_e64 v42, -v128, v141, vcc
	v_mul_f32_e32 v41, v42, v41
	v_mul_f32_e32 v41, 0x3fb8aa3b, v41
	v_exp_f32_e32 v41, v41
	v_sub_u32_e32 v40, v48, v116
	v_cvt_f32_i32_e32 v40, v40
	v_cmp_lt_i32_e32 vcc, v48, v116
	v_mul_f32_e32 v37, v37, v41
	s_nop 0
	v_cndmask_b32_e64 v41, -v128, v141, vcc
	v_mul_f32_e32 v40, v41, v40
	v_sub_u32_e32 v41, v48, v117
	v_cvt_f32_i32_e32 v41, v41
	v_mul_f32_e32 v40, 0x3fb8aa3b, v40
	v_exp_f32_e32 v40, v40
	v_cmp_lt_i32_e32 vcc, v48, v117
	v_mul_f32_e32 v38, v38, v40
	s_nop 0
	v_cndmask_b32_e64 v42, -v128, v141, vcc
	v_mul_f32_e32 v41, v42, v41
	v_mul_f32_e32 v41, 0x3fb8aa3b, v41
	v_exp_f32_e32 v41, v41
	v_sub_u32_e32 v40, v48, v118
	v_cvt_f32_i32_e32 v40, v40
	v_cmp_lt_i32_e32 vcc, v48, v118
	v_mul_f32_e32 v39, v39, v41
	s_nop 0
	v_cndmask_b32_e64 v41, -v128, v141, vcc
	v_mul_f32_e32 v40, v41, v40
	v_sub_u32_e32 v41, v48, v119
	v_cvt_f32_i32_e32 v41, v41
	v_cmp_lt_i32_e32 vcc, v48, v119
	v_mul_f32_e32 v40, 0x3fb8aa3b, v40
	v_exp_f32_e32 v40, v40
	v_cndmask_b32_e64 v42, -v128, v141, vcc
	v_mul_f32_e32 v41, v42, v41
	v_sub_u32_e32 v42, v48, v126
	v_cvt_f32_i32_e32 v42, v42
	v_cmp_lt_i32_e32 vcc, v48, v126
	v_mul_f32_e32 v41, 0x3fb8aa3b, v41
	v_exp_f32_e32 v41, v41
	v_cndmask_b32_e64 v43, -v128, v141, vcc
	v_mul_f32_e32 v42, v43, v42
	v_sub_u32_e32 v43, v48, v127
	v_cvt_f32_i32_e32 v43, v43
	v_cmp_lt_i32_e32 vcc, v48, v127
	v_mul_f32_e32 v42, 0x3fb8aa3b, v42
	v_exp_f32_e32 v42, v42
	v_cndmask_b32_e64 v46, -v128, v141, vcc
	v_mul_f32_e32 v43, v46, v43
	v_mul_f32_e32 v43, 0x3fb8aa3b, v43
	v_exp_f32_e32 v43, v43
	v_mul_f32_e32 v40, v32, v40
	v_mul_f32_e32 v41, v33, v41
	v_mul_f32_e32 v42, v34, v42
	v_mul_f32_e32 v35, v35, v43
	v_cvt_pk_bf16_f32 v32, v36, v37
	v_cvt_pk_bf16_f32 v33, v38, v39
	v_cvt_pk_bf16_f32 v34, v40, v41
	v_cvt_pk_bf16_f32 v35, v42, v35
	global_store_dwordx4 v[44:45], v[32:35], off offset:256 sc1
	s_nop 1
	v_add_u32_e32 v32, 0xa0, v132
	v_sub_u32_e32 v34, v32, v130
	v_cvt_f32_i32_e32 v36, v34
	v_ashrrev_i32_e32 v33, 31, v32
	v_cmp_lt_i32_e32 vcc, v32, v130
	v_lshl_add_u64 v[34:35], s[52:53], 0, v[32:33]
	s_nop 0
	v_cndmask_b32_e64 v33, -v128, v141, vcc
	v_mul_f32_e32 v33, v33, v36
	v_sub_u32_e32 v36, v32, v148
	v_cvt_f32_i32_e32 v36, v36
	v_mul_f32_e32 v33, 0x3fb8aa3b, v33
	v_exp_f32_e32 v33, v33
	v_cmp_gt_i32_e32 vcc, v32, v130
	v_mul_f32_e32 v28, v28, v33
	s_nop 0
	v_cndmask_b32_e64 v37, v141, -v128, vcc
	v_mul_f32_e32 v36, v37, v36
	v_mul_f32_e32 v36, 0x3fb8aa3b, v36
	v_exp_f32_e32 v36, v36
	v_sub_u32_e32 v33, v32, v146
	v_cvt_f32_i32_e32 v33, v33
	v_cmp_lt_i32_e32 vcc, v32, v146
	v_mul_f32_e32 v29, v29, v36
	s_nop 0
	v_cndmask_b32_e64 v36, -v128, v141, vcc
	v_mul_f32_e32 v33, v36, v33
	v_sub_u32_e32 v36, v32, v147
	v_cvt_f32_i32_e32 v36, v36
	v_mul_f32_e32 v33, 0x3fb8aa3b, v33
	v_exp_f32_e32 v33, v33
	v_cmp_lt_i32_e32 vcc, v32, v147
	v_mul_f32_e32 v30, v30, v33
	s_nop 0
	v_cndmask_b32_e64 v37, -v128, v141, vcc
	v_mul_f32_e32 v36, v37, v36
	v_mul_f32_e32 v36, 0x3fb8aa3b, v36
	v_exp_f32_e32 v36, v36
	v_sub_u32_e32 v33, v32, v142
	v_cvt_f32_i32_e32 v33, v33
	v_cmp_lt_i32_e32 vcc, v32, v142
	v_mul_f32_e32 v31, v31, v36
	s_nop 0
	v_cndmask_b32_e64 v36, -v128, v141, vcc
	v_mul_f32_e32 v33, v36, v33
	v_sub_u32_e32 v36, v32, v143
	v_cvt_f32_i32_e32 v36, v36
	v_cmp_lt_i32_e32 vcc, v32, v143
	v_mul_f32_e32 v33, 0x3fb8aa3b, v33
	v_exp_f32_e32 v33, v33
	v_cndmask_b32_e64 v37, -v128, v141, vcc
	v_mul_f32_e32 v36, v37, v36
	v_sub_u32_e32 v37, v32, v144
	v_cvt_f32_i32_e32 v37, v37
	v_cmp_lt_i32_e32 vcc, v32, v144
	v_mul_f32_e32 v36, 0x3fb8aa3b, v36
	v_exp_f32_e32 v36, v36
	v_cndmask_b32_e64 v38, -v128, v141, vcc
	v_mul_f32_e32 v37, v38, v37
	v_sub_u32_e32 v38, v32, v145
	v_cvt_f32_i32_e32 v38, v38
	v_cmp_lt_i32_e32 vcc, v32, v145
	v_mul_f32_e32 v37, 0x3fb8aa3b, v37
	v_exp_f32_e32 v37, v37
	v_cndmask_b32_e64 v39, -v128, v141, vcc
	v_mul_f32_e32 v38, v39, v38
	v_mul_f32_e32 v38, 0x3fb8aa3b, v38
	v_exp_f32_e32 v38, v38
	v_mul_f32_e32 v33, v24, v33
	v_cvt_pk_bf16_f32 v24, v28, v29
	v_mad_u64_u32 v[28:29], s[54:55], v34, s77, v[120:121]
	v_mad_i32_i24 v29, v35, s77, v29
	v_mul_f32_e32 v27, v27, v38
	v_lshl_add_u64 v[28:29], v[28:29], 0, v[122:123]
	v_mul_f32_e32 v36, v25, v36
	v_mul_f32_e32 v37, v26, v37
	v_cvt_pk_bf16_f32 v25, v30, v31
	v_cvt_pk_bf16_f32 v26, v33, v36
	v_cvt_pk_bf16_f32 v27, v37, v27
	global_store_dwordx4 v[28:29], v[24:27], off sc1
	s_nop 1
	v_sub_u32_e32 v24, v32, v125
	v_cvt_f32_i32_e32 v24, v24
	v_cmp_lt_i32_e32 vcc, v32, v125
	v_sub_u32_e32 v26, v32, v124
	s_nop 0
	v_cndmask_b32_e64 v25, -v128, v141, vcc
	v_mul_f32_e32 v24, v25, v24
	v_cvt_f32_i32_e32 v25, v26
	v_mul_f32_e32 v24, 0x3fb8aa3b, v24
	v_exp_f32_e32 v24, v24
	v_cmp_lt_i32_e32 vcc, v32, v124
	v_mul_f32_e32 v20, v20, v24
	s_nop 0
	v_cndmask_b32_e64 v26, -v128, v141, vcc
	v_mul_f32_e32 v25, v26, v25
	v_mul_f32_e32 v25, 0x3fb8aa3b, v25
	v_exp_f32_e32 v25, v25
	v_sub_u32_e32 v24, v32, v116
	v_cvt_f32_i32_e32 v24, v24
	v_cmp_lt_i32_e32 vcc, v32, v116
	v_mul_f32_e32 v21, v21, v25
	s_nop 0
	v_cndmask_b32_e64 v25, -v128, v141, vcc
	v_mul_f32_e32 v24, v25, v24
	v_sub_u32_e32 v25, v32, v117
	v_cvt_f32_i32_e32 v25, v25
	v_mul_f32_e32 v24, 0x3fb8aa3b, v24
	v_exp_f32_e32 v24, v24
	v_cmp_lt_i32_e32 vcc, v32, v117
	v_mul_f32_e32 v22, v22, v24
	s_nop 0
	v_cndmask_b32_e64 v26, -v128, v141, vcc
	v_mul_f32_e32 v25, v26, v25
	v_mul_f32_e32 v25, 0x3fb8aa3b, v25
	v_exp_f32_e32 v25, v25
	v_sub_u32_e32 v24, v32, v118
	v_cvt_f32_i32_e32 v24, v24
	v_cmp_lt_i32_e32 vcc, v32, v118
	v_mul_f32_e32 v23, v23, v25
	s_nop 0
	v_cndmask_b32_e64 v25, -v128, v141, vcc
	v_mul_f32_e32 v24, v25, v24
	v_sub_u32_e32 v25, v32, v119
	v_cvt_f32_i32_e32 v25, v25
	v_cmp_lt_i32_e32 vcc, v32, v119
	v_mul_f32_e32 v24, 0x3fb8aa3b, v24
	v_exp_f32_e32 v24, v24
	v_cndmask_b32_e64 v26, -v128, v141, vcc
	v_mul_f32_e32 v25, v26, v25
	v_sub_u32_e32 v26, v32, v126
	v_cvt_f32_i32_e32 v26, v26
	v_cmp_lt_i32_e32 vcc, v32, v126
	v_mul_f32_e32 v25, 0x3fb8aa3b, v25
	v_exp_f32_e32 v25, v25
	v_cndmask_b32_e64 v27, -v128, v141, vcc
	v_mul_f32_e32 v26, v27, v26
	v_sub_u32_e32 v27, v32, v127
	v_cvt_f32_i32_e32 v27, v27
	v_cmp_lt_i32_e32 vcc, v32, v127
	v_mul_f32_e32 v26, 0x3fb8aa3b, v26
	v_exp_f32_e32 v26, v26
	v_cndmask_b32_e64 v30, -v128, v141, vcc
	v_mul_f32_e32 v27, v30, v27
	v_mul_f32_e32 v27, 0x3fb8aa3b, v27
	v_exp_f32_e32 v27, v27
	v_mul_f32_e32 v24, v16, v24
	v_mul_f32_e32 v25, v17, v25
	v_mul_f32_e32 v26, v18, v26
	v_mul_f32_e32 v19, v19, v27
	v_cvt_pk_bf16_f32 v16, v20, v21
	v_cvt_pk_bf16_f32 v17, v22, v23
	v_cvt_pk_bf16_f32 v18, v24, v25
	v_cvt_pk_bf16_f32 v19, v26, v19
	global_store_dwordx4 v[28:29], v[16:19], off offset:256 sc1
	s_nop 1
	v_add_u32_e32 v16, 0xb0, v132
	v_sub_u32_e32 v18, v16, v130
	v_cvt_f32_i32_e32 v20, v18
	v_ashrrev_i32_e32 v17, 31, v16
	v_cmp_lt_i32_e32 vcc, v16, v130
	v_lshl_add_u64 v[18:19], s[52:53], 0, v[16:17]
	s_nop 0
	v_cndmask_b32_e64 v17, -v128, v141, vcc
	v_mul_f32_e32 v17, v17, v20
	v_sub_u32_e32 v20, v16, v148
	v_cvt_f32_i32_e32 v20, v20
	v_mul_f32_e32 v17, 0x3fb8aa3b, v17
	v_exp_f32_e32 v17, v17
	v_cmp_gt_i32_e32 vcc, v16, v130
	v_mul_f32_e32 v12, v12, v17
	s_nop 0
	v_cndmask_b32_e64 v21, v141, -v128, vcc
	v_mul_f32_e32 v20, v21, v20
	v_mul_f32_e32 v20, 0x3fb8aa3b, v20
	v_exp_f32_e32 v20, v20
	v_sub_u32_e32 v17, v16, v146
	v_cvt_f32_i32_e32 v17, v17
	v_cmp_lt_i32_e32 vcc, v16, v146
	v_mul_f32_e32 v13, v13, v20
	s_nop 0
	v_cndmask_b32_e64 v20, -v128, v141, vcc
	v_mul_f32_e32 v17, v20, v17
	v_sub_u32_e32 v20, v16, v147
	v_cvt_f32_i32_e32 v20, v20
	v_mul_f32_e32 v17, 0x3fb8aa3b, v17
	v_exp_f32_e32 v17, v17
	v_cmp_lt_i32_e32 vcc, v16, v147
	v_mul_f32_e32 v14, v14, v17
	s_nop 0
	v_cndmask_b32_e64 v21, -v128, v141, vcc
	v_mul_f32_e32 v20, v21, v20
	v_mul_f32_e32 v20, 0x3fb8aa3b, v20
	v_exp_f32_e32 v20, v20
	v_sub_u32_e32 v17, v16, v142
	v_cvt_f32_i32_e32 v17, v17
	v_cmp_lt_i32_e32 vcc, v16, v142
	v_mul_f32_e32 v15, v15, v20
	s_nop 0
	v_cndmask_b32_e64 v20, -v128, v141, vcc
	v_mul_f32_e32 v17, v20, v17
	v_sub_u32_e32 v20, v16, v143
	v_cvt_f32_i32_e32 v20, v20
	v_cmp_lt_i32_e32 vcc, v16, v143
	v_mul_f32_e32 v17, 0x3fb8aa3b, v17
	v_exp_f32_e32 v17, v17
	v_cndmask_b32_e64 v21, -v128, v141, vcc
	v_mul_f32_e32 v20, v21, v20
	v_sub_u32_e32 v21, v16, v144
	v_cvt_f32_i32_e32 v21, v21
	v_cmp_lt_i32_e32 vcc, v16, v144
	v_mul_f32_e32 v20, 0x3fb8aa3b, v20
	v_exp_f32_e32 v20, v20
	v_cndmask_b32_e64 v22, -v128, v141, vcc
	v_mul_f32_e32 v21, v22, v21
	v_sub_u32_e32 v22, v16, v145
	v_cvt_f32_i32_e32 v22, v22
	v_cmp_lt_i32_e32 vcc, v16, v145
	v_mul_f32_e32 v21, 0x3fb8aa3b, v21
	v_exp_f32_e32 v21, v21
	v_cndmask_b32_e64 v23, -v128, v141, vcc
	v_mul_f32_e32 v22, v23, v22
	v_mul_f32_e32 v22, 0x3fb8aa3b, v22
	v_exp_f32_e32 v22, v22
	v_mul_f32_e32 v17, v8, v17
	v_cvt_pk_bf16_f32 v8, v12, v13
	v_mad_u64_u32 v[12:13], s[52:53], v18, s77, v[120:121]
	v_mad_i32_i24 v13, v19, s77, v13
	v_mul_f32_e32 v11, v11, v22
	v_lshl_add_u64 v[12:13], v[12:13], 0, v[122:123]
	v_mul_f32_e32 v20, v9, v20
	v_mul_f32_e32 v21, v10, v21
	v_cvt_pk_bf16_f32 v9, v14, v15
	v_cvt_pk_bf16_f32 v10, v17, v20
	v_cvt_pk_bf16_f32 v11, v21, v11
	global_store_dwordx4 v[12:13], v[8:11], off sc1
	s_nop 1
	v_sub_u32_e32 v8, v16, v125
	v_cvt_f32_i32_e32 v8, v8
	v_cmp_lt_i32_e32 vcc, v16, v125
	v_sub_u32_e32 v10, v16, v124
	s_nop 0
	v_cndmask_b32_e64 v9, -v128, v141, vcc
	v_mul_f32_e32 v8, v9, v8
	v_cvt_f32_i32_e32 v9, v10
	v_cmp_lt_i32_e32 vcc, v16, v124
	v_mul_f32_e32 v8, 0x3fb8aa3b, v8
	v_exp_f32_e32 v8, v8
	v_cndmask_b32_e64 v10, -v128, v141, vcc
	v_mul_f32_e32 v9, v10, v9
	v_sub_u32_e32 v10, v16, v116
	v_cvt_f32_i32_e32 v10, v10
	v_cmp_lt_i32_e32 vcc, v16, v116
	v_mul_f32_e32 v9, 0x3fb8aa3b, v9
	v_exp_f32_e32 v9, v9
	v_cndmask_b32_e64 v11, -v128, v141, vcc
	v_mul_f32_e32 v10, v11, v10
	v_sub_u32_e32 v11, v16, v117
	v_cvt_f32_i32_e32 v11, v11
	v_cmp_lt_i32_e32 vcc, v16, v117
	v_mul_f32_e32 v10, 0x3fb8aa3b, v10
	v_exp_f32_e32 v10, v10
	v_cndmask_b32_e64 v14, -v128, v141, vcc
	v_mul_f32_e32 v11, v14, v11
	v_sub_u32_e32 v14, v16, v118
	v_cvt_f32_i32_e32 v14, v14
	v_cmp_lt_i32_e32 vcc, v16, v118
	v_mul_f32_e32 v11, 0x3fb8aa3b, v11
	v_exp_f32_e32 v11, v11
	v_cndmask_b32_e64 v15, -v128, v141, vcc
	v_mul_f32_e32 v14, v15, v14
	v_sub_u32_e32 v15, v16, v119
	v_cvt_f32_i32_e32 v15, v15
	v_cmp_lt_i32_e32 vcc, v16, v119
	v_mul_f32_e32 v14, 0x3fb8aa3b, v14
	v_exp_f32_e32 v14, v14
	v_cndmask_b32_e64 v17, -v128, v141, vcc
	v_mul_f32_e32 v15, v17, v15
	v_sub_u32_e32 v17, v16, v126
	v_cvt_f32_i32_e32 v17, v17
	v_cmp_lt_i32_e32 vcc, v16, v126
	v_mul_f32_e32 v15, 0x3fb8aa3b, v15
	v_exp_f32_e32 v15, v15
	v_cndmask_b32_e64 v18, -v128, v141, vcc
	v_mul_f32_e32 v17, v18, v17
	v_sub_u32_e32 v18, v16, v127
	v_cvt_f32_i32_e32 v18, v18
	v_cmp_lt_i32_e32 vcc, v16, v127
	v_mul_f32_e32 v17, 0x3fb8aa3b, v17
	v_exp_f32_e32 v17, v17
	v_cndmask_b32_e64 v16, -v128, v141, vcc
	v_mul_f32_e32 v16, v16, v18
	v_mul_f32_e32 v16, 0x3fb8aa3b, v16
	v_exp_f32_e32 v16, v16
	v_mul_f32_e32 v17, v2, v17
	v_mul_f32_e32 v2, v1, v15
	v_mul_f32_e32 v14, v0, v14
	v_mul_f32_e32 v1, v7, v11
	v_mul_f32_e32 v0, v5, v9
	v_mul_f32_e32 v3, v3, v16
	v_mul_f32_e32 v6, v6, v10
	v_mul_f32_e32 v4, v4, v8
	v_cvt_pk_bf16_f32 v0, v4, v0
	v_cvt_pk_bf16_f32 v1, v6, v1
	v_cvt_pk_bf16_f32 v2, v14, v2
	v_cvt_pk_bf16_f32 v3, v17, v3
	global_store_dwordx4 v[12:13], v[0:3], off offset:256 sc1
	s_andn2_b64 vcc, exec, s[50:51]
	s_mov_b64 s[50:51], -1
	s_cbranch_vccnz .LBB0_544
	s_andn2_b64 vcc, exec, s[4:5]
	s_cbranch_vccnz .LBB0_543
	s_barrier
	s_branch .LBB0_543

.LBB0_579:
	s_ashr_i32 s49, s48, 31
	s_ashr_i32 s45, s44, 31
	v_mov_b32_e32 v128, v131
	v_mov_b32_e32 v137, v132
	s_lshl_b64 s[48:49], s[48:49], 14
	s_lshl_b64 s[44:45], s[44:45], 8
	s_add_u32 s44, s48, s44
	v_add_u32_e32 v138, s21, v128
	s_addc_u32 s45, s49, s45
	v_ashrrev_i32_e32 v139, 31, v138
	v_lshlrev_b32_e32 v140, 3, v137
	v_lshl_add_u64 v[142:143], s[44:45], 0, v[138:139]
	v_ashrrev_i32_e32 v141, 31, v140
	v_lshlrev_b64 v[142:143], 9, v[142:143]
	v_lshl_add_u64 v[142:143], s[30:31], 0, v[142:143]
	v_lshlrev_b64 v[140:141], 1, v[140:141]
	v_lshl_add_u64 v[142:143], v[142:143], 0, v[140:141]
	v_cvt_pk_bf16_f32 v124, v124, v125
	v_cvt_pk_bf16_f32 v125, v126, v127
	v_cvt_pk_bf16_f32 v126, v120, v121
	v_cvt_pk_bf16_f32 v127, v122, v123
	global_store_dwordx4 v[142:143], v[124:127], off sc1
	v_cvt_pk_bf16_f32 v116, v116, v117
	v_cvt_pk_bf16_f32 v117, v118, v119
	v_cvt_pk_bf16_f32 v118, v112, v113
	v_add_u32_e32 v112, 16, v138
	v_ashrrev_i32_e32 v113, 31, v112
	v_lshl_add_u64 v[112:113], s[44:45], 0, v[112:113]
	v_lshlrev_b64 v[112:113], 9, v[112:113]
	v_lshl_add_u64 v[112:113], s[30:31], 0, v[112:113]
	v_lshl_add_u64 v[112:113], v[112:113], 0, v[140:141]
	v_cvt_pk_bf16_f32 v119, v114, v115
	global_store_dwordx4 v[142:143], v[116:119], off offset:256 sc1
	v_cvt_pk_bf16_f32 v108, v108, v109
	v_cvt_pk_bf16_f32 v109, v110, v111
	v_cvt_pk_bf16_f32 v110, v104, v105
	v_cvt_pk_bf16_f32 v111, v106, v107
	global_store_dwordx4 v[112:113], v[108:111], off sc1
	v_cvt_pk_bf16_f32 v100, v100, v101
	v_cvt_pk_bf16_f32 v101, v102, v103
	v_cvt_pk_bf16_f32 v102, v96, v97
	v_add_u32_e32 v96, 32, v138
	v_ashrrev_i32_e32 v97, 31, v96
	v_lshl_add_u64 v[96:97], s[44:45], 0, v[96:97]
	v_lshlrev_b64 v[96:97], 9, v[96:97]
	v_lshl_add_u64 v[96:97], s[30:31], 0, v[96:97]
	v_lshl_add_u64 v[96:97], v[96:97], 0, v[140:141]
	v_cvt_pk_bf16_f32 v103, v98, v99
	global_store_dwordx4 v[112:113], v[100:103], off offset:256 sc1
	v_cvt_pk_bf16_f32 v92, v92, v93
	v_cvt_pk_bf16_f32 v93, v94, v95
	v_cvt_pk_bf16_f32 v94, v88, v89
	v_cvt_pk_bf16_f32 v95, v90, v91
	global_store_dwordx4 v[96:97], v[92:95], off sc1
	v_cvt_pk_bf16_f32 v84, v84, v85
	v_cvt_pk_bf16_f32 v85, v86, v87
	v_cvt_pk_bf16_f32 v86, v80, v81
	v_add_u32_e32 v80, 48, v138
	v_ashrrev_i32_e32 v81, 31, v80
	v_lshl_add_u64 v[80:81], s[44:45], 0, v[80:81]
	v_lshlrev_b64 v[80:81], 9, v[80:81]
	v_lshl_add_u64 v[80:81], s[30:31], 0, v[80:81]
	v_lshl_add_u64 v[80:81], v[80:81], 0, v[140:141]
	v_cvt_pk_bf16_f32 v87, v82, v83
	global_store_dwordx4 v[96:97], v[84:87], off offset:256 sc1
	v_cvt_pk_bf16_f32 v76, v76, v77
	v_cvt_pk_bf16_f32 v77, v78, v79
	v_cvt_pk_bf16_f32 v78, v72, v73
	v_cvt_pk_bf16_f32 v79, v74, v75
	global_store_dwordx4 v[80:81], v[76:79], off sc1
	v_cvt_pk_bf16_f32 v68, v68, v69
	v_cvt_pk_bf16_f32 v69, v70, v71
	v_cvt_pk_bf16_f32 v70, v64, v65
	v_add_u32_e32 v64, 0x80, v138
	v_ashrrev_i32_e32 v65, 31, v64
	v_lshl_add_u64 v[64:65], s[44:45], 0, v[64:65]
	v_lshlrev_b64 v[64:65], 9, v[64:65]
	v_lshl_add_u64 v[64:65], s[30:31], 0, v[64:65]
	v_lshl_add_u64 v[64:65], v[64:65], 0, v[140:141]
	v_cvt_pk_bf16_f32 v71, v66, v67
	global_store_dwordx4 v[80:81], v[68:71], off offset:256 sc1
	v_cvt_pk_bf16_f32 v60, v60, v61
	v_cvt_pk_bf16_f32 v61, v62, v63
	v_cvt_pk_bf16_f32 v62, v56, v57
	v_cvt_pk_bf16_f32 v63, v58, v59
	global_store_dwordx4 v[64:65], v[60:63], off sc1
	v_cvt_pk_bf16_f32 v52, v52, v53
	v_cvt_pk_bf16_f32 v53, v54, v55
	v_cvt_pk_bf16_f32 v54, v48, v49
	v_add_u32_e32 v48, 0x90, v138
	v_ashrrev_i32_e32 v49, 31, v48
	v_lshl_add_u64 v[48:49], s[44:45], 0, v[48:49]
	v_lshlrev_b64 v[48:49], 9, v[48:49]
	v_lshl_add_u64 v[48:49], s[30:31], 0, v[48:49]
	v_lshl_add_u64 v[48:49], v[48:49], 0, v[140:141]
	v_cvt_pk_bf16_f32 v55, v50, v51
	global_store_dwordx4 v[64:65], v[52:55], off offset:256 sc1
	v_cvt_pk_bf16_f32 v44, v44, v45
	v_cvt_pk_bf16_f32 v45, v46, v47
	v_cvt_pk_bf16_f32 v46, v40, v41
	v_cvt_pk_bf16_f32 v47, v42, v43
	global_store_dwordx4 v[48:49], v[44:47], off sc1
	v_cvt_pk_bf16_f32 v36, v36, v37
	v_cvt_pk_bf16_f32 v37, v38, v39
	v_cvt_pk_bf16_f32 v38, v32, v33
	v_add_u32_e32 v32, 0xa0, v138
	v_ashrrev_i32_e32 v33, 31, v32
	v_lshl_add_u64 v[32:33], s[44:45], 0, v[32:33]
	v_lshlrev_b64 v[32:33], 9, v[32:33]
	v_lshl_add_u64 v[32:33], s[30:31], 0, v[32:33]
	v_lshl_add_u64 v[32:33], v[32:33], 0, v[140:141]
	v_cvt_pk_bf16_f32 v39, v34, v35
	global_store_dwordx4 v[48:49], v[36:39], off offset:256 sc1
	v_cvt_pk_bf16_f32 v28, v28, v29
	v_cvt_pk_bf16_f32 v29, v30, v31
	v_cvt_pk_bf16_f32 v30, v24, v25
	v_cvt_pk_bf16_f32 v31, v26, v27
	global_store_dwordx4 v[32:33], v[28:31], off sc1
	v_cvt_pk_bf16_f32 v20, v20, v21
	v_cvt_pk_bf16_f32 v21, v22, v23
	v_cvt_pk_bf16_f32 v22, v16, v17
	v_add_u32_e32 v16, 0xb0, v138
	v_ashrrev_i32_e32 v17, 31, v16
	v_lshl_add_u64 v[16:17], s[44:45], 0, v[16:17]
	v_lshlrev_b64 v[16:17], 9, v[16:17]
	v_lshl_add_u64 v[16:17], s[30:31], 0, v[16:17]
	v_lshl_add_u64 v[16:17], v[16:17], 0, v[140:141]
	s_andn2_b64 vcc, exec, s[46:47]
	s_mov_b64 s[44:45], -1
	v_cvt_pk_bf16_f32 v23, v18, v19
	global_store_dwordx4 v[32:33], v[20:23], off offset:256 sc1
	v_cvt_pk_bf16_f32 v12, v12, v13
	v_cvt_pk_bf16_f32 v13, v14, v15
	v_cvt_pk_bf16_f32 v14, v8, v9
	v_cvt_pk_bf16_f32 v15, v10, v11
	global_store_dwordx4 v[16:17], v[12:15], off sc1
	v_cvt_pk_bf16_f32 v4, v4, v5
	v_cvt_pk_bf16_f32 v5, v6, v7
	v_cvt_pk_bf16_f32 v6, v0, v1
	v_cvt_pk_bf16_f32 v7, v2, v3
	global_store_dwordx4 v[16:17], v[4:7], off offset:256 sc1
	s_cbranch_vccnz .LBB0_571
	s_andn2_b64 vcc, exec, s[4:5]
	s_cbranch_vccnz .LBB0_570
	s_barrier
	s_branch .LBB0_570

.LBB0_633:
	v_ashrrev_i32_e32 v139, 31, v138
	v_lshl_add_u64 v[138:139], s[36:37], 0, v[138:139]
	v_lshlrev_b64 v[138:139], 11, v[138:139]
	s_addk_i32 s42, 0x400
	v_lshl_add_u64 v[138:139], v[136:137], 0, v[138:139]
	s_cmpk_lg_i32 s42, 0x1000
	global_store_dwordx4 v[138:139], v[128:131], off nt sc1
	s_cbranch_scc0 .LBB0_612

.LBB0_637:
	v_ashrrev_i32_e32 v139, 31, v138
	v_lshl_add_u64 v[138:139], s[36:37], 0, v[138:139]
	v_lshlrev_b64 v[138:139], 11, v[138:139]
	v_lshl_add_u64 v[184:185], v[136:137], 0, v[138:139]
	v_add_u32_e32 v139, 0x200, v180
	v_ashrrev_i32_e32 v138, 7, v139
	v_lshrrev_b32_e32 v186, 7, v139
	v_mul_lo_u32 v139, v138, s26
	v_add_u32_e32 v187, 0, v139
	v_bitop3_b32 v139, v186, v134, 24 bitop3:0x6c
	v_lshl_add_u32 v180, v138, 2, s2
	v_lshl_add_u32 v181, v139, 1, v187
	ds_read_b32 v139, v180 offset:1024
	ds_read_b128 v[180:183], v181
	global_store_dwordx4 v[184:185], v[128:131], off nt sc1
	s_and_b64 vcc, exec, s[8:9]
	s_waitcnt lgkmcnt(0)
	v_lshlrev_b32_e32 v184, 16, v180
	v_bitop3_b32 v128, v186, v143, 24 bitop3:0x6c
	v_lshl_add_u32 v128, v128, 1, v187
	ds_read_b128 v[128:131], v128
	v_and_b32_e32 v180, 0xffff0000, v180
	v_mul_f32_e32 v194, v139, v184
	v_mul_f32_e32 v195, v139, v180
	v_lshlrev_b32_e32 v193, 16, v181
	v_and_b32_e32 v192, 0xffff0000, v181
	v_lshlrev_b32_e32 v191, 16, v182
	v_and_b32_e32 v190, 0xffff0000, v182
	v_lshlrev_b32_e32 v189, 16, v183
	v_and_b32_e32 v188, 0xffff0000, v183
	s_waitcnt lgkmcnt(0)
	v_lshlrev_b32_e32 v187, 16, v128
	v_and_b32_e32 v186, 0xffff0000, v128
	v_lshlrev_b32_e32 v185, 16, v129
	v_and_b32_e32 v184, 0xffff0000, v129
	v_lshlrev_b32_e32 v183, 16, v130
	v_and_b32_e32 v182, 0xffff0000, v130
	v_lshlrev_b32_e32 v181, 16, v131
	v_and_b32_e32 v180, 0xffff0000, v131
	s_cbranch_vccnz .LBB0_640
	v_mov_b32_e32 v128, 0
	v_cvt_pk_fp8_f32 v128, v194, v195
	v_mul_f32_e32 v196, v139, v191
	v_mul_f32_e32 v197, v139, v190
	v_mov_b32_e32 v129, 0
	v_cvt_pk_fp8_f32 v129, v196, v197
	v_mul_f32_e32 v130, v139, v193
	v_mul_f32_e32 v131, v139, v192
	v_cvt_pk_fp8_f32 v128, v130, v131 op_sel:[0,0,1]
	v_mul_f32_e32 v130, v139, v189
	v_mul_f32_e32 v131, v139, v188
	v_cvt_pk_fp8_f32 v129, v130, v131 op_sel:[0,0,1]
	v_mul_f32_e32 v131, v139, v187
	v_mul_f32_e32 v196, v139, v186
	v_mov_b32_e32 v130, 0
	v_cvt_pk_fp8_f32 v130, v131, v196
	v_mul_f32_e32 v198, v139, v183
	v_mul_f32_e32 v199, v139, v182
	v_mov_b32_e32 v131, 0
	v_cvt_pk_fp8_f32 v131, v198, v199
	v_mul_f32_e32 v196, v139, v185
	v_mul_f32_e32 v197, v139, v184
	v_cvt_pk_fp8_f32 v130, v196, v197 op_sel:[0,0,1]
	v_mul_f32_e32 v196, v139, v181
	v_mul_f32_e32 v197, v139, v180
	v_cvt_pk_fp8_f32 v131, v196, v197 op_sel:[0,0,1]
	s_cbranch_execnz .LBB0_633
	s_branch .LBB0_632

.LBB0_668:
	v_ashrrev_i32_e32 v139, 31, v138
	v_lshl_add_u64 v[138:139], s[14:15], 0, v[138:139]
	v_lshlrev_b64 v[138:139], 11, v[138:139]
	s_addk_i32 s3, 0x400
	v_lshl_add_u64 v[138:139], v[136:137], 0, v[138:139]
	s_cmpk_lg_i32 s3, 0x1000
	global_store_dwordx4 v[138:139], v[128:131], off nt sc1
	s_cbranch_scc0 .LBB0_647

.LBB0_672:
	v_ashrrev_i32_e32 v139, 31, v138
	v_lshl_add_u64 v[138:139], s[14:15], 0, v[138:139]
	v_lshlrev_b64 v[138:139], 11, v[138:139]
	v_lshl_add_u64 v[184:185], v[136:137], 0, v[138:139]
	v_add_u32_e32 v139, 0x200, v180
	v_ashrrev_i32_e32 v138, 7, v139
	v_lshrrev_b32_e32 v186, 7, v139
	v_mul_lo_u32 v139, v138, s27
	v_add_u32_e32 v187, 0, v139
	v_bitop3_b32 v139, v186, v134, 24 bitop3:0x6c
	v_lshl_add_u32 v180, v138, 2, s26
	v_lshl_add_u32 v181, v139, 1, v187
	ds_read_b32 v139, v180 offset:1024
	ds_read_b128 v[180:183], v181
	global_store_dwordx4 v[184:185], v[128:131], off nt sc1
	s_and_b64 vcc, exec, s[8:9]
	s_waitcnt lgkmcnt(0)
	v_lshlrev_b32_e32 v184, 16, v180
	v_bitop3_b32 v128, v186, v143, 24 bitop3:0x6c
	v_lshl_add_u32 v128, v128, 1, v187
	ds_read_b128 v[128:131], v128
	v_and_b32_e32 v180, 0xffff0000, v180
	v_mul_f32_e32 v194, v139, v184
	v_mul_f32_e32 v195, v139, v180
	v_lshlrev_b32_e32 v193, 16, v181
	v_and_b32_e32 v192, 0xffff0000, v181
	v_lshlrev_b32_e32 v191, 16, v182
	v_and_b32_e32 v190, 0xffff0000, v182
	v_lshlrev_b32_e32 v189, 16, v183
	v_and_b32_e32 v188, 0xffff0000, v183
	s_waitcnt lgkmcnt(0)
	v_lshlrev_b32_e32 v187, 16, v128
	v_and_b32_e32 v186, 0xffff0000, v128
	v_lshlrev_b32_e32 v185, 16, v129
	v_and_b32_e32 v184, 0xffff0000, v129
	v_lshlrev_b32_e32 v183, 16, v130
	v_and_b32_e32 v182, 0xffff0000, v130
	v_lshlrev_b32_e32 v181, 16, v131
	v_and_b32_e32 v180, 0xffff0000, v131
	s_cbranch_vccnz .LBB0_675
	v_mov_b32_e32 v128, 0
	v_cvt_pk_fp8_f32 v128, v194, v195
	v_mul_f32_e32 v196, v139, v191
	v_mul_f32_e32 v197, v139, v190
	v_mov_b32_e32 v129, 0
	v_cvt_pk_fp8_f32 v129, v196, v197
	v_mul_f32_e32 v130, v139, v193
	v_mul_f32_e32 v131, v139, v192
	v_cvt_pk_fp8_f32 v128, v130, v131 op_sel:[0,0,1]
	v_mul_f32_e32 v130, v139, v189
	v_mul_f32_e32 v131, v139, v188
	v_cvt_pk_fp8_f32 v129, v130, v131 op_sel:[0,0,1]
	v_mul_f32_e32 v131, v139, v187
	v_mul_f32_e32 v196, v139, v186
	v_mov_b32_e32 v130, 0
	v_cvt_pk_fp8_f32 v130, v131, v196
	v_mul_f32_e32 v198, v139, v183
	v_mul_f32_e32 v199, v139, v182
	v_mov_b32_e32 v131, 0
	v_cvt_pk_fp8_f32 v131, v198, v199
	v_mul_f32_e32 v196, v139, v185
	v_mul_f32_e32 v197, v139, v184
	v_cvt_pk_fp8_f32 v130, v196, v197 op_sel:[0,0,1]
	v_mul_f32_e32 v196, v139, v181
	v_mul_f32_e32 v197, v139, v180
	v_cvt_pk_fp8_f32 v131, v196, v197 op_sel:[0,0,1]
	s_cbranch_execnz .LBB0_668
	s_branch .LBB0_667

.LBB0_703:
	v_ashrrev_i32_e32 v139, 31, v138
	v_lshl_add_u64 v[138:139], s[14:15], 0, v[138:139]
	v_lshlrev_b64 v[138:139], 11, v[138:139]
	s_addk_i32 s0, 0x400
	v_lshl_add_u64 v[138:139], v[136:137], 0, v[138:139]
	s_cmpk_lg_i32 s0, 0x1000
	global_store_dwordx4 v[138:139], v[128:131], off nt sc1
	s_cbranch_scc0 .LBB0_682

.LBB0_815:
	v_mov_b32_e32 v128, v132
	v_mov_b32_e32 v137, v131
	s_ashr_i32 s52, s70, 2
	s_lshl_b32 s53, s70, 8
	s_and_b32 s53, s53, 0x300
	v_lshl_add_u32 v128, v128, 3, s64
	s_add_i32 s52, s52, s33
	v_lshl_add_u32 v138, v137, 7, s52
	v_cvt_pk_bf16_f32 v124, v124, v125
	v_cvt_pk_bf16_f32 v125, v126, v127
	v_cvt_pk_bf16_f32 v126, v120, v121
	v_cvt_pk_bf16_f32 v127, v122, v123
	v_add_lshl_u32 v122, v128, s53, 1
	v_ashrrev_i32_e32 v139, 31, v138
	v_and_b32_e32 v122, 0xffffff00, v122
	v_lshlrev_b64 v[140:141], 12, v[138:139]
	v_ashrrev_i32_e32 v123, 31, v122
	v_and_b32_e32 v142, 0x78, v128
	v_lshl_add_u64 v[120:121], s[34:35], 0, v[140:141]
	v_lshlrev_b64 v[122:123], 1, v[122:123]
	v_lshl_add_u64 v[120:121], v[120:121], 0, v[122:123]
	v_lshlrev_b32_e32 v128, 1, v142
	v_lshl_add_u64 v[120:121], v[120:121], 0, v[128:129]
	global_store_dwordx4 v[120:121], v[124:127], off sc1
	v_cvt_pk_bf16_f32 v116, v116, v117
	v_cvt_pk_bf16_f32 v117, v118, v119
	v_cvt_pk_bf16_f32 v118, v112, v113
	v_add_u32_e32 v112, 0x800, v138
	v_ashrrev_i32_e32 v113, 31, v112
	v_lshlrev_b64 v[112:113], 12, v[112:113]
	v_cvt_pk_bf16_f32 v119, v114, v115
	global_store_dwordx4 v[120:121], v[116:119], off offset:512 sc1
	v_cvt_pk_bf16_f32 v108, v108, v109
	v_cvt_pk_bf16_f32 v109, v110, v111
	v_cvt_pk_bf16_f32 v110, v104, v105
	v_lshl_add_u64 v[104:105], s[34:35], 0, v[112:113]
	v_lshl_add_u64 v[104:105], v[104:105], 0, v[122:123]
	v_lshl_add_u64 v[104:105], v[104:105], 0, v[128:129]
	v_cvt_pk_bf16_f32 v111, v106, v107
	global_store_dwordx4 v[104:105], v[108:111], off sc1
	v_cvt_pk_bf16_f32 v100, v100, v101
	v_cvt_pk_bf16_f32 v101, v102, v103
	v_cvt_pk_bf16_f32 v102, v96, v97
	v_add_u32_e32 v96, 0x1000, v138
	v_ashrrev_i32_e32 v97, 31, v96
	v_lshlrev_b64 v[96:97], 12, v[96:97]
	v_cvt_pk_bf16_f32 v103, v98, v99
	global_store_dwordx4 v[104:105], v[100:103], off offset:512 sc1
	v_cvt_pk_bf16_f32 v92, v92, v93
	v_cvt_pk_bf16_f32 v93, v94, v95
	v_cvt_pk_bf16_f32 v94, v88, v89
	v_lshl_add_u64 v[88:89], s[34:35], 0, v[96:97]
	v_lshl_add_u64 v[88:89], v[88:89], 0, v[122:123]
	v_lshl_add_u64 v[88:89], v[88:89], 0, v[128:129]
	v_cvt_pk_bf16_f32 v95, v90, v91
	global_store_dwordx4 v[88:89], v[92:95], off sc1
	v_cvt_pk_bf16_f32 v84, v84, v85
	v_cvt_pk_bf16_f32 v85, v86, v87
	v_cvt_pk_bf16_f32 v86, v80, v81
	v_add_u32_e32 v80, 0x1800, v138
	v_ashrrev_i32_e32 v81, 31, v80
	v_lshlrev_b64 v[80:81], 12, v[80:81]
	v_cvt_pk_bf16_f32 v87, v82, v83
	global_store_dwordx4 v[88:89], v[84:87], off offset:512 sc1
	v_cvt_pk_bf16_f32 v76, v76, v77
	v_cvt_pk_bf16_f32 v77, v78, v79
	v_cvt_pk_bf16_f32 v78, v72, v73
	v_lshl_add_u64 v[72:73], s[34:35], 0, v[80:81]
	v_lshl_add_u64 v[72:73], v[72:73], 0, v[122:123]
	v_lshl_add_u64 v[72:73], v[72:73], 0, v[128:129]
	s_andn2_b64 vcc, exec, s[50:51]
	s_mov_b64 s[50:51], -1
	v_cvt_pk_bf16_f32 v79, v74, v75
	global_store_dwordx4 v[72:73], v[76:79], off sc1
	v_cvt_pk_bf16_f32 v68, v68, v69
	v_cvt_pk_bf16_f32 v69, v70, v71
	v_cvt_pk_bf16_f32 v70, v64, v65
	v_cvt_pk_bf16_f32 v71, v66, v67
	global_store_dwordx4 v[72:73], v[68:71], off offset:512 sc1
	v_cvt_pk_bf16_f32 v60, v60, v61
	v_cvt_pk_bf16_f32 v61, v62, v63
	v_cvt_pk_bf16_f32 v62, v56, v57
	v_cvt_pk_bf16_f32 v63, v58, v59
	global_store_dwordx4 v[120:121], v[60:63], off offset:256 sc1
	v_cvt_pk_bf16_f32 v52, v52, v53
	v_cvt_pk_bf16_f32 v53, v54, v55
	v_cvt_pk_bf16_f32 v54, v48, v49
	v_cvt_pk_bf16_f32 v55, v50, v51
	global_store_dwordx4 v[120:121], v[52:55], off offset:768 sc1
	v_cvt_pk_bf16_f32 v44, v44, v45
	v_cvt_pk_bf16_f32 v45, v46, v47
	v_cvt_pk_bf16_f32 v46, v40, v41
	v_cvt_pk_bf16_f32 v47, v42, v43
	global_store_dwordx4 v[104:105], v[44:47], off offset:256 sc1
	v_cvt_pk_bf16_f32 v36, v36, v37
	v_cvt_pk_bf16_f32 v37, v38, v39
	v_cvt_pk_bf16_f32 v38, v32, v33
	v_cvt_pk_bf16_f32 v39, v34, v35
	global_store_dwordx4 v[104:105], v[36:39], off offset:768 sc1
	v_cvt_pk_bf16_f32 v28, v28, v29
	v_cvt_pk_bf16_f32 v29, v30, v31
	v_cvt_pk_bf16_f32 v30, v24, v25
	v_cvt_pk_bf16_f32 v31, v26, v27
	global_store_dwordx4 v[88:89], v[28:31], off offset:256 sc1
	v_cvt_pk_bf16_f32 v20, v20, v21
	v_cvt_pk_bf16_f32 v21, v22, v23
	v_cvt_pk_bf16_f32 v22, v16, v17
	v_cvt_pk_bf16_f32 v23, v18, v19
	global_store_dwordx4 v[88:89], v[20:23], off offset:768 sc1
	v_cvt_pk_bf16_f32 v12, v12, v13
	v_cvt_pk_bf16_f32 v13, v14, v15
	v_cvt_pk_bf16_f32 v14, v8, v9
	v_cvt_pk_bf16_f32 v15, v10, v11
	global_store_dwordx4 v[72:73], v[12:15], off offset:256 sc1
	v_cvt_pk_bf16_f32 v4, v4, v5
	v_cvt_pk_bf16_f32 v5, v6, v7
	v_cvt_pk_bf16_f32 v6, v0, v1
	v_cvt_pk_bf16_f32 v7, v2, v3
	global_store_dwordx4 v[72:73], v[4:7], off offset:768 sc1
	s_cbranch_vccnz .LBB0_807
	s_andn2_b64 vcc, exec, s[8:9]
	s_cbranch_vccnz .LBB0_806
	s_barrier
	s_branch .LBB0_806

.LBB0_1003:
	v_ashrrev_i32_e32 v139, 31, v138
	v_lshl_add_u64 v[138:139], s[30:31], 0, v[138:139]
	v_lshlrev_b64 v[138:139], 11, v[138:139]
	s_addk_i32 s38, 0x400
	v_lshl_add_u64 v[138:139], v[136:137], 0, v[138:139]
	s_cmpk_lg_i32 s38, 0x1000
	global_store_dwordx4 v[138:139], v[128:131], off nt sc1
	s_cbranch_scc0 .LBB0_982

.LBB0_1007:
	v_ashrrev_i32_e32 v139, 31, v138
	v_lshl_add_u64 v[138:139], s[30:31], 0, v[138:139]
	v_lshlrev_b64 v[138:139], 11, v[138:139]
	v_lshl_add_u64 v[184:185], v[136:137], 0, v[138:139]
	v_add_u32_e32 v139, 0x200, v180
	v_ashrrev_i32_e32 v138, 7, v139
	v_lshrrev_b32_e32 v186, 7, v139
	v_mul_lo_u32 v139, v138, s20
	v_add_u32_e32 v187, 0, v139
	v_bitop3_b32 v139, v186, v134, 24 bitop3:0x6c
	v_lshl_add_u32 v180, v138, 2, s3
	v_lshl_add_u32 v181, v139, 1, v187
	ds_read_b32 v139, v180 offset:1024
	ds_read_b128 v[180:183], v181
	global_store_dwordx4 v[184:185], v[128:131], off nt sc1
	s_and_b64 vcc, exec, s[8:9]
	s_waitcnt lgkmcnt(0)
	v_lshlrev_b32_e32 v184, 16, v180
	v_bitop3_b32 v128, v186, v143, 24 bitop3:0x6c
	v_lshl_add_u32 v128, v128, 1, v187
	ds_read_b128 v[128:131], v128
	v_and_b32_e32 v180, 0xffff0000, v180
	v_mul_f32_e32 v194, v139, v184
	v_mul_f32_e32 v195, v139, v180
	v_lshlrev_b32_e32 v193, 16, v181
	v_and_b32_e32 v192, 0xffff0000, v181
	v_lshlrev_b32_e32 v191, 16, v182
	v_and_b32_e32 v190, 0xffff0000, v182
	v_lshlrev_b32_e32 v189, 16, v183
	v_and_b32_e32 v188, 0xffff0000, v183
	s_waitcnt lgkmcnt(0)
	v_lshlrev_b32_e32 v187, 16, v128
	v_and_b32_e32 v186, 0xffff0000, v128
	v_lshlrev_b32_e32 v185, 16, v129
	v_and_b32_e32 v184, 0xffff0000, v129
	v_lshlrev_b32_e32 v183, 16, v130
	v_and_b32_e32 v182, 0xffff0000, v130
	v_lshlrev_b32_e32 v181, 16, v131
	v_and_b32_e32 v180, 0xffff0000, v131
	s_cbranch_vccnz .LBB0_1010
	v_mov_b32_e32 v128, 0
	v_cvt_pk_fp8_f32 v128, v194, v195
	v_mul_f32_e32 v196, v139, v191
	v_mul_f32_e32 v197, v139, v190
	v_mov_b32_e32 v129, 0
	v_cvt_pk_fp8_f32 v129, v196, v197
	v_mul_f32_e32 v130, v139, v193
	v_mul_f32_e32 v131, v139, v192
	v_cvt_pk_fp8_f32 v128, v130, v131 op_sel:[0,0,1]
	v_mul_f32_e32 v130, v139, v189
	v_mul_f32_e32 v131, v139, v188
	v_cvt_pk_fp8_f32 v129, v130, v131 op_sel:[0,0,1]
	v_mul_f32_e32 v131, v139, v187
	v_mul_f32_e32 v196, v139, v186
	v_mov_b32_e32 v130, 0
	v_cvt_pk_fp8_f32 v130, v131, v196
	v_mul_f32_e32 v198, v139, v183
	v_mul_f32_e32 v199, v139, v182
	v_mov_b32_e32 v131, 0
	v_cvt_pk_fp8_f32 v131, v198, v199
	v_mul_f32_e32 v196, v139, v185
	v_mul_f32_e32 v197, v139, v184
	v_cvt_pk_fp8_f32 v130, v196, v197 op_sel:[0,0,1]
	v_mul_f32_e32 v196, v139, v181
	v_mul_f32_e32 v197, v139, v180
	v_cvt_pk_fp8_f32 v131, v196, v197 op_sel:[0,0,1]
	s_cbranch_execnz .LBB0_1003
	s_branch .LBB0_1002

.LBB0_1026:
	s_lshl_b32 s52, s92, 8
	v_mov_b32_e32 v64, v67
	v_mov_b32_e32 v72, v68
	s_add_i32 s52, s52, s21
	v_cvt_pk_bf16_f32 v60, v60, v61
	v_cvt_pk_bf16_f32 v61, v62, v63
	v_cvt_pk_bf16_f32 v62, v56, v57
	v_cvt_pk_bf16_f32 v63, v58, v59
	s_andn2_b64 vcc, exec, s[50:51]
	v_add_u32_e32 v76, s52, v64
	v_ashrrev_i32_e32 v74, 3, v76
	v_ashrrev_i32_e32 v75, 31, v74
	v_lshl_add_u32 v72, v72, 3, s65
	v_lshlrev_b64 v[56:57], 12, v[74:75]
	v_lshlrev_b32_e32 v58, 8, v64
	v_ashrrev_i32_e32 v73, 31, v72
	v_lshl_add_u64 v[56:57], s[30:31], 0, v[56:57]
	v_and_b32_e32 v64, 0x700, v58
	v_lshl_add_u64 v[56:57], v[56:57], 0, v[64:65]
	v_lshlrev_b64 v[58:59], 1, v[72:73]
	v_lshl_add_u64 v[56:57], v[56:57], 0, v[58:59]
	global_store_dwordx4 v[56:57], v[60:63], off sc1
	v_add_u32_e32 v56, 16, v76
	v_ashrrev_i32_e32 v56, 3, v56
	v_ashrrev_i32_e32 v57, 31, v56
	v_cvt_pk_bf16_f32 v52, v52, v53
	v_cvt_pk_bf16_f32 v53, v54, v55
	v_cvt_pk_bf16_f32 v54, v48, v49
	v_lshlrev_b64 v[48:49], 12, v[56:57]
	v_lshl_add_u64 v[48:49], s[30:31], 0, v[48:49]
	v_lshl_add_u64 v[48:49], v[48:49], 0, v[64:65]
	v_lshl_add_u64 v[48:49], v[48:49], 0, v[58:59]
	v_cvt_pk_bf16_f32 v55, v50, v51
	global_store_dwordx4 v[48:49], v[52:55], off sc1
	v_add_u32_e32 v48, 32, v76
	v_ashrrev_i32_e32 v48, 3, v48
	v_ashrrev_i32_e32 v49, 31, v48
	v_cvt_pk_bf16_f32 v44, v44, v45
	v_cvt_pk_bf16_f32 v45, v46, v47
	v_cvt_pk_bf16_f32 v46, v40, v41
	v_lshlrev_b64 v[40:41], 12, v[48:49]
	v_lshl_add_u64 v[40:41], s[30:31], 0, v[40:41]
	v_lshl_add_u64 v[40:41], v[40:41], 0, v[64:65]
	v_lshl_add_u64 v[40:41], v[40:41], 0, v[58:59]
	v_cvt_pk_bf16_f32 v47, v42, v43
	global_store_dwordx4 v[40:41], v[44:47], off sc1
	v_add_u32_e32 v40, 48, v76
	v_ashrrev_i32_e32 v40, 3, v40
	v_ashrrev_i32_e32 v41, 31, v40
	v_cvt_pk_bf16_f32 v36, v36, v37
	v_cvt_pk_bf16_f32 v37, v38, v39
	v_cvt_pk_bf16_f32 v38, v32, v33
	v_lshlrev_b64 v[32:33], 12, v[40:41]
	v_lshl_add_u64 v[32:33], s[30:31], 0, v[32:33]
	v_lshl_add_u64 v[32:33], v[32:33], 0, v[64:65]
	v_lshl_add_u64 v[32:33], v[32:33], 0, v[58:59]
	v_cvt_pk_bf16_f32 v39, v34, v35
	global_store_dwordx4 v[32:33], v[36:39], off sc1
	v_add_u32_e32 v32, 0x80, v76
	v_ashrrev_i32_e32 v32, 3, v32
	v_ashrrev_i32_e32 v33, 31, v32
	v_cvt_pk_bf16_f32 v28, v28, v29
	v_cvt_pk_bf16_f32 v29, v30, v31
	v_cvt_pk_bf16_f32 v30, v24, v25
	v_lshlrev_b64 v[24:25], 12, v[32:33]
	v_lshl_add_u64 v[24:25], s[30:31], 0, v[24:25]
	v_lshl_add_u64 v[24:25], v[24:25], 0, v[64:65]
	v_lshl_add_u64 v[24:25], v[24:25], 0, v[58:59]
	v_cvt_pk_bf16_f32 v31, v26, v27
	global_store_dwordx4 v[24:25], v[28:31], off sc1
	v_add_u32_e32 v24, 0x90, v76
	v_ashrrev_i32_e32 v24, 3, v24
	v_ashrrev_i32_e32 v25, 31, v24
	v_cvt_pk_bf16_f32 v20, v20, v21
	v_cvt_pk_bf16_f32 v21, v22, v23
	v_cvt_pk_bf16_f32 v22, v16, v17
	v_lshlrev_b64 v[16:17], 12, v[24:25]
	v_lshl_add_u64 v[16:17], s[30:31], 0, v[16:17]
	v_lshl_add_u64 v[16:17], v[16:17], 0, v[64:65]
	v_lshl_add_u64 v[16:17], v[16:17], 0, v[58:59]
	v_cvt_pk_bf16_f32 v23, v18, v19
	global_store_dwordx4 v[16:17], v[20:23], off sc1
	v_add_u32_e32 v16, 0xa0, v76
	v_ashrrev_i32_e32 v16, 3, v16
	v_ashrrev_i32_e32 v17, 31, v16
	v_cvt_pk_bf16_f32 v12, v12, v13
	v_cvt_pk_bf16_f32 v13, v14, v15
	v_cvt_pk_bf16_f32 v14, v8, v9
	v_lshlrev_b64 v[8:9], 12, v[16:17]
	v_lshl_add_u64 v[8:9], s[30:31], 0, v[8:9]
	v_lshl_add_u64 v[8:9], v[8:9], 0, v[64:65]
	v_lshl_add_u64 v[8:9], v[8:9], 0, v[58:59]
	v_cvt_pk_bf16_f32 v15, v10, v11
	global_store_dwordx4 v[8:9], v[12:15], off sc1
	v_add_u32_e32 v8, 0xb0, v76
	v_ashrrev_i32_e32 v8, 3, v8
	v_ashrrev_i32_e32 v9, 31, v8
	v_cvt_pk_bf16_f32 v4, v4, v5
	v_cvt_pk_bf16_f32 v5, v6, v7
	v_cvt_pk_bf16_f32 v6, v0, v1
	v_lshlrev_b64 v[0:1], 12, v[8:9]
	v_lshl_add_u64 v[0:1], s[30:31], 0, v[0:1]
	v_lshl_add_u64 v[0:1], v[0:1], 0, v[64:65]
	v_lshl_add_u64 v[0:1], v[0:1], 0, v[58:59]
	s_mov_b64 s[50:51], -1
	v_cvt_pk_bf16_f32 v7, v2, v3
	global_store_dwordx4 v[0:1], v[4:7], off sc1
	s_cbranch_vccnz .LBB0_1018
	s_andn2_b64 vcc, exec, s[34:35]
	s_cbranch_vccnz .LBB0_1017
	s_barrier
	s_branch .LBB0_1017

.LBB0_1077:
	s_or_b64 exec, exec, s[52:53]
	v_add_u32_e32 v128, s21, v132
	s_lshl_b32 s52, s4, 8
	s_lshl_b32 s4, s76, 8
	s_or_b32 s4, s4, s68
	v_add_u32_e32 v164, s52, v128
	v_lshl_add_u32 v132, v131, 3, s4
	v_ashrrev_i32_e32 v165, 31, v164
	v_ashrrev_i32_e32 v133, 31, v132
	v_lshlrev_b64 v[152:153], 11, v[164:165]
	s_waitcnt lgkmcnt(0)
	v_lshl_add_u64 v[130:131], v[132:133], 2, s[18:19]
	v_lshl_add_u64 v[152:153], s[8:9], 0, v[152:153]
	v_lshlrev_b64 v[132:133], 1, v[132:133]
	s_waitcnt lgkmcnt(0)
	s_barrier
	v_lshl_add_u64 v[166:167], v[152:153], 0, v[132:133]
	global_load_dwordx4 v[144:147], v[130:131], off offset:16
	global_load_dwordx4 v[148:151], v[130:131], off
	global_load_dwordx4 v[152:155], v[166:167], off
	s_add_i32 s41, 0, 0x20000
	v_lshl_add_u32 v160, v128, 5, s41
	ds_read_b128 v[156:159], v160
	ds_read_b128 v[160:163], v160 offset:16
	s_waitcnt lgkmcnt(0)
	v_add_f32_e32 v169, v156, v158
	v_mov_b32_e32 v168, v157
	v_add_f32_e32 v157, v169, v160
	v_mov_b32_e32 v172, v161
	v_add_f32_e32 v161, v157, v162
	v_fmamk_f32 v156, v161, 0xbe800000, v156
	v_fmac_f32_e32 v158, 0xbe800000, v161
	v_fmamk_f32 v157, v161, 0xbe800000, v160
	v_fmac_f32_e32 v162, 0xbe800000, v161
	v_mov_b32_e32 v170, v159
	v_mov_b32_e32 v174, v163
	v_mul_f32_e32 v169, v156, v156
	v_mul_f32_e32 v171, v158, v158
	v_mul_f32_e32 v173, v157, v157
	v_mul_f32_e32 v175, v162, v162
	v_pk_add_f32 v[156:157], v[168:169], v[170:171]
	v_pk_add_f32 v[158:159], v[172:173], v[174:175]
	v_fmac_f32_e32 v125, 0xbe800000, v161
	v_pk_add_f32 v[156:157], v[156:157], v[158:159]
	v_fmac_f32_e32 v124, 0xbe800000, v161
	v_fmac_f32_e32 v156, 0x42800000, v157
	v_fmamk_f32 v156, v156, 0x3b800000, v142
	v_mul_f32_e32 v157, 0x4f800000, v156
	v_cmp_gt_f32_e32 vcc, s74, v156
	v_fmac_f32_e32 v121, 0xbe800000, v161
	v_fmac_f32_e32 v120, 0xbe800000, v161
	v_cndmask_b32_e32 v156, v156, v157, vcc
	v_sqrt_f32_e32 v157, v156
	v_fmac_f32_e32 v127, 0xbe800000, v161
	v_fmac_f32_e32 v126, 0xbe800000, v161
	v_fmac_f32_e32 v123, 0xbe800000, v161
	v_add_u32_e32 v158, -1, v157
	v_add_u32_e32 v159, 1, v157
	v_fma_f32 v160, -v158, v157, v156
	v_fma_f32 v162, -v159, v157, v156
	v_cmp_ge_f32_e64 s[4:5], 0, v160
	v_fmac_f32_e32 v122, 0xbe800000, v161
	v_fmac_f32_e32 v115, 0xbe800000, v161
	v_cndmask_b32_e64 v157, v157, v158, s[4:5]
	v_cmp_lt_f32_e64 s[4:5], 0, v162
	v_fmac_f32_e32 v114, 0xbe800000, v161
	v_fmac_f32_e32 v119, 0xbe800000, v161
	v_cndmask_b32_e64 v157, v157, v159, s[4:5]
	v_mul_f32_e32 v158, 0x37800000, v157
	v_cndmask_b32_e32 v157, v157, v158, vcc
	v_cmp_class_f32_e32 vcc, v156, v143
	v_fmac_f32_e32 v118, 0xbe800000, v161
	v_fmac_f32_e32 v117, 0xbe800000, v161
	v_cndmask_b32_e32 v156, v157, v156, vcc
	v_div_scale_f32 v157, s[4:5], v156, v156, 1.0
	v_rcp_f32_e32 v158, v157
	v_div_scale_f32 v159, vcc, 1.0, v156, 1.0
	v_fmac_f32_e32 v116, 0xbe800000, v161
	v_fma_f32 v160, -v157, v158, 1.0
	v_fmac_f32_e32 v158, v160, v158
	v_mul_f32_e32 v160, v159, v158
	v_fma_f32 v162, -v157, v160, v159
	v_fmac_f32_e32 v160, v162, v158
	v_fma_f32 v157, -v157, v160, v159
	v_div_fmas_f32 v157, v157, v158, v160
	v_div_fixup_f32 v156, v157, v156, 1.0
	v_pk_mul_f32 v[124:125], v[124:125], v[156:157] op_sel_hi:[1,0]
	v_pk_mul_f32 v[120:121], v[120:121], v[156:157] op_sel_hi:[1,0]
	v_pk_mul_f32 v[126:127], v[126:127], v[156:157] op_sel_hi:[1,0]
	v_pk_mul_f32 v[122:123], v[122:123], v[156:157] op_sel_hi:[1,0]
	v_fmac_f32_e32 v113, 0xbe800000, v161
	v_fmac_f32_e32 v112, 0xbe800000, v161
	v_pk_mul_f32 v[114:115], v[114:115], v[156:157] op_sel_hi:[1,0]
	v_pk_mul_f32 v[116:117], v[116:117], v[156:157] op_sel_hi:[1,0]
	s_waitcnt vmcnt(0)
	v_pk_mul_f32 v[120:121], v[144:145], v[120:121]
	v_pk_mul_f32 v[124:125], v[148:149], v[124:125]
	v_lshlrev_b32_e32 v144, 16, v152
	v_mul_f32_e32 v124, v124, v144
	v_and_b32_e32 v144, 0xffff0000, v152
	v_pk_mul_f32 v[126:127], v[150:151], v[126:127]
	v_mul_f32_e32 v125, v125, v144
	v_lshlrev_b32_e32 v144, 16, v153
	v_mul_f32_e32 v126, v126, v144
	v_and_b32_e32 v144, 0xffff0000, v153
	v_mul_f32_e32 v127, v127, v144
	v_lshlrev_b32_e32 v144, 16, v154
	v_mul_f32_e32 v144, v120, v144
	v_and_b32_e32 v120, 0xffff0000, v154
	v_pk_mul_f32 v[122:123], v[146:147], v[122:123]
	v_mul_f32_e32 v145, v121, v120
	v_lshlrev_b32_e32 v120, 16, v155
	v_mul_f32_e32 v146, v122, v120
	v_and_b32_e32 v120, 0xffff0000, v155
	v_mul_f32_e32 v123, v123, v120
	v_cvt_pk_bf16_f32 v120, v124, v125
	v_cvt_pk_bf16_f32 v121, v126, v127
	v_cvt_pk_bf16_f32 v122, v144, v145
	v_lshlrev_b64 v[144:145], 12, v[164:165]
	v_lshl_add_u64 v[144:145], s[30:31], 0, v[144:145]
	v_lshl_add_u64 v[148:149], v[144:145], 0, v[132:133]
	v_cvt_pk_bf16_f32 v123, v146, v123
	global_store_dwordx4 v[148:149], v[120:123], off offset:2048 sc1
	global_load_dwordx4 v[124:127], v[166:167], off offset:256
	s_nop 0
	global_load_dwordx4 v[120:123], v[130:131], off offset:512
	global_load_dwordx4 v[144:147], v[130:131], off offset:528
	v_add_u32_e32 v154, 16, v128
	v_add_u32_e32 v150, s52, v154
	v_ashrrev_i32_e32 v151, 31, v150
	v_lshlrev_b64 v[152:153], 11, v[150:151]
	v_pk_mul_f32 v[118:119], v[118:119], v[156:157] op_sel_hi:[1,0]
	v_pk_mul_f32 v[112:113], v[112:113], v[156:157] op_sel_hi:[1,0]
	v_lshl_add_u64 v[152:153], s[8:9], 0, v[152:153]
	v_lshl_add_u64 v[152:153], v[152:153], 0, v[132:133]
	s_waitcnt vmcnt(2)
	v_lshlrev_b32_e32 v158, 16, v127
	v_and_b32_e32 v127, 0xffff0000, v127
	s_waitcnt vmcnt(0)
	v_pk_mul_f32 v[114:115], v[146:147], v[114:115]
	v_lshlrev_b32_e32 v155, 16, v124
	v_and_b32_e32 v124, 0xffff0000, v124
	v_lshlrev_b32_e32 v156, 16, v125
	v_and_b32_e32 v125, 0xffff0000, v125
	v_lshlrev_b32_e32 v157, 16, v126
	v_and_b32_e32 v126, 0xffff0000, v126
	v_pk_mul_f32 v[118:119], v[122:123], v[118:119]
	v_pk_mul_f32 v[116:117], v[120:121], v[116:117]
	v_pk_mul_f32 v[112:113], v[144:145], v[112:113]
	v_mul_f32_e32 v115, v115, v127
	v_mul_f32_e32 v116, v116, v155
	v_mul_f32_e32 v117, v117, v124
	v_mul_f32_e32 v118, v118, v156
	v_mul_f32_e32 v119, v119, v125
	v_mul_f32_e32 v120, v112, v157
	v_mul_f32_e32 v121, v113, v126
	v_mul_f32_e32 v122, v114, v158
	v_cvt_pk_bf16_f32 v112, v116, v117
	v_cvt_pk_bf16_f32 v113, v118, v119
	v_cvt_pk_bf16_f32 v114, v120, v121
	v_cvt_pk_bf16_f32 v115, v122, v115
	global_store_dwordx4 v[148:149], v[112:115], off offset:2304 sc1
	global_load_dwordx4 v[116:119], v[152:153], off
	s_nop 0
	global_load_dwordx4 v[112:115], v[130:131], off
	global_load_dwordx4 v[120:123], v[130:131], off offset:16
	v_lshl_add_u32 v144, v154, 5, s41
	ds_read_b128 v[124:127], v144
	ds_read_b128 v[144:147], v144 offset:16
	s_waitcnt lgkmcnt(1)
	v_add_f32_e32 v149, v124, v126
	v_mov_b32_e32 v148, v125
	s_waitcnt lgkmcnt(0)
	v_add_f32_e32 v125, v149, v144
	v_mov_b32_e32 v156, v145
	v_add_f32_e32 v145, v125, v146
	v_fmamk_f32 v124, v145, 0xbe800000, v124
	v_fmac_f32_e32 v126, 0xbe800000, v145
	v_fmamk_f32 v125, v145, 0xbe800000, v144
	v_fmac_f32_e32 v146, 0xbe800000, v145
	v_mov_b32_e32 v154, v127
	v_mov_b32_e32 v158, v147
	v_mul_f32_e32 v149, v124, v124
	v_mul_f32_e32 v155, v126, v126
	v_mul_f32_e32 v157, v125, v125
	v_mul_f32_e32 v159, v146, v146
	v_pk_add_f32 v[124:125], v[148:149], v[154:155]
	v_pk_add_f32 v[126:127], v[156:157], v[158:159]
	v_fmac_f32_e32 v105, 0xbe800000, v145
	v_pk_add_f32 v[124:125], v[124:125], v[126:127]
	v_fmac_f32_e32 v104, 0xbe800000, v145
	v_fmac_f32_e32 v124, 0x42800000, v125
	v_fmamk_f32 v124, v124, 0x3b800000, v142
	v_mul_f32_e32 v125, 0x4f800000, v124
	v_cmp_gt_f32_e32 vcc, s74, v124
	v_fmac_f32_e32 v111, 0xbe800000, v145
	v_fmac_f32_e32 v110, 0xbe800000, v145
	v_cndmask_b32_e32 v124, v124, v125, vcc
	v_sqrt_f32_e32 v125, v124
	v_fmac_f32_e32 v109, 0xbe800000, v145
	v_fmac_f32_e32 v108, 0xbe800000, v145
	v_fmac_f32_e32 v107, 0xbe800000, v145
	v_add_u32_e32 v126, -1, v125
	v_add_u32_e32 v127, 1, v125
	v_fma_f32 v144, -v126, v125, v124
	v_fma_f32 v146, -v127, v125, v124
	v_cmp_ge_f32_e64 s[4:5], 0, v144
	v_fmac_f32_e32 v106, 0xbe800000, v145
	v_fmac_f32_e32 v99, 0xbe800000, v145
	v_cndmask_b32_e64 v125, v125, v126, s[4:5]
	v_cmp_lt_f32_e64 s[4:5], 0, v146
	v_fmac_f32_e32 v98, 0xbe800000, v145
	v_fmac_f32_e32 v103, 0xbe800000, v145
	v_cndmask_b32_e64 v125, v125, v127, s[4:5]
	v_mul_f32_e32 v126, 0x37800000, v125
	v_cndmask_b32_e32 v125, v125, v126, vcc
	v_cmp_class_f32_e32 vcc, v124, v143
	v_fmac_f32_e32 v102, 0xbe800000, v145
	v_fmac_f32_e32 v101, 0xbe800000, v145
	v_cndmask_b32_e32 v124, v125, v124, vcc
	v_div_scale_f32 v125, s[4:5], v124, v124, 1.0
	v_rcp_f32_e32 v126, v125
	v_div_scale_f32 v127, vcc, 1.0, v124, 1.0
	v_fmac_f32_e32 v100, 0xbe800000, v145
	v_fma_f32 v144, -v125, v126, 1.0
	v_fmac_f32_e32 v126, v144, v126
	v_mul_f32_e32 v144, v127, v126
	v_fma_f32 v146, -v125, v144, v127
	v_fmac_f32_e32 v144, v146, v126
	v_fma_f32 v125, -v125, v144, v127
	v_div_fmas_f32 v125, v125, v126, v144
	v_div_fixup_f32 v124, v125, v124, 1.0
	v_pk_mul_f32 v[104:105], v[104:105], v[124:125] op_sel_hi:[1,0]
	v_pk_mul_f32 v[108:109], v[108:109], v[124:125] op_sel_hi:[1,0]
	v_pk_mul_f32 v[110:111], v[110:111], v[124:125] op_sel_hi:[1,0]
	v_pk_mul_f32 v[106:107], v[106:107], v[124:125] op_sel_hi:[1,0]
	v_fmac_f32_e32 v97, 0xbe800000, v145
	v_fmac_f32_e32 v96, 0xbe800000, v145
	s_waitcnt vmcnt(2)
	v_lshlrev_b32_e32 v127, 16, v118
	v_and_b32_e32 v118, 0xffff0000, v118
	s_waitcnt vmcnt(0)
	v_pk_mul_f32 v[104:105], v[120:121], v[104:105]
	v_lshlrev_b32_e32 v125, 16, v116
	v_and_b32_e32 v116, 0xffff0000, v116
	v_lshlrev_b32_e32 v126, 16, v117
	v_and_b32_e32 v117, 0xffff0000, v117
	v_lshlrev_b32_e32 v144, 16, v119
	v_pk_mul_f32 v[110:111], v[114:115], v[110:111]
	v_pk_mul_f32 v[108:109], v[112:113], v[108:109]
	v_pk_mul_f32 v[106:107], v[122:123], v[106:107]
	v_mul_f32_e32 v112, v104, v127
	v_mul_f32_e32 v113, v105, v118
	v_mul_f32_e32 v108, v108, v125
	v_mul_f32_e32 v109, v109, v116
	v_mul_f32_e32 v110, v110, v126
	v_mul_f32_e32 v111, v111, v117
	v_mul_f32_e32 v114, v106, v144
	v_cvt_pk_bf16_f32 v104, v108, v109
	v_cvt_pk_bf16_f32 v105, v110, v111
	v_cvt_pk_bf16_f32 v106, v112, v113
	v_lshlrev_b64 v[112:113], 12, v[150:151]
	v_and_b32_e32 v119, 0xffff0000, v119
	v_lshl_add_u64 v[112:113], s[30:31], 0, v[112:113]
	v_mul_f32_e32 v107, v107, v119
	v_lshl_add_u64 v[116:117], v[112:113], 0, v[132:133]
	v_cvt_pk_bf16_f32 v107, v114, v107
	global_store_dwordx4 v[116:117], v[104:107], off offset:2048 sc1
	global_load_dwordx4 v[108:111], v[152:153], off offset:256
	s_nop 0
	global_load_dwordx4 v[104:107], v[130:131], off offset:512
	global_load_dwordx4 v[112:115], v[130:131], off offset:528
	v_add_u32_e32 v122, 32, v128
	v_add_u32_e32 v118, s52, v122
	v_ashrrev_i32_e32 v119, 31, v118
	v_pk_mul_f32 v[98:99], v[98:99], v[124:125] op_sel_hi:[1,0]
	v_lshlrev_b64 v[120:121], 11, v[118:119]
	v_pk_mul_f32 v[100:101], v[100:101], v[124:125] op_sel_hi:[1,0]
	v_pk_mul_f32 v[102:103], v[102:103], v[124:125] op_sel_hi:[1,0]
	v_pk_mul_f32 v[96:97], v[96:97], v[124:125] op_sel_hi:[1,0]
	v_lshl_add_u64 v[120:121], s[8:9], 0, v[120:121]
	v_lshl_add_u64 v[120:121], v[120:121], 0, v[132:133]
	s_waitcnt vmcnt(2)
	v_lshlrev_b32_e32 v126, 16, v111
	v_and_b32_e32 v111, 0xffff0000, v111
	s_waitcnt vmcnt(0)
	v_pk_mul_f32 v[98:99], v[114:115], v[98:99]
	v_lshlrev_b32_e32 v123, 16, v108
	v_and_b32_e32 v108, 0xffff0000, v108
	v_lshlrev_b32_e32 v124, 16, v109
	v_and_b32_e32 v109, 0xffff0000, v109
	v_lshlrev_b32_e32 v125, 16, v110
	v_and_b32_e32 v110, 0xffff0000, v110
	v_pk_mul_f32 v[102:103], v[106:107], v[102:103]
	v_pk_mul_f32 v[100:101], v[104:105], v[100:101]
	v_pk_mul_f32 v[96:97], v[112:113], v[96:97]
	v_mul_f32_e32 v99, v99, v111
	v_mul_f32_e32 v100, v100, v123
	v_mul_f32_e32 v101, v101, v108
	v_mul_f32_e32 v102, v102, v124
	v_mul_f32_e32 v103, v103, v109
	v_mul_f32_e32 v104, v96, v125
	v_mul_f32_e32 v105, v97, v110
	v_mul_f32_e32 v106, v98, v126
	v_cvt_pk_bf16_f32 v96, v100, v101
	v_cvt_pk_bf16_f32 v97, v102, v103
	v_cvt_pk_bf16_f32 v98, v104, v105
	v_cvt_pk_bf16_f32 v99, v106, v99
	global_store_dwordx4 v[116:117], v[96:99], off offset:2304 sc1
	global_load_dwordx4 v[100:103], v[120:121], off
	s_nop 0
	global_load_dwordx4 v[96:99], v[130:131], off
	global_load_dwordx4 v[104:107], v[130:131], off offset:16
	v_lshl_add_u32 v112, v122, 5, s41
	ds_read_b128 v[108:111], v112
	ds_read_b128 v[112:115], v112 offset:16
	s_waitcnt lgkmcnt(1)
	v_add_f32_e32 v117, v108, v110
	v_mov_b32_e32 v116, v109
	s_waitcnt lgkmcnt(0)
	v_add_f32_e32 v109, v117, v112
	v_mov_b32_e32 v124, v113
	v_add_f32_e32 v113, v109, v114
	v_fmamk_f32 v108, v113, 0xbe800000, v108
	v_fmac_f32_e32 v110, 0xbe800000, v113
	v_fmamk_f32 v109, v113, 0xbe800000, v112
	v_fmac_f32_e32 v114, 0xbe800000, v113
	v_mov_b32_e32 v122, v111
	v_mov_b32_e32 v126, v115
	v_mul_f32_e32 v117, v108, v108
	v_mul_f32_e32 v123, v110, v110
	v_mul_f32_e32 v125, v109, v109
	v_mul_f32_e32 v127, v114, v114
	v_pk_add_f32 v[108:109], v[116:117], v[122:123]
	v_pk_add_f32 v[110:111], v[124:125], v[126:127]
	v_fmac_f32_e32 v89, 0xbe800000, v113
	v_pk_add_f32 v[108:109], v[108:109], v[110:111]
	v_fmac_f32_e32 v88, 0xbe800000, v113
	v_fmac_f32_e32 v108, 0x42800000, v109
	v_fmamk_f32 v108, v108, 0x3b800000, v142
	v_mul_f32_e32 v109, 0x4f800000, v108
	v_cmp_gt_f32_e32 vcc, s74, v108
	v_fmac_f32_e32 v95, 0xbe800000, v113
	v_fmac_f32_e32 v94, 0xbe800000, v113
	v_cndmask_b32_e32 v108, v108, v109, vcc
	v_sqrt_f32_e32 v109, v108
	v_fmac_f32_e32 v93, 0xbe800000, v113
	v_fmac_f32_e32 v92, 0xbe800000, v113
	v_fmac_f32_e32 v91, 0xbe800000, v113
	v_add_u32_e32 v110, -1, v109
	v_add_u32_e32 v111, 1, v109
	v_fma_f32 v112, -v110, v109, v108
	v_fma_f32 v114, -v111, v109, v108
	v_cmp_ge_f32_e64 s[4:5], 0, v112
	v_fmac_f32_e32 v90, 0xbe800000, v113
	v_fmac_f32_e32 v83, 0xbe800000, v113
	v_cndmask_b32_e64 v109, v109, v110, s[4:5]
	v_cmp_lt_f32_e64 s[4:5], 0, v114
	v_fmac_f32_e32 v82, 0xbe800000, v113
	v_fmac_f32_e32 v87, 0xbe800000, v113
	v_cndmask_b32_e64 v109, v109, v111, s[4:5]
	v_mul_f32_e32 v110, 0x37800000, v109
	v_cndmask_b32_e32 v109, v109, v110, vcc
	v_cmp_class_f32_e32 vcc, v108, v143
	v_fmac_f32_e32 v86, 0xbe800000, v113
	v_fmac_f32_e32 v85, 0xbe800000, v113
	v_cndmask_b32_e32 v108, v109, v108, vcc
	v_div_scale_f32 v109, s[4:5], v108, v108, 1.0
	v_rcp_f32_e32 v110, v109
	v_div_scale_f32 v111, vcc, 1.0, v108, 1.0
	v_fmac_f32_e32 v84, 0xbe800000, v113
	v_fma_f32 v112, -v109, v110, 1.0
	v_fmac_f32_e32 v110, v112, v110
	v_mul_f32_e32 v112, v111, v110
	v_fma_f32 v114, -v109, v112, v111
	v_fmac_f32_e32 v112, v114, v110
	v_fma_f32 v109, -v109, v112, v111
	v_div_fmas_f32 v109, v109, v110, v112
	v_div_fixup_f32 v108, v109, v108, 1.0
	v_pk_mul_f32 v[88:89], v[88:89], v[108:109] op_sel_hi:[1,0]
	v_pk_mul_f32 v[92:93], v[92:93], v[108:109] op_sel_hi:[1,0]
	v_pk_mul_f32 v[94:95], v[94:95], v[108:109] op_sel_hi:[1,0]
	v_pk_mul_f32 v[90:91], v[90:91], v[108:109] op_sel_hi:[1,0]
	v_fmac_f32_e32 v81, 0xbe800000, v113
	v_fmac_f32_e32 v80, 0xbe800000, v113
	s_waitcnt vmcnt(2)
	v_lshlrev_b32_e32 v111, 16, v102
	v_and_b32_e32 v102, 0xffff0000, v102
	s_waitcnt vmcnt(0)
	v_pk_mul_f32 v[88:89], v[104:105], v[88:89]
	v_lshlrev_b32_e32 v109, 16, v100
	v_and_b32_e32 v100, 0xffff0000, v100
	v_lshlrev_b32_e32 v110, 16, v101
	v_and_b32_e32 v101, 0xffff0000, v101
	v_lshlrev_b32_e32 v112, 16, v103
	v_pk_mul_f32 v[94:95], v[98:99], v[94:95]
	v_pk_mul_f32 v[92:93], v[96:97], v[92:93]
	v_pk_mul_f32 v[90:91], v[106:107], v[90:91]
	v_mul_f32_e32 v96, v88, v111
	v_mul_f32_e32 v97, v89, v102
	v_mul_f32_e32 v92, v92, v109
	v_mul_f32_e32 v93, v93, v100
	v_mul_f32_e32 v94, v94, v110
	v_mul_f32_e32 v95, v95, v101
	v_mul_f32_e32 v98, v90, v112
	v_cvt_pk_bf16_f32 v88, v92, v93
	v_cvt_pk_bf16_f32 v89, v94, v95
	v_cvt_pk_bf16_f32 v90, v96, v97
	v_lshlrev_b64 v[96:97], 12, v[118:119]
	v_and_b32_e32 v103, 0xffff0000, v103
	v_lshl_add_u64 v[96:97], s[30:31], 0, v[96:97]
	v_mul_f32_e32 v91, v91, v103
	v_lshl_add_u64 v[100:101], v[96:97], 0, v[132:133]
	v_cvt_pk_bf16_f32 v91, v98, v91
	global_store_dwordx4 v[100:101], v[88:91], off offset:2048 sc1
	global_load_dwordx4 v[92:95], v[120:121], off offset:256
	s_nop 0
	global_load_dwordx4 v[88:91], v[130:131], off offset:512
	global_load_dwordx4 v[96:99], v[130:131], off offset:528
	v_add_u32_e32 v106, 48, v128
	v_add_u32_e32 v102, s52, v106
	v_ashrrev_i32_e32 v103, 31, v102
	v_pk_mul_f32 v[82:83], v[82:83], v[108:109] op_sel_hi:[1,0]
	v_lshlrev_b64 v[104:105], 11, v[102:103]
	v_pk_mul_f32 v[84:85], v[84:85], v[108:109] op_sel_hi:[1,0]
	v_pk_mul_f32 v[86:87], v[86:87], v[108:109] op_sel_hi:[1,0]
	v_pk_mul_f32 v[80:81], v[80:81], v[108:109] op_sel_hi:[1,0]
	v_lshl_add_u64 v[104:105], s[8:9], 0, v[104:105]
	v_lshl_add_u64 v[104:105], v[104:105], 0, v[132:133]
	s_waitcnt vmcnt(2)
	v_lshlrev_b32_e32 v110, 16, v95
	v_and_b32_e32 v95, 0xffff0000, v95
	s_waitcnt vmcnt(0)
	v_pk_mul_f32 v[82:83], v[98:99], v[82:83]
	v_lshlrev_b32_e32 v107, 16, v92
	v_and_b32_e32 v92, 0xffff0000, v92
	v_lshlrev_b32_e32 v108, 16, v93
	v_and_b32_e32 v93, 0xffff0000, v93
	v_lshlrev_b32_e32 v109, 16, v94
	v_and_b32_e32 v94, 0xffff0000, v94
	v_pk_mul_f32 v[86:87], v[90:91], v[86:87]
	v_pk_mul_f32 v[84:85], v[88:89], v[84:85]
	v_pk_mul_f32 v[80:81], v[96:97], v[80:81]
	v_mul_f32_e32 v83, v83, v95
	v_mul_f32_e32 v84, v84, v107
	v_mul_f32_e32 v85, v85, v92
	v_mul_f32_e32 v86, v86, v108
	v_mul_f32_e32 v87, v87, v93
	v_mul_f32_e32 v88, v80, v109
	v_mul_f32_e32 v89, v81, v94
	v_mul_f32_e32 v90, v82, v110
	v_cvt_pk_bf16_f32 v80, v84, v85
	v_cvt_pk_bf16_f32 v81, v86, v87
	v_cvt_pk_bf16_f32 v82, v88, v89
	v_cvt_pk_bf16_f32 v83, v90, v83
	global_store_dwordx4 v[100:101], v[80:83], off offset:2304 sc1
	global_load_dwordx4 v[84:87], v[104:105], off
	s_nop 0
	global_load_dwordx4 v[80:83], v[130:131], off
	global_load_dwordx4 v[88:91], v[130:131], off offset:16
	v_lshl_add_u32 v96, v106, 5, s41
	ds_read_b128 v[92:95], v96
	ds_read_b128 v[96:99], v96 offset:16
	s_waitcnt lgkmcnt(1)
	v_add_f32_e32 v101, v92, v94
	v_mov_b32_e32 v100, v93
	s_waitcnt lgkmcnt(0)
	v_add_f32_e32 v93, v101, v96
	v_mov_b32_e32 v108, v97
	v_add_f32_e32 v97, v93, v98
	v_fmamk_f32 v92, v97, 0xbe800000, v92
	v_fmac_f32_e32 v94, 0xbe800000, v97
	v_fmamk_f32 v93, v97, 0xbe800000, v96
	v_fmac_f32_e32 v98, 0xbe800000, v97
	v_mov_b32_e32 v106, v95
	v_mov_b32_e32 v110, v99
	v_mul_f32_e32 v101, v92, v92
	v_mul_f32_e32 v107, v94, v94
	v_mul_f32_e32 v109, v93, v93
	v_mul_f32_e32 v111, v98, v98
	v_pk_add_f32 v[92:93], v[100:101], v[106:107]
	v_pk_add_f32 v[94:95], v[108:109], v[110:111]
	v_fmac_f32_e32 v73, 0xbe800000, v97
	v_pk_add_f32 v[92:93], v[92:93], v[94:95]
	v_fmac_f32_e32 v72, 0xbe800000, v97
	v_fmac_f32_e32 v92, 0x42800000, v93
	v_fmamk_f32 v92, v92, 0x3b800000, v142
	v_mul_f32_e32 v93, 0x4f800000, v92
	v_cmp_gt_f32_e32 vcc, s74, v92
	v_fmac_f32_e32 v79, 0xbe800000, v97
	v_fmac_f32_e32 v78, 0xbe800000, v97
	v_cndmask_b32_e32 v92, v92, v93, vcc
	v_sqrt_f32_e32 v93, v92
	v_fmac_f32_e32 v77, 0xbe800000, v97
	v_fmac_f32_e32 v76, 0xbe800000, v97
	v_fmac_f32_e32 v75, 0xbe800000, v97
	v_add_u32_e32 v94, -1, v93
	v_add_u32_e32 v95, 1, v93
	v_fma_f32 v96, -v94, v93, v92
	v_fma_f32 v98, -v95, v93, v92
	v_cmp_ge_f32_e64 s[4:5], 0, v96
	v_fmac_f32_e32 v74, 0xbe800000, v97
	v_fmac_f32_e32 v67, 0xbe800000, v97
	v_cndmask_b32_e64 v93, v93, v94, s[4:5]
	v_cmp_lt_f32_e64 s[4:5], 0, v98
	v_fmac_f32_e32 v66, 0xbe800000, v97
	v_fmac_f32_e32 v71, 0xbe800000, v97
	v_cndmask_b32_e64 v93, v93, v95, s[4:5]
	v_mul_f32_e32 v94, 0x37800000, v93
	v_cndmask_b32_e32 v93, v93, v94, vcc
	v_cmp_class_f32_e32 vcc, v92, v143
	v_fmac_f32_e32 v70, 0xbe800000, v97
	v_fmac_f32_e32 v69, 0xbe800000, v97
	v_cndmask_b32_e32 v92, v93, v92, vcc
	v_div_scale_f32 v93, s[4:5], v92, v92, 1.0
	v_rcp_f32_e32 v94, v93
	v_div_scale_f32 v95, vcc, 1.0, v92, 1.0
	v_fmac_f32_e32 v68, 0xbe800000, v97
	v_fma_f32 v96, -v93, v94, 1.0
	v_fmac_f32_e32 v94, v96, v94
	v_mul_f32_e32 v96, v95, v94
	v_fma_f32 v98, -v93, v96, v95
	v_fmac_f32_e32 v96, v98, v94
	v_fma_f32 v93, -v93, v96, v95
	v_div_fmas_f32 v93, v93, v94, v96
	v_div_fixup_f32 v92, v93, v92, 1.0
	v_pk_mul_f32 v[72:73], v[72:73], v[92:93] op_sel_hi:[1,0]
	v_pk_mul_f32 v[76:77], v[76:77], v[92:93] op_sel_hi:[1,0]
	v_pk_mul_f32 v[78:79], v[78:79], v[92:93] op_sel_hi:[1,0]
	v_pk_mul_f32 v[74:75], v[74:75], v[92:93] op_sel_hi:[1,0]
	v_fmac_f32_e32 v65, 0xbe800000, v97
	v_fmac_f32_e32 v64, 0xbe800000, v97
	s_waitcnt vmcnt(2)
	v_lshlrev_b32_e32 v95, 16, v86
	v_and_b32_e32 v86, 0xffff0000, v86
	s_waitcnt vmcnt(0)
	v_pk_mul_f32 v[72:73], v[88:89], v[72:73]
	v_lshlrev_b32_e32 v93, 16, v84
	v_and_b32_e32 v84, 0xffff0000, v84
	v_lshlrev_b32_e32 v94, 16, v85
	v_and_b32_e32 v85, 0xffff0000, v85
	v_lshlrev_b32_e32 v96, 16, v87
	v_pk_mul_f32 v[78:79], v[82:83], v[78:79]
	v_pk_mul_f32 v[76:77], v[80:81], v[76:77]
	v_pk_mul_f32 v[74:75], v[90:91], v[74:75]
	v_mul_f32_e32 v80, v72, v95
	v_mul_f32_e32 v81, v73, v86
	v_mul_f32_e32 v76, v76, v93
	v_mul_f32_e32 v77, v77, v84
	v_mul_f32_e32 v78, v78, v94
	v_mul_f32_e32 v79, v79, v85
	v_mul_f32_e32 v82, v74, v96
	v_cvt_pk_bf16_f32 v72, v76, v77
	v_cvt_pk_bf16_f32 v73, v78, v79
	v_cvt_pk_bf16_f32 v74, v80, v81
	v_lshlrev_b64 v[80:81], 12, v[102:103]
	v_and_b32_e32 v87, 0xffff0000, v87
	v_lshl_add_u64 v[80:81], s[30:31], 0, v[80:81]
	v_mul_f32_e32 v75, v75, v87
	v_lshl_add_u64 v[84:85], v[80:81], 0, v[132:133]
	v_cvt_pk_bf16_f32 v75, v82, v75
	global_store_dwordx4 v[84:85], v[72:75], off offset:2048 sc1
	global_load_dwordx4 v[76:79], v[104:105], off offset:256
	s_nop 0
	global_load_dwordx4 v[72:75], v[130:131], off offset:512
	global_load_dwordx4 v[80:83], v[130:131], off offset:528
	v_add_u32_e32 v90, 0x80, v128
	v_add_u32_e32 v86, s52, v90
	v_ashrrev_i32_e32 v87, 31, v86
	v_pk_mul_f32 v[66:67], v[66:67], v[92:93] op_sel_hi:[1,0]
	v_lshlrev_b64 v[88:89], 11, v[86:87]
	v_pk_mul_f32 v[68:69], v[68:69], v[92:93] op_sel_hi:[1,0]
	v_pk_mul_f32 v[70:71], v[70:71], v[92:93] op_sel_hi:[1,0]
	v_pk_mul_f32 v[64:65], v[64:65], v[92:93] op_sel_hi:[1,0]
	v_lshl_add_u64 v[88:89], s[8:9], 0, v[88:89]
	v_lshl_add_u64 v[88:89], v[88:89], 0, v[132:133]
	s_waitcnt vmcnt(2)
	v_lshlrev_b32_e32 v94, 16, v79
	v_and_b32_e32 v79, 0xffff0000, v79
	s_waitcnt vmcnt(0)
	v_pk_mul_f32 v[66:67], v[82:83], v[66:67]
	v_lshlrev_b32_e32 v91, 16, v76
	v_and_b32_e32 v76, 0xffff0000, v76
	v_lshlrev_b32_e32 v92, 16, v77
	v_and_b32_e32 v77, 0xffff0000, v77
	v_lshlrev_b32_e32 v93, 16, v78
	v_and_b32_e32 v78, 0xffff0000, v78
	v_pk_mul_f32 v[70:71], v[74:75], v[70:71]
	v_pk_mul_f32 v[68:69], v[72:73], v[68:69]
	v_pk_mul_f32 v[64:65], v[80:81], v[64:65]
	v_mul_f32_e32 v67, v67, v79
	v_mul_f32_e32 v68, v68, v91
	v_mul_f32_e32 v69, v69, v76
	v_mul_f32_e32 v70, v70, v92
	v_mul_f32_e32 v71, v71, v77
	v_mul_f32_e32 v72, v64, v93
	v_mul_f32_e32 v73, v65, v78
	v_mul_f32_e32 v74, v66, v94
	v_cvt_pk_bf16_f32 v64, v68, v69
	v_cvt_pk_bf16_f32 v65, v70, v71
	v_cvt_pk_bf16_f32 v66, v72, v73
	v_cvt_pk_bf16_f32 v67, v74, v67
	global_store_dwordx4 v[84:85], v[64:67], off offset:2304 sc1
	global_load_dwordx4 v[68:71], v[88:89], off
	s_nop 0
	global_load_dwordx4 v[64:67], v[130:131], off
	global_load_dwordx4 v[72:75], v[130:131], off offset:16
	v_lshl_add_u32 v80, v90, 5, s41
	ds_read_b128 v[76:79], v80
	ds_read_b128 v[80:83], v80 offset:16
	s_waitcnt lgkmcnt(1)
	v_add_f32_e32 v85, v76, v78
	v_mov_b32_e32 v84, v77
	s_waitcnt lgkmcnt(0)
	v_add_f32_e32 v77, v85, v80
	v_mov_b32_e32 v92, v81
	v_add_f32_e32 v81, v77, v82
	v_fmamk_f32 v76, v81, 0xbe800000, v76
	v_fmac_f32_e32 v78, 0xbe800000, v81
	v_fmamk_f32 v77, v81, 0xbe800000, v80
	v_fmac_f32_e32 v82, 0xbe800000, v81
	v_mov_b32_e32 v90, v79
	v_mov_b32_e32 v94, v83
	v_mul_f32_e32 v85, v76, v76
	v_mul_f32_e32 v91, v78, v78
	v_mul_f32_e32 v93, v77, v77
	v_mul_f32_e32 v95, v82, v82
	v_pk_add_f32 v[76:77], v[84:85], v[90:91]
	v_pk_add_f32 v[78:79], v[92:93], v[94:95]
	v_fmac_f32_e32 v57, 0xbe800000, v81
	v_pk_add_f32 v[76:77], v[76:77], v[78:79]
	v_fmac_f32_e32 v56, 0xbe800000, v81
	v_fmac_f32_e32 v76, 0x42800000, v77
	v_fmamk_f32 v76, v76, 0x3b800000, v142
	v_mul_f32_e32 v77, 0x4f800000, v76
	v_cmp_gt_f32_e32 vcc, s74, v76
	v_fmac_f32_e32 v63, 0xbe800000, v81
	v_fmac_f32_e32 v62, 0xbe800000, v81
	v_cndmask_b32_e32 v76, v76, v77, vcc
	v_sqrt_f32_e32 v77, v76
	v_fmac_f32_e32 v61, 0xbe800000, v81
	v_fmac_f32_e32 v60, 0xbe800000, v81
	v_fmac_f32_e32 v59, 0xbe800000, v81
	v_add_u32_e32 v78, -1, v77
	v_add_u32_e32 v79, 1, v77
	v_fma_f32 v80, -v78, v77, v76
	v_fma_f32 v82, -v79, v77, v76
	v_cmp_ge_f32_e64 s[4:5], 0, v80
	v_fmac_f32_e32 v58, 0xbe800000, v81
	v_fmac_f32_e32 v51, 0xbe800000, v81
	v_cndmask_b32_e64 v77, v77, v78, s[4:5]
	v_cmp_lt_f32_e64 s[4:5], 0, v82
	v_fmac_f32_e32 v50, 0xbe800000, v81
	v_fmac_f32_e32 v55, 0xbe800000, v81
	v_cndmask_b32_e64 v77, v77, v79, s[4:5]
	v_mul_f32_e32 v78, 0x37800000, v77
	v_cndmask_b32_e32 v77, v77, v78, vcc
	v_cmp_class_f32_e32 vcc, v76, v143
	v_fmac_f32_e32 v54, 0xbe800000, v81
	v_fmac_f32_e32 v53, 0xbe800000, v81
	v_cndmask_b32_e32 v76, v77, v76, vcc
	v_div_scale_f32 v77, s[4:5], v76, v76, 1.0
	v_rcp_f32_e32 v78, v77
	v_div_scale_f32 v79, vcc, 1.0, v76, 1.0
	v_fmac_f32_e32 v52, 0xbe800000, v81
	v_fma_f32 v80, -v77, v78, 1.0
	v_fmac_f32_e32 v78, v80, v78
	v_mul_f32_e32 v80, v79, v78
	v_fma_f32 v82, -v77, v80, v79
	v_fmac_f32_e32 v80, v82, v78
	v_fma_f32 v77, -v77, v80, v79
	v_div_fmas_f32 v77, v77, v78, v80
	v_div_fixup_f32 v76, v77, v76, 1.0
	v_pk_mul_f32 v[56:57], v[56:57], v[76:77] op_sel_hi:[1,0]
	v_pk_mul_f32 v[60:61], v[60:61], v[76:77] op_sel_hi:[1,0]
	v_pk_mul_f32 v[62:63], v[62:63], v[76:77] op_sel_hi:[1,0]
	v_pk_mul_f32 v[58:59], v[58:59], v[76:77] op_sel_hi:[1,0]
	v_fmac_f32_e32 v49, 0xbe800000, v81
	v_fmac_f32_e32 v48, 0xbe800000, v81
	s_waitcnt vmcnt(2)
	v_lshlrev_b32_e32 v79, 16, v70
	v_and_b32_e32 v70, 0xffff0000, v70
	s_waitcnt vmcnt(0)
	v_pk_mul_f32 v[56:57], v[72:73], v[56:57]
	v_lshlrev_b32_e32 v77, 16, v68
	v_and_b32_e32 v68, 0xffff0000, v68
	v_lshlrev_b32_e32 v78, 16, v69
	v_and_b32_e32 v69, 0xffff0000, v69
	v_lshlrev_b32_e32 v80, 16, v71
	v_pk_mul_f32 v[62:63], v[66:67], v[62:63]
	v_pk_mul_f32 v[60:61], v[64:65], v[60:61]
	v_pk_mul_f32 v[58:59], v[74:75], v[58:59]
	v_mul_f32_e32 v64, v56, v79
	v_mul_f32_e32 v65, v57, v70
	v_mul_f32_e32 v60, v60, v77
	v_mul_f32_e32 v61, v61, v68
	v_mul_f32_e32 v62, v62, v78
	v_mul_f32_e32 v63, v63, v69
	v_mul_f32_e32 v66, v58, v80
	v_cvt_pk_bf16_f32 v56, v60, v61
	v_cvt_pk_bf16_f32 v57, v62, v63
	v_cvt_pk_bf16_f32 v58, v64, v65
	v_lshlrev_b64 v[64:65], 12, v[86:87]
	v_and_b32_e32 v71, 0xffff0000, v71
	v_lshl_add_u64 v[64:65], s[30:31], 0, v[64:65]
	v_mul_f32_e32 v59, v59, v71
	v_lshl_add_u64 v[68:69], v[64:65], 0, v[132:133]
	v_cvt_pk_bf16_f32 v59, v66, v59
	global_store_dwordx4 v[68:69], v[56:59], off offset:2048 sc1
	global_load_dwordx4 v[60:63], v[88:89], off offset:256
	s_nop 0
	global_load_dwordx4 v[56:59], v[130:131], off offset:512
	global_load_dwordx4 v[64:67], v[130:131], off offset:528
	v_add_u32_e32 v74, 0x90, v128
	v_add_u32_e32 v70, s52, v74
	v_ashrrev_i32_e32 v71, 31, v70
	v_pk_mul_f32 v[50:51], v[50:51], v[76:77] op_sel_hi:[1,0]
	v_lshlrev_b64 v[72:73], 11, v[70:71]
	v_pk_mul_f32 v[52:53], v[52:53], v[76:77] op_sel_hi:[1,0]
	v_pk_mul_f32 v[54:55], v[54:55], v[76:77] op_sel_hi:[1,0]
	v_pk_mul_f32 v[48:49], v[48:49], v[76:77] op_sel_hi:[1,0]
	v_lshl_add_u64 v[72:73], s[8:9], 0, v[72:73]
	v_lshl_add_u64 v[72:73], v[72:73], 0, v[132:133]
	s_waitcnt vmcnt(2)
	v_lshlrev_b32_e32 v78, 16, v63
	v_and_b32_e32 v63, 0xffff0000, v63
	s_waitcnt vmcnt(0)
	v_pk_mul_f32 v[50:51], v[66:67], v[50:51]
	v_lshlrev_b32_e32 v75, 16, v60
	v_and_b32_e32 v60, 0xffff0000, v60
	v_lshlrev_b32_e32 v76, 16, v61
	v_and_b32_e32 v61, 0xffff0000, v61
	v_lshlrev_b32_e32 v77, 16, v62
	v_and_b32_e32 v62, 0xffff0000, v62
	v_pk_mul_f32 v[54:55], v[58:59], v[54:55]
	v_pk_mul_f32 v[52:53], v[56:57], v[52:53]
	v_pk_mul_f32 v[48:49], v[64:65], v[48:49]
	v_mul_f32_e32 v51, v51, v63
	v_mul_f32_e32 v52, v52, v75
	v_mul_f32_e32 v53, v53, v60
	v_mul_f32_e32 v54, v54, v76
	v_mul_f32_e32 v55, v55, v61
	v_mul_f32_e32 v56, v48, v77
	v_mul_f32_e32 v57, v49, v62
	v_mul_f32_e32 v58, v50, v78
	v_cvt_pk_bf16_f32 v48, v52, v53
	v_cvt_pk_bf16_f32 v49, v54, v55
	v_cvt_pk_bf16_f32 v50, v56, v57
	v_cvt_pk_bf16_f32 v51, v58, v51
	global_store_dwordx4 v[68:69], v[48:51], off offset:2304 sc1
	global_load_dwordx4 v[52:55], v[72:73], off
	s_nop 0
	global_load_dwordx4 v[48:51], v[130:131], off
	global_load_dwordx4 v[56:59], v[130:131], off offset:16
	v_lshl_add_u32 v64, v74, 5, s41
	ds_read_b128 v[60:63], v64
	ds_read_b128 v[64:67], v64 offset:16
	s_waitcnt lgkmcnt(1)
	v_add_f32_e32 v69, v60, v62
	v_mov_b32_e32 v68, v61
	s_waitcnt lgkmcnt(0)
	v_add_f32_e32 v61, v69, v64
	v_mov_b32_e32 v76, v65
	v_add_f32_e32 v65, v61, v66
	v_fmamk_f32 v60, v65, 0xbe800000, v60
	v_fmac_f32_e32 v62, 0xbe800000, v65
	v_fmamk_f32 v61, v65, 0xbe800000, v64
	v_fmac_f32_e32 v66, 0xbe800000, v65
	v_mov_b32_e32 v74, v63
	v_mov_b32_e32 v78, v67
	v_mul_f32_e32 v69, v60, v60
	v_mul_f32_e32 v75, v62, v62
	v_mul_f32_e32 v77, v61, v61
	v_mul_f32_e32 v79, v66, v66
	v_pk_add_f32 v[60:61], v[68:69], v[74:75]
	v_pk_add_f32 v[62:63], v[76:77], v[78:79]
	v_fmac_f32_e32 v41, 0xbe800000, v65
	v_pk_add_f32 v[60:61], v[60:61], v[62:63]
	v_fmac_f32_e32 v40, 0xbe800000, v65
	v_fmac_f32_e32 v60, 0x42800000, v61
	v_fmamk_f32 v60, v60, 0x3b800000, v142
	v_mul_f32_e32 v61, 0x4f800000, v60
	v_cmp_gt_f32_e32 vcc, s74, v60
	v_fmac_f32_e32 v47, 0xbe800000, v65
	v_fmac_f32_e32 v46, 0xbe800000, v65
	v_cndmask_b32_e32 v60, v60, v61, vcc
	v_sqrt_f32_e32 v61, v60
	v_fmac_f32_e32 v45, 0xbe800000, v65
	v_fmac_f32_e32 v44, 0xbe800000, v65
	v_fmac_f32_e32 v43, 0xbe800000, v65
	v_add_u32_e32 v62, -1, v61
	v_add_u32_e32 v63, 1, v61
	v_fma_f32 v64, -v62, v61, v60
	v_fma_f32 v66, -v63, v61, v60
	v_cmp_ge_f32_e64 s[4:5], 0, v64
	v_fmac_f32_e32 v42, 0xbe800000, v65
	v_fmac_f32_e32 v35, 0xbe800000, v65
	v_cndmask_b32_e64 v61, v61, v62, s[4:5]
	v_cmp_lt_f32_e64 s[4:5], 0, v66
	v_fmac_f32_e32 v34, 0xbe800000, v65
	v_fmac_f32_e32 v39, 0xbe800000, v65
	v_cndmask_b32_e64 v61, v61, v63, s[4:5]
	v_mul_f32_e32 v62, 0x37800000, v61
	v_cndmask_b32_e32 v61, v61, v62, vcc
	v_cmp_class_f32_e32 vcc, v60, v143
	v_fmac_f32_e32 v38, 0xbe800000, v65
	v_fmac_f32_e32 v37, 0xbe800000, v65
	v_cndmask_b32_e32 v60, v61, v60, vcc
	v_div_scale_f32 v61, s[4:5], v60, v60, 1.0
	v_rcp_f32_e32 v62, v61
	v_div_scale_f32 v63, vcc, 1.0, v60, 1.0
	v_fmac_f32_e32 v36, 0xbe800000, v65
	v_fma_f32 v64, -v61, v62, 1.0
	v_fmac_f32_e32 v62, v64, v62
	v_mul_f32_e32 v64, v63, v62
	v_fma_f32 v66, -v61, v64, v63
	v_fmac_f32_e32 v64, v66, v62
	v_fma_f32 v61, -v61, v64, v63
	v_div_fmas_f32 v61, v61, v62, v64
	v_div_fixup_f32 v60, v61, v60, 1.0
	v_pk_mul_f32 v[40:41], v[40:41], v[60:61] op_sel_hi:[1,0]
	v_pk_mul_f32 v[44:45], v[44:45], v[60:61] op_sel_hi:[1,0]
	v_pk_mul_f32 v[46:47], v[46:47], v[60:61] op_sel_hi:[1,0]
	v_pk_mul_f32 v[42:43], v[42:43], v[60:61] op_sel_hi:[1,0]
	v_fmac_f32_e32 v33, 0xbe800000, v65
	v_fmac_f32_e32 v32, 0xbe800000, v65
	s_waitcnt vmcnt(2)
	v_lshlrev_b32_e32 v63, 16, v54
	v_and_b32_e32 v54, 0xffff0000, v54
	s_waitcnt vmcnt(0)
	v_pk_mul_f32 v[40:41], v[56:57], v[40:41]
	v_lshlrev_b32_e32 v61, 16, v52
	v_and_b32_e32 v52, 0xffff0000, v52
	v_lshlrev_b32_e32 v62, 16, v53
	v_and_b32_e32 v53, 0xffff0000, v53
	v_lshlrev_b32_e32 v64, 16, v55
	v_pk_mul_f32 v[46:47], v[50:51], v[46:47]
	v_pk_mul_f32 v[44:45], v[48:49], v[44:45]
	v_pk_mul_f32 v[42:43], v[58:59], v[42:43]
	v_mul_f32_e32 v48, v40, v63
	v_mul_f32_e32 v49, v41, v54
	v_mul_f32_e32 v44, v44, v61
	v_mul_f32_e32 v45, v45, v52
	v_mul_f32_e32 v46, v46, v62
	v_mul_f32_e32 v47, v47, v53
	v_mul_f32_e32 v50, v42, v64
	v_cvt_pk_bf16_f32 v40, v44, v45
	v_cvt_pk_bf16_f32 v41, v46, v47
	v_cvt_pk_bf16_f32 v42, v48, v49
	v_lshlrev_b64 v[48:49], 12, v[70:71]
	v_and_b32_e32 v55, 0xffff0000, v55
	v_lshl_add_u64 v[48:49], s[30:31], 0, v[48:49]
	v_mul_f32_e32 v43, v43, v55
	v_lshl_add_u64 v[52:53], v[48:49], 0, v[132:133]
	v_cvt_pk_bf16_f32 v43, v50, v43
	global_store_dwordx4 v[52:53], v[40:43], off offset:2048 sc1
	global_load_dwordx4 v[44:47], v[72:73], off offset:256
	s_nop 0
	global_load_dwordx4 v[40:43], v[130:131], off offset:512
	global_load_dwordx4 v[48:51], v[130:131], off offset:528
	v_add_u32_e32 v58, 0xa0, v128
	v_add_u32_e32 v54, s52, v58
	v_ashrrev_i32_e32 v55, 31, v54
	v_pk_mul_f32 v[34:35], v[34:35], v[60:61] op_sel_hi:[1,0]
	v_lshlrev_b64 v[56:57], 11, v[54:55]
	v_pk_mul_f32 v[36:37], v[36:37], v[60:61] op_sel_hi:[1,0]
	v_pk_mul_f32 v[38:39], v[38:39], v[60:61] op_sel_hi:[1,0]
	v_pk_mul_f32 v[32:33], v[32:33], v[60:61] op_sel_hi:[1,0]
	v_lshl_add_u64 v[56:57], s[8:9], 0, v[56:57]
	v_lshl_add_u64 v[56:57], v[56:57], 0, v[132:133]
	s_waitcnt vmcnt(2)
	v_lshlrev_b32_e32 v62, 16, v47
	v_and_b32_e32 v47, 0xffff0000, v47
	s_waitcnt vmcnt(0)
	v_pk_mul_f32 v[34:35], v[50:51], v[34:35]
	v_lshlrev_b32_e32 v59, 16, v44
	v_and_b32_e32 v44, 0xffff0000, v44
	v_lshlrev_b32_e32 v60, 16, v45
	v_and_b32_e32 v45, 0xffff0000, v45
	v_lshlrev_b32_e32 v61, 16, v46
	v_and_b32_e32 v46, 0xffff0000, v46
	v_pk_mul_f32 v[38:39], v[42:43], v[38:39]
	v_pk_mul_f32 v[36:37], v[40:41], v[36:37]
	v_pk_mul_f32 v[32:33], v[48:49], v[32:33]
	v_mul_f32_e32 v35, v35, v47
	v_mul_f32_e32 v36, v36, v59
	v_mul_f32_e32 v37, v37, v44
	v_mul_f32_e32 v38, v38, v60
	v_mul_f32_e32 v39, v39, v45
	v_mul_f32_e32 v40, v32, v61
	v_mul_f32_e32 v41, v33, v46
	v_mul_f32_e32 v42, v34, v62
	v_cvt_pk_bf16_f32 v32, v36, v37
	v_cvt_pk_bf16_f32 v33, v38, v39
	v_cvt_pk_bf16_f32 v34, v40, v41
	v_cvt_pk_bf16_f32 v35, v42, v35
	global_store_dwordx4 v[52:53], v[32:35], off offset:2304 sc1
	global_load_dwordx4 v[36:39], v[56:57], off
	s_nop 0
	global_load_dwordx4 v[32:35], v[130:131], off
	global_load_dwordx4 v[40:43], v[130:131], off offset:16
	v_lshl_add_u32 v48, v58, 5, s41
	ds_read_b128 v[44:47], v48
	ds_read_b128 v[48:51], v48 offset:16
	s_waitcnt lgkmcnt(1)
	v_add_f32_e32 v53, v44, v46
	v_mov_b32_e32 v52, v45
	s_waitcnt lgkmcnt(0)
	v_add_f32_e32 v45, v53, v48
	v_mov_b32_e32 v60, v49
	v_add_f32_e32 v49, v45, v50
	v_fmamk_f32 v44, v49, 0xbe800000, v44
	v_fmac_f32_e32 v46, 0xbe800000, v49
	v_fmamk_f32 v45, v49, 0xbe800000, v48
	v_fmac_f32_e32 v50, 0xbe800000, v49
	v_mov_b32_e32 v58, v47
	v_mov_b32_e32 v62, v51
	v_mul_f32_e32 v53, v44, v44
	v_mul_f32_e32 v59, v46, v46
	v_mul_f32_e32 v61, v45, v45
	v_mul_f32_e32 v63, v50, v50
	v_pk_add_f32 v[44:45], v[52:53], v[58:59]
	v_pk_add_f32 v[46:47], v[60:61], v[62:63]
	v_fmac_f32_e32 v25, 0xbe800000, v49
	v_pk_add_f32 v[44:45], v[44:45], v[46:47]
	v_fmac_f32_e32 v24, 0xbe800000, v49
	v_fmac_f32_e32 v44, 0x42800000, v45
	v_fmamk_f32 v44, v44, 0x3b800000, v142
	v_mul_f32_e32 v45, 0x4f800000, v44
	v_cmp_gt_f32_e32 vcc, s74, v44
	v_fmac_f32_e32 v31, 0xbe800000, v49
	v_fmac_f32_e32 v30, 0xbe800000, v49
	v_cndmask_b32_e32 v44, v44, v45, vcc
	v_sqrt_f32_e32 v45, v44
	v_fmac_f32_e32 v29, 0xbe800000, v49
	v_fmac_f32_e32 v28, 0xbe800000, v49
	v_fmac_f32_e32 v27, 0xbe800000, v49
	v_add_u32_e32 v46, -1, v45
	v_add_u32_e32 v47, 1, v45
	v_fma_f32 v48, -v46, v45, v44
	v_fma_f32 v50, -v47, v45, v44
	v_cmp_ge_f32_e64 s[4:5], 0, v48
	v_fmac_f32_e32 v26, 0xbe800000, v49
	v_fmac_f32_e32 v19, 0xbe800000, v49
	v_cndmask_b32_e64 v45, v45, v46, s[4:5]
	v_cmp_lt_f32_e64 s[4:5], 0, v50
	v_fmac_f32_e32 v18, 0xbe800000, v49
	v_fmac_f32_e32 v23, 0xbe800000, v49
	v_cndmask_b32_e64 v45, v45, v47, s[4:5]
	v_mul_f32_e32 v46, 0x37800000, v45
	v_cndmask_b32_e32 v45, v45, v46, vcc
	v_cmp_class_f32_e32 vcc, v44, v143
	v_fmac_f32_e32 v22, 0xbe800000, v49
	v_fmac_f32_e32 v21, 0xbe800000, v49
	v_cndmask_b32_e32 v44, v45, v44, vcc
	v_div_scale_f32 v45, s[4:5], v44, v44, 1.0
	v_rcp_f32_e32 v46, v45
	v_div_scale_f32 v47, vcc, 1.0, v44, 1.0
	v_fmac_f32_e32 v20, 0xbe800000, v49
	v_fma_f32 v48, -v45, v46, 1.0
	v_fmac_f32_e32 v46, v48, v46
	v_mul_f32_e32 v48, v47, v46
	v_fma_f32 v50, -v45, v48, v47
	v_fmac_f32_e32 v48, v50, v46
	v_fma_f32 v45, -v45, v48, v47
	v_div_fmas_f32 v45, v45, v46, v48
	v_div_fixup_f32 v44, v45, v44, 1.0
	v_pk_mul_f32 v[24:25], v[24:25], v[44:45] op_sel_hi:[1,0]
	v_pk_mul_f32 v[28:29], v[28:29], v[44:45] op_sel_hi:[1,0]
	v_pk_mul_f32 v[30:31], v[30:31], v[44:45] op_sel_hi:[1,0]
	v_pk_mul_f32 v[26:27], v[26:27], v[44:45] op_sel_hi:[1,0]
	v_fmac_f32_e32 v17, 0xbe800000, v49
	v_fmac_f32_e32 v16, 0xbe800000, v49
	s_waitcnt vmcnt(2)
	v_lshlrev_b32_e32 v47, 16, v38
	v_and_b32_e32 v38, 0xffff0000, v38
	s_waitcnt vmcnt(0)
	v_pk_mul_f32 v[24:25], v[40:41], v[24:25]
	v_lshlrev_b32_e32 v45, 16, v36
	v_and_b32_e32 v36, 0xffff0000, v36
	v_lshlrev_b32_e32 v46, 16, v37
	v_and_b32_e32 v37, 0xffff0000, v37
	v_lshlrev_b32_e32 v48, 16, v39
	v_pk_mul_f32 v[30:31], v[34:35], v[30:31]
	v_pk_mul_f32 v[28:29], v[32:33], v[28:29]
	v_pk_mul_f32 v[26:27], v[42:43], v[26:27]
	v_mul_f32_e32 v32, v24, v47
	v_mul_f32_e32 v33, v25, v38
	v_mul_f32_e32 v28, v28, v45
	v_mul_f32_e32 v29, v29, v36
	v_mul_f32_e32 v30, v30, v46
	v_mul_f32_e32 v31, v31, v37
	v_mul_f32_e32 v34, v26, v48
	v_cvt_pk_bf16_f32 v24, v28, v29
	v_cvt_pk_bf16_f32 v25, v30, v31
	v_cvt_pk_bf16_f32 v26, v32, v33
	v_lshlrev_b64 v[32:33], 12, v[54:55]
	v_and_b32_e32 v39, 0xffff0000, v39
	v_lshl_add_u64 v[32:33], s[30:31], 0, v[32:33]
	v_mul_f32_e32 v27, v27, v39
	v_lshl_add_u64 v[36:37], v[32:33], 0, v[132:133]
	v_cvt_pk_bf16_f32 v27, v34, v27
	global_store_dwordx4 v[36:37], v[24:27], off offset:2048 sc1
	global_load_dwordx4 v[28:31], v[56:57], off offset:256
	s_nop 0
	global_load_dwordx4 v[24:27], v[130:131], off offset:512
	global_load_dwordx4 v[32:35], v[130:131], off offset:528
	v_add_u32_e32 v42, 0xb0, v128
	v_add_u32_e32 v38, s52, v42
	v_ashrrev_i32_e32 v39, 31, v38
	v_pk_mul_f32 v[18:19], v[18:19], v[44:45] op_sel_hi:[1,0]
	v_lshlrev_b64 v[40:41], 11, v[38:39]
	v_pk_mul_f32 v[20:21], v[20:21], v[44:45] op_sel_hi:[1,0]
	v_pk_mul_f32 v[22:23], v[22:23], v[44:45] op_sel_hi:[1,0]
	v_pk_mul_f32 v[16:17], v[16:17], v[44:45] op_sel_hi:[1,0]
	v_lshl_add_u64 v[40:41], s[8:9], 0, v[40:41]
	v_lshl_add_u64 v[40:41], v[40:41], 0, v[132:133]
	s_waitcnt vmcnt(2)
	v_lshlrev_b32_e32 v46, 16, v31
	v_and_b32_e32 v31, 0xffff0000, v31
	s_waitcnt vmcnt(0)
	v_pk_mul_f32 v[18:19], v[34:35], v[18:19]
	v_lshlrev_b32_e32 v43, 16, v28
	v_and_b32_e32 v28, 0xffff0000, v28
	v_lshlrev_b32_e32 v44, 16, v29
	v_and_b32_e32 v29, 0xffff0000, v29
	v_lshlrev_b32_e32 v45, 16, v30
	v_and_b32_e32 v30, 0xffff0000, v30
	v_pk_mul_f32 v[22:23], v[26:27], v[22:23]
	v_pk_mul_f32 v[20:21], v[24:25], v[20:21]
	v_pk_mul_f32 v[16:17], v[32:33], v[16:17]
	v_mul_f32_e32 v19, v19, v31
	v_mul_f32_e32 v20, v20, v43
	v_mul_f32_e32 v21, v21, v28
	v_mul_f32_e32 v22, v22, v44
	v_mul_f32_e32 v23, v23, v29
	v_mul_f32_e32 v24, v16, v45
	v_mul_f32_e32 v25, v17, v30
	v_mul_f32_e32 v26, v18, v46
	v_cvt_pk_bf16_f32 v16, v20, v21
	v_cvt_pk_bf16_f32 v17, v22, v23
	v_cvt_pk_bf16_f32 v18, v24, v25
	v_cvt_pk_bf16_f32 v19, v26, v19
	global_store_dwordx4 v[36:37], v[16:19], off offset:2304 sc1
	global_load_dwordx4 v[20:23], v[40:41], off
	s_nop 0
	global_load_dwordx4 v[16:19], v[130:131], off
	global_load_dwordx4 v[24:27], v[130:131], off offset:16
	v_lshl_add_u32 v32, v42, 5, s41
	ds_read_b128 v[28:31], v32
	ds_read_b128 v[32:35], v32 offset:16
	s_waitcnt lgkmcnt(1)
	v_add_f32_e32 v37, v28, v30
	v_mov_b32_e32 v36, v29
	s_waitcnt lgkmcnt(0)
	v_add_f32_e32 v29, v37, v32
	v_mov_b32_e32 v44, v33
	v_add_f32_e32 v33, v29, v34
	v_fmamk_f32 v28, v33, 0xbe800000, v28
	v_fmac_f32_e32 v30, 0xbe800000, v33
	v_fmamk_f32 v29, v33, 0xbe800000, v32
	v_fmac_f32_e32 v34, 0xbe800000, v33
	v_mov_b32_e32 v42, v31
	v_mov_b32_e32 v46, v35
	v_mul_f32_e32 v37, v28, v28
	v_mul_f32_e32 v43, v30, v30
	v_mul_f32_e32 v45, v29, v29
	v_mul_f32_e32 v47, v34, v34
	v_pk_add_f32 v[28:29], v[36:37], v[42:43]
	v_pk_add_f32 v[30:31], v[44:45], v[46:47]
	v_fmac_f32_e32 v9, 0xbe800000, v33
	v_pk_add_f32 v[28:29], v[28:29], v[30:31]
	v_fmac_f32_e32 v8, 0xbe800000, v33
	v_fmac_f32_e32 v28, 0x42800000, v29
	v_fmamk_f32 v28, v28, 0x3b800000, v142
	v_mul_f32_e32 v29, 0x4f800000, v28
	v_cmp_gt_f32_e32 vcc, s74, v28
	v_fmac_f32_e32 v15, 0xbe800000, v33
	v_fmac_f32_e32 v14, 0xbe800000, v33
	v_cndmask_b32_e32 v28, v28, v29, vcc
	v_sqrt_f32_e32 v29, v28
	v_fmac_f32_e32 v13, 0xbe800000, v33
	v_fmac_f32_e32 v12, 0xbe800000, v33
	v_fmac_f32_e32 v11, 0xbe800000, v33
	v_add_u32_e32 v30, -1, v29
	v_add_u32_e32 v31, 1, v29
	v_fma_f32 v32, -v30, v29, v28
	v_fma_f32 v34, -v31, v29, v28
	v_cmp_ge_f32_e64 s[4:5], 0, v32
	v_fmac_f32_e32 v10, 0xbe800000, v33
	v_fmac_f32_e32 v3, 0xbe800000, v33
	v_cndmask_b32_e64 v29, v29, v30, s[4:5]
	v_cmp_lt_f32_e64 s[4:5], 0, v34
	v_fmac_f32_e32 v2, 0xbe800000, v33
	v_fmac_f32_e32 v7, 0xbe800000, v33
	v_cndmask_b32_e64 v29, v29, v31, s[4:5]
	v_mul_f32_e32 v30, 0x37800000, v29
	v_cndmask_b32_e32 v29, v29, v30, vcc
	v_cmp_class_f32_e32 vcc, v28, v143
	v_fmac_f32_e32 v6, 0xbe800000, v33
	v_fmac_f32_e32 v5, 0xbe800000, v33
	v_cndmask_b32_e32 v28, v29, v28, vcc
	v_div_scale_f32 v29, s[4:5], v28, v28, 1.0
	v_rcp_f32_e32 v30, v29
	v_div_scale_f32 v31, vcc, 1.0, v28, 1.0
	v_fmac_f32_e32 v4, 0xbe800000, v33
	v_fma_f32 v32, -v29, v30, 1.0
	v_fmac_f32_e32 v30, v32, v30
	v_mul_f32_e32 v32, v31, v30
	v_fma_f32 v34, -v29, v32, v31
	v_fmac_f32_e32 v32, v34, v30
	v_fma_f32 v29, -v29, v32, v31
	v_div_fmas_f32 v29, v29, v30, v32
	v_div_fixup_f32 v28, v29, v28, 1.0
	v_pk_mul_f32 v[8:9], v[8:9], v[28:29] op_sel_hi:[1,0]
	v_pk_mul_f32 v[12:13], v[12:13], v[28:29] op_sel_hi:[1,0]
	v_pk_mul_f32 v[14:15], v[14:15], v[28:29] op_sel_hi:[1,0]
	v_pk_mul_f32 v[10:11], v[10:11], v[28:29] op_sel_hi:[1,0]
	v_fmac_f32_e32 v1, 0xbe800000, v33
	v_fmac_f32_e32 v0, 0xbe800000, v33
	s_andn2_b64 vcc, exec, s[50:51]
	s_mov_b64 s[4:5], -1
	s_waitcnt vmcnt(2)
	v_lshlrev_b32_e32 v31, 16, v22
	v_and_b32_e32 v22, 0xffff0000, v22
	s_waitcnt vmcnt(0)
	v_pk_mul_f32 v[8:9], v[24:25], v[8:9]
	v_lshlrev_b32_e32 v29, 16, v20
	v_and_b32_e32 v20, 0xffff0000, v20
	v_lshlrev_b32_e32 v30, 16, v21
	v_and_b32_e32 v21, 0xffff0000, v21
	v_lshlrev_b32_e32 v32, 16, v23
	v_pk_mul_f32 v[14:15], v[18:19], v[14:15]
	v_pk_mul_f32 v[12:13], v[16:17], v[12:13]
	v_pk_mul_f32 v[10:11], v[26:27], v[10:11]
	v_mul_f32_e32 v16, v8, v31
	v_mul_f32_e32 v17, v9, v22
	v_mul_f32_e32 v12, v12, v29
	v_mul_f32_e32 v13, v13, v20
	v_mul_f32_e32 v14, v14, v30
	v_mul_f32_e32 v15, v15, v21
	v_mul_f32_e32 v18, v10, v32
	v_cvt_pk_bf16_f32 v8, v12, v13
	v_cvt_pk_bf16_f32 v9, v14, v15
	v_cvt_pk_bf16_f32 v10, v16, v17
	v_lshlrev_b64 v[16:17], 12, v[38:39]
	v_and_b32_e32 v23, 0xffff0000, v23
	v_lshl_add_u64 v[16:17], s[30:31], 0, v[16:17]
	v_mul_f32_e32 v11, v11, v23
	v_lshl_add_u64 v[20:21], v[16:17], 0, v[132:133]
	v_cvt_pk_bf16_f32 v11, v18, v11
	global_store_dwordx4 v[20:21], v[8:11], off offset:2048 sc1
	global_load_dwordx4 v[12:15], v[40:41], off offset:256
	s_nop 0
	global_load_dwordx4 v[8:11], v[130:131], off offset:512
	global_load_dwordx4 v[16:19], v[130:131], off offset:528
	v_pk_mul_f32 v[2:3], v[2:3], v[28:29] op_sel_hi:[1,0]
	v_pk_mul_f32 v[4:5], v[4:5], v[28:29] op_sel_hi:[1,0]
	v_pk_mul_f32 v[6:7], v[6:7], v[28:29] op_sel_hi:[1,0]
	v_pk_mul_f32 v[0:1], v[0:1], v[28:29] op_sel_hi:[1,0]
	s_waitcnt vmcnt(2)
	v_lshlrev_b32_e32 v25, 16, v15
	v_and_b32_e32 v15, 0xffff0000, v15
	s_waitcnt vmcnt(0)
	v_pk_mul_f32 v[2:3], v[18:19], v[2:3]
	v_lshlrev_b32_e32 v22, 16, v12
	v_and_b32_e32 v12, 0xffff0000, v12
	v_lshlrev_b32_e32 v23, 16, v13
	v_and_b32_e32 v13, 0xffff0000, v13
	v_lshlrev_b32_e32 v24, 16, v14
	v_and_b32_e32 v14, 0xffff0000, v14
	v_pk_mul_f32 v[6:7], v[10:11], v[6:7]
	v_pk_mul_f32 v[4:5], v[8:9], v[4:5]
	v_pk_mul_f32 v[0:1], v[16:17], v[0:1]
	v_mul_f32_e32 v3, v3, v15
	v_mul_f32_e32 v4, v4, v22
	v_mul_f32_e32 v5, v5, v12
	v_mul_f32_e32 v6, v6, v23
	v_mul_f32_e32 v7, v7, v13
	v_mul_f32_e32 v8, v0, v24
	v_mul_f32_e32 v9, v1, v14
	v_mul_f32_e32 v10, v2, v25
	v_cvt_pk_bf16_f32 v0, v4, v5
	v_cvt_pk_bf16_f32 v1, v6, v7
	v_cvt_pk_bf16_f32 v2, v8, v9
	v_cvt_pk_bf16_f32 v3, v10, v3
	global_store_dwordx4 v[20:21], v[0:3], off offset:2304 sc1
	s_waitcnt lgkmcnt(0)
	s_barrier
	s_cbranch_vccnz .LBB0_1053
	s_andn2_b64 vcc, exec, s[6:7]
	s_cbranch_vccnz .LBB0_1052
	s_barrier
	s_branch .LBB0_1052

.LBB0_1129:
	v_ashrrev_i32_e32 v139, 31, v138
	v_lshl_add_u64 v[138:139], s[34:35], 0, v[138:139]
	v_lshlrev_b64 v[138:139], 11, v[138:139]
	v_lshl_add_u64 v[184:185], v[136:137], 0, v[138:139]
	v_add_u32_e32 v139, 0x200, v180
	v_ashrrev_i32_e32 v138, 7, v139
	v_lshrrev_b32_e32 v186, 7, v139
	v_mul_lo_u32 v139, v138, s22
	v_add_u32_e32 v187, 0, v139
	v_bitop3_b32 v139, v186, v134, 24 bitop3:0x6c
	v_lshl_add_u32 v180, v138, 2, s2
	v_lshl_add_u32 v181, v139, 1, v187
	ds_read_b32 v139, v180 offset:1024
	ds_read_b128 v[180:183], v181
	global_store_dwordx4 v[184:185], v[128:131], off nt sc1
	s_and_b64 vcc, exec, s[8:9]
	s_waitcnt lgkmcnt(0)
	v_lshlrev_b32_e32 v184, 16, v180
	v_bitop3_b32 v128, v186, v143, 24 bitop3:0x6c
	v_lshl_add_u32 v128, v128, 1, v187
	ds_read_b128 v[128:131], v128
	v_and_b32_e32 v180, 0xffff0000, v180
	v_mul_f32_e32 v194, v139, v184
	v_mul_f32_e32 v195, v139, v180
	v_lshlrev_b32_e32 v193, 16, v181
	v_and_b32_e32 v192, 0xffff0000, v181
	v_lshlrev_b32_e32 v191, 16, v182
	v_and_b32_e32 v190, 0xffff0000, v182
	v_lshlrev_b32_e32 v189, 16, v183
	v_and_b32_e32 v188, 0xffff0000, v183
	s_waitcnt lgkmcnt(0)
	v_lshlrev_b32_e32 v187, 16, v128
	v_and_b32_e32 v186, 0xffff0000, v128
	v_lshlrev_b32_e32 v185, 16, v129
	v_and_b32_e32 v184, 0xffff0000, v129
	v_lshlrev_b32_e32 v183, 16, v130
	v_and_b32_e32 v182, 0xffff0000, v130
	v_lshlrev_b32_e32 v181, 16, v131
	v_and_b32_e32 v180, 0xffff0000, v131
	s_cbranch_vccnz .LBB0_1132
	v_mov_b32_e32 v128, 0
	v_cvt_pk_fp8_f32 v128, v194, v195
	v_mul_f32_e32 v196, v139, v191
	v_mul_f32_e32 v197, v139, v190
	v_mov_b32_e32 v129, 0
	v_cvt_pk_fp8_f32 v129, v196, v197
	v_mul_f32_e32 v130, v139, v193
	v_mul_f32_e32 v131, v139, v192
	v_cvt_pk_fp8_f32 v128, v130, v131 op_sel:[0,0,1]
	v_mul_f32_e32 v130, v139, v189
	v_mul_f32_e32 v131, v139, v188
	v_cvt_pk_fp8_f32 v129, v130, v131 op_sel:[0,0,1]
	v_mul_f32_e32 v131, v139, v187
	v_mul_f32_e32 v196, v139, v186
	v_mov_b32_e32 v130, 0
	v_cvt_pk_fp8_f32 v130, v131, v196
	v_mul_f32_e32 v198, v139, v183
	v_mul_f32_e32 v199, v139, v182
	v_mov_b32_e32 v131, 0
	v_cvt_pk_fp8_f32 v131, v198, v199
	v_mul_f32_e32 v196, v139, v185
	v_mul_f32_e32 v197, v139, v184
	v_cvt_pk_fp8_f32 v130, v196, v197 op_sel:[0,0,1]
	v_mul_f32_e32 v196, v139, v181
	v_mul_f32_e32 v197, v139, v180
	v_cvt_pk_fp8_f32 v131, v196, v197 op_sel:[0,0,1]
	s_cbranch_execnz .LBB0_1125
	s_branch .LBB0_1124

.LBB0_1160:
	v_ashrrev_i32_e32 v139, 31, v138
	v_lshl_add_u64 v[138:139], s[18:19], 0, v[138:139]
	v_lshlrev_b64 v[138:139], 11, v[138:139]
	s_addk_i32 s3, 0x400
	v_lshl_add_u64 v[138:139], v[136:137], 0, v[138:139]
	s_cmpk_lg_i32 s3, 0x1000
	global_store_dwordx4 v[138:139], v[128:131], off nt sc1
	s_cbranch_scc0 .LBB0_1139

; #define GAS __attribute__((address_space(1)))
; #define LAS __attribute__((address_space(3)))
; __device__ __forceinline__ void do_slabs_impl(LAS unsigned char* lds, unsigned char* ws, const float* w_up, const float* w_dn, const float* w_in, int vcu, int G, int wave, int j0, int j1) {
;     ...
;         if (done.valid) {
; #pragma unroll 2
;             for (int i = 0; i < 8; ++i) { const int q = tid + NTHR * i, n = q >> 7, kc = q & 127; const float inv = red[256 + n];
;                 const int sx_ = ((n >> 3) & 3) << 3;
;                 const v4u a = *(const LAS v4u*)(slab + n * PITCH + ((kc * 16) ^ sx_)), b = *(const LAS v4u*)(slab + n * PITCH + ((kc * 16 + 8) ^ sx_));
;                 const unsigned src[8] = {a.x, a.y, a.z, a.w, b.x, b.y, b.z, b.w}; unsigned o[4];
;                 if (done.fp8) {
; #pragma unroll
;                     for (int d = 0; d < 4; ++d) { int w = __builtin_amdgcn_cvt_pk_fp8_f32(bf_lo(src[2 * d]) * inv, bf_hi(src[2 * d]) * inv, 0, false);
;                         w = __builtin_amdgcn_cvt_pk_fp8_f32(bf_lo(src[2 * d + 1]) * inv, bf_hi(src[2 * d + 1]) * inv, w, true); o[d] = (unsigned)w; }
;                 } else {
; #pragma unroll
;                 for (int d = 0; d < 4; ++d) { unsigned w = 0u;
; #pragma unroll
;                     for (int h2 = 0; h2 < 2; ++h2) { const unsigned u2 = src[2 * d + h2]; const int q0 = (int)__builtin_rintf(bf_lo(u2) * inv), q1 = (int)__builtin_rintf(bf_hi(u2) * inv);
;                         w |= ((unsigned)(q0 & 0xff) << (16 * h2)) | ((unsigned)(q1 & 0xff) << (16 * h2 + 8)); }
;                     o[d] = w; }
;                 }
;                 __builtin_nontemporal_store((v4u){o[0], o[1], o[2], o[3]}, (GAS v4u*)(done.WQ + ((size_t)done.e * done.NS + done.n0 + n) * D + kc * 16)); }
.LBB0_1164:
	v_ashrrev_i32_e32 v139, 31, v138
	v_lshl_add_u64 v[138:139], s[18:19], 0, v[138:139]
	v_lshlrev_b64 v[138:139], 11, v[138:139]
	v_lshl_add_u64 v[184:185], v[136:137], 0, v[138:139]
	v_add_u32_e32 v139, 0x200, v180
	v_ashrrev_i32_e32 v138, 7, v139
	v_lshrrev_b32_e32 v186, 7, v139
	v_mul_lo_u32 v139, v138, s2
	v_add_u32_e32 v187, 0, v139
	v_bitop3_b32 v139, v186, v134, 24 bitop3:0x6c
	v_lshl_add_u32 v180, v138, 2, s1
	v_lshl_add_u32 v181, v139, 1, v187
	ds_read_b32 v139, v180 offset:1024
	ds_read_b128 v[180:183], v181
	global_store_dwordx4 v[184:185], v[128:131], off nt sc1
	s_and_b64 vcc, exec, s[8:9]
	s_waitcnt lgkmcnt(0)
	v_lshlrev_b32_e32 v184, 16, v180
	v_bitop3_b32 v128, v186, v143, 24 bitop3:0x6c
	v_lshl_add_u32 v128, v128, 1, v187
	ds_read_b128 v[128:131], v128
	v_and_b32_e32 v180, 0xffff0000, v180
	v_mul_f32_e32 v194, v139, v184
	v_mul_f32_e32 v195, v139, v180
	v_lshlrev_b32_e32 v193, 16, v181
	v_and_b32_e32 v192, 0xffff0000, v181
	v_lshlrev_b32_e32 v191, 16, v182
	v_and_b32_e32 v190, 0xffff0000, v182
	v_lshlrev_b32_e32 v189, 16, v183
	v_and_b32_e32 v188, 0xffff0000, v183
	s_waitcnt lgkmcnt(0)
	v_lshlrev_b32_e32 v187, 16, v128
	v_and_b32_e32 v186, 0xffff0000, v128
	v_lshlrev_b32_e32 v185, 16, v129
	v_and_b32_e32 v184, 0xffff0000, v129
	v_lshlrev_b32_e32 v183, 16, v130
	v_and_b32_e32 v182, 0xffff0000, v130
	v_lshlrev_b32_e32 v181, 16, v131
	v_and_b32_e32 v180, 0xffff0000, v131
	s_cbranch_vccnz .LBB0_1167
	v_mov_b32_e32 v128, 0
	v_cvt_pk_fp8_f32 v128, v194, v195
	v_mul_f32_e32 v196, v139, v191
	v_mul_f32_e32 v197, v139, v190
	v_mov_b32_e32 v129, 0
	v_cvt_pk_fp8_f32 v129, v196, v197
	v_mul_f32_e32 v130, v139, v193
	v_mul_f32_e32 v131, v139, v192
	v_cvt_pk_fp8_f32 v128, v130, v131 op_sel:[0,0,1]
	v_mul_f32_e32 v130, v139, v189
	v_mul_f32_e32 v131, v139, v188
	v_cvt_pk_fp8_f32 v129, v130, v131 op_sel:[0,0,1]
	v_mul_f32_e32 v131, v139, v187
	v_mul_f32_e32 v196, v139, v186
	v_mov_b32_e32 v130, 0
	v_cvt_pk_fp8_f32 v130, v131, v196
	v_mul_f32_e32 v198, v139, v183
	v_mul_f32_e32 v199, v139, v182
	v_mov_b32_e32 v131, 0
	v_cvt_pk_fp8_f32 v131, v198, v199
	v_mul_f32_e32 v196, v139, v185
	v_mul_f32_e32 v197, v139, v184
	v_cvt_pk_fp8_f32 v130, v196, v197 op_sel:[0,0,1]
	v_mul_f32_e32 v196, v139, v181
	v_mul_f32_e32 v197, v139, v180
	v_cvt_pk_fp8_f32 v131, v196, v197 op_sel:[0,0,1]
	s_cbranch_execnz .LBB0_1160
	s_branch .LBB0_1159

; #define GAS __attribute__((address_space(1)))
; #define LAS __attribute__((address_space(3)))
; __device__ __forceinline__ void do_slabs_impl(LAS unsigned char* lds, unsigned char* ws, const float* w_up, const float* w_dn, const float* w_in, int vcu, int G, int wave, int j0, int j1) {
;     ...
;         if (done.valid) {
; #pragma unroll 2
;             for (int i = 0; i < 8; ++i) { const int q = tid + NTHR * i, n = q >> 7, kc = q & 127; const float inv = red[256 + n];
;                 const int sx_ = ((n >> 3) & 3) << 3;
;                 const v4u a = *(const LAS v4u*)(slab + n * PITCH + ((kc * 16) ^ sx_)), b = *(const LAS v4u*)(slab + n * PITCH + ((kc * 16 + 8) ^ sx_));
;                 const unsigned src[8] = {a.x, a.y, a.z, a.w, b.x, b.y, b.z, b.w}; unsigned o[4];
;                 if (done.fp8) {
; #pragma unroll
;                     for (int d = 0; d < 4; ++d) { int w = __builtin_amdgcn_cvt_pk_fp8_f32(bf_lo(src[2 * d]) * inv, bf_hi(src[2 * d]) * inv, 0, false);
;                         w = __builtin_amdgcn_cvt_pk_fp8_f32(bf_lo(src[2 * d + 1]) * inv, bf_hi(src[2 * d + 1]) * inv, w, true); o[d] = (unsigned)w; }
;                 } else {
; #pragma unroll
;                 for (int d = 0; d < 4; ++d) { unsigned w = 0u;
; #pragma unroll
;                     for (int h2 = 0; h2 < 2; ++h2) { const unsigned u2 = src[2 * d + h2]; const int q0 = (int)__builtin_rintf(bf_lo(u2) * inv), q1 = (int)__builtin_rintf(bf_hi(u2) * inv);
;                         w |= ((unsigned)(q0 & 0xff) << (16 * h2)) | ((unsigned)(q1 & 0xff) << (16 * h2 + 8)); }
;                     o[d] = w; }
;                 }
;                 __builtin_nontemporal_store((v4u){o[0], o[1], o[2], o[3]}, (GAS v4u*)(done.WQ + ((size_t)done.e * done.NS + done.n0 + n) * D + kc * 16)); }
.LBB0_1252:
	v_ashrrev_i32_e32 v139, 31, v138
	v_lshl_add_u64 v[138:139], s[36:37], 0, v[138:139]
	v_lshlrev_b64 v[138:139], 11, v[138:139]
	v_lshl_add_u64 v[184:185], v[136:137], 0, v[138:139]
	v_add_u32_e32 v139, 0x200, v180
	v_ashrrev_i32_e32 v138, 7, v139
	v_lshrrev_b32_e32 v186, 7, v139
	v_mul_lo_u32 v139, v138, s3
	v_add_u32_e32 v187, 0, v139
	v_bitop3_b32 v139, v186, v134, 24 bitop3:0x6c
	v_lshl_add_u32 v180, v138, 2, s2
	v_lshl_add_u32 v181, v139, 1, v187
	ds_read_b32 v139, v180 offset:1024
	ds_read_b128 v[180:183], v181
	global_store_dwordx4 v[184:185], v[128:131], off nt sc1
	s_and_b64 vcc, exec, s[8:9]
	s_waitcnt lgkmcnt(0)
	v_lshlrev_b32_e32 v184, 16, v180
	v_bitop3_b32 v128, v186, v143, 24 bitop3:0x6c
	v_lshl_add_u32 v128, v128, 1, v187
	ds_read_b128 v[128:131], v128
	v_and_b32_e32 v180, 0xffff0000, v180
	v_mul_f32_e32 v194, v139, v184
	v_mul_f32_e32 v195, v139, v180
	v_lshlrev_b32_e32 v193, 16, v181
	v_and_b32_e32 v192, 0xffff0000, v181
	v_lshlrev_b32_e32 v191, 16, v182
	v_and_b32_e32 v190, 0xffff0000, v182
	v_lshlrev_b32_e32 v189, 16, v183
	v_and_b32_e32 v188, 0xffff0000, v183
	s_waitcnt lgkmcnt(0)
	v_lshlrev_b32_e32 v187, 16, v128
	v_and_b32_e32 v186, 0xffff0000, v128
	v_lshlrev_b32_e32 v185, 16, v129
	v_and_b32_e32 v184, 0xffff0000, v129
	v_lshlrev_b32_e32 v183, 16, v130
	v_and_b32_e32 v182, 0xffff0000, v130
	v_lshlrev_b32_e32 v181, 16, v131
	v_and_b32_e32 v180, 0xffff0000, v131
	s_cbranch_vccnz .LBB0_1255
	v_mov_b32_e32 v128, 0
	v_cvt_pk_fp8_f32 v128, v194, v195
	v_mul_f32_e32 v196, v139, v191
	v_mul_f32_e32 v197, v139, v190
	v_mov_b32_e32 v129, 0
	v_cvt_pk_fp8_f32 v129, v196, v197
	v_mul_f32_e32 v130, v139, v193
	v_mul_f32_e32 v131, v139, v192
	v_cvt_pk_fp8_f32 v128, v130, v131 op_sel:[0,0,1]
	v_mul_f32_e32 v130, v139, v189
	v_mul_f32_e32 v131, v139, v188
	v_cvt_pk_fp8_f32 v129, v130, v131 op_sel:[0,0,1]
	v_mul_f32_e32 v131, v139, v187
	v_mul_f32_e32 v196, v139, v186
	v_mov_b32_e32 v130, 0
	v_cvt_pk_fp8_f32 v130, v131, v196
	v_mul_f32_e32 v198, v139, v183
	v_mul_f32_e32 v199, v139, v182
	v_mov_b32_e32 v131, 0
	v_cvt_pk_fp8_f32 v131, v198, v199
	v_mul_f32_e32 v196, v139, v185
	v_mul_f32_e32 v197, v139, v184
	v_cvt_pk_fp8_f32 v130, v196, v197 op_sel:[0,0,1]
	v_mul_f32_e32 v196, v139, v181
	v_mul_f32_e32 v197, v139, v180
	v_cvt_pk_fp8_f32 v131, v196, v197 op_sel:[0,0,1]
	s_cbranch_execnz .LBB0_1248
	s_branch .LBB0_1247

; #define GAS __attribute__((address_space(1)))
; #define LAS __attribute__((address_space(3)))
; __device__ __forceinline__ void do_slabs_impl(LAS unsigned char* lds, unsigned char* ws, const float* w_up, const float* w_dn, const float* w_in, int vcu, int G, int wave, int j0, int j1) {
;     ...
;             for (int i = 0; i < 8; ++i) { const int q = tid + NTHR * i, n = q >> 7, kc = q & 127; const float inv = red[256 + n];
;                 const int sx_ = ((n >> 3) & 3) << 3;
;                 const v4u a = *(const LAS v4u*)(slab + n * PITCH + ((kc * 16) ^ sx_)), b = *(const LAS v4u*)(slab + n * PITCH + ((kc * 16 + 8) ^ sx_));
;                 const unsigned src[8] = {a.x, a.y, a.z, a.w, b.x, b.y, b.z, b.w}; unsigned o[4];
;                 if (done.fp8) {
; #pragma unroll
;                     for (int d = 0; d < 4; ++d) { int w = __builtin_amdgcn_cvt_pk_fp8_f32(bf_lo(src[2 * d]) * inv, bf_hi(src[2 * d]) * inv, 0, false);
;                         w = __builtin_amdgcn_cvt_pk_fp8_f32(bf_lo(src[2 * d + 1]) * inv, bf_hi(src[2 * d + 1]) * inv, w, true); o[d] = (unsigned)w; }
;                 } else {
; #pragma unroll
;                 for (int d = 0; d < 4; ++d) { unsigned w = 0u;
; #pragma unroll
;                     for (int h2 = 0; h2 < 2; ++h2) { const unsigned u2 = src[2 * d + h2]; const int q0 = (int)__builtin_rintf(bf_lo(u2) * inv), q1 = (int)__builtin_rintf(bf_hi(u2) * inv);
;                         w |= ((unsigned)(q0 & 0xff) << (16 * h2)) | ((unsigned)(q1 & 0xff) << (16 * h2 + 8)); }
;                     o[d] = w; }
;                 }
;                 __builtin_nontemporal_store((v4u){o[0], o[1], o[2], o[3]}, (GAS v4u*)(done.WQ + ((size_t)done.e * done.NS + done.n0 + n) * D + kc * 16)); }
.LBB0_1292:
	v_ashrrev_i32_e32 v137, 31, v136
	v_lshl_add_u64 v[136:137], s[52:53], 0, v[136:137]
	v_lshlrev_b64 v[136:137], 11, v[136:137]
	s_addk_i32 s60, 0x400
	v_lshl_add_u64 v[136:137], v[134:135], 0, v[136:137]
	s_cmpk_lg_i32 s60, 0x1000
	global_store_dwordx4 v[136:137], v[128:131], off nt sc1
	s_cbranch_scc0 .LBB0_1271

; #define GAS __attribute__((address_space(1)))
; #define LAS __attribute__((address_space(3)))
; __device__ __forceinline__ void do_slabs_impl(LAS unsigned char* lds, unsigned char* ws, const float* w_up, const float* w_dn, const float* w_in, int vcu, int G, int wave, int j0, int j1) {
;     ...
;         if (done.valid) {
; #pragma unroll 2
;             for (int i = 0; i < 8; ++i) { const int q = tid + NTHR * i, n = q >> 7, kc = q & 127; const float inv = red[256 + n];
;                 const int sx_ = ((n >> 3) & 3) << 3;
;                 const v4u a = *(const LAS v4u*)(slab + n * PITCH + ((kc * 16) ^ sx_)), b = *(const LAS v4u*)(slab + n * PITCH + ((kc * 16 + 8) ^ sx_));
;                 const unsigned src[8] = {a.x, a.y, a.z, a.w, b.x, b.y, b.z, b.w}; unsigned o[4];
;                 if (done.fp8) {
; #pragma unroll
;                     for (int d = 0; d < 4; ++d) { int w = __builtin_amdgcn_cvt_pk_fp8_f32(bf_lo(src[2 * d]) * inv, bf_hi(src[2 * d]) * inv, 0, false);
;                         w = __builtin_amdgcn_cvt_pk_fp8_f32(bf_lo(src[2 * d + 1]) * inv, bf_hi(src[2 * d + 1]) * inv, w, true); o[d] = (unsigned)w; }
;                 } else {
; #pragma unroll
;                 for (int d = 0; d < 4; ++d) { unsigned w = 0u;
; #pragma unroll
;                     for (int h2 = 0; h2 < 2; ++h2) { const unsigned u2 = src[2 * d + h2]; const int q0 = (int)__builtin_rintf(bf_lo(u2) * inv), q1 = (int)__builtin_rintf(bf_hi(u2) * inv);
;                         w |= ((unsigned)(q0 & 0xff) << (16 * h2)) | ((unsigned)(q1 & 0xff) << (16 * h2 + 8)); }
;                     o[d] = w; }
;                 }
;                 __builtin_nontemporal_store((v4u){o[0], o[1], o[2], o[3]}, (GAS v4u*)(done.WQ + ((size_t)done.e * done.NS + done.n0 + n) * D + kc * 16)); }
.LBB0_1296:
	v_ashrrev_i32_e32 v137, 31, v136
	v_lshl_add_u64 v[136:137], s[52:53], 0, v[136:137]
	v_lshlrev_b64 v[136:137], 11, v[136:137]
	v_lshl_add_u64 v[186:187], v[134:135], 0, v[136:137]
	v_add_u32_e32 v137, 0x200, v181
	v_ashrrev_i32_e32 v136, 7, v137
	v_lshrrev_b32_e32 v188, 7, v137
	v_mul_lo_u32 v137, v136, s82
	v_add_u32_e32 v189, 0, v137
	v_bitop3_b32 v137, v188, v144, 24 bitop3:0x6c
	v_lshl_add_u32 v181, v136, 2, s2
	v_lshl_add_u32 v182, v137, 1, v189
	ds_read_b32 v137, v181 offset:1024
	ds_read_b128 v[182:185], v182
	global_store_dwordx4 v[186:187], v[128:131], off nt sc1
	s_and_b64 vcc, exec, s[8:9]
	s_waitcnt lgkmcnt(0)
	v_lshlrev_b32_e32 v181, 16, v182
	v_bitop3_b32 v128, v188, v142, 24 bitop3:0x6c
	v_lshl_add_u32 v128, v128, 1, v189
	ds_read_b128 v[128:131], v128
	v_mul_f32_e32 v195, v137, v181
	v_and_b32_e32 v181, 0xffff0000, v182
	v_mul_f32_e32 v196, v137, v181
	v_lshlrev_b32_e32 v194, 16, v183
	v_and_b32_e32 v193, 0xffff0000, v183
	v_lshlrev_b32_e32 v192, 16, v184
	v_and_b32_e32 v191, 0xffff0000, v184
	v_lshlrev_b32_e32 v190, 16, v185
	v_and_b32_e32 v189, 0xffff0000, v185
	s_waitcnt lgkmcnt(0)
	v_lshlrev_b32_e32 v188, 16, v128
	v_and_b32_e32 v187, 0xffff0000, v128
	v_lshlrev_b32_e32 v186, 16, v129
	v_and_b32_e32 v185, 0xffff0000, v129
	v_lshlrev_b32_e32 v184, 16, v130
	v_and_b32_e32 v183, 0xffff0000, v130
	v_lshlrev_b32_e32 v182, 16, v131
	v_and_b32_e32 v181, 0xffff0000, v131
	s_cbranch_vccnz .LBB0_1299
	v_mov_b32_e32 v128, v145
	v_cvt_pk_fp8_f32 v128, v195, v196
	v_mul_f32_e32 v197, v137, v192
	v_mul_f32_e32 v198, v137, v191
	v_mov_b32_e32 v129, v145
	v_cvt_pk_fp8_f32 v129, v197, v198
	v_mul_f32_e32 v130, v137, v194
	v_mul_f32_e32 v131, v137, v193
	v_cvt_pk_fp8_f32 v128, v130, v131 op_sel:[0,0,1]
	v_mul_f32_e32 v130, v137, v190
	v_mul_f32_e32 v131, v137, v189
	v_cvt_pk_fp8_f32 v129, v130, v131 op_sel:[0,0,1]
	v_mul_f32_e32 v131, v137, v188
	v_mul_f32_e32 v197, v137, v187
	v_mov_b32_e32 v130, v145
	v_cvt_pk_fp8_f32 v130, v131, v197
	v_mul_f32_e32 v199, v137, v184
	v_mul_f32_e32 v200, v137, v183
	v_mov_b32_e32 v131, v145
	v_cvt_pk_fp8_f32 v131, v199, v200
	v_mul_f32_e32 v197, v137, v186
	v_mul_f32_e32 v198, v137, v185
	v_cvt_pk_fp8_f32 v130, v197, v198 op_sel:[0,0,1]
	v_mul_f32_e32 v197, v137, v182
	v_mul_f32_e32 v198, v137, v181
	v_cvt_pk_fp8_f32 v131, v197, v198 op_sel:[0,0,1]
	s_cbranch_execnz .LBB0_1292
	s_branch .LBB0_1291

; #define GAS __attribute__((address_space(1)))
; #define LAS __attribute__((address_space(3)))
; __device__ __forceinline__ v4u pack8(const f32x4 a, const f32x4 b) { v4u w; w.x = cvt_pk_bf16(a[0], a[1]); w.y = cvt_pk_bf16(a[2], a[3]); w.z = cvt_pk_bf16(b[0], b[1]); w.w = cvt_pk_bf16(b[2], b[3]); return w; }
; #define EPI_LOOP_AM for (int ai = 0; ai < 2; ++ai) _Pragma("unroll") for (int m = 0; m < 4; ++m)
;     __device__ __forceinline__ void operator()(Acc& acc, const Unit& u, LAS unsigned char*, int wr, int wc, int fr, int fq) const {
;         const int colb = u.p1 * 256 + wc * 32 + 8 * fq;
; #pragma unroll
;         for (int bj = 0; bj < 2; ++bj) { const int col = colb + bj * 128;
;             const f32x4 ga = *(const GAS f32x4*)(g0 + col), gb = *(const GAS f32x4*)(g0 + col + 4), ba = *(const GAS f32x4*)(b0 + col), bb = *(const GAS f32x4*)(b0 + col + 4);
; #pragma unroll
;             EPI_LOOP_AM { const int row = u.p0 * 256 + 128 * ai + 64 * wr + 16 * m + fr; const f32x2 st = *(const GAS f32x2*)(st0 + 2 * row); const size_t off = (size_t)row * D + col;
;                 const f32x4 xa = *(const GAS f32x4*)(x + off), xb = *(const GAS f32x4*)(x + off + 4);
;                 *(GAS v4u*)(z1 + off) = pack8(((xa - st.x) * st.y * ga + ba) * ALPHA + acc[ai][bj][m][0], ((xb - st.x) * st.y * gb + bb) * ALPHA + acc[ai][bj][m][1]); } }
;     }
.LBB0_1325:
	s_lshl_b32 s1, s92, 8
	s_or_b32 s1, s1, s80
	s_andn2_b64 vcc, exec, s[60:61]
	v_lshl_add_u32 v146, v171, 3, s1
	s_lshl_b32 s1, s62, 8
	s_add_i32 s1, s1, s78
	v_add_u32_e32 v164, s1, v170
	s_mov_b64 s[60:61], -1
	v_lshl_add_u32 v158, v164, 11, v146
	v_lshlrev_b32_e32 v160, 3, v164
	v_lshlrev_b32_e32 v161, 2, v146
	v_lshlrev_b32_e32 v159, 1, v158
	v_lshlrev_b32_e32 v158, 2, v158
	global_load_dwordx4 v[136:139], v161, s[14:15]
	global_load_dwordx4 v[128:131], v161, s[14:15] offset:16
	global_load_dwordx4 v[132:135], v161, s[16:17]
	global_load_dwordx4 v[140:143], v161, s[16:17] offset:16
	global_load_dwordx2 v[182:183], v160, s[40:41]
	global_load_dwordx4 v[196:199], v158, s[12:13]
	global_load_dwordx4 v[200:203], v158, s[12:13] offset:16
	s_add_u32 s98, s12, 0x20000
	s_addc_u32 s99, s13, 0
	global_load_dwordx2 v[184:185], v160, s[40:41] offset:128
	global_load_dwordx4 v[204:207], v158, s[98:99]
	global_load_dwordx4 v[208:211], v158, s[98:99] offset:16
	s_add_u32 s98, s12, 0x40000
	s_addc_u32 s99, s13, 0
	global_load_dwordx2 v[186:187], v160, s[40:41] offset:256
	global_load_dwordx4 v[212:215], v158, s[98:99]
	global_load_dwordx4 v[216:219], v158, s[98:99] offset:16
	s_add_u32 s98, s12, 0x60000
	s_addc_u32 s99, s13, 0
	global_load_dwordx2 v[148:149], v160, s[40:41] offset:384
	global_load_dwordx4 v[220:223], v158, s[98:99]
	global_load_dwordx4 v[224:227], v158, s[98:99] offset:16
	s_add_u32 s98, s12, 0x100000
	s_addc_u32 s99, s13, 0
	global_load_dwordx2 v[150:151], v160, s[40:41] offset:1024
	global_load_dwordx4 v[228:231], v158, s[98:99]
	global_load_dwordx4 v[232:235], v158, s[98:99] offset:16
	s_add_u32 s98, s12, 0x120000
	s_addc_u32 s99, s13, 0
	global_load_dwordx2 v[152:153], v160, s[40:41] offset:1152
	global_load_dwordx4 v[236:239], v158, s[98:99]
	global_load_dwordx4 v[240:243], v158, s[98:99] offset:16
	s_add_u32 s98, s12, 0x140000
	s_addc_u32 s99, s13, 0
	global_load_dwordx2 v[154:155], v160, s[40:41] offset:1280
	global_load_dwordx4 v[244:247], v158, s[98:99]
	global_load_dwordx4 v[248:251], v158, s[98:99] offset:16
	s_add_u32 s98, s12, 0x160000
	s_addc_u32 s99, s13, 0
	global_load_dwordx2 v[156:157], v160, s[40:41] offset:1408
	global_load_dwordx4 v[174:177], v158, s[98:99]
	global_load_dwordx4 v[178:181], v158, s[98:99] offset:16
	s_waitcnt vmcnt(21)
	v_sub_f32_e32 v196, v196, v182
	v_sub_f32_e32 v197, v197, v182
	v_sub_f32_e32 v198, v198, v182
	v_sub_f32_e32 v199, v199, v182
	v_sub_f32_e32 v200, v200, v182
	v_sub_f32_e32 v201, v201, v182
	v_sub_f32_e32 v202, v202, v182
	v_sub_f32_e32 v203, v203, v182
	v_pk_mul_f32 v[196:197], v[182:183], v[196:197] op_sel:[1,0]
	v_pk_mul_f32 v[198:199], v[182:183], v[198:199] op_sel:[1,0]
	v_pk_mul_f32 v[200:201], v[182:183], v[200:201] op_sel:[1,0]
	v_pk_mul_f32 v[202:203], v[182:183], v[202:203] op_sel:[1,0]
	v_pk_fma_f32 v[196:197], v[136:137], v[196:197], v[132:133]
	v_pk_fma_f32 v[198:199], v[138:139], v[198:199], v[134:135]
	v_pk_fma_f32 v[200:201], v[128:129], v[200:201], v[140:141]
	v_pk_fma_f32 v[202:203], v[130:131], v[202:203], v[142:143]
	v_pk_fma_f32 v[124:125], v[196:197], s[50:51], v[124:125] op_sel_hi:[1,0,1]
	v_pk_fma_f32 v[126:127], v[198:199], s[50:51], v[126:127] op_sel_hi:[1,0,1]
	v_pk_fma_f32 v[120:121], v[200:201], s[50:51], v[120:121] op_sel_hi:[1,0,1]
	v_pk_fma_f32 v[122:123], v[202:203], s[50:51], v[122:123] op_sel_hi:[1,0,1]
	v_cvt_pk_bf16_f32 v196, v124, v125
	v_cvt_pk_bf16_f32 v197, v126, v127
	v_cvt_pk_bf16_f32 v198, v120, v121
	v_cvt_pk_bf16_f32 v199, v122, v123
	global_store_dwordx4 v159, v[196:199], s[38:39] sc1
	s_waitcnt vmcnt(19)
	v_sub_f32_e32 v204, v204, v184
	v_sub_f32_e32 v205, v205, v184
	v_sub_f32_e32 v206, v206, v184
	v_sub_f32_e32 v207, v207, v184
	v_sub_f32_e32 v208, v208, v184
	v_sub_f32_e32 v209, v209, v184
	v_sub_f32_e32 v210, v210, v184
	v_sub_f32_e32 v211, v211, v184
	v_pk_mul_f32 v[204:205], v[184:185], v[204:205] op_sel:[1,0]
	v_pk_mul_f32 v[206:207], v[184:185], v[206:207] op_sel:[1,0]
	v_pk_mul_f32 v[208:209], v[184:185], v[208:209] op_sel:[1,0]
	v_pk_mul_f32 v[210:211], v[184:185], v[210:211] op_sel:[1,0]
	v_pk_fma_f32 v[204:205], v[136:137], v[204:205], v[132:133]
	v_pk_fma_f32 v[206:207], v[138:139], v[206:207], v[134:135]
	v_pk_fma_f32 v[208:209], v[128:129], v[208:209], v[140:141]
	v_pk_fma_f32 v[210:211], v[130:131], v[210:211], v[142:143]
	v_pk_fma_f32 v[116:117], v[204:205], s[50:51], v[116:117] op_sel_hi:[1,0,1]
	v_pk_fma_f32 v[118:119], v[206:207], s[50:51], v[118:119] op_sel_hi:[1,0,1]
	v_pk_fma_f32 v[112:113], v[208:209], s[50:51], v[112:113] op_sel_hi:[1,0,1]
	v_pk_fma_f32 v[114:115], v[210:211], s[50:51], v[114:115] op_sel_hi:[1,0,1]
	v_cvt_pk_bf16_f32 v204, v116, v117
	v_cvt_pk_bf16_f32 v205, v118, v119
	v_cvt_pk_bf16_f32 v206, v112, v113
	v_cvt_pk_bf16_f32 v207, v114, v115
	s_add_u32 s100, s38, 0x10000
	s_addc_u32 s101, s39, 0
	global_store_dwordx4 v159, v[204:207], s[100:101] sc1
	s_waitcnt vmcnt(17)
	v_sub_f32_e32 v212, v212, v186
	v_sub_f32_e32 v213, v213, v186
	v_sub_f32_e32 v214, v214, v186
	v_sub_f32_e32 v215, v215, v186
	v_sub_f32_e32 v216, v216, v186
	v_sub_f32_e32 v217, v217, v186
	v_sub_f32_e32 v218, v218, v186
	v_sub_f32_e32 v219, v219, v186
	v_pk_mul_f32 v[212:213], v[186:187], v[212:213] op_sel:[1,0]
	v_pk_mul_f32 v[214:215], v[186:187], v[214:215] op_sel:[1,0]
	v_pk_mul_f32 v[216:217], v[186:187], v[216:217] op_sel:[1,0]
	v_pk_mul_f32 v[218:219], v[186:187], v[218:219] op_sel:[1,0]
	v_pk_fma_f32 v[212:213], v[136:137], v[212:213], v[132:133]
	v_pk_fma_f32 v[214:215], v[138:139], v[214:215], v[134:135]
	v_pk_fma_f32 v[216:217], v[128:129], v[216:217], v[140:141]
	v_pk_fma_f32 v[218:219], v[130:131], v[218:219], v[142:143]
	v_pk_fma_f32 v[108:109], v[212:213], s[50:51], v[108:109] op_sel_hi:[1,0,1]
	v_pk_fma_f32 v[110:111], v[214:215], s[50:51], v[110:111] op_sel_hi:[1,0,1]
	v_pk_fma_f32 v[104:105], v[216:217], s[50:51], v[104:105] op_sel_hi:[1,0,1]
	v_pk_fma_f32 v[106:107], v[218:219], s[50:51], v[106:107] op_sel_hi:[1,0,1]
	v_cvt_pk_bf16_f32 v212, v108, v109
	v_cvt_pk_bf16_f32 v213, v110, v111
	v_cvt_pk_bf16_f32 v214, v104, v105
	v_cvt_pk_bf16_f32 v215, v106, v107
	s_add_u32 s100, s38, 0x20000
	s_addc_u32 s101, s39, 0
	global_store_dwordx4 v159, v[212:215], s[100:101] sc1
	s_waitcnt vmcnt(15)
; #define GAS __attribute__((address_space(1)))
; #define LAS __attribute__((address_space(3)))
; __device__ __forceinline__ v4u pack8(const f32x4 a, const f32x4 b) { v4u w; w.x = cvt_pk_bf16(a[0], a[1]); w.y = cvt_pk_bf16(a[2], a[3]); w.z = cvt_pk_bf16(b[0], b[1]); w.w = cvt_pk_bf16(b[2], b[3]); return w; }
; #define EPI_LOOP_AM for (int ai = 0; ai < 2; ++ai) _Pragma("unroll") for (int m = 0; m < 4; ++m)
;     __device__ __forceinline__ void operator()(Acc& acc, const Unit& u, LAS unsigned char*, int wr, int wc, int fr, int fq) const {
;         const int colb = u.p1 * 256 + wc * 32 + 8 * fq;
; #pragma unroll
;         for (int bj = 0; bj < 2; ++bj) { const int col = colb + bj * 128;
;             const f32x4 ga = *(const GAS f32x4*)(g0 + col), gb = *(const GAS f32x4*)(g0 + col + 4), ba = *(const GAS f32x4*)(b0 + col), bb = *(const GAS f32x4*)(b0 + col + 4);
; #pragma unroll
;             EPI_LOOP_AM { const int row = u.p0 * 256 + 128 * ai + 64 * wr + 16 * m + fr; const f32x2 st = *(const GAS f32x2*)(st0 + 2 * row); const size_t off = (size_t)row * D + col;
;                 const f32x4 xa = *(const GAS f32x4*)(x + off), xb = *(const GAS f32x4*)(x + off + 4);
;                 *(GAS v4u*)(z1 + off) = pack8(((xa - st.x) * st.y * ga + ba) * ALPHA + acc[ai][bj][m][0], ((xb - st.x) * st.y * gb + bb) * ALPHA + acc[ai][bj][m][1]); } }
;     }
	v_sub_f32_e32 v220, v220, v148
	v_sub_f32_e32 v221, v221, v148
	v_sub_f32_e32 v222, v222, v148
	v_sub_f32_e32 v223, v223, v148
	v_sub_f32_e32 v224, v224, v148
	v_sub_f32_e32 v225, v225, v148
	v_sub_f32_e32 v226, v226, v148
	v_sub_f32_e32 v227, v227, v148
	v_pk_mul_f32 v[220:221], v[148:149], v[220:221] op_sel:[1,0]
	v_pk_mul_f32 v[222:223], v[148:149], v[222:223] op_sel:[1,0]
	v_pk_mul_f32 v[224:225], v[148:149], v[224:225] op_sel:[1,0]
	v_pk_mul_f32 v[226:227], v[148:149], v[226:227] op_sel:[1,0]
	v_pk_fma_f32 v[220:221], v[136:137], v[220:221], v[132:133]
	v_pk_fma_f32 v[222:223], v[138:139], v[222:223], v[134:135]
	v_pk_fma_f32 v[224:225], v[128:129], v[224:225], v[140:141]
	v_pk_fma_f32 v[226:227], v[130:131], v[226:227], v[142:143]
	v_pk_fma_f32 v[100:101], v[220:221], s[50:51], v[100:101] op_sel_hi:[1,0,1]
	v_pk_fma_f32 v[102:103], v[222:223], s[50:51], v[102:103] op_sel_hi:[1,0,1]
	v_pk_fma_f32 v[96:97], v[224:225], s[50:51], v[96:97] op_sel_hi:[1,0,1]
	v_pk_fma_f32 v[98:99], v[226:227], s[50:51], v[98:99] op_sel_hi:[1,0,1]
	v_cvt_pk_bf16_f32 v220, v100, v101
	v_cvt_pk_bf16_f32 v221, v102, v103
	v_cvt_pk_bf16_f32 v222, v96, v97
	v_cvt_pk_bf16_f32 v223, v98, v99
	s_add_u32 s100, s38, 0x30000
	s_addc_u32 s101, s39, 0
	global_store_dwordx4 v159, v[220:223], s[100:101] sc1
	s_waitcnt vmcnt(13)
	v_sub_f32_e32 v228, v228, v150
	v_sub_f32_e32 v229, v229, v150
	v_sub_f32_e32 v230, v230, v150
	v_sub_f32_e32 v231, v231, v150
	v_sub_f32_e32 v232, v232, v150
	v_sub_f32_e32 v233, v233, v150
	v_sub_f32_e32 v234, v234, v150
	v_sub_f32_e32 v235, v235, v150
	v_pk_mul_f32 v[228:229], v[150:151], v[228:229] op_sel:[1,0]
	v_pk_mul_f32 v[230:231], v[150:151], v[230:231] op_sel:[1,0]
	v_pk_mul_f32 v[232:233], v[150:151], v[232:233] op_sel:[1,0]
	v_pk_mul_f32 v[234:235], v[150:151], v[234:235] op_sel:[1,0]
	v_pk_fma_f32 v[228:229], v[136:137], v[228:229], v[132:133]
	v_pk_fma_f32 v[230:231], v[138:139], v[230:231], v[134:135]
	v_pk_fma_f32 v[232:233], v[128:129], v[232:233], v[140:141]
	v_pk_fma_f32 v[234:235], v[130:131], v[234:235], v[142:143]
	v_pk_fma_f32 v[92:93], v[228:229], s[50:51], v[92:93] op_sel_hi:[1,0,1]
	v_pk_fma_f32 v[94:95], v[230:231], s[50:51], v[94:95] op_sel_hi:[1,0,1]
	v_pk_fma_f32 v[88:89], v[232:233], s[50:51], v[88:89] op_sel_hi:[1,0,1]
	v_pk_fma_f32 v[90:91], v[234:235], s[50:51], v[90:91] op_sel_hi:[1,0,1]
	v_cvt_pk_bf16_f32 v228, v92, v93
	v_cvt_pk_bf16_f32 v229, v94, v95
	v_cvt_pk_bf16_f32 v230, v88, v89
	v_cvt_pk_bf16_f32 v231, v90, v91
	s_add_u32 s100, s38, 0x80000
	s_addc_u32 s101, s39, 0
	global_store_dwordx4 v159, v[228:231], s[100:101] sc1
	s_waitcnt vmcnt(11)
	v_sub_f32_e32 v236, v236, v152
	v_sub_f32_e32 v237, v237, v152
	v_sub_f32_e32 v238, v238, v152
	v_sub_f32_e32 v239, v239, v152
	v_sub_f32_e32 v240, v240, v152
	v_sub_f32_e32 v241, v241, v152
	v_sub_f32_e32 v242, v242, v152
	v_sub_f32_e32 v243, v243, v152
	v_pk_mul_f32 v[236:237], v[152:153], v[236:237] op_sel:[1,0]
	v_pk_mul_f32 v[238:239], v[152:153], v[238:239] op_sel:[1,0]
	v_pk_mul_f32 v[240:241], v[152:153], v[240:241] op_sel:[1,0]
	v_pk_mul_f32 v[242:243], v[152:153], v[242:243] op_sel:[1,0]
	v_pk_fma_f32 v[236:237], v[136:137], v[236:237], v[132:133]
	v_pk_fma_f32 v[238:239], v[138:139], v[238:239], v[134:135]
	v_pk_fma_f32 v[240:241], v[128:129], v[240:241], v[140:141]
	v_pk_fma_f32 v[242:243], v[130:131], v[242:243], v[142:143]
	v_pk_fma_f32 v[84:85], v[236:237], s[50:51], v[84:85] op_sel_hi:[1,0,1]
	v_pk_fma_f32 v[86:87], v[238:239], s[50:51], v[86:87] op_sel_hi:[1,0,1]
	v_pk_fma_f32 v[80:81], v[240:241], s[50:51], v[80:81] op_sel_hi:[1,0,1]
	v_pk_fma_f32 v[82:83], v[242:243], s[50:51], v[82:83] op_sel_hi:[1,0,1]
	v_cvt_pk_bf16_f32 v236, v84, v85
	v_cvt_pk_bf16_f32 v237, v86, v87
	v_cvt_pk_bf16_f32 v238, v80, v81
	v_cvt_pk_bf16_f32 v239, v82, v83
	s_add_u32 s100, s38, 0x90000
	s_addc_u32 s101, s39, 0
	global_store_dwordx4 v159, v[236:239], s[100:101] sc1
	s_waitcnt vmcnt(9)
	v_sub_f32_e32 v244, v244, v154
	v_sub_f32_e32 v245, v245, v154
	v_sub_f32_e32 v246, v246, v154
	v_sub_f32_e32 v247, v247, v154
	v_sub_f32_e32 v248, v248, v154
	v_sub_f32_e32 v249, v249, v154
	v_sub_f32_e32 v250, v250, v154
	v_sub_f32_e32 v251, v251, v154
	v_pk_mul_f32 v[244:245], v[154:155], v[244:245] op_sel:[1,0]
	v_pk_mul_f32 v[246:247], v[154:155], v[246:247] op_sel:[1,0]
	v_pk_mul_f32 v[248:249], v[154:155], v[248:249] op_sel:[1,0]
	v_pk_mul_f32 v[250:251], v[154:155], v[250:251] op_sel:[1,0]
	v_pk_fma_f32 v[244:245], v[136:137], v[244:245], v[132:133]
	v_pk_fma_f32 v[246:247], v[138:139], v[246:247], v[134:135]
	v_pk_fma_f32 v[248:249], v[128:129], v[248:249], v[140:141]
	v_pk_fma_f32 v[250:251], v[130:131], v[250:251], v[142:143]
	v_pk_fma_f32 v[76:77], v[244:245], s[50:51], v[76:77] op_sel_hi:[1,0,1]
	v_pk_fma_f32 v[78:79], v[246:247], s[50:51], v[78:79] op_sel_hi:[1,0,1]
	v_pk_fma_f32 v[72:73], v[248:249], s[50:51], v[72:73] op_sel_hi:[1,0,1]
	v_pk_fma_f32 v[74:75], v[250:251], s[50:51], v[74:75] op_sel_hi:[1,0,1]
	v_cvt_pk_bf16_f32 v244, v76, v77
	v_cvt_pk_bf16_f32 v245, v78, v79
	v_cvt_pk_bf16_f32 v246, v72, v73
	v_cvt_pk_bf16_f32 v247, v74, v75
	s_add_u32 s100, s38, 0xa0000
	s_addc_u32 s101, s39, 0
	global_store_dwordx4 v159, v[244:247], s[100:101] sc1
	s_waitcnt vmcnt(7)
; #define GAS __attribute__((address_space(1)))
; #define LAS __attribute__((address_space(3)))
; __device__ __forceinline__ v4u pack8(const f32x4 a, const f32x4 b) { v4u w; w.x = cvt_pk_bf16(a[0], a[1]); w.y = cvt_pk_bf16(a[2], a[3]); w.z = cvt_pk_bf16(b[0], b[1]); w.w = cvt_pk_bf16(b[2], b[3]); return w; }
; #define EPI_LOOP_AM for (int ai = 0; ai < 2; ++ai) _Pragma("unroll") for (int m = 0; m < 4; ++m)
;     __device__ __forceinline__ void operator()(Acc& acc, const Unit& u, LAS unsigned char*, int wr, int wc, int fr, int fq) const {
;         const int colb = u.p1 * 256 + wc * 32 + 8 * fq;
; #pragma unroll
;         for (int bj = 0; bj < 2; ++bj) { const int col = colb + bj * 128;
;             const f32x4 ga = *(const GAS f32x4*)(g0 + col), gb = *(const GAS f32x4*)(g0 + col + 4), ba = *(const GAS f32x4*)(b0 + col), bb = *(const GAS f32x4*)(b0 + col + 4);
; #pragma unroll
;             EPI_LOOP_AM { const int row = u.p0 * 256 + 128 * ai + 64 * wr + 16 * m + fr; const f32x2 st = *(const GAS f32x2*)(st0 + 2 * row); const size_t off = (size_t)row * D + col;
;                 const f32x4 xa = *(const GAS f32x4*)(x + off), xb = *(const GAS f32x4*)(x + off + 4);
;                 *(GAS v4u*)(z1 + off) = pack8(((xa - st.x) * st.y * ga + ba) * ALPHA + acc[ai][bj][m][0], ((xb - st.x) * st.y * gb + bb) * ALPHA + acc[ai][bj][m][1]); } }
;     }
	v_sub_f32_e32 v174, v174, v156
	v_sub_f32_e32 v175, v175, v156
	v_sub_f32_e32 v176, v176, v156
	v_sub_f32_e32 v177, v177, v156
	v_sub_f32_e32 v178, v178, v156
	v_sub_f32_e32 v179, v179, v156
	v_sub_f32_e32 v180, v180, v156
	v_sub_f32_e32 v181, v181, v156
	v_pk_mul_f32 v[174:175], v[156:157], v[174:175] op_sel:[1,0]
	v_pk_mul_f32 v[176:177], v[156:157], v[176:177] op_sel:[1,0]
	v_pk_mul_f32 v[178:179], v[156:157], v[178:179] op_sel:[1,0]
	v_pk_mul_f32 v[180:181], v[156:157], v[180:181] op_sel:[1,0]
	v_pk_fma_f32 v[174:175], v[136:137], v[174:175], v[132:133]
	v_pk_fma_f32 v[176:177], v[138:139], v[176:177], v[134:135]
	v_pk_fma_f32 v[178:179], v[128:129], v[178:179], v[140:141]
	v_pk_fma_f32 v[180:181], v[130:131], v[180:181], v[142:143]
	v_pk_fma_f32 v[64:65], v[174:175], s[50:51], v[64:65] op_sel_hi:[1,0,1]
	v_pk_fma_f32 v[66:67], v[176:177], s[50:51], v[66:67] op_sel_hi:[1,0,1]
	v_pk_fma_f32 v[56:57], v[178:179], s[50:51], v[56:57] op_sel_hi:[1,0,1]
	v_pk_fma_f32 v[58:59], v[180:181], s[50:51], v[58:59] op_sel_hi:[1,0,1]
	v_cvt_pk_bf16_f32 v174, v64, v65
	v_cvt_pk_bf16_f32 v175, v66, v67
	v_cvt_pk_bf16_f32 v176, v56, v57
	v_cvt_pk_bf16_f32 v177, v58, v59
	s_add_u32 s100, s38, 0xb0000
	s_addc_u32 s101, s39, 0
	global_store_dwordx4 v159, v[174:177], s[100:101] sc1
	global_load_dwordx4 v[136:139], v161, s[14:15] offset:512
	global_load_dwordx4 v[128:131], v161, s[14:15] offset:528
	global_load_dwordx4 v[132:135], v161, s[16:17] offset:512
	global_load_dwordx4 v[140:143], v161, s[16:17] offset:528
	global_load_dwordx2 v[182:183], v160, s[40:41]
	global_load_dwordx4 v[196:199], v158, s[12:13] offset:512
	global_load_dwordx4 v[200:203], v158, s[12:13] offset:528
	s_add_u32 s98, s12, 0x20000
	s_addc_u32 s99, s13, 0
	global_load_dwordx2 v[184:185], v160, s[40:41] offset:128
	global_load_dwordx4 v[204:207], v158, s[98:99] offset:512
	global_load_dwordx4 v[208:211], v158, s[98:99] offset:528
	s_add_u32 s98, s12, 0x40000
	s_addc_u32 s99, s13, 0
	global_load_dwordx2 v[186:187], v160, s[40:41] offset:256
	global_load_dwordx4 v[212:215], v158, s[98:99] offset:512
	global_load_dwordx4 v[216:219], v158, s[98:99] offset:528
	s_add_u32 s98, s12, 0x60000
	s_addc_u32 s99, s13, 0
	global_load_dwordx2 v[148:149], v160, s[40:41] offset:384
	global_load_dwordx4 v[220:223], v158, s[98:99] offset:512
	global_load_dwordx4 v[224:227], v158, s[98:99] offset:528
	s_add_u32 s98, s12, 0x100000
	s_addc_u32 s99, s13, 0
	global_load_dwordx2 v[150:151], v160, s[40:41] offset:1024
	global_load_dwordx4 v[228:231], v158, s[98:99] offset:512
	global_load_dwordx4 v[232:235], v158, s[98:99] offset:528
	s_add_u32 s98, s12, 0x120000
	s_addc_u32 s99, s13, 0
	global_load_dwordx2 v[152:153], v160, s[40:41] offset:1152
	global_load_dwordx4 v[236:239], v158, s[98:99] offset:512
	global_load_dwordx4 v[240:243], v158, s[98:99] offset:528
	s_add_u32 s98, s12, 0x140000
	s_addc_u32 s99, s13, 0
	global_load_dwordx2 v[154:155], v160, s[40:41] offset:1280
	global_load_dwordx4 v[244:247], v158, s[98:99] offset:512
	global_load_dwordx4 v[248:251], v158, s[98:99] offset:528
	s_add_u32 s98, s12, 0x160000
	s_addc_u32 s99, s13, 0
	global_load_dwordx2 v[156:157], v160, s[40:41] offset:1408
	global_load_dwordx4 v[174:177], v158, s[98:99] offset:512
	global_load_dwordx4 v[178:181], v158, s[98:99] offset:528
	s_waitcnt vmcnt(21)
	v_sub_f32_e32 v196, v196, v182
	v_sub_f32_e32 v197, v197, v182
	v_sub_f32_e32 v198, v198, v182
	v_sub_f32_e32 v199, v199, v182
	v_sub_f32_e32 v200, v200, v182
	v_sub_f32_e32 v201, v201, v182
	v_sub_f32_e32 v202, v202, v182
	v_sub_f32_e32 v203, v203, v182
	v_pk_mul_f32 v[196:197], v[182:183], v[196:197] op_sel:[1,0]
	v_pk_mul_f32 v[198:199], v[182:183], v[198:199] op_sel:[1,0]
	v_pk_mul_f32 v[200:201], v[182:183], v[200:201] op_sel:[1,0]
	v_pk_mul_f32 v[202:203], v[182:183], v[202:203] op_sel:[1,0]
	v_pk_fma_f32 v[196:197], v[136:137], v[196:197], v[132:133]
	v_pk_fma_f32 v[198:199], v[138:139], v[198:199], v[134:135]
	v_pk_fma_f32 v[200:201], v[128:129], v[200:201], v[140:141]
	v_pk_fma_f32 v[202:203], v[130:131], v[202:203], v[142:143]
	v_pk_fma_f32 v[68:69], v[196:197], s[50:51], v[68:69] op_sel_hi:[1,0,1]
	v_pk_fma_f32 v[70:71], v[198:199], s[50:51], v[70:71] op_sel_hi:[1,0,1]
	v_pk_fma_f32 v[60:61], v[200:201], s[50:51], v[60:61] op_sel_hi:[1,0,1]
	v_pk_fma_f32 v[62:63], v[202:203], s[50:51], v[62:63] op_sel_hi:[1,0,1]
	v_cvt_pk_bf16_f32 v196, v68, v69
	v_cvt_pk_bf16_f32 v197, v70, v71
	v_cvt_pk_bf16_f32 v198, v60, v61
	v_cvt_pk_bf16_f32 v199, v62, v63
	global_store_dwordx4 v159, v[196:199], s[38:39] offset:256 sc1
	s_waitcnt vmcnt(19)
	v_sub_f32_e32 v204, v204, v184
	v_sub_f32_e32 v205, v205, v184
	v_sub_f32_e32 v206, v206, v184
	v_sub_f32_e32 v207, v207, v184
	v_sub_f32_e32 v208, v208, v184
	v_sub_f32_e32 v209, v209, v184
	v_sub_f32_e32 v210, v210, v184
	v_sub_f32_e32 v211, v211, v184
	v_pk_mul_f32 v[204:205], v[184:185], v[204:205] op_sel:[1,0]
	v_pk_mul_f32 v[206:207], v[184:185], v[206:207] op_sel:[1,0]
	v_pk_mul_f32 v[208:209], v[184:185], v[208:209] op_sel:[1,0]
	v_pk_mul_f32 v[210:211], v[184:185], v[210:211] op_sel:[1,0]
	v_pk_fma_f32 v[204:205], v[136:137], v[204:205], v[132:133]
	v_pk_fma_f32 v[206:207], v[138:139], v[206:207], v[134:135]
	v_pk_fma_f32 v[208:209], v[128:129], v[208:209], v[140:141]
	v_pk_fma_f32 v[210:211], v[130:131], v[210:211], v[142:143]
	v_pk_fma_f32 v[52:53], v[204:205], s[50:51], v[52:53] op_sel_hi:[1,0,1]
	v_pk_fma_f32 v[54:55], v[206:207], s[50:51], v[54:55] op_sel_hi:[1,0,1]
	v_pk_fma_f32 v[48:49], v[208:209], s[50:51], v[48:49] op_sel_hi:[1,0,1]
	v_pk_fma_f32 v[50:51], v[210:211], s[50:51], v[50:51] op_sel_hi:[1,0,1]
	v_cvt_pk_bf16_f32 v204, v52, v53
	v_cvt_pk_bf16_f32 v205, v54, v55
	v_cvt_pk_bf16_f32 v206, v48, v49
	v_cvt_pk_bf16_f32 v207, v50, v51
	s_add_u32 s100, s38, 0x10000
	s_addc_u32 s101, s39, 0
	global_store_dwordx4 v159, v[204:207], s[100:101] offset:256 sc1
	s_waitcnt vmcnt(17)
; #define GAS __attribute__((address_space(1)))
; #define LAS __attribute__((address_space(3)))
; __device__ __forceinline__ v4u pack8(const f32x4 a, const f32x4 b) { v4u w; w.x = cvt_pk_bf16(a[0], a[1]); w.y = cvt_pk_bf16(a[2], a[3]); w.z = cvt_pk_bf16(b[0], b[1]); w.w = cvt_pk_bf16(b[2], b[3]); return w; }
; #define EPI_LOOP_AM for (int ai = 0; ai < 2; ++ai) _Pragma("unroll") for (int m = 0; m < 4; ++m)
;     __device__ __forceinline__ void operator()(Acc& acc, const Unit& u, LAS unsigned char*, int wr, int wc, int fr, int fq) const {
;         const int colb = u.p1 * 256 + wc * 32 + 8 * fq;
; #pragma unroll
;         for (int bj = 0; bj < 2; ++bj) { const int col = colb + bj * 128;
;             const f32x4 ga = *(const GAS f32x4*)(g0 + col), gb = *(const GAS f32x4*)(g0 + col + 4), ba = *(const GAS f32x4*)(b0 + col), bb = *(const GAS f32x4*)(b0 + col + 4);
; #pragma unroll
;             EPI_LOOP_AM { const int row = u.p0 * 256 + 128 * ai + 64 * wr + 16 * m + fr; const f32x2 st = *(const GAS f32x2*)(st0 + 2 * row); const size_t off = (size_t)row * D + col;
;                 const f32x4 xa = *(const GAS f32x4*)(x + off), xb = *(const GAS f32x4*)(x + off + 4);
;                 *(GAS v4u*)(z1 + off) = pack8(((xa - st.x) * st.y * ga + ba) * ALPHA + acc[ai][bj][m][0], ((xb - st.x) * st.y * gb + bb) * ALPHA + acc[ai][bj][m][1]); } }
;     }
	v_sub_f32_e32 v212, v212, v186
	v_sub_f32_e32 v213, v213, v186
	v_sub_f32_e32 v214, v214, v186
	v_sub_f32_e32 v215, v215, v186
	v_sub_f32_e32 v216, v216, v186
	v_sub_f32_e32 v217, v217, v186
	v_sub_f32_e32 v218, v218, v186
	v_sub_f32_e32 v219, v219, v186
	v_pk_mul_f32 v[212:213], v[186:187], v[212:213] op_sel:[1,0]
	v_pk_mul_f32 v[214:215], v[186:187], v[214:215] op_sel:[1,0]
	v_pk_mul_f32 v[216:217], v[186:187], v[216:217] op_sel:[1,0]
	v_pk_mul_f32 v[218:219], v[186:187], v[218:219] op_sel:[1,0]
	v_pk_fma_f32 v[212:213], v[136:137], v[212:213], v[132:133]
	v_pk_fma_f32 v[214:215], v[138:139], v[214:215], v[134:135]
	v_pk_fma_f32 v[216:217], v[128:129], v[216:217], v[140:141]
	v_pk_fma_f32 v[218:219], v[130:131], v[218:219], v[142:143]
	v_pk_fma_f32 v[44:45], v[212:213], s[50:51], v[44:45] op_sel_hi:[1,0,1]
	v_pk_fma_f32 v[46:47], v[214:215], s[50:51], v[46:47] op_sel_hi:[1,0,1]
	v_pk_fma_f32 v[40:41], v[216:217], s[50:51], v[40:41] op_sel_hi:[1,0,1]
	v_pk_fma_f32 v[42:43], v[218:219], s[50:51], v[42:43] op_sel_hi:[1,0,1]
	v_cvt_pk_bf16_f32 v212, v44, v45
	v_cvt_pk_bf16_f32 v213, v46, v47
	v_cvt_pk_bf16_f32 v214, v40, v41
	v_cvt_pk_bf16_f32 v215, v42, v43
	s_add_u32 s100, s38, 0x20000
	s_addc_u32 s101, s39, 0
	global_store_dwordx4 v159, v[212:215], s[100:101] offset:256 sc1
	s_waitcnt vmcnt(15)
	v_sub_f32_e32 v220, v220, v148
	v_sub_f32_e32 v221, v221, v148
	v_sub_f32_e32 v222, v222, v148
	v_sub_f32_e32 v223, v223, v148
	v_sub_f32_e32 v224, v224, v148
	v_sub_f32_e32 v225, v225, v148
	v_sub_f32_e32 v226, v226, v148
	v_sub_f32_e32 v227, v227, v148
	v_pk_mul_f32 v[220:221], v[148:149], v[220:221] op_sel:[1,0]
	v_pk_mul_f32 v[222:223], v[148:149], v[222:223] op_sel:[1,0]
	v_pk_mul_f32 v[224:225], v[148:149], v[224:225] op_sel:[1,0]
	v_pk_mul_f32 v[226:227], v[148:149], v[226:227] op_sel:[1,0]
	v_pk_fma_f32 v[220:221], v[136:137], v[220:221], v[132:133]
	v_pk_fma_f32 v[222:223], v[138:139], v[222:223], v[134:135]
	v_pk_fma_f32 v[224:225], v[128:129], v[224:225], v[140:141]
	v_pk_fma_f32 v[226:227], v[130:131], v[226:227], v[142:143]
	v_pk_fma_f32 v[36:37], v[220:221], s[50:51], v[36:37] op_sel_hi:[1,0,1]
	v_pk_fma_f32 v[38:39], v[222:223], s[50:51], v[38:39] op_sel_hi:[1,0,1]
	v_pk_fma_f32 v[32:33], v[224:225], s[50:51], v[32:33] op_sel_hi:[1,0,1]
	v_pk_fma_f32 v[34:35], v[226:227], s[50:51], v[34:35] op_sel_hi:[1,0,1]
	v_cvt_pk_bf16_f32 v220, v36, v37
	v_cvt_pk_bf16_f32 v221, v38, v39
	v_cvt_pk_bf16_f32 v222, v32, v33
	v_cvt_pk_bf16_f32 v223, v34, v35
	s_add_u32 s100, s38, 0x30000
	s_addc_u32 s101, s39, 0
	global_store_dwordx4 v159, v[220:223], s[100:101] offset:256 sc1
	s_waitcnt vmcnt(13)
	v_sub_f32_e32 v228, v228, v150
	v_sub_f32_e32 v229, v229, v150
	v_sub_f32_e32 v230, v230, v150
	v_sub_f32_e32 v231, v231, v150
	v_sub_f32_e32 v232, v232, v150
	v_sub_f32_e32 v233, v233, v150
	v_sub_f32_e32 v234, v234, v150
	v_sub_f32_e32 v235, v235, v150
	v_pk_mul_f32 v[228:229], v[150:151], v[228:229] op_sel:[1,0]
	v_pk_mul_f32 v[230:231], v[150:151], v[230:231] op_sel:[1,0]
	v_pk_mul_f32 v[232:233], v[150:151], v[232:233] op_sel:[1,0]
	v_pk_mul_f32 v[234:235], v[150:151], v[234:235] op_sel:[1,0]
	v_pk_fma_f32 v[228:229], v[136:137], v[228:229], v[132:133]
	v_pk_fma_f32 v[230:231], v[138:139], v[230:231], v[134:135]
	v_pk_fma_f32 v[232:233], v[128:129], v[232:233], v[140:141]
	v_pk_fma_f32 v[234:235], v[130:131], v[234:235], v[142:143]
	v_pk_fma_f32 v[28:29], v[228:229], s[50:51], v[28:29] op_sel_hi:[1,0,1]
	v_pk_fma_f32 v[30:31], v[230:231], s[50:51], v[30:31] op_sel_hi:[1,0,1]
	v_pk_fma_f32 v[24:25], v[232:233], s[50:51], v[24:25] op_sel_hi:[1,0,1]
	v_pk_fma_f32 v[26:27], v[234:235], s[50:51], v[26:27] op_sel_hi:[1,0,1]
	v_cvt_pk_bf16_f32 v228, v28, v29
	v_cvt_pk_bf16_f32 v229, v30, v31
	v_cvt_pk_bf16_f32 v230, v24, v25
	v_cvt_pk_bf16_f32 v231, v26, v27
	s_add_u32 s100, s38, 0x80000
	s_addc_u32 s101, s39, 0
	global_store_dwordx4 v159, v[228:231], s[100:101] offset:256 sc1
	s_waitcnt vmcnt(11)
; #define GAS __attribute__((address_space(1)))
; #define LAS __attribute__((address_space(3)))
; __device__ __forceinline__ v4u pack8(const f32x4 a, const f32x4 b) { v4u w; w.x = cvt_pk_bf16(a[0], a[1]); w.y = cvt_pk_bf16(a[2], a[3]); w.z = cvt_pk_bf16(b[0], b[1]); w.w = cvt_pk_bf16(b[2], b[3]); return w; }
; #define G_BAR __builtin_amdgcn_s_barrier()
; #define EPI_LOOP_AM for (int ai = 0; ai < 2; ++ai) _Pragma("unroll") for (int m = 0; m < 4; ++m)
;     ...
;         if (wr == 1) G_BAR;
;     }
;     __device__ __forceinline__ void operator()(Acc& acc, const Unit& u, LAS unsigned char*, int wr, int wc, int fr, int fq) const {
;         const int colb = u.p1 * 256 + wc * 32 + 8 * fq;
; #pragma unroll
;         for (int bj = 0; bj < 2; ++bj) { const int col = colb + bj * 128;
;             const f32x4 ga = *(const GAS f32x4*)(g0 + col), gb = *(const GAS f32x4*)(g0 + col + 4), ba = *(const GAS f32x4*)(b0 + col), bb = *(const GAS f32x4*)(b0 + col + 4);
; #pragma unroll
;             EPI_LOOP_AM { const int row = u.p0 * 256 + 128 * ai + 64 * wr + 16 * m + fr; const f32x2 st = *(const GAS f32x2*)(st0 + 2 * row); const size_t off = (size_t)row * D + col;
;                 const f32x4 xa = *(const GAS f32x4*)(x + off), xb = *(const GAS f32x4*)(x + off + 4);
;                 *(GAS v4u*)(z1 + off) = pack8(((xa - st.x) * st.y * ga + ba) * ALPHA + acc[ai][bj][m][0], ((xb - st.x) * st.y * gb + bb) * ALPHA + acc[ai][bj][m][1]); } }
;     }
	v_sub_f32_e32 v236, v236, v152
	v_sub_f32_e32 v237, v237, v152
	v_sub_f32_e32 v238, v238, v152
	v_sub_f32_e32 v239, v239, v152
	v_sub_f32_e32 v240, v240, v152
	v_sub_f32_e32 v241, v241, v152
	v_sub_f32_e32 v242, v242, v152
	v_sub_f32_e32 v243, v243, v152
	v_pk_mul_f32 v[236:237], v[152:153], v[236:237] op_sel:[1,0]
	v_pk_mul_f32 v[238:239], v[152:153], v[238:239] op_sel:[1,0]
	v_pk_mul_f32 v[240:241], v[152:153], v[240:241] op_sel:[1,0]
	v_pk_mul_f32 v[242:243], v[152:153], v[242:243] op_sel:[1,0]
	v_pk_fma_f32 v[236:237], v[136:137], v[236:237], v[132:133]
	v_pk_fma_f32 v[238:239], v[138:139], v[238:239], v[134:135]
	v_pk_fma_f32 v[240:241], v[128:129], v[240:241], v[140:141]
	v_pk_fma_f32 v[242:243], v[130:131], v[242:243], v[142:143]
	v_pk_fma_f32 v[20:21], v[236:237], s[50:51], v[20:21] op_sel_hi:[1,0,1]
	v_pk_fma_f32 v[22:23], v[238:239], s[50:51], v[22:23] op_sel_hi:[1,0,1]
	v_pk_fma_f32 v[16:17], v[240:241], s[50:51], v[16:17] op_sel_hi:[1,0,1]
	v_pk_fma_f32 v[18:19], v[242:243], s[50:51], v[18:19] op_sel_hi:[1,0,1]
	v_cvt_pk_bf16_f32 v236, v20, v21
	v_cvt_pk_bf16_f32 v237, v22, v23
	v_cvt_pk_bf16_f32 v238, v16, v17
	v_cvt_pk_bf16_f32 v239, v18, v19
	s_add_u32 s100, s38, 0x90000
	s_addc_u32 s101, s39, 0
	global_store_dwordx4 v159, v[236:239], s[100:101] offset:256 sc1
	s_waitcnt vmcnt(9)
	v_sub_f32_e32 v244, v244, v154
	v_sub_f32_e32 v245, v245, v154
	v_sub_f32_e32 v246, v246, v154
	v_sub_f32_e32 v247, v247, v154
	v_sub_f32_e32 v248, v248, v154
	v_sub_f32_e32 v249, v249, v154
	v_sub_f32_e32 v250, v250, v154
	v_sub_f32_e32 v251, v251, v154
	v_pk_mul_f32 v[244:245], v[154:155], v[244:245] op_sel:[1,0]
	v_pk_mul_f32 v[246:247], v[154:155], v[246:247] op_sel:[1,0]
	v_pk_mul_f32 v[248:249], v[154:155], v[248:249] op_sel:[1,0]
	v_pk_mul_f32 v[250:251], v[154:155], v[250:251] op_sel:[1,0]
	v_pk_fma_f32 v[244:245], v[136:137], v[244:245], v[132:133]
	v_pk_fma_f32 v[246:247], v[138:139], v[246:247], v[134:135]
	v_pk_fma_f32 v[248:249], v[128:129], v[248:249], v[140:141]
	v_pk_fma_f32 v[250:251], v[130:131], v[250:251], v[142:143]
	v_pk_fma_f32 v[12:13], v[244:245], s[50:51], v[12:13] op_sel_hi:[1,0,1]
	v_pk_fma_f32 v[14:15], v[246:247], s[50:51], v[14:15] op_sel_hi:[1,0,1]
	v_pk_fma_f32 v[8:9], v[248:249], s[50:51], v[8:9] op_sel_hi:[1,0,1]
	v_pk_fma_f32 v[10:11], v[250:251], s[50:51], v[10:11] op_sel_hi:[1,0,1]
	v_cvt_pk_bf16_f32 v244, v12, v13
	v_cvt_pk_bf16_f32 v245, v14, v15
	v_cvt_pk_bf16_f32 v246, v8, v9
	v_cvt_pk_bf16_f32 v247, v10, v11
	s_add_u32 s100, s38, 0xa0000
	s_addc_u32 s101, s39, 0
	global_store_dwordx4 v159, v[244:247], s[100:101] offset:256 sc1
	s_waitcnt vmcnt(7)
	v_sub_f32_e32 v174, v174, v156
	v_sub_f32_e32 v175, v175, v156
	v_sub_f32_e32 v176, v176, v156
	v_sub_f32_e32 v177, v177, v156
	v_sub_f32_e32 v178, v178, v156
	v_sub_f32_e32 v179, v179, v156
	v_sub_f32_e32 v180, v180, v156
	v_sub_f32_e32 v181, v181, v156
	v_pk_mul_f32 v[174:175], v[156:157], v[174:175] op_sel:[1,0]
	v_pk_mul_f32 v[176:177], v[156:157], v[176:177] op_sel:[1,0]
	v_pk_mul_f32 v[178:179], v[156:157], v[178:179] op_sel:[1,0]
	v_pk_mul_f32 v[180:181], v[156:157], v[180:181] op_sel:[1,0]
	v_pk_fma_f32 v[174:175], v[136:137], v[174:175], v[132:133]
	v_pk_fma_f32 v[176:177], v[138:139], v[176:177], v[134:135]
	v_pk_fma_f32 v[178:179], v[128:129], v[178:179], v[140:141]
	v_pk_fma_f32 v[180:181], v[130:131], v[180:181], v[142:143]
	v_pk_fma_f32 v[4:5], v[174:175], s[50:51], v[4:5] op_sel_hi:[1,0,1]
	v_pk_fma_f32 v[6:7], v[176:177], s[50:51], v[6:7] op_sel_hi:[1,0,1]
	v_pk_fma_f32 v[0:1], v[178:179], s[50:51], v[0:1] op_sel_hi:[1,0,1]
	v_pk_fma_f32 v[2:3], v[180:181], s[50:51], v[2:3] op_sel_hi:[1,0,1]
	v_cvt_pk_bf16_f32 v174, v4, v5
	v_cvt_pk_bf16_f32 v175, v6, v7
	v_cvt_pk_bf16_f32 v176, v0, v1
	v_cvt_pk_bf16_f32 v177, v2, v3
	s_add_u32 s100, s38, 0xb0000
	s_addc_u32 s101, s39, 0
	global_store_dwordx4 v159, v[174:177], s[100:101] offset:256 sc1
	s_cbranch_vccnz .LBB0_1310
	s_and_b64 vcc, exec, s[4:5]
	s_cbranch_vccnz .LBB0_1309
	s_barrier
	s_branch .LBB0_1309

; #define GAS __attribute__((address_space(1)))
; #define LAS __attribute__((address_space(3)))
; __device__ __forceinline__ void do_slabs_impl(LAS unsigned char* lds, unsigned char* ws, const float* w_up, const float* w_dn, const float* w_in, int vcu, int G, int wave, int j0, int j1) {
;     ...
;             for (int i = 0; i < 8; ++i) { const int q = tid + NTHR * i, n = q >> 7, kc = q & 127; const float inv = red[256 + n];
;                 const int sx_ = ((n >> 3) & 3) << 3;
;                 const v4u a = *(const LAS v4u*)(slab + n * PITCH + ((kc * 16) ^ sx_)), b = *(const LAS v4u*)(slab + n * PITCH + ((kc * 16 + 8) ^ sx_));
;                 const unsigned src[8] = {a.x, a.y, a.z, a.w, b.x, b.y, b.z, b.w}; unsigned o[4];
;                 if (done.fp8) {
; #pragma unroll
;                     for (int d = 0; d < 4; ++d) { int w = __builtin_amdgcn_cvt_pk_fp8_f32(bf_lo(src[2 * d]) * inv, bf_hi(src[2 * d]) * inv, 0, false);
;                         w = __builtin_amdgcn_cvt_pk_fp8_f32(bf_lo(src[2 * d + 1]) * inv, bf_hi(src[2 * d + 1]) * inv, w, true); o[d] = (unsigned)w; }
;                 } else {
; #pragma unroll
;                 for (int d = 0; d < 4; ++d) { unsigned w = 0u;
; #pragma unroll
;                     for (int h2 = 0; h2 < 2; ++h2) { const unsigned u2 = src[2 * d + h2]; const int q0 = (int)__builtin_rintf(bf_lo(u2) * inv), q1 = (int)__builtin_rintf(bf_hi(u2) * inv);
;                         w |= ((unsigned)(q0 & 0xff) << (16 * h2)) | ((unsigned)(q1 & 0xff) << (16 * h2 + 8)); }
;                     o[d] = w; }
;                 }
;                 __builtin_nontemporal_store((v4u){o[0], o[1], o[2], o[3]}, (GAS v4u*)(done.WQ + ((size_t)done.e * done.NS + done.n0 + n) * D + kc * 16)); }
.LBB0_1374:
	v_ashrrev_i32_e32 v139, 31, v138
	v_lshl_add_u64 v[138:139], s[12:13], 0, v[138:139]
	v_lshlrev_b64 v[138:139], 11, v[138:139]
	s_addk_i32 s0, 0x400
	v_lshl_add_u64 v[138:139], v[136:137], 0, v[138:139]
	s_cmpk_lg_i32 s0, 0x1000
	global_store_dwordx4 v[138:139], v[128:131], off nt sc1
	s_cbranch_scc0 .LBB0_1353

; #define GAS __attribute__((address_space(1)))
; #define LAS __attribute__((address_space(3)))
; __device__ __forceinline__ void do_slabs_impl(LAS unsigned char* lds, unsigned char* ws, const float* w_up, const float* w_dn, const float* w_in, int vcu, int G, int wave, int j0, int j1) {
;     ...
;         if (done.valid) {
; #pragma unroll 2
;             for (int i = 0; i < 8; ++i) { const int q = tid + NTHR * i, n = q >> 7, kc = q & 127; const float inv = red[256 + n];
;                 const int sx_ = ((n >> 3) & 3) << 3;
;                 const v4u a = *(const LAS v4u*)(slab + n * PITCH + ((kc * 16) ^ sx_)), b = *(const LAS v4u*)(slab + n * PITCH + ((kc * 16 + 8) ^ sx_));
;                 const unsigned src[8] = {a.x, a.y, a.z, a.w, b.x, b.y, b.z, b.w}; unsigned o[4];
;                 if (done.fp8) {
; #pragma unroll
;                     for (int d = 0; d < 4; ++d) { int w = __builtin_amdgcn_cvt_pk_fp8_f32(bf_lo(src[2 * d]) * inv, bf_hi(src[2 * d]) * inv, 0, false);
;                         w = __builtin_amdgcn_cvt_pk_fp8_f32(bf_lo(src[2 * d + 1]) * inv, bf_hi(src[2 * d + 1]) * inv, w, true); o[d] = (unsigned)w; }
;                 } else {
; #pragma unroll
;                 for (int d = 0; d < 4; ++d) { unsigned w = 0u;
; #pragma unroll
;                     for (int h2 = 0; h2 < 2; ++h2) { const unsigned u2 = src[2 * d + h2]; const int q0 = (int)__builtin_rintf(bf_lo(u2) * inv), q1 = (int)__builtin_rintf(bf_hi(u2) * inv);
;                         w |= ((unsigned)(q0 & 0xff) << (16 * h2)) | ((unsigned)(q1 & 0xff) << (16 * h2 + 8)); }
;                     o[d] = w; }
;                 }
;                 __builtin_nontemporal_store((v4u){o[0], o[1], o[2], o[3]}, (GAS v4u*)(done.WQ + ((size_t)done.e * done.NS + done.n0 + n) * D + kc * 16)); }
.LBB0_1378:
	v_ashrrev_i32_e32 v139, 31, v138
	v_lshl_add_u64 v[138:139], s[12:13], 0, v[138:139]
	v_lshlrev_b64 v[138:139], 11, v[138:139]
	v_lshl_add_u64 v[184:185], v[136:137], 0, v[138:139]
	v_add_u32_e32 v139, 0x200, v180
	v_ashrrev_i32_e32 v138, 7, v139
	v_lshrrev_b32_e32 v186, 7, v139
	v_mul_lo_u32 v139, v138, s3
	v_add_u32_e32 v187, 0, v139
	v_bitop3_b32 v139, v186, v134, 24 bitop3:0x6c
	v_lshl_add_u32 v180, v138, 2, s2
	v_lshl_add_u32 v181, v139, 1, v187
	ds_read_b32 v139, v180 offset:1024
	ds_read_b128 v[180:183], v181
	global_store_dwordx4 v[184:185], v[128:131], off nt sc1
	s_and_b64 vcc, exec, s[8:9]
	s_waitcnt lgkmcnt(0)
	v_lshlrev_b32_e32 v184, 16, v180
	v_bitop3_b32 v128, v186, v143, 24 bitop3:0x6c
	v_lshl_add_u32 v128, v128, 1, v187
	ds_read_b128 v[128:131], v128
	v_and_b32_e32 v180, 0xffff0000, v180
	v_mul_f32_e32 v194, v139, v184
	v_mul_f32_e32 v195, v139, v180
	v_lshlrev_b32_e32 v193, 16, v181
	v_and_b32_e32 v192, 0xffff0000, v181
	v_lshlrev_b32_e32 v191, 16, v182
	v_and_b32_e32 v190, 0xffff0000, v182
	v_lshlrev_b32_e32 v189, 16, v183
	v_and_b32_e32 v188, 0xffff0000, v183
	s_waitcnt lgkmcnt(0)
	v_lshlrev_b32_e32 v187, 16, v128
	v_and_b32_e32 v186, 0xffff0000, v128
	v_lshlrev_b32_e32 v185, 16, v129
	v_and_b32_e32 v184, 0xffff0000, v129
	v_lshlrev_b32_e32 v183, 16, v130
	v_and_b32_e32 v182, 0xffff0000, v130
	v_lshlrev_b32_e32 v181, 16, v131
	v_and_b32_e32 v180, 0xffff0000, v131
	s_cbranch_vccnz .LBB0_1381
	v_mov_b32_e32 v128, 0
	v_cvt_pk_fp8_f32 v128, v194, v195
	v_mul_f32_e32 v196, v139, v191
	v_mul_f32_e32 v197, v139, v190
	v_mov_b32_e32 v129, 0
	v_cvt_pk_fp8_f32 v129, v196, v197
	v_mul_f32_e32 v130, v139, v193
	v_mul_f32_e32 v131, v139, v192
	v_cvt_pk_fp8_f32 v128, v130, v131 op_sel:[0,0,1]
	v_mul_f32_e32 v130, v139, v189
	v_mul_f32_e32 v131, v139, v188
	v_cvt_pk_fp8_f32 v129, v130, v131 op_sel:[0,0,1]
	v_mul_f32_e32 v131, v139, v187
	v_mul_f32_e32 v196, v139, v186
	v_mov_b32_e32 v130, 0
	v_cvt_pk_fp8_f32 v130, v131, v196
	v_mul_f32_e32 v198, v139, v183
	v_mul_f32_e32 v199, v139, v182
	v_mov_b32_e32 v131, 0
	v_cvt_pk_fp8_f32 v131, v198, v199
	v_mul_f32_e32 v196, v139, v185
	v_mul_f32_e32 v197, v139, v184
	v_cvt_pk_fp8_f32 v130, v196, v197 op_sel:[0,0,1]
	v_mul_f32_e32 v196, v139, v181
	v_mul_f32_e32 v197, v139, v180
	v_cvt_pk_fp8_f32 v131, v196, v197 op_sel:[0,0,1]
	s_cbranch_execnz .LBB0_1374
	s_branch .LBB0_1373

; #define GAS __attribute__((address_space(1)))
; #define LAS __attribute__((address_space(3)))
; __device__ __forceinline__ void do_slabs_impl(LAS unsigned char* lds, unsigned char* ws, const float* w_up, const float* w_dn, const float* w_in, int vcu, int G, int wave, int j0, int j1) {
;     ...
;             for (int i = 0; i < 8; ++i) { const int q = tid + NTHR * i, n = q >> 7, kc = q & 127; const float inv = red[256 + n];
;                 const int sx_ = ((n >> 3) & 3) << 3;
;                 const v4u a = *(const LAS v4u*)(slab + n * PITCH + ((kc * 16) ^ sx_)), b = *(const LAS v4u*)(slab + n * PITCH + ((kc * 16 + 8) ^ sx_));
;                 const unsigned src[8] = {a.x, a.y, a.z, a.w, b.x, b.y, b.z, b.w}; unsigned o[4];
;                 if (done.fp8) {
; #pragma unroll
;                     for (int d = 0; d < 4; ++d) { int w = __builtin_amdgcn_cvt_pk_fp8_f32(bf_lo(src[2 * d]) * inv, bf_hi(src[2 * d]) * inv, 0, false);
;                         w = __builtin_amdgcn_cvt_pk_fp8_f32(bf_lo(src[2 * d + 1]) * inv, bf_hi(src[2 * d + 1]) * inv, w, true); o[d] = (unsigned)w; }
;                 } else {
; #pragma unroll
;                 for (int d = 0; d < 4; ++d) { unsigned w = 0u;
; #pragma unroll
;                     for (int h2 = 0; h2 < 2; ++h2) { const unsigned u2 = src[2 * d + h2]; const int q0 = (int)__builtin_rintf(bf_lo(u2) * inv), q1 = (int)__builtin_rintf(bf_hi(u2) * inv);
;                         w |= ((unsigned)(q0 & 0xff) << (16 * h2)) | ((unsigned)(q1 & 0xff) << (16 * h2 + 8)); }
;                     o[d] = w; }
;                 }
;                 __builtin_nontemporal_store((v4u){o[0], o[1], o[2], o[3]}, (GAS v4u*)(done.WQ + ((size_t)done.e * done.NS + done.n0 + n) * D + kc * 16)); }
.LBB0_1423:
	v_ashrrev_i32_e32 v139, 31, v138
	v_lshl_add_u64 v[138:139], s[12:13], 0, v[138:139]
	v_lshlrev_b64 v[138:139], 11, v[138:139]
	s_addk_i32 s22, 0x400
	v_lshl_add_u64 v[138:139], v[136:137], 0, v[138:139]
	s_cmpk_lg_i32 s22, 0x1000
	global_store_dwordx4 v[138:139], v[128:131], off nt sc1
	s_cbranch_scc0 .LBB0_1402

; #define GAS __attribute__((address_space(1)))
; #define LAS __attribute__((address_space(3)))
; __device__ __forceinline__ void do_slabs_impl(LAS unsigned char* lds, unsigned char* ws, const float* w_up, const float* w_dn, const float* w_in, int vcu, int G, int wave, int j0, int j1) {
;     ...
;         if (done.valid) {
; #pragma unroll 2
;             for (int i = 0; i < 8; ++i) { const int q = tid + NTHR * i, n = q >> 7, kc = q & 127; const float inv = red[256 + n];
;                 const int sx_ = ((n >> 3) & 3) << 3;
;                 const v4u a = *(const LAS v4u*)(slab + n * PITCH + ((kc * 16) ^ sx_)), b = *(const LAS v4u*)(slab + n * PITCH + ((kc * 16 + 8) ^ sx_));
;                 const unsigned src[8] = {a.x, a.y, a.z, a.w, b.x, b.y, b.z, b.w}; unsigned o[4];
;                 if (done.fp8) {
; #pragma unroll
;                     for (int d = 0; d < 4; ++d) { int w = __builtin_amdgcn_cvt_pk_fp8_f32(bf_lo(src[2 * d]) * inv, bf_hi(src[2 * d]) * inv, 0, false);
;                         w = __builtin_amdgcn_cvt_pk_fp8_f32(bf_lo(src[2 * d + 1]) * inv, bf_hi(src[2 * d + 1]) * inv, w, true); o[d] = (unsigned)w; }
;                 } else {
; #pragma unroll
;                 for (int d = 0; d < 4; ++d) { unsigned w = 0u;
; #pragma unroll
;                     for (int h2 = 0; h2 < 2; ++h2) { const unsigned u2 = src[2 * d + h2]; const int q0 = (int)__builtin_rintf(bf_lo(u2) * inv), q1 = (int)__builtin_rintf(bf_hi(u2) * inv);
;                         w |= ((unsigned)(q0 & 0xff) << (16 * h2)) | ((unsigned)(q1 & 0xff) << (16 * h2 + 8)); }
;                     o[d] = w; }
;                 }
;                 __builtin_nontemporal_store((v4u){o[0], o[1], o[2], o[3]}, (GAS v4u*)(done.WQ + ((size_t)done.e * done.NS + done.n0 + n) * D + kc * 16)); }
.LBB0_1427:
	v_ashrrev_i32_e32 v139, 31, v138
	v_lshl_add_u64 v[138:139], s[12:13], 0, v[138:139]
	v_lshlrev_b64 v[138:139], 11, v[138:139]
	v_lshl_add_u64 v[184:185], v[136:137], 0, v[138:139]
	v_add_u32_e32 v139, 0x200, v180
	v_ashrrev_i32_e32 v138, 7, v139
	v_lshrrev_b32_e32 v186, 7, v139
	v_mul_lo_u32 v139, v138, s21
	v_add_u32_e32 v187, 0, v139
	v_bitop3_b32 v139, v186, v134, 24 bitop3:0x6c
	v_lshl_add_u32 v180, v138, 2, s20
	v_lshl_add_u32 v181, v139, 1, v187
	ds_read_b32 v139, v180 offset:1024
	ds_read_b128 v[180:183], v181
	global_store_dwordx4 v[184:185], v[128:131], off nt sc1
	s_and_b64 vcc, exec, s[8:9]
	s_waitcnt lgkmcnt(0)
	v_lshlrev_b32_e32 v184, 16, v180
	v_bitop3_b32 v128, v186, v143, 24 bitop3:0x6c
	v_lshl_add_u32 v128, v128, 1, v187
	ds_read_b128 v[128:131], v128
	v_and_b32_e32 v180, 0xffff0000, v180
	v_mul_f32_e32 v194, v139, v184
	v_mul_f32_e32 v195, v139, v180
	v_lshlrev_b32_e32 v193, 16, v181
	v_and_b32_e32 v192, 0xffff0000, v181
	v_lshlrev_b32_e32 v191, 16, v182
	v_and_b32_e32 v190, 0xffff0000, v182
	v_lshlrev_b32_e32 v189, 16, v183
	v_and_b32_e32 v188, 0xffff0000, v183
	s_waitcnt lgkmcnt(0)
	v_lshlrev_b32_e32 v187, 16, v128
	v_and_b32_e32 v186, 0xffff0000, v128
	v_lshlrev_b32_e32 v185, 16, v129
	v_and_b32_e32 v184, 0xffff0000, v129
	v_lshlrev_b32_e32 v183, 16, v130
	v_and_b32_e32 v182, 0xffff0000, v130
	v_lshlrev_b32_e32 v181, 16, v131
	v_and_b32_e32 v180, 0xffff0000, v131
	s_cbranch_vccnz .LBB0_1430
	v_mov_b32_e32 v128, 0
	v_cvt_pk_fp8_f32 v128, v194, v195
	v_mul_f32_e32 v196, v139, v191
	v_mul_f32_e32 v197, v139, v190
	v_mov_b32_e32 v129, 0
	v_cvt_pk_fp8_f32 v129, v196, v197
	v_mul_f32_e32 v130, v139, v193
	v_mul_f32_e32 v131, v139, v192
	v_cvt_pk_fp8_f32 v128, v130, v131 op_sel:[0,0,1]
	v_mul_f32_e32 v130, v139, v189
	v_mul_f32_e32 v131, v139, v188
	v_cvt_pk_fp8_f32 v129, v130, v131 op_sel:[0,0,1]
	v_mul_f32_e32 v131, v139, v187
	v_mul_f32_e32 v196, v139, v186
	v_mov_b32_e32 v130, 0
	v_cvt_pk_fp8_f32 v130, v131, v196
	v_mul_f32_e32 v198, v139, v183
	v_mul_f32_e32 v199, v139, v182
	v_mov_b32_e32 v131, 0
	v_cvt_pk_fp8_f32 v131, v198, v199
	v_mul_f32_e32 v196, v139, v185
	v_mul_f32_e32 v197, v139, v184
	v_cvt_pk_fp8_f32 v130, v196, v197 op_sel:[0,0,1]
	v_mul_f32_e32 v196, v139, v181
	v_mul_f32_e32 v197, v139, v180
	v_cvt_pk_fp8_f32 v131, v196, v197 op_sel:[0,0,1]
	s_cbranch_execnz .LBB0_1423
	s_branch .LBB0_1422

; #define GAS __attribute__((address_space(1)))
; #define LAS __attribute__((address_space(3)))
; __device__ __forceinline__ void do_slabs_impl(LAS unsigned char* lds, unsigned char* ws, const float* w_up, const float* w_dn, const float* w_in, int vcu, int G, int wave, int j0, int j1) {
;     ...
;             for (int i = 0; i < 8; ++i) { const int q = tid + NTHR * i, n = q >> 7, kc = q & 127; const float inv = red[256 + n];
;                 const int sx_ = ((n >> 3) & 3) << 3;
;                 const v4u a = *(const LAS v4u*)(slab + n * PITCH + ((kc * 16) ^ sx_)), b = *(const LAS v4u*)(slab + n * PITCH + ((kc * 16 + 8) ^ sx_));
;                 const unsigned src[8] = {a.x, a.y, a.z, a.w, b.x, b.y, b.z, b.w}; unsigned o[4];
;                 if (done.fp8) {
; #pragma unroll
;                     for (int d = 0; d < 4; ++d) { int w = __builtin_amdgcn_cvt_pk_fp8_f32(bf_lo(src[2 * d]) * inv, bf_hi(src[2 * d]) * inv, 0, false);
;                         w = __builtin_amdgcn_cvt_pk_fp8_f32(bf_lo(src[2 * d + 1]) * inv, bf_hi(src[2 * d + 1]) * inv, w, true); o[d] = (unsigned)w; }
;                 } else {
; #pragma unroll
;                 for (int d = 0; d < 4; ++d) { unsigned w = 0u;
; #pragma unroll
;                     for (int h2 = 0; h2 < 2; ++h2) { const unsigned u2 = src[2 * d + h2]; const int q0 = (int)__builtin_rintf(bf_lo(u2) * inv), q1 = (int)__builtin_rintf(bf_hi(u2) * inv);
;                         w |= ((unsigned)(q0 & 0xff) << (16 * h2)) | ((unsigned)(q1 & 0xff) << (16 * h2 + 8)); }
;                     o[d] = w; }
;                 }
;                 __builtin_nontemporal_store((v4u){o[0], o[1], o[2], o[3]}, (GAS v4u*)(done.WQ + ((size_t)done.e * done.NS + done.n0 + n) * D + kc * 16)); }
.LBB0_1599:
	v_add_u32_e32 v199, s16, v196
	v_ashrrev_i32_e32 v202, 7, v199
	v_lshl_add_u32 v128, v202, 2, s0
	ds_read_b32 v203, v128 offset:1024
	v_mul_lo_u32 v128, v202, s29
	v_lshrrev_b32_e32 v244, 7, v199
	v_add_u32_e32 v243, 0, v128
	v_bitop3_b32 v128, v244, v198, 24 bitop3:0x6c
	v_lshl_add_u32 v128, v128, 1, v243
	ds_read_b128 v[128:131], v128
	v_bitop3_b32 v244, v244, v210, 24 bitop3:0x6c
	v_lshl_add_u32 v243, v244, 1, v243
	s_addk_i32 s16, 0x400
	s_cmpk_lg_i32 s16, 0x1000
	s_waitcnt lgkmcnt(0)
	v_lshlrev_b32_e32 v245, 16, v128
	v_and_b32_e32 v128, 0xffff0000, v128
	v_mul_f32_e32 v248, v203, v245
	ds_read_b128 v[244:247], v243
	v_mul_f32_e32 v243, v203, v128
	v_mov_b32_e32 v128, v193
	v_cvt_pk_fp8_f32 v128, v248, v243
	v_lshlrev_b32_e32 v243, 16, v129
	v_and_b32_e32 v129, 0xffff0000, v129
	v_mul_f32_e32 v243, v203, v243
	v_mul_f32_e32 v129, v203, v129
	v_cvt_pk_fp8_f32 v128, v243, v129 op_sel:[0,0,1]
	v_lshlrev_b32_e32 v129, 16, v130
	v_mul_f32_e32 v243, v203, v129
	v_and_b32_e32 v129, 0xffff0000, v130
	v_mul_f32_e32 v130, v203, v129
	v_mov_b32_e32 v129, v193
	v_cvt_pk_fp8_f32 v129, v243, v130
	v_lshlrev_b32_e32 v130, 16, v131
	v_and_b32_e32 v131, 0xffff0000, v131
	v_mul_f32_e32 v130, v203, v130
	v_mul_f32_e32 v131, v203, v131
	v_cvt_pk_fp8_f32 v129, v130, v131 op_sel:[0,0,1]
	s_waitcnt lgkmcnt(0)
	v_lshlrev_b32_e32 v130, 16, v244
	v_mul_f32_e32 v131, v203, v130
	v_and_b32_e32 v130, 0xffff0000, v244
	v_mul_f32_e32 v243, v203, v130
	v_mov_b32_e32 v130, v193
	v_cvt_pk_fp8_f32 v130, v131, v243
	v_lshlrev_b32_e32 v131, 16, v245
	v_and_b32_e32 v243, 0xffff0000, v245
	v_mul_f32_e32 v131, v203, v131
	v_mul_f32_e32 v243, v203, v243
	v_cvt_pk_fp8_f32 v130, v131, v243 op_sel:[0,0,1]
	v_lshlrev_b32_e32 v131, 16, v246
	v_mul_f32_e32 v243, v203, v131
	v_and_b32_e32 v131, 0xffff0000, v246
	v_mul_f32_e32 v244, v203, v131
	v_mov_b32_e32 v131, v193
	v_cvt_pk_fp8_f32 v131, v243, v244
	v_lshlrev_b32_e32 v243, 16, v247
	v_and_b32_e32 v244, 0xffff0000, v247
	v_mul_f32_e32 v243, v203, v243
	v_mul_f32_e32 v203, v203, v244
	v_cvt_pk_fp8_f32 v131, v243, v203 op_sel:[0,0,1]
	v_ashrrev_i32_e32 v203, 31, v202
	v_lshl_add_u64 v[202:203], s[50:51], 0, v[202:203]
	v_lshlrev_b64 v[202:203], 11, v[202:203]
	v_lshl_add_u64 v[202:203], v[200:201], 0, v[202:203]
	global_store_dwordx4 v[202:203], v[128:131], off nt sc1
	s_nop 1
	v_add_u32_e32 v128, 0x200, v199
	v_ashrrev_i32_e32 v202, 7, v128
	v_lshl_add_u32 v129, v202, 2, s0
	ds_read_b32 v199, v129 offset:1024
	v_mul_lo_u32 v129, v202, s29
	v_lshrrev_b32_e32 v128, 7, v128
	v_add_u32_e32 v129, 0, v129
	v_bitop3_b32 v130, v128, v198, 24 bitop3:0x6c
	v_lshl_add_u32 v130, v130, 1, v129
	ds_read_b128 v[244:247], v130
	v_bitop3_b32 v128, v128, v210, 24 bitop3:0x6c
	v_lshl_add_u32 v128, v128, 1, v129
	s_waitcnt lgkmcnt(0)
	v_lshlrev_b32_e32 v130, 16, v244
	v_and_b32_e32 v243, 0xffff0000, v244
	v_mul_f32_e32 v203, v199, v130
	v_mul_f32_e32 v243, v199, v243
	v_mov_b32_e32 v244, v193
	v_cvt_pk_fp8_f32 v244, v203, v243
	v_lshlrev_b32_e32 v203, 16, v245
	v_and_b32_e32 v243, 0xffff0000, v245
	v_mul_f32_e32 v203, v199, v203
	v_mul_f32_e32 v243, v199, v243
	v_cvt_pk_fp8_f32 v244, v203, v243 op_sel:[0,0,1]
	v_lshlrev_b32_e32 v203, 16, v246
	v_and_b32_e32 v243, 0xffff0000, v246
	ds_read_b128 v[128:131], v128
	v_mul_f32_e32 v203, v199, v203
	v_mul_f32_e32 v243, v199, v243
	v_mov_b32_e32 v245, v193
	v_cvt_pk_fp8_f32 v245, v203, v243
	v_lshlrev_b32_e32 v203, 16, v247
	v_and_b32_e32 v243, 0xffff0000, v247
	v_mul_f32_e32 v203, v199, v203
	v_mul_f32_e32 v243, v199, v243
	v_cvt_pk_fp8_f32 v245, v203, v243 op_sel:[0,0,1]
	s_waitcnt lgkmcnt(0)
	v_lshlrev_b32_e32 v203, 16, v128
	v_and_b32_e32 v128, 0xffff0000, v128
	v_mul_f32_e32 v203, v199, v203
	v_mul_f32_e32 v128, v199, v128
	v_mov_b32_e32 v246, v193
	v_cvt_pk_fp8_f32 v246, v203, v128
	v_lshlrev_b32_e32 v128, 16, v129
	v_and_b32_e32 v129, 0xffff0000, v129
	v_mul_f32_e32 v128, v199, v128
	v_mul_f32_e32 v129, v199, v129
	v_cvt_pk_fp8_f32 v246, v128, v129 op_sel:[0,0,1]
	v_lshlrev_b32_e32 v128, 16, v130
	v_and_b32_e32 v129, 0xffff0000, v130
	v_mul_f32_e32 v128, v199, v128
	v_mul_f32_e32 v129, v199, v129
	v_mov_b32_e32 v247, v193
	v_cvt_pk_fp8_f32 v247, v128, v129
	v_lshlrev_b32_e32 v128, 16, v131
	v_and_b32_e32 v129, 0xffff0000, v131
	v_mul_f32_e32 v128, v199, v128
	v_mul_f32_e32 v129, v199, v129
	v_cvt_pk_fp8_f32 v247, v128, v129 op_sel:[0,0,1]
	v_ashrrev_i32_e32 v203, 31, v202
	v_lshl_add_u64 v[128:129], s[50:51], 0, v[202:203]
	v_lshlrev_b64 v[128:129], 11, v[128:129]
	v_lshl_add_u64 v[128:129], v[200:201], 0, v[128:129]
	global_store_dwordx4 v[128:129], v[244:247], off nt sc1
	s_cbranch_scc1 .LBB0_1599
	s_branch .LBB0_1586

; #define GAS __attribute__((address_space(1)))
; __device__ __forceinline__ void p9_combine(Frame& F, const LAS int* tstart) {
;     ...
;     for (int m = gw; m < T; m += NGW) {
;         const float mean1 = st1[2 * m], rstd1 = st1[2 * m + 1];
;         size_t ro[4]; float gk[4];
; #pragma unroll
;         for (int k = 0; k < 4; ++k) { const int e = topi[4 * m + k]; ro[k] = ((size_t)tstart[e] * 256 + posb[4 * m + k]) * D; gk[k] = gate[4 * m + k]; }
;         f32x4 v[8]; float s = 0.f;
; #pragma unroll
;         for (int j = 0; j < 8; ++j) { const int col = 4 * lane + 256 * j;
;             const v2u zw = *(const GAS v2u*)(z1 + (size_t)m * D + col); const f32x4 zv = (f32x4){bf_lo(zw.x), bf_hi(zw.x), bf_lo(zw.y), bf_hi(zw.y)}, g = *(const GAS f32x4*)(F.ln1_g + col), b = *(const GAS f32x4*)(F.ln1_b + col);
;             f32x4 a = ((zv - mean1) * rstd1 * g + b) * ALPHA;
; #pragma unroll
;             for (int k = 0; k < 4; ++k) { const int w = *(const GAS int*)(yr + ro[k] + col); const f32x2 lo = __builtin_amdgcn_cvt_pk_f32_fp8(w, false), hi = __builtin_amdgcn_cvt_pk_f32_fp8(w, true); const float g = gk[k] * (1.f / 32.f);
;                 a[0] += g * lo.x; a[1] += g * lo.y; a[2] += g * hi.x; a[3] += g * hi.y; }
;             v[j] = a; s += (a[0] + a[1]) + (a[2] + a[3]); }
.LBB0_1798:
	s_ashr_i32 s7, s6, 31
	s_lshl_b64 s[0:1], s[6:7], 2
	s_add_u32 s0, s18, s0
	s_addc_u32 s1, s19, s1
	s_ashr_i32 s9, s8, 31
	global_load_dwordx2 v[118:119], v[116:117], off
	global_load_dwordx2 v[120:121], v[116:117], off offset:512
	global_load_dwordx4 v[0:3], v[74:75], off
	global_load_dwordx4 v[4:7], v[74:75], off offset:1024
	global_load_dwordx4 v[12:15], v[76:77], off
	global_load_dwordx4 v[8:11], v[76:77], off offset:1024
	global_load_dwordx2 v[122:123], v[116:117], off offset:1024
	global_load_dwordx2 v[124:125], v[116:117], off offset:1536
	global_load_dwordx4 v[16:19], v[74:75], off offset:2048
	global_load_dwordx4 v[20:23], v[74:75], off offset:3072
	global_load_dwordx4 v[28:31], v[76:77], off offset:2048
	global_load_dwordx4 v[24:27], v[76:77], off offset:3072
	global_load_dwordx4 v[32:35], v[78:79], off
	global_load_dwordx4 v[40:43], v[80:81], off
	global_load_dwordx2 v[126:127], v[116:117], off offset:2048
	global_load_dwordx2 v[128:129], v[116:117], off offset:2560
	global_load_dwordx4 v[48:51], v[82:83], off
	global_load_dwordx4 v[52:55], v[84:85], off
	global_load_dwordx4 v[56:59], v[86:87], off
	global_load_dwordx4 v[60:63], v[88:89], off
	global_load_dwordx2 v[130:131], v[116:117], off offset:3072
	global_load_dwordx2 v[132:133], v[116:117], off offset:3584
	global_load_dwordx4 v[64:67], v[90:91], off
	global_load_dwordx4 v[68:71], v[92:93], off
	global_load_dwordx4 v[36:39], v[94:95], off
	global_load_dwordx4 v[44:47], v[96:97], off
	global_load_dwordx2 v[152:153], v140, s[0:1]
	s_lshl_b64 s[0:1], s[8:9], 2
	s_add_u32 s26, s20, s0
	s_addc_u32 s27, s21, s1
	global_load_dwordx4 v[144:147], v140, s[26:27]
	s_add_u32 s26, s24, s0
	s_addc_u32 s27, s25, s1
	s_add_u32 s0, s22, s0
	s_addc_u32 s1, s23, s1
	global_load_dword v154, v140, s[26:27]
	global_load_dword v143, v140, s[0:1]
	s_add_i32 s26, s8, 1
	s_ashr_i32 s27, s26, 31
	s_lshl_b64 s[0:1], s[26:27], 2
	s_add_u32 s26, s24, s0
	s_addc_u32 s27, s25, s1
	global_load_dwordx3 v[148:150], v140, s[26:27]
	s_add_u32 s0, s22, s0
	s_addc_u32 s1, s23, s1
	global_load_dword v151, v140, s[0:1]
	s_add_i32 s26, s8, 2
	s_ashr_i32 s27, s26, 31
	s_lshl_b64 s[0:1], s[26:27], 2
	s_add_u32 s0, s22, s0
	s_addc_u32 s1, s23, s1
	global_load_dwordx2 v[156:157], v140, s[0:1]
	s_add_i32 s2, s2, s16
	s_add_i32 s6, s6, s13
	s_add_i32 s8, s8, s14
	v_lshl_add_u64 v[116:117], v[116:117], 0, s[10:11]
	s_cmpk_lt_i32 s2, 0x4000
	s_waitcnt vmcnt(31)
	v_lshlrev_b32_e32 v160, 16, v120
	v_and_b32_e32 v161, 0xffff0000, v120
	v_lshlrev_b32_e32 v162, 16, v121
	v_and_b32_e32 v163, 0xffff0000, v121
	s_waitcnt vmcnt(26)
	v_lshlrev_b32_e32 v164, 16, v122
	v_and_b32_e32 v165, 0xffff0000, v122
	v_lshlrev_b32_e32 v166, 16, v123
	v_and_b32_e32 v167, 0xffff0000, v123
	s_waitcnt vmcnt(25)
	v_lshlrev_b32_e32 v168, 16, v124
	v_and_b32_e32 v169, 0xffff0000, v124
	v_lshlrev_b32_e32 v170, 16, v125
	v_and_b32_e32 v171, 0xffff0000, v125
	s_waitcnt vmcnt(18)
	v_lshlrev_b32_e32 v172, 16, v126
	v_and_b32_e32 v173, 0xffff0000, v126
	v_lshlrev_b32_e32 v174, 16, v127
	v_and_b32_e32 v175, 0xffff0000, v127
	s_waitcnt vmcnt(17)
	v_lshlrev_b32_e32 v176, 16, v128
	v_and_b32_e32 v177, 0xffff0000, v128
	v_lshlrev_b32_e32 v178, 16, v129
	v_and_b32_e32 v179, 0xffff0000, v129
	s_waitcnt vmcnt(12)
	v_lshlrev_b32_e32 v180, 16, v130
	v_and_b32_e32 v181, 0xffff0000, v130
	v_lshlrev_b32_e32 v158, 16, v119
	v_and_b32_e32 v159, 0xffff0000, v119
	s_waitcnt vmcnt(6)
	v_sub_f32_e32 v121, v159, v152
	v_sub_f32_e32 v120, v158, v152
	v_sub_f32_e32 v123, v161, v152
	v_sub_f32_e32 v122, v160, v152
	v_sub_f32_e32 v125, v163, v152
	v_sub_f32_e32 v124, v162, v152
	v_sub_f32_e32 v127, v165, v152
	v_sub_f32_e32 v126, v164, v152
	v_sub_f32_e32 v129, v167, v152
	v_sub_f32_e32 v128, v166, v152
	v_sub_f32_e32 v159, v173, v152
	v_sub_f32_e32 v158, v172, v152
	v_sub_f32_e32 v161, v175, v152
	v_sub_f32_e32 v160, v174, v152
	v_pk_mul_f32 v[124:125], v[152:153], v[124:125] op_sel:[1,0]
	v_pk_mul_f32 v[122:123], v[152:153], v[122:123] op_sel:[1,0]
	v_pk_mul_f32 v[128:129], v[152:153], v[128:129] op_sel:[1,0]
	v_pk_mul_f32 v[126:127], v[152:153], v[126:127] op_sel:[1,0]
	v_pk_mul_f32 v[160:161], v[152:153], v[160:161] op_sel:[1,0]
	v_pk_mul_f32 v[158:159], v[152:153], v[158:159] op_sel:[1,0]
	v_pk_fma_f32 v[4:5], v[4:5], v[122:123], v[8:9]
	v_pk_fma_f32 v[6:7], v[6:7], v[124:125], v[10:11]
	v_pk_fma_f32 v[8:9], v[16:17], v[126:127], v[28:29]
	v_pk_fma_f32 v[10:11], v[18:19], v[128:129], v[30:31]
	v_pk_fma_f32 v[16:17], v[32:33], v[158:159], v[40:41]
	v_pk_fma_f32 v[18:19], v[34:35], v[160:161], v[42:43]
	s_waitcnt vmcnt(5)
	v_lshlrev_b32_e32 v32, 2, v144
	v_lshlrev_b32_e32 v34, 2, v146
	v_lshlrev_b32_e32 v33, 2, v145
	v_lshlrev_b32_e32 v35, 2, v147
	v_add_u32_e32 v32, s3, v32
	v_add_u32_e32 v40, s3, v34
	v_lshlrev_b32_e32 v155, 16, v118
	v_and_b32_e32 v118, 0xffff0000, v118
	v_add_u32_e32 v33, s3, v33
	v_add_u32_e32 v35, s3, v35
	ds_read_b32 v32, v32
	ds_read_b32 v34, v33
	ds_read_b32 v40, v40
	ds_read_b32 v42, v35
	v_lshlrev_b32_e32 v182, 16, v131
	v_and_b32_e32 v183, 0xffff0000, v131
	v_sub_f32_e32 v119, v118, v152
	v_sub_f32_e32 v118, v155, v152
	v_sub_f32_e32 v131, v169, v152
	v_sub_f32_e32 v130, v168, v152
	v_sub_f32_e32 v163, v177, v152
	v_sub_f32_e32 v162, v176, v152
	v_pk_mul_f32 v[118:119], v[152:153], v[118:119] op_sel:[1,0]
	v_pk_mul_f32 v[130:131], v[152:153], v[130:131] op_sel:[1,0]
	v_pk_mul_f32 v[162:163], v[152:153], v[162:163] op_sel:[1,0]
	s_waitcnt vmcnt(4)
	v_ashrrev_i32_e32 v155, 31, v154
	s_waitcnt lgkmcnt(3)
; #define GAS __attribute__((address_space(1)))
; __device__ __forceinline__ void p9_combine(Frame& F, const LAS int* tstart) {
;     ...
;         for (int k = 0; k < 4; ++k) { const int e = topi[4 * m + k]; ro[k] = ((size_t)tstart[e] * 256 + posb[4 * m + k]) * D; gk[k] = gate[4 * m + k]; }
;         f32x4 v[8]; float s = 0.f;
; #pragma unroll
;         for (int j = 0; j < 8; ++j) { const int col = 4 * lane + 256 * j;
;             const v2u zw = *(const GAS v2u*)(z1 + (size_t)m * D + col); const f32x4 zv = (f32x4){bf_lo(zw.x), bf_hi(zw.x), bf_lo(zw.y), bf_hi(zw.y)}, g = *(const GAS f32x4*)(F.ln1_g + col), b = *(const GAS f32x4*)(F.ln1_b + col);
;             f32x4 a = ((zv - mean1) * rstd1 * g + b) * ALPHA;
; #pragma unroll
;             for (int k = 0; k < 4; ++k) { const int w = *(const GAS int*)(yr + ro[k] + col); const f32x2 lo = __builtin_amdgcn_cvt_pk_f32_fp8(w, false), hi = __builtin_amdgcn_cvt_pk_f32_fp8(w, true); const float g = gk[k] * (1.f / 32.f);
;                 a[0] += g * lo.x; a[1] += g * lo.y; a[2] += g * hi.x; a[3] += g * hi.y; }
;             v[j] = a; s += (a[0] + a[1]) + (a[2] + a[3]); }
	v_ashrrev_i32_e32 v33, 31, v32
	v_lshlrev_b32_e32 v186, 16, v133
	v_and_b32_e32 v187, 0xffff0000, v133
	v_pk_fma_f32 v[0:1], v[0:1], v[118:119], v[12:13]
	v_pk_fma_f32 v[12:13], v[20:21], v[130:131], v[24:25]
	v_pk_fma_f32 v[20:21], v[48:49], v[162:163], v[52:53]
	v_lshlrev_b64 v[48:49], 11, v[154:155]
	v_lshlrev_b64 v[32:33], 19, v[32:33]
	v_lshlrev_b32_e32 v184, 16, v132
	v_and_b32_e32 v185, 0xffff0000, v132
	v_sub_f32_e32 v133, v171, v152
	v_sub_f32_e32 v132, v170, v152
	v_sub_f32_e32 v165, v179, v152
	v_sub_f32_e32 v164, v178, v152
	v_sub_f32_e32 v169, v183, v152
	v_sub_f32_e32 v168, v182, v152
	v_sub_f32_e32 v173, v187, v152
	v_sub_f32_e32 v172, v186, v152
	s_waitcnt lgkmcnt(2)
	v_ashrrev_i32_e32 v35, 31, v34
	s_waitcnt vmcnt(2)
	v_ashrrev_i32_e32 v53, 31, v148
	v_mov_b32_e32 v52, v148
	v_lshl_add_u64 v[32:33], v[48:49], 0, v[32:33]
	v_sub_f32_e32 v167, v181, v152
	v_sub_f32_e32 v166, v180, v152
	v_pk_mul_f32 v[120:121], v[152:153], v[120:121] op_sel:[1,0]
	v_pk_mul_f32 v[132:133], v[152:153], v[132:133] op_sel:[1,0]
	v_pk_mul_f32 v[164:165], v[152:153], v[164:165] op_sel:[1,0]
	v_pk_mul_f32 v[168:169], v[152:153], v[168:169] op_sel:[1,0]
	v_pk_mul_f32 v[172:173], v[152:153], v[172:173] op_sel:[1,0]
	v_lshlrev_b64 v[34:35], 19, v[34:35]
	v_lshlrev_b64 v[48:49], 11, v[52:53]
	v_lshl_add_u64 v[32:33], v[72:73], 0, v[32:33]
	v_pk_mul_f32 v[166:167], v[152:153], v[166:167] op_sel:[1,0]
	v_pk_fma_f32 v[2:3], v[2:3], v[120:121], v[14:15]
	v_pk_fma_f32 v[14:15], v[22:23], v[132:133], v[26:27]
	v_pk_fma_f32 v[22:23], v[50:51], v[164:165], v[54:55]
	v_pk_fma_f32 v[26:27], v[58:59], v[168:169], v[62:63]
	v_pk_fma_f32 v[30:31], v[66:67], v[172:173], v[70:71]
	v_lshl_add_u64 v[34:35], v[48:49], 0, v[34:35]
	global_load_dword v49, v[32:33], off
	global_load_dword v51, v[32:33], off offset:256
	global_load_dword v58, v[32:33], off offset:512
	global_load_dword v62, v[32:33], off offset:768
	global_load_dword v66, v[32:33], off offset:1024
	global_load_dword v70, v[32:33], off offset:1280
	global_load_dword v120, v[32:33], off offset:1536
	v_pk_fma_f32 v[24:25], v[56:57], v[166:167], v[60:61]
	s_waitcnt lgkmcnt(1)
	v_ashrrev_i32_e32 v41, 31, v40
	s_waitcnt lgkmcnt(0)
	v_ashrrev_i32_e32 v43, 31, v42
	v_ashrrev_i32_e32 v55, 31, v149
	v_mov_b32_e32 v54, v149
	v_ashrrev_i32_e32 v57, 31, v150
	v_mov_b32_e32 v56, v150
	v_lshlrev_b64 v[40:41], 19, v[40:41]
	v_lshlrev_b64 v[42:43], 19, v[42:43]
	v_lshlrev_b64 v[52:53], 11, v[54:55]
	v_lshlrev_b64 v[54:55], 11, v[56:57]
	v_sub_f32_e32 v171, v185, v152
	v_sub_f32_e32 v170, v184, v152
	v_lshl_add_u64 v[40:41], v[52:53], 0, v[40:41]
	v_lshl_add_u64 v[42:43], v[54:55], 0, v[42:43]
	v_lshl_add_u64 v[34:35], v[72:73], 0, v[34:35]
	v_pk_mul_f32 v[152:153], v[152:153], v[170:171] op_sel:[1,0]
	v_mul_f32_e32 v50, 0x3d000000, v143
	v_lshl_add_u64 v[40:41], v[72:73], 0, v[40:41]
	v_lshl_add_u64 v[42:43], v[72:73], 0, v[42:43]
	global_load_dword v124, v[34:35], off
	global_load_dword v128, v[40:41], off
	global_load_dword v132, v[42:43], off
	global_load_dword v143, v[34:35], off offset:256
	global_load_dword v150, v[40:41], off offset:256
	global_load_dword v154, v[42:43], off offset:256
	global_load_dword v158, v[34:35], off offset:512
	global_load_dword v162, v[40:41], off offset:512
	global_load_dword v166, v[42:43], off offset:512
	global_load_dword v170, v[34:35], off offset:768
	global_load_dword v174, v[40:41], off offset:768
	global_load_dword v178, v[42:43], off offset:768
	global_load_dword v182, v[34:35], off offset:1024
	global_load_dword v186, v[40:41], off offset:1024
	global_load_dword v190, v[42:43], off offset:1024
	global_load_dword v194, v[34:35], off offset:1280
	global_load_dword v198, v[40:41], off offset:1280
	global_load_dword v202, v[42:43], off offset:1280
	global_load_dword v206, v[34:35], off offset:1536
	global_load_dword v210, v[40:41], off offset:1536
	global_load_dword v214, v[42:43], off offset:1536
	s_nop 0
	global_load_dword v33, v[32:33], off offset:1792
	s_nop 0
	global_load_dword v35, v[34:35], off offset:1792
	s_nop 0
	global_load_dword v226, v[40:41], off offset:1792
	global_load_dword v230, v[42:43], off offset:1792
	v_pk_fma_f32 v[28:29], v[64:65], v[152:153], v[68:69]
	s_waitcnt vmcnt(33)
	v_mul_f32_e32 v48, 0x3d000000, v151
	s_waitcnt vmcnt(32)
	v_mul_f32_e32 v32, 0x3d000000, v156
	v_mul_f32_e32 v34, 0x3d000000, v157
	v_pk_mul_f32 v[2:3], v[2:3], s[12:13] op_sel_hi:[1,0]
	v_pk_mul_f32 v[0:1], v[0:1], s[12:13] op_sel_hi:[1,0]
	v_pk_mul_f32 v[6:7], v[6:7], s[12:13] op_sel_hi:[1,0]
	v_pk_mul_f32 v[4:5], v[4:5], s[12:13] op_sel_hi:[1,0]
	v_pk_mul_f32 v[10:11], v[10:11], s[12:13] op_sel_hi:[1,0]
	v_pk_mul_f32 v[8:9], v[8:9], s[12:13] op_sel_hi:[1,0]
	v_pk_mul_f32 v[14:15], v[14:15], s[12:13] op_sel_hi:[1,0]
	v_pk_mul_f32 v[12:13], v[12:13], s[12:13] op_sel_hi:[1,0]
	v_pk_mul_f32 v[18:19], v[18:19], s[12:13] op_sel_hi:[1,0]
	v_pk_mul_f32 v[16:17], v[16:17], s[12:13] op_sel_hi:[1,0]
	v_pk_mul_f32 v[20:21], v[20:21], s[12:13] op_sel_hi:[1,0]
	v_pk_mul_f32 v[22:23], v[22:23], s[12:13] op_sel_hi:[1,0]
	v_pk_mul_f32 v[26:27], v[26:27], s[12:13] op_sel_hi:[1,0]
	v_pk_mul_f32 v[24:25], v[24:25], s[12:13] op_sel_hi:[1,0]
	v_pk_mul_f32 v[30:31], v[30:31], s[12:13] op_sel_hi:[1,0]
	v_pk_mul_f32 v[28:29], v[28:29], s[12:13] op_sel_hi:[1,0]
	s_waitcnt vmcnt(31)
	v_cvt_pk_f32_fp8_e32 v[40:41], v49
	v_cvt_pk_f32_fp8_sdwa v[42:43], v49 src0_sel:WORD_1
	s_waitcnt vmcnt(30)
	v_cvt_pk_f32_fp8_e32 v[52:53], v51
	v_cvt_pk_f32_fp8_sdwa v[54:55], v51 src0_sel:WORD_1
	s_waitcnt vmcnt(29)
	v_cvt_pk_f32_fp8_e32 v[56:57], v58
	v_cvt_pk_f32_fp8_sdwa v[58:59], v58 src0_sel:WORD_1
	s_waitcnt vmcnt(28)
; #define GAS __attribute__((address_space(1)))
; __device__ __forceinline__ void p9_combine(Frame& F, const LAS int* tstart) {
;     ...
;         for (int j = 0; j < 8; ++j) { const int col = 4 * lane + 256 * j;
;             const v2u zw = *(const GAS v2u*)(z1 + (size_t)m * D + col); const f32x4 zv = (f32x4){bf_lo(zw.x), bf_hi(zw.x), bf_lo(zw.y), bf_hi(zw.y)}, g = *(const GAS f32x4*)(F.ln1_g + col), b = *(const GAS f32x4*)(F.ln1_b + col);
;             f32x4 a = ((zv - mean1) * rstd1 * g + b) * ALPHA;
; #pragma unroll
;             for (int k = 0; k < 4; ++k) { const int w = *(const GAS int*)(yr + ro[k] + col); const f32x2 lo = __builtin_amdgcn_cvt_pk_f32_fp8(w, false), hi = __builtin_amdgcn_cvt_pk_f32_fp8(w, true); const float g = gk[k] * (1.f / 32.f);
;                 a[0] += g * lo.x; a[1] += g * lo.y; a[2] += g * hi.x; a[3] += g * hi.y; }
;             v[j] = a; s += (a[0] + a[1]) + (a[2] + a[3]); }
	v_cvt_pk_f32_fp8_e32 v[60:61], v62
	v_cvt_pk_f32_fp8_sdwa v[62:63], v62 src0_sel:WORD_1
	s_waitcnt vmcnt(27)
	v_cvt_pk_f32_fp8_e32 v[64:65], v66
	v_cvt_pk_f32_fp8_sdwa v[66:67], v66 src0_sel:WORD_1
	s_waitcnt vmcnt(26)
	v_cvt_pk_f32_fp8_e32 v[68:69], v70
	s_waitcnt vmcnt(24)
	v_cvt_pk_f32_fp8_e32 v[122:123], v124
	v_cvt_pk_f32_fp8_sdwa v[124:125], v124 src0_sel:WORD_1
	s_waitcnt vmcnt(21)
	v_cvt_pk_f32_fp8_e32 v[144:145], v143
	v_cvt_pk_f32_fp8_sdwa v[146:147], v143 src0_sel:WORD_1
	v_cvt_pk_f32_fp8_sdwa v[70:71], v70 src0_sel:WORD_1
	v_cvt_pk_f32_fp8_e32 v[118:119], v120
	v_cvt_pk_f32_fp8_sdwa v[120:121], v120 src0_sel:WORD_1
	v_cvt_pk_f32_fp8_e32 v[126:127], v128
	v_cvt_pk_f32_fp8_sdwa v[128:129], v128 src0_sel:WORD_1
	s_waitcnt vmcnt(20)
	v_cvt_pk_f32_fp8_e32 v[148:149], v150
	v_cvt_pk_f32_fp8_sdwa v[150:151], v150 src0_sel:WORD_1
	s_waitcnt vmcnt(18)
	v_cvt_pk_f32_fp8_e32 v[156:157], v158
	v_cvt_pk_f32_fp8_sdwa v[158:159], v158 src0_sel:WORD_1
	s_waitcnt vmcnt(15)
	v_cvt_pk_f32_fp8_e32 v[168:169], v170
	v_cvt_pk_f32_fp8_sdwa v[170:171], v170 src0_sel:WORD_1
	s_waitcnt vmcnt(12)
	v_cvt_pk_f32_fp8_e32 v[180:181], v182
	v_cvt_pk_f32_fp8_sdwa v[182:183], v182 src0_sel:WORD_1
	s_waitcnt vmcnt(9)
	v_cvt_pk_f32_fp8_e32 v[192:193], v194
	s_waitcnt vmcnt(3)
	v_cvt_pk_f32_fp8_e32 v[216:217], v33
	v_cvt_pk_f32_fp8_sdwa v[218:219], v33 src0_sel:WORD_1
	v_cvt_pk_f32_fp8_e32 v[130:131], v132
	v_cvt_pk_f32_fp8_sdwa v[132:133], v132 src0_sel:WORD_1
	v_cvt_pk_f32_fp8_e32 v[152:153], v154
	v_cvt_pk_f32_fp8_sdwa v[154:155], v154 src0_sel:WORD_1
	v_cvt_pk_f32_fp8_e32 v[160:161], v162
	v_cvt_pk_f32_fp8_sdwa v[162:163], v162 src0_sel:WORD_1
	v_cvt_pk_f32_fp8_e32 v[172:173], v174
	v_cvt_pk_f32_fp8_sdwa v[174:175], v174 src0_sel:WORD_1
	v_cvt_pk_f32_fp8_e32 v[184:185], v186
	v_cvt_pk_f32_fp8_sdwa v[186:187], v186 src0_sel:WORD_1
	v_cvt_pk_f32_fp8_sdwa v[194:195], v194 src0_sel:WORD_1
	v_cvt_pk_f32_fp8_e32 v[196:197], v198
	v_cvt_pk_f32_fp8_e32 v[204:205], v206
	v_cvt_pk_f32_fp8_sdwa v[206:207], v206 src0_sel:WORD_1
	s_waitcnt vmcnt(2)
	v_cvt_pk_f32_fp8_e32 v[220:221], v35
	v_cvt_pk_f32_fp8_sdwa v[222:223], v35 src0_sel:WORD_1
	v_cvt_pk_f32_fp8_e32 v[164:165], v166
	v_cvt_pk_f32_fp8_sdwa v[166:167], v166 src0_sel:WORD_1
	v_cvt_pk_f32_fp8_e32 v[176:177], v178
	v_cvt_pk_f32_fp8_sdwa v[178:179], v178 src0_sel:WORD_1
	v_cvt_pk_f32_fp8_e32 v[188:189], v190
	v_cvt_pk_f32_fp8_sdwa v[190:191], v190 src0_sel:WORD_1
	v_cvt_pk_f32_fp8_sdwa v[198:199], v198 src0_sel:WORD_1
	v_cvt_pk_f32_fp8_e32 v[200:201], v202
	v_cvt_pk_f32_fp8_e32 v[208:209], v210
	v_pk_fma_f32 v[0:1], v[50:51], v[40:41], v[0:1] op_sel_hi:[0,1,1]
	v_pk_fma_f32 v[2:3], v[50:51], v[42:43], v[2:3] op_sel_hi:[0,1,1]
	v_pk_fma_f32 v[4:5], v[50:51], v[52:53], v[4:5] op_sel_hi:[0,1,1]
	v_pk_fma_f32 v[6:7], v[50:51], v[54:55], v[6:7] op_sel_hi:[0,1,1]
	v_cvt_pk_f32_fp8_sdwa v[202:203], v202 src0_sel:WORD_1
	v_cvt_pk_f32_fp8_e32 v[212:213], v214
	v_pk_fma_f32 v[8:9], v[50:51], v[56:57], v[8:9] op_sel_hi:[0,1,1]
	v_pk_fma_f32 v[10:11], v[50:51], v[58:59], v[10:11] op_sel_hi:[0,1,1]
	v_pk_fma_f32 v[12:13], v[50:51], v[60:61], v[12:13] op_sel_hi:[0,1,1]
	v_pk_fma_f32 v[14:15], v[50:51], v[62:63], v[14:15] op_sel_hi:[0,1,1]
	v_pk_fma_f32 v[16:17], v[50:51], v[64:65], v[16:17] op_sel_hi:[0,1,1]
	v_pk_fma_f32 v[18:19], v[50:51], v[66:67], v[18:19] op_sel_hi:[0,1,1]
	v_pk_fma_f32 v[20:21], v[50:51], v[68:69], v[20:21] op_sel_hi:[0,1,1]
	v_pk_fma_f32 v[0:1], v[48:49], v[122:123], v[0:1] op_sel_hi:[0,1,1]
	v_pk_fma_f32 v[2:3], v[48:49], v[124:125], v[2:3] op_sel_hi:[0,1,1]
	v_pk_fma_f32 v[4:5], v[48:49], v[144:145], v[4:5] op_sel_hi:[0,1,1]
	v_pk_fma_f32 v[6:7], v[48:49], v[146:147], v[6:7] op_sel_hi:[0,1,1]
	v_cvt_pk_f32_fp8_sdwa v[210:211], v210 src0_sel:WORD_1
	v_pk_fma_f32 v[22:23], v[50:51], v[70:71], v[22:23] op_sel_hi:[0,1,1]
	v_pk_fma_f32 v[24:25], v[50:51], v[118:119], v[24:25] op_sel_hi:[0,1,1]
	v_pk_fma_f32 v[26:27], v[50:51], v[120:121], v[26:27] op_sel_hi:[0,1,1]
	v_pk_fma_f32 v[8:9], v[48:49], v[156:157], v[8:9] op_sel_hi:[0,1,1]
	v_pk_fma_f32 v[10:11], v[48:49], v[158:159], v[10:11] op_sel_hi:[0,1,1]
	v_pk_fma_f32 v[12:13], v[48:49], v[168:169], v[12:13] op_sel_hi:[0,1,1]
	v_pk_fma_f32 v[14:15], v[48:49], v[170:171], v[14:15] op_sel_hi:[0,1,1]
	v_pk_fma_f32 v[16:17], v[48:49], v[180:181], v[16:17] op_sel_hi:[0,1,1]
	v_pk_fma_f32 v[18:19], v[48:49], v[182:183], v[18:19] op_sel_hi:[0,1,1]
	v_pk_fma_f32 v[20:21], v[48:49], v[192:193], v[20:21] op_sel_hi:[0,1,1]
	v_pk_fma_f32 v[28:29], v[50:51], v[216:217], v[28:29] op_sel_hi:[0,1,1]
	v_pk_fma_f32 v[30:31], v[50:51], v[218:219], v[30:31] op_sel_hi:[0,1,1]
	v_pk_fma_f32 v[0:1], v[32:33], v[126:127], v[0:1] op_sel_hi:[0,1,1]
	v_pk_fma_f32 v[2:3], v[32:33], v[128:129], v[2:3] op_sel_hi:[0,1,1]
	v_pk_fma_f32 v[4:5], v[32:33], v[148:149], v[4:5] op_sel_hi:[0,1,1]
	v_pk_fma_f32 v[6:7], v[32:33], v[150:151], v[6:7] op_sel_hi:[0,1,1]
	v_cvt_pk_f32_fp8_sdwa v[214:215], v214 src0_sel:WORD_1
	s_waitcnt vmcnt(1)
; #define GAS __attribute__((address_space(1)))
; __device__ __forceinline__ void p9_combine(Frame& F, const LAS int* tstart) {
;     ...
;         for (int j = 0; j < 8; ++j) { const int col = 4 * lane + 256 * j;
;             const v2u zw = *(const GAS v2u*)(z1 + (size_t)m * D + col); const f32x4 zv = (f32x4){bf_lo(zw.x), bf_hi(zw.x), bf_lo(zw.y), bf_hi(zw.y)}, g = *(const GAS f32x4*)(F.ln1_g + col), b = *(const GAS f32x4*)(F.ln1_b + col);
;             f32x4 a = ((zv - mean1) * rstd1 * g + b) * ALPHA;
; #pragma unroll
;             for (int k = 0; k < 4; ++k) { const int w = *(const GAS int*)(yr + ro[k] + col); const f32x2 lo = __builtin_amdgcn_cvt_pk_f32_fp8(w, false), hi = __builtin_amdgcn_cvt_pk_f32_fp8(w, true); const float g = gk[k] * (1.f / 32.f);
;                 a[0] += g * lo.x; a[1] += g * lo.y; a[2] += g * hi.x; a[3] += g * hi.y; }
;             v[j] = a; s += (a[0] + a[1]) + (a[2] + a[3]); }
;         const float mean = wave_sum(s) * (1.f / D); float s2 = 0.f;
; #pragma unroll
;         for (int j = 0; j < 8; ++j) { v[j] = v[j] - mean; s2 += (v[j][0] * v[j][0] + v[j][1] * v[j][1]) + (v[j][2] * v[j][2] + v[j][3] * v[j][3]); }
;         const float rstd = 1.f / sqrtf(wave_sum(s2) * (1.f / D) + LN_EPS);
; #pragma unroll
;         for (int j = 0; j < 8; ++j) { const int col = 4 * lane + 256 * j; const f32x4 g = *(const GAS f32x4*)(F.ln2_g + col), b = *(const GAS f32x4*)(F.ln2_b + col);
	v_cvt_pk_f32_fp8_e32 v[224:225], v226
	v_pk_fma_f32 v[22:23], v[48:49], v[194:195], v[22:23] op_sel_hi:[0,1,1]
	v_pk_fma_f32 v[24:25], v[48:49], v[204:205], v[24:25] op_sel_hi:[0,1,1]
	v_pk_fma_f32 v[26:27], v[48:49], v[206:207], v[26:27] op_sel_hi:[0,1,1]
	v_pk_fma_f32 v[8:9], v[32:33], v[160:161], v[8:9] op_sel_hi:[0,1,1]
	v_pk_fma_f32 v[10:11], v[32:33], v[162:163], v[10:11] op_sel_hi:[0,1,1]
	v_pk_fma_f32 v[12:13], v[32:33], v[172:173], v[12:13] op_sel_hi:[0,1,1]
	v_pk_fma_f32 v[14:15], v[32:33], v[174:175], v[14:15] op_sel_hi:[0,1,1]
	v_pk_fma_f32 v[16:17], v[32:33], v[184:185], v[16:17] op_sel_hi:[0,1,1]
	v_pk_fma_f32 v[18:19], v[32:33], v[186:187], v[18:19] op_sel_hi:[0,1,1]
	v_pk_fma_f32 v[20:21], v[32:33], v[196:197], v[20:21] op_sel_hi:[0,1,1]
	v_pk_fma_f32 v[28:29], v[48:49], v[220:221], v[28:29] op_sel_hi:[0,1,1]
	v_pk_fma_f32 v[30:31], v[48:49], v[222:223], v[30:31] op_sel_hi:[0,1,1]
	v_pk_fma_f32 v[40:41], v[34:35], v[130:131], v[0:1] op_sel_hi:[0,1,1]
	v_pk_fma_f32 v[42:43], v[34:35], v[132:133], v[2:3] op_sel_hi:[0,1,1]
	v_pk_fma_f32 v[48:49], v[34:35], v[152:153], v[4:5] op_sel_hi:[0,1,1]
	v_pk_fma_f32 v[50:51], v[34:35], v[154:155], v[6:7] op_sel_hi:[0,1,1]
	v_cvt_pk_f32_fp8_sdwa v[226:227], v226 src0_sel:WORD_1
	v_pk_fma_f32 v[22:23], v[32:33], v[198:199], v[22:23] op_sel_hi:[0,1,1]
	v_pk_fma_f32 v[24:25], v[32:33], v[208:209], v[24:25] op_sel_hi:[0,1,1]
	v_pk_fma_f32 v[52:53], v[34:35], v[164:165], v[8:9] op_sel_hi:[0,1,1]
	v_pk_fma_f32 v[54:55], v[34:35], v[166:167], v[10:11] op_sel_hi:[0,1,1]
	v_pk_fma_f32 v[56:57], v[34:35], v[176:177], v[12:13] op_sel_hi:[0,1,1]
	v_pk_fma_f32 v[58:59], v[34:35], v[178:179], v[14:15] op_sel_hi:[0,1,1]
	v_pk_fma_f32 v[12:13], v[34:35], v[188:189], v[16:17] op_sel_hi:[0,1,1]
	v_pk_fma_f32 v[60:61], v[34:35], v[190:191], v[18:19] op_sel_hi:[0,1,1]
	v_pk_fma_f32 v[8:9], v[34:35], v[200:201], v[20:21] op_sel_hi:[0,1,1]
	v_mov_b32_e32 v14, v40
	v_mov_b32_e32 v15, v48
	v_mov_b32_e32 v16, v41
	v_mov_b32_e32 v17, v49
	v_mov_b32_e32 v18, v42
	v_mov_b32_e32 v19, v50
	v_mov_b32_e32 v20, v43
	v_mov_b32_e32 v21, v51
	v_pk_fma_f32 v[10:11], v[34:35], v[202:203], v[22:23] op_sel_hi:[0,1,1]
	v_pk_fma_f32 v[4:5], v[34:35], v[212:213], v[24:25] op_sel_hi:[0,1,1]
	v_mov_b32_e32 v22, v52
	v_mov_b32_e32 v23, v54
	v_mov_b32_e32 v24, v53
	v_mov_b32_e32 v25, v55
	v_pk_add_f32 v[14:15], v[14:15], v[16:17]
	v_pk_add_f32 v[16:17], v[18:19], v[20:21]
	v_pk_fma_f32 v[26:27], v[32:33], v[210:211], v[26:27] op_sel_hi:[0,1,1]
	v_pk_add_f32 v[18:19], v[22:23], v[24:25]
	v_pk_add_f32 v[14:15], v[14:15], v[16:17]
	s_waitcnt vmcnt(0)
	v_cvt_pk_f32_fp8_e32 v[228:229], v230
	v_cvt_pk_f32_fp8_sdwa v[230:231], v230 src0_sel:WORD_1
	v_pk_fma_f32 v[6:7], v[34:35], v[214:215], v[26:27] op_sel_hi:[0,1,1]
	v_pk_fma_f32 v[0:1], v[32:33], v[224:225], v[28:29] op_sel_hi:[0,1,1]
	v_pk_add_f32 v[26:27], v[56:57], v[56:57] op_sel:[0,1] op_sel_hi:[1,0]
	v_pk_add_f32 v[28:29], v[58:59], v[58:59] op_sel:[0,1] op_sel_hi:[1,0]
	v_pk_add_f32 v[16:17], v[18:19], v[18:19] op_sel:[0,1] op_sel_hi:[1,0]
	v_add_f32_e32 v14, 0, v14
	v_pk_fma_f32 v[2:3], v[32:33], v[226:227], v[30:31] op_sel_hi:[0,1,1]
	v_mov_b32_e32 v31, v12
	v_mov_b32_e32 v27, v60
	v_mov_b32_e32 v29, v61
	v_mov_b32_e32 v17, v13
	v_add_f32_e32 v30, v14, v15
	v_mov_b32_e32 v32, v8
	v_mov_b32_e32 v33, v10
	v_mov_b32_e32 v62, v9
	v_mov_b32_e32 v63, v11
	v_pk_add_f32 v[18:19], v[26:27], v[28:29]
	v_pk_add_f32 v[14:15], v[30:31], v[16:17]
	v_pk_add_f32 v[20:21], v[32:33], v[62:63]
	v_pk_add_f32 v[14:15], v[14:15], v[18:19]
	v_pk_add_f32 v[64:65], v[4:5], v[4:5] op_sel:[0,1] op_sel_hi:[1,0]
	v_pk_add_f32 v[66:67], v[6:7], v[6:7] op_sel:[0,1] op_sel_hi:[1,0]
	v_pk_fma_f32 v[0:1], v[34:35], v[228:229], v[0:1] op_sel_hi:[0,1,1]
	v_pk_fma_f32 v[2:3], v[34:35], v[230:231], v[2:3] op_sel_hi:[0,1,1]
	v_pk_add_f32 v[20:21], v[20:21], v[20:21] op_sel:[0,1] op_sel_hi:[1,0]
	v_pk_add_f32 v[14:15], v[14:15], v[14:15] op_sel:[0,1] op_sel_hi:[1,0]
	v_mov_b32_e32 v65, v2
	v_mov_b32_e32 v67, v3
	v_mov_b32_e32 v21, v1
	v_mov_b32_e32 v15, v0
	v_pk_add_f32 v[22:23], v[64:65], v[66:67]
	v_pk_add_f32 v[14:15], v[14:15], v[20:21]
	s_nop 0
	v_pk_add_f32 v[14:15], v[14:15], v[22:23]
	s_nop 0
	v_add_f32_e32 v14, v14, v15
	global_load_dwordx4 v[144:147], v[94:95], off offset:1024
	global_load_dwordx4 v[148:151], v[96:97], off offset:1024
	global_load_dwordx4 v[152:155], v[94:95], off offset:2048
	global_load_dwordx4 v[156:159], v[96:97], off offset:2048
	global_load_dwordx4 v[160:163], v[94:95], off offset:3072
	global_load_dwordx4 v[164:167], v[96:97], off offset:3072
	global_load_dwordx4 v[168:171], v[98:99], off
	global_load_dwordx4 v[172:175], v[100:101], off
	global_load_dwordx4 v[176:179], v[102:103], off
	global_load_dwordx4 v[180:183], v[104:105], off
	global_load_dwordx4 v[184:187], v[106:107], off
	global_load_dwordx4 v[188:191], v[108:109], off
	global_load_dwordx4 v[192:195], v[110:111], off
	global_load_dwordx4 v[196:199], v[112:113], off
	s_waitcnt lgkmcnt(0)
	s_nop 1
	v_add_f32_dpp v14, v14, v14 quad_perm:[1,0,3,2] row_mask:0xf bank_mask:0xf
	s_waitcnt lgkmcnt(0)
	s_nop 1
	v_add_f32_dpp v14, v14, v14 quad_perm:[2,3,0,1] row_mask:0xf bank_mask:0xf
	s_waitcnt lgkmcnt(0)
	s_nop 1
	v_add_f32_dpp v14, v14, v14 row_half_mirror row_mask:0xf bank_mask:0xf
	s_waitcnt lgkmcnt(0)
	s_nop 1
	v_add_f32_dpp v14, v14, v14 row_mirror row_mask:0xf bank_mask:0xf
	s_waitcnt lgkmcnt(0)
	v_mov_b32_e32 v15, v14
	s_nop 1
	v_permlane16_swap_b32_e32 v14, v15
	v_add_f32_e32 v14, v14, v15
	s_waitcnt lgkmcnt(0)
; __device__ __forceinline__ void p9_combine(Frame& F, const LAS int* tstart) {
;     ...
;         const float mean = wave_sum(s) * (1.f / D); float s2 = 0.f;
; #pragma unroll
;         for (int j = 0; j < 8; ++j) { v[j] = v[j] - mean; s2 += (v[j][0] * v[j][0] + v[j][1] * v[j][1]) + (v[j][2] * v[j][2] + v[j][3] * v[j][3]); }
;         const float rstd = 1.f / sqrtf(wave_sum(s2) * (1.f / D) + LN_EPS);
	v_mov_b32_e32 v15, v14
	s_nop 1
	v_permlane32_swap_b32_e32 v14, v15
	v_add_f32_e32 v14, v14, v15
	v_fmamk_f32 v43, v14, 0xba000000, v43
	v_fmamk_f32 v41, v14, 0xba000000, v41
	v_fmamk_f32 v51, v14, 0xba000000, v51
	v_fmamk_f32 v49, v14, 0xba000000, v49
	v_fmac_f32_e32 v42, 0xba000000, v14
	v_fmac_f32_e32 v40, 0xba000000, v14
	v_fmac_f32_e32 v50, 0xba000000, v14
	v_fmac_f32_e32 v48, 0xba000000, v14
	v_fmamk_f32 v53, v14, 0xba000000, v53
	v_fmac_f32_e32 v52, 0xba000000, v14
	v_fmamk_f32 v55, v14, 0xba000000, v55
	v_fmac_f32_e32 v54, 0xba000000, v14
	v_mov_b32_e32 v16, v41
	v_mov_b32_e32 v17, v49
	v_mov_b32_e32 v20, v43
	v_mov_b32_e32 v21, v51
	v_fmamk_f32 v57, v14, 0xba000000, v57
	v_fmac_f32_e32 v56, 0xba000000, v14
	v_fmamk_f32 v59, v14, 0xba000000, v59
	v_fmac_f32_e32 v58, 0xba000000, v14
	v_fmamk_f32 v61, v14, 0xba000000, v61
	v_fmac_f32_e32 v60, 0xba000000, v14
	v_fmamk_f32 v13, v14, 0xba000000, v13
	v_fmac_f32_e32 v12, 0xba000000, v14
	v_fmamk_f32 v9, v14, 0xba000000, v9
	v_fmac_f32_e32 v8, 0xba000000, v14
	v_fmamk_f32 v11, v14, 0xba000000, v11
	v_fmac_f32_e32 v10, 0xba000000, v14
	v_fmamk_f32 v5, v14, 0xba000000, v5
	v_fmac_f32_e32 v4, 0xba000000, v14
	v_fmamk_f32 v7, v14, 0xba000000, v7
	v_fmac_f32_e32 v6, 0xba000000, v14
	v_fmamk_f32 v3, v14, 0xba000000, v3
	v_fmac_f32_e32 v2, 0xba000000, v14
	v_fmamk_f32 v1, v14, 0xba000000, v1
	v_fmac_f32_e32 v0, 0xba000000, v14
	v_mov_b32_e32 v14, v40
	v_mov_b32_e32 v15, v48
	v_mov_b32_e32 v18, v42
	v_mov_b32_e32 v19, v50
	v_pk_mul_f32 v[22:23], v[54:55], v[54:55]
	v_pk_mul_f32 v[24:25], v[52:53], v[52:53]
	v_pk_mul_f32 v[16:17], v[16:17], v[16:17]
	v_pk_mul_f32 v[20:21], v[20:21], v[20:21]
	v_pk_mov_b32 v[64:65], v[24:25], v[22:23] op_sel:[1,0]
	v_mov_b32_e32 v25, v23
	v_pk_fma_f32 v[14:15], v[14:15], v[14:15], v[16:17]
	v_pk_fma_f32 v[16:17], v[18:19], v[18:19], v[20:21]
	v_mul_f32_e32 v26, v56, v56
	v_mul_f32_e32 v28, v58, v58
	v_pk_add_f32 v[18:19], v[64:65], v[24:25]
	v_pk_add_f32 v[14:15], v[14:15], v[16:17]
	v_pk_fma_f32 v[22:23], v[56:57], v[56:57], v[26:27] op_sel_hi:[1,1,0]
	v_pk_fma_f32 v[26:27], v[58:59], v[58:59], v[28:29] op_sel_hi:[1,1,0]
	v_pk_add_f32 v[16:17], v[18:19], v[18:19] op_sel_hi:[0,1]
	v_pk_add_f32 v[14:15], v[14:15], v[14:15] op_sel_hi:[0,1]
	v_pk_mul_f32 v[30:31], v[10:11], v[10:11]
	v_pk_mul_f32 v[32:33], v[8:9], v[8:9]
	v_mul_f32_e32 v22, v12, v12
	v_mul_f32_e32 v26, v13, v13
	v_mul_f32_e32 v16, v60, v60
	v_mul_f32_e32 v14, v61, v61
	v_pk_mov_b32 v[28:29], v[32:33], v[30:31] op_sel:[1,0]
	v_mov_b32_e32 v33, v31
	v_pk_add_f32 v[18:19], v[22:23], v[26:27]
	v_pk_add_f32 v[14:15], v[16:17], v[14:15]
	v_mul_f32_e32 v34, v4, v4
	v_mul_f32_e32 v62, v6, v6
	v_pk_add_f32 v[20:21], v[28:29], v[32:33]
	v_pk_add_f32 v[14:15], v[18:19], v[14:15]
	v_pk_fma_f32 v[30:31], v[4:5], v[4:5], v[34:35] op_sel_hi:[1,1,0]
	v_pk_fma_f32 v[34:35], v[6:7], v[6:7], v[62:63] op_sel_hi:[1,1,0]
	v_pk_add_f32 v[20:21], v[20:21], v[20:21] op_sel_hi:[0,1]
	v_pk_add_f32 v[14:15], v[14:15], v[14:15] op_sel_hi:[0,1]
	v_mul_f32_e32 v30, v0, v0
	v_mul_f32_e32 v34, v1, v1
	v_mul_f32_e32 v20, v2, v2
	v_mul_f32_e32 v14, v3, v3
	v_pk_add_f32 v[22:23], v[30:31], v[34:35]
	v_pk_add_f32 v[14:15], v[20:21], v[14:15]
	s_nop 0
	v_pk_add_f32 v[14:15], v[22:23], v[14:15]
	s_nop 0
	v_add_f32_e32 v14, v14, v15
	s_waitcnt lgkmcnt(0)
	s_nop 1
	v_add_f32_dpp v14, v14, v14 quad_perm:[1,0,3,2] row_mask:0xf bank_mask:0xf
	s_waitcnt lgkmcnt(0)
	s_nop 1
	v_add_f32_dpp v14, v14, v14 quad_perm:[2,3,0,1] row_mask:0xf bank_mask:0xf
	s_waitcnt lgkmcnt(0)
	s_nop 1
	v_add_f32_dpp v14, v14, v14 row_half_mirror row_mask:0xf bank_mask:0xf
	s_waitcnt lgkmcnt(0)
	s_nop 1
	v_add_f32_dpp v14, v14, v14 row_mirror row_mask:0xf bank_mask:0xf
	s_waitcnt lgkmcnt(0)
; #define GAS __attribute__((address_space(1)))
; __device__ __forceinline__ void p9_combine(Frame& F, const LAS int* tstart) {
;     ...
;         const float rstd = 1.f / sqrtf(wave_sum(s2) * (1.f / D) + LN_EPS);
; #pragma unroll
;         for (int j = 0; j < 8; ++j) { const int col = 4 * lane + 256 * j; const f32x4 g = *(const GAS f32x4*)(F.ln2_g + col), b = *(const GAS f32x4*)(F.ln2_b + col);
;             *(GAS f32x4*)(F.out + (size_t)m * D + col) = v[j] * rstd * g + b; }
	v_mov_b32_e32 v15, v14
	s_nop 1
	v_permlane16_swap_b32_e32 v14, v15
	v_add_f32_e32 v14, v14, v15
	s_waitcnt lgkmcnt(0)
	v_mov_b32_e32 v15, v14
	s_nop 1
	v_permlane32_swap_b32_e32 v14, v15
	v_add_f32_e32 v14, v14, v15
	v_fmamk_f32 v14, v14, 0x3a000000, v141
	v_mul_f32_e32 v15, 0x4f800000, v14
	v_cmp_gt_f32_e32 vcc, s15, v14
	s_nop 1
	v_cndmask_b32_e32 v14, v14, v15, vcc
	v_sqrt_f32_e32 v15, v14
	s_nop 0
	v_add_u32_e32 v16, -1, v15
	v_add_u32_e32 v17, 1, v15
	v_fma_f32 v18, -v16, v15, v14
	v_fma_f32 v19, -v17, v15, v14
	v_cmp_ge_f32_e64 s[0:1], 0, v18
	s_nop 1
	v_cndmask_b32_e64 v15, v15, v16, s[0:1]
	v_cmp_lt_f32_e64 s[0:1], 0, v19
	s_nop 1
	v_cndmask_b32_e64 v15, v15, v17, s[0:1]
	v_mul_f32_e32 v16, 0x37800000, v15
	v_cndmask_b32_e32 v15, v15, v16, vcc
	v_cmp_class_f32_e32 vcc, v14, v142
	s_nop 1
	v_cndmask_b32_e32 v14, v15, v14, vcc
	v_div_scale_f32 v15, s[0:1], v14, v14, 1.0
	v_rcp_f32_e32 v17, v15
	v_div_scale_f32 v16, vcc, 1.0, v14, 1.0
	v_fma_f32 v18, -v15, v17, 1.0
	v_fmac_f32_e32 v17, v18, v17
	v_mul_f32_e32 v18, v16, v17
	v_fma_f32 v19, -v15, v18, v16
	v_fmac_f32_e32 v18, v19, v17
	v_fma_f32 v15, -v15, v18, v16
	v_div_fmas_f32 v15, v15, v17, v18
	v_div_fixup_f32 v22, v15, v14, 1.0
	v_pk_mul_f32 v[14:15], v[40:41], v[22:23] op_sel_hi:[1,0]
	v_pk_mul_f32 v[16:17], v[42:43], v[22:23] op_sel_hi:[1,0]
	v_pk_fma_f32 v[14:15], v[36:37], v[14:15], v[44:45]
	v_pk_fma_f32 v[16:17], v[38:39], v[16:17], v[46:47]
	global_store_dwordx4 v[114:115], v[14:17], off offset:-4096 sc1
	v_pk_mul_f32 v[24:25], v[50:51], v[22:23] op_sel_hi:[1,0]
	v_pk_mul_f32 v[26:27], v[48:49], v[22:23] op_sel_hi:[1,0]
	v_pk_mul_f32 v[12:13], v[12:13], v[22:23] op_sel_hi:[1,0]
	v_pk_mul_f32 v[10:11], v[10:11], v[22:23] op_sel_hi:[1,0]
	v_pk_mul_f32 v[8:9], v[8:9], v[22:23] op_sel_hi:[1,0]
	v_pk_mul_f32 v[6:7], v[6:7], v[22:23] op_sel_hi:[1,0]
	v_pk_mul_f32 v[4:5], v[4:5], v[22:23] op_sel_hi:[1,0]
	v_pk_mul_f32 v[2:3], v[2:3], v[22:23] op_sel_hi:[1,0]
	v_pk_mul_f32 v[0:1], v[0:1], v[22:23] op_sel_hi:[1,0]
	s_waitcnt vmcnt(1)
	v_pk_fma_f32 v[14:15], v[144:145], v[26:27], v[148:149]
	v_pk_fma_f32 v[16:17], v[146:147], v[24:25], v[150:151]
	global_store_dwordx4 v[114:115], v[14:17], off offset:-3072 sc1
	v_pk_mul_f32 v[24:25], v[54:55], v[22:23] op_sel_hi:[1,0]
	v_pk_mul_f32 v[26:27], v[52:53], v[22:23] op_sel_hi:[1,0]
	s_nop 0
	v_pk_fma_f32 v[16:17], v[154:155], v[24:25], v[158:159]
	v_pk_fma_f32 v[14:15], v[152:153], v[26:27], v[156:157]
	global_store_dwordx4 v[114:115], v[14:17], off offset:-2048 sc1
	v_pk_mul_f32 v[24:25], v[58:59], v[22:23] op_sel_hi:[1,0]
	v_pk_mul_f32 v[26:27], v[56:57], v[22:23] op_sel_hi:[1,0]
	s_nop 0
	v_pk_fma_f32 v[16:17], v[162:163], v[24:25], v[166:167]
	v_pk_fma_f32 v[14:15], v[160:161], v[26:27], v[164:165]
	global_store_dwordx4 v[114:115], v[14:17], off offset:-1024 sc1
	v_pk_mul_f32 v[24:25], v[60:61], v[22:23] op_sel_hi:[1,0]
	s_nop 1
	v_pk_fma_f32 v[12:13], v[168:169], v[12:13], v[172:173]
	v_pk_fma_f32 v[14:15], v[170:171], v[24:25], v[174:175]
	global_store_dwordx4 v[114:115], v[12:15], off sc1
	v_pk_fma_f32 v[8:9], v[176:177], v[8:9], v[180:181]
	v_pk_fma_f32 v[10:11], v[178:179], v[10:11], v[182:183]
	global_store_dwordx4 v[114:115], v[8:11], off offset:1024 sc1
	v_pk_fma_f32 v[4:5], v[184:185], v[4:5], v[188:189]
	v_pk_fma_f32 v[6:7], v[186:187], v[6:7], v[190:191]
	global_store_dwordx4 v[114:115], v[4:7], off offset:2048 sc1
	v_pk_fma_f32 v[0:1], v[192:193], v[0:1], v[196:197]
	v_pk_fma_f32 v[2:3], v[194:195], v[2:3], v[198:199]
	global_store_dwordx4 v[114:115], v[0:3], off offset:3072 sc1
	v_lshl_add_u64 v[114:115], v[114:115], 0, s[4:5]
	s_cbranch_scc1 .LBB0_1798
